# nt policy on the f32 weight loads of every conversion item (once-read data), on top of default-policy SwiGLU stores
# speedup vs baseline: 1.0080x; 1.0005x over previous
; __device__ __forceinline__ unsigned f2bf(float f) { unsigned u = __builtin_bit_cast(unsigned, f); return (u + 0x7fffu + ((u >> 16) & 1u)) >> 16; }
; __device__ __forceinline__ void p0_prologue(Frame& F, const Args& a) {
;     ...
;     { bf16* WFT = (bf16*)(F.ws + WS_WFT); const float* w = a.in[7];
;       for (int i = blockIdx.x * (NWAVES * 64) + tid; i < 16 * D; i += F.G * NWAVES * 64) { const int hh = i & 15, k = i >> 4; WFT[hh * D + k] = (bf16)f2bf(w[(size_t)k * (3 * D + 16) + 3 * D + hh]); } }
.LBB0_31:
	v_ashrrev_i32_e32 v1, 4, v0
	v_mad_i64_i32 v[8:9], s[18:19], v1, s14, v[6:7]
	v_lshl_add_u64 v[8:9], v[8:9], 0, v[2:3]
	v_add_co_u32_e32 v8, vcc, 0x3000, v8
	v_add_u32_e32 v0, s3, v0
	s_nop 0
	v_addc_co_u32_e32 v9, vcc, 0, v9, vcc
	global_load_dword v5, v[8:9], off nt
	v_add_u32_e32 v8, v1, v4
	v_cmp_lt_i32_e32 vcc, s16, v0
	v_ashrrev_i32_e32 v9, 31, v8
	s_or_b64 s[0:1], vcc, s[0:1]
	v_lshl_add_u64 v[8:9], v[8:9], 1, s[12:13]
	s_waitcnt vmcnt(0)
	v_bfe_u32 v1, v5, 16, 1
	v_add3_u32 v1, v5, v1, s15
	global_store_short_d16_hi v[8:9], v1, off
	s_andn2_b64 exec, exec, s[0:1]
	s_cbranch_execnz .LBB0_31

; #define LAS __attribute__((address_space(3)))
; __device__ __forceinline__ void tr_item8(const float* W, int ld, int K, int nblk, int item, unsigned char* WT, bool gu, float scale, LAS float* scr, int lane) {
;     const int kb = item / nblk, nb = item % nblk, k0 = 64 * kb, n0 = 32 * nb;
;     int drow0 = n0;
;     if (gu) { const int bj = n0 / FF, j = n0 - bj * FF; drow0 = 256 * (j / 128) + 128 * bj + (j % 128); }
;     { float t_[32];
; #pragma unroll
;       for (int i = 0; i < 32; ++i) t_[i] = W[(size_t)(k0 + 2 * i + (lane >> 5)) * ld + n0 + (lane & 31)];
; #pragma unroll
;       for (int i = 0; i < 32; ++i) scr[(2 * i + (lane >> 5)) * 33 + (lane & 31)] = t_[i] * scale; }
; __device__ __forceinline__ void convert_items(Frame& F, const Args& a, int lo, int hi, int w, int nw) {
;     ...
;     for (int it = lo + w; it < hi; it += nw) {
;         int r = it;
;         if (r < I_FI) { tr_item(a.in[7], 3 * D + 16, D, 96, r, (bf16*)(F.ws + WS_WFOXIN), false, scr, lane); continue; } r -= I_FI;
;         if (r < I_FO) { tr_item(a.in[9], D, D, 32, r, (bf16*)(F.ws + WS_WFOXOUT), false, scr, lane); continue; } r -= I_FO;
;         if (r < I_SI) { tr_item(a.in[10], D + 512, D, 48, r, (bf16*)(F.ws + WS_WSWAIN), false, scr, lane); continue; } r -= I_SI;
;         if (r < I_SO) { tr_item(a.in[12], D, D, 32, r, (bf16*)(F.ws + WS_WSWAOUT), false, scr, lane); continue; } r -= I_SO;
;         if (r < I_GU) { tr_item8(a.in[14], 2 * FF, D, 224, r, F.ws + WS_WGU, true, WSC_GU, scr, lane); continue; } r -= I_GU;
;         if (r < I_DN) { tr_item8(a.in[15], D, FF, 32, r, F.ws + WS_WDN, false, WSC_DN, scr, lane); continue; } r -= I_DN;
;         if (r < NE * I_GU) { const int e = r / I_GU, rr = r % I_GU; tr_item8(a.in[18] + (size_t)e * D * 2 * FF, 2 * FF, D, 224, rr, F.ws + WS_WMGU + (size_t)e * 2 * FF * D, true, WSC_GU, scr, lane); continue; } r -= NE * I_GU;
.LBB0_35:
	s_cmpk_gt_i32 s14, 0x5ff
	s_mov_b64 s[10:11], -1
	s_cbranch_scc0 .LBB0_57
	s_cmpk_gt_u32 s14, 0x7ff
	s_cbranch_scc0 .LBB0_54
	s_cmpk_gt_u32 s14, 0xaff
	s_cbranch_scc0 .LBB0_51
	s_cmpk_gt_u32 s14, 0xcff
	s_cbranch_scc0 .LBB0_48
	s_cmpk_gt_u32 s14, 0x1aff
	s_cbranch_scc0 .LBB0_45
	s_cmpk_gt_u32 s14, 0x21ff
	s_cbranch_scc0 .LBB0_42
	s_add_i32 s0, s14, 0xde00
	s_bfe_u32 s10, s0, 0x70009
	s_mulk_i32 s10, 0x2493
	s_lshr_b32 s10, s10, 16
	s_mulk_i32 s10, 0xe00
	s_sub_i32 s0, s0, s10
	s_bfe_u32 s10, s0, 0xb0005
	s_mulk_i32 s10, 0x2493
	s_lshr_b32 s10, s10, 16
	s_mul_i32 s11, s10, 0xe0
	s_sub_i32 s0, s0, s11
	s_lshl_b32 s11, s0, 5
	s_and_b32 s12, s0, 0xffff
	s_cmpk_gt_u32 s12, 0x6f
	s_cselect_b32 s26, 0xfffff200, 0
	s_cselect_b32 s27, 0x80, 0
	s_lshl_b32 s0, s0, 7
	s_lshl_b32 s10, s10, 6
	s_and_b32 s0, s0, 0x3ff80
	v_add_u32_e32 v64, s10, v28
	v_lshl_add_u64 v[46:47], v[0:1], 0, s[0:1]
	v_mad_i64_i32 v[48:49], s[12:13], v64, s21, v[46:47]
	v_add_u32_e32 v50, 2, v64
	v_add_u32_e32 v52, 4, v64
	v_add_u32_e32 v54, 6, v64
	v_add_u32_e32 v56, 8, v64
	v_add_u32_e32 v58, 10, v64
	v_add_u32_e32 v60, 12, v64
	v_add_u32_e32 v62, 14, v64
	v_mad_i64_i32 v[50:51], s[12:13], v50, s21, v[46:47]
	v_mad_i64_i32 v[52:53], s[12:13], v52, s21, v[46:47]
	v_mad_i64_i32 v[54:55], s[12:13], v54, s21, v[46:47]
	v_mad_i64_i32 v[56:57], s[12:13], v56, s21, v[46:47]
	v_mad_i64_i32 v[58:59], s[12:13], v58, s21, v[46:47]
	v_mad_i64_i32 v[60:61], s[12:13], v60, s21, v[46:47]
	v_mad_i64_i32 v[62:63], s[12:13], v62, s21, v[46:47]
	global_load_dword v65, v[48:49], off nt
	global_load_dword v66, v[50:51], off nt
	global_load_dword v67, v[52:53], off nt
	global_load_dword v68, v[54:55], off nt
	global_load_dword v69, v[56:57], off nt
	global_load_dword v70, v[58:59], off nt
	global_load_dword v71, v[60:61], off nt
	global_load_dword v72, v[62:63], off nt
	v_add_u32_e32 v48, 16, v64
	v_mad_i64_i32 v[48:49], s[12:13], v48, s21, v[46:47]
	v_add_u32_e32 v50, 18, v64
	v_add_u32_e32 v52, 20, v64
	v_add_u32_e32 v54, 22, v64
	v_add_u32_e32 v56, 24, v64
	v_add_u32_e32 v58, 26, v64
	v_add_u32_e32 v60, 28, v64
	v_add_u32_e32 v62, 30, v64
	v_mad_i64_i32 v[50:51], s[12:13], v50, s21, v[46:47]
	v_mad_i64_i32 v[52:53], s[12:13], v52, s21, v[46:47]
	v_mad_i64_i32 v[54:55], s[12:13], v54, s21, v[46:47]
	v_mad_i64_i32 v[56:57], s[12:13], v56, s21, v[46:47]
	v_mad_i64_i32 v[58:59], s[12:13], v58, s21, v[46:47]
	v_mad_i64_i32 v[60:61], s[12:13], v60, s21, v[46:47]
	v_mad_i64_i32 v[62:63], s[12:13], v62, s21, v[46:47]
	global_load_dword v73, v[48:49], off nt
	global_load_dword v74, v[50:51], off nt
	global_load_dword v75, v[52:53], off nt
	global_load_dword v76, v[54:55], off nt
	global_load_dword v77, v[56:57], off nt
	global_load_dword v78, v[58:59], off nt
	global_load_dword v79, v[60:61], off nt
	global_load_dword v80, v[62:63], off nt
	v_add_u32_e32 v48, 32, v64
	v_add_u32_e32 v50, 34, v64
	v_add_u32_e32 v52, 36, v64
	v_add_u32_e32 v54, 38, v64
	v_add_u32_e32 v60, 44, v64
	v_mad_i64_i32 v[48:49], s[12:13], v48, s21, v[46:47]
	v_mad_i64_i32 v[50:51], s[12:13], v50, s21, v[46:47]
	v_mad_i64_i32 v[52:53], s[12:13], v52, s21, v[46:47]
	v_mad_i64_i32 v[54:55], s[12:13], v54, s21, v[46:47]
	v_add_u32_e32 v56, 40, v64
	v_add_u32_e32 v58, 42, v64
	v_mad_i64_i32 v[60:61], s[12:13], v60, s21, v[46:47]
	v_add_u32_e32 v62, 46, v64
	v_mad_i64_i32 v[56:57], s[12:13], v56, s21, v[46:47]
	v_mad_i64_i32 v[58:59], s[12:13], v58, s21, v[46:47]
	v_mad_i64_i32 v[62:63], s[12:13], v62, s21, v[46:47]
	global_load_dword v81, v[48:49], off nt
	global_load_dword v82, v[50:51], off nt
	global_load_dword v83, v[52:53], off nt
	global_load_dword v84, v[54:55], off nt
	global_load_dword v85, v[56:57], off nt
	global_load_dword v86, v[58:59], off nt
	s_nop 0
	global_load_dword v60, v[60:61], off nt
	s_nop 0
	global_load_dword v61, v[62:63], off nt
	v_add_u32_e32 v48, 48, v64
	v_add_u32_e32 v50, 50, v64
	v_add_u32_e32 v52, 52, v64
	v_add_u32_e32 v54, 54, v64
	v_mad_i64_i32 v[48:49], s[12:13], v48, s21, v[46:47]
	v_mad_i64_i32 v[50:51], s[12:13], v50, s21, v[46:47]
	v_mad_i64_i32 v[52:53], s[12:13], v52, s21, v[46:47]
	v_mad_i64_i32 v[54:55], s[12:13], v54, s21, v[46:47]
	v_add_u32_e32 v56, 56, v64
	v_add_u32_e32 v58, 58, v64
	v_mad_i64_i32 v[56:57], s[12:13], v56, s21, v[46:47]
	v_mad_i64_i32 v[58:59], s[12:13], v58, s21, v[46:47]
	global_load_dword v62, v[48:49], off nt
	s_nop 0
	global_load_dword v50, v[50:51], off nt
	s_nop 0
	global_load_dword v51, v[52:53], off nt
	s_nop 0
	global_load_dword v52, v[54:55], off nt
	global_load_dword v53, v[56:57], off nt
	s_nop 0
	global_load_dword v54, v[58:59], off nt
	v_add_u32_e32 v48, 60, v64
	v_add_u32_e32 v55, 62, v64
	v_mad_i64_i32 v[48:49], s[12:13], v48, s21, v[46:47]
	v_mad_i64_i32 v[46:47], s[12:13], v55, s21, v[46:47]
	global_load_dword v48, v[48:49], off nt
	s_nop 0
	global_load_dword v46, v[46:47], off nt
	s_waitcnt vmcnt(31)
	v_mul_f32_e32 v47, 0x42800000, v65
	s_waitcnt vmcnt(30)
	v_mul_f32_e32 v49, 0x42800000, v66
	ds_write2_b32 v29, v47, v49 offset1:66
	s_waitcnt vmcnt(29)
	v_mul_f32_e32 v47, 0x42800000, v67
	s_waitcnt vmcnt(28)
	v_mul_f32_e32 v49, 0x42800000, v68
	ds_write2_b32 v29, v47, v49 offset0:132 offset1:198
	s_waitcnt vmcnt(27)
	v_mul_f32_e32 v47, 0x42800000, v69
	s_waitcnt vmcnt(26)
	v_mul_f32_e32 v49, 0x42800000, v70
	ds_write2_b32 v38, v47, v49 offset0:8 offset1:74
	s_waitcnt vmcnt(25)
	v_mul_f32_e32 v47, 0x42800000, v71
	s_waitcnt vmcnt(24)
	v_mul_f32_e32 v49, 0x42800000, v72
	ds_write2_b32 v38, v47, v49 offset0:140 offset1:206
	s_add_i32 s0, s26, s11
	s_sext_i32_i16 s11, s0
	s_bfe_u32 s11, s11, 0x70018
	s_add_i32 s11, s0, s11
	s_sext_i32_i16 s12, s11
	s_and_b32 s11, s11, 0xff80
	s_sub_i32 s0, s0, s11
	s_lshl_b32 s12, s12, 1
	s_sext_i32_i16 s0, s0
	s_waitcnt vmcnt(23)
; __device__ __forceinline__ unsigned cvt_pk4_fp8(float a, float b, float c, float d) { int w = 0; w = __builtin_amdgcn_cvt_pk_fp8_f32(a, b, w, false); w = __builtin_amdgcn_cvt_pk_fp8_f32(c, d, w, true); return (unsigned)w; }
; #define GAS __attribute__((address_space(1)))
; #define LAS __attribute__((address_space(3)))
; #define LDS_WAIT() asm volatile("s_waitcnt lgkmcnt(0)" ::: "memory")
; __device__ __forceinline__ void tr_item8(const float* W, int ld, int K, int nblk, int item, unsigned char* WT, bool gu, float scale, LAS float* scr, int lane) {
;     ...
;       for (int i = 0; i < 32; ++i) t_[i] = W[(size_t)(k0 + 2 * i + (lane >> 5)) * ld + n0 + (lane & 31)];
; #pragma unroll
;       for (int i = 0; i < 32; ++i) scr[(2 * i + (lane >> 5)) * 33 + (lane & 31)] = t_[i] * scale; }
;     LDS_WAIT(); asm volatile("" ::: "memory");
;     const int c = lane & 3;
; #pragma unroll
;     for (int j = 0; j < 2; ++j) { const int n = (lane >> 2) + 16 * j; const LAS float* sp = scr + (16 * c) * 33 + n;
;         v4u o; o.x = pg8::cvt_pk4_fp8(sp[0 * 33], sp[1 * 33], sp[2 * 33], sp[3 * 33]); o.y = pg8::cvt_pk4_fp8(sp[4 * 33], sp[5 * 33], sp[6 * 33], sp[7 * 33]);
;         o.z = pg8::cvt_pk4_fp8(sp[8 * 33], sp[9 * 33], sp[10 * 33], sp[11 * 33]); o.w = pg8::cvt_pk4_fp8(sp[12 * 33], sp[13 * 33], sp[14 * 33], sp[15 * 33]);
;         *(GAS v4u*)(WT + (size_t)(drow0 + n) * K + k0 + 16 * c) = o; }
;     LDS_WAIT(); asm volatile("" ::: "memory");
	v_mul_f32_e32 v47, 0x42800000, v73
	s_waitcnt vmcnt(22)
	v_mul_f32_e32 v49, 0x42800000, v74
	ds_write2_b32 v39, v47, v49 offset0:16 offset1:82
	s_waitcnt vmcnt(21)
	v_mul_f32_e32 v47, 0x42800000, v75
	s_waitcnt vmcnt(20)
	v_mul_f32_e32 v49, 0x42800000, v76
	ds_write2_b32 v39, v47, v49 offset0:148 offset1:214
	s_waitcnt vmcnt(19)
	v_mul_f32_e32 v47, 0x42800000, v77
	s_waitcnt vmcnt(18)
	v_mul_f32_e32 v49, 0x42800000, v78
	ds_write2_b32 v40, v47, v49 offset0:24 offset1:90
	s_waitcnt vmcnt(17)
	v_mul_f32_e32 v47, 0x42800000, v79
	s_waitcnt vmcnt(16)
	v_mul_f32_e32 v49, 0x42800000, v80
	ds_write2_b32 v40, v47, v49 offset0:156 offset1:222
	s_and_b32 s12, s12, 0xffffff00
	s_add_i32 s0, s27, s0
	s_add_i32 s0, s0, s12
	s_mov_b32 s11, s1
	s_waitcnt vmcnt(15)
	v_mul_f32_e32 v47, 0x42800000, v81
	s_waitcnt vmcnt(14)
	v_mul_f32_e32 v49, 0x42800000, v82
	ds_write2_b32 v41, v47, v49 offset0:32 offset1:98
	s_waitcnt vmcnt(13)
	v_mul_f32_e32 v47, 0x42800000, v83
	s_waitcnt vmcnt(12)
	v_mul_f32_e32 v49, 0x42800000, v84
	ds_write2_b32 v41, v47, v49 offset0:164 offset1:230
	s_waitcnt vmcnt(11)
	v_mul_f32_e32 v47, 0x42800000, v85
	s_waitcnt vmcnt(10)
	v_mul_f32_e32 v49, 0x42800000, v86
	ds_write2_b32 v42, v47, v49 offset0:40 offset1:106
	s_waitcnt vmcnt(9)
	v_mul_f32_e32 v47, 0x42800000, v60
	s_waitcnt vmcnt(8)
	v_mul_f32_e32 v49, 0x42800000, v61
	ds_write2_b32 v42, v47, v49 offset0:172 offset1:238
	v_add_u32_e32 v84, s0, v30
	v_ashrrev_i32_e32 v85, 31, v84
	v_lshlrev_b64 v[84:85], 10, v[84:85]
	s_waitcnt vmcnt(7)
	v_mul_f32_e32 v47, 0x42800000, v62
	s_waitcnt vmcnt(6)
	v_mul_f32_e32 v49, 0x42800000, v50
	ds_write2_b32 v43, v47, v49 offset0:48 offset1:114
	s_waitcnt vmcnt(5)
	v_mul_f32_e32 v47, 0x42800000, v51
	s_waitcnt vmcnt(4)
	v_mul_f32_e32 v49, 0x42800000, v52
	ds_write2_b32 v43, v47, v49 offset0:180 offset1:246
	s_waitcnt vmcnt(3)
	v_mul_f32_e32 v47, 0x42800000, v53
	s_waitcnt vmcnt(2)
	v_mul_f32_e32 v49, 0x42800000, v54
	ds_write2_b32 v44, v47, v49 offset0:56 offset1:122
	v_mov_b32_e32 v49, 0
	v_lshl_add_u64 v[50:51], v[14:15], 0, s[10:11]
	s_waitcnt vmcnt(1)
	v_mul_f32_e32 v47, 0x42800000, v48
	s_waitcnt vmcnt(0)
	v_mul_f32_e32 v46, 0x42800000, v46
	ds_write2_b32 v44, v47, v46 offset0:188 offset1:254
	s_waitcnt lgkmcnt(0)
	ds_read2_b32 v[52:53], v31 offset1:16
	ds_read2_b32 v[54:55], v31 offset0:33 offset1:49
	ds_read2_b32 v[56:57], v31 offset0:66 offset1:82
	ds_read2_b32 v[58:59], v31 offset0:99 offset1:115
	ds_read2_b32 v[60:61], v31 offset0:132 offset1:148
	ds_read2_b32 v[62:63], v31 offset0:165 offset1:181
	ds_read2_b32 v[64:65], v31 offset0:198 offset1:214
	ds_read2_b32 v[66:67], v31 offset0:231 offset1:247
	ds_read2_b32 v[68:69], v45 offset0:8 offset1:24
	ds_read2_b32 v[70:71], v45 offset0:41 offset1:57
	ds_read2_b32 v[72:73], v45 offset0:74 offset1:90
	ds_read2_b32 v[74:75], v45 offset0:107 offset1:123
	ds_read2_b32 v[76:77], v45 offset0:140 offset1:156
	ds_read2_b32 v[78:79], v45 offset0:173 offset1:189
	v_mov_b32_e32 v46, 0
	v_mov_b32_e32 v47, 0
	v_mov_b32_e32 v48, 0
	ds_read2_b32 v[80:81], v45 offset0:206 offset1:222
	ds_read2_b32 v[82:83], v45 offset0:239 offset1:255
	s_waitcnt lgkmcnt(14)
	v_cvt_pk_fp8_f32 v46, v52, v54
	s_waitcnt lgkmcnt(10)
	v_cvt_pk_fp8_f32 v47, v60, v62
	s_waitcnt lgkmcnt(6)
	v_cvt_pk_fp8_f32 v48, v68, v70
	s_waitcnt lgkmcnt(2)
	v_cvt_pk_fp8_f32 v49, v76, v78
	v_cvt_pk_fp8_f32 v46, v56, v58 op_sel:[0,0,1]
	v_cvt_pk_fp8_f32 v47, v64, v66 op_sel:[0,0,1]
	v_cvt_pk_fp8_f32 v48, v72, v74 op_sel:[0,0,1]
	s_waitcnt lgkmcnt(0)
	v_cvt_pk_fp8_f32 v49, v80, v82 op_sel:[0,0,1]
	v_lshl_add_u64 v[84:85], v[50:51], 0, v[84:85]
	v_add_u32_e32 v52, s0, v32
	s_mov_b64 s[10:11], 0
	global_store_dwordx4 v[84:85], v[46:49], off
	s_nop 1
	v_mov_b32_e32 v46, 0
	v_mov_b32_e32 v47, 0
	v_mov_b32_e32 v48, 0
	v_mov_b32_e32 v49, 0
	v_cvt_pk_fp8_f32 v46, v53, v55
	v_cvt_pk_fp8_f32 v47, v61, v63
	v_cvt_pk_fp8_f32 v48, v69, v71
	v_cvt_pk_fp8_f32 v49, v77, v79
	v_cvt_pk_fp8_f32 v46, v57, v59 op_sel:[0,0,1]
	v_cvt_pk_fp8_f32 v47, v65, v67 op_sel:[0,0,1]
	v_cvt_pk_fp8_f32 v48, v73, v75 op_sel:[0,0,1]
	v_cvt_pk_fp8_f32 v49, v81, v83 op_sel:[0,0,1]
	v_ashrrev_i32_e32 v53, 31, v52
	v_lshlrev_b64 v[52:53], 10, v[52:53]
	v_lshl_add_u64 v[50:51], v[50:51], 0, v[52:53]
	global_store_dwordx4 v[50:51], v[46:49], off
	s_waitcnt lgkmcnt(0)
; __device__ __forceinline__ void tr_item8(const float* W, int ld, int K, int nblk, int item, unsigned char* WT, bool gu, float scale, LAS float* scr, int lane) {
;     const int kb = item / nblk, nb = item % nblk, k0 = 64 * kb, n0 = 32 * nb;
;     int drow0 = n0;
;     if (gu) { const int bj = n0 / FF, j = n0 - bj * FF; drow0 = 256 * (j / 128) + 128 * bj + (j % 128); }
;     { float t_[32];
; #pragma unroll
;       for (int i = 0; i < 32; ++i) t_[i] = W[(size_t)(k0 + 2 * i + (lane >> 5)) * ld + n0 + (lane & 31)];
; #pragma unroll
;       for (int i = 0; i < 32; ++i) scr[(2 * i + (lane >> 5)) * 33 + (lane & 31)] = t_[i] * scale; }
; __device__ __forceinline__ void convert_items(Frame& F, const Args& a, int lo, int hi, int w, int nw) {
;     ...
;         if (r < I_DN) { tr_item8(a.in[15], D, FF, 32, r, F.ws + WS_WDN, false, WSC_DN, scr, lane); continue; } r -= I_DN;
.LBB0_42:
	s_andn2_b64 vcc, exec, s[10:11]
	s_cbranch_vccnz .LBB0_44
	s_lshl_b32 s0, s14, 5
	s_and_b32 s10, s18, 0x1ffc0
	s_and_b32 s12, s0, 0x3e0
	v_add_u32_e32 v46, s10, v28
	s_lshl_b32 s0, s12, 2
	v_ashrrev_i32_e32 v47, 31, v46
	v_lshl_add_u64 v[48:49], v[2:3], 0, s[0:1]
	v_lshlrev_b64 v[46:47], 12, v[46:47]
	v_lshl_add_u64 v[46:47], v[48:49], 0, v[46:47]
	v_add_co_u32_e32 v48, vcc, 0x2000, v46
	s_mov_b32 s11, s1
	s_nop 0
	v_addc_co_u32_e32 v49, vcc, 0, v47, vcc
	v_add_co_u32_e32 v50, vcc, 0x4000, v46
	s_nop 1
	v_addc_co_u32_e32 v51, vcc, 0, v47, vcc
	v_add_co_u32_e32 v52, vcc, 0x6000, v46
	s_nop 1
	v_addc_co_u32_e32 v53, vcc, 0, v47, vcc
	v_add_co_u32_e32 v54, vcc, 0x8000, v46
	s_nop 1
	v_addc_co_u32_e32 v55, vcc, 0, v47, vcc
	v_add_co_u32_e32 v56, vcc, 0xa000, v46
	s_nop 1
	v_addc_co_u32_e32 v57, vcc, 0, v47, vcc
	v_add_co_u32_e32 v58, vcc, 0xc000, v46
	s_nop 1
	v_addc_co_u32_e32 v59, vcc, 0, v47, vcc
	v_add_co_u32_e32 v60, vcc, 0xe000, v46
	s_nop 1
	v_addc_co_u32_e32 v61, vcc, 0, v47, vcc
	global_load_dword v64, v[46:47], off nt
	global_load_dword v65, v[48:49], off nt
	global_load_dword v66, v[50:51], off nt
	global_load_dword v67, v[52:53], off nt
	global_load_dword v68, v[54:55], off nt
	global_load_dword v69, v[56:57], off nt
	global_load_dword v70, v[58:59], off nt
	global_load_dword v71, v[60:61], off nt
	v_add_co_u32_e32 v48, vcc, 0x10000, v46
	s_nop 1
	v_addc_co_u32_e32 v49, vcc, 0, v47, vcc
	v_add_co_u32_e32 v50, vcc, 0x12000, v46
	s_nop 1
	v_addc_co_u32_e32 v51, vcc, 0, v47, vcc
	v_add_co_u32_e32 v52, vcc, 0x14000, v46
	s_nop 1
	v_addc_co_u32_e32 v53, vcc, 0, v47, vcc
	v_add_co_u32_e32 v54, vcc, 0x16000, v46
	s_nop 1
	v_addc_co_u32_e32 v55, vcc, 0, v47, vcc
	v_add_co_u32_e32 v56, vcc, 0x18000, v46
	s_nop 1
	v_addc_co_u32_e32 v57, vcc, 0, v47, vcc
	v_add_co_u32_e32 v58, vcc, 0x1a000, v46
	s_nop 1
	v_addc_co_u32_e32 v59, vcc, 0, v47, vcc
	v_add_co_u32_e32 v60, vcc, 0x1c000, v46
	s_nop 1
	v_addc_co_u32_e32 v61, vcc, 0, v47, vcc
	v_add_co_u32_e32 v62, vcc, 0x1e000, v46
	s_nop 1
	v_addc_co_u32_e32 v63, vcc, 0, v47, vcc
	global_load_dword v72, v[48:49], off nt
	global_load_dword v73, v[50:51], off nt
	global_load_dword v74, v[52:53], off nt
	global_load_dword v75, v[54:55], off nt
	global_load_dword v76, v[56:57], off nt
	global_load_dword v77, v[58:59], off nt
	global_load_dword v78, v[60:61], off nt
	global_load_dword v79, v[62:63], off nt
	v_add_co_u32_e32 v48, vcc, 0x20000, v46
	s_nop 1
	v_addc_co_u32_e32 v49, vcc, 0, v47, vcc
	v_add_co_u32_e32 v50, vcc, 0x22000, v46
	s_nop 1
	v_addc_co_u32_e32 v51, vcc, 0, v47, vcc
	v_add_co_u32_e32 v52, vcc, 0x24000, v46
	s_nop 1
	v_addc_co_u32_e32 v53, vcc, 0, v47, vcc
	v_add_co_u32_e32 v54, vcc, 0x26000, v46
	s_nop 1
	v_addc_co_u32_e32 v55, vcc, 0, v47, vcc
	v_add_co_u32_e32 v56, vcc, 0x28000, v46
	s_nop 1
	v_addc_co_u32_e32 v57, vcc, 0, v47, vcc
	v_add_co_u32_e32 v58, vcc, 0x2a000, v46
	s_nop 1
	v_addc_co_u32_e32 v59, vcc, 0, v47, vcc
	v_add_co_u32_e32 v60, vcc, 0x2c000, v46
	s_nop 1
	v_addc_co_u32_e32 v61, vcc, 0, v47, vcc
	v_add_co_u32_e32 v62, vcc, 0x2e000, v46
	s_nop 1
	v_addc_co_u32_e32 v63, vcc, 0, v47, vcc
	global_load_dword v80, v[48:49], off nt
	global_load_dword v81, v[50:51], off nt
	global_load_dword v82, v[52:53], off nt
	global_load_dword v83, v[54:55], off nt
	global_load_dword v84, v[56:57], off nt
	global_load_dword v85, v[58:59], off nt
	s_nop 0
	global_load_dword v60, v[60:61], off nt
	s_nop 0
	global_load_dword v61, v[62:63], off nt
	v_add_co_u32_e32 v48, vcc, 0x30000, v46
	s_nop 1
	v_addc_co_u32_e32 v49, vcc, 0, v47, vcc
	v_add_co_u32_e32 v50, vcc, 0x32000, v46
	s_nop 1
	v_addc_co_u32_e32 v51, vcc, 0, v47, vcc
	v_add_co_u32_e32 v52, vcc, 0x34000, v46
	s_nop 1
	v_addc_co_u32_e32 v53, vcc, 0, v47, vcc
	v_add_co_u32_e32 v54, vcc, 0x36000, v46
	s_nop 1
	v_addc_co_u32_e32 v55, vcc, 0, v47, vcc
	v_add_co_u32_e32 v56, vcc, 0x38000, v46
	s_nop 1
	v_addc_co_u32_e32 v57, vcc, 0, v47, vcc
	v_add_co_u32_e32 v58, vcc, 0x3a000, v46
	s_nop 1
	v_addc_co_u32_e32 v59, vcc, 0, v47, vcc
	global_load_dword v62, v[48:49], off nt
	s_nop 0
	global_load_dword v50, v[50:51], off nt
	s_nop 0
	global_load_dword v51, v[52:53], off nt
	s_nop 0
	global_load_dword v52, v[54:55], off nt
	global_load_dword v53, v[56:57], off nt
	s_nop 0
	global_load_dword v54, v[58:59], off nt
	v_add_co_u32_e32 v48, vcc, 0x3c000, v46
	s_nop 1
	v_addc_co_u32_e32 v49, vcc, 0, v47, vcc
	v_add_co_u32_e32 v46, vcc, 0x3e000, v46
	s_nop 1
	v_addc_co_u32_e32 v47, vcc, 0, v47, vcc
	global_load_dword v48, v[48:49], off nt
	s_nop 0
	global_load_dword v46, v[46:47], off nt
	s_waitcnt vmcnt(31)
	v_mul_f32_e32 v47, 0x43000000, v64
	s_waitcnt vmcnt(30)
; __device__ __forceinline__ unsigned cvt_pk4_fp8(float a, float b, float c, float d) { int w = 0; w = __builtin_amdgcn_cvt_pk_fp8_f32(a, b, w, false); w = __builtin_amdgcn_cvt_pk_fp8_f32(c, d, w, true); return (unsigned)w; }
; #define GAS __attribute__((address_space(1)))
; #define LAS __attribute__((address_space(3)))
; #define LDS_WAIT() asm volatile("s_waitcnt lgkmcnt(0)" ::: "memory")
; __device__ __forceinline__ void tr_item8(const float* W, int ld, int K, int nblk, int item, unsigned char* WT, bool gu, float scale, LAS float* scr, int lane) {
;     ...
;       for (int i = 0; i < 32; ++i) scr[(2 * i + (lane >> 5)) * 33 + (lane & 31)] = t_[i] * scale; }
;     LDS_WAIT(); asm volatile("" ::: "memory");
;     const int c = lane & 3;
; #pragma unroll
;     for (int j = 0; j < 2; ++j) { const int n = (lane >> 2) + 16 * j; const LAS float* sp = scr + (16 * c) * 33 + n;
;         v4u o; o.x = pg8::cvt_pk4_fp8(sp[0 * 33], sp[1 * 33], sp[2 * 33], sp[3 * 33]); o.y = pg8::cvt_pk4_fp8(sp[4 * 33], sp[5 * 33], sp[6 * 33], sp[7 * 33]);
;         o.z = pg8::cvt_pk4_fp8(sp[8 * 33], sp[9 * 33], sp[10 * 33], sp[11 * 33]); o.w = pg8::cvt_pk4_fp8(sp[12 * 33], sp[13 * 33], sp[14 * 33], sp[15 * 33]);
;         *(GAS v4u*)(WT + (size_t)(drow0 + n) * K + k0 + 16 * c) = o; }
;     LDS_WAIT(); asm volatile("" ::: "memory");
	v_mul_f32_e32 v49, 0x43000000, v65
	ds_write2_b32 v29, v47, v49 offset1:66
	s_waitcnt vmcnt(29)
	v_mul_f32_e32 v47, 0x43000000, v66
	s_waitcnt vmcnt(28)
	v_mul_f32_e32 v49, 0x43000000, v67
	ds_write2_b32 v29, v47, v49 offset0:132 offset1:198
	s_waitcnt vmcnt(27)
	v_mul_f32_e32 v47, 0x43000000, v68
	s_waitcnt vmcnt(26)
	v_mul_f32_e32 v49, 0x43000000, v69
	ds_write2_b32 v38, v47, v49 offset0:8 offset1:74
	s_waitcnt vmcnt(25)
	v_mul_f32_e32 v47, 0x43000000, v70
	s_waitcnt vmcnt(24)
	v_mul_f32_e32 v49, 0x43000000, v71
	ds_write2_b32 v38, v47, v49 offset0:140 offset1:206
	s_waitcnt vmcnt(23)
	v_mul_f32_e32 v47, 0x43000000, v72
	s_waitcnt vmcnt(22)
	v_mul_f32_e32 v49, 0x43000000, v73
	ds_write2_b32 v39, v47, v49 offset0:16 offset1:82
	s_waitcnt vmcnt(21)
	v_mul_f32_e32 v47, 0x43000000, v74
	s_waitcnt vmcnt(20)
	v_mul_f32_e32 v49, 0x43000000, v75
	ds_write2_b32 v39, v47, v49 offset0:148 offset1:214
	s_waitcnt vmcnt(19)
	v_mul_f32_e32 v47, 0x43000000, v76
	s_waitcnt vmcnt(18)
	v_mul_f32_e32 v49, 0x43000000, v77
	ds_write2_b32 v40, v47, v49 offset0:24 offset1:90
	s_waitcnt vmcnt(17)
	v_mul_f32_e32 v47, 0x43000000, v78
	s_waitcnt vmcnt(16)
	v_mul_f32_e32 v49, 0x43000000, v79
	ds_write2_b32 v40, v47, v49 offset0:156 offset1:222
	s_waitcnt vmcnt(15)
	v_mul_f32_e32 v47, 0x43000000, v80
	s_waitcnt vmcnt(14)
	v_mul_f32_e32 v49, 0x43000000, v81
	ds_write2_b32 v41, v47, v49 offset0:32 offset1:98
	s_waitcnt vmcnt(13)
	v_mul_f32_e32 v47, 0x43000000, v82
	s_waitcnt vmcnt(12)
	v_mul_f32_e32 v49, 0x43000000, v83
	ds_write2_b32 v41, v47, v49 offset0:164 offset1:230
	s_waitcnt vmcnt(11)
	v_mul_f32_e32 v47, 0x43000000, v84
	s_waitcnt vmcnt(10)
	v_mul_f32_e32 v49, 0x43000000, v85
	ds_write2_b32 v42, v47, v49 offset0:40 offset1:106
	s_waitcnt vmcnt(9)
	v_mul_f32_e32 v47, 0x43000000, v60
	s_waitcnt vmcnt(8)
	v_mul_f32_e32 v49, 0x43000000, v61
	ds_write2_b32 v42, v47, v49 offset0:172 offset1:238
	s_waitcnt vmcnt(7)
	v_mul_f32_e32 v47, 0x43000000, v62
	s_waitcnt vmcnt(6)
	v_mul_f32_e32 v49, 0x43000000, v50
	ds_write2_b32 v43, v47, v49 offset0:48 offset1:114
	s_waitcnt vmcnt(5)
	v_mul_f32_e32 v47, 0x43000000, v51
	s_waitcnt vmcnt(4)
	v_mul_f32_e32 v49, 0x43000000, v52
	ds_write2_b32 v43, v47, v49 offset0:180 offset1:246
	s_waitcnt vmcnt(3)
	v_mul_f32_e32 v47, 0x43000000, v53
	s_waitcnt vmcnt(2)
	v_mul_f32_e32 v49, 0x43000000, v54
	ds_write2_b32 v44, v47, v49 offset0:56 offset1:122
	v_mov_b32_e32 v49, 0
	v_lshl_add_u64 v[50:51], v[16:17], 0, s[10:11]
	s_waitcnt vmcnt(1)
	v_mul_f32_e32 v47, 0x43000000, v48
	s_waitcnt vmcnt(0)
	v_mul_f32_e32 v46, 0x43000000, v46
	ds_write2_b32 v44, v47, v46 offset0:188 offset1:254
	s_waitcnt lgkmcnt(0)
	ds_read2_b32 v[52:53], v31 offset1:16
	ds_read2_b32 v[54:55], v31 offset0:33 offset1:49
	ds_read2_b32 v[56:57], v31 offset0:66 offset1:82
	ds_read2_b32 v[58:59], v31 offset0:99 offset1:115
	ds_read2_b32 v[60:61], v31 offset0:132 offset1:148
	ds_read2_b32 v[62:63], v31 offset0:165 offset1:181
	ds_read2_b32 v[64:65], v31 offset0:198 offset1:214
	ds_read2_b32 v[66:67], v31 offset0:231 offset1:247
	ds_read2_b32 v[68:69], v45 offset0:8 offset1:24
	ds_read2_b32 v[70:71], v45 offset0:41 offset1:57
	ds_read2_b32 v[72:73], v45 offset0:74 offset1:90
	ds_read2_b32 v[74:75], v45 offset0:107 offset1:123
	ds_read2_b32 v[76:77], v45 offset0:140 offset1:156
	ds_read2_b32 v[78:79], v45 offset0:173 offset1:189
	v_mov_b32_e32 v46, 0
	v_mov_b32_e32 v47, 0
	v_mov_b32_e32 v48, 0
	ds_read2_b32 v[80:81], v45 offset0:206 offset1:222
	ds_read2_b32 v[82:83], v45 offset0:239 offset1:255
	s_waitcnt lgkmcnt(14)
	v_cvt_pk_fp8_f32 v46, v52, v54
	s_waitcnt lgkmcnt(10)
	v_cvt_pk_fp8_f32 v47, v60, v62
	s_waitcnt lgkmcnt(6)
	v_cvt_pk_fp8_f32 v48, v68, v70
	s_waitcnt lgkmcnt(2)
	v_cvt_pk_fp8_f32 v49, v76, v78
	v_cvt_pk_fp8_f32 v46, v56, v58 op_sel:[0,0,1]
	v_cvt_pk_fp8_f32 v47, v64, v66 op_sel:[0,0,1]
	v_cvt_pk_fp8_f32 v48, v72, v74 op_sel:[0,0,1]
	s_waitcnt lgkmcnt(0)
	v_cvt_pk_fp8_f32 v49, v80, v82 op_sel:[0,0,1]
	v_add_u32_e32 v52, s12, v30
	v_mad_i64_i32 v[84:85], s[10:11], v52, s20, v[50:51]
	global_store_dwordx4 v[84:85], v[46:49], off
	v_add_u32_e32 v52, s12, v32
	v_mad_i64_i32 v[50:51], s[10:11], v52, s20, v[50:51]
	v_mov_b32_e32 v46, 0
	v_mov_b32_e32 v47, 0
	v_mov_b32_e32 v48, 0
	v_mov_b32_e32 v49, 0
	v_cvt_pk_fp8_f32 v46, v53, v55
	v_cvt_pk_fp8_f32 v47, v61, v63
	v_cvt_pk_fp8_f32 v48, v69, v71
	v_cvt_pk_fp8_f32 v49, v77, v79
	v_cvt_pk_fp8_f32 v46, v57, v59 op_sel:[0,0,1]
	v_cvt_pk_fp8_f32 v47, v65, v67 op_sel:[0,0,1]
	v_cvt_pk_fp8_f32 v48, v73, v75 op_sel:[0,0,1]
	v_cvt_pk_fp8_f32 v49, v81, v83 op_sel:[0,0,1]
	global_store_dwordx4 v[50:51], v[46:49], off
	s_waitcnt lgkmcnt(0)

; __device__ __forceinline__ void tr_item8(const float* W, int ld, int K, int nblk, int item, unsigned char* WT, bool gu, float scale, LAS float* scr, int lane) {
;     const int kb = item / nblk, nb = item % nblk, k0 = 64 * kb, n0 = 32 * nb;
;     int drow0 = n0;
;     if (gu) { const int bj = n0 / FF, j = n0 - bj * FF; drow0 = 256 * (j / 128) + 128 * bj + (j % 128); }
;     { float t_[32];
; #pragma unroll
;       for (int i = 0; i < 32; ++i) t_[i] = W[(size_t)(k0 + 2 * i + (lane >> 5)) * ld + n0 + (lane & 31)];
; #pragma unroll
;       for (int i = 0; i < 32; ++i) scr[(2 * i + (lane >> 5)) * 33 + (lane & 31)] = t_[i] * scale; }
; __device__ __forceinline__ void convert_items(Frame& F, const Args& a, int lo, int hi, int w, int nw) {
;     ...
;         if (r < I_GU) { tr_item8(a.in[14], 2 * FF, D, 224, r, F.ws + WS_WGU, true, WSC_GU, scr, lane); continue; } r -= I_GU;
.LBB0_45:
	s_andn2_b64 vcc, exec, s[10:11]
	s_cbranch_vccnz .LBB0_47
	s_add_i32 s0, s14, 0xf300
	s_bfe_u32 s10, s0, 0xb0005
	s_mulk_i32 s10, 0x2493
	s_lshr_b32 s10, s10, 16
	s_mul_i32 s11, s10, 0xe0
	s_sub_i32 s0, s0, s11
	s_lshl_b32 s11, s0, 5
	s_and_b32 s12, s0, 0xffff
	s_cmpk_gt_u32 s12, 0x6f
	s_cselect_b32 s26, 0xfffff200, 0
	s_cselect_b32 s27, 0x80, 0
	s_lshl_b32 s0, s0, 7
	s_lshl_b32 s10, s10, 6
	s_and_b32 s0, s0, 0x3ff80
	v_add_u32_e32 v64, s10, v28
	v_lshl_add_u64 v[46:47], v[4:5], 0, s[0:1]
	v_mad_i64_i32 v[48:49], s[12:13], v64, s21, v[46:47]
	v_add_u32_e32 v50, 2, v64
	v_add_u32_e32 v52, 4, v64
	v_add_u32_e32 v54, 6, v64
	v_add_u32_e32 v56, 8, v64
	v_add_u32_e32 v58, 10, v64
	v_add_u32_e32 v60, 12, v64
	v_add_u32_e32 v62, 14, v64
	v_mad_i64_i32 v[50:51], s[12:13], v50, s21, v[46:47]
	v_mad_i64_i32 v[52:53], s[12:13], v52, s21, v[46:47]
	v_mad_i64_i32 v[54:55], s[12:13], v54, s21, v[46:47]
	v_mad_i64_i32 v[56:57], s[12:13], v56, s21, v[46:47]
	v_mad_i64_i32 v[58:59], s[12:13], v58, s21, v[46:47]
	v_mad_i64_i32 v[60:61], s[12:13], v60, s21, v[46:47]
	v_mad_i64_i32 v[62:63], s[12:13], v62, s21, v[46:47]
	global_load_dword v65, v[48:49], off nt
	global_load_dword v66, v[50:51], off nt
	global_load_dword v67, v[52:53], off nt
	global_load_dword v68, v[54:55], off nt
	global_load_dword v69, v[56:57], off nt
	global_load_dword v70, v[58:59], off nt
	global_load_dword v71, v[60:61], off nt
	global_load_dword v72, v[62:63], off nt
	v_add_u32_e32 v48, 16, v64
	v_mad_i64_i32 v[48:49], s[12:13], v48, s21, v[46:47]
	v_add_u32_e32 v50, 18, v64
	v_add_u32_e32 v52, 20, v64
	v_add_u32_e32 v54, 22, v64
	v_add_u32_e32 v56, 24, v64
	v_add_u32_e32 v58, 26, v64
	v_add_u32_e32 v60, 28, v64
	v_add_u32_e32 v62, 30, v64
	v_mad_i64_i32 v[50:51], s[12:13], v50, s21, v[46:47]
	v_mad_i64_i32 v[52:53], s[12:13], v52, s21, v[46:47]
	v_mad_i64_i32 v[54:55], s[12:13], v54, s21, v[46:47]
	v_mad_i64_i32 v[56:57], s[12:13], v56, s21, v[46:47]
	v_mad_i64_i32 v[58:59], s[12:13], v58, s21, v[46:47]
	v_mad_i64_i32 v[60:61], s[12:13], v60, s21, v[46:47]
	v_mad_i64_i32 v[62:63], s[12:13], v62, s21, v[46:47]
	global_load_dword v73, v[48:49], off nt
	global_load_dword v74, v[50:51], off nt
	global_load_dword v75, v[52:53], off nt
	global_load_dword v76, v[54:55], off nt
	global_load_dword v77, v[56:57], off nt
	global_load_dword v78, v[58:59], off nt
	global_load_dword v79, v[60:61], off nt
	global_load_dword v80, v[62:63], off nt
	v_add_u32_e32 v48, 32, v64
	v_add_u32_e32 v50, 34, v64
	v_add_u32_e32 v52, 36, v64
	v_add_u32_e32 v54, 38, v64
	v_add_u32_e32 v60, 44, v64
	v_mad_i64_i32 v[48:49], s[12:13], v48, s21, v[46:47]
	v_mad_i64_i32 v[50:51], s[12:13], v50, s21, v[46:47]
	v_mad_i64_i32 v[52:53], s[12:13], v52, s21, v[46:47]
	v_mad_i64_i32 v[54:55], s[12:13], v54, s21, v[46:47]
	v_add_u32_e32 v56, 40, v64
	v_add_u32_e32 v58, 42, v64
	v_mad_i64_i32 v[60:61], s[12:13], v60, s21, v[46:47]
	v_add_u32_e32 v62, 46, v64
	v_mad_i64_i32 v[56:57], s[12:13], v56, s21, v[46:47]
	v_mad_i64_i32 v[58:59], s[12:13], v58, s21, v[46:47]
	v_mad_i64_i32 v[62:63], s[12:13], v62, s21, v[46:47]
	global_load_dword v81, v[48:49], off nt
	global_load_dword v82, v[50:51], off nt
	global_load_dword v83, v[52:53], off nt
	global_load_dword v84, v[54:55], off nt
	global_load_dword v85, v[56:57], off nt
	global_load_dword v86, v[58:59], off nt
	s_nop 0
	global_load_dword v60, v[60:61], off nt
	s_nop 0
	global_load_dword v61, v[62:63], off nt
	v_add_u32_e32 v48, 48, v64
	v_add_u32_e32 v50, 50, v64
	v_add_u32_e32 v52, 52, v64
	v_add_u32_e32 v54, 54, v64
	v_mad_i64_i32 v[48:49], s[12:13], v48, s21, v[46:47]
	v_mad_i64_i32 v[50:51], s[12:13], v50, s21, v[46:47]
	v_mad_i64_i32 v[52:53], s[12:13], v52, s21, v[46:47]
	v_mad_i64_i32 v[54:55], s[12:13], v54, s21, v[46:47]
	v_add_u32_e32 v56, 56, v64
	v_add_u32_e32 v58, 58, v64
	v_mad_i64_i32 v[56:57], s[12:13], v56, s21, v[46:47]
	v_mad_i64_i32 v[58:59], s[12:13], v58, s21, v[46:47]
	global_load_dword v62, v[48:49], off nt
	s_nop 0
	global_load_dword v50, v[50:51], off nt
	s_nop 0
	global_load_dword v51, v[52:53], off nt
	s_nop 0
	global_load_dword v52, v[54:55], off nt
	global_load_dword v53, v[56:57], off nt
	s_nop 0
	global_load_dword v54, v[58:59], off nt
	v_add_u32_e32 v48, 60, v64
	v_add_u32_e32 v55, 62, v64
	v_mad_i64_i32 v[48:49], s[12:13], v48, s21, v[46:47]
	v_mad_i64_i32 v[46:47], s[12:13], v55, s21, v[46:47]
	global_load_dword v48, v[48:49], off nt
	s_nop 0
	global_load_dword v46, v[46:47], off nt
	s_waitcnt vmcnt(31)
	v_mul_f32_e32 v47, 0x42800000, v65
	s_waitcnt vmcnt(30)
	v_mul_f32_e32 v49, 0x42800000, v66
	ds_write2_b32 v29, v47, v49 offset1:66
	s_waitcnt vmcnt(29)
	v_mul_f32_e32 v47, 0x42800000, v67
	s_waitcnt vmcnt(28)
	v_mul_f32_e32 v49, 0x42800000, v68
	ds_write2_b32 v29, v47, v49 offset0:132 offset1:198
	s_waitcnt vmcnt(27)
; __device__ __forceinline__ unsigned cvt_pk4_fp8(float a, float b, float c, float d) { int w = 0; w = __builtin_amdgcn_cvt_pk_fp8_f32(a, b, w, false); w = __builtin_amdgcn_cvt_pk_fp8_f32(c, d, w, true); return (unsigned)w; }
; #define GAS __attribute__((address_space(1)))
; #define LAS __attribute__((address_space(3)))
; #define LDS_WAIT() asm volatile("s_waitcnt lgkmcnt(0)" ::: "memory")
; __device__ __forceinline__ void tr_item8(const float* W, int ld, int K, int nblk, int item, unsigned char* WT, bool gu, float scale, LAS float* scr, int lane) {
;     ...
;     if (gu) { const int bj = n0 / FF, j = n0 - bj * FF; drow0 = 256 * (j / 128) + 128 * bj + (j % 128); }
;     ...
;       for (int i = 0; i < 32; ++i) scr[(2 * i + (lane >> 5)) * 33 + (lane & 31)] = t_[i] * scale; }
;     LDS_WAIT(); asm volatile("" ::: "memory");
;     const int c = lane & 3;
; #pragma unroll
;     for (int j = 0; j < 2; ++j) { const int n = (lane >> 2) + 16 * j; const LAS float* sp = scr + (16 * c) * 33 + n;
;         v4u o; o.x = pg8::cvt_pk4_fp8(sp[0 * 33], sp[1 * 33], sp[2 * 33], sp[3 * 33]); o.y = pg8::cvt_pk4_fp8(sp[4 * 33], sp[5 * 33], sp[6 * 33], sp[7 * 33]);
;         o.z = pg8::cvt_pk4_fp8(sp[8 * 33], sp[9 * 33], sp[10 * 33], sp[11 * 33]); o.w = pg8::cvt_pk4_fp8(sp[12 * 33], sp[13 * 33], sp[14 * 33], sp[15 * 33]);
;         *(GAS v4u*)(WT + (size_t)(drow0 + n) * K + k0 + 16 * c) = o; }
;     LDS_WAIT(); asm volatile("" ::: "memory");
	v_mul_f32_e32 v47, 0x42800000, v69
	s_waitcnt vmcnt(26)
	v_mul_f32_e32 v49, 0x42800000, v70
	ds_write2_b32 v38, v47, v49 offset0:8 offset1:74
	s_waitcnt vmcnt(25)
	v_mul_f32_e32 v47, 0x42800000, v71
	s_waitcnt vmcnt(24)
	v_mul_f32_e32 v49, 0x42800000, v72
	ds_write2_b32 v38, v47, v49 offset0:140 offset1:206
	s_add_i32 s0, s26, s11
	s_sext_i32_i16 s11, s0
	s_bfe_u32 s11, s11, 0x70018
	s_add_i32 s11, s0, s11
	s_sext_i32_i16 s12, s11
	s_and_b32 s11, s11, 0xff80
	s_sub_i32 s0, s0, s11
	s_lshl_b32 s12, s12, 1
	s_sext_i32_i16 s0, s0
	s_waitcnt vmcnt(23)
	v_mul_f32_e32 v47, 0x42800000, v73
	s_waitcnt vmcnt(22)
	v_mul_f32_e32 v49, 0x42800000, v74
	ds_write2_b32 v39, v47, v49 offset0:16 offset1:82
	s_waitcnt vmcnt(21)
	v_mul_f32_e32 v47, 0x42800000, v75
	s_waitcnt vmcnt(20)
	v_mul_f32_e32 v49, 0x42800000, v76
	ds_write2_b32 v39, v47, v49 offset0:148 offset1:214
	s_waitcnt vmcnt(19)
	v_mul_f32_e32 v47, 0x42800000, v77
	s_waitcnt vmcnt(18)
	v_mul_f32_e32 v49, 0x42800000, v78
	ds_write2_b32 v40, v47, v49 offset0:24 offset1:90
	s_waitcnt vmcnt(17)
	v_mul_f32_e32 v47, 0x42800000, v79
	s_waitcnt vmcnt(16)
	v_mul_f32_e32 v49, 0x42800000, v80
	ds_write2_b32 v40, v47, v49 offset0:156 offset1:222
	s_and_b32 s12, s12, 0xffffff00
	s_add_i32 s0, s27, s0
	s_add_i32 s0, s0, s12
	s_mov_b32 s11, s1
	s_waitcnt vmcnt(15)
	v_mul_f32_e32 v47, 0x42800000, v81
	s_waitcnt vmcnt(14)
	v_mul_f32_e32 v49, 0x42800000, v82
	ds_write2_b32 v41, v47, v49 offset0:32 offset1:98
	s_waitcnt vmcnt(13)
	v_mul_f32_e32 v47, 0x42800000, v83
	s_waitcnt vmcnt(12)
	v_mul_f32_e32 v49, 0x42800000, v84
	ds_write2_b32 v41, v47, v49 offset0:164 offset1:230
	s_waitcnt vmcnt(11)
	v_mul_f32_e32 v47, 0x42800000, v85
	s_waitcnt vmcnt(10)
	v_mul_f32_e32 v49, 0x42800000, v86
	ds_write2_b32 v42, v47, v49 offset0:40 offset1:106
	s_waitcnt vmcnt(9)
	v_mul_f32_e32 v47, 0x42800000, v60
	s_waitcnt vmcnt(8)
	v_mul_f32_e32 v49, 0x42800000, v61
	ds_write2_b32 v42, v47, v49 offset0:172 offset1:238
	v_add_u32_e32 v84, s0, v30
	v_ashrrev_i32_e32 v85, 31, v84
	v_lshlrev_b64 v[84:85], 10, v[84:85]
	s_waitcnt vmcnt(7)
	v_mul_f32_e32 v47, 0x42800000, v62
	s_waitcnt vmcnt(6)
	v_mul_f32_e32 v49, 0x42800000, v50
	ds_write2_b32 v43, v47, v49 offset0:48 offset1:114
	s_waitcnt vmcnt(5)
	v_mul_f32_e32 v47, 0x42800000, v51
	s_waitcnt vmcnt(4)
	v_mul_f32_e32 v49, 0x42800000, v52
	ds_write2_b32 v43, v47, v49 offset0:180 offset1:246
	s_waitcnt vmcnt(3)
	v_mul_f32_e32 v47, 0x42800000, v53
	s_waitcnt vmcnt(2)
	v_mul_f32_e32 v49, 0x42800000, v54
	ds_write2_b32 v44, v47, v49 offset0:56 offset1:122
	v_mov_b32_e32 v49, 0
	v_lshl_add_u64 v[50:51], v[18:19], 0, s[10:11]
	s_waitcnt vmcnt(1)
	v_mul_f32_e32 v47, 0x42800000, v48
	s_waitcnt vmcnt(0)
	v_mul_f32_e32 v46, 0x42800000, v46
	ds_write2_b32 v44, v47, v46 offset0:188 offset1:254
	s_waitcnt lgkmcnt(0)
	ds_read2_b32 v[52:53], v31 offset1:16
	ds_read2_b32 v[54:55], v31 offset0:33 offset1:49
	ds_read2_b32 v[56:57], v31 offset0:66 offset1:82
	ds_read2_b32 v[58:59], v31 offset0:99 offset1:115
	ds_read2_b32 v[60:61], v31 offset0:132 offset1:148
	ds_read2_b32 v[62:63], v31 offset0:165 offset1:181
	ds_read2_b32 v[64:65], v31 offset0:198 offset1:214
	ds_read2_b32 v[66:67], v31 offset0:231 offset1:247
	ds_read2_b32 v[68:69], v45 offset0:8 offset1:24
	ds_read2_b32 v[70:71], v45 offset0:41 offset1:57
	ds_read2_b32 v[72:73], v45 offset0:74 offset1:90
	ds_read2_b32 v[74:75], v45 offset0:107 offset1:123
	ds_read2_b32 v[76:77], v45 offset0:140 offset1:156
	ds_read2_b32 v[78:79], v45 offset0:173 offset1:189
	v_mov_b32_e32 v46, 0
	v_mov_b32_e32 v47, 0
	v_mov_b32_e32 v48, 0
	ds_read2_b32 v[80:81], v45 offset0:206 offset1:222
	ds_read2_b32 v[82:83], v45 offset0:239 offset1:255
	s_waitcnt lgkmcnt(14)
	v_cvt_pk_fp8_f32 v46, v52, v54
	s_waitcnt lgkmcnt(10)
	v_cvt_pk_fp8_f32 v47, v60, v62
	s_waitcnt lgkmcnt(6)
	v_cvt_pk_fp8_f32 v48, v68, v70
	s_waitcnt lgkmcnt(2)
	v_cvt_pk_fp8_f32 v49, v76, v78
	v_cvt_pk_fp8_f32 v46, v56, v58 op_sel:[0,0,1]
	v_cvt_pk_fp8_f32 v47, v64, v66 op_sel:[0,0,1]
	v_cvt_pk_fp8_f32 v48, v72, v74 op_sel:[0,0,1]
	s_waitcnt lgkmcnt(0)
	v_cvt_pk_fp8_f32 v49, v80, v82 op_sel:[0,0,1]
	v_lshl_add_u64 v[84:85], v[50:51], 0, v[84:85]
	v_add_u32_e32 v52, s0, v32
	global_store_dwordx4 v[84:85], v[46:49], off
	s_nop 1
	v_mov_b32_e32 v46, 0
	v_mov_b32_e32 v47, 0
	v_mov_b32_e32 v48, 0
	v_mov_b32_e32 v49, 0
	v_cvt_pk_fp8_f32 v46, v53, v55
	v_cvt_pk_fp8_f32 v47, v61, v63
	v_cvt_pk_fp8_f32 v48, v69, v71
	v_cvt_pk_fp8_f32 v49, v77, v79
	v_cvt_pk_fp8_f32 v46, v57, v59 op_sel:[0,0,1]
	v_cvt_pk_fp8_f32 v47, v65, v67 op_sel:[0,0,1]
	v_cvt_pk_fp8_f32 v48, v73, v75 op_sel:[0,0,1]
	v_cvt_pk_fp8_f32 v49, v81, v83 op_sel:[0,0,1]
	v_ashrrev_i32_e32 v53, 31, v52
	v_lshlrev_b64 v[52:53], 10, v[52:53]
	v_lshl_add_u64 v[50:51], v[50:51], 0, v[52:53]
	global_store_dwordx4 v[50:51], v[46:49], off
	s_waitcnt lgkmcnt(0)

; __device__ __forceinline__ void tr_item(const float* W, int ld, int K, int nblk, int item, bf16* WT, bool gu, LAS float* scr, int lane) {
;     ...
;       for (int i = 0; i < 32; ++i) t_[i] = W[(size_t)(k0 + 2 * i + (lane >> 5)) * ld + n0 + (lane & 31)];
; #pragma unroll
;       for (int i = 0; i < 32; ++i) scr[(2 * i + (lane >> 5)) * 33 + (lane & 31)] = t_[i]; }
; __device__ __forceinline__ void convert_items(Frame& F, const Args& a, int lo, int hi, int w, int nw) {
;     ...
;         if (r < I_SO) { tr_item(a.in[12], D, D, 32, r, (bf16*)(F.ws + WS_WSWAOUT), false, scr, lane); continue; } r -= I_SO;
.LBB0_48:
	s_andn2_b64 vcc, exec, s[10:11]
	s_cbranch_vccnz .LBB0_50
	s_add_i32 s0, s18, 0x2000
	s_and_b32 s11, s0, 0x1ffc0
	s_and_b32 s10, s16, 0x3e0
	v_add_u32_e32 v46, s11, v28
	s_lshl_b32 s0, s10, 2
	v_ashrrev_i32_e32 v47, 31, v46
	v_lshl_add_u64 v[48:49], v[6:7], 0, s[0:1]
	v_lshlrev_b64 v[46:47], 12, v[46:47]
	v_lshl_add_u64 v[46:47], v[48:49], 0, v[46:47]
	v_add_co_u32_e32 v48, vcc, 0x2000, v46
	s_lshl_b32 s0, s11, 1
	s_nop 0
	v_addc_co_u32_e32 v49, vcc, 0, v47, vcc
	v_add_co_u32_e32 v50, vcc, 0x4000, v46
	s_nop 1
	v_addc_co_u32_e32 v51, vcc, 0, v47, vcc
	v_add_co_u32_e32 v52, vcc, 0x6000, v46
	s_nop 1
	v_addc_co_u32_e32 v53, vcc, 0, v47, vcc
	v_add_co_u32_e32 v54, vcc, 0x8000, v46
	s_nop 1
	v_addc_co_u32_e32 v55, vcc, 0, v47, vcc
	v_add_co_u32_e32 v56, vcc, 0xa000, v46
	s_nop 1
	v_addc_co_u32_e32 v57, vcc, 0, v47, vcc
	v_add_co_u32_e32 v58, vcc, 0xc000, v46
	s_nop 1
	v_addc_co_u32_e32 v59, vcc, 0, v47, vcc
	v_add_co_u32_e32 v60, vcc, 0xe000, v46
	s_nop 1
	v_addc_co_u32_e32 v61, vcc, 0, v47, vcc
	global_load_dword v64, v[46:47], off nt
	global_load_dword v65, v[48:49], off nt
	global_load_dword v66, v[50:51], off nt
	global_load_dword v67, v[52:53], off nt
	global_load_dword v68, v[54:55], off nt
	global_load_dword v69, v[56:57], off nt
	global_load_dword v70, v[58:59], off nt
	global_load_dword v71, v[60:61], off nt
	v_add_co_u32_e32 v48, vcc, 0x10000, v46
	s_nop 1
	v_addc_co_u32_e32 v49, vcc, 0, v47, vcc
	v_add_co_u32_e32 v50, vcc, 0x12000, v46
	s_nop 1
	v_addc_co_u32_e32 v51, vcc, 0, v47, vcc
	v_add_co_u32_e32 v52, vcc, 0x14000, v46
	s_nop 1
	v_addc_co_u32_e32 v53, vcc, 0, v47, vcc
	v_add_co_u32_e32 v54, vcc, 0x16000, v46
	s_nop 1
	v_addc_co_u32_e32 v55, vcc, 0, v47, vcc
	v_add_co_u32_e32 v56, vcc, 0x18000, v46
	s_nop 1
	v_addc_co_u32_e32 v57, vcc, 0, v47, vcc
	v_add_co_u32_e32 v58, vcc, 0x1a000, v46
	s_nop 1
	v_addc_co_u32_e32 v59, vcc, 0, v47, vcc
	v_add_co_u32_e32 v60, vcc, 0x1c000, v46
	s_nop 1
	v_addc_co_u32_e32 v61, vcc, 0, v47, vcc
	v_add_co_u32_e32 v62, vcc, 0x1e000, v46
	s_nop 1
	v_addc_co_u32_e32 v63, vcc, 0, v47, vcc
	global_load_dword v72, v[48:49], off nt
	global_load_dword v73, v[50:51], off nt
	global_load_dword v74, v[52:53], off nt
	global_load_dword v75, v[54:55], off nt
	global_load_dword v76, v[56:57], off nt
	global_load_dword v77, v[58:59], off nt
	global_load_dword v78, v[60:61], off nt
	global_load_dword v79, v[62:63], off nt
	v_add_co_u32_e32 v48, vcc, 0x20000, v46
	s_nop 1
	v_addc_co_u32_e32 v49, vcc, 0, v47, vcc
	v_add_co_u32_e32 v50, vcc, 0x22000, v46
	s_nop 1
	v_addc_co_u32_e32 v51, vcc, 0, v47, vcc
	v_add_co_u32_e32 v52, vcc, 0x24000, v46
	s_nop 1
	v_addc_co_u32_e32 v53, vcc, 0, v47, vcc
	v_add_co_u32_e32 v54, vcc, 0x26000, v46
	s_nop 1
	v_addc_co_u32_e32 v55, vcc, 0, v47, vcc
	v_add_co_u32_e32 v56, vcc, 0x28000, v46
	s_nop 1
	v_addc_co_u32_e32 v57, vcc, 0, v47, vcc
	v_add_co_u32_e32 v58, vcc, 0x2a000, v46
	s_nop 1
	v_addc_co_u32_e32 v59, vcc, 0, v47, vcc
	v_add_co_u32_e32 v60, vcc, 0x2c000, v46
	s_nop 1
	v_addc_co_u32_e32 v61, vcc, 0, v47, vcc
	v_add_co_u32_e32 v62, vcc, 0x2e000, v46
	s_nop 1
	v_addc_co_u32_e32 v63, vcc, 0, v47, vcc
	global_load_dword v80, v[48:49], off nt
	global_load_dword v81, v[50:51], off nt
	global_load_dword v82, v[52:53], off nt
	global_load_dword v83, v[54:55], off nt
	global_load_dword v84, v[56:57], off nt
	global_load_dword v85, v[58:59], off nt
	global_load_dword v86, v[60:61], off nt
	s_nop 0
	global_load_dword v62, v[62:63], off nt
	v_add_co_u32_e32 v48, vcc, 0x30000, v46
	s_nop 1
	v_addc_co_u32_e32 v49, vcc, 0, v47, vcc
	v_add_co_u32_e32 v50, vcc, 0x32000, v46
	s_nop 1
	v_addc_co_u32_e32 v51, vcc, 0, v47, vcc
	v_add_co_u32_e32 v52, vcc, 0x34000, v46
	s_nop 1
	v_addc_co_u32_e32 v53, vcc, 0, v47, vcc
	v_add_co_u32_e32 v54, vcc, 0x36000, v46
	s_nop 1
	v_addc_co_u32_e32 v55, vcc, 0, v47, vcc
	v_add_co_u32_e32 v56, vcc, 0x38000, v46
	s_nop 1
	v_addc_co_u32_e32 v57, vcc, 0, v47, vcc
	v_add_co_u32_e32 v58, vcc, 0x3a000, v46
	s_nop 1
	v_addc_co_u32_e32 v59, vcc, 0, v47, vcc
	v_add_co_u32_e32 v60, vcc, 0x3c000, v46
	s_nop 1
	v_addc_co_u32_e32 v61, vcc, 0, v47, vcc
	v_add_co_u32_e32 v46, vcc, 0x3e000, v46
	s_nop 1
	v_addc_co_u32_e32 v47, vcc, 0, v47, vcc
	global_load_dword v48, v[48:49], off nt
	s_nop 0
	global_load_dword v49, v[50:51], off nt
	s_nop 0
	global_load_dword v50, v[52:53], off nt
	global_load_dword v51, v[54:55], off nt
	s_nop 0
	global_load_dword v52, v[56:57], off nt
	global_load_dword v53, v[58:59], off nt
	global_load_dword v54, v[60:61], off nt
	s_nop 0
	global_load_dword v46, v[46:47], off nt
	s_waitcnt vmcnt(30)
	ds_write2_b32 v29, v64, v65 offset1:66
	s_waitcnt vmcnt(28)
	ds_write2_b32 v29, v66, v67 offset0:132 offset1:198
	s_waitcnt vmcnt(26)
	ds_write2_b32 v38, v68, v69 offset0:8 offset1:74
	s_waitcnt vmcnt(24)
	ds_write2_b32 v38, v70, v71 offset0:140 offset1:206
	s_waitcnt vmcnt(22)
	ds_write2_b32 v39, v72, v73 offset0:16 offset1:82
	s_waitcnt vmcnt(20)
	ds_write2_b32 v39, v74, v75 offset0:148 offset1:214
	s_waitcnt vmcnt(18)
	ds_write2_b32 v40, v76, v77 offset0:24 offset1:90
	s_waitcnt vmcnt(16)
	ds_write2_b32 v40, v78, v79 offset0:156 offset1:222
	s_waitcnt vmcnt(14)
	ds_write2_b32 v41, v80, v81 offset0:32 offset1:98
	s_waitcnt vmcnt(12)
	ds_write2_b32 v41, v82, v83 offset0:164 offset1:230
	s_waitcnt vmcnt(10)
; #define GAS __attribute__((address_space(1)))
; #define LAS __attribute__((address_space(3)))
; #define LDS_WAIT() asm volatile("s_waitcnt lgkmcnt(0)" ::: "memory")
; __device__ __forceinline__ unsigned pk2(float lo, float hi) { return f2bf(lo) | (f2bf(hi) << 16); }
; __device__ __forceinline__ void tr_item(const float* W, int ld, int K, int nblk, int item, bf16* WT, bool gu, LAS float* scr, int lane) {
;     ...
;       for (int i = 0; i < 32; ++i) scr[(2 * i + (lane >> 5)) * 33 + (lane & 31)] = t_[i]; }
;     LDS_WAIT(); asm volatile("" ::: "memory");
;     const int c = lane & 7;
; #pragma unroll
;     for (int j = 0; j < 4; ++j) { const int n = (lane >> 3) + 8 * j; const LAS float* s = scr + (8 * c) * 33 + n;
;         v4u o; o.x = pk2(s[0 * 33], s[1 * 33]); o.y = pk2(s[2 * 33], s[3 * 33]); o.z = pk2(s[4 * 33], s[5 * 33]); o.w = pk2(s[6 * 33], s[7 * 33]);
;         *(GAS v4u*)(WT + (size_t)(drow0 + n) * K + k0 + 8 * c) = o; }
;     LDS_WAIT(); asm volatile("" ::: "memory");
	ds_write2_b32 v42, v84, v85 offset0:40 offset1:106
	s_waitcnt vmcnt(8)
	ds_write2_b32 v42, v86, v62 offset0:172 offset1:238
	s_waitcnt vmcnt(6)
	ds_write2_b32 v43, v48, v49 offset0:48 offset1:114
	s_waitcnt vmcnt(4)
	ds_write2_b32 v43, v50, v51 offset0:180 offset1:246
	s_waitcnt vmcnt(2)
	ds_write2_b32 v44, v52, v53 offset0:56 offset1:122
	s_waitcnt vmcnt(0)
	ds_write2_b32 v44, v54, v46 offset0:188 offset1:254
	s_waitcnt lgkmcnt(0)
	ds_read2_b32 v[50:51], v34 offset1:8
	ds_read2_b32 v[54:55], v34 offset0:33 offset1:41
	ds_read2_b32 v[56:57], v34 offset0:66 offset1:74
	ds_read2_b32 v[58:59], v34 offset0:99 offset1:107
	ds_read2_b32 v[60:61], v34 offset0:132 offset1:140
	s_waitcnt lgkmcnt(4)
	v_bfe_u32 v46, v50, 16, 1
	v_add3_u32 v46, v50, v46, s22
	s_waitcnt lgkmcnt(3)
	v_bfe_u32 v47, v54, 16, 1
	v_lshrrev_b32_e32 v46, 16, v46
	v_add3_u32 v47, v54, v47, s22
	ds_read2_b32 v[62:63], v34 offset0:165 offset1:173
	v_and_or_b32 v46, v47, s23, v46
	s_waitcnt lgkmcnt(3)
	v_bfe_u32 v47, v56, 16, 1
	v_add3_u32 v47, v56, v47, s22
	s_waitcnt lgkmcnt(2)
	v_bfe_u32 v48, v58, 16, 1
	ds_read2_b32 v[64:65], v34 offset0:198 offset1:206
	v_lshrrev_b32_e32 v47, 16, v47
	v_add3_u32 v48, v58, v48, s22
	ds_read2_b32 v[66:67], v34 offset0:231 offset1:239
	v_and_or_b32 v47, v48, s23, v47
	s_waitcnt lgkmcnt(3)
	v_bfe_u32 v48, v60, 16, 1
	v_add3_u32 v48, v60, v48, s22
	s_waitcnt lgkmcnt(2)
	v_bfe_u32 v49, v62, 16, 1
	v_lshrrev_b32_e32 v48, 16, v48
	v_add3_u32 v49, v62, v49, s22
	v_and_or_b32 v48, v49, s23, v48
	s_waitcnt lgkmcnt(1)
	v_bfe_u32 v49, v64, 16, 1
	v_add_u32_e32 v68, s10, v33
	v_add3_u32 v49, v64, v49, s22
	s_waitcnt lgkmcnt(0)
	v_bfe_u32 v50, v66, 16, 1
	v_ashrrev_i32_e32 v69, 31, v68
	v_lshl_add_u64 v[52:53], v[20:21], 0, s[0:1]
	v_lshrrev_b32_e32 v49, 16, v49
	v_add3_u32 v50, v66, v50, s22
	v_lshlrev_b64 v[68:69], 11, v[68:69]
	v_and_or_b32 v49, v50, s23, v49
	v_lshl_add_u64 v[68:69], v[52:53], 0, v[68:69]
	global_store_dwordx4 v[68:69], v[46:49], off
	v_bfe_u32 v50, v67, 16, 1
	v_add3_u32 v50, v67, v50, s22
	v_bfe_u32 v46, v51, 16, 1
	v_add3_u32 v46, v51, v46, s22
	v_bfe_u32 v47, v55, 16, 1
	v_lshrrev_b32_e32 v46, 16, v46
	v_add3_u32 v47, v55, v47, s22
	v_and_or_b32 v46, v47, s23, v46
	v_bfe_u32 v47, v57, 16, 1
	v_add3_u32 v47, v57, v47, s22
	v_bfe_u32 v48, v59, 16, 1
	v_lshrrev_b32_e32 v47, 16, v47
	v_add3_u32 v48, v59, v48, s22
	v_and_or_b32 v47, v48, s23, v47
	v_bfe_u32 v48, v61, 16, 1
	v_add3_u32 v48, v61, v48, s22
	v_bfe_u32 v49, v63, 16, 1
	v_lshrrev_b32_e32 v48, 16, v48
	v_add3_u32 v49, v63, v49, s22
	v_and_or_b32 v48, v49, s23, v48
	v_bfe_u32 v49, v65, 16, 1
	v_add3_u32 v49, v65, v49, s22
	v_lshrrev_b32_e32 v49, 16, v49
	v_and_or_b32 v49, v50, s23, v49
	v_add_u32_e32 v50, s10, v35
	v_ashrrev_i32_e32 v51, 31, v50
	v_lshlrev_b64 v[50:51], 11, v[50:51]
	ds_read2_b32 v[54:55], v34 offset0:16 offset1:24
	v_lshl_add_u64 v[50:51], v[52:53], 0, v[50:51]
	global_store_dwordx4 v[50:51], v[46:49], off
	ds_read2_b32 v[50:51], v34 offset0:49 offset1:57
	ds_read2_b32 v[56:57], v34 offset0:82 offset1:90
	ds_read2_b32 v[58:59], v34 offset0:115 offset1:123
	s_waitcnt lgkmcnt(3)
	v_bfe_u32 v46, v54, 16, 1
	v_add3_u32 v46, v54, v46, s22
	s_waitcnt lgkmcnt(2)
	v_bfe_u32 v47, v50, 16, 1
	ds_read2_b32 v[60:61], v34 offset0:148 offset1:156
	v_lshrrev_b32_e32 v46, 16, v46
	v_add3_u32 v47, v50, v47, s22
	ds_read2_b32 v[62:63], v34 offset0:181 offset1:189
	v_and_or_b32 v46, v47, s23, v46
	s_waitcnt lgkmcnt(3)
	v_bfe_u32 v47, v56, 16, 1
	v_add3_u32 v47, v56, v47, s22
	s_waitcnt lgkmcnt(2)
	v_bfe_u32 v48, v58, 16, 1
	ds_read2_b32 v[64:65], v34 offset0:214 offset1:222
	v_lshrrev_b32_e32 v47, 16, v47
	v_add3_u32 v48, v58, v48, s22
	ds_read2_b32 v[66:67], v34 offset0:247 offset1:255
	v_and_or_b32 v47, v48, s23, v47
	s_waitcnt lgkmcnt(3)
	v_bfe_u32 v48, v60, 16, 1
	v_add3_u32 v48, v60, v48, s22
	s_waitcnt lgkmcnt(2)
	v_bfe_u32 v49, v62, 16, 1
	v_lshrrev_b32_e32 v48, 16, v48
	v_add3_u32 v49, v62, v49, s22
	v_and_or_b32 v48, v49, s23, v48
	s_waitcnt lgkmcnt(1)
	v_bfe_u32 v49, v64, 16, 1
	v_add_u32_e32 v68, s10, v36
	v_add3_u32 v49, v64, v49, s22
	s_waitcnt lgkmcnt(0)
	v_bfe_u32 v50, v66, 16, 1
	v_ashrrev_i32_e32 v69, 31, v68
	v_lshrrev_b32_e32 v49, 16, v49
	v_add3_u32 v50, v66, v50, s22
	v_lshlrev_b64 v[68:69], 11, v[68:69]
	v_and_or_b32 v49, v50, s23, v49
	v_lshl_add_u64 v[68:69], v[52:53], 0, v[68:69]
	global_store_dwordx4 v[68:69], v[46:49], off
	v_bfe_u32 v50, v67, 16, 1
	v_add3_u32 v50, v67, v50, s22
	v_bfe_u32 v46, v55, 16, 1
	v_add3_u32 v46, v55, v46, s22
	v_bfe_u32 v47, v51, 16, 1
	v_lshrrev_b32_e32 v46, 16, v46
	v_add3_u32 v47, v51, v47, s22
	v_and_or_b32 v46, v47, s23, v46
	v_bfe_u32 v47, v57, 16, 1
	v_add3_u32 v47, v57, v47, s22
	v_bfe_u32 v48, v59, 16, 1
	v_lshrrev_b32_e32 v47, 16, v47
	v_add3_u32 v48, v59, v48, s22
	v_and_or_b32 v47, v48, s23, v47
	v_bfe_u32 v48, v61, 16, 1
	v_add3_u32 v48, v61, v48, s22
	v_bfe_u32 v49, v63, 16, 1
	v_lshrrev_b32_e32 v48, 16, v48
	v_add3_u32 v49, v63, v49, s22
	v_and_or_b32 v48, v49, s23, v48
	v_bfe_u32 v49, v65, 16, 1
	v_add3_u32 v49, v65, v49, s22
	v_lshrrev_b32_e32 v49, 16, v49
	v_and_or_b32 v49, v50, s23, v49
	v_add_u32_e32 v50, s10, v37
	v_ashrrev_i32_e32 v51, 31, v50
	v_lshlrev_b64 v[50:51], 11, v[50:51]
	v_lshl_add_u64 v[50:51], v[52:53], 0, v[50:51]
	global_store_dwordx4 v[50:51], v[46:49], off
	s_waitcnt lgkmcnt(0)

; __device__ __forceinline__ void tr_item(const float* W, int ld, int K, int nblk, int item, bf16* WT, bool gu, LAS float* scr, int lane) {
;     ...
;       for (int i = 0; i < 32; ++i) t_[i] = W[(size_t)(k0 + 2 * i + (lane >> 5)) * ld + n0 + (lane & 31)];
; #pragma unroll
;       for (int i = 0; i < 32; ++i) scr[(2 * i + (lane >> 5)) * 33 + (lane & 31)] = t_[i]; }
; __device__ __forceinline__ void convert_items(Frame& F, const Args& a, int lo, int hi, int w, int nw) {
;     ...
;         if (r < I_SI) { tr_item(a.in[10], D + 512, D, 48, r, (bf16*)(F.ws + WS_WSWAIN), false, scr, lane); continue; } r -= I_SI;
.LBB0_51:
	s_andn2_b64 vcc, exec, s[10:11]
	s_cbranch_vccnz .LBB0_53
	s_add_i32 s0, s14, 0xf800
	s_and_b32 s10, s0, 0xffff
	s_mul_i32 s10, s10, 0xaaab
	s_lshr_b32 s11, s10, 21
	s_mul_i32 s10, s11, 48
	s_sub_i32 s0, s0, s10
	s_lshl_b32 s0, s0, 5
	s_and_b32 s10, s0, 0xffe0
	v_lshl_add_u32 v64, s11, 6, v28
	s_lshl_b32 s0, s10, 2
	v_lshl_add_u64 v[46:47], v[8:9], 0, s[0:1]
	v_add_u32_e32 v50, 2, v64
	v_add_u32_e32 v52, 4, v64
	v_add_u32_e32 v54, 6, v64
	v_add_u32_e32 v56, 8, v64
	v_add_u32_e32 v58, 10, v64
	v_add_u32_e32 v60, 12, v64
	v_add_u32_e32 v62, 14, v64
	v_mad_i64_i32 v[48:49], s[12:13], v64, s24, v[46:47]
	v_mad_i64_i32 v[50:51], s[12:13], v50, s24, v[46:47]
	v_mad_i64_i32 v[52:53], s[12:13], v52, s24, v[46:47]
	v_mad_i64_i32 v[54:55], s[12:13], v54, s24, v[46:47]
	v_mad_i64_i32 v[56:57], s[12:13], v56, s24, v[46:47]
	v_mad_i64_i32 v[58:59], s[12:13], v58, s24, v[46:47]
	v_mad_i64_i32 v[60:61], s[12:13], v60, s24, v[46:47]
	v_mad_i64_i32 v[62:63], s[12:13], v62, s24, v[46:47]
	global_load_dword v65, v[48:49], off nt
	global_load_dword v66, v[50:51], off nt
	global_load_dword v67, v[52:53], off nt
	global_load_dword v68, v[54:55], off nt
	global_load_dword v69, v[56:57], off nt
	global_load_dword v70, v[58:59], off nt
	global_load_dword v71, v[60:61], off nt
	global_load_dword v72, v[62:63], off nt
	v_add_u32_e32 v48, 16, v64
	v_add_u32_e32 v50, 18, v64
	v_add_u32_e32 v52, 20, v64
	v_add_u32_e32 v54, 22, v64
	v_add_u32_e32 v56, 24, v64
	v_add_u32_e32 v58, 26, v64
	v_add_u32_e32 v60, 28, v64
	v_add_u32_e32 v62, 30, v64
	v_mad_i64_i32 v[48:49], s[12:13], v48, s24, v[46:47]
	v_mad_i64_i32 v[50:51], s[12:13], v50, s24, v[46:47]
	v_mad_i64_i32 v[52:53], s[12:13], v52, s24, v[46:47]
	v_mad_i64_i32 v[54:55], s[12:13], v54, s24, v[46:47]
	v_mad_i64_i32 v[56:57], s[12:13], v56, s24, v[46:47]
	v_mad_i64_i32 v[58:59], s[12:13], v58, s24, v[46:47]
	v_mad_i64_i32 v[60:61], s[12:13], v60, s24, v[46:47]
	v_mad_i64_i32 v[62:63], s[12:13], v62, s24, v[46:47]
	global_load_dword v73, v[48:49], off nt
	global_load_dword v74, v[50:51], off nt
	global_load_dword v75, v[52:53], off nt
	global_load_dword v76, v[54:55], off nt
	global_load_dword v77, v[56:57], off nt
	global_load_dword v78, v[58:59], off nt
	global_load_dword v79, v[60:61], off nt
	global_load_dword v80, v[62:63], off nt
	v_add_u32_e32 v48, 32, v64
	v_add_u32_e32 v50, 34, v64
	v_add_u32_e32 v52, 36, v64
	v_add_u32_e32 v54, 38, v64
	v_add_u32_e32 v56, 40, v64
	v_add_u32_e32 v58, 42, v64
	v_add_u32_e32 v60, 44, v64
	v_add_u32_e32 v62, 46, v64
	v_mad_i64_i32 v[48:49], s[12:13], v48, s24, v[46:47]
	v_mad_i64_i32 v[50:51], s[12:13], v50, s24, v[46:47]
	v_mad_i64_i32 v[52:53], s[12:13], v52, s24, v[46:47]
	v_mad_i64_i32 v[54:55], s[12:13], v54, s24, v[46:47]
	v_mad_i64_i32 v[56:57], s[12:13], v56, s24, v[46:47]
	v_mad_i64_i32 v[58:59], s[12:13], v58, s24, v[46:47]
	v_mad_i64_i32 v[60:61], s[12:13], v60, s24, v[46:47]
	v_mad_i64_i32 v[62:63], s[12:13], v62, s24, v[46:47]
	global_load_dword v81, v[48:49], off nt
	global_load_dword v82, v[50:51], off nt
	global_load_dword v83, v[52:53], off nt
	global_load_dword v84, v[54:55], off nt
	global_load_dword v85, v[56:57], off nt
	global_load_dword v86, v[58:59], off nt
	global_load_dword v87, v[60:61], off nt
	s_nop 0
	global_load_dword v62, v[62:63], off nt
	v_add_u32_e32 v48, 48, v64
	v_add_u32_e32 v50, 50, v64
	v_add_u32_e32 v52, 52, v64
	v_add_u32_e32 v54, 54, v64
	v_add_u32_e32 v56, 56, v64
	v_add_u32_e32 v58, 58, v64
	v_add_u32_e32 v60, 60, v64
	v_add_u32_e32 v63, 62, v64
	v_mad_i64_i32 v[48:49], s[12:13], v48, s24, v[46:47]
	v_mad_i64_i32 v[50:51], s[12:13], v50, s24, v[46:47]
	v_mad_i64_i32 v[52:53], s[12:13], v52, s24, v[46:47]
	v_mad_i64_i32 v[54:55], s[12:13], v54, s24, v[46:47]
	v_mad_i64_i32 v[56:57], s[12:13], v56, s24, v[46:47]
	v_mad_i64_i32 v[58:59], s[12:13], v58, s24, v[46:47]
	v_mad_i64_i32 v[60:61], s[12:13], v60, s24, v[46:47]
	v_mad_i64_i32 v[46:47], s[12:13], v63, s24, v[46:47]
	global_load_dword v48, v[48:49], off nt
	s_nop 0
	global_load_dword v49, v[50:51], off nt
	s_nop 0
	global_load_dword v50, v[52:53], off nt
	global_load_dword v51, v[54:55], off nt
	s_nop 0
	global_load_dword v52, v[56:57], off nt
	global_load_dword v53, v[58:59], off nt
	global_load_dword v54, v[60:61], off nt
	s_nop 0
	global_load_dword v46, v[46:47], off nt
	s_waitcnt vmcnt(30)
	ds_write2_b32 v29, v65, v66 offset1:66
	s_waitcnt vmcnt(28)
	ds_write2_b32 v29, v67, v68 offset0:132 offset1:198
	s_waitcnt vmcnt(26)
	ds_write2_b32 v38, v69, v70 offset0:8 offset1:74
	s_waitcnt vmcnt(24)
	ds_write2_b32 v38, v71, v72 offset0:140 offset1:206
	s_waitcnt vmcnt(22)
	ds_write2_b32 v39, v73, v74 offset0:16 offset1:82
	s_waitcnt vmcnt(20)
	ds_write2_b32 v39, v75, v76 offset0:148 offset1:214
	s_waitcnt vmcnt(18)
	ds_write2_b32 v40, v77, v78 offset0:24 offset1:90
	s_waitcnt vmcnt(16)
	ds_write2_b32 v40, v79, v80 offset0:156 offset1:222
	s_waitcnt vmcnt(14)
	ds_write2_b32 v41, v81, v82 offset0:32 offset1:98
	s_waitcnt vmcnt(12)
	ds_write2_b32 v41, v83, v84 offset0:164 offset1:230
	s_waitcnt vmcnt(10)
	ds_write2_b32 v42, v85, v86 offset0:40 offset1:106
	s_waitcnt vmcnt(8)
	ds_write2_b32 v42, v87, v62 offset0:172 offset1:238
	s_waitcnt vmcnt(6)
; #define GAS __attribute__((address_space(1)))
; #define LAS __attribute__((address_space(3)))
; #define LDS_WAIT() asm volatile("s_waitcnt lgkmcnt(0)" ::: "memory")
; __device__ __forceinline__ unsigned pk2(float lo, float hi) { return f2bf(lo) | (f2bf(hi) << 16); }
; __device__ __forceinline__ void tr_item(const float* W, int ld, int K, int nblk, int item, bf16* WT, bool gu, LAS float* scr, int lane) {
;     ...
;       for (int i = 0; i < 32; ++i) scr[(2 * i + (lane >> 5)) * 33 + (lane & 31)] = t_[i]; }
;     LDS_WAIT(); asm volatile("" ::: "memory");
;     const int c = lane & 7;
; #pragma unroll
;     for (int j = 0; j < 4; ++j) { const int n = (lane >> 3) + 8 * j; const LAS float* s = scr + (8 * c) * 33 + n;
;         v4u o; o.x = pk2(s[0 * 33], s[1 * 33]); o.y = pk2(s[2 * 33], s[3 * 33]); o.z = pk2(s[4 * 33], s[5 * 33]); o.w = pk2(s[6 * 33], s[7 * 33]);
;         *(GAS v4u*)(WT + (size_t)(drow0 + n) * K + k0 + 8 * c) = o; }
;     LDS_WAIT(); asm volatile("" ::: "memory");
	ds_write2_b32 v43, v48, v49 offset0:48 offset1:114
	s_waitcnt vmcnt(4)
	ds_write2_b32 v43, v50, v51 offset0:180 offset1:246
	s_waitcnt vmcnt(2)
	ds_write2_b32 v44, v52, v53 offset0:56 offset1:122
	s_waitcnt vmcnt(0)
	ds_write2_b32 v44, v54, v46 offset0:188 offset1:254
	s_waitcnt lgkmcnt(0)
	ds_read2_b32 v[50:51], v34 offset1:8
	ds_read2_b32 v[54:55], v34 offset0:33 offset1:41
	ds_read2_b32 v[56:57], v34 offset0:66 offset1:74
	ds_read2_b32 v[58:59], v34 offset0:99 offset1:107
	ds_read2_b32 v[60:61], v34 offset0:132 offset1:140
	s_waitcnt lgkmcnt(4)
	v_bfe_u32 v46, v50, 16, 1
	v_add3_u32 v46, v50, v46, s22
	s_waitcnt lgkmcnt(3)
	v_bfe_u32 v47, v54, 16, 1
	v_lshrrev_b32_e32 v46, 16, v46
	v_add3_u32 v47, v54, v47, s22
	ds_read2_b32 v[62:63], v34 offset0:165 offset1:173
	v_and_or_b32 v46, v47, s23, v46
	s_waitcnt lgkmcnt(3)
	v_bfe_u32 v47, v56, 16, 1
	v_add3_u32 v47, v56, v47, s22
	s_waitcnt lgkmcnt(2)
	v_bfe_u32 v48, v58, 16, 1
	ds_read2_b32 v[64:65], v34 offset0:198 offset1:206
	v_lshrrev_b32_e32 v47, 16, v47
	v_add3_u32 v48, v58, v48, s22
	ds_read2_b32 v[66:67], v34 offset0:231 offset1:239
	v_and_or_b32 v47, v48, s23, v47
	s_waitcnt lgkmcnt(3)
	v_bfe_u32 v48, v60, 16, 1
	v_add3_u32 v48, v60, v48, s22
	s_waitcnt lgkmcnt(2)
	v_bfe_u32 v49, v62, 16, 1
	v_lshrrev_b32_e32 v48, 16, v48
	v_add3_u32 v49, v62, v49, s22
	v_and_or_b32 v48, v49, s23, v48
	s_waitcnt lgkmcnt(1)
	v_bfe_u32 v49, v64, 16, 1
	v_add_u32_e32 v68, s10, v33
	s_lshl_b32 s0, s11, 7
	v_add3_u32 v49, v64, v49, s22
	s_waitcnt lgkmcnt(0)
	v_bfe_u32 v50, v66, 16, 1
	v_ashrrev_i32_e32 v69, 31, v68
	v_lshl_add_u64 v[52:53], v[22:23], 0, s[0:1]
	v_lshrrev_b32_e32 v49, 16, v49
	v_add3_u32 v50, v66, v50, s22
	v_lshlrev_b64 v[68:69], 11, v[68:69]
	v_and_or_b32 v49, v50, s23, v49
	v_lshl_add_u64 v[68:69], v[52:53], 0, v[68:69]
	global_store_dwordx4 v[68:69], v[46:49], off
	v_bfe_u32 v50, v67, 16, 1
	v_add3_u32 v50, v67, v50, s22
	v_bfe_u32 v46, v51, 16, 1
	v_add3_u32 v46, v51, v46, s22
	v_bfe_u32 v47, v55, 16, 1
	v_lshrrev_b32_e32 v46, 16, v46
	v_add3_u32 v47, v55, v47, s22
	v_and_or_b32 v46, v47, s23, v46
	v_bfe_u32 v47, v57, 16, 1
	v_add3_u32 v47, v57, v47, s22
	v_bfe_u32 v48, v59, 16, 1
	v_lshrrev_b32_e32 v47, 16, v47
	v_add3_u32 v48, v59, v48, s22
	v_and_or_b32 v47, v48, s23, v47
	v_bfe_u32 v48, v61, 16, 1
	v_add3_u32 v48, v61, v48, s22
	v_bfe_u32 v49, v63, 16, 1
	v_lshrrev_b32_e32 v48, 16, v48
	v_add3_u32 v49, v63, v49, s22
	v_and_or_b32 v48, v49, s23, v48
	v_bfe_u32 v49, v65, 16, 1
	v_add3_u32 v49, v65, v49, s22
	v_lshrrev_b32_e32 v49, 16, v49
	v_and_or_b32 v49, v50, s23, v49
	v_add_u32_e32 v50, s10, v35
	v_ashrrev_i32_e32 v51, 31, v50
	v_lshlrev_b64 v[50:51], 11, v[50:51]
	ds_read2_b32 v[54:55], v34 offset0:16 offset1:24
	v_lshl_add_u64 v[50:51], v[52:53], 0, v[50:51]
	global_store_dwordx4 v[50:51], v[46:49], off
	ds_read2_b32 v[50:51], v34 offset0:49 offset1:57
	ds_read2_b32 v[56:57], v34 offset0:82 offset1:90
	ds_read2_b32 v[58:59], v34 offset0:115 offset1:123
	s_waitcnt lgkmcnt(3)
	v_bfe_u32 v46, v54, 16, 1
	v_add3_u32 v46, v54, v46, s22
	s_waitcnt lgkmcnt(2)
	v_bfe_u32 v47, v50, 16, 1
	ds_read2_b32 v[60:61], v34 offset0:148 offset1:156
	v_lshrrev_b32_e32 v46, 16, v46
	v_add3_u32 v47, v50, v47, s22
	ds_read2_b32 v[62:63], v34 offset0:181 offset1:189
	v_and_or_b32 v46, v47, s23, v46
	s_waitcnt lgkmcnt(3)
	v_bfe_u32 v47, v56, 16, 1
	v_add3_u32 v47, v56, v47, s22
	s_waitcnt lgkmcnt(2)
	v_bfe_u32 v48, v58, 16, 1
	ds_read2_b32 v[64:65], v34 offset0:214 offset1:222
	v_lshrrev_b32_e32 v47, 16, v47
	v_add3_u32 v48, v58, v48, s22
	ds_read2_b32 v[66:67], v34 offset0:247 offset1:255
	v_and_or_b32 v47, v48, s23, v47
	s_waitcnt lgkmcnt(3)
	v_bfe_u32 v48, v60, 16, 1
	v_add3_u32 v48, v60, v48, s22
	s_waitcnt lgkmcnt(2)
	v_bfe_u32 v49, v62, 16, 1
	v_lshrrev_b32_e32 v48, 16, v48
	v_add3_u32 v49, v62, v49, s22
	v_and_or_b32 v48, v49, s23, v48
	s_waitcnt lgkmcnt(1)
	v_bfe_u32 v49, v64, 16, 1
	v_add_u32_e32 v68, s10, v36
	v_add3_u32 v49, v64, v49, s22
	s_waitcnt lgkmcnt(0)
	v_bfe_u32 v50, v66, 16, 1
	v_ashrrev_i32_e32 v69, 31, v68
	v_lshrrev_b32_e32 v49, 16, v49
	v_add3_u32 v50, v66, v50, s22
	v_lshlrev_b64 v[68:69], 11, v[68:69]
	v_and_or_b32 v49, v50, s23, v49
	v_lshl_add_u64 v[68:69], v[52:53], 0, v[68:69]
	global_store_dwordx4 v[68:69], v[46:49], off
	v_bfe_u32 v50, v67, 16, 1
	v_add3_u32 v50, v67, v50, s22
	v_bfe_u32 v46, v55, 16, 1
	v_add3_u32 v46, v55, v46, s22
	v_bfe_u32 v47, v51, 16, 1
	v_lshrrev_b32_e32 v46, 16, v46
	v_add3_u32 v47, v51, v47, s22
	v_and_or_b32 v46, v47, s23, v46
	v_bfe_u32 v47, v57, 16, 1
	v_add3_u32 v47, v57, v47, s22
	v_bfe_u32 v48, v59, 16, 1
	v_lshrrev_b32_e32 v47, 16, v47
	v_add3_u32 v48, v59, v48, s22
	v_and_or_b32 v47, v48, s23, v47
	v_bfe_u32 v48, v61, 16, 1
	v_add3_u32 v48, v61, v48, s22
	v_bfe_u32 v49, v63, 16, 1
	v_lshrrev_b32_e32 v48, 16, v48
	v_add3_u32 v49, v63, v49, s22
	v_and_or_b32 v48, v49, s23, v48
	v_bfe_u32 v49, v65, 16, 1
	v_add3_u32 v49, v65, v49, s22
	v_lshrrev_b32_e32 v49, 16, v49
	v_and_or_b32 v49, v50, s23, v49
	v_add_u32_e32 v50, s10, v37
	v_ashrrev_i32_e32 v51, 31, v50
	v_lshlrev_b64 v[50:51], 11, v[50:51]
	v_lshl_add_u64 v[50:51], v[52:53], 0, v[50:51]
	global_store_dwordx4 v[50:51], v[46:49], off
	s_waitcnt lgkmcnt(0)

; __device__ __forceinline__ void tr_item(const float* W, int ld, int K, int nblk, int item, bf16* WT, bool gu, LAS float* scr, int lane) {
;     ...
;       for (int i = 0; i < 32; ++i) t_[i] = W[(size_t)(k0 + 2 * i + (lane >> 5)) * ld + n0 + (lane & 31)];
; #pragma unroll
;       for (int i = 0; i < 32; ++i) scr[(2 * i + (lane >> 5)) * 33 + (lane & 31)] = t_[i]; }
; __device__ __forceinline__ void convert_items(Frame& F, const Args& a, int lo, int hi, int w, int nw) {
;     ...
;         if (r < I_FO) { tr_item(a.in[9], D, D, 32, r, (bf16*)(F.ws + WS_WFOXOUT), false, scr, lane); continue; } r -= I_FO;
.LBB0_54:
	s_andn2_b64 vcc, exec, s[10:11]
	s_cbranch_vccnz .LBB0_56
	s_add_i32 s0, s18, 0x2a00
	s_and_b32 s11, s0, 0x1ffc0
	s_and_b32 s10, s16, 0x3e0
	v_add_u32_e32 v46, s11, v28
	s_lshl_b32 s0, s10, 2
	v_ashrrev_i32_e32 v47, 31, v46
	v_lshl_add_u64 v[48:49], v[10:11], 0, s[0:1]
	v_lshlrev_b64 v[46:47], 12, v[46:47]
	v_lshl_add_u64 v[46:47], v[48:49], 0, v[46:47]
	v_add_co_u32_e32 v48, vcc, 0x2000, v46
	s_lshl_b32 s0, s11, 1
	s_nop 0
	v_addc_co_u32_e32 v49, vcc, 0, v47, vcc
	v_add_co_u32_e32 v50, vcc, 0x4000, v46
	s_nop 1
	v_addc_co_u32_e32 v51, vcc, 0, v47, vcc
	v_add_co_u32_e32 v52, vcc, 0x6000, v46
	s_nop 1
	v_addc_co_u32_e32 v53, vcc, 0, v47, vcc
	v_add_co_u32_e32 v54, vcc, 0x8000, v46
	s_nop 1
	v_addc_co_u32_e32 v55, vcc, 0, v47, vcc
	v_add_co_u32_e32 v56, vcc, 0xa000, v46
	s_nop 1
	v_addc_co_u32_e32 v57, vcc, 0, v47, vcc
	v_add_co_u32_e32 v58, vcc, 0xc000, v46
	s_nop 1
	v_addc_co_u32_e32 v59, vcc, 0, v47, vcc
	v_add_co_u32_e32 v60, vcc, 0xe000, v46
	s_nop 1
	v_addc_co_u32_e32 v61, vcc, 0, v47, vcc
	global_load_dword v64, v[46:47], off nt
	global_load_dword v65, v[48:49], off nt
	global_load_dword v66, v[50:51], off nt
	global_load_dword v67, v[52:53], off nt
	global_load_dword v68, v[54:55], off nt
	global_load_dword v69, v[56:57], off nt
	global_load_dword v70, v[58:59], off nt
	global_load_dword v71, v[60:61], off nt
	v_add_co_u32_e32 v48, vcc, 0x10000, v46
	s_nop 1
	v_addc_co_u32_e32 v49, vcc, 0, v47, vcc
	v_add_co_u32_e32 v50, vcc, 0x12000, v46
	s_nop 1
	v_addc_co_u32_e32 v51, vcc, 0, v47, vcc
	v_add_co_u32_e32 v52, vcc, 0x14000, v46
	s_nop 1
	v_addc_co_u32_e32 v53, vcc, 0, v47, vcc
	v_add_co_u32_e32 v54, vcc, 0x16000, v46
	s_nop 1
	v_addc_co_u32_e32 v55, vcc, 0, v47, vcc
	v_add_co_u32_e32 v56, vcc, 0x18000, v46
	s_nop 1
	v_addc_co_u32_e32 v57, vcc, 0, v47, vcc
	v_add_co_u32_e32 v58, vcc, 0x1a000, v46
	s_nop 1
	v_addc_co_u32_e32 v59, vcc, 0, v47, vcc
	v_add_co_u32_e32 v60, vcc, 0x1c000, v46
	s_nop 1
	v_addc_co_u32_e32 v61, vcc, 0, v47, vcc
	v_add_co_u32_e32 v62, vcc, 0x1e000, v46
	s_nop 1
	v_addc_co_u32_e32 v63, vcc, 0, v47, vcc
	global_load_dword v72, v[48:49], off nt
	global_load_dword v73, v[50:51], off nt
	global_load_dword v74, v[52:53], off nt
	global_load_dword v75, v[54:55], off nt
	global_load_dword v76, v[56:57], off nt
	global_load_dword v77, v[58:59], off nt
	global_load_dword v78, v[60:61], off nt
	global_load_dword v79, v[62:63], off nt
	v_add_co_u32_e32 v48, vcc, 0x20000, v46
	s_nop 1
	v_addc_co_u32_e32 v49, vcc, 0, v47, vcc
	v_add_co_u32_e32 v50, vcc, 0x22000, v46
	s_nop 1
	v_addc_co_u32_e32 v51, vcc, 0, v47, vcc
	v_add_co_u32_e32 v52, vcc, 0x24000, v46
	s_nop 1
	v_addc_co_u32_e32 v53, vcc, 0, v47, vcc
	v_add_co_u32_e32 v54, vcc, 0x26000, v46
	s_nop 1
	v_addc_co_u32_e32 v55, vcc, 0, v47, vcc
	v_add_co_u32_e32 v56, vcc, 0x28000, v46
	s_nop 1
	v_addc_co_u32_e32 v57, vcc, 0, v47, vcc
	v_add_co_u32_e32 v58, vcc, 0x2a000, v46
	s_nop 1
	v_addc_co_u32_e32 v59, vcc, 0, v47, vcc
	v_add_co_u32_e32 v60, vcc, 0x2c000, v46
	s_nop 1
	v_addc_co_u32_e32 v61, vcc, 0, v47, vcc
	v_add_co_u32_e32 v62, vcc, 0x2e000, v46
	s_nop 1
	v_addc_co_u32_e32 v63, vcc, 0, v47, vcc
	global_load_dword v80, v[48:49], off nt
	global_load_dword v81, v[50:51], off nt
	global_load_dword v82, v[52:53], off nt
	global_load_dword v83, v[54:55], off nt
	global_load_dword v84, v[56:57], off nt
	global_load_dword v85, v[58:59], off nt
	global_load_dword v86, v[60:61], off nt
	s_nop 0
	global_load_dword v62, v[62:63], off nt
	v_add_co_u32_e32 v48, vcc, 0x30000, v46
	s_nop 1
	v_addc_co_u32_e32 v49, vcc, 0, v47, vcc
	v_add_co_u32_e32 v50, vcc, 0x32000, v46
	s_nop 1
	v_addc_co_u32_e32 v51, vcc, 0, v47, vcc
	v_add_co_u32_e32 v52, vcc, 0x34000, v46
	s_nop 1
	v_addc_co_u32_e32 v53, vcc, 0, v47, vcc
	v_add_co_u32_e32 v54, vcc, 0x36000, v46
	s_nop 1
	v_addc_co_u32_e32 v55, vcc, 0, v47, vcc
	v_add_co_u32_e32 v56, vcc, 0x38000, v46
	s_nop 1
	v_addc_co_u32_e32 v57, vcc, 0, v47, vcc
	v_add_co_u32_e32 v58, vcc, 0x3a000, v46
	s_nop 1
	v_addc_co_u32_e32 v59, vcc, 0, v47, vcc
	v_add_co_u32_e32 v60, vcc, 0x3c000, v46
	s_nop 1
	v_addc_co_u32_e32 v61, vcc, 0, v47, vcc
	v_add_co_u32_e32 v46, vcc, 0x3e000, v46
	s_nop 1
	v_addc_co_u32_e32 v47, vcc, 0, v47, vcc
	global_load_dword v48, v[48:49], off nt
	s_nop 0
	global_load_dword v49, v[50:51], off nt
	s_nop 0
	global_load_dword v50, v[52:53], off nt
	global_load_dword v51, v[54:55], off nt
	s_nop 0
	global_load_dword v52, v[56:57], off nt
	global_load_dword v53, v[58:59], off nt
	global_load_dword v54, v[60:61], off nt
	s_nop 0
	global_load_dword v46, v[46:47], off nt
	s_waitcnt vmcnt(30)
	ds_write2_b32 v29, v64, v65 offset1:66
	s_waitcnt vmcnt(28)
	ds_write2_b32 v29, v66, v67 offset0:132 offset1:198
	s_waitcnt vmcnt(26)
	ds_write2_b32 v38, v68, v69 offset0:8 offset1:74
	s_waitcnt vmcnt(24)
	ds_write2_b32 v38, v70, v71 offset0:140 offset1:206
	s_waitcnt vmcnt(22)
	ds_write2_b32 v39, v72, v73 offset0:16 offset1:82
	s_waitcnt vmcnt(20)
	ds_write2_b32 v39, v74, v75 offset0:148 offset1:214
	s_waitcnt vmcnt(18)
	ds_write2_b32 v40, v76, v77 offset0:24 offset1:90
	s_waitcnt vmcnt(16)
	ds_write2_b32 v40, v78, v79 offset0:156 offset1:222
	s_waitcnt vmcnt(14)
	ds_write2_b32 v41, v80, v81 offset0:32 offset1:98
	s_waitcnt vmcnt(12)
	ds_write2_b32 v41, v82, v83 offset0:164 offset1:230
	s_waitcnt vmcnt(10)
; #define GAS __attribute__((address_space(1)))
; #define LAS __attribute__((address_space(3)))
; #define LDS_WAIT() asm volatile("s_waitcnt lgkmcnt(0)" ::: "memory")
; __device__ __forceinline__ unsigned pk2(float lo, float hi) { return f2bf(lo) | (f2bf(hi) << 16); }
; __device__ __forceinline__ void tr_item(const float* W, int ld, int K, int nblk, int item, bf16* WT, bool gu, LAS float* scr, int lane) {
;     ...
;       for (int i = 0; i < 32; ++i) scr[(2 * i + (lane >> 5)) * 33 + (lane & 31)] = t_[i]; }
;     LDS_WAIT(); asm volatile("" ::: "memory");
;     const int c = lane & 7;
; #pragma unroll
;     for (int j = 0; j < 4; ++j) { const int n = (lane >> 3) + 8 * j; const LAS float* s = scr + (8 * c) * 33 + n;
;         v4u o; o.x = pk2(s[0 * 33], s[1 * 33]); o.y = pk2(s[2 * 33], s[3 * 33]); o.z = pk2(s[4 * 33], s[5 * 33]); o.w = pk2(s[6 * 33], s[7 * 33]);
;         *(GAS v4u*)(WT + (size_t)(drow0 + n) * K + k0 + 8 * c) = o; }
;     LDS_WAIT(); asm volatile("" ::: "memory");
	ds_write2_b32 v42, v84, v85 offset0:40 offset1:106
	s_waitcnt vmcnt(8)
	ds_write2_b32 v42, v86, v62 offset0:172 offset1:238
	s_waitcnt vmcnt(6)
	ds_write2_b32 v43, v48, v49 offset0:48 offset1:114
	s_waitcnt vmcnt(4)
	ds_write2_b32 v43, v50, v51 offset0:180 offset1:246
	s_waitcnt vmcnt(2)
	ds_write2_b32 v44, v52, v53 offset0:56 offset1:122
	s_waitcnt vmcnt(0)
	ds_write2_b32 v44, v54, v46 offset0:188 offset1:254
	s_waitcnt lgkmcnt(0)
	ds_read2_b32 v[50:51], v34 offset1:8
	ds_read2_b32 v[54:55], v34 offset0:33 offset1:41
	ds_read2_b32 v[56:57], v34 offset0:66 offset1:74
	ds_read2_b32 v[58:59], v34 offset0:99 offset1:107
	ds_read2_b32 v[60:61], v34 offset0:132 offset1:140
	s_waitcnt lgkmcnt(4)
	v_bfe_u32 v46, v50, 16, 1
	v_add3_u32 v46, v50, v46, s22
	s_waitcnt lgkmcnt(3)
	v_bfe_u32 v47, v54, 16, 1
	v_lshrrev_b32_e32 v46, 16, v46
	v_add3_u32 v47, v54, v47, s22
	ds_read2_b32 v[62:63], v34 offset0:165 offset1:173
	v_and_or_b32 v46, v47, s23, v46
	s_waitcnt lgkmcnt(3)
	v_bfe_u32 v47, v56, 16, 1
	v_add3_u32 v47, v56, v47, s22
	s_waitcnt lgkmcnt(2)
	v_bfe_u32 v48, v58, 16, 1
	ds_read2_b32 v[64:65], v34 offset0:198 offset1:206
	v_lshrrev_b32_e32 v47, 16, v47
	v_add3_u32 v48, v58, v48, s22
	ds_read2_b32 v[66:67], v34 offset0:231 offset1:239
	v_and_or_b32 v47, v48, s23, v47
	s_waitcnt lgkmcnt(3)
	v_bfe_u32 v48, v60, 16, 1
	v_add3_u32 v48, v60, v48, s22
	s_waitcnt lgkmcnt(2)
	v_bfe_u32 v49, v62, 16, 1
	v_lshrrev_b32_e32 v48, 16, v48
	v_add3_u32 v49, v62, v49, s22
	v_and_or_b32 v48, v49, s23, v48
	s_waitcnt lgkmcnt(1)
	v_bfe_u32 v49, v64, 16, 1
	v_add_u32_e32 v68, s10, v33
	v_add3_u32 v49, v64, v49, s22
	s_waitcnt lgkmcnt(0)
	v_bfe_u32 v50, v66, 16, 1
	v_ashrrev_i32_e32 v69, 31, v68
	v_lshl_add_u64 v[52:53], v[24:25], 0, s[0:1]
	v_lshrrev_b32_e32 v49, 16, v49
	v_add3_u32 v50, v66, v50, s22
	v_lshlrev_b64 v[68:69], 11, v[68:69]
	v_and_or_b32 v49, v50, s23, v49
	v_lshl_add_u64 v[68:69], v[52:53], 0, v[68:69]
	global_store_dwordx4 v[68:69], v[46:49], off
	v_bfe_u32 v50, v67, 16, 1
	v_add3_u32 v50, v67, v50, s22
	v_bfe_u32 v46, v51, 16, 1
	v_add3_u32 v46, v51, v46, s22
	v_bfe_u32 v47, v55, 16, 1
	v_lshrrev_b32_e32 v46, 16, v46
	v_add3_u32 v47, v55, v47, s22
	v_and_or_b32 v46, v47, s23, v46
	v_bfe_u32 v47, v57, 16, 1
	v_add3_u32 v47, v57, v47, s22
	v_bfe_u32 v48, v59, 16, 1
	v_lshrrev_b32_e32 v47, 16, v47
	v_add3_u32 v48, v59, v48, s22
	v_and_or_b32 v47, v48, s23, v47
	v_bfe_u32 v48, v61, 16, 1
	v_add3_u32 v48, v61, v48, s22
	v_bfe_u32 v49, v63, 16, 1
	v_lshrrev_b32_e32 v48, 16, v48
	v_add3_u32 v49, v63, v49, s22
	v_and_or_b32 v48, v49, s23, v48
	v_bfe_u32 v49, v65, 16, 1
	v_add3_u32 v49, v65, v49, s22
	v_lshrrev_b32_e32 v49, 16, v49
	v_and_or_b32 v49, v50, s23, v49
	v_add_u32_e32 v50, s10, v35
	v_ashrrev_i32_e32 v51, 31, v50
	v_lshlrev_b64 v[50:51], 11, v[50:51]
	ds_read2_b32 v[54:55], v34 offset0:16 offset1:24
	v_lshl_add_u64 v[50:51], v[52:53], 0, v[50:51]
	global_store_dwordx4 v[50:51], v[46:49], off
	ds_read2_b32 v[50:51], v34 offset0:49 offset1:57
	ds_read2_b32 v[56:57], v34 offset0:82 offset1:90
	ds_read2_b32 v[58:59], v34 offset0:115 offset1:123
	s_waitcnt lgkmcnt(3)
	v_bfe_u32 v46, v54, 16, 1
	v_add3_u32 v46, v54, v46, s22
	s_waitcnt lgkmcnt(2)
	v_bfe_u32 v47, v50, 16, 1
	ds_read2_b32 v[60:61], v34 offset0:148 offset1:156
	v_lshrrev_b32_e32 v46, 16, v46
	v_add3_u32 v47, v50, v47, s22
	ds_read2_b32 v[62:63], v34 offset0:181 offset1:189
	v_and_or_b32 v46, v47, s23, v46
	s_waitcnt lgkmcnt(3)
	v_bfe_u32 v47, v56, 16, 1
	v_add3_u32 v47, v56, v47, s22
	s_waitcnt lgkmcnt(2)
	v_bfe_u32 v48, v58, 16, 1
	ds_read2_b32 v[64:65], v34 offset0:214 offset1:222
	v_lshrrev_b32_e32 v47, 16, v47
	v_add3_u32 v48, v58, v48, s22
	ds_read2_b32 v[66:67], v34 offset0:247 offset1:255
	v_and_or_b32 v47, v48, s23, v47
	s_waitcnt lgkmcnt(3)
	v_bfe_u32 v48, v60, 16, 1
	v_add3_u32 v48, v60, v48, s22
	s_waitcnt lgkmcnt(2)
	v_bfe_u32 v49, v62, 16, 1
	v_lshrrev_b32_e32 v48, 16, v48
	v_add3_u32 v49, v62, v49, s22
	v_and_or_b32 v48, v49, s23, v48
	s_waitcnt lgkmcnt(1)
	v_bfe_u32 v49, v64, 16, 1
	v_add_u32_e32 v68, s10, v36
	v_add3_u32 v49, v64, v49, s22
	s_waitcnt lgkmcnt(0)
	v_bfe_u32 v50, v66, 16, 1
	v_ashrrev_i32_e32 v69, 31, v68
	v_lshrrev_b32_e32 v49, 16, v49
	v_add3_u32 v50, v66, v50, s22
	v_lshlrev_b64 v[68:69], 11, v[68:69]
	v_and_or_b32 v49, v50, s23, v49
	v_lshl_add_u64 v[68:69], v[52:53], 0, v[68:69]
	global_store_dwordx4 v[68:69], v[46:49], off
	v_bfe_u32 v50, v67, 16, 1
	v_add3_u32 v50, v67, v50, s22
	v_bfe_u32 v46, v55, 16, 1
	v_add3_u32 v46, v55, v46, s22
	v_bfe_u32 v47, v51, 16, 1
	v_lshrrev_b32_e32 v46, 16, v46
	v_add3_u32 v47, v51, v47, s22
	v_and_or_b32 v46, v47, s23, v46
	v_bfe_u32 v47, v57, 16, 1
	v_add3_u32 v47, v57, v47, s22
	v_bfe_u32 v48, v59, 16, 1
	v_lshrrev_b32_e32 v47, 16, v47
	v_add3_u32 v48, v59, v48, s22
	v_and_or_b32 v47, v48, s23, v47
	v_bfe_u32 v48, v61, 16, 1
	v_add3_u32 v48, v61, v48, s22
	v_bfe_u32 v49, v63, 16, 1
	v_lshrrev_b32_e32 v48, 16, v48
	v_add3_u32 v49, v63, v49, s22
	v_and_or_b32 v48, v49, s23, v48
	v_bfe_u32 v49, v65, 16, 1
	v_add3_u32 v49, v65, v49, s22
	v_lshrrev_b32_e32 v49, 16, v49
	v_and_or_b32 v49, v50, s23, v49
	v_add_u32_e32 v50, s10, v37
	v_ashrrev_i32_e32 v51, 31, v50
	v_lshlrev_b64 v[50:51], 11, v[50:51]
	v_lshl_add_u64 v[50:51], v[52:53], 0, v[50:51]
	global_store_dwordx4 v[50:51], v[46:49], off
	s_waitcnt lgkmcnt(0)

; __device__ __forceinline__ void tr_item(const float* W, int ld, int K, int nblk, int item, bf16* WT, bool gu, LAS float* scr, int lane) {
;     ...
;       for (int i = 0; i < 32; ++i) t_[i] = W[(size_t)(k0 + 2 * i + (lane >> 5)) * ld + n0 + (lane & 31)];
; #pragma unroll
;       for (int i = 0; i < 32; ++i) scr[(2 * i + (lane >> 5)) * 33 + (lane & 31)] = t_[i]; }
; __device__ __forceinline__ void convert_items(Frame& F, const Args& a, int lo, int hi, int w, int nw) {
;     ...
;         if (r < I_FI) { tr_item(a.in[7], 3 * D + 16, D, 96, r, (bf16*)(F.ws + WS_WFOXIN), false, scr, lane); continue; } r -= I_FI;
.LBB0_57:
	s_andn2_b64 vcc, exec, s[10:11]
	s_cbranch_vccnz .LBB0_34
	s_mul_hi_i32 s0, s14, 0x2aaaaaab
	s_lshr_b32 s10, s0, 31
	s_ashr_i32 s0, s0, 4
	s_add_i32 s0, s0, s10
	s_lshl_b32 s12, s0, 6
	s_mulk_i32 s0, 0xf400
	s_add_i32 s10, s16, s0
	v_add_u32_e32 v64, s12, v28
	s_ashr_i32 s11, s10, 31
	v_lshl_add_u64 v[46:47], s[10:11], 2, v[12:13]
	v_add_u32_e32 v50, 2, v64
	v_add_u32_e32 v52, 4, v64
	v_add_u32_e32 v54, 6, v64
	v_add_u32_e32 v56, 8, v64
	v_add_u32_e32 v58, 10, v64
	v_add_u32_e32 v60, 12, v64
	v_add_u32_e32 v62, 14, v64
	v_mad_i64_i32 v[48:49], s[26:27], v64, s25, v[46:47]
	v_mad_i64_i32 v[50:51], s[26:27], v50, s25, v[46:47]
	v_mad_i64_i32 v[52:53], s[26:27], v52, s25, v[46:47]
	v_mad_i64_i32 v[54:55], s[26:27], v54, s25, v[46:47]
	v_mad_i64_i32 v[56:57], s[26:27], v56, s25, v[46:47]
	v_mad_i64_i32 v[58:59], s[26:27], v58, s25, v[46:47]
	v_mad_i64_i32 v[60:61], s[26:27], v60, s25, v[46:47]
	v_mad_i64_i32 v[62:63], s[26:27], v62, s25, v[46:47]
	global_load_dword v65, v[48:49], off nt
	global_load_dword v66, v[50:51], off nt
	global_load_dword v67, v[52:53], off nt
	global_load_dword v68, v[54:55], off nt
	global_load_dword v69, v[56:57], off nt
	global_load_dword v70, v[58:59], off nt
	global_load_dword v71, v[60:61], off nt
	global_load_dword v72, v[62:63], off nt
	v_add_u32_e32 v48, 16, v64
	v_add_u32_e32 v50, 18, v64
	v_add_u32_e32 v52, 20, v64
	v_add_u32_e32 v54, 22, v64
	v_add_u32_e32 v56, 24, v64
	v_add_u32_e32 v58, 26, v64
	v_add_u32_e32 v60, 28, v64
	v_add_u32_e32 v62, 30, v64
	v_mad_i64_i32 v[48:49], s[26:27], v48, s25, v[46:47]
	v_mad_i64_i32 v[50:51], s[26:27], v50, s25, v[46:47]
	v_mad_i64_i32 v[52:53], s[26:27], v52, s25, v[46:47]
	v_mad_i64_i32 v[54:55], s[26:27], v54, s25, v[46:47]
	v_mad_i64_i32 v[56:57], s[26:27], v56, s25, v[46:47]
	v_mad_i64_i32 v[58:59], s[26:27], v58, s25, v[46:47]
	v_mad_i64_i32 v[60:61], s[26:27], v60, s25, v[46:47]
	v_mad_i64_i32 v[62:63], s[26:27], v62, s25, v[46:47]
	global_load_dword v73, v[48:49], off nt
	global_load_dword v74, v[50:51], off nt
	global_load_dword v75, v[52:53], off nt
	global_load_dword v76, v[54:55], off nt
	global_load_dword v77, v[56:57], off nt
	global_load_dword v78, v[58:59], off nt
	global_load_dword v79, v[60:61], off nt
	global_load_dword v80, v[62:63], off nt
	v_add_u32_e32 v48, 32, v64
	v_add_u32_e32 v50, 34, v64
	v_add_u32_e32 v52, 36, v64
	v_add_u32_e32 v54, 38, v64
	v_add_u32_e32 v56, 40, v64
	v_add_u32_e32 v58, 42, v64
	v_add_u32_e32 v60, 44, v64
	v_add_u32_e32 v62, 46, v64
	v_mad_i64_i32 v[48:49], s[26:27], v48, s25, v[46:47]
	v_mad_i64_i32 v[50:51], s[26:27], v50, s25, v[46:47]
	v_mad_i64_i32 v[52:53], s[26:27], v52, s25, v[46:47]
	v_mad_i64_i32 v[54:55], s[26:27], v54, s25, v[46:47]
	v_mad_i64_i32 v[56:57], s[26:27], v56, s25, v[46:47]
	v_mad_i64_i32 v[58:59], s[26:27], v58, s25, v[46:47]
	v_mad_i64_i32 v[60:61], s[26:27], v60, s25, v[46:47]
	v_mad_i64_i32 v[62:63], s[26:27], v62, s25, v[46:47]
	global_load_dword v81, v[48:49], off nt
	global_load_dword v82, v[50:51], off nt
	global_load_dword v83, v[52:53], off nt
	global_load_dword v84, v[54:55], off nt
	global_load_dword v85, v[56:57], off nt
	global_load_dword v86, v[58:59], off nt
	global_load_dword v87, v[60:61], off nt
	s_nop 0
	global_load_dword v62, v[62:63], off nt
	v_add_u32_e32 v48, 48, v64
	v_add_u32_e32 v50, 50, v64
	v_add_u32_e32 v52, 52, v64
	v_add_u32_e32 v54, 54, v64
	v_add_u32_e32 v56, 56, v64
	v_add_u32_e32 v58, 58, v64
	v_add_u32_e32 v60, 60, v64
	v_add_u32_e32 v63, 62, v64
	v_mad_i64_i32 v[48:49], s[26:27], v48, s25, v[46:47]
	v_mad_i64_i32 v[50:51], s[26:27], v50, s25, v[46:47]
	v_mad_i64_i32 v[52:53], s[26:27], v52, s25, v[46:47]
	v_mad_i64_i32 v[54:55], s[26:27], v54, s25, v[46:47]
	v_mad_i64_i32 v[56:57], s[26:27], v56, s25, v[46:47]
	v_mad_i64_i32 v[58:59], s[26:27], v58, s25, v[46:47]
	v_mad_i64_i32 v[60:61], s[26:27], v60, s25, v[46:47]
	v_mad_i64_i32 v[46:47], s[26:27], v63, s25, v[46:47]
	global_load_dword v48, v[48:49], off nt
	s_nop 0
	global_load_dword v49, v[50:51], off nt
	s_nop 0
	global_load_dword v50, v[52:53], off nt
	global_load_dword v51, v[54:55], off nt
	s_nop 0
	global_load_dword v52, v[56:57], off nt
	global_load_dword v53, v[58:59], off nt
	global_load_dword v54, v[60:61], off nt
	s_nop 0
	global_load_dword v46, v[46:47], off nt
	s_waitcnt vmcnt(30)
	ds_write2_b32 v29, v65, v66 offset1:66
	s_waitcnt vmcnt(28)
	ds_write2_b32 v29, v67, v68 offset0:132 offset1:198
	s_waitcnt vmcnt(26)
	ds_write2_b32 v38, v69, v70 offset0:8 offset1:74
	s_waitcnt vmcnt(24)
	ds_write2_b32 v38, v71, v72 offset0:140 offset1:206
	s_waitcnt vmcnt(22)
	ds_write2_b32 v39, v73, v74 offset0:16 offset1:82
	s_waitcnt vmcnt(20)
	ds_write2_b32 v39, v75, v76 offset0:148 offset1:214
	s_waitcnt vmcnt(18)
	ds_write2_b32 v40, v77, v78 offset0:24 offset1:90
	s_waitcnt vmcnt(16)
	ds_write2_b32 v40, v79, v80 offset0:156 offset1:222
	s_waitcnt vmcnt(14)
	ds_write2_b32 v41, v81, v82 offset0:32 offset1:98
	s_waitcnt vmcnt(12)
	ds_write2_b32 v41, v83, v84 offset0:164 offset1:230
	s_waitcnt vmcnt(10)
	ds_write2_b32 v42, v85, v86 offset0:40 offset1:106
	s_waitcnt vmcnt(8)
	ds_write2_b32 v42, v87, v62 offset0:172 offset1:238
	s_waitcnt vmcnt(6)
; #define GAS __attribute__((address_space(1)))
; #define LAS __attribute__((address_space(3)))
; #define LDS_WAIT() asm volatile("s_waitcnt lgkmcnt(0)" ::: "memory")
; __device__ __forceinline__ unsigned pk2(float lo, float hi) { return f2bf(lo) | (f2bf(hi) << 16); }
; __device__ __forceinline__ void tr_item(const float* W, int ld, int K, int nblk, int item, bf16* WT, bool gu, LAS float* scr, int lane) {
;     ...
;       for (int i = 0; i < 32; ++i) scr[(2 * i + (lane >> 5)) * 33 + (lane & 31)] = t_[i]; }
;     LDS_WAIT(); asm volatile("" ::: "memory");
;     const int c = lane & 7;
; #pragma unroll
;     for (int j = 0; j < 4; ++j) { const int n = (lane >> 3) + 8 * j; const LAS float* s = scr + (8 * c) * 33 + n;
;         v4u o; o.x = pk2(s[0 * 33], s[1 * 33]); o.y = pk2(s[2 * 33], s[3 * 33]); o.z = pk2(s[4 * 33], s[5 * 33]); o.w = pk2(s[6 * 33], s[7 * 33]);
;         *(GAS v4u*)(WT + (size_t)(drow0 + n) * K + k0 + 8 * c) = o; }
;     LDS_WAIT(); asm volatile("" ::: "memory");
	ds_write2_b32 v43, v48, v49 offset0:48 offset1:114
	s_waitcnt vmcnt(4)
	ds_write2_b32 v43, v50, v51 offset0:180 offset1:246
	s_waitcnt vmcnt(2)
	ds_write2_b32 v44, v52, v53 offset0:56 offset1:122
	s_waitcnt vmcnt(0)
	ds_write2_b32 v44, v54, v46 offset0:188 offset1:254
	s_waitcnt lgkmcnt(0)
	ds_read2_b32 v[50:51], v34 offset1:8
	ds_read2_b32 v[54:55], v34 offset0:33 offset1:41
	ds_read2_b32 v[56:57], v34 offset0:66 offset1:74
	ds_read2_b32 v[58:59], v34 offset0:99 offset1:107
	ds_read2_b32 v[60:61], v34 offset0:132 offset1:140
	s_waitcnt lgkmcnt(4)
	v_bfe_u32 v46, v50, 16, 1
	v_add3_u32 v46, v50, v46, s22
	s_waitcnt lgkmcnt(3)
	v_bfe_u32 v47, v54, 16, 1
	v_lshrrev_b32_e32 v46, 16, v46
	v_add3_u32 v47, v54, v47, s22
	ds_read2_b32 v[62:63], v34 offset0:165 offset1:173
	v_and_or_b32 v46, v47, s23, v46
	s_waitcnt lgkmcnt(3)
	v_bfe_u32 v47, v56, 16, 1
	v_add3_u32 v47, v56, v47, s22
	s_waitcnt lgkmcnt(2)
	v_bfe_u32 v48, v58, 16, 1
	ds_read2_b32 v[64:65], v34 offset0:198 offset1:206
	v_lshrrev_b32_e32 v47, 16, v47
	v_add3_u32 v48, v58, v48, s22
	ds_read2_b32 v[66:67], v34 offset0:231 offset1:239
	v_and_or_b32 v47, v48, s23, v47
	s_waitcnt lgkmcnt(3)
	v_bfe_u32 v48, v60, 16, 1
	v_add3_u32 v48, v60, v48, s22
	s_waitcnt lgkmcnt(2)
	v_bfe_u32 v49, v62, 16, 1
	v_lshrrev_b32_e32 v48, 16, v48
	v_add3_u32 v49, v62, v49, s22
	v_and_or_b32 v48, v49, s23, v48
	s_waitcnt lgkmcnt(1)
	v_bfe_u32 v49, v64, 16, 1
	v_add_u32_e32 v68, s10, v33
	s_ashr_i32 s13, s12, 31
	v_add3_u32 v49, v64, v49, s22
	s_waitcnt lgkmcnt(0)
	v_bfe_u32 v50, v66, 16, 1
	v_ashrrev_i32_e32 v69, 31, v68
	v_lshl_add_u64 v[52:53], s[12:13], 1, v[26:27]
	v_lshrrev_b32_e32 v49, 16, v49
	v_add3_u32 v50, v66, v50, s22
	v_lshlrev_b64 v[70:71], 11, v[68:69]
	v_and_or_b32 v49, v50, s23, v49
	v_lshl_add_u64 v[70:71], v[52:53], 0, v[70:71]
	global_store_dwordx4 v[70:71], v[46:49], off
	v_bfe_u32 v50, v67, 16, 1
	v_add3_u32 v50, v67, v50, s22
	v_bfe_u32 v46, v51, 16, 1
	v_add3_u32 v46, v51, v46, s22
	v_bfe_u32 v47, v55, 16, 1
	v_lshrrev_b32_e32 v46, 16, v46
	v_add3_u32 v47, v55, v47, s22
	v_and_or_b32 v46, v47, s23, v46
	v_bfe_u32 v47, v57, 16, 1
	v_add3_u32 v47, v57, v47, s22
	v_bfe_u32 v48, v59, 16, 1
	v_lshrrev_b32_e32 v47, 16, v47
	v_add3_u32 v48, v59, v48, s22
	v_and_or_b32 v47, v48, s23, v47
	v_bfe_u32 v48, v61, 16, 1
	v_add3_u32 v48, v61, v48, s22
	v_bfe_u32 v49, v63, 16, 1
	v_lshrrev_b32_e32 v48, 16, v48
	v_add3_u32 v49, v63, v49, s22
	v_and_or_b32 v48, v49, s23, v48
	v_bfe_u32 v49, v65, 16, 1
	v_add3_u32 v49, v65, v49, s22
	v_lshrrev_b32_e32 v49, 16, v49
	v_and_or_b32 v49, v50, s23, v49
	v_add_u32_e32 v50, 8, v68
	v_ashrrev_i32_e32 v51, 31, v50
	v_lshlrev_b64 v[50:51], 11, v[50:51]
	ds_read2_b32 v[54:55], v34 offset0:16 offset1:24
	v_lshl_add_u64 v[50:51], v[52:53], 0, v[50:51]
	global_store_dwordx4 v[50:51], v[46:49], off
	ds_read2_b32 v[50:51], v34 offset0:49 offset1:57
	ds_read2_b32 v[56:57], v34 offset0:82 offset1:90
	ds_read2_b32 v[58:59], v34 offset0:115 offset1:123
	s_waitcnt lgkmcnt(3)
	v_bfe_u32 v46, v54, 16, 1
	v_add3_u32 v46, v54, v46, s22
	s_waitcnt lgkmcnt(2)
	v_bfe_u32 v47, v50, 16, 1
	ds_read2_b32 v[60:61], v34 offset0:148 offset1:156
	v_lshrrev_b32_e32 v46, 16, v46
	v_add3_u32 v47, v50, v47, s22
	ds_read2_b32 v[62:63], v34 offset0:181 offset1:189
	v_and_or_b32 v46, v47, s23, v46
	s_waitcnt lgkmcnt(3)
	v_bfe_u32 v47, v56, 16, 1
	v_add3_u32 v47, v56, v47, s22
	s_waitcnt lgkmcnt(2)
	v_bfe_u32 v48, v58, 16, 1
	ds_read2_b32 v[64:65], v34 offset0:214 offset1:222
	v_lshrrev_b32_e32 v47, 16, v47
	v_add3_u32 v48, v58, v48, s22
	ds_read2_b32 v[66:67], v34 offset0:247 offset1:255
	v_and_or_b32 v47, v48, s23, v47
	s_waitcnt lgkmcnt(3)
	v_bfe_u32 v48, v60, 16, 1
	v_add3_u32 v48, v60, v48, s22
	s_waitcnt lgkmcnt(2)
	v_bfe_u32 v49, v62, 16, 1
	v_lshrrev_b32_e32 v48, 16, v48
	v_add3_u32 v49, v62, v49, s22
	v_and_or_b32 v48, v49, s23, v48
	s_waitcnt lgkmcnt(1)
	v_bfe_u32 v49, v64, 16, 1
	v_add_u32_e32 v70, 16, v68
	v_add3_u32 v49, v64, v49, s22
	s_waitcnt lgkmcnt(0)
	v_bfe_u32 v50, v66, 16, 1
	v_ashrrev_i32_e32 v71, 31, v70
	v_lshrrev_b32_e32 v49, 16, v49
	v_add3_u32 v50, v66, v50, s22
	v_lshlrev_b64 v[70:71], 11, v[70:71]
	v_and_or_b32 v49, v50, s23, v49
	v_lshl_add_u64 v[70:71], v[52:53], 0, v[70:71]
	global_store_dwordx4 v[70:71], v[46:49], off
	v_bfe_u32 v50, v67, 16, 1
	v_add3_u32 v50, v67, v50, s22
	v_bfe_u32 v46, v55, 16, 1
	v_add3_u32 v46, v55, v46, s22
	v_bfe_u32 v47, v51, 16, 1
	v_lshrrev_b32_e32 v46, 16, v46
	v_add3_u32 v47, v51, v47, s22
	v_and_or_b32 v46, v47, s23, v46
	v_bfe_u32 v47, v57, 16, 1
	v_add3_u32 v47, v57, v47, s22
	v_bfe_u32 v48, v59, 16, 1
	v_lshrrev_b32_e32 v47, 16, v47
	v_add3_u32 v48, v59, v48, s22
	v_and_or_b32 v47, v48, s23, v47
	v_bfe_u32 v48, v61, 16, 1
	v_add3_u32 v48, v61, v48, s22
	v_bfe_u32 v49, v63, 16, 1
	v_lshrrev_b32_e32 v48, 16, v48
	v_add3_u32 v49, v63, v49, s22
	v_and_or_b32 v48, v49, s23, v48
	v_bfe_u32 v49, v65, 16, 1
	v_add3_u32 v49, v65, v49, s22
	v_lshrrev_b32_e32 v49, 16, v49
	v_and_or_b32 v49, v50, s23, v49
	v_add_u32_e32 v50, 24, v68
	v_ashrrev_i32_e32 v51, 31, v50
	v_lshlrev_b64 v[50:51], 11, v[50:51]
	v_lshl_add_u64 v[50:51], v[52:53], 0, v[50:51]
	global_store_dwordx4 v[50:51], v[46:49], off
	s_waitcnt lgkmcnt(0)
	s_branch .LBB0_34

; __device__ __forceinline__ void tr_item8(const float* W, int ld, int K, int nblk, int item, unsigned char* WT, bool gu, float scale, LAS float* scr, int lane) {
;     ...
;     { float t_[32];
; #pragma unroll
;       for (int i = 0; i < 32; ++i) t_[i] = W[(size_t)(k0 + 2 * i + (lane >> 5)) * ld + n0 + (lane & 31)];
; #pragma unroll
;       for (int i = 0; i < 32; ++i) scr[(2 * i + (lane >> 5)) * 33 + (lane & 31)] = t_[i] * scale; }
; __device__ __forceinline__ void convert_items(Frame& F, const Args& a, int lo, int hi, int w, int nw) {
;     ...
;     for (int it = lo + w; it < hi; it += nw) {
;         int r = it;
;         if (r < I_FI) { tr_item(a.in[7], 3 * D + 16, D, 96, r, (bf16*)(F.ws + WS_WFOXIN), false, scr, lane); continue; } r -= I_FI;
;         if (r < I_FO) { tr_item(a.in[9], D, D, 32, r, (bf16*)(F.ws + WS_WFOXOUT), false, scr, lane); continue; } r -= I_FO;
;         if (r < I_SI) { tr_item(a.in[10], D + 512, D, 48, r, (bf16*)(F.ws + WS_WSWAIN), false, scr, lane); continue; } r -= I_SI;
;         if (r < I_SO) { tr_item(a.in[12], D, D, 32, r, (bf16*)(F.ws + WS_WSWAOUT), false, scr, lane); continue; } r -= I_SO;
;         if (r < I_GU) { tr_item8(a.in[14], 2 * FF, D, 224, r, F.ws + WS_WGU, true, WSC_GU, scr, lane); continue; } r -= I_GU;
;         if (r < I_DN) { tr_item8(a.in[15], D, FF, 32, r, F.ws + WS_WDN, false, WSC_DN, scr, lane); continue; } r -= I_DN;
;         if (r < NE * I_GU) { const int e = r / I_GU, rr = r % I_GU; tr_item8(a.in[18] + (size_t)e * D * 2 * FF, 2 * FF, D, 224, rr, F.ws + WS_WMGU + (size_t)e * 2 * FF * D, true, WSC_GU, scr, lane); continue; } r -= NE * I_GU;
.LBB0_559:
	s_cmpk_gt_i32 s3, 0x5ff
	s_mov_b64 s[4:5], -1
	s_cbranch_scc0 .LBB0_581
	s_cmpk_gt_u32 s3, 0x7ff
	s_cbranch_scc0 .LBB0_578
	s_cmpk_gt_u32 s3, 0xaff
	s_cbranch_scc0 .LBB0_575
	s_cmpk_gt_u32 s3, 0xcff
	s_cbranch_scc0 .LBB0_572
	s_cmpk_gt_u32 s3, 0x1aff
	s_cbranch_scc0 .LBB0_569
	s_cmpk_gt_u32 s3, 0x21ff
	s_cbranch_scc0 .LBB0_566
	s_add_i32 s0, s3, 0xde00
	s_bfe_u32 s4, s0, 0x70009
	s_mulk_i32 s4, 0x2493
	s_lshr_b32 s4, s4, 16
	s_mulk_i32 s4, 0xe00
	s_sub_i32 s0, s0, s4
	s_bfe_u32 s4, s0, 0xb0005
	s_mulk_i32 s4, 0x2493
	s_lshr_b32 s4, s4, 16
	s_mul_i32 s5, s4, 0xe0
	s_sub_i32 s0, s0, s5
	s_lshl_b32 s5, s0, 5
	s_and_b32 s6, s0, 0xffff
	s_cmpk_gt_u32 s6, 0x6f
	s_cselect_b32 s17, 0xfffff200, 0
	s_cselect_b32 s18, 0x80, 0
	s_lshl_b32 s0, s0, 7
	s_lshl_b32 s4, s4, 6
	s_and_b32 s0, s0, 0x3ff80
	v_add_u32_e32 v64, s4, v28
	v_lshl_add_u64 v[46:47], v[24:25], 0, s[0:1]
	v_mad_i64_i32 v[48:49], s[6:7], v64, s12, v[46:47]
	v_add_u32_e32 v50, 2, v64
	v_add_u32_e32 v52, 4, v64
	v_add_u32_e32 v54, 6, v64
	v_add_u32_e32 v56, 8, v64
	v_add_u32_e32 v58, 10, v64
	v_add_u32_e32 v60, 12, v64
	v_add_u32_e32 v62, 14, v64
	v_mad_i64_i32 v[50:51], s[6:7], v50, s12, v[46:47]
	v_mad_i64_i32 v[52:53], s[6:7], v52, s12, v[46:47]
	v_mad_i64_i32 v[54:55], s[6:7], v54, s12, v[46:47]
	v_mad_i64_i32 v[56:57], s[6:7], v56, s12, v[46:47]
	v_mad_i64_i32 v[58:59], s[6:7], v58, s12, v[46:47]
	v_mad_i64_i32 v[60:61], s[6:7], v60, s12, v[46:47]
	v_mad_i64_i32 v[62:63], s[6:7], v62, s12, v[46:47]
	global_load_dword v65, v[48:49], off nt
	global_load_dword v66, v[50:51], off nt
	global_load_dword v67, v[52:53], off nt
	global_load_dword v68, v[54:55], off nt
	global_load_dword v69, v[56:57], off nt
	global_load_dword v70, v[58:59], off nt
	global_load_dword v71, v[60:61], off nt
	global_load_dword v72, v[62:63], off nt
	v_add_u32_e32 v48, 16, v64
	v_mad_i64_i32 v[48:49], s[6:7], v48, s12, v[46:47]
	v_add_u32_e32 v50, 18, v64
	v_add_u32_e32 v52, 20, v64
	v_add_u32_e32 v54, 22, v64
	v_add_u32_e32 v56, 24, v64
	v_add_u32_e32 v58, 26, v64
	v_add_u32_e32 v60, 28, v64
	v_add_u32_e32 v62, 30, v64
	v_mad_i64_i32 v[50:51], s[6:7], v50, s12, v[46:47]
	v_mad_i64_i32 v[52:53], s[6:7], v52, s12, v[46:47]
	v_mad_i64_i32 v[54:55], s[6:7], v54, s12, v[46:47]
	v_mad_i64_i32 v[56:57], s[6:7], v56, s12, v[46:47]
	v_mad_i64_i32 v[58:59], s[6:7], v58, s12, v[46:47]
	v_mad_i64_i32 v[60:61], s[6:7], v60, s12, v[46:47]
	v_mad_i64_i32 v[62:63], s[6:7], v62, s12, v[46:47]
	global_load_dword v73, v[48:49], off nt
	global_load_dword v74, v[50:51], off nt
	global_load_dword v75, v[52:53], off nt
	global_load_dword v76, v[54:55], off nt
	global_load_dword v77, v[56:57], off nt
	global_load_dword v78, v[58:59], off nt
	global_load_dword v79, v[60:61], off nt
	global_load_dword v80, v[62:63], off nt
	v_add_u32_e32 v48, 32, v64
	v_add_u32_e32 v50, 34, v64
	v_add_u32_e32 v52, 36, v64
	v_add_u32_e32 v54, 38, v64
	v_add_u32_e32 v60, 44, v64
	v_mad_i64_i32 v[48:49], s[6:7], v48, s12, v[46:47]
	v_mad_i64_i32 v[50:51], s[6:7], v50, s12, v[46:47]
	v_mad_i64_i32 v[52:53], s[6:7], v52, s12, v[46:47]
	v_mad_i64_i32 v[54:55], s[6:7], v54, s12, v[46:47]
	v_add_u32_e32 v56, 40, v64
	v_add_u32_e32 v58, 42, v64
	v_mad_i64_i32 v[60:61], s[6:7], v60, s12, v[46:47]
	v_add_u32_e32 v62, 46, v64
	v_mad_i64_i32 v[56:57], s[6:7], v56, s12, v[46:47]
	v_mad_i64_i32 v[58:59], s[6:7], v58, s12, v[46:47]
	v_mad_i64_i32 v[62:63], s[6:7], v62, s12, v[46:47]
	global_load_dword v81, v[48:49], off nt
	global_load_dword v82, v[50:51], off nt
	global_load_dword v83, v[52:53], off nt
	global_load_dword v84, v[54:55], off nt
	global_load_dword v85, v[56:57], off nt
	global_load_dword v86, v[58:59], off nt
	s_nop 0
	global_load_dword v60, v[60:61], off nt
	s_nop 0
	global_load_dword v61, v[62:63], off nt
	v_add_u32_e32 v48, 48, v64
	v_add_u32_e32 v50, 50, v64
	v_add_u32_e32 v52, 52, v64
	v_add_u32_e32 v54, 54, v64
	v_mad_i64_i32 v[48:49], s[6:7], v48, s12, v[46:47]
	v_mad_i64_i32 v[50:51], s[6:7], v50, s12, v[46:47]
	v_mad_i64_i32 v[52:53], s[6:7], v52, s12, v[46:47]
	v_mad_i64_i32 v[54:55], s[6:7], v54, s12, v[46:47]
	v_add_u32_e32 v56, 56, v64
	v_add_u32_e32 v58, 58, v64
	v_mad_i64_i32 v[56:57], s[6:7], v56, s12, v[46:47]
	v_mad_i64_i32 v[58:59], s[6:7], v58, s12, v[46:47]
	global_load_dword v62, v[48:49], off nt
	s_nop 0
	global_load_dword v50, v[50:51], off nt
	s_nop 0
	global_load_dword v51, v[52:53], off nt
	s_nop 0
	global_load_dword v52, v[54:55], off nt
	global_load_dword v53, v[56:57], off nt
	s_nop 0
	global_load_dword v54, v[58:59], off nt
	v_add_u32_e32 v48, 60, v64
	v_add_u32_e32 v55, 62, v64
	v_mad_i64_i32 v[48:49], s[6:7], v48, s12, v[46:47]
	v_mad_i64_i32 v[46:47], s[6:7], v55, s12, v[46:47]
	global_load_dword v48, v[48:49], off nt
	s_nop 0
	global_load_dword v46, v[46:47], off nt
	s_waitcnt vmcnt(0)
; __device__ __forceinline__ unsigned cvt_pk4_fp8(float a, float b, float c, float d) { int w = 0; w = __builtin_amdgcn_cvt_pk_fp8_f32(a, b, w, false); w = __builtin_amdgcn_cvt_pk_fp8_f32(c, d, w, true); return (unsigned)w; }
; #define GAS __attribute__((address_space(1)))
; #define LAS __attribute__((address_space(3)))
; #define LDS_WAIT() asm volatile("s_waitcnt lgkmcnt(0)" ::: "memory")
; __device__ __forceinline__ void tr_item8(const float* W, int ld, int K, int nblk, int item, unsigned char* WT, bool gu, float scale, LAS float* scr, int lane) {
;     ...
;       for (int i = 0; i < 32; ++i) t_[i] = W[(size_t)(k0 + 2 * i + (lane >> 5)) * ld + n0 + (lane & 31)];
; #pragma unroll
;       for (int i = 0; i < 32; ++i) scr[(2 * i + (lane >> 5)) * 33 + (lane & 31)] = t_[i] * scale; }
;     LDS_WAIT(); asm volatile("" ::: "memory");
;     const int c = lane & 3;
; #pragma unroll
;     for (int j = 0; j < 2; ++j) { const int n = (lane >> 2) + 16 * j; const LAS float* sp = scr + (16 * c) * 33 + n;
;         v4u o; o.x = pg8::cvt_pk4_fp8(sp[0 * 33], sp[1 * 33], sp[2 * 33], sp[3 * 33]); o.y = pg8::cvt_pk4_fp8(sp[4 * 33], sp[5 * 33], sp[6 * 33], sp[7 * 33]);
;         o.z = pg8::cvt_pk4_fp8(sp[8 * 33], sp[9 * 33], sp[10 * 33], sp[11 * 33]); o.w = pg8::cvt_pk4_fp8(sp[12 * 33], sp[13 * 33], sp[14 * 33], sp[15 * 33]);
;         *(GAS v4u*)(WT + (size_t)(drow0 + n) * K + k0 + 16 * c) = o; }
;     LDS_WAIT(); asm volatile("" ::: "memory");
	v_mul_f32_e32 v47, 0x42800000, v65
	v_mul_f32_e32 v49, 0x42800000, v66
	ds_write2_b32 v29, v47, v49 offset1:66
	v_mul_f32_e32 v47, 0x42800000, v67
	v_mul_f32_e32 v49, 0x42800000, v68
	ds_write2_b32 v29, v47, v49 offset0:132 offset1:198
	v_mul_f32_e32 v47, 0x42800000, v69
	v_mul_f32_e32 v49, 0x42800000, v70
	ds_write2_b32 v38, v47, v49 offset0:8 offset1:74
	v_mul_f32_e32 v47, 0x42800000, v71
	v_mul_f32_e32 v49, 0x42800000, v72
	ds_write2_b32 v38, v47, v49 offset0:140 offset1:206
	s_add_i32 s0, s17, s5
	s_sext_i32_i16 s5, s0
	s_bfe_u32 s5, s5, 0x70018
	s_add_i32 s5, s0, s5
	s_sext_i32_i16 s6, s5
	s_and_b32 s5, s5, 0xff80
	s_sub_i32 s0, s0, s5
	s_lshl_b32 s6, s6, 1
	s_sext_i32_i16 s0, s0
	v_mul_f32_e32 v47, 0x42800000, v73
	v_mul_f32_e32 v49, 0x42800000, v74
	ds_write2_b32 v39, v47, v49 offset0:16 offset1:82
	v_mul_f32_e32 v47, 0x42800000, v75
	v_mul_f32_e32 v49, 0x42800000, v76
	ds_write2_b32 v39, v47, v49 offset0:148 offset1:214
	v_mul_f32_e32 v47, 0x42800000, v77
	v_mul_f32_e32 v49, 0x42800000, v78
	ds_write2_b32 v40, v47, v49 offset0:24 offset1:90
	v_mul_f32_e32 v47, 0x42800000, v79
	v_mul_f32_e32 v49, 0x42800000, v80
	ds_write2_b32 v40, v47, v49 offset0:156 offset1:222
	s_and_b32 s6, s6, 0xffffff00
	s_add_i32 s0, s18, s0
	s_add_i32 s0, s0, s6
	s_mov_b32 s5, s1
	v_mul_f32_e32 v47, 0x42800000, v81
	v_mul_f32_e32 v49, 0x42800000, v82
	ds_write2_b32 v41, v47, v49 offset0:32 offset1:98
	v_mul_f32_e32 v47, 0x42800000, v83
	v_mul_f32_e32 v49, 0x42800000, v84
	ds_write2_b32 v41, v47, v49 offset0:164 offset1:230
	v_mul_f32_e32 v47, 0x42800000, v85
	v_mul_f32_e32 v49, 0x42800000, v86
	ds_write2_b32 v42, v47, v49 offset0:40 offset1:106
	v_mul_f32_e32 v47, 0x42800000, v60
	v_mul_f32_e32 v49, 0x42800000, v61
	ds_write2_b32 v42, v47, v49 offset0:172 offset1:238
	v_add_u32_e32 v84, s0, v30
	v_ashrrev_i32_e32 v85, 31, v84
	v_lshlrev_b64 v[84:85], 10, v[84:85]
	v_mul_f32_e32 v47, 0x42800000, v62
	v_mul_f32_e32 v49, 0x42800000, v50
	ds_write2_b32 v43, v47, v49 offset0:48 offset1:114
	v_mul_f32_e32 v47, 0x42800000, v51
	v_mul_f32_e32 v49, 0x42800000, v52
	ds_write2_b32 v43, v47, v49 offset0:180 offset1:246
	v_mul_f32_e32 v47, 0x42800000, v53
	v_mul_f32_e32 v49, 0x42800000, v54
	ds_write2_b32 v44, v47, v49 offset0:56 offset1:122
	v_mov_b32_e32 v49, 0
	v_lshl_add_u64 v[50:51], v[26:27], 0, s[4:5]
	v_mul_f32_e32 v47, 0x42800000, v48
	v_mul_f32_e32 v46, 0x42800000, v46
	ds_write2_b32 v44, v47, v46 offset0:188 offset1:254
	s_waitcnt lgkmcnt(0)
	ds_read2_b32 v[52:53], v31 offset1:16
	ds_read2_b32 v[54:55], v31 offset0:33 offset1:49
	ds_read2_b32 v[56:57], v31 offset0:66 offset1:82
	ds_read2_b32 v[58:59], v31 offset0:99 offset1:115
	ds_read2_b32 v[60:61], v31 offset0:132 offset1:148
	ds_read2_b32 v[62:63], v31 offset0:165 offset1:181
	ds_read2_b32 v[64:65], v31 offset0:198 offset1:214
	ds_read2_b32 v[66:67], v31 offset0:231 offset1:247
	ds_read2_b32 v[68:69], v45 offset0:8 offset1:24
	ds_read2_b32 v[70:71], v45 offset0:41 offset1:57
	ds_read2_b32 v[72:73], v45 offset0:74 offset1:90
	ds_read2_b32 v[74:75], v45 offset0:107 offset1:123
	ds_read2_b32 v[76:77], v45 offset0:140 offset1:156
	ds_read2_b32 v[78:79], v45 offset0:173 offset1:189
	v_mov_b32_e32 v46, 0
	v_mov_b32_e32 v47, 0
	v_mov_b32_e32 v48, 0
	ds_read2_b32 v[80:81], v45 offset0:206 offset1:222
	ds_read2_b32 v[82:83], v45 offset0:239 offset1:255
	s_waitcnt lgkmcnt(14)
	v_cvt_pk_fp8_f32 v46, v52, v54
	s_waitcnt lgkmcnt(10)
	v_cvt_pk_fp8_f32 v47, v60, v62
	s_waitcnt lgkmcnt(6)
	v_cvt_pk_fp8_f32 v48, v68, v70
	s_waitcnt lgkmcnt(2)
	v_cvt_pk_fp8_f32 v49, v76, v78
	v_cvt_pk_fp8_f32 v46, v56, v58 op_sel:[0,0,1]
	v_cvt_pk_fp8_f32 v47, v64, v66 op_sel:[0,0,1]
	v_cvt_pk_fp8_f32 v48, v72, v74 op_sel:[0,0,1]
	s_waitcnt lgkmcnt(0)
	v_cvt_pk_fp8_f32 v49, v80, v82 op_sel:[0,0,1]
	v_lshl_add_u64 v[84:85], v[50:51], 0, v[84:85]
	v_add_u32_e32 v52, s0, v32
	s_mov_b64 s[4:5], 0
	global_store_dwordx4 v[84:85], v[46:49], off
	s_nop 1
	v_mov_b32_e32 v46, 0
	v_mov_b32_e32 v47, 0
	v_mov_b32_e32 v48, 0
	v_mov_b32_e32 v49, 0
	v_cvt_pk_fp8_f32 v46, v53, v55
	v_cvt_pk_fp8_f32 v47, v61, v63
	v_cvt_pk_fp8_f32 v48, v69, v71
	v_cvt_pk_fp8_f32 v49, v77, v79
	v_cvt_pk_fp8_f32 v46, v57, v59 op_sel:[0,0,1]
	v_cvt_pk_fp8_f32 v47, v65, v67 op_sel:[0,0,1]
	v_cvt_pk_fp8_f32 v48, v73, v75 op_sel:[0,0,1]
	v_cvt_pk_fp8_f32 v49, v81, v83 op_sel:[0,0,1]
	v_ashrrev_i32_e32 v53, 31, v52
	v_lshlrev_b64 v[52:53], 10, v[52:53]
	v_lshl_add_u64 v[50:51], v[50:51], 0, v[52:53]
	global_store_dwordx4 v[50:51], v[46:49], off
	s_waitcnt lgkmcnt(0)
; __device__ __forceinline__ void tr_item8(const float* W, int ld, int K, int nblk, int item, unsigned char* WT, bool gu, float scale, LAS float* scr, int lane) {
;     const int kb = item / nblk, nb = item % nblk, k0 = 64 * kb, n0 = 32 * nb;
;     int drow0 = n0;
;     if (gu) { const int bj = n0 / FF, j = n0 - bj * FF; drow0 = 256 * (j / 128) + 128 * bj + (j % 128); }
;     { float t_[32];
; #pragma unroll
;       for (int i = 0; i < 32; ++i) t_[i] = W[(size_t)(k0 + 2 * i + (lane >> 5)) * ld + n0 + (lane & 31)];
; #pragma unroll
;       for (int i = 0; i < 32; ++i) scr[(2 * i + (lane >> 5)) * 33 + (lane & 31)] = t_[i] * scale; }
; __device__ __forceinline__ void convert_items(Frame& F, const Args& a, int lo, int hi, int w, int nw) {
;     ...
;         if (r < I_DN) { tr_item8(a.in[15], D, FF, 32, r, F.ws + WS_WDN, false, WSC_DN, scr, lane); continue; } r -= I_DN;
.LBB0_566:
	s_andn2_b64 vcc, exec, s[4:5]
	s_cbranch_vccnz .LBB0_568
	s_lshl_b32 s0, s3, 5
	s_and_b32 s4, s10, 0x1ffc0
	s_and_b32 s6, s0, 0x3e0
	v_add_u32_e32 v46, s4, v28
	s_lshl_b32 s0, s6, 2
	v_ashrrev_i32_e32 v47, 31, v46
	v_lshl_add_u64 v[48:49], v[0:1], 0, s[0:1]
	v_lshlrev_b64 v[46:47], 12, v[46:47]
	v_lshl_add_u64 v[46:47], v[48:49], 0, v[46:47]
	v_add_co_u32_e32 v48, vcc, 0x2000, v46
	s_mov_b32 s5, s1
	s_nop 0
	v_addc_co_u32_e32 v49, vcc, 0, v47, vcc
	v_add_co_u32_e32 v50, vcc, 0x4000, v46
	s_nop 1
	v_addc_co_u32_e32 v51, vcc, 0, v47, vcc
	v_add_co_u32_e32 v52, vcc, 0x6000, v46
	s_nop 1
	v_addc_co_u32_e32 v53, vcc, 0, v47, vcc
	v_add_co_u32_e32 v54, vcc, 0x8000, v46
	s_nop 1
	v_addc_co_u32_e32 v55, vcc, 0, v47, vcc
	v_add_co_u32_e32 v56, vcc, 0xa000, v46
	s_nop 1
	v_addc_co_u32_e32 v57, vcc, 0, v47, vcc
	v_add_co_u32_e32 v58, vcc, 0xc000, v46
	s_nop 1
	v_addc_co_u32_e32 v59, vcc, 0, v47, vcc
	v_add_co_u32_e32 v60, vcc, 0xe000, v46
	s_nop 1
	v_addc_co_u32_e32 v61, vcc, 0, v47, vcc
	global_load_dword v64, v[46:47], off nt
	global_load_dword v65, v[48:49], off nt
	global_load_dword v66, v[50:51], off nt
	global_load_dword v67, v[52:53], off nt
	global_load_dword v68, v[54:55], off nt
	global_load_dword v69, v[56:57], off nt
	global_load_dword v70, v[58:59], off nt
	global_load_dword v71, v[60:61], off nt
	v_add_co_u32_e32 v48, vcc, 0x10000, v46
	s_nop 1
	v_addc_co_u32_e32 v49, vcc, 0, v47, vcc
	v_add_co_u32_e32 v50, vcc, 0x12000, v46
	s_nop 1
	v_addc_co_u32_e32 v51, vcc, 0, v47, vcc
	v_add_co_u32_e32 v52, vcc, 0x14000, v46
	s_nop 1
	v_addc_co_u32_e32 v53, vcc, 0, v47, vcc
	v_add_co_u32_e32 v54, vcc, 0x16000, v46
	s_nop 1
	v_addc_co_u32_e32 v55, vcc, 0, v47, vcc
	v_add_co_u32_e32 v56, vcc, 0x18000, v46
	s_nop 1
	v_addc_co_u32_e32 v57, vcc, 0, v47, vcc
	v_add_co_u32_e32 v58, vcc, 0x1a000, v46
	s_nop 1
	v_addc_co_u32_e32 v59, vcc, 0, v47, vcc
	v_add_co_u32_e32 v60, vcc, 0x1c000, v46
	s_nop 1
	v_addc_co_u32_e32 v61, vcc, 0, v47, vcc
	v_add_co_u32_e32 v62, vcc, 0x1e000, v46
	s_nop 1
	v_addc_co_u32_e32 v63, vcc, 0, v47, vcc
	global_load_dword v72, v[48:49], off nt
	global_load_dword v73, v[50:51], off nt
	global_load_dword v74, v[52:53], off nt
	global_load_dword v75, v[54:55], off nt
	global_load_dword v76, v[56:57], off nt
	global_load_dword v77, v[58:59], off nt
	global_load_dword v78, v[60:61], off nt
	global_load_dword v79, v[62:63], off nt
	v_add_co_u32_e32 v48, vcc, 0x20000, v46
	s_nop 1
	v_addc_co_u32_e32 v49, vcc, 0, v47, vcc
	v_add_co_u32_e32 v50, vcc, 0x22000, v46
	s_nop 1
	v_addc_co_u32_e32 v51, vcc, 0, v47, vcc
	v_add_co_u32_e32 v52, vcc, 0x24000, v46
	s_nop 1
	v_addc_co_u32_e32 v53, vcc, 0, v47, vcc
	v_add_co_u32_e32 v54, vcc, 0x26000, v46
	s_nop 1
	v_addc_co_u32_e32 v55, vcc, 0, v47, vcc
	v_add_co_u32_e32 v56, vcc, 0x28000, v46
	s_nop 1
	v_addc_co_u32_e32 v57, vcc, 0, v47, vcc
	v_add_co_u32_e32 v58, vcc, 0x2a000, v46
	s_nop 1
	v_addc_co_u32_e32 v59, vcc, 0, v47, vcc
	v_add_co_u32_e32 v60, vcc, 0x2c000, v46
	s_nop 1
	v_addc_co_u32_e32 v61, vcc, 0, v47, vcc
	v_add_co_u32_e32 v62, vcc, 0x2e000, v46
	s_nop 1
	v_addc_co_u32_e32 v63, vcc, 0, v47, vcc
	global_load_dword v80, v[48:49], off nt
	global_load_dword v81, v[50:51], off nt
	global_load_dword v82, v[52:53], off nt
	global_load_dword v83, v[54:55], off nt
	global_load_dword v84, v[56:57], off nt
	global_load_dword v85, v[58:59], off nt
	s_nop 0
	global_load_dword v60, v[60:61], off nt
	s_nop 0
	global_load_dword v61, v[62:63], off nt
	v_add_co_u32_e32 v48, vcc, 0x30000, v46
	s_nop 1
	v_addc_co_u32_e32 v49, vcc, 0, v47, vcc
	v_add_co_u32_e32 v50, vcc, 0x32000, v46
	s_nop 1
	v_addc_co_u32_e32 v51, vcc, 0, v47, vcc
	v_add_co_u32_e32 v52, vcc, 0x34000, v46
	s_nop 1
	v_addc_co_u32_e32 v53, vcc, 0, v47, vcc
	v_add_co_u32_e32 v54, vcc, 0x36000, v46
	s_nop 1
	v_addc_co_u32_e32 v55, vcc, 0, v47, vcc
	v_add_co_u32_e32 v56, vcc, 0x38000, v46
	s_nop 1
	v_addc_co_u32_e32 v57, vcc, 0, v47, vcc
	v_add_co_u32_e32 v58, vcc, 0x3a000, v46
	s_nop 1
	v_addc_co_u32_e32 v59, vcc, 0, v47, vcc
	global_load_dword v62, v[48:49], off nt
	s_nop 0
	global_load_dword v50, v[50:51], off nt
	s_nop 0
	global_load_dword v51, v[52:53], off nt
	s_nop 0
	global_load_dword v52, v[54:55], off nt
	global_load_dword v53, v[56:57], off nt
	s_nop 0
	global_load_dword v54, v[58:59], off nt
	v_add_co_u32_e32 v48, vcc, 0x3c000, v46
	s_nop 1
	v_addc_co_u32_e32 v49, vcc, 0, v47, vcc
	v_add_co_u32_e32 v46, vcc, 0x3e000, v46
	s_nop 1
	v_addc_co_u32_e32 v47, vcc, 0, v47, vcc
	global_load_dword v48, v[48:49], off nt
	s_nop 0
	global_load_dword v46, v[46:47], off nt
	s_waitcnt vmcnt(0)
; __device__ __forceinline__ unsigned cvt_pk4_fp8(float a, float b, float c, float d) { int w = 0; w = __builtin_amdgcn_cvt_pk_fp8_f32(a, b, w, false); w = __builtin_amdgcn_cvt_pk_fp8_f32(c, d, w, true); return (unsigned)w; }
; #define GAS __attribute__((address_space(1)))
; #define LAS __attribute__((address_space(3)))
; #define LDS_WAIT() asm volatile("s_waitcnt lgkmcnt(0)" ::: "memory")
; __device__ __forceinline__ void tr_item8(const float* W, int ld, int K, int nblk, int item, unsigned char* WT, bool gu, float scale, LAS float* scr, int lane) {
;     ...
;       for (int i = 0; i < 32; ++i) scr[(2 * i + (lane >> 5)) * 33 + (lane & 31)] = t_[i] * scale; }
;     LDS_WAIT(); asm volatile("" ::: "memory");
;     const int c = lane & 3;
; #pragma unroll
;     for (int j = 0; j < 2; ++j) { const int n = (lane >> 2) + 16 * j; const LAS float* sp = scr + (16 * c) * 33 + n;
;         v4u o; o.x = pg8::cvt_pk4_fp8(sp[0 * 33], sp[1 * 33], sp[2 * 33], sp[3 * 33]); o.y = pg8::cvt_pk4_fp8(sp[4 * 33], sp[5 * 33], sp[6 * 33], sp[7 * 33]);
;         o.z = pg8::cvt_pk4_fp8(sp[8 * 33], sp[9 * 33], sp[10 * 33], sp[11 * 33]); o.w = pg8::cvt_pk4_fp8(sp[12 * 33], sp[13 * 33], sp[14 * 33], sp[15 * 33]);
;         *(GAS v4u*)(WT + (size_t)(drow0 + n) * K + k0 + 16 * c) = o; }
;     LDS_WAIT(); asm volatile("" ::: "memory");
	v_mul_f32_e32 v47, 0x43000000, v64
	v_mul_f32_e32 v49, 0x43000000, v65
	ds_write2_b32 v29, v47, v49 offset1:66
	v_mul_f32_e32 v47, 0x43000000, v66
	v_mul_f32_e32 v49, 0x43000000, v67
	ds_write2_b32 v29, v47, v49 offset0:132 offset1:198
	v_mul_f32_e32 v47, 0x43000000, v68
	v_mul_f32_e32 v49, 0x43000000, v69
	ds_write2_b32 v38, v47, v49 offset0:8 offset1:74
	v_mul_f32_e32 v47, 0x43000000, v70
	v_mul_f32_e32 v49, 0x43000000, v71
	ds_write2_b32 v38, v47, v49 offset0:140 offset1:206
	v_mul_f32_e32 v47, 0x43000000, v72
	v_mul_f32_e32 v49, 0x43000000, v73
	ds_write2_b32 v39, v47, v49 offset0:16 offset1:82
	v_mul_f32_e32 v47, 0x43000000, v74
	v_mul_f32_e32 v49, 0x43000000, v75
	ds_write2_b32 v39, v47, v49 offset0:148 offset1:214
	v_mul_f32_e32 v47, 0x43000000, v76
	v_mul_f32_e32 v49, 0x43000000, v77
	ds_write2_b32 v40, v47, v49 offset0:24 offset1:90
	v_mul_f32_e32 v47, 0x43000000, v78
	v_mul_f32_e32 v49, 0x43000000, v79
	ds_write2_b32 v40, v47, v49 offset0:156 offset1:222
	v_mul_f32_e32 v47, 0x43000000, v80
	v_mul_f32_e32 v49, 0x43000000, v81
	ds_write2_b32 v41, v47, v49 offset0:32 offset1:98
	v_mul_f32_e32 v47, 0x43000000, v82
	v_mul_f32_e32 v49, 0x43000000, v83
	ds_write2_b32 v41, v47, v49 offset0:164 offset1:230
	v_mul_f32_e32 v47, 0x43000000, v84
	v_mul_f32_e32 v49, 0x43000000, v85
	ds_write2_b32 v42, v47, v49 offset0:40 offset1:106
	v_mul_f32_e32 v47, 0x43000000, v60
	v_mul_f32_e32 v49, 0x43000000, v61
	ds_write2_b32 v42, v47, v49 offset0:172 offset1:238
	v_mul_f32_e32 v47, 0x43000000, v62
	v_mul_f32_e32 v49, 0x43000000, v50
	ds_write2_b32 v43, v47, v49 offset0:48 offset1:114
	v_mul_f32_e32 v47, 0x43000000, v51
	v_mul_f32_e32 v49, 0x43000000, v52
	ds_write2_b32 v43, v47, v49 offset0:180 offset1:246
	v_mul_f32_e32 v47, 0x43000000, v53
	v_mul_f32_e32 v49, 0x43000000, v54
	ds_write2_b32 v44, v47, v49 offset0:56 offset1:122
	v_mov_b32_e32 v49, 0
	v_lshl_add_u64 v[50:51], v[12:13], 0, s[4:5]
	v_mul_f32_e32 v47, 0x43000000, v48
	v_mul_f32_e32 v46, 0x43000000, v46
	ds_write2_b32 v44, v47, v46 offset0:188 offset1:254
	s_waitcnt lgkmcnt(0)
	ds_read2_b32 v[52:53], v31 offset1:16
	ds_read2_b32 v[54:55], v31 offset0:33 offset1:49
	ds_read2_b32 v[56:57], v31 offset0:66 offset1:82
	ds_read2_b32 v[58:59], v31 offset0:99 offset1:115
	ds_read2_b32 v[60:61], v31 offset0:132 offset1:148
	ds_read2_b32 v[62:63], v31 offset0:165 offset1:181
	ds_read2_b32 v[64:65], v31 offset0:198 offset1:214
	ds_read2_b32 v[66:67], v31 offset0:231 offset1:247
	ds_read2_b32 v[68:69], v45 offset0:8 offset1:24
	ds_read2_b32 v[70:71], v45 offset0:41 offset1:57
	ds_read2_b32 v[72:73], v45 offset0:74 offset1:90
	ds_read2_b32 v[74:75], v45 offset0:107 offset1:123
	ds_read2_b32 v[76:77], v45 offset0:140 offset1:156
	ds_read2_b32 v[78:79], v45 offset0:173 offset1:189
	v_mov_b32_e32 v46, 0
	v_mov_b32_e32 v47, 0
	v_mov_b32_e32 v48, 0
	ds_read2_b32 v[80:81], v45 offset0:206 offset1:222
	ds_read2_b32 v[82:83], v45 offset0:239 offset1:255
	s_waitcnt lgkmcnt(14)
	v_cvt_pk_fp8_f32 v46, v52, v54
	s_waitcnt lgkmcnt(10)
	v_cvt_pk_fp8_f32 v47, v60, v62
	s_waitcnt lgkmcnt(6)
	v_cvt_pk_fp8_f32 v48, v68, v70
	s_waitcnt lgkmcnt(2)
	v_cvt_pk_fp8_f32 v49, v76, v78
	v_cvt_pk_fp8_f32 v46, v56, v58 op_sel:[0,0,1]
	v_cvt_pk_fp8_f32 v47, v64, v66 op_sel:[0,0,1]
	v_cvt_pk_fp8_f32 v48, v72, v74 op_sel:[0,0,1]
	s_waitcnt lgkmcnt(0)
	v_cvt_pk_fp8_f32 v49, v80, v82 op_sel:[0,0,1]
	v_add_u32_e32 v52, s6, v30
	v_mad_i64_i32 v[84:85], s[4:5], v52, s11, v[50:51]
	global_store_dwordx4 v[84:85], v[46:49], off
	v_add_u32_e32 v52, s6, v32
	v_mad_i64_i32 v[50:51], s[4:5], v52, s11, v[50:51]
	v_mov_b32_e32 v46, 0
	v_mov_b32_e32 v47, 0
	v_mov_b32_e32 v48, 0
	v_mov_b32_e32 v49, 0
	v_cvt_pk_fp8_f32 v46, v53, v55
	v_cvt_pk_fp8_f32 v47, v61, v63
	v_cvt_pk_fp8_f32 v48, v69, v71
	v_cvt_pk_fp8_f32 v49, v77, v79
	v_cvt_pk_fp8_f32 v46, v57, v59 op_sel:[0,0,1]
	v_cvt_pk_fp8_f32 v47, v65, v67 op_sel:[0,0,1]
	v_cvt_pk_fp8_f32 v48, v73, v75 op_sel:[0,0,1]
	v_cvt_pk_fp8_f32 v49, v81, v83 op_sel:[0,0,1]
	global_store_dwordx4 v[50:51], v[46:49], off
	s_waitcnt lgkmcnt(0)

; __device__ __forceinline__ void tr_item8(const float* W, int ld, int K, int nblk, int item, unsigned char* WT, bool gu, float scale, LAS float* scr, int lane) {
;     const int kb = item / nblk, nb = item % nblk, k0 = 64 * kb, n0 = 32 * nb;
;     int drow0 = n0;
;     if (gu) { const int bj = n0 / FF, j = n0 - bj * FF; drow0 = 256 * (j / 128) + 128 * bj + (j % 128); }
;     { float t_[32];
; #pragma unroll
;       for (int i = 0; i < 32; ++i) t_[i] = W[(size_t)(k0 + 2 * i + (lane >> 5)) * ld + n0 + (lane & 31)];
; #pragma unroll
;       for (int i = 0; i < 32; ++i) scr[(2 * i + (lane >> 5)) * 33 + (lane & 31)] = t_[i] * scale; }
; __device__ __forceinline__ void convert_items(Frame& F, const Args& a, int lo, int hi, int w, int nw) {
;     ...
;         if (r < I_GU) { tr_item8(a.in[14], 2 * FF, D, 224, r, F.ws + WS_WGU, true, WSC_GU, scr, lane); continue; } r -= I_GU;
.LBB0_569:
	s_andn2_b64 vcc, exec, s[4:5]
	s_cbranch_vccnz .LBB0_571
	s_add_i32 s0, s3, 0xf300
	s_bfe_u32 s4, s0, 0xb0005
	s_mulk_i32 s4, 0x2493
	s_lshr_b32 s4, s4, 16
	s_mul_i32 s5, s4, 0xe0
	s_sub_i32 s0, s0, s5
	s_lshl_b32 s5, s0, 5
	s_and_b32 s6, s0, 0xffff
	s_cmpk_gt_u32 s6, 0x6f
	s_cselect_b32 s17, 0xfffff200, 0
	s_cselect_b32 s18, 0x80, 0
	s_lshl_b32 s0, s0, 7
	s_lshl_b32 s4, s4, 6
	s_and_b32 s0, s0, 0x3ff80
	v_add_u32_e32 v64, s4, v28
	v_lshl_add_u64 v[46:47], v[2:3], 0, s[0:1]
	v_mad_i64_i32 v[48:49], s[6:7], v64, s12, v[46:47]
	v_add_u32_e32 v50, 2, v64
	v_add_u32_e32 v52, 4, v64
	v_add_u32_e32 v54, 6, v64
	v_add_u32_e32 v56, 8, v64
	v_add_u32_e32 v58, 10, v64
	v_add_u32_e32 v60, 12, v64
	v_add_u32_e32 v62, 14, v64
	v_mad_i64_i32 v[50:51], s[6:7], v50, s12, v[46:47]
	v_mad_i64_i32 v[52:53], s[6:7], v52, s12, v[46:47]
	v_mad_i64_i32 v[54:55], s[6:7], v54, s12, v[46:47]
	v_mad_i64_i32 v[56:57], s[6:7], v56, s12, v[46:47]
	v_mad_i64_i32 v[58:59], s[6:7], v58, s12, v[46:47]
	v_mad_i64_i32 v[60:61], s[6:7], v60, s12, v[46:47]
	v_mad_i64_i32 v[62:63], s[6:7], v62, s12, v[46:47]
	global_load_dword v65, v[48:49], off nt
	global_load_dword v66, v[50:51], off nt
	global_load_dword v67, v[52:53], off nt
	global_load_dword v68, v[54:55], off nt
	global_load_dword v69, v[56:57], off nt
	global_load_dword v70, v[58:59], off nt
	global_load_dword v71, v[60:61], off nt
	global_load_dword v72, v[62:63], off nt
	v_add_u32_e32 v48, 16, v64
	v_mad_i64_i32 v[48:49], s[6:7], v48, s12, v[46:47]
	v_add_u32_e32 v50, 18, v64
	v_add_u32_e32 v52, 20, v64
	v_add_u32_e32 v54, 22, v64
	v_add_u32_e32 v56, 24, v64
	v_add_u32_e32 v58, 26, v64
	v_add_u32_e32 v60, 28, v64
	v_add_u32_e32 v62, 30, v64
	v_mad_i64_i32 v[50:51], s[6:7], v50, s12, v[46:47]
	v_mad_i64_i32 v[52:53], s[6:7], v52, s12, v[46:47]
	v_mad_i64_i32 v[54:55], s[6:7], v54, s12, v[46:47]
	v_mad_i64_i32 v[56:57], s[6:7], v56, s12, v[46:47]
	v_mad_i64_i32 v[58:59], s[6:7], v58, s12, v[46:47]
	v_mad_i64_i32 v[60:61], s[6:7], v60, s12, v[46:47]
	v_mad_i64_i32 v[62:63], s[6:7], v62, s12, v[46:47]
	global_load_dword v73, v[48:49], off nt
	global_load_dword v74, v[50:51], off nt
	global_load_dword v75, v[52:53], off nt
	global_load_dword v76, v[54:55], off nt
	global_load_dword v77, v[56:57], off nt
	global_load_dword v78, v[58:59], off nt
	global_load_dword v79, v[60:61], off nt
	global_load_dword v80, v[62:63], off nt
	v_add_u32_e32 v48, 32, v64
	v_add_u32_e32 v50, 34, v64
	v_add_u32_e32 v52, 36, v64
	v_add_u32_e32 v54, 38, v64
	v_add_u32_e32 v60, 44, v64
	v_mad_i64_i32 v[48:49], s[6:7], v48, s12, v[46:47]
	v_mad_i64_i32 v[50:51], s[6:7], v50, s12, v[46:47]
	v_mad_i64_i32 v[52:53], s[6:7], v52, s12, v[46:47]
	v_mad_i64_i32 v[54:55], s[6:7], v54, s12, v[46:47]
	v_add_u32_e32 v56, 40, v64
	v_add_u32_e32 v58, 42, v64
	v_mad_i64_i32 v[60:61], s[6:7], v60, s12, v[46:47]
	v_add_u32_e32 v62, 46, v64
	v_mad_i64_i32 v[56:57], s[6:7], v56, s12, v[46:47]
	v_mad_i64_i32 v[58:59], s[6:7], v58, s12, v[46:47]
	v_mad_i64_i32 v[62:63], s[6:7], v62, s12, v[46:47]
	global_load_dword v81, v[48:49], off nt
	global_load_dword v82, v[50:51], off nt
	global_load_dword v83, v[52:53], off nt
	global_load_dword v84, v[54:55], off nt
	global_load_dword v85, v[56:57], off nt
	global_load_dword v86, v[58:59], off nt
	s_nop 0
	global_load_dword v60, v[60:61], off nt
	s_nop 0
	global_load_dword v61, v[62:63], off nt
	v_add_u32_e32 v48, 48, v64
	v_add_u32_e32 v50, 50, v64
	v_add_u32_e32 v52, 52, v64
	v_add_u32_e32 v54, 54, v64
	v_mad_i64_i32 v[48:49], s[6:7], v48, s12, v[46:47]
	v_mad_i64_i32 v[50:51], s[6:7], v50, s12, v[46:47]
	v_mad_i64_i32 v[52:53], s[6:7], v52, s12, v[46:47]
	v_mad_i64_i32 v[54:55], s[6:7], v54, s12, v[46:47]
	v_add_u32_e32 v56, 56, v64
	v_add_u32_e32 v58, 58, v64
	v_mad_i64_i32 v[56:57], s[6:7], v56, s12, v[46:47]
	v_mad_i64_i32 v[58:59], s[6:7], v58, s12, v[46:47]
	global_load_dword v62, v[48:49], off nt
	s_nop 0
	global_load_dword v50, v[50:51], off nt
	s_nop 0
	global_load_dword v51, v[52:53], off nt
	s_nop 0
	global_load_dword v52, v[54:55], off nt
	global_load_dword v53, v[56:57], off nt
	s_nop 0
	global_load_dword v54, v[58:59], off nt
	v_add_u32_e32 v48, 60, v64
	v_add_u32_e32 v55, 62, v64
	v_mad_i64_i32 v[48:49], s[6:7], v48, s12, v[46:47]
	v_mad_i64_i32 v[46:47], s[6:7], v55, s12, v[46:47]
	global_load_dword v48, v[48:49], off nt
	s_nop 0
	global_load_dword v46, v[46:47], off nt
	s_waitcnt vmcnt(0)
; __device__ __forceinline__ unsigned cvt_pk4_fp8(float a, float b, float c, float d) { int w = 0; w = __builtin_amdgcn_cvt_pk_fp8_f32(a, b, w, false); w = __builtin_amdgcn_cvt_pk_fp8_f32(c, d, w, true); return (unsigned)w; }
; #define GAS __attribute__((address_space(1)))
; #define LAS __attribute__((address_space(3)))
; #define LDS_WAIT() asm volatile("s_waitcnt lgkmcnt(0)" ::: "memory")
; __device__ __forceinline__ void tr_item8(const float* W, int ld, int K, int nblk, int item, unsigned char* WT, bool gu, float scale, LAS float* scr, int lane) {
;     ...
;     if (gu) { const int bj = n0 / FF, j = n0 - bj * FF; drow0 = 256 * (j / 128) + 128 * bj + (j % 128); }
;     ...
;       for (int i = 0; i < 32; ++i) t_[i] = W[(size_t)(k0 + 2 * i + (lane >> 5)) * ld + n0 + (lane & 31)];
; #pragma unroll
;       for (int i = 0; i < 32; ++i) scr[(2 * i + (lane >> 5)) * 33 + (lane & 31)] = t_[i] * scale; }
;     LDS_WAIT(); asm volatile("" ::: "memory");
;     const int c = lane & 3;
; #pragma unroll
;     for (int j = 0; j < 2; ++j) { const int n = (lane >> 2) + 16 * j; const LAS float* sp = scr + (16 * c) * 33 + n;
;         v4u o; o.x = pg8::cvt_pk4_fp8(sp[0 * 33], sp[1 * 33], sp[2 * 33], sp[3 * 33]); o.y = pg8::cvt_pk4_fp8(sp[4 * 33], sp[5 * 33], sp[6 * 33], sp[7 * 33]);
;         o.z = pg8::cvt_pk4_fp8(sp[8 * 33], sp[9 * 33], sp[10 * 33], sp[11 * 33]); o.w = pg8::cvt_pk4_fp8(sp[12 * 33], sp[13 * 33], sp[14 * 33], sp[15 * 33]);
;         *(GAS v4u*)(WT + (size_t)(drow0 + n) * K + k0 + 16 * c) = o; }
;     LDS_WAIT(); asm volatile("" ::: "memory");
	v_mul_f32_e32 v47, 0x42800000, v65
	v_mul_f32_e32 v49, 0x42800000, v66
	ds_write2_b32 v29, v47, v49 offset1:66
	v_mul_f32_e32 v47, 0x42800000, v67
	v_mul_f32_e32 v49, 0x42800000, v68
	ds_write2_b32 v29, v47, v49 offset0:132 offset1:198
	v_mul_f32_e32 v47, 0x42800000, v69
	v_mul_f32_e32 v49, 0x42800000, v70
	ds_write2_b32 v38, v47, v49 offset0:8 offset1:74
	v_mul_f32_e32 v47, 0x42800000, v71
	v_mul_f32_e32 v49, 0x42800000, v72
	ds_write2_b32 v38, v47, v49 offset0:140 offset1:206
	s_add_i32 s0, s17, s5
	s_sext_i32_i16 s5, s0
	s_bfe_u32 s5, s5, 0x70018
	s_add_i32 s5, s0, s5
	s_sext_i32_i16 s6, s5
	s_and_b32 s5, s5, 0xff80
	s_sub_i32 s0, s0, s5
	s_lshl_b32 s6, s6, 1
	s_sext_i32_i16 s0, s0
	v_mul_f32_e32 v47, 0x42800000, v73
	v_mul_f32_e32 v49, 0x42800000, v74
	ds_write2_b32 v39, v47, v49 offset0:16 offset1:82
	v_mul_f32_e32 v47, 0x42800000, v75
	v_mul_f32_e32 v49, 0x42800000, v76
	ds_write2_b32 v39, v47, v49 offset0:148 offset1:214
	v_mul_f32_e32 v47, 0x42800000, v77
	v_mul_f32_e32 v49, 0x42800000, v78
	ds_write2_b32 v40, v47, v49 offset0:24 offset1:90
	v_mul_f32_e32 v47, 0x42800000, v79
	v_mul_f32_e32 v49, 0x42800000, v80
	ds_write2_b32 v40, v47, v49 offset0:156 offset1:222
	s_and_b32 s6, s6, 0xffffff00
	s_add_i32 s0, s18, s0
	s_add_i32 s0, s0, s6
	s_mov_b32 s5, s1
	v_mul_f32_e32 v47, 0x42800000, v81
	v_mul_f32_e32 v49, 0x42800000, v82
	ds_write2_b32 v41, v47, v49 offset0:32 offset1:98
	v_mul_f32_e32 v47, 0x42800000, v83
	v_mul_f32_e32 v49, 0x42800000, v84
	ds_write2_b32 v41, v47, v49 offset0:164 offset1:230
	v_mul_f32_e32 v47, 0x42800000, v85
	v_mul_f32_e32 v49, 0x42800000, v86
	ds_write2_b32 v42, v47, v49 offset0:40 offset1:106
	v_mul_f32_e32 v47, 0x42800000, v60
	v_mul_f32_e32 v49, 0x42800000, v61
	ds_write2_b32 v42, v47, v49 offset0:172 offset1:238
	v_add_u32_e32 v84, s0, v30
	v_ashrrev_i32_e32 v85, 31, v84
	v_lshlrev_b64 v[84:85], 10, v[84:85]
	v_mul_f32_e32 v47, 0x42800000, v62
	v_mul_f32_e32 v49, 0x42800000, v50
	ds_write2_b32 v43, v47, v49 offset0:48 offset1:114
	v_mul_f32_e32 v47, 0x42800000, v51
	v_mul_f32_e32 v49, 0x42800000, v52
	ds_write2_b32 v43, v47, v49 offset0:180 offset1:246
	v_mul_f32_e32 v47, 0x42800000, v53
	v_mul_f32_e32 v49, 0x42800000, v54
	ds_write2_b32 v44, v47, v49 offset0:56 offset1:122
	v_mov_b32_e32 v49, 0
	v_lshl_add_u64 v[50:51], v[14:15], 0, s[4:5]
	v_mul_f32_e32 v47, 0x42800000, v48
	v_mul_f32_e32 v46, 0x42800000, v46
	ds_write2_b32 v44, v47, v46 offset0:188 offset1:254
	s_waitcnt lgkmcnt(0)
	ds_read2_b32 v[52:53], v31 offset1:16
	ds_read2_b32 v[54:55], v31 offset0:33 offset1:49
	ds_read2_b32 v[56:57], v31 offset0:66 offset1:82
	ds_read2_b32 v[58:59], v31 offset0:99 offset1:115
	ds_read2_b32 v[60:61], v31 offset0:132 offset1:148
	ds_read2_b32 v[62:63], v31 offset0:165 offset1:181
	ds_read2_b32 v[64:65], v31 offset0:198 offset1:214
	ds_read2_b32 v[66:67], v31 offset0:231 offset1:247
	ds_read2_b32 v[68:69], v45 offset0:8 offset1:24
	ds_read2_b32 v[70:71], v45 offset0:41 offset1:57
	ds_read2_b32 v[72:73], v45 offset0:74 offset1:90
	ds_read2_b32 v[74:75], v45 offset0:107 offset1:123
	ds_read2_b32 v[76:77], v45 offset0:140 offset1:156
	ds_read2_b32 v[78:79], v45 offset0:173 offset1:189
	v_mov_b32_e32 v46, 0
	v_mov_b32_e32 v47, 0
	v_mov_b32_e32 v48, 0
	ds_read2_b32 v[80:81], v45 offset0:206 offset1:222
	ds_read2_b32 v[82:83], v45 offset0:239 offset1:255
	s_waitcnt lgkmcnt(14)
	v_cvt_pk_fp8_f32 v46, v52, v54
	s_waitcnt lgkmcnt(10)
	v_cvt_pk_fp8_f32 v47, v60, v62
	s_waitcnt lgkmcnt(6)
	v_cvt_pk_fp8_f32 v48, v68, v70
	s_waitcnt lgkmcnt(2)
	v_cvt_pk_fp8_f32 v49, v76, v78
	v_cvt_pk_fp8_f32 v46, v56, v58 op_sel:[0,0,1]
	v_cvt_pk_fp8_f32 v47, v64, v66 op_sel:[0,0,1]
	v_cvt_pk_fp8_f32 v48, v72, v74 op_sel:[0,0,1]
	s_waitcnt lgkmcnt(0)
	v_cvt_pk_fp8_f32 v49, v80, v82 op_sel:[0,0,1]
	v_lshl_add_u64 v[84:85], v[50:51], 0, v[84:85]
	v_add_u32_e32 v52, s0, v32
	global_store_dwordx4 v[84:85], v[46:49], off
	s_nop 1
	v_mov_b32_e32 v46, 0
	v_mov_b32_e32 v47, 0
	v_mov_b32_e32 v48, 0
	v_mov_b32_e32 v49, 0
	v_cvt_pk_fp8_f32 v46, v53, v55
	v_cvt_pk_fp8_f32 v47, v61, v63
	v_cvt_pk_fp8_f32 v48, v69, v71
	v_cvt_pk_fp8_f32 v49, v77, v79
	v_cvt_pk_fp8_f32 v46, v57, v59 op_sel:[0,0,1]
	v_cvt_pk_fp8_f32 v47, v65, v67 op_sel:[0,0,1]
	v_cvt_pk_fp8_f32 v48, v73, v75 op_sel:[0,0,1]
	v_cvt_pk_fp8_f32 v49, v81, v83 op_sel:[0,0,1]
	v_ashrrev_i32_e32 v53, 31, v52
	v_lshlrev_b64 v[52:53], 10, v[52:53]
	v_lshl_add_u64 v[50:51], v[50:51], 0, v[52:53]
	global_store_dwordx4 v[50:51], v[46:49], off
	s_waitcnt lgkmcnt(0)

; __device__ __forceinline__ void tr_item(const float* W, int ld, int K, int nblk, int item, bf16* WT, bool gu, LAS float* scr, int lane) {
;     ...
;       for (int i = 0; i < 32; ++i) t_[i] = W[(size_t)(k0 + 2 * i + (lane >> 5)) * ld + n0 + (lane & 31)];
; #pragma unroll
;       for (int i = 0; i < 32; ++i) scr[(2 * i + (lane >> 5)) * 33 + (lane & 31)] = t_[i]; }
; __device__ __forceinline__ void convert_items(Frame& F, const Args& a, int lo, int hi, int w, int nw) {
;     ...
;         if (r < I_SO) { tr_item(a.in[12], D, D, 32, r, (bf16*)(F.ws + WS_WSWAOUT), false, scr, lane); continue; } r -= I_SO;
.LBB0_572:
	s_andn2_b64 vcc, exec, s[4:5]
	s_cbranch_vccnz .LBB0_574
	s_add_i32 s0, s10, 0x2000
	s_and_b32 s5, s0, 0x1ffc0
	s_and_b32 s4, s9, 0x3e0
	v_add_u32_e32 v46, s5, v28
	s_lshl_b32 s0, s4, 2
	v_ashrrev_i32_e32 v47, 31, v46
	v_lshl_add_u64 v[48:49], v[4:5], 0, s[0:1]
	v_lshlrev_b64 v[46:47], 12, v[46:47]
	v_lshl_add_u64 v[46:47], v[48:49], 0, v[46:47]
	v_add_co_u32_e32 v48, vcc, 0x2000, v46
	s_lshl_b32 s0, s5, 1
	s_nop 0
	v_addc_co_u32_e32 v49, vcc, 0, v47, vcc
	v_add_co_u32_e32 v50, vcc, 0x4000, v46
	s_nop 1
	v_addc_co_u32_e32 v51, vcc, 0, v47, vcc
	v_add_co_u32_e32 v52, vcc, 0x6000, v46
	s_nop 1
	v_addc_co_u32_e32 v53, vcc, 0, v47, vcc
	v_add_co_u32_e32 v54, vcc, 0x8000, v46
	s_nop 1
	v_addc_co_u32_e32 v55, vcc, 0, v47, vcc
	v_add_co_u32_e32 v56, vcc, 0xa000, v46
	s_nop 1
	v_addc_co_u32_e32 v57, vcc, 0, v47, vcc
	v_add_co_u32_e32 v58, vcc, 0xc000, v46
	s_nop 1
	v_addc_co_u32_e32 v59, vcc, 0, v47, vcc
	v_add_co_u32_e32 v60, vcc, 0xe000, v46
	s_nop 1
	v_addc_co_u32_e32 v61, vcc, 0, v47, vcc
	global_load_dword v64, v[46:47], off nt
	global_load_dword v65, v[48:49], off nt
	global_load_dword v66, v[50:51], off nt
	global_load_dword v67, v[52:53], off nt
	global_load_dword v68, v[54:55], off nt
	global_load_dword v69, v[56:57], off nt
	global_load_dword v70, v[58:59], off nt
	global_load_dword v71, v[60:61], off nt
	v_add_co_u32_e32 v48, vcc, 0x10000, v46
	s_nop 1
	v_addc_co_u32_e32 v49, vcc, 0, v47, vcc
	v_add_co_u32_e32 v50, vcc, 0x12000, v46
	s_nop 1
	v_addc_co_u32_e32 v51, vcc, 0, v47, vcc
	v_add_co_u32_e32 v52, vcc, 0x14000, v46
	s_nop 1
	v_addc_co_u32_e32 v53, vcc, 0, v47, vcc
	v_add_co_u32_e32 v54, vcc, 0x16000, v46
	s_nop 1
	v_addc_co_u32_e32 v55, vcc, 0, v47, vcc
	v_add_co_u32_e32 v56, vcc, 0x18000, v46
	s_nop 1
	v_addc_co_u32_e32 v57, vcc, 0, v47, vcc
	v_add_co_u32_e32 v58, vcc, 0x1a000, v46
	s_nop 1
	v_addc_co_u32_e32 v59, vcc, 0, v47, vcc
	v_add_co_u32_e32 v60, vcc, 0x1c000, v46
	s_nop 1
	v_addc_co_u32_e32 v61, vcc, 0, v47, vcc
	v_add_co_u32_e32 v62, vcc, 0x1e000, v46
	s_nop 1
	v_addc_co_u32_e32 v63, vcc, 0, v47, vcc
	global_load_dword v72, v[48:49], off nt
	global_load_dword v73, v[50:51], off nt
	global_load_dword v74, v[52:53], off nt
	global_load_dword v75, v[54:55], off nt
	global_load_dword v76, v[56:57], off nt
	global_load_dword v77, v[58:59], off nt
	global_load_dword v78, v[60:61], off nt
	global_load_dword v79, v[62:63], off nt
	v_add_co_u32_e32 v48, vcc, 0x20000, v46
	s_nop 1
	v_addc_co_u32_e32 v49, vcc, 0, v47, vcc
	v_add_co_u32_e32 v50, vcc, 0x22000, v46
	s_nop 1
	v_addc_co_u32_e32 v51, vcc, 0, v47, vcc
	v_add_co_u32_e32 v52, vcc, 0x24000, v46
	s_nop 1
	v_addc_co_u32_e32 v53, vcc, 0, v47, vcc
	v_add_co_u32_e32 v54, vcc, 0x26000, v46
	s_nop 1
	v_addc_co_u32_e32 v55, vcc, 0, v47, vcc
	v_add_co_u32_e32 v56, vcc, 0x28000, v46
	s_nop 1
	v_addc_co_u32_e32 v57, vcc, 0, v47, vcc
	v_add_co_u32_e32 v58, vcc, 0x2a000, v46
	s_nop 1
	v_addc_co_u32_e32 v59, vcc, 0, v47, vcc
	v_add_co_u32_e32 v60, vcc, 0x2c000, v46
	s_nop 1
	v_addc_co_u32_e32 v61, vcc, 0, v47, vcc
	v_add_co_u32_e32 v62, vcc, 0x2e000, v46
	s_nop 1
	v_addc_co_u32_e32 v63, vcc, 0, v47, vcc
	global_load_dword v80, v[48:49], off nt
	global_load_dword v81, v[50:51], off nt
	global_load_dword v82, v[52:53], off nt
	global_load_dword v83, v[54:55], off nt
	global_load_dword v84, v[56:57], off nt
	global_load_dword v85, v[58:59], off nt
	global_load_dword v86, v[60:61], off nt
	s_nop 0
	global_load_dword v62, v[62:63], off nt
	v_add_co_u32_e32 v48, vcc, 0x30000, v46
	s_nop 1
	v_addc_co_u32_e32 v49, vcc, 0, v47, vcc
	v_add_co_u32_e32 v50, vcc, 0x32000, v46
	s_nop 1
	v_addc_co_u32_e32 v51, vcc, 0, v47, vcc
	v_add_co_u32_e32 v52, vcc, 0x34000, v46
	s_nop 1
	v_addc_co_u32_e32 v53, vcc, 0, v47, vcc
	v_add_co_u32_e32 v54, vcc, 0x36000, v46
	s_nop 1
	v_addc_co_u32_e32 v55, vcc, 0, v47, vcc
	v_add_co_u32_e32 v56, vcc, 0x38000, v46
	s_nop 1
	v_addc_co_u32_e32 v57, vcc, 0, v47, vcc
	v_add_co_u32_e32 v58, vcc, 0x3a000, v46
	s_nop 1
	v_addc_co_u32_e32 v59, vcc, 0, v47, vcc
	v_add_co_u32_e32 v60, vcc, 0x3c000, v46
	s_nop 1
	v_addc_co_u32_e32 v61, vcc, 0, v47, vcc
	v_add_co_u32_e32 v46, vcc, 0x3e000, v46
	s_nop 1
	v_addc_co_u32_e32 v47, vcc, 0, v47, vcc
	global_load_dword v48, v[48:49], off nt
	s_nop 0
	global_load_dword v49, v[50:51], off nt
	s_nop 0
	global_load_dword v50, v[52:53], off nt
	global_load_dword v51, v[54:55], off nt
	s_nop 0
	global_load_dword v52, v[56:57], off nt
	global_load_dword v53, v[58:59], off nt
	global_load_dword v54, v[60:61], off nt
	s_nop 0
	global_load_dword v46, v[46:47], off nt
	s_waitcnt vmcnt(0)
	ds_write2_b32 v29, v64, v65 offset1:66
	ds_write2_b32 v29, v66, v67 offset0:132 offset1:198
	ds_write2_b32 v38, v68, v69 offset0:8 offset1:74
	ds_write2_b32 v38, v70, v71 offset0:140 offset1:206
	ds_write2_b32 v39, v72, v73 offset0:16 offset1:82
	ds_write2_b32 v39, v74, v75 offset0:148 offset1:214
	ds_write2_b32 v40, v76, v77 offset0:24 offset1:90
	ds_write2_b32 v40, v78, v79 offset0:156 offset1:222
	ds_write2_b32 v41, v80, v81 offset0:32 offset1:98
	ds_write2_b32 v41, v82, v83 offset0:164 offset1:230
	ds_write2_b32 v42, v84, v85 offset0:40 offset1:106
	ds_write2_b32 v42, v86, v62 offset0:172 offset1:238
	ds_write2_b32 v43, v48, v49 offset0:48 offset1:114
	ds_write2_b32 v43, v50, v51 offset0:180 offset1:246
	ds_write2_b32 v44, v52, v53 offset0:56 offset1:122
	ds_write2_b32 v44, v54, v46 offset0:188 offset1:254
	s_waitcnt lgkmcnt(0)
; #define GAS __attribute__((address_space(1)))
; #define LAS __attribute__((address_space(3)))
; #define LDS_WAIT() asm volatile("s_waitcnt lgkmcnt(0)" ::: "memory")
; __device__ __forceinline__ unsigned pk2(float lo, float hi) { return f2bf(lo) | (f2bf(hi) << 16); }
; __device__ __forceinline__ void tr_item(const float* W, int ld, int K, int nblk, int item, bf16* WT, bool gu, LAS float* scr, int lane) {
;     ...
;       for (int i = 0; i < 32; ++i) scr[(2 * i + (lane >> 5)) * 33 + (lane & 31)] = t_[i]; }
;     LDS_WAIT(); asm volatile("" ::: "memory");
;     const int c = lane & 7;
; #pragma unroll
;     for (int j = 0; j < 4; ++j) { const int n = (lane >> 3) + 8 * j; const LAS float* s = scr + (8 * c) * 33 + n;
;         v4u o; o.x = pk2(s[0 * 33], s[1 * 33]); o.y = pk2(s[2 * 33], s[3 * 33]); o.z = pk2(s[4 * 33], s[5 * 33]); o.w = pk2(s[6 * 33], s[7 * 33]);
;         *(GAS v4u*)(WT + (size_t)(drow0 + n) * K + k0 + 8 * c) = o; }
;     LDS_WAIT(); asm volatile("" ::: "memory");
	ds_read2_b32 v[50:51], v34 offset1:8
	ds_read2_b32 v[54:55], v34 offset0:33 offset1:41
	ds_read2_b32 v[56:57], v34 offset0:66 offset1:74
	ds_read2_b32 v[58:59], v34 offset0:99 offset1:107
	ds_read2_b32 v[60:61], v34 offset0:132 offset1:140
	s_waitcnt lgkmcnt(4)
	v_bfe_u32 v46, v50, 16, 1
	v_add3_u32 v46, v50, v46, s13
	s_waitcnt lgkmcnt(3)
	v_bfe_u32 v47, v54, 16, 1
	v_lshrrev_b32_e32 v46, 16, v46
	v_add3_u32 v47, v54, v47, s13
	ds_read2_b32 v[62:63], v34 offset0:165 offset1:173
	v_and_or_b32 v46, v47, s14, v46
	s_waitcnt lgkmcnt(3)
	v_bfe_u32 v47, v56, 16, 1
	v_add3_u32 v47, v56, v47, s13
	s_waitcnt lgkmcnt(2)
	v_bfe_u32 v48, v58, 16, 1
	ds_read2_b32 v[64:65], v34 offset0:198 offset1:206
	v_lshrrev_b32_e32 v47, 16, v47
	v_add3_u32 v48, v58, v48, s13
	ds_read2_b32 v[66:67], v34 offset0:231 offset1:239
	v_and_or_b32 v47, v48, s14, v47
	s_waitcnt lgkmcnt(3)
	v_bfe_u32 v48, v60, 16, 1
	v_add3_u32 v48, v60, v48, s13
	s_waitcnt lgkmcnt(2)
	v_bfe_u32 v49, v62, 16, 1
	v_lshrrev_b32_e32 v48, 16, v48
	v_add3_u32 v49, v62, v49, s13
	v_and_or_b32 v48, v49, s14, v48
	s_waitcnt lgkmcnt(1)
	v_bfe_u32 v49, v64, 16, 1
	v_add_u32_e32 v68, s4, v33
	v_add3_u32 v49, v64, v49, s13
	s_waitcnt lgkmcnt(0)
	v_bfe_u32 v50, v66, 16, 1
	v_ashrrev_i32_e32 v69, 31, v68
	v_lshl_add_u64 v[52:53], v[16:17], 0, s[0:1]
	v_lshrrev_b32_e32 v49, 16, v49
	v_add3_u32 v50, v66, v50, s13
	v_lshlrev_b64 v[68:69], 11, v[68:69]
	v_and_or_b32 v49, v50, s14, v49
	v_lshl_add_u64 v[68:69], v[52:53], 0, v[68:69]
	global_store_dwordx4 v[68:69], v[46:49], off
	v_bfe_u32 v50, v67, 16, 1
	v_add3_u32 v50, v67, v50, s13
	v_bfe_u32 v46, v51, 16, 1
	v_add3_u32 v46, v51, v46, s13
	v_bfe_u32 v47, v55, 16, 1
	v_lshrrev_b32_e32 v46, 16, v46
	v_add3_u32 v47, v55, v47, s13
	v_and_or_b32 v46, v47, s14, v46
	v_bfe_u32 v47, v57, 16, 1
	v_add3_u32 v47, v57, v47, s13
	v_bfe_u32 v48, v59, 16, 1
	v_lshrrev_b32_e32 v47, 16, v47
	v_add3_u32 v48, v59, v48, s13
	v_and_or_b32 v47, v48, s14, v47
	v_bfe_u32 v48, v61, 16, 1
	v_add3_u32 v48, v61, v48, s13
	v_bfe_u32 v49, v63, 16, 1
	v_lshrrev_b32_e32 v48, 16, v48
	v_add3_u32 v49, v63, v49, s13
	v_and_or_b32 v48, v49, s14, v48
	v_bfe_u32 v49, v65, 16, 1
	v_add3_u32 v49, v65, v49, s13
	v_lshrrev_b32_e32 v49, 16, v49
	v_and_or_b32 v49, v50, s14, v49
	v_add_u32_e32 v50, s4, v35
	v_ashrrev_i32_e32 v51, 31, v50
	v_lshlrev_b64 v[50:51], 11, v[50:51]
	ds_read2_b32 v[54:55], v34 offset0:16 offset1:24
	v_lshl_add_u64 v[50:51], v[52:53], 0, v[50:51]
	global_store_dwordx4 v[50:51], v[46:49], off
	ds_read2_b32 v[50:51], v34 offset0:49 offset1:57
	ds_read2_b32 v[56:57], v34 offset0:82 offset1:90
	ds_read2_b32 v[58:59], v34 offset0:115 offset1:123
	s_waitcnt lgkmcnt(3)
	v_bfe_u32 v46, v54, 16, 1
	v_add3_u32 v46, v54, v46, s13
	s_waitcnt lgkmcnt(2)
	v_bfe_u32 v47, v50, 16, 1
	ds_read2_b32 v[60:61], v34 offset0:148 offset1:156
	v_lshrrev_b32_e32 v46, 16, v46
	v_add3_u32 v47, v50, v47, s13
	ds_read2_b32 v[62:63], v34 offset0:181 offset1:189
	v_and_or_b32 v46, v47, s14, v46
	s_waitcnt lgkmcnt(3)
	v_bfe_u32 v47, v56, 16, 1
	v_add3_u32 v47, v56, v47, s13
	s_waitcnt lgkmcnt(2)
	v_bfe_u32 v48, v58, 16, 1
	ds_read2_b32 v[64:65], v34 offset0:214 offset1:222
	v_lshrrev_b32_e32 v47, 16, v47
	v_add3_u32 v48, v58, v48, s13
	ds_read2_b32 v[66:67], v34 offset0:247 offset1:255
	v_and_or_b32 v47, v48, s14, v47
	s_waitcnt lgkmcnt(3)
	v_bfe_u32 v48, v60, 16, 1
	v_add3_u32 v48, v60, v48, s13
	s_waitcnt lgkmcnt(2)
	v_bfe_u32 v49, v62, 16, 1
	v_lshrrev_b32_e32 v48, 16, v48
	v_add3_u32 v49, v62, v49, s13
	v_and_or_b32 v48, v49, s14, v48
	s_waitcnt lgkmcnt(1)
	v_bfe_u32 v49, v64, 16, 1
	v_add_u32_e32 v68, s4, v36
	v_add3_u32 v49, v64, v49, s13
	s_waitcnt lgkmcnt(0)
	v_bfe_u32 v50, v66, 16, 1
	v_ashrrev_i32_e32 v69, 31, v68
	v_lshrrev_b32_e32 v49, 16, v49
	v_add3_u32 v50, v66, v50, s13
	v_lshlrev_b64 v[68:69], 11, v[68:69]
	v_and_or_b32 v49, v50, s14, v49
	v_lshl_add_u64 v[68:69], v[52:53], 0, v[68:69]
	global_store_dwordx4 v[68:69], v[46:49], off
	v_bfe_u32 v50, v67, 16, 1
	v_add3_u32 v50, v67, v50, s13
	v_bfe_u32 v46, v55, 16, 1
	v_add3_u32 v46, v55, v46, s13
	v_bfe_u32 v47, v51, 16, 1
	v_lshrrev_b32_e32 v46, 16, v46
	v_add3_u32 v47, v51, v47, s13
	v_and_or_b32 v46, v47, s14, v46
	v_bfe_u32 v47, v57, 16, 1
	v_add3_u32 v47, v57, v47, s13
	v_bfe_u32 v48, v59, 16, 1
	v_lshrrev_b32_e32 v47, 16, v47
	v_add3_u32 v48, v59, v48, s13
	v_and_or_b32 v47, v48, s14, v47
	v_bfe_u32 v48, v61, 16, 1
	v_add3_u32 v48, v61, v48, s13
	v_bfe_u32 v49, v63, 16, 1
	v_lshrrev_b32_e32 v48, 16, v48
	v_add3_u32 v49, v63, v49, s13
	v_and_or_b32 v48, v49, s14, v48
	v_bfe_u32 v49, v65, 16, 1
	v_add3_u32 v49, v65, v49, s13
	v_lshrrev_b32_e32 v49, 16, v49
	v_and_or_b32 v49, v50, s14, v49
	v_add_u32_e32 v50, s4, v37
	v_ashrrev_i32_e32 v51, 31, v50
	v_lshlrev_b64 v[50:51], 11, v[50:51]
	v_lshl_add_u64 v[50:51], v[52:53], 0, v[50:51]
	global_store_dwordx4 v[50:51], v[46:49], off
	s_waitcnt lgkmcnt(0)

; __device__ __forceinline__ void tr_item(const float* W, int ld, int K, int nblk, int item, bf16* WT, bool gu, LAS float* scr, int lane) {
;     ...
;       for (int i = 0; i < 32; ++i) t_[i] = W[(size_t)(k0 + 2 * i + (lane >> 5)) * ld + n0 + (lane & 31)];
; #pragma unroll
;       for (int i = 0; i < 32; ++i) scr[(2 * i + (lane >> 5)) * 33 + (lane & 31)] = t_[i]; }
; __device__ __forceinline__ void convert_items(Frame& F, const Args& a, int lo, int hi, int w, int nw) {
;     ...
;         if (r < I_SI) { tr_item(a.in[10], D + 512, D, 48, r, (bf16*)(F.ws + WS_WSWAIN), false, scr, lane); continue; } r -= I_SI;
.LBB0_575:
	s_andn2_b64 vcc, exec, s[4:5]
	s_cbranch_vccnz .LBB0_577
	s_add_i32 s0, s3, 0xf800
	s_and_b32 s4, s0, 0xffff
	s_mul_i32 s4, s4, 0xaaab
	s_lshr_b32 s5, s4, 21
	s_mul_i32 s4, s5, 48
	s_sub_i32 s0, s0, s4
	s_lshl_b32 s0, s0, 5
	s_and_b32 s4, s0, 0xffe0
	v_lshl_add_u32 v64, s5, 6, v28
	s_lshl_b32 s0, s4, 2
	v_lshl_add_u64 v[46:47], v[6:7], 0, s[0:1]
	v_add_u32_e32 v50, 2, v64
	v_add_u32_e32 v52, 4, v64
	v_add_u32_e32 v54, 6, v64
	v_add_u32_e32 v56, 8, v64
	v_add_u32_e32 v58, 10, v64
	v_add_u32_e32 v60, 12, v64
	v_add_u32_e32 v62, 14, v64
	v_mad_i64_i32 v[48:49], s[6:7], v64, s15, v[46:47]
	v_mad_i64_i32 v[50:51], s[6:7], v50, s15, v[46:47]
	v_mad_i64_i32 v[52:53], s[6:7], v52, s15, v[46:47]
	v_mad_i64_i32 v[54:55], s[6:7], v54, s15, v[46:47]
	v_mad_i64_i32 v[56:57], s[6:7], v56, s15, v[46:47]
	v_mad_i64_i32 v[58:59], s[6:7], v58, s15, v[46:47]
	v_mad_i64_i32 v[60:61], s[6:7], v60, s15, v[46:47]
	v_mad_i64_i32 v[62:63], s[6:7], v62, s15, v[46:47]
	global_load_dword v65, v[48:49], off nt
	global_load_dword v66, v[50:51], off nt
	global_load_dword v67, v[52:53], off nt
	global_load_dword v68, v[54:55], off nt
	global_load_dword v69, v[56:57], off nt
	global_load_dword v70, v[58:59], off nt
	global_load_dword v71, v[60:61], off nt
	global_load_dword v72, v[62:63], off nt
	v_add_u32_e32 v48, 16, v64
	v_add_u32_e32 v50, 18, v64
	v_add_u32_e32 v52, 20, v64
	v_add_u32_e32 v54, 22, v64
	v_add_u32_e32 v56, 24, v64
	v_add_u32_e32 v58, 26, v64
	v_add_u32_e32 v60, 28, v64
	v_add_u32_e32 v62, 30, v64
	v_mad_i64_i32 v[48:49], s[6:7], v48, s15, v[46:47]
	v_mad_i64_i32 v[50:51], s[6:7], v50, s15, v[46:47]
	v_mad_i64_i32 v[52:53], s[6:7], v52, s15, v[46:47]
	v_mad_i64_i32 v[54:55], s[6:7], v54, s15, v[46:47]
	v_mad_i64_i32 v[56:57], s[6:7], v56, s15, v[46:47]
	v_mad_i64_i32 v[58:59], s[6:7], v58, s15, v[46:47]
	v_mad_i64_i32 v[60:61], s[6:7], v60, s15, v[46:47]
	v_mad_i64_i32 v[62:63], s[6:7], v62, s15, v[46:47]
	global_load_dword v73, v[48:49], off nt
	global_load_dword v74, v[50:51], off nt
	global_load_dword v75, v[52:53], off nt
	global_load_dword v76, v[54:55], off nt
	global_load_dword v77, v[56:57], off nt
	global_load_dword v78, v[58:59], off nt
	global_load_dword v79, v[60:61], off nt
	global_load_dword v80, v[62:63], off nt
	v_add_u32_e32 v48, 32, v64
	v_add_u32_e32 v50, 34, v64
	v_add_u32_e32 v52, 36, v64
	v_add_u32_e32 v54, 38, v64
	v_add_u32_e32 v56, 40, v64
	v_add_u32_e32 v58, 42, v64
	v_add_u32_e32 v60, 44, v64
	v_add_u32_e32 v62, 46, v64
	v_mad_i64_i32 v[48:49], s[6:7], v48, s15, v[46:47]
	v_mad_i64_i32 v[50:51], s[6:7], v50, s15, v[46:47]
	v_mad_i64_i32 v[52:53], s[6:7], v52, s15, v[46:47]
	v_mad_i64_i32 v[54:55], s[6:7], v54, s15, v[46:47]
	v_mad_i64_i32 v[56:57], s[6:7], v56, s15, v[46:47]
	v_mad_i64_i32 v[58:59], s[6:7], v58, s15, v[46:47]
	v_mad_i64_i32 v[60:61], s[6:7], v60, s15, v[46:47]
	v_mad_i64_i32 v[62:63], s[6:7], v62, s15, v[46:47]
	global_load_dword v81, v[48:49], off nt
	global_load_dword v82, v[50:51], off nt
	global_load_dword v83, v[52:53], off nt
	global_load_dword v84, v[54:55], off nt
	global_load_dword v85, v[56:57], off nt
	global_load_dword v86, v[58:59], off nt
	global_load_dword v87, v[60:61], off nt
	s_nop 0
	global_load_dword v62, v[62:63], off nt
	v_add_u32_e32 v48, 48, v64
	v_add_u32_e32 v50, 50, v64
	v_add_u32_e32 v52, 52, v64
	v_add_u32_e32 v54, 54, v64
	v_add_u32_e32 v56, 56, v64
	v_add_u32_e32 v58, 58, v64
	v_add_u32_e32 v60, 60, v64
	v_add_u32_e32 v63, 62, v64
	v_mad_i64_i32 v[48:49], s[6:7], v48, s15, v[46:47]
	v_mad_i64_i32 v[50:51], s[6:7], v50, s15, v[46:47]
	v_mad_i64_i32 v[52:53], s[6:7], v52, s15, v[46:47]
	v_mad_i64_i32 v[54:55], s[6:7], v54, s15, v[46:47]
	v_mad_i64_i32 v[56:57], s[6:7], v56, s15, v[46:47]
	v_mad_i64_i32 v[58:59], s[6:7], v58, s15, v[46:47]
	v_mad_i64_i32 v[60:61], s[6:7], v60, s15, v[46:47]
	v_mad_i64_i32 v[46:47], s[6:7], v63, s15, v[46:47]
	global_load_dword v48, v[48:49], off nt
	s_nop 0
	global_load_dword v49, v[50:51], off nt
	s_nop 0
	global_load_dword v50, v[52:53], off nt
	global_load_dword v51, v[54:55], off nt
	s_nop 0
	global_load_dword v52, v[56:57], off nt
	global_load_dword v53, v[58:59], off nt
	global_load_dword v54, v[60:61], off nt
	s_nop 0
	global_load_dword v46, v[46:47], off nt
	s_waitcnt vmcnt(0)
	ds_write2_b32 v29, v65, v66 offset1:66
	ds_write2_b32 v29, v67, v68 offset0:132 offset1:198
	ds_write2_b32 v38, v69, v70 offset0:8 offset1:74
	ds_write2_b32 v38, v71, v72 offset0:140 offset1:206
	ds_write2_b32 v39, v73, v74 offset0:16 offset1:82
	ds_write2_b32 v39, v75, v76 offset0:148 offset1:214
	ds_write2_b32 v40, v77, v78 offset0:24 offset1:90
	ds_write2_b32 v40, v79, v80 offset0:156 offset1:222
	ds_write2_b32 v41, v81, v82 offset0:32 offset1:98
	ds_write2_b32 v41, v83, v84 offset0:164 offset1:230
	ds_write2_b32 v42, v85, v86 offset0:40 offset1:106
	ds_write2_b32 v42, v87, v62 offset0:172 offset1:238
	ds_write2_b32 v43, v48, v49 offset0:48 offset1:114
	ds_write2_b32 v43, v50, v51 offset0:180 offset1:246
	ds_write2_b32 v44, v52, v53 offset0:56 offset1:122
	ds_write2_b32 v44, v54, v46 offset0:188 offset1:254
	s_waitcnt lgkmcnt(0)
; #define GAS __attribute__((address_space(1)))
; #define LAS __attribute__((address_space(3)))
; #define LDS_WAIT() asm volatile("s_waitcnt lgkmcnt(0)" ::: "memory")
; __device__ __forceinline__ unsigned pk2(float lo, float hi) { return f2bf(lo) | (f2bf(hi) << 16); }
; __device__ __forceinline__ void tr_item(const float* W, int ld, int K, int nblk, int item, bf16* WT, bool gu, LAS float* scr, int lane) {
;     ...
;     const int c = lane & 7;
; #pragma unroll
;     for (int j = 0; j < 4; ++j) { const int n = (lane >> 3) + 8 * j; const LAS float* s = scr + (8 * c) * 33 + n;
;         v4u o; o.x = pk2(s[0 * 33], s[1 * 33]); o.y = pk2(s[2 * 33], s[3 * 33]); o.z = pk2(s[4 * 33], s[5 * 33]); o.w = pk2(s[6 * 33], s[7 * 33]);
;         *(GAS v4u*)(WT + (size_t)(drow0 + n) * K + k0 + 8 * c) = o; }
;     LDS_WAIT(); asm volatile("" ::: "memory");
	ds_read2_b32 v[50:51], v34 offset1:8
	ds_read2_b32 v[54:55], v34 offset0:33 offset1:41
	ds_read2_b32 v[56:57], v34 offset0:66 offset1:74
	ds_read2_b32 v[58:59], v34 offset0:99 offset1:107
	ds_read2_b32 v[60:61], v34 offset0:132 offset1:140
	s_waitcnt lgkmcnt(4)
	v_bfe_u32 v46, v50, 16, 1
	v_add3_u32 v46, v50, v46, s13
	s_waitcnt lgkmcnt(3)
	v_bfe_u32 v47, v54, 16, 1
	v_lshrrev_b32_e32 v46, 16, v46
	v_add3_u32 v47, v54, v47, s13
	ds_read2_b32 v[62:63], v34 offset0:165 offset1:173
	v_and_or_b32 v46, v47, s14, v46
	s_waitcnt lgkmcnt(3)
	v_bfe_u32 v47, v56, 16, 1
	v_add3_u32 v47, v56, v47, s13
	s_waitcnt lgkmcnt(2)
	v_bfe_u32 v48, v58, 16, 1
	ds_read2_b32 v[64:65], v34 offset0:198 offset1:206
	v_lshrrev_b32_e32 v47, 16, v47
	v_add3_u32 v48, v58, v48, s13
	ds_read2_b32 v[66:67], v34 offset0:231 offset1:239
	v_and_or_b32 v47, v48, s14, v47
	s_waitcnt lgkmcnt(3)
	v_bfe_u32 v48, v60, 16, 1
	v_add3_u32 v48, v60, v48, s13
	s_waitcnt lgkmcnt(2)
	v_bfe_u32 v49, v62, 16, 1
	v_lshrrev_b32_e32 v48, 16, v48
	v_add3_u32 v49, v62, v49, s13
	v_and_or_b32 v48, v49, s14, v48
	s_waitcnt lgkmcnt(1)
	v_bfe_u32 v49, v64, 16, 1
	v_add_u32_e32 v68, s4, v33
	s_lshl_b32 s0, s5, 7
	v_add3_u32 v49, v64, v49, s13
	s_waitcnt lgkmcnt(0)
	v_bfe_u32 v50, v66, 16, 1
	v_ashrrev_i32_e32 v69, 31, v68
	v_lshl_add_u64 v[52:53], v[18:19], 0, s[0:1]
	v_lshrrev_b32_e32 v49, 16, v49
	v_add3_u32 v50, v66, v50, s13
	v_lshlrev_b64 v[68:69], 11, v[68:69]
	v_and_or_b32 v49, v50, s14, v49
	v_lshl_add_u64 v[68:69], v[52:53], 0, v[68:69]
	global_store_dwordx4 v[68:69], v[46:49], off
	v_bfe_u32 v50, v67, 16, 1
	v_add3_u32 v50, v67, v50, s13
	v_bfe_u32 v46, v51, 16, 1
	v_add3_u32 v46, v51, v46, s13
	v_bfe_u32 v47, v55, 16, 1
	v_lshrrev_b32_e32 v46, 16, v46
	v_add3_u32 v47, v55, v47, s13
	v_and_or_b32 v46, v47, s14, v46
	v_bfe_u32 v47, v57, 16, 1
	v_add3_u32 v47, v57, v47, s13
	v_bfe_u32 v48, v59, 16, 1
	v_lshrrev_b32_e32 v47, 16, v47
	v_add3_u32 v48, v59, v48, s13
	v_and_or_b32 v47, v48, s14, v47
	v_bfe_u32 v48, v61, 16, 1
	v_add3_u32 v48, v61, v48, s13
	v_bfe_u32 v49, v63, 16, 1
	v_lshrrev_b32_e32 v48, 16, v48
	v_add3_u32 v49, v63, v49, s13
	v_and_or_b32 v48, v49, s14, v48
	v_bfe_u32 v49, v65, 16, 1
	v_add3_u32 v49, v65, v49, s13
	v_lshrrev_b32_e32 v49, 16, v49
	v_and_or_b32 v49, v50, s14, v49
	v_add_u32_e32 v50, s4, v35
	v_ashrrev_i32_e32 v51, 31, v50
	v_lshlrev_b64 v[50:51], 11, v[50:51]
	ds_read2_b32 v[54:55], v34 offset0:16 offset1:24
	v_lshl_add_u64 v[50:51], v[52:53], 0, v[50:51]
	global_store_dwordx4 v[50:51], v[46:49], off
	ds_read2_b32 v[50:51], v34 offset0:49 offset1:57
	ds_read2_b32 v[56:57], v34 offset0:82 offset1:90
	ds_read2_b32 v[58:59], v34 offset0:115 offset1:123
	s_waitcnt lgkmcnt(3)
	v_bfe_u32 v46, v54, 16, 1
	v_add3_u32 v46, v54, v46, s13
	s_waitcnt lgkmcnt(2)
	v_bfe_u32 v47, v50, 16, 1
	ds_read2_b32 v[60:61], v34 offset0:148 offset1:156
	v_lshrrev_b32_e32 v46, 16, v46
	v_add3_u32 v47, v50, v47, s13
	ds_read2_b32 v[62:63], v34 offset0:181 offset1:189
	v_and_or_b32 v46, v47, s14, v46
	s_waitcnt lgkmcnt(3)
	v_bfe_u32 v47, v56, 16, 1
	v_add3_u32 v47, v56, v47, s13
	s_waitcnt lgkmcnt(2)
	v_bfe_u32 v48, v58, 16, 1
	ds_read2_b32 v[64:65], v34 offset0:214 offset1:222
	v_lshrrev_b32_e32 v47, 16, v47
	v_add3_u32 v48, v58, v48, s13
	ds_read2_b32 v[66:67], v34 offset0:247 offset1:255
	v_and_or_b32 v47, v48, s14, v47
	s_waitcnt lgkmcnt(3)
	v_bfe_u32 v48, v60, 16, 1
	v_add3_u32 v48, v60, v48, s13
	s_waitcnt lgkmcnt(2)
	v_bfe_u32 v49, v62, 16, 1
	v_lshrrev_b32_e32 v48, 16, v48
	v_add3_u32 v49, v62, v49, s13
	v_and_or_b32 v48, v49, s14, v48
	s_waitcnt lgkmcnt(1)
	v_bfe_u32 v49, v64, 16, 1
	v_add_u32_e32 v68, s4, v36
	v_add3_u32 v49, v64, v49, s13
	s_waitcnt lgkmcnt(0)
	v_bfe_u32 v50, v66, 16, 1
	v_ashrrev_i32_e32 v69, 31, v68
	v_lshrrev_b32_e32 v49, 16, v49
	v_add3_u32 v50, v66, v50, s13
	v_lshlrev_b64 v[68:69], 11, v[68:69]
	v_and_or_b32 v49, v50, s14, v49
	v_lshl_add_u64 v[68:69], v[52:53], 0, v[68:69]
	global_store_dwordx4 v[68:69], v[46:49], off
	v_bfe_u32 v50, v67, 16, 1
	v_add3_u32 v50, v67, v50, s13
	v_bfe_u32 v46, v55, 16, 1
	v_add3_u32 v46, v55, v46, s13
	v_bfe_u32 v47, v51, 16, 1
	v_lshrrev_b32_e32 v46, 16, v46
	v_add3_u32 v47, v51, v47, s13
	v_and_or_b32 v46, v47, s14, v46
	v_bfe_u32 v47, v57, 16, 1
	v_add3_u32 v47, v57, v47, s13
	v_bfe_u32 v48, v59, 16, 1
	v_lshrrev_b32_e32 v47, 16, v47
	v_add3_u32 v48, v59, v48, s13
	v_and_or_b32 v47, v48, s14, v47
	v_bfe_u32 v48, v61, 16, 1
	v_add3_u32 v48, v61, v48, s13
	v_bfe_u32 v49, v63, 16, 1
	v_lshrrev_b32_e32 v48, 16, v48
	v_add3_u32 v49, v63, v49, s13
	v_and_or_b32 v48, v49, s14, v48
	v_bfe_u32 v49, v65, 16, 1
	v_add3_u32 v49, v65, v49, s13
	v_lshrrev_b32_e32 v49, 16, v49
	v_and_or_b32 v49, v50, s14, v49
	v_add_u32_e32 v50, s4, v37
	v_ashrrev_i32_e32 v51, 31, v50
	v_lshlrev_b64 v[50:51], 11, v[50:51]
	v_lshl_add_u64 v[50:51], v[52:53], 0, v[50:51]
	global_store_dwordx4 v[50:51], v[46:49], off
	s_waitcnt lgkmcnt(0)

; #define LDS_WAIT() asm volatile("s_waitcnt lgkmcnt(0)" ::: "memory")
; __device__ __forceinline__ void tr_item(const float* W, int ld, int K, int nblk, int item, bf16* WT, bool gu, LAS float* scr, int lane) {
;     const int kb = item / nblk, nb = item % nblk, k0 = 64 * kb, n0 = 32 * nb;
;     int drow0 = n0;
;     if (gu) { const int bj = n0 / FF, j = n0 - bj * FF; drow0 = 256 * (j / 128) + 128 * bj + (j % 128); }
;     { float t_[32];
; #pragma unroll
;       for (int i = 0; i < 32; ++i) t_[i] = W[(size_t)(k0 + 2 * i + (lane >> 5)) * ld + n0 + (lane & 31)];
; #pragma unroll
;       for (int i = 0; i < 32; ++i) scr[(2 * i + (lane >> 5)) * 33 + (lane & 31)] = t_[i]; }
;     LDS_WAIT(); asm volatile("" ::: "memory");
.LBB0_578:
	s_andn2_b64 vcc, exec, s[4:5]
	s_cbranch_vccnz .LBB0_580
	s_add_i32 s0, s10, 0x2a00
	s_and_b32 s5, s0, 0x1ffc0
	s_and_b32 s4, s9, 0x3e0
	v_add_u32_e32 v46, s5, v28
	s_lshl_b32 s0, s4, 2
	v_ashrrev_i32_e32 v47, 31, v46
	v_lshl_add_u64 v[48:49], v[8:9], 0, s[0:1]
	v_lshlrev_b64 v[46:47], 12, v[46:47]
	v_lshl_add_u64 v[46:47], v[48:49], 0, v[46:47]
	v_add_co_u32_e32 v48, vcc, 0x2000, v46
	s_lshl_b32 s0, s5, 1
	s_nop 0
	v_addc_co_u32_e32 v49, vcc, 0, v47, vcc
	v_add_co_u32_e32 v50, vcc, 0x4000, v46
	s_nop 1
	v_addc_co_u32_e32 v51, vcc, 0, v47, vcc
	v_add_co_u32_e32 v52, vcc, 0x6000, v46
	s_nop 1
	v_addc_co_u32_e32 v53, vcc, 0, v47, vcc
	v_add_co_u32_e32 v54, vcc, 0x8000, v46
	s_nop 1
	v_addc_co_u32_e32 v55, vcc, 0, v47, vcc
	v_add_co_u32_e32 v56, vcc, 0xa000, v46
	s_nop 1
	v_addc_co_u32_e32 v57, vcc, 0, v47, vcc
	v_add_co_u32_e32 v58, vcc, 0xc000, v46
	s_nop 1
	v_addc_co_u32_e32 v59, vcc, 0, v47, vcc
	v_add_co_u32_e32 v60, vcc, 0xe000, v46
	s_nop 1
	v_addc_co_u32_e32 v61, vcc, 0, v47, vcc
	global_load_dword v64, v[46:47], off nt
	global_load_dword v65, v[48:49], off nt
	global_load_dword v66, v[50:51], off nt
	global_load_dword v67, v[52:53], off nt
	global_load_dword v68, v[54:55], off nt
	global_load_dword v69, v[56:57], off nt
	global_load_dword v70, v[58:59], off nt
	global_load_dword v71, v[60:61], off nt
	v_add_co_u32_e32 v48, vcc, 0x10000, v46
	s_nop 1
	v_addc_co_u32_e32 v49, vcc, 0, v47, vcc
	v_add_co_u32_e32 v50, vcc, 0x12000, v46
	s_nop 1
	v_addc_co_u32_e32 v51, vcc, 0, v47, vcc
	v_add_co_u32_e32 v52, vcc, 0x14000, v46
	s_nop 1
	v_addc_co_u32_e32 v53, vcc, 0, v47, vcc
	v_add_co_u32_e32 v54, vcc, 0x16000, v46
	s_nop 1
	v_addc_co_u32_e32 v55, vcc, 0, v47, vcc
	v_add_co_u32_e32 v56, vcc, 0x18000, v46
	s_nop 1
	v_addc_co_u32_e32 v57, vcc, 0, v47, vcc
	v_add_co_u32_e32 v58, vcc, 0x1a000, v46
	s_nop 1
	v_addc_co_u32_e32 v59, vcc, 0, v47, vcc
	v_add_co_u32_e32 v60, vcc, 0x1c000, v46
	s_nop 1
	v_addc_co_u32_e32 v61, vcc, 0, v47, vcc
	v_add_co_u32_e32 v62, vcc, 0x1e000, v46
	s_nop 1
	v_addc_co_u32_e32 v63, vcc, 0, v47, vcc
	global_load_dword v72, v[48:49], off nt
	global_load_dword v73, v[50:51], off nt
	global_load_dword v74, v[52:53], off nt
	global_load_dword v75, v[54:55], off nt
	global_load_dword v76, v[56:57], off nt
	global_load_dword v77, v[58:59], off nt
	global_load_dword v78, v[60:61], off nt
	global_load_dword v79, v[62:63], off nt
	v_add_co_u32_e32 v48, vcc, 0x20000, v46
	s_nop 1
	v_addc_co_u32_e32 v49, vcc, 0, v47, vcc
	v_add_co_u32_e32 v50, vcc, 0x22000, v46
	s_nop 1
	v_addc_co_u32_e32 v51, vcc, 0, v47, vcc
	v_add_co_u32_e32 v52, vcc, 0x24000, v46
	s_nop 1
	v_addc_co_u32_e32 v53, vcc, 0, v47, vcc
	v_add_co_u32_e32 v54, vcc, 0x26000, v46
	s_nop 1
	v_addc_co_u32_e32 v55, vcc, 0, v47, vcc
	v_add_co_u32_e32 v56, vcc, 0x28000, v46
	s_nop 1
	v_addc_co_u32_e32 v57, vcc, 0, v47, vcc
	v_add_co_u32_e32 v58, vcc, 0x2a000, v46
	s_nop 1
	v_addc_co_u32_e32 v59, vcc, 0, v47, vcc
	v_add_co_u32_e32 v60, vcc, 0x2c000, v46
	s_nop 1
	v_addc_co_u32_e32 v61, vcc, 0, v47, vcc
	v_add_co_u32_e32 v62, vcc, 0x2e000, v46
	s_nop 1
	v_addc_co_u32_e32 v63, vcc, 0, v47, vcc
	global_load_dword v80, v[48:49], off nt
	global_load_dword v81, v[50:51], off nt
	global_load_dword v82, v[52:53], off nt
	global_load_dword v83, v[54:55], off nt
	global_load_dword v84, v[56:57], off nt
	global_load_dword v85, v[58:59], off nt
	global_load_dword v86, v[60:61], off nt
	s_nop 0
	global_load_dword v62, v[62:63], off nt
	v_add_co_u32_e32 v48, vcc, 0x30000, v46
	s_nop 1
	v_addc_co_u32_e32 v49, vcc, 0, v47, vcc
	v_add_co_u32_e32 v50, vcc, 0x32000, v46
	s_nop 1
	v_addc_co_u32_e32 v51, vcc, 0, v47, vcc
	v_add_co_u32_e32 v52, vcc, 0x34000, v46
	s_nop 1
	v_addc_co_u32_e32 v53, vcc, 0, v47, vcc
	v_add_co_u32_e32 v54, vcc, 0x36000, v46
	s_nop 1
	v_addc_co_u32_e32 v55, vcc, 0, v47, vcc
	v_add_co_u32_e32 v56, vcc, 0x38000, v46
	s_nop 1
	v_addc_co_u32_e32 v57, vcc, 0, v47, vcc
	v_add_co_u32_e32 v58, vcc, 0x3a000, v46
	s_nop 1
	v_addc_co_u32_e32 v59, vcc, 0, v47, vcc
	v_add_co_u32_e32 v60, vcc, 0x3c000, v46
	s_nop 1
	v_addc_co_u32_e32 v61, vcc, 0, v47, vcc
	v_add_co_u32_e32 v46, vcc, 0x3e000, v46
	s_nop 1
	v_addc_co_u32_e32 v47, vcc, 0, v47, vcc
	global_load_dword v48, v[48:49], off nt
	s_nop 0
	global_load_dword v49, v[50:51], off nt
	s_nop 0
	global_load_dword v50, v[52:53], off nt
	global_load_dword v51, v[54:55], off nt
	s_nop 0
	global_load_dword v52, v[56:57], off nt
	global_load_dword v53, v[58:59], off nt
	global_load_dword v54, v[60:61], off nt
	s_nop 0
	global_load_dword v46, v[46:47], off nt
	s_waitcnt vmcnt(0)
	ds_write2_b32 v29, v64, v65 offset1:66
	ds_write2_b32 v29, v66, v67 offset0:132 offset1:198
	ds_write2_b32 v38, v68, v69 offset0:8 offset1:74
	ds_write2_b32 v38, v70, v71 offset0:140 offset1:206
	ds_write2_b32 v39, v72, v73 offset0:16 offset1:82
	ds_write2_b32 v39, v74, v75 offset0:148 offset1:214
	ds_write2_b32 v40, v76, v77 offset0:24 offset1:90
	ds_write2_b32 v40, v78, v79 offset0:156 offset1:222
	ds_write2_b32 v41, v80, v81 offset0:32 offset1:98
	ds_write2_b32 v41, v82, v83 offset0:164 offset1:230
	ds_write2_b32 v42, v84, v85 offset0:40 offset1:106
	ds_write2_b32 v42, v86, v62 offset0:172 offset1:238
	ds_write2_b32 v43, v48, v49 offset0:48 offset1:114
	ds_write2_b32 v43, v50, v51 offset0:180 offset1:246
	ds_write2_b32 v44, v52, v53 offset0:56 offset1:122
	ds_write2_b32 v44, v54, v46 offset0:188 offset1:254
	s_waitcnt lgkmcnt(0)
; #define GAS __attribute__((address_space(1)))
; #define LAS __attribute__((address_space(3)))
; #define LDS_WAIT() asm volatile("s_waitcnt lgkmcnt(0)" ::: "memory")
; __device__ __forceinline__ unsigned pk2(float lo, float hi) { return f2bf(lo) | (f2bf(hi) << 16); }
; __device__ __forceinline__ void tr_item(const float* W, int ld, int K, int nblk, int item, bf16* WT, bool gu, LAS float* scr, int lane) {
;     ...
;     const int c = lane & 7;
; #pragma unroll
;     for (int j = 0; j < 4; ++j) { const int n = (lane >> 3) + 8 * j; const LAS float* s = scr + (8 * c) * 33 + n;
;         v4u o; o.x = pk2(s[0 * 33], s[1 * 33]); o.y = pk2(s[2 * 33], s[3 * 33]); o.z = pk2(s[4 * 33], s[5 * 33]); o.w = pk2(s[6 * 33], s[7 * 33]);
;         *(GAS v4u*)(WT + (size_t)(drow0 + n) * K + k0 + 8 * c) = o; }
;     LDS_WAIT(); asm volatile("" ::: "memory");
	ds_read2_b32 v[50:51], v34 offset1:8
	ds_read2_b32 v[54:55], v34 offset0:33 offset1:41
	ds_read2_b32 v[56:57], v34 offset0:66 offset1:74
	ds_read2_b32 v[58:59], v34 offset0:99 offset1:107
	ds_read2_b32 v[60:61], v34 offset0:132 offset1:140
	s_waitcnt lgkmcnt(4)
	v_bfe_u32 v46, v50, 16, 1
	v_add3_u32 v46, v50, v46, s13
	s_waitcnt lgkmcnt(3)
	v_bfe_u32 v47, v54, 16, 1
	v_lshrrev_b32_e32 v46, 16, v46
	v_add3_u32 v47, v54, v47, s13
	ds_read2_b32 v[62:63], v34 offset0:165 offset1:173
	v_and_or_b32 v46, v47, s14, v46
	s_waitcnt lgkmcnt(3)
	v_bfe_u32 v47, v56, 16, 1
	v_add3_u32 v47, v56, v47, s13
	s_waitcnt lgkmcnt(2)
	v_bfe_u32 v48, v58, 16, 1
	ds_read2_b32 v[64:65], v34 offset0:198 offset1:206
	v_lshrrev_b32_e32 v47, 16, v47
	v_add3_u32 v48, v58, v48, s13
	ds_read2_b32 v[66:67], v34 offset0:231 offset1:239
	v_and_or_b32 v47, v48, s14, v47
	s_waitcnt lgkmcnt(3)
	v_bfe_u32 v48, v60, 16, 1
	v_add3_u32 v48, v60, v48, s13
	s_waitcnt lgkmcnt(2)
	v_bfe_u32 v49, v62, 16, 1
	v_lshrrev_b32_e32 v48, 16, v48
	v_add3_u32 v49, v62, v49, s13
	v_and_or_b32 v48, v49, s14, v48
	s_waitcnt lgkmcnt(1)
	v_bfe_u32 v49, v64, 16, 1
	v_add_u32_e32 v68, s4, v33
	v_add3_u32 v49, v64, v49, s13
	s_waitcnt lgkmcnt(0)
	v_bfe_u32 v50, v66, 16, 1
	v_ashrrev_i32_e32 v69, 31, v68
	v_lshl_add_u64 v[52:53], v[20:21], 0, s[0:1]
	v_lshrrev_b32_e32 v49, 16, v49
	v_add3_u32 v50, v66, v50, s13
	v_lshlrev_b64 v[68:69], 11, v[68:69]
	v_and_or_b32 v49, v50, s14, v49
	v_lshl_add_u64 v[68:69], v[52:53], 0, v[68:69]
	global_store_dwordx4 v[68:69], v[46:49], off
	v_bfe_u32 v50, v67, 16, 1
	v_add3_u32 v50, v67, v50, s13
	v_bfe_u32 v46, v51, 16, 1
	v_add3_u32 v46, v51, v46, s13
	v_bfe_u32 v47, v55, 16, 1
	v_lshrrev_b32_e32 v46, 16, v46
	v_add3_u32 v47, v55, v47, s13
	v_and_or_b32 v46, v47, s14, v46
	v_bfe_u32 v47, v57, 16, 1
	v_add3_u32 v47, v57, v47, s13
	v_bfe_u32 v48, v59, 16, 1
	v_lshrrev_b32_e32 v47, 16, v47
	v_add3_u32 v48, v59, v48, s13
	v_and_or_b32 v47, v48, s14, v47
	v_bfe_u32 v48, v61, 16, 1
	v_add3_u32 v48, v61, v48, s13
	v_bfe_u32 v49, v63, 16, 1
	v_lshrrev_b32_e32 v48, 16, v48
	v_add3_u32 v49, v63, v49, s13
	v_and_or_b32 v48, v49, s14, v48
	v_bfe_u32 v49, v65, 16, 1
	v_add3_u32 v49, v65, v49, s13
	v_lshrrev_b32_e32 v49, 16, v49
	v_and_or_b32 v49, v50, s14, v49
	v_add_u32_e32 v50, s4, v35
	v_ashrrev_i32_e32 v51, 31, v50
	v_lshlrev_b64 v[50:51], 11, v[50:51]
	ds_read2_b32 v[54:55], v34 offset0:16 offset1:24
	v_lshl_add_u64 v[50:51], v[52:53], 0, v[50:51]
	global_store_dwordx4 v[50:51], v[46:49], off
	ds_read2_b32 v[50:51], v34 offset0:49 offset1:57
	ds_read2_b32 v[56:57], v34 offset0:82 offset1:90
	ds_read2_b32 v[58:59], v34 offset0:115 offset1:123
	s_waitcnt lgkmcnt(3)
	v_bfe_u32 v46, v54, 16, 1
	v_add3_u32 v46, v54, v46, s13
	s_waitcnt lgkmcnt(2)
	v_bfe_u32 v47, v50, 16, 1
	ds_read2_b32 v[60:61], v34 offset0:148 offset1:156
	v_lshrrev_b32_e32 v46, 16, v46
	v_add3_u32 v47, v50, v47, s13
	ds_read2_b32 v[62:63], v34 offset0:181 offset1:189
	v_and_or_b32 v46, v47, s14, v46
	s_waitcnt lgkmcnt(3)
	v_bfe_u32 v47, v56, 16, 1
	v_add3_u32 v47, v56, v47, s13
	s_waitcnt lgkmcnt(2)
	v_bfe_u32 v48, v58, 16, 1
	ds_read2_b32 v[64:65], v34 offset0:214 offset1:222
	v_lshrrev_b32_e32 v47, 16, v47
	v_add3_u32 v48, v58, v48, s13
	ds_read2_b32 v[66:67], v34 offset0:247 offset1:255
	v_and_or_b32 v47, v48, s14, v47
	s_waitcnt lgkmcnt(3)
	v_bfe_u32 v48, v60, 16, 1
	v_add3_u32 v48, v60, v48, s13
	s_waitcnt lgkmcnt(2)
	v_bfe_u32 v49, v62, 16, 1
	v_lshrrev_b32_e32 v48, 16, v48
	v_add3_u32 v49, v62, v49, s13
	v_and_or_b32 v48, v49, s14, v48
	s_waitcnt lgkmcnt(1)
	v_bfe_u32 v49, v64, 16, 1
	v_add_u32_e32 v68, s4, v36
	v_add3_u32 v49, v64, v49, s13
	s_waitcnt lgkmcnt(0)
	v_bfe_u32 v50, v66, 16, 1
	v_ashrrev_i32_e32 v69, 31, v68
	v_lshrrev_b32_e32 v49, 16, v49
	v_add3_u32 v50, v66, v50, s13
	v_lshlrev_b64 v[68:69], 11, v[68:69]
	v_and_or_b32 v49, v50, s14, v49
	v_lshl_add_u64 v[68:69], v[52:53], 0, v[68:69]
	global_store_dwordx4 v[68:69], v[46:49], off
	v_bfe_u32 v50, v67, 16, 1
	v_add3_u32 v50, v67, v50, s13
	v_bfe_u32 v46, v55, 16, 1
	v_add3_u32 v46, v55, v46, s13
	v_bfe_u32 v47, v51, 16, 1
	v_lshrrev_b32_e32 v46, 16, v46
	v_add3_u32 v47, v51, v47, s13
	v_and_or_b32 v46, v47, s14, v46
	v_bfe_u32 v47, v57, 16, 1
	v_add3_u32 v47, v57, v47, s13
	v_bfe_u32 v48, v59, 16, 1
	v_lshrrev_b32_e32 v47, 16, v47
	v_add3_u32 v48, v59, v48, s13
	v_and_or_b32 v47, v48, s14, v47
	v_bfe_u32 v48, v61, 16, 1
	v_add3_u32 v48, v61, v48, s13
	v_bfe_u32 v49, v63, 16, 1
	v_lshrrev_b32_e32 v48, 16, v48
	v_add3_u32 v49, v63, v49, s13
	v_and_or_b32 v48, v49, s14, v48
	v_bfe_u32 v49, v65, 16, 1
	v_add3_u32 v49, v65, v49, s13
	v_lshrrev_b32_e32 v49, 16, v49
	v_and_or_b32 v49, v50, s14, v49
	v_add_u32_e32 v50, s4, v37
	v_ashrrev_i32_e32 v51, 31, v50
	v_lshlrev_b64 v[50:51], 11, v[50:51]
	v_lshl_add_u64 v[50:51], v[52:53], 0, v[50:51]
	global_store_dwordx4 v[50:51], v[46:49], off
	s_waitcnt lgkmcnt(0)

; #define LDS_WAIT() asm volatile("s_waitcnt lgkmcnt(0)" ::: "memory")
; __device__ __forceinline__ void tr_item(const float* W, int ld, int K, int nblk, int item, bf16* WT, bool gu, LAS float* scr, int lane) {
;     const int kb = item / nblk, nb = item % nblk, k0 = 64 * kb, n0 = 32 * nb;
;     int drow0 = n0;
;     if (gu) { const int bj = n0 / FF, j = n0 - bj * FF; drow0 = 256 * (j / 128) + 128 * bj + (j % 128); }
;     { float t_[32];
; #pragma unroll
;       for (int i = 0; i < 32; ++i) t_[i] = W[(size_t)(k0 + 2 * i + (lane >> 5)) * ld + n0 + (lane & 31)];
; #pragma unroll
;       for (int i = 0; i < 32; ++i) scr[(2 * i + (lane >> 5)) * 33 + (lane & 31)] = t_[i]; }
;     LDS_WAIT(); asm volatile("" ::: "memory");
.LBB0_581:
	s_andn2_b64 vcc, exec, s[4:5]
	s_cbranch_vccnz .LBB0_558
	s_mul_hi_i32 s0, s3, 0x2aaaaaab
	s_lshr_b32 s4, s0, 31
	s_ashr_i32 s0, s0, 4
	s_add_i32 s0, s0, s4
	s_lshl_b32 s6, s0, 6
	s_mulk_i32 s0, 0xf400
	s_add_i32 s4, s9, s0
	v_add_u32_e32 v64, s6, v28
	s_ashr_i32 s5, s4, 31
	v_lshl_add_u64 v[46:47], s[4:5], 2, v[10:11]
	v_add_u32_e32 v50, 2, v64
	v_add_u32_e32 v52, 4, v64
	v_add_u32_e32 v54, 6, v64
	v_add_u32_e32 v56, 8, v64
	v_add_u32_e32 v58, 10, v64
	v_add_u32_e32 v60, 12, v64
	v_add_u32_e32 v62, 14, v64
	v_mad_i64_i32 v[48:49], s[18:19], v64, s16, v[46:47]
	v_mad_i64_i32 v[50:51], s[18:19], v50, s16, v[46:47]
	v_mad_i64_i32 v[52:53], s[18:19], v52, s16, v[46:47]
	v_mad_i64_i32 v[54:55], s[18:19], v54, s16, v[46:47]
	v_mad_i64_i32 v[56:57], s[18:19], v56, s16, v[46:47]
	v_mad_i64_i32 v[58:59], s[18:19], v58, s16, v[46:47]
	v_mad_i64_i32 v[60:61], s[18:19], v60, s16, v[46:47]
	v_mad_i64_i32 v[62:63], s[18:19], v62, s16, v[46:47]
	global_load_dword v65, v[48:49], off nt
	global_load_dword v66, v[50:51], off nt
	global_load_dword v67, v[52:53], off nt
	global_load_dword v68, v[54:55], off nt
	global_load_dword v69, v[56:57], off nt
	global_load_dword v70, v[58:59], off nt
	global_load_dword v71, v[60:61], off nt
	global_load_dword v72, v[62:63], off nt
	v_add_u32_e32 v48, 16, v64
	v_add_u32_e32 v50, 18, v64
	v_add_u32_e32 v52, 20, v64
	v_add_u32_e32 v54, 22, v64
	v_add_u32_e32 v56, 24, v64
	v_add_u32_e32 v58, 26, v64
	v_add_u32_e32 v60, 28, v64
	v_add_u32_e32 v62, 30, v64
	v_mad_i64_i32 v[48:49], s[18:19], v48, s16, v[46:47]
	v_mad_i64_i32 v[50:51], s[18:19], v50, s16, v[46:47]
	v_mad_i64_i32 v[52:53], s[18:19], v52, s16, v[46:47]
	v_mad_i64_i32 v[54:55], s[18:19], v54, s16, v[46:47]
	v_mad_i64_i32 v[56:57], s[18:19], v56, s16, v[46:47]
	v_mad_i64_i32 v[58:59], s[18:19], v58, s16, v[46:47]
	v_mad_i64_i32 v[60:61], s[18:19], v60, s16, v[46:47]
	v_mad_i64_i32 v[62:63], s[18:19], v62, s16, v[46:47]
	global_load_dword v73, v[48:49], off nt
	global_load_dword v74, v[50:51], off nt
	global_load_dword v75, v[52:53], off nt
	global_load_dword v76, v[54:55], off nt
	global_load_dword v77, v[56:57], off nt
	global_load_dword v78, v[58:59], off nt
	global_load_dword v79, v[60:61], off nt
	global_load_dword v80, v[62:63], off nt
	v_add_u32_e32 v48, 32, v64
	v_add_u32_e32 v50, 34, v64
	v_add_u32_e32 v52, 36, v64
	v_add_u32_e32 v54, 38, v64
	v_add_u32_e32 v56, 40, v64
	v_add_u32_e32 v58, 42, v64
	v_add_u32_e32 v60, 44, v64
	v_add_u32_e32 v62, 46, v64
	v_mad_i64_i32 v[48:49], s[18:19], v48, s16, v[46:47]
	v_mad_i64_i32 v[50:51], s[18:19], v50, s16, v[46:47]
	v_mad_i64_i32 v[52:53], s[18:19], v52, s16, v[46:47]
	v_mad_i64_i32 v[54:55], s[18:19], v54, s16, v[46:47]
	v_mad_i64_i32 v[56:57], s[18:19], v56, s16, v[46:47]
	v_mad_i64_i32 v[58:59], s[18:19], v58, s16, v[46:47]
	v_mad_i64_i32 v[60:61], s[18:19], v60, s16, v[46:47]
	v_mad_i64_i32 v[62:63], s[18:19], v62, s16, v[46:47]
	global_load_dword v81, v[48:49], off nt
	global_load_dword v82, v[50:51], off nt
	global_load_dword v83, v[52:53], off nt
	global_load_dword v84, v[54:55], off nt
	global_load_dword v85, v[56:57], off nt
	global_load_dword v86, v[58:59], off nt
	global_load_dword v87, v[60:61], off nt
	s_nop 0
	global_load_dword v62, v[62:63], off nt
	v_add_u32_e32 v48, 48, v64
	v_add_u32_e32 v50, 50, v64
	v_add_u32_e32 v52, 52, v64
	v_add_u32_e32 v54, 54, v64
	v_add_u32_e32 v56, 56, v64
	v_add_u32_e32 v58, 58, v64
	v_add_u32_e32 v60, 60, v64
	v_add_u32_e32 v63, 62, v64
	v_mad_i64_i32 v[48:49], s[18:19], v48, s16, v[46:47]
	v_mad_i64_i32 v[50:51], s[18:19], v50, s16, v[46:47]
	v_mad_i64_i32 v[52:53], s[18:19], v52, s16, v[46:47]
	v_mad_i64_i32 v[54:55], s[18:19], v54, s16, v[46:47]
	v_mad_i64_i32 v[56:57], s[18:19], v56, s16, v[46:47]
	v_mad_i64_i32 v[58:59], s[18:19], v58, s16, v[46:47]
	v_mad_i64_i32 v[60:61], s[18:19], v60, s16, v[46:47]
	v_mad_i64_i32 v[46:47], s[18:19], v63, s16, v[46:47]
	global_load_dword v48, v[48:49], off nt
	s_nop 0
	global_load_dword v49, v[50:51], off nt
	s_nop 0
	global_load_dword v50, v[52:53], off nt
	global_load_dword v51, v[54:55], off nt
	s_nop 0
	global_load_dword v52, v[56:57], off nt
	global_load_dword v53, v[58:59], off nt
	global_load_dword v54, v[60:61], off nt
	s_nop 0
	global_load_dword v46, v[46:47], off nt
	s_waitcnt vmcnt(0)
	ds_write2_b32 v29, v65, v66 offset1:66
	ds_write2_b32 v29, v67, v68 offset0:132 offset1:198
	ds_write2_b32 v38, v69, v70 offset0:8 offset1:74
	ds_write2_b32 v38, v71, v72 offset0:140 offset1:206
	ds_write2_b32 v39, v73, v74 offset0:16 offset1:82
	ds_write2_b32 v39, v75, v76 offset0:148 offset1:214
	ds_write2_b32 v40, v77, v78 offset0:24 offset1:90
	ds_write2_b32 v40, v79, v80 offset0:156 offset1:222
	ds_write2_b32 v41, v81, v82 offset0:32 offset1:98
	ds_write2_b32 v41, v83, v84 offset0:164 offset1:230
	ds_write2_b32 v42, v85, v86 offset0:40 offset1:106
	ds_write2_b32 v42, v87, v62 offset0:172 offset1:238
	ds_write2_b32 v43, v48, v49 offset0:48 offset1:114
	ds_write2_b32 v43, v50, v51 offset0:180 offset1:246
	ds_write2_b32 v44, v52, v53 offset0:56 offset1:122
	ds_write2_b32 v44, v54, v46 offset0:188 offset1:254
	s_waitcnt lgkmcnt(0)
; #define GAS __attribute__((address_space(1)))
; #define LAS __attribute__((address_space(3)))
; #define LDS_WAIT() asm volatile("s_waitcnt lgkmcnt(0)" ::: "memory")
; __device__ __forceinline__ unsigned pk2(float lo, float hi) { return f2bf(lo) | (f2bf(hi) << 16); }
; __device__ __forceinline__ void tr_item(const float* W, int ld, int K, int nblk, int item, bf16* WT, bool gu, LAS float* scr, int lane) {
;     ...
;     const int c = lane & 7;
; #pragma unroll
;     for (int j = 0; j < 4; ++j) { const int n = (lane >> 3) + 8 * j; const LAS float* s = scr + (8 * c) * 33 + n;
;         v4u o; o.x = pk2(s[0 * 33], s[1 * 33]); o.y = pk2(s[2 * 33], s[3 * 33]); o.z = pk2(s[4 * 33], s[5 * 33]); o.w = pk2(s[6 * 33], s[7 * 33]);
;         *(GAS v4u*)(WT + (size_t)(drow0 + n) * K + k0 + 8 * c) = o; }
;     LDS_WAIT(); asm volatile("" ::: "memory");
	ds_read2_b32 v[50:51], v34 offset1:8
	ds_read2_b32 v[54:55], v34 offset0:33 offset1:41
	ds_read2_b32 v[56:57], v34 offset0:66 offset1:74
	ds_read2_b32 v[58:59], v34 offset0:99 offset1:107
	ds_read2_b32 v[60:61], v34 offset0:132 offset1:140
	s_waitcnt lgkmcnt(4)
	v_bfe_u32 v46, v50, 16, 1
	v_add3_u32 v46, v50, v46, s13
	s_waitcnt lgkmcnt(3)
	v_bfe_u32 v47, v54, 16, 1
	v_lshrrev_b32_e32 v46, 16, v46
	v_add3_u32 v47, v54, v47, s13
	ds_read2_b32 v[62:63], v34 offset0:165 offset1:173
	v_and_or_b32 v46, v47, s14, v46
	s_waitcnt lgkmcnt(3)
	v_bfe_u32 v47, v56, 16, 1
	v_add3_u32 v47, v56, v47, s13
	s_waitcnt lgkmcnt(2)
	v_bfe_u32 v48, v58, 16, 1
	ds_read2_b32 v[64:65], v34 offset0:198 offset1:206
	v_lshrrev_b32_e32 v47, 16, v47
	v_add3_u32 v48, v58, v48, s13
	ds_read2_b32 v[66:67], v34 offset0:231 offset1:239
	v_and_or_b32 v47, v48, s14, v47
	s_waitcnt lgkmcnt(3)
	v_bfe_u32 v48, v60, 16, 1
	v_add3_u32 v48, v60, v48, s13
	s_waitcnt lgkmcnt(2)
	v_bfe_u32 v49, v62, 16, 1
	v_lshrrev_b32_e32 v48, 16, v48
	v_add3_u32 v49, v62, v49, s13
	v_and_or_b32 v48, v49, s14, v48
	s_waitcnt lgkmcnt(1)
	v_bfe_u32 v49, v64, 16, 1
	v_add_u32_e32 v68, s4, v33
	s_ashr_i32 s7, s6, 31
	v_add3_u32 v49, v64, v49, s13
	s_waitcnt lgkmcnt(0)
	v_bfe_u32 v50, v66, 16, 1
	v_ashrrev_i32_e32 v69, 31, v68
	v_lshl_add_u64 v[52:53], s[6:7], 1, v[22:23]
	v_lshrrev_b32_e32 v49, 16, v49
	v_add3_u32 v50, v66, v50, s13
	v_lshlrev_b64 v[70:71], 11, v[68:69]
	v_and_or_b32 v49, v50, s14, v49
	v_lshl_add_u64 v[70:71], v[52:53], 0, v[70:71]
	global_store_dwordx4 v[70:71], v[46:49], off
	v_bfe_u32 v50, v67, 16, 1
	v_add3_u32 v50, v67, v50, s13
	v_bfe_u32 v46, v51, 16, 1
	v_add3_u32 v46, v51, v46, s13
	v_bfe_u32 v47, v55, 16, 1
	v_lshrrev_b32_e32 v46, 16, v46
	v_add3_u32 v47, v55, v47, s13
	v_and_or_b32 v46, v47, s14, v46
	v_bfe_u32 v47, v57, 16, 1
	v_add3_u32 v47, v57, v47, s13
	v_bfe_u32 v48, v59, 16, 1
	v_lshrrev_b32_e32 v47, 16, v47
	v_add3_u32 v48, v59, v48, s13
	v_and_or_b32 v47, v48, s14, v47
	v_bfe_u32 v48, v61, 16, 1
	v_add3_u32 v48, v61, v48, s13
	v_bfe_u32 v49, v63, 16, 1
	v_lshrrev_b32_e32 v48, 16, v48
	v_add3_u32 v49, v63, v49, s13
	v_and_or_b32 v48, v49, s14, v48
	v_bfe_u32 v49, v65, 16, 1
	v_add3_u32 v49, v65, v49, s13
	v_lshrrev_b32_e32 v49, 16, v49
	v_and_or_b32 v49, v50, s14, v49
	v_add_u32_e32 v50, 8, v68
	v_ashrrev_i32_e32 v51, 31, v50
	v_lshlrev_b64 v[50:51], 11, v[50:51]
	ds_read2_b32 v[54:55], v34 offset0:16 offset1:24
	v_lshl_add_u64 v[50:51], v[52:53], 0, v[50:51]
	global_store_dwordx4 v[50:51], v[46:49], off
	ds_read2_b32 v[50:51], v34 offset0:49 offset1:57
	ds_read2_b32 v[56:57], v34 offset0:82 offset1:90
	ds_read2_b32 v[58:59], v34 offset0:115 offset1:123
	s_waitcnt lgkmcnt(3)
	v_bfe_u32 v46, v54, 16, 1
	v_add3_u32 v46, v54, v46, s13
	s_waitcnt lgkmcnt(2)
	v_bfe_u32 v47, v50, 16, 1
	ds_read2_b32 v[60:61], v34 offset0:148 offset1:156
	v_lshrrev_b32_e32 v46, 16, v46
	v_add3_u32 v47, v50, v47, s13
	ds_read2_b32 v[62:63], v34 offset0:181 offset1:189
	v_and_or_b32 v46, v47, s14, v46
	s_waitcnt lgkmcnt(3)
	v_bfe_u32 v47, v56, 16, 1
	v_add3_u32 v47, v56, v47, s13
	s_waitcnt lgkmcnt(2)
	v_bfe_u32 v48, v58, 16, 1
	ds_read2_b32 v[64:65], v34 offset0:214 offset1:222
	v_lshrrev_b32_e32 v47, 16, v47
	v_add3_u32 v48, v58, v48, s13
	ds_read2_b32 v[66:67], v34 offset0:247 offset1:255
	v_and_or_b32 v47, v48, s14, v47
	s_waitcnt lgkmcnt(3)
	v_bfe_u32 v48, v60, 16, 1
	v_add3_u32 v48, v60, v48, s13
	s_waitcnt lgkmcnt(2)
	v_bfe_u32 v49, v62, 16, 1
	v_lshrrev_b32_e32 v48, 16, v48
	v_add3_u32 v49, v62, v49, s13
	v_and_or_b32 v48, v49, s14, v48
	s_waitcnt lgkmcnt(1)
	v_bfe_u32 v49, v64, 16, 1
	v_add_u32_e32 v70, 16, v68
	v_add3_u32 v49, v64, v49, s13
	s_waitcnt lgkmcnt(0)
	v_bfe_u32 v50, v66, 16, 1
	v_ashrrev_i32_e32 v71, 31, v70
	v_lshrrev_b32_e32 v49, 16, v49
	v_add3_u32 v50, v66, v50, s13
	v_lshlrev_b64 v[70:71], 11, v[70:71]
	v_and_or_b32 v49, v50, s14, v49
	v_lshl_add_u64 v[70:71], v[52:53], 0, v[70:71]
	global_store_dwordx4 v[70:71], v[46:49], off
	v_bfe_u32 v50, v67, 16, 1
	v_add3_u32 v50, v67, v50, s13
	v_bfe_u32 v46, v55, 16, 1
	v_add3_u32 v46, v55, v46, s13
	v_bfe_u32 v47, v51, 16, 1
	v_lshrrev_b32_e32 v46, 16, v46
	v_add3_u32 v47, v51, v47, s13
	v_and_or_b32 v46, v47, s14, v46
	v_bfe_u32 v47, v57, 16, 1
	v_add3_u32 v47, v57, v47, s13
	v_bfe_u32 v48, v59, 16, 1
	v_lshrrev_b32_e32 v47, 16, v47
	v_add3_u32 v48, v59, v48, s13
	v_and_or_b32 v47, v48, s14, v47
	v_bfe_u32 v48, v61, 16, 1
	v_add3_u32 v48, v61, v48, s13
	v_bfe_u32 v49, v63, 16, 1
	v_lshrrev_b32_e32 v48, 16, v48
	v_add3_u32 v49, v63, v49, s13
	v_and_or_b32 v48, v49, s14, v48
	v_bfe_u32 v49, v65, 16, 1
	v_add3_u32 v49, v65, v49, s13
	v_lshrrev_b32_e32 v49, 16, v49
	v_and_or_b32 v49, v50, s14, v49
	v_add_u32_e32 v50, 24, v68
	v_ashrrev_i32_e32 v51, 31, v50
	v_lshlrev_b64 v[50:51], 11, v[50:51]
	v_lshl_add_u64 v[50:51], v[52:53], 0, v[50:51]
	global_store_dwordx4 v[50:51], v[46:49], off
	s_waitcnt lgkmcnt(0)
	s_branch .LBB0_558

; __device__ __forceinline__ void tr_item8(const float* W, int ld, int K, int nblk, int item, unsigned char* WT, bool gu, float scale, LAS float* scr, int lane) {
;     const int kb = item / nblk, nb = item % nblk, k0 = 64 * kb, n0 = 32 * nb;
;     int drow0 = n0;
;     if (gu) { const int bj = n0 / FF, j = n0 - bj * FF; drow0 = 256 * (j / 128) + 128 * bj + (j % 128); }
;     { float t_[32];
; #pragma unroll
;       for (int i = 0; i < 32; ++i) t_[i] = W[(size_t)(k0 + 2 * i + (lane >> 5)) * ld + n0 + (lane & 31)];
; #pragma unroll
; __device__ __forceinline__ void convert_items(Frame& F, const Args& a, int lo, int hi, int w, int nw) {
;     ...
;         int r = it;
;         if (r < I_FI) { tr_item(a.in[7], 3 * D + 16, D, 96, r, (bf16*)(F.ws + WS_WFOXIN), false, scr, lane); continue; } r -= I_FI;
;         if (r < I_FO) { tr_item(a.in[9], D, D, 32, r, (bf16*)(F.ws + WS_WFOXOUT), false, scr, lane); continue; } r -= I_FO;
;         if (r < I_SI) { tr_item(a.in[10], D + 512, D, 48, r, (bf16*)(F.ws + WS_WSWAIN), false, scr, lane); continue; } r -= I_SI;
;         if (r < I_SO) { tr_item(a.in[12], D, D, 32, r, (bf16*)(F.ws + WS_WSWAOUT), false, scr, lane); continue; } r -= I_SO;
;         if (r < I_GU) { tr_item8(a.in[14], 2 * FF, D, 224, r, F.ws + WS_WGU, true, WSC_GU, scr, lane); continue; } r -= I_GU;
;         if (r < I_DN) { tr_item8(a.in[15], D, FF, 32, r, F.ws + WS_WDN, false, WSC_DN, scr, lane); continue; } r -= I_DN;
;         if (r < NE * I_GU) { const int e = r / I_GU, rr = r % I_GU; tr_item8(a.in[18] + (size_t)e * D * 2 * FF, 2 * FF, D, 224, rr, F.ws + WS_WMGU + (size_t)e * 2 * FF * D, true, WSC_GU, scr, lane); continue; } r -= NE * I_GU;
.LBB0_1132:
	s_cmpk_gt_i32 s37, 0x5ff
	s_mov_b64 s[24:25], -1
	s_cbranch_scc0 .LBB0_1154
	s_cmpk_gt_u32 s37, 0x7ff
	s_cbranch_scc0 .LBB0_1151
	s_cmpk_gt_u32 s37, 0xaff
	s_cbranch_scc0 .LBB0_1148
	s_cmpk_gt_u32 s37, 0xcff
	s_cbranch_scc0 .LBB0_1145
	s_cmpk_gt_u32 s37, 0x1aff
	s_cbranch_scc0 .LBB0_1142
	s_cmpk_gt_u32 s37, 0x21ff
	s_cbranch_scc0 .LBB0_1139
	s_add_i32 s16, s37, 0xde00
	s_bfe_u32 s24, s16, 0x70009
	s_mulk_i32 s24, 0x2493
	s_lshr_b32 s24, s24, 16
	s_mul_i32 s25, s24, 0xe00
	s_sub_i32 s16, s16, s25
	s_mul_i32 s25, s24, 0x1c00000
	s_add_u32 s27, s72, s25
	s_addc_u32 s51, s73, 0
	s_mul_i32 s24, s24, 0x700000
	s_add_u32 s24, s3, s24
	s_addc_u32 s25, s30, 0
	s_bfe_u32 s26, s16, 0xb0005
	s_mulk_i32 s26, 0x2493
	s_lshr_b32 s26, s26, 16
	s_mul_i32 s50, s26, 0xe0
	s_sub_i32 s50, s16, s50
	s_lshl_b32 s16, s50, 5
	s_and_b32 s52, s50, 0xffff
	s_cmpk_gt_u32 s52, 0x6f
	s_cselect_b32 s52, 0xfffff200, 0
	s_cselect_b32 s53, 0x80, 0
	s_add_i32 s16, s52, s16
	s_sext_i32_i16 s52, s16
	s_bfe_u32 s52, s52, 0x70018
	s_add_i32 s52, s16, s52
	s_sext_i32_i16 s54, s52
	s_and_b32 s52, s52, 0xff80
	s_sub_i32 s16, s16, s52
	s_lshl_b32 s54, s54, 1
	s_sext_i32_i16 s16, s16
	s_and_b32 s54, s54, 0xffffff00
	s_add_i32 s16, s53, s16
	s_lshl_b32 s50, s50, 7
	s_add_i32 s16, s16, s54
	s_lshl_b32 s26, s26, 6
	s_and_b32 s50, s50, 0x3ff80
	s_add_u32 s50, s27, s50
	s_addc_u32 s51, s51, 0
	v_add_u32_e32 v50, s26, v30
	v_lshl_add_u64 v[28:29], s[50:51], 0, v[0:1]
	v_mad_i64_i32 v[48:49], s[50:51], v50, s45, v[28:29]
	global_load_dword v51, v[48:49], off nt
	v_add_u32_e32 v48, 2, v50
	v_mad_i64_i32 v[48:49], s[50:51], v48, s45, v[28:29]
	global_load_dword v52, v[48:49], off nt
	v_add_u32_e32 v48, 4, v50
	v_mad_i64_i32 v[48:49], s[50:51], v48, s45, v[28:29]
	global_load_dword v53, v[48:49], off nt
	v_add_u32_e32 v48, 6, v50
	v_mad_i64_i32 v[48:49], s[50:51], v48, s45, v[28:29]
	global_load_dword v54, v[48:49], off nt
	v_add_u32_e32 v48, 8, v50
	v_mad_i64_i32 v[48:49], s[50:51], v48, s45, v[28:29]
	global_load_dword v55, v[48:49], off nt
	v_add_u32_e32 v48, 10, v50
	v_mad_i64_i32 v[48:49], s[50:51], v48, s45, v[28:29]
	global_load_dword v56, v[48:49], off nt
	v_add_u32_e32 v48, 12, v50
	v_mad_i64_i32 v[48:49], s[50:51], v48, s45, v[28:29]
	global_load_dword v57, v[48:49], off nt
	v_add_u32_e32 v48, 14, v50
	v_mad_i64_i32 v[48:49], s[50:51], v48, s45, v[28:29]
	global_load_dword v58, v[48:49], off nt
	v_add_u32_e32 v48, 16, v50
	v_mad_i64_i32 v[48:49], s[50:51], v48, s45, v[28:29]
	global_load_dword v59, v[48:49], off nt
	v_add_u32_e32 v48, 18, v50
	v_mad_i64_i32 v[48:49], s[50:51], v48, s45, v[28:29]
	global_load_dword v60, v[48:49], off nt
	v_add_u32_e32 v48, 20, v50
	v_mad_i64_i32 v[48:49], s[50:51], v48, s45, v[28:29]
	global_load_dword v61, v[48:49], off nt
	v_add_u32_e32 v48, 22, v50
	v_mad_i64_i32 v[48:49], s[50:51], v48, s45, v[28:29]
	global_load_dword v62, v[48:49], off nt
	v_add_u32_e32 v48, 24, v50
	v_mad_i64_i32 v[48:49], s[50:51], v48, s45, v[28:29]
	global_load_dword v63, v[48:49], off nt
	v_add_u32_e32 v48, 26, v50
	v_mad_i64_i32 v[48:49], s[50:51], v48, s45, v[28:29]
	global_load_dword v64, v[48:49], off nt
	v_add_u32_e32 v48, 28, v50
	v_mad_i64_i32 v[48:49], s[50:51], v48, s45, v[28:29]
	global_load_dword v65, v[48:49], off nt
	v_add_u32_e32 v48, 30, v50
	v_mad_i64_i32 v[48:49], s[50:51], v48, s45, v[28:29]
	global_load_dword v66, v[48:49], off nt
	v_add_u32_e32 v48, 32, v50
	v_mad_i64_i32 v[48:49], s[50:51], v48, s45, v[28:29]
	global_load_dword v67, v[48:49], off nt
	v_add_u32_e32 v48, 34, v50
	v_mad_i64_i32 v[48:49], s[50:51], v48, s45, v[28:29]
	global_load_dword v68, v[48:49], off nt
	v_add_u32_e32 v48, 36, v50
	v_mad_i64_i32 v[48:49], s[50:51], v48, s45, v[28:29]
	global_load_dword v69, v[48:49], off nt
	v_add_u32_e32 v48, 38, v50
	v_mad_i64_i32 v[48:49], s[50:51], v48, s45, v[28:29]
	global_load_dword v70, v[48:49], off nt
	v_add_u32_e32 v48, 40, v50
	v_mad_i64_i32 v[48:49], s[50:51], v48, s45, v[28:29]
	global_load_dword v71, v[48:49], off nt
	v_add_u32_e32 v48, 42, v50
	v_mad_i64_i32 v[48:49], s[50:51], v48, s45, v[28:29]
	global_load_dword v72, v[48:49], off nt
	v_add_u32_e32 v48, 44, v50
	v_mad_i64_i32 v[48:49], s[50:51], v48, s45, v[28:29]
	global_load_dword v73, v[48:49], off nt
	v_add_u32_e32 v48, 46, v50
	v_mad_i64_i32 v[48:49], s[50:51], v48, s45, v[28:29]
	global_load_dword v74, v[48:49], off nt
	v_add_u32_e32 v48, 48, v50
	v_mad_i64_i32 v[48:49], s[50:51], v48, s45, v[28:29]
	global_load_dword v75, v[48:49], off nt
	v_add_u32_e32 v48, 50, v50
	v_mad_i64_i32 v[48:49], s[50:51], v48, s45, v[28:29]
	global_load_dword v76, v[48:49], off nt
	v_add_u32_e32 v48, 52, v50
	v_mad_i64_i32 v[48:49], s[50:51], v48, s45, v[28:29]
	global_load_dword v77, v[48:49], off nt
	v_add_u32_e32 v48, 54, v50
	v_mad_i64_i32 v[48:49], s[50:51], v48, s45, v[28:29]
	global_load_dword v78, v[48:49], off nt
	v_add_u32_e32 v48, 56, v50
	v_mad_i64_i32 v[48:49], s[50:51], v48, s45, v[28:29]
	global_load_dword v79, v[48:49], off nt
	v_add_u32_e32 v48, 58, v50
	v_mad_i64_i32 v[48:49], s[50:51], v48, s45, v[28:29]
	global_load_dword v80, v[48:49], off nt
	v_add_u32_e32 v48, 60, v50
	v_mad_i64_i32 v[48:49], s[50:51], v48, s45, v[28:29]
	global_load_dword v48, v[48:49], off nt
	v_add_u32_e32 v49, 62, v50
	v_mad_i64_i32 v[28:29], s[50:51], v49, s45, v[28:29]
	global_load_dword v28, v[28:29], off nt
	s_waitcnt vmcnt(0)
; __device__ __forceinline__ unsigned cvt_pk4_fp8(float a, float b, float c, float d) { int w = 0; w = __builtin_amdgcn_cvt_pk_fp8_f32(a, b, w, false); w = __builtin_amdgcn_cvt_pk_fp8_f32(c, d, w, true); return (unsigned)w; }
; #define GAS __attribute__((address_space(1)))
; #define LAS __attribute__((address_space(3)))
; #define LDS_WAIT() asm volatile("s_waitcnt lgkmcnt(0)" ::: "memory")
; __device__ __forceinline__ void tr_item8(const float* W, int ld, int K, int nblk, int item, unsigned char* WT, bool gu, float scale, LAS float* scr, int lane) {
;     ...
;       for (int i = 0; i < 32; ++i) scr[(2 * i + (lane >> 5)) * 33 + (lane & 31)] = t_[i] * scale; }
;     LDS_WAIT(); asm volatile("" ::: "memory");
;     const int c = lane & 3;
; #pragma unroll
;     for (int j = 0; j < 2; ++j) { const int n = (lane >> 2) + 16 * j; const LAS float* sp = scr + (16 * c) * 33 + n;
;         v4u o; o.x = pg8::cvt_pk4_fp8(sp[0 * 33], sp[1 * 33], sp[2 * 33], sp[3 * 33]); o.y = pg8::cvt_pk4_fp8(sp[4 * 33], sp[5 * 33], sp[6 * 33], sp[7 * 33]);
;         o.z = pg8::cvt_pk4_fp8(sp[8 * 33], sp[9 * 33], sp[10 * 33], sp[11 * 33]); o.w = pg8::cvt_pk4_fp8(sp[12 * 33], sp[13 * 33], sp[14 * 33], sp[15 * 33]);
;         *(GAS v4u*)(WT + (size_t)(drow0 + n) * K + k0 + 16 * c) = o; }
;     LDS_WAIT(); asm volatile("" ::: "memory");
	v_mul_f32_e32 v29, 0x42800000, v51
	v_mul_f32_e32 v49, 0x42800000, v52
	ds_write2_b32 v31, v29, v49 offset1:66
	v_mul_f32_e32 v29, 0x42800000, v53
	v_mul_f32_e32 v49, 0x42800000, v54
	ds_write2_b32 v31, v29, v49 offset0:132 offset1:198
	v_mul_f32_e32 v29, 0x42800000, v55
	v_mul_f32_e32 v49, 0x42800000, v56
	ds_write2_b32 v40, v29, v49 offset0:8 offset1:74
	v_mul_f32_e32 v29, 0x42800000, v57
	v_mul_f32_e32 v49, 0x42800000, v58
	ds_write2_b32 v40, v29, v49 offset0:140 offset1:206
	v_mul_f32_e32 v29, 0x42800000, v59
	v_mul_f32_e32 v49, 0x42800000, v60
	ds_write2_b32 v41, v29, v49 offset0:16 offset1:82
	v_mul_f32_e32 v29, 0x42800000, v61
	v_mul_f32_e32 v49, 0x42800000, v62
	ds_write2_b32 v41, v29, v49 offset0:148 offset1:214
	v_mul_f32_e32 v29, 0x42800000, v63
	v_mul_f32_e32 v49, 0x42800000, v64
	ds_write2_b32 v42, v29, v49 offset0:24 offset1:90
	v_mul_f32_e32 v29, 0x42800000, v65
	v_mul_f32_e32 v49, 0x42800000, v66
	ds_write2_b32 v42, v29, v49 offset0:156 offset1:222
	v_mul_f32_e32 v29, 0x42800000, v67
	v_mul_f32_e32 v49, 0x42800000, v68
	ds_write2_b32 v43, v29, v49 offset0:32 offset1:98
	v_mul_f32_e32 v29, 0x42800000, v69
	v_mov_b32_e32 v50, v1
	v_mov_b32_e32 v51, v1
	s_add_u32 s24, s24, s26
	v_mul_f32_e32 v49, 0x42800000, v70
	ds_write2_b32 v43, v29, v49 offset0:164 offset1:230
	v_add_u32_e32 v84, s16, v32
	s_addc_u32 s25, s25, 0
	v_mul_f32_e32 v29, 0x42800000, v71
	v_ashrrev_i32_e32 v85, 31, v84
	v_lshlrev_b64 v[84:85], 10, v[84:85]
	v_readlane_b32 s52, v254, 36
	v_mul_f32_e32 v49, 0x42800000, v72
	ds_write2_b32 v44, v29, v49 offset0:40 offset1:106
	v_readlane_b32 s58, v254, 42
	v_readlane_b32 s59, v254, 43
	v_mul_f32_e32 v29, 0x42800000, v73
	v_readlane_b32 s60, v254, 44
	v_readlane_b32 s61, v254, 45
	v_readlane_b32 s62, v254, 46
	v_mul_f32_e32 v49, 0x42800000, v74
	ds_write2_b32 v44, v29, v49 offset0:172 offset1:238
	v_readlane_b32 s63, v254, 47
	v_readlane_b32 s64, v254, 48
	v_mul_f32_e32 v29, 0x42800000, v75
	v_readlane_b32 s65, v254, 49
	v_readlane_b32 s66, v254, 50
	v_readlane_b32 s67, v254, 51
	v_mul_f32_e32 v49, 0x42800000, v76
	ds_write2_b32 v45, v29, v49 offset0:48 offset1:114
	s_mov_b64 s[58:59], s[62:63]
	s_mov_b64 s[60:61], s[64:65]
	v_mul_f32_e32 v29, 0x42800000, v77
	v_readlane_b32 s53, v254, 37
	v_readlane_b32 s54, v254, 38
	v_readlane_b32 s55, v254, 39
	v_mul_f32_e32 v49, 0x42800000, v78
	ds_write2_b32 v45, v29, v49 offset0:180 offset1:246
	v_readlane_b32 s56, v254, 40
	v_readlane_b32 s57, v254, 41
	v_mul_f32_e32 v29, 0x42800000, v79
	s_mov_b64 s[62:63], s[66:67]
	v_mul_f32_e32 v49, 0x42800000, v80
	ds_write2_b32 v46, v29, v49 offset0:56 offset1:122
	v_mov_b32_e32 v49, v1
	v_mul_f32_e32 v29, 0x42800000, v48
	v_mov_b32_e32 v48, v1
	v_mul_f32_e32 v28, 0x42800000, v28
	ds_write2_b32 v46, v29, v28 offset0:188 offset1:254
	s_waitcnt lgkmcnt(0)
	ds_read2_b32 v[52:53], v33 offset1:16
	ds_read2_b32 v[54:55], v33 offset0:33 offset1:49
	ds_read2_b32 v[56:57], v33 offset0:66 offset1:82
	ds_read2_b32 v[58:59], v33 offset0:99 offset1:115
	ds_read2_b32 v[60:61], v33 offset0:132 offset1:148
	ds_read2_b32 v[62:63], v33 offset0:165 offset1:181
	ds_read2_b32 v[64:65], v33 offset0:198 offset1:214
	ds_read2_b32 v[66:67], v33 offset0:231 offset1:247
	ds_read2_b32 v[68:69], v47 offset0:8 offset1:24
	ds_read2_b32 v[70:71], v47 offset0:41 offset1:57
	ds_read2_b32 v[72:73], v47 offset0:74 offset1:90
	ds_read2_b32 v[74:75], v47 offset0:107 offset1:123
	ds_read2_b32 v[76:77], v47 offset0:140 offset1:156
	ds_read2_b32 v[78:79], v47 offset0:173 offset1:189
	ds_read2_b32 v[80:81], v47 offset0:206 offset1:222
	ds_read2_b32 v[82:83], v47 offset0:239 offset1:255
	s_waitcnt lgkmcnt(14)
	v_cvt_pk_fp8_f32 v48, v52, v54
	s_waitcnt lgkmcnt(10)
	v_cvt_pk_fp8_f32 v49, v60, v62
	s_waitcnt lgkmcnt(6)
	v_cvt_pk_fp8_f32 v50, v68, v70
	s_waitcnt lgkmcnt(2)
	v_cvt_pk_fp8_f32 v51, v76, v78
	v_cvt_pk_fp8_f32 v48, v56, v58 op_sel:[0,0,1]
	v_cvt_pk_fp8_f32 v49, v64, v66 op_sel:[0,0,1]
	v_cvt_pk_fp8_f32 v50, v72, v74 op_sel:[0,0,1]
	s_waitcnt lgkmcnt(0)
	v_cvt_pk_fp8_f32 v51, v80, v82 op_sel:[0,0,1]
	v_lshl_add_u64 v[28:29], s[24:25], 0, v[2:3]
	v_lshl_add_u64 v[84:85], v[28:29], 0, v[84:85]
	v_add_u32_e32 v52, s16, v34
	global_store_dwordx4 v[84:85], v[48:51], off
	s_mov_b64 s[24:25], 0
	s_nop 0
	v_mov_b32_e32 v48, v1
	v_mov_b32_e32 v49, v1
	v_mov_b32_e32 v50, v1
	v_mov_b32_e32 v51, v1
	v_cvt_pk_fp8_f32 v48, v53, v55
	v_cvt_pk_fp8_f32 v49, v61, v63
	v_cvt_pk_fp8_f32 v50, v69, v71
	v_cvt_pk_fp8_f32 v51, v77, v79
	v_cvt_pk_fp8_f32 v48, v57, v59 op_sel:[0,0,1]
	v_cvt_pk_fp8_f32 v49, v65, v67 op_sel:[0,0,1]
	v_cvt_pk_fp8_f32 v50, v73, v75 op_sel:[0,0,1]
	v_cvt_pk_fp8_f32 v51, v81, v83 op_sel:[0,0,1]
	v_ashrrev_i32_e32 v53, 31, v52
	v_lshlrev_b64 v[52:53], 10, v[52:53]
	v_lshl_add_u64 v[28:29], v[28:29], 0, v[52:53]
	global_store_dwordx4 v[28:29], v[48:51], off
	s_waitcnt lgkmcnt(0)
; __device__ __forceinline__ void tr_item8(const float* W, int ld, int K, int nblk, int item, unsigned char* WT, bool gu, float scale, LAS float* scr, int lane) {
;     const int kb = item / nblk, nb = item % nblk, k0 = 64 * kb, n0 = 32 * nb;
;     int drow0 = n0;
;     if (gu) { const int bj = n0 / FF, j = n0 - bj * FF; drow0 = 256 * (j / 128) + 128 * bj + (j % 128); }
;     { float t_[32];
; #pragma unroll
;       for (int i = 0; i < 32; ++i) t_[i] = W[(size_t)(k0 + 2 * i + (lane >> 5)) * ld + n0 + (lane & 31)];
; #pragma unroll
.LBB0_1139:
	s_andn2_b64 vcc, exec, s[24:25]
	s_cbranch_vccnz .LBB0_1141
	s_lshl_b32 s16, s37, 5
	s_and_b32 s24, s42, 0x1ffc0
	s_and_b32 s26, s16, 0x3e0
	v_add_u32_e32 v28, s24, v30
	s_lshl_b32 s16, s26, 2
	v_ashrrev_i32_e32 v29, 31, v28
	v_lshl_add_u64 v[48:49], v[4:5], 0, s[16:17]
	v_lshlrev_b64 v[28:29], 12, v[28:29]
	v_lshl_add_u64 v[28:29], v[48:49], 0, v[28:29]
	v_add_co_u32_e32 v48, vcc, 0x2000, v28
	global_load_dword v50, v[28:29], off nt
	s_nop 0
	v_addc_co_u32_e32 v49, vcc, 0, v29, vcc
	global_load_dword v51, v[48:49], off nt
	v_add_co_u32_e32 v48, vcc, 0x4000, v28
	s_mov_b32 s25, s17
	s_nop 0
	v_addc_co_u32_e32 v49, vcc, 0, v29, vcc
	global_load_dword v52, v[48:49], off nt
	v_add_co_u32_e32 v48, vcc, 0x6000, v28
	s_nop 1
	v_addc_co_u32_e32 v49, vcc, 0, v29, vcc
	global_load_dword v53, v[48:49], off nt
	v_add_co_u32_e32 v48, vcc, 0x8000, v28
	s_nop 1
	v_addc_co_u32_e32 v49, vcc, 0, v29, vcc
	global_load_dword v54, v[48:49], off nt
	v_add_co_u32_e32 v48, vcc, 0xa000, v28
	s_nop 1
	v_addc_co_u32_e32 v49, vcc, 0, v29, vcc
	global_load_dword v55, v[48:49], off nt
	v_add_co_u32_e32 v48, vcc, 0xc000, v28
	s_nop 1
	v_addc_co_u32_e32 v49, vcc, 0, v29, vcc
	global_load_dword v56, v[48:49], off nt
	v_add_co_u32_e32 v48, vcc, 0xe000, v28
	s_nop 1
	v_addc_co_u32_e32 v49, vcc, 0, v29, vcc
	global_load_dword v57, v[48:49], off nt
	v_add_co_u32_e32 v48, vcc, 0x10000, v28
	s_nop 1
	v_addc_co_u32_e32 v49, vcc, 0, v29, vcc
	global_load_dword v58, v[48:49], off nt
	v_add_co_u32_e32 v48, vcc, 0x12000, v28
	s_nop 1
	v_addc_co_u32_e32 v49, vcc, 0, v29, vcc
	global_load_dword v59, v[48:49], off nt
	v_add_co_u32_e32 v48, vcc, 0x14000, v28
	s_nop 1
	v_addc_co_u32_e32 v49, vcc, 0, v29, vcc
	global_load_dword v60, v[48:49], off nt
	v_add_co_u32_e32 v48, vcc, 0x16000, v28
	s_nop 1
	v_addc_co_u32_e32 v49, vcc, 0, v29, vcc
	global_load_dword v61, v[48:49], off nt
	v_add_co_u32_e32 v48, vcc, 0x18000, v28
	s_nop 1
	v_addc_co_u32_e32 v49, vcc, 0, v29, vcc
	global_load_dword v62, v[48:49], off nt
	v_add_co_u32_e32 v48, vcc, 0x1a000, v28
	s_nop 1
	v_addc_co_u32_e32 v49, vcc, 0, v29, vcc
	global_load_dword v63, v[48:49], off nt
	v_add_co_u32_e32 v48, vcc, 0x1c000, v28
	s_nop 1
	v_addc_co_u32_e32 v49, vcc, 0, v29, vcc
	global_load_dword v64, v[48:49], off nt
	v_add_co_u32_e32 v48, vcc, 0x1e000, v28
	s_nop 1
	v_addc_co_u32_e32 v49, vcc, 0, v29, vcc
	global_load_dword v65, v[48:49], off nt
	v_add_co_u32_e32 v48, vcc, 0x20000, v28
	s_nop 1
	v_addc_co_u32_e32 v49, vcc, 0, v29, vcc
	global_load_dword v66, v[48:49], off nt
	v_add_co_u32_e32 v48, vcc, 0x22000, v28
	s_nop 1
	v_addc_co_u32_e32 v49, vcc, 0, v29, vcc
	global_load_dword v67, v[48:49], off nt
	v_add_co_u32_e32 v48, vcc, 0x24000, v28
	s_nop 1
	v_addc_co_u32_e32 v49, vcc, 0, v29, vcc
	global_load_dword v68, v[48:49], off nt
	v_add_co_u32_e32 v48, vcc, 0x26000, v28
	s_nop 1
	v_addc_co_u32_e32 v49, vcc, 0, v29, vcc
	global_load_dword v69, v[48:49], off nt
	v_add_co_u32_e32 v48, vcc, 0x28000, v28
	s_nop 1
	v_addc_co_u32_e32 v49, vcc, 0, v29, vcc
	global_load_dword v70, v[48:49], off nt
	v_add_co_u32_e32 v48, vcc, 0x2a000, v28
	s_nop 1
	v_addc_co_u32_e32 v49, vcc, 0, v29, vcc
	global_load_dword v71, v[48:49], off nt
	v_add_co_u32_e32 v48, vcc, 0x2c000, v28
	s_nop 1
	v_addc_co_u32_e32 v49, vcc, 0, v29, vcc
	global_load_dword v72, v[48:49], off nt
	v_add_co_u32_e32 v48, vcc, 0x2e000, v28
	s_nop 1
	v_addc_co_u32_e32 v49, vcc, 0, v29, vcc
	global_load_dword v73, v[48:49], off nt
	v_add_co_u32_e32 v48, vcc, 0x30000, v28
	s_nop 1
	v_addc_co_u32_e32 v49, vcc, 0, v29, vcc
	global_load_dword v74, v[48:49], off nt
	v_add_co_u32_e32 v48, vcc, 0x32000, v28
	s_nop 1
	v_addc_co_u32_e32 v49, vcc, 0, v29, vcc
	global_load_dword v75, v[48:49], off nt
	v_add_co_u32_e32 v48, vcc, 0x34000, v28
	s_nop 1
	v_addc_co_u32_e32 v49, vcc, 0, v29, vcc
	global_load_dword v76, v[48:49], off nt
	v_add_co_u32_e32 v48, vcc, 0x36000, v28
	s_nop 1
	v_addc_co_u32_e32 v49, vcc, 0, v29, vcc
	global_load_dword v77, v[48:49], off nt
	v_add_co_u32_e32 v48, vcc, 0x38000, v28
	s_nop 1
	v_addc_co_u32_e32 v49, vcc, 0, v29, vcc
	global_load_dword v78, v[48:49], off nt
	v_add_co_u32_e32 v48, vcc, 0x3a000, v28
	s_nop 1
	v_addc_co_u32_e32 v49, vcc, 0, v29, vcc
	global_load_dword v79, v[48:49], off nt
	v_add_co_u32_e32 v48, vcc, 0x3c000, v28
	s_nop 1
	v_addc_co_u32_e32 v49, vcc, 0, v29, vcc
	v_add_co_u32_e32 v28, vcc, 0x3e000, v28
	global_load_dword v48, v[48:49], off nt
	s_nop 0
	v_addc_co_u32_e32 v29, vcc, 0, v29, vcc
	global_load_dword v28, v[28:29], off nt
	s_waitcnt vmcnt(0)
; __device__ __forceinline__ unsigned cvt_pk4_fp8(float a, float b, float c, float d) { int w = 0; w = __builtin_amdgcn_cvt_pk_fp8_f32(a, b, w, false); w = __builtin_amdgcn_cvt_pk_fp8_f32(c, d, w, true); return (unsigned)w; }
; #define GAS __attribute__((address_space(1)))
; #define LAS __attribute__((address_space(3)))
; #define LDS_WAIT() asm volatile("s_waitcnt lgkmcnt(0)" ::: "memory")
; __device__ __forceinline__ void tr_item8(const float* W, int ld, int K, int nblk, int item, unsigned char* WT, bool gu, float scale, LAS float* scr, int lane) {
;     ...
;       for (int i = 0; i < 32; ++i) scr[(2 * i + (lane >> 5)) * 33 + (lane & 31)] = t_[i] * scale; }
;     LDS_WAIT(); asm volatile("" ::: "memory");
;     const int c = lane & 3;
; #pragma unroll
;     for (int j = 0; j < 2; ++j) { const int n = (lane >> 2) + 16 * j; const LAS float* sp = scr + (16 * c) * 33 + n;
;         v4u o; o.x = pg8::cvt_pk4_fp8(sp[0 * 33], sp[1 * 33], sp[2 * 33], sp[3 * 33]); o.y = pg8::cvt_pk4_fp8(sp[4 * 33], sp[5 * 33], sp[6 * 33], sp[7 * 33]);
;         o.z = pg8::cvt_pk4_fp8(sp[8 * 33], sp[9 * 33], sp[10 * 33], sp[11 * 33]); o.w = pg8::cvt_pk4_fp8(sp[12 * 33], sp[13 * 33], sp[14 * 33], sp[15 * 33]);
;         *(GAS v4u*)(WT + (size_t)(drow0 + n) * K + k0 + 16 * c) = o; }
;     LDS_WAIT(); asm volatile("" ::: "memory");
	v_mul_f32_e32 v29, 0x43000000, v50
	v_mul_f32_e32 v49, 0x43000000, v51
	ds_write2_b32 v31, v29, v49 offset1:66
	v_mul_f32_e32 v29, 0x43000000, v52
	v_mul_f32_e32 v49, 0x43000000, v53
	ds_write2_b32 v31, v29, v49 offset0:132 offset1:198
	v_mul_f32_e32 v29, 0x43000000, v54
	v_mul_f32_e32 v49, 0x43000000, v55
	ds_write2_b32 v40, v29, v49 offset0:8 offset1:74
	v_mul_f32_e32 v29, 0x43000000, v56
	v_mul_f32_e32 v49, 0x43000000, v57
	ds_write2_b32 v40, v29, v49 offset0:140 offset1:206
	v_mul_f32_e32 v29, 0x43000000, v58
	v_mul_f32_e32 v49, 0x43000000, v59
	ds_write2_b32 v41, v29, v49 offset0:16 offset1:82
	v_mul_f32_e32 v29, 0x43000000, v60
	v_mul_f32_e32 v49, 0x43000000, v61
	ds_write2_b32 v41, v29, v49 offset0:148 offset1:214
	v_mul_f32_e32 v29, 0x43000000, v62
	v_mul_f32_e32 v49, 0x43000000, v63
	ds_write2_b32 v42, v29, v49 offset0:24 offset1:90
	v_mul_f32_e32 v29, 0x43000000, v64
	v_mul_f32_e32 v49, 0x43000000, v65
	ds_write2_b32 v42, v29, v49 offset0:156 offset1:222
	v_mul_f32_e32 v29, 0x43000000, v66
	v_mul_f32_e32 v49, 0x43000000, v67
	ds_write2_b32 v43, v29, v49 offset0:32 offset1:98
	v_mul_f32_e32 v29, 0x43000000, v68
	v_mul_f32_e32 v49, 0x43000000, v69
	ds_write2_b32 v43, v29, v49 offset0:164 offset1:230
	v_mul_f32_e32 v29, 0x43000000, v70
	v_mul_f32_e32 v49, 0x43000000, v71
	ds_write2_b32 v44, v29, v49 offset0:40 offset1:106
	v_mul_f32_e32 v29, 0x43000000, v72
	v_mul_f32_e32 v49, 0x43000000, v73
	ds_write2_b32 v44, v29, v49 offset0:172 offset1:238
	v_mov_b32_e32 v50, 0
	v_mov_b32_e32 v51, 0
	v_mul_f32_e32 v29, 0x43000000, v74
	v_mul_f32_e32 v49, 0x43000000, v75
	ds_write2_b32 v45, v29, v49 offset0:48 offset1:114
	v_mul_f32_e32 v29, 0x43000000, v76
	v_mul_f32_e32 v49, 0x43000000, v77
	ds_write2_b32 v45, v29, v49 offset0:180 offset1:246
	v_mul_f32_e32 v29, 0x43000000, v78
	v_mul_f32_e32 v49, 0x43000000, v79
	ds_write2_b32 v46, v29, v49 offset0:56 offset1:122
	v_mov_b32_e32 v49, 0
	v_mul_f32_e32 v29, 0x43000000, v48
	v_mov_b32_e32 v48, 0
	v_mul_f32_e32 v28, 0x43000000, v28
	ds_write2_b32 v46, v29, v28 offset0:188 offset1:254
	s_waitcnt lgkmcnt(0)
	ds_read2_b32 v[52:53], v33 offset1:16
	ds_read2_b32 v[54:55], v33 offset0:33 offset1:49
	ds_read2_b32 v[56:57], v33 offset0:66 offset1:82
	ds_read2_b32 v[58:59], v33 offset0:99 offset1:115
	ds_read2_b32 v[60:61], v33 offset0:132 offset1:148
	ds_read2_b32 v[62:63], v33 offset0:165 offset1:181
	ds_read2_b32 v[64:65], v33 offset0:198 offset1:214
	ds_read2_b32 v[66:67], v33 offset0:231 offset1:247
	ds_read2_b32 v[68:69], v47 offset0:8 offset1:24
	ds_read2_b32 v[70:71], v47 offset0:41 offset1:57
	ds_read2_b32 v[72:73], v47 offset0:74 offset1:90
	ds_read2_b32 v[74:75], v47 offset0:107 offset1:123
	ds_read2_b32 v[76:77], v47 offset0:140 offset1:156
	ds_read2_b32 v[78:79], v47 offset0:173 offset1:189
	ds_read2_b32 v[80:81], v47 offset0:206 offset1:222
	ds_read2_b32 v[82:83], v47 offset0:239 offset1:255
	s_waitcnt lgkmcnt(14)
	v_cvt_pk_fp8_f32 v48, v52, v54
	s_waitcnt lgkmcnt(10)
	v_cvt_pk_fp8_f32 v49, v60, v62
	s_waitcnt lgkmcnt(6)
	v_cvt_pk_fp8_f32 v50, v68, v70
	s_waitcnt lgkmcnt(2)
	v_cvt_pk_fp8_f32 v51, v76, v78
	v_cvt_pk_fp8_f32 v48, v56, v58 op_sel:[0,0,1]
	v_cvt_pk_fp8_f32 v49, v64, v66 op_sel:[0,0,1]
	v_cvt_pk_fp8_f32 v50, v72, v74 op_sel:[0,0,1]
	s_waitcnt lgkmcnt(0)
	v_cvt_pk_fp8_f32 v51, v80, v82 op_sel:[0,0,1]
	v_lshl_add_u64 v[28:29], v[18:19], 0, s[24:25]
	v_add_u32_e32 v52, s26, v32
	v_mad_i64_i32 v[84:85], s[24:25], v52, s44, v[28:29]
	global_store_dwordx4 v[84:85], v[48:51], off
	v_add_u32_e32 v52, s26, v34
	v_mad_i64_i32 v[28:29], s[24:25], v52, s44, v[28:29]
	v_mov_b32_e32 v48, 0
	v_mov_b32_e32 v49, 0
	v_mov_b32_e32 v50, 0
	v_mov_b32_e32 v51, 0
	v_cvt_pk_fp8_f32 v48, v53, v55
	v_cvt_pk_fp8_f32 v49, v61, v63
	v_cvt_pk_fp8_f32 v50, v69, v71
	v_cvt_pk_fp8_f32 v51, v77, v79
	v_cvt_pk_fp8_f32 v48, v57, v59 op_sel:[0,0,1]
	v_cvt_pk_fp8_f32 v49, v65, v67 op_sel:[0,0,1]
	v_cvt_pk_fp8_f32 v50, v73, v75 op_sel:[0,0,1]
	v_cvt_pk_fp8_f32 v51, v81, v83 op_sel:[0,0,1]
	global_store_dwordx4 v[28:29], v[48:51], off
	s_waitcnt lgkmcnt(0)

; __device__ __forceinline__ void tr_item8(const float* W, int ld, int K, int nblk, int item, unsigned char* WT, bool gu, float scale, LAS float* scr, int lane) {
;     const int kb = item / nblk, nb = item % nblk, k0 = 64 * kb, n0 = 32 * nb;
;     int drow0 = n0;
;     if (gu) { const int bj = n0 / FF, j = n0 - bj * FF; drow0 = 256 * (j / 128) + 128 * bj + (j % 128); }
;     { float t_[32];
; #pragma unroll
;       for (int i = 0; i < 32; ++i) t_[i] = W[(size_t)(k0 + 2 * i + (lane >> 5)) * ld + n0 + (lane & 31)];
; #pragma unroll
.LBB0_1142:
	s_andn2_b64 vcc, exec, s[24:25]
	s_cbranch_vccnz .LBB0_1144
	s_add_i32 s16, s37, 0xf300
	s_bfe_u32 s24, s16, 0xb0005
	s_mulk_i32 s24, 0x2493
	s_lshr_b32 s24, s24, 16
	s_mul_i32 s25, s24, 0xe0
	s_sub_i32 s16, s16, s25
	s_lshl_b32 s25, s16, 5
	s_and_b32 s26, s16, 0xffff
	s_cmpk_gt_u32 s26, 0x6f
	s_cselect_b32 s50, 0xfffff200, 0
	s_cselect_b32 s51, 0x80, 0
	s_lshl_b32 s16, s16, 7
	s_lshl_b32 s24, s24, 6
	s_and_b32 s16, s16, 0x3ff80
	v_add_u32_e32 v64, s24, v30
	v_lshl_add_u64 v[28:29], v[6:7], 0, s[16:17]
	v_mad_i64_i32 v[48:49], s[26:27], v64, s45, v[28:29]
	v_add_u32_e32 v50, 2, v64
	v_add_u32_e32 v52, 4, v64
	v_add_u32_e32 v54, 6, v64
	v_add_u32_e32 v56, 8, v64
	v_add_u32_e32 v58, 10, v64
	v_add_u32_e32 v60, 12, v64
	v_add_u32_e32 v62, 14, v64
	v_mad_i64_i32 v[50:51], s[26:27], v50, s45, v[28:29]
	v_mad_i64_i32 v[52:53], s[26:27], v52, s45, v[28:29]
	v_mad_i64_i32 v[54:55], s[26:27], v54, s45, v[28:29]
	v_mad_i64_i32 v[56:57], s[26:27], v56, s45, v[28:29]
	v_mad_i64_i32 v[58:59], s[26:27], v58, s45, v[28:29]
	v_mad_i64_i32 v[60:61], s[26:27], v60, s45, v[28:29]
	v_mad_i64_i32 v[62:63], s[26:27], v62, s45, v[28:29]
	global_load_dword v65, v[48:49], off nt
	global_load_dword v66, v[50:51], off nt
	global_load_dword v67, v[52:53], off nt
	global_load_dword v68, v[54:55], off nt
	global_load_dword v69, v[56:57], off nt
	global_load_dword v70, v[58:59], off nt
	global_load_dword v71, v[60:61], off nt
	global_load_dword v72, v[62:63], off nt
	v_add_u32_e32 v48, 16, v64
	v_mad_i64_i32 v[48:49], s[26:27], v48, s45, v[28:29]
	v_add_u32_e32 v50, 18, v64
	v_add_u32_e32 v52, 20, v64
	v_add_u32_e32 v54, 22, v64
	v_add_u32_e32 v56, 24, v64
	v_add_u32_e32 v58, 26, v64
	v_add_u32_e32 v60, 28, v64
	v_add_u32_e32 v62, 30, v64
	v_mad_i64_i32 v[50:51], s[26:27], v50, s45, v[28:29]
	v_mad_i64_i32 v[52:53], s[26:27], v52, s45, v[28:29]
	v_mad_i64_i32 v[54:55], s[26:27], v54, s45, v[28:29]
	v_mad_i64_i32 v[56:57], s[26:27], v56, s45, v[28:29]
	v_mad_i64_i32 v[58:59], s[26:27], v58, s45, v[28:29]
	v_mad_i64_i32 v[60:61], s[26:27], v60, s45, v[28:29]
	v_mad_i64_i32 v[62:63], s[26:27], v62, s45, v[28:29]
	global_load_dword v73, v[48:49], off nt
	global_load_dword v74, v[50:51], off nt
	global_load_dword v75, v[52:53], off nt
	global_load_dword v76, v[54:55], off nt
	global_load_dword v77, v[56:57], off nt
	global_load_dword v78, v[58:59], off nt
	global_load_dword v79, v[60:61], off nt
	global_load_dword v80, v[62:63], off nt
	v_add_u32_e32 v48, 32, v64
	v_add_u32_e32 v50, 34, v64
	v_add_u32_e32 v52, 36, v64
	v_add_u32_e32 v54, 38, v64
	v_add_u32_e32 v60, 44, v64
	v_mad_i64_i32 v[48:49], s[26:27], v48, s45, v[28:29]
	v_mad_i64_i32 v[50:51], s[26:27], v50, s45, v[28:29]
	v_mad_i64_i32 v[52:53], s[26:27], v52, s45, v[28:29]
	v_mad_i64_i32 v[54:55], s[26:27], v54, s45, v[28:29]
	v_add_u32_e32 v56, 40, v64
	v_add_u32_e32 v58, 42, v64
	v_mad_i64_i32 v[60:61], s[26:27], v60, s45, v[28:29]
	v_add_u32_e32 v62, 46, v64
	v_mad_i64_i32 v[56:57], s[26:27], v56, s45, v[28:29]
	v_mad_i64_i32 v[58:59], s[26:27], v58, s45, v[28:29]
	v_mad_i64_i32 v[62:63], s[26:27], v62, s45, v[28:29]
	global_load_dword v81, v[48:49], off nt
	global_load_dword v82, v[50:51], off nt
	global_load_dword v83, v[52:53], off nt
	global_load_dword v84, v[54:55], off nt
	global_load_dword v85, v[56:57], off nt
	global_load_dword v86, v[58:59], off nt
	s_nop 0
	global_load_dword v60, v[60:61], off nt
	s_nop 0
	global_load_dword v61, v[62:63], off nt
	v_add_u32_e32 v48, 48, v64
	v_add_u32_e32 v50, 50, v64
	v_add_u32_e32 v52, 52, v64
	v_add_u32_e32 v54, 54, v64
	v_mad_i64_i32 v[48:49], s[26:27], v48, s45, v[28:29]
	v_mad_i64_i32 v[50:51], s[26:27], v50, s45, v[28:29]
	v_mad_i64_i32 v[52:53], s[26:27], v52, s45, v[28:29]
	v_mad_i64_i32 v[54:55], s[26:27], v54, s45, v[28:29]
	v_add_u32_e32 v56, 56, v64
	v_add_u32_e32 v58, 58, v64
	v_mad_i64_i32 v[56:57], s[26:27], v56, s45, v[28:29]
	v_mad_i64_i32 v[58:59], s[26:27], v58, s45, v[28:29]
	global_load_dword v62, v[48:49], off nt
	s_nop 0
	global_load_dword v50, v[50:51], off nt
	s_nop 0
	global_load_dword v51, v[52:53], off nt
	s_nop 0
	global_load_dword v52, v[54:55], off nt
	global_load_dword v53, v[56:57], off nt
	s_nop 0
	global_load_dword v54, v[58:59], off nt
	v_add_u32_e32 v48, 60, v64
	v_add_u32_e32 v55, 62, v64
	v_mad_i64_i32 v[48:49], s[26:27], v48, s45, v[28:29]
	v_mad_i64_i32 v[28:29], s[26:27], v55, s45, v[28:29]
	global_load_dword v48, v[48:49], off nt
	s_nop 0
	global_load_dword v28, v[28:29], off nt
	s_waitcnt vmcnt(0)
; __device__ __forceinline__ unsigned cvt_pk4_fp8(float a, float b, float c, float d) { int w = 0; w = __builtin_amdgcn_cvt_pk_fp8_f32(a, b, w, false); w = __builtin_amdgcn_cvt_pk_fp8_f32(c, d, w, true); return (unsigned)w; }
; #define GAS __attribute__((address_space(1)))
; #define LAS __attribute__((address_space(3)))
; #define LDS_WAIT() asm volatile("s_waitcnt lgkmcnt(0)" ::: "memory")
; __device__ __forceinline__ void tr_item8(const float* W, int ld, int K, int nblk, int item, unsigned char* WT, bool gu, float scale, LAS float* scr, int lane) {
;     ...
;     if (gu) { const int bj = n0 / FF, j = n0 - bj * FF; drow0 = 256 * (j / 128) + 128 * bj + (j % 128); }
;     { float t_[32];
; #pragma unroll
;       for (int i = 0; i < 32; ++i) t_[i] = W[(size_t)(k0 + 2 * i + (lane >> 5)) * ld + n0 + (lane & 31)];
; #pragma unroll
;       for (int i = 0; i < 32; ++i) scr[(2 * i + (lane >> 5)) * 33 + (lane & 31)] = t_[i] * scale; }
;     LDS_WAIT(); asm volatile("" ::: "memory");
;     const int c = lane & 3;
; #pragma unroll
;     for (int j = 0; j < 2; ++j) { const int n = (lane >> 2) + 16 * j; const LAS float* sp = scr + (16 * c) * 33 + n;
;         v4u o; o.x = pg8::cvt_pk4_fp8(sp[0 * 33], sp[1 * 33], sp[2 * 33], sp[3 * 33]); o.y = pg8::cvt_pk4_fp8(sp[4 * 33], sp[5 * 33], sp[6 * 33], sp[7 * 33]);
;         o.z = pg8::cvt_pk4_fp8(sp[8 * 33], sp[9 * 33], sp[10 * 33], sp[11 * 33]); o.w = pg8::cvt_pk4_fp8(sp[12 * 33], sp[13 * 33], sp[14 * 33], sp[15 * 33]);
;         *(GAS v4u*)(WT + (size_t)(drow0 + n) * K + k0 + 16 * c) = o; }
;     LDS_WAIT(); asm volatile("" ::: "memory");
	v_mul_f32_e32 v29, 0x42800000, v65
	v_mul_f32_e32 v49, 0x42800000, v66
	ds_write2_b32 v31, v29, v49 offset1:66
	v_mul_f32_e32 v29, 0x42800000, v67
	v_mul_f32_e32 v49, 0x42800000, v68
	ds_write2_b32 v31, v29, v49 offset0:132 offset1:198
	v_mul_f32_e32 v29, 0x42800000, v69
	v_mul_f32_e32 v49, 0x42800000, v70
	ds_write2_b32 v40, v29, v49 offset0:8 offset1:74
	v_mul_f32_e32 v29, 0x42800000, v71
	v_mul_f32_e32 v49, 0x42800000, v72
	ds_write2_b32 v40, v29, v49 offset0:140 offset1:206
	s_add_i32 s16, s50, s25
	s_sext_i32_i16 s25, s16
	s_bfe_u32 s25, s25, 0x70018
	s_add_i32 s25, s16, s25
	s_sext_i32_i16 s26, s25
	s_and_b32 s25, s25, 0xff80
	s_sub_i32 s16, s16, s25
	s_lshl_b32 s26, s26, 1
	s_sext_i32_i16 s16, s16
	v_mul_f32_e32 v29, 0x42800000, v73
	v_mul_f32_e32 v49, 0x42800000, v74
	ds_write2_b32 v41, v29, v49 offset0:16 offset1:82
	v_mul_f32_e32 v29, 0x42800000, v75
	v_mul_f32_e32 v49, 0x42800000, v76
	ds_write2_b32 v41, v29, v49 offset0:148 offset1:214
	v_mul_f32_e32 v29, 0x42800000, v77
	v_mul_f32_e32 v49, 0x42800000, v78
	ds_write2_b32 v42, v29, v49 offset0:24 offset1:90
	v_mul_f32_e32 v29, 0x42800000, v79
	v_mul_f32_e32 v49, 0x42800000, v80
	ds_write2_b32 v42, v29, v49 offset0:156 offset1:222
	s_and_b32 s26, s26, 0xffffff00
	s_add_i32 s16, s51, s16
	s_add_i32 s16, s16, s26
	s_mov_b32 s25, s17
	v_mul_f32_e32 v29, 0x42800000, v81
	v_mul_f32_e32 v49, 0x42800000, v82
	ds_write2_b32 v43, v29, v49 offset0:32 offset1:98
	v_mul_f32_e32 v29, 0x42800000, v83
	v_mul_f32_e32 v49, 0x42800000, v84
	ds_write2_b32 v43, v29, v49 offset0:164 offset1:230
	v_mul_f32_e32 v29, 0x42800000, v85
	v_mul_f32_e32 v49, 0x42800000, v86
	ds_write2_b32 v44, v29, v49 offset0:40 offset1:106
	v_mul_f32_e32 v29, 0x42800000, v60
	v_mul_f32_e32 v49, 0x42800000, v61
	ds_write2_b32 v44, v29, v49 offset0:172 offset1:238
	v_add_u32_e32 v84, s16, v32
	v_ashrrev_i32_e32 v85, 31, v84
	v_lshlrev_b64 v[84:85], 10, v[84:85]
	v_mul_f32_e32 v29, 0x42800000, v62
	v_mul_f32_e32 v49, 0x42800000, v50
	ds_write2_b32 v45, v29, v49 offset0:48 offset1:114
	v_mul_f32_e32 v29, 0x42800000, v51
	v_mul_f32_e32 v49, 0x42800000, v52
	ds_write2_b32 v45, v29, v49 offset0:180 offset1:246
	v_mul_f32_e32 v29, 0x42800000, v53
	v_mul_f32_e32 v49, 0x42800000, v54
	ds_write2_b32 v46, v29, v49 offset0:56 offset1:122
	v_mov_b32_e32 v49, 0
	v_mov_b32_e32 v50, 0
	v_mul_f32_e32 v29, 0x42800000, v48
	v_mul_f32_e32 v28, 0x42800000, v28
	ds_write2_b32 v46, v29, v28 offset0:188 offset1:254
	s_waitcnt lgkmcnt(0)
	ds_read2_b32 v[52:53], v33 offset1:16
	ds_read2_b32 v[54:55], v33 offset0:33 offset1:49
	ds_read2_b32 v[56:57], v33 offset0:66 offset1:82
	ds_read2_b32 v[58:59], v33 offset0:99 offset1:115
	ds_read2_b32 v[60:61], v33 offset0:132 offset1:148
	ds_read2_b32 v[62:63], v33 offset0:165 offset1:181
	ds_read2_b32 v[64:65], v33 offset0:198 offset1:214
	ds_read2_b32 v[66:67], v33 offset0:231 offset1:247
	ds_read2_b32 v[68:69], v47 offset0:8 offset1:24
	ds_read2_b32 v[70:71], v47 offset0:41 offset1:57
	ds_read2_b32 v[72:73], v47 offset0:74 offset1:90
	ds_read2_b32 v[74:75], v47 offset0:107 offset1:123
	ds_read2_b32 v[76:77], v47 offset0:140 offset1:156
	ds_read2_b32 v[78:79], v47 offset0:173 offset1:189
	v_mov_b32_e32 v48, 0
	ds_read2_b32 v[80:81], v47 offset0:206 offset1:222
	ds_read2_b32 v[82:83], v47 offset0:239 offset1:255
	v_mov_b32_e32 v51, 0
	s_waitcnt lgkmcnt(14)
	v_cvt_pk_fp8_f32 v48, v52, v54
	s_waitcnt lgkmcnt(10)
	v_cvt_pk_fp8_f32 v49, v60, v62
	s_waitcnt lgkmcnt(6)
	v_cvt_pk_fp8_f32 v50, v68, v70
	s_waitcnt lgkmcnt(2)
	v_cvt_pk_fp8_f32 v51, v76, v78
	v_cvt_pk_fp8_f32 v48, v56, v58 op_sel:[0,0,1]
	v_cvt_pk_fp8_f32 v49, v64, v66 op_sel:[0,0,1]
	v_cvt_pk_fp8_f32 v50, v72, v74 op_sel:[0,0,1]
	s_waitcnt lgkmcnt(0)
	v_cvt_pk_fp8_f32 v51, v80, v82 op_sel:[0,0,1]
	v_lshl_add_u64 v[28:29], v[20:21], 0, s[24:25]
	v_lshl_add_u64 v[84:85], v[28:29], 0, v[84:85]
	v_add_u32_e32 v52, s16, v34
	global_store_dwordx4 v[84:85], v[48:51], off
	s_nop 1
	v_mov_b32_e32 v48, 0
	v_mov_b32_e32 v49, 0
	v_mov_b32_e32 v50, 0
	v_mov_b32_e32 v51, 0
	v_cvt_pk_fp8_f32 v48, v53, v55
	v_cvt_pk_fp8_f32 v49, v61, v63
	v_cvt_pk_fp8_f32 v50, v69, v71
	v_cvt_pk_fp8_f32 v51, v77, v79
	v_cvt_pk_fp8_f32 v48, v57, v59 op_sel:[0,0,1]
	v_cvt_pk_fp8_f32 v49, v65, v67 op_sel:[0,0,1]
	v_cvt_pk_fp8_f32 v50, v73, v75 op_sel:[0,0,1]
	v_cvt_pk_fp8_f32 v51, v81, v83 op_sel:[0,0,1]
	v_ashrrev_i32_e32 v53, 31, v52
	v_lshlrev_b64 v[52:53], 10, v[52:53]
	v_lshl_add_u64 v[28:29], v[28:29], 0, v[52:53]
	global_store_dwordx4 v[28:29], v[48:51], off
	s_waitcnt lgkmcnt(0)

; #define LDS_WAIT() asm volatile("s_waitcnt lgkmcnt(0)" ::: "memory")
; __device__ __forceinline__ void tr_item(const float* W, int ld, int K, int nblk, int item, bf16* WT, bool gu, LAS float* scr, int lane) {
;     const int kb = item / nblk, nb = item % nblk, k0 = 64 * kb, n0 = 32 * nb;
;     int drow0 = n0;
;     if (gu) { const int bj = n0 / FF, j = n0 - bj * FF; drow0 = 256 * (j / 128) + 128 * bj + (j % 128); }
;     { float t_[32];
; #pragma unroll
;       for (int i = 0; i < 32; ++i) t_[i] = W[(size_t)(k0 + 2 * i + (lane >> 5)) * ld + n0 + (lane & 31)];
; #pragma unroll
;       for (int i = 0; i < 32; ++i) scr[(2 * i + (lane >> 5)) * 33 + (lane & 31)] = t_[i]; }
;     LDS_WAIT(); asm volatile("" ::: "memory");
.LBB0_1145:
	s_andn2_b64 vcc, exec, s[24:25]
	s_cbranch_vccnz .LBB0_1147
	s_add_i32 s16, s42, 0x2000
	s_and_b32 s25, s16, 0x1ffc0
	s_and_b32 s24, s40, 0x3e0
	v_add_u32_e32 v28, s25, v30
	s_lshl_b32 s16, s24, 2
	v_ashrrev_i32_e32 v29, 31, v28
	v_lshl_add_u64 v[48:49], v[8:9], 0, s[16:17]
	v_lshlrev_b64 v[28:29], 12, v[28:29]
	v_lshl_add_u64 v[28:29], v[48:49], 0, v[28:29]
	v_add_co_u32_e32 v48, vcc, 0x2000, v28
	global_load_dword v50, v[28:29], off nt
	s_nop 0
	v_addc_co_u32_e32 v49, vcc, 0, v29, vcc
	global_load_dword v51, v[48:49], off nt
	v_add_co_u32_e32 v48, vcc, 0x4000, v28
	s_lshl_b32 s16, s25, 1
	s_nop 0
	v_addc_co_u32_e32 v49, vcc, 0, v29, vcc
	global_load_dword v52, v[48:49], off nt
	v_add_co_u32_e32 v48, vcc, 0x6000, v28
	s_nop 1
	v_addc_co_u32_e32 v49, vcc, 0, v29, vcc
	global_load_dword v53, v[48:49], off nt
	v_add_co_u32_e32 v48, vcc, 0x8000, v28
	s_nop 1
	v_addc_co_u32_e32 v49, vcc, 0, v29, vcc
	global_load_dword v54, v[48:49], off nt
	v_add_co_u32_e32 v48, vcc, 0xa000, v28
	s_nop 1
	v_addc_co_u32_e32 v49, vcc, 0, v29, vcc
	global_load_dword v55, v[48:49], off nt
	v_add_co_u32_e32 v48, vcc, 0xc000, v28
	s_nop 1
	v_addc_co_u32_e32 v49, vcc, 0, v29, vcc
	global_load_dword v56, v[48:49], off nt
	v_add_co_u32_e32 v48, vcc, 0xe000, v28
	s_nop 1
	v_addc_co_u32_e32 v49, vcc, 0, v29, vcc
	global_load_dword v57, v[48:49], off nt
	v_add_co_u32_e32 v48, vcc, 0x10000, v28
	s_nop 1
	v_addc_co_u32_e32 v49, vcc, 0, v29, vcc
	global_load_dword v58, v[48:49], off nt
	v_add_co_u32_e32 v48, vcc, 0x12000, v28
	s_nop 1
	v_addc_co_u32_e32 v49, vcc, 0, v29, vcc
	global_load_dword v59, v[48:49], off nt
	v_add_co_u32_e32 v48, vcc, 0x14000, v28
	s_nop 1
	v_addc_co_u32_e32 v49, vcc, 0, v29, vcc
	global_load_dword v60, v[48:49], off nt
	v_add_co_u32_e32 v48, vcc, 0x16000, v28
	s_nop 1
	v_addc_co_u32_e32 v49, vcc, 0, v29, vcc
	global_load_dword v61, v[48:49], off nt
	v_add_co_u32_e32 v48, vcc, 0x18000, v28
	s_nop 1
	v_addc_co_u32_e32 v49, vcc, 0, v29, vcc
	global_load_dword v62, v[48:49], off nt
	v_add_co_u32_e32 v48, vcc, 0x1a000, v28
	s_nop 1
	v_addc_co_u32_e32 v49, vcc, 0, v29, vcc
	global_load_dword v63, v[48:49], off nt
	v_add_co_u32_e32 v48, vcc, 0x1c000, v28
	s_nop 1
	v_addc_co_u32_e32 v49, vcc, 0, v29, vcc
	global_load_dword v64, v[48:49], off nt
	v_add_co_u32_e32 v48, vcc, 0x1e000, v28
	s_nop 1
	v_addc_co_u32_e32 v49, vcc, 0, v29, vcc
	global_load_dword v65, v[48:49], off nt
	v_add_co_u32_e32 v48, vcc, 0x20000, v28
	s_nop 1
	v_addc_co_u32_e32 v49, vcc, 0, v29, vcc
	global_load_dword v66, v[48:49], off nt
	v_add_co_u32_e32 v48, vcc, 0x22000, v28
	s_nop 1
	v_addc_co_u32_e32 v49, vcc, 0, v29, vcc
	global_load_dword v67, v[48:49], off nt
	v_add_co_u32_e32 v48, vcc, 0x24000, v28
	s_nop 1
	v_addc_co_u32_e32 v49, vcc, 0, v29, vcc
	global_load_dword v68, v[48:49], off nt
	v_add_co_u32_e32 v48, vcc, 0x26000, v28
	s_nop 1
	v_addc_co_u32_e32 v49, vcc, 0, v29, vcc
	global_load_dword v69, v[48:49], off nt
	v_add_co_u32_e32 v48, vcc, 0x28000, v28
	s_nop 1
	v_addc_co_u32_e32 v49, vcc, 0, v29, vcc
	global_load_dword v70, v[48:49], off nt
	v_add_co_u32_e32 v48, vcc, 0x2a000, v28
	s_nop 1
	v_addc_co_u32_e32 v49, vcc, 0, v29, vcc
	global_load_dword v71, v[48:49], off nt
	v_add_co_u32_e32 v48, vcc, 0x2c000, v28
	s_nop 1
	v_addc_co_u32_e32 v49, vcc, 0, v29, vcc
	global_load_dword v72, v[48:49], off nt
	v_add_co_u32_e32 v48, vcc, 0x2e000, v28
	s_nop 1
	v_addc_co_u32_e32 v49, vcc, 0, v29, vcc
	global_load_dword v73, v[48:49], off nt
	v_add_co_u32_e32 v48, vcc, 0x30000, v28
	s_nop 1
	v_addc_co_u32_e32 v49, vcc, 0, v29, vcc
	global_load_dword v74, v[48:49], off nt
	v_add_co_u32_e32 v48, vcc, 0x32000, v28
	s_nop 1
	v_addc_co_u32_e32 v49, vcc, 0, v29, vcc
	global_load_dword v75, v[48:49], off nt
	v_add_co_u32_e32 v48, vcc, 0x34000, v28
	s_nop 1
	v_addc_co_u32_e32 v49, vcc, 0, v29, vcc
	global_load_dword v76, v[48:49], off nt
	v_add_co_u32_e32 v48, vcc, 0x36000, v28
	s_nop 1
	v_addc_co_u32_e32 v49, vcc, 0, v29, vcc
	global_load_dword v77, v[48:49], off nt
	v_add_co_u32_e32 v48, vcc, 0x38000, v28
	s_nop 1
	v_addc_co_u32_e32 v49, vcc, 0, v29, vcc
	global_load_dword v78, v[48:49], off nt
	v_add_co_u32_e32 v48, vcc, 0x3a000, v28
	s_nop 1
	v_addc_co_u32_e32 v49, vcc, 0, v29, vcc
	global_load_dword v79, v[48:49], off nt
	v_add_co_u32_e32 v48, vcc, 0x3c000, v28
	s_nop 1
	v_addc_co_u32_e32 v49, vcc, 0, v29, vcc
	v_add_co_u32_e32 v28, vcc, 0x3e000, v28
	global_load_dword v48, v[48:49], off nt
	s_nop 0
	v_addc_co_u32_e32 v29, vcc, 0, v29, vcc
	global_load_dword v28, v[28:29], off nt
	s_waitcnt vmcnt(0)
	ds_write2_b32 v31, v50, v51 offset1:66
	ds_write2_b32 v31, v52, v53 offset0:132 offset1:198
	ds_write2_b32 v40, v54, v55 offset0:8 offset1:74
	ds_write2_b32 v40, v56, v57 offset0:140 offset1:206
	ds_write2_b32 v41, v58, v59 offset0:16 offset1:82
	ds_write2_b32 v41, v60, v61 offset0:148 offset1:214
	ds_write2_b32 v42, v62, v63 offset0:24 offset1:90
	ds_write2_b32 v42, v64, v65 offset0:156 offset1:222
	ds_write2_b32 v43, v66, v67 offset0:32 offset1:98
	ds_write2_b32 v43, v68, v69 offset0:164 offset1:230
	ds_write2_b32 v44, v70, v71 offset0:40 offset1:106
	ds_write2_b32 v44, v72, v73 offset0:172 offset1:238
	ds_write2_b32 v45, v74, v75 offset0:48 offset1:114
	ds_write2_b32 v45, v76, v77 offset0:180 offset1:246
	ds_write2_b32 v46, v78, v79 offset0:56 offset1:122
	ds_write2_b32 v46, v48, v28 offset0:188 offset1:254
	s_waitcnt lgkmcnt(0)
; #define GAS __attribute__((address_space(1)))
; #define LAS __attribute__((address_space(3)))
; #define LDS_WAIT() asm volatile("s_waitcnt lgkmcnt(0)" ::: "memory")
; __device__ __forceinline__ unsigned pk2(float lo, float hi) { return f2bf(lo) | (f2bf(hi) << 16); }
; __device__ __forceinline__ void tr_item(const float* W, int ld, int K, int nblk, int item, bf16* WT, bool gu, LAS float* scr, int lane) {
;     ...
;     const int c = lane & 7;
; #pragma unroll
;     for (int j = 0; j < 4; ++j) { const int n = (lane >> 3) + 8 * j; const LAS float* s = scr + (8 * c) * 33 + n;
;         v4u o; o.x = pk2(s[0 * 33], s[1 * 33]); o.y = pk2(s[2 * 33], s[3 * 33]); o.z = pk2(s[4 * 33], s[5 * 33]); o.w = pk2(s[6 * 33], s[7 * 33]);
;         *(GAS v4u*)(WT + (size_t)(drow0 + n) * K + k0 + 8 * c) = o; }
;     LDS_WAIT(); asm volatile("" ::: "memory");
	ds_read2_b32 v[52:53], v36 offset0:33 offset1:41
	ds_read2_b32 v[54:55], v36 offset1:8
	ds_read2_b32 v[56:57], v36 offset0:66 offset1:74
	ds_read2_b32 v[58:59], v36 offset0:99 offset1:107
	ds_read2_b32 v[60:61], v36 offset0:132 offset1:140
	ds_read2_b32 v[62:63], v36 offset0:165 offset1:173
	ds_read2_b32 v[64:65], v36 offset0:198 offset1:206
	ds_read2_b32 v[66:67], v36 offset0:231 offset1:239
	s_waitcnt lgkmcnt(7)
	v_bfe_u32 v49, v52, 16, 1
	s_waitcnt lgkmcnt(6)
	v_bfe_u32 v48, v54, 16, 1
	v_add3_u32 v48, v54, v48, s46
	v_lshrrev_b32_e32 v48, 16, v48
	v_add3_u32 v49, v52, v49, s46
	v_and_or_b32 v48, v49, s47, v48
	s_waitcnt lgkmcnt(5)
	v_bfe_u32 v49, v56, 16, 1
	v_add3_u32 v49, v56, v49, s46
	s_waitcnt lgkmcnt(4)
	v_bfe_u32 v50, v58, 16, 1
	v_lshrrev_b32_e32 v49, 16, v49
	v_add3_u32 v50, v58, v50, s46
	v_and_or_b32 v49, v50, s47, v49
	s_waitcnt lgkmcnt(3)
	v_bfe_u32 v50, v60, 16, 1
	v_add3_u32 v50, v60, v50, s46
	s_waitcnt lgkmcnt(2)
	v_bfe_u32 v51, v62, 16, 1
	v_lshrrev_b32_e32 v50, 16, v50
	v_add3_u32 v51, v62, v51, s46
	v_and_or_b32 v50, v51, s47, v50
	s_waitcnt lgkmcnt(1)
	v_bfe_u32 v51, v64, 16, 1
	v_add_u32_e32 v68, s24, v35
	v_add3_u32 v51, v64, v51, s46
	s_waitcnt lgkmcnt(0)
	v_bfe_u32 v52, v66, 16, 1
	v_ashrrev_i32_e32 v69, 31, v68
	v_lshl_add_u64 v[28:29], v[22:23], 0, s[16:17]
	v_lshrrev_b32_e32 v51, 16, v51
	v_add3_u32 v52, v66, v52, s46
	v_lshlrev_b64 v[68:69], 11, v[68:69]
	v_and_or_b32 v51, v52, s47, v51
	v_lshl_add_u64 v[68:69], v[28:29], 0, v[68:69]
	global_store_dwordx4 v[68:69], v[48:51], off
	v_bfe_u32 v52, v67, 16, 1
	v_add3_u32 v52, v67, v52, s46
	v_bfe_u32 v48, v55, 16, 1
	v_add3_u32 v48, v55, v48, s46
	v_bfe_u32 v49, v53, 16, 1
	v_lshrrev_b32_e32 v48, 16, v48
	v_add3_u32 v49, v53, v49, s46
	v_and_or_b32 v48, v49, s47, v48
	v_bfe_u32 v49, v57, 16, 1
	v_add3_u32 v49, v57, v49, s46
	v_bfe_u32 v50, v59, 16, 1
	v_lshrrev_b32_e32 v49, 16, v49
	v_add3_u32 v50, v59, v50, s46
	v_and_or_b32 v49, v50, s47, v49
	v_bfe_u32 v50, v61, 16, 1
	v_add3_u32 v50, v61, v50, s46
	v_bfe_u32 v51, v63, 16, 1
	v_lshrrev_b32_e32 v50, 16, v50
	v_add3_u32 v51, v63, v51, s46
	v_and_or_b32 v50, v51, s47, v50
	v_bfe_u32 v51, v65, 16, 1
	v_add3_u32 v51, v65, v51, s46
	v_lshrrev_b32_e32 v51, 16, v51
	v_and_or_b32 v51, v52, s47, v51
	v_add_u32_e32 v52, s24, v37
	v_ashrrev_i32_e32 v53, 31, v52
	v_lshlrev_b64 v[52:53], 11, v[52:53]
	v_lshl_add_u64 v[52:53], v[28:29], 0, v[52:53]
	global_store_dwordx4 v[52:53], v[48:51], off
	ds_read2_b32 v[52:53], v36 offset0:49 offset1:57
	ds_read2_b32 v[54:55], v36 offset0:16 offset1:24
	ds_read2_b32 v[56:57], v36 offset0:82 offset1:90
	ds_read2_b32 v[58:59], v36 offset0:115 offset1:123
	ds_read2_b32 v[60:61], v36 offset0:148 offset1:156
	ds_read2_b32 v[62:63], v36 offset0:181 offset1:189
	ds_read2_b32 v[64:65], v36 offset0:214 offset1:222
	ds_read2_b32 v[66:67], v36 offset0:247 offset1:255
	s_waitcnt lgkmcnt(7)
	v_bfe_u32 v49, v52, 16, 1
	s_waitcnt lgkmcnt(6)
	v_bfe_u32 v48, v54, 16, 1
	v_add3_u32 v48, v54, v48, s46
	v_lshrrev_b32_e32 v48, 16, v48
	v_add3_u32 v49, v52, v49, s46
	v_and_or_b32 v48, v49, s47, v48
	s_waitcnt lgkmcnt(5)
	v_bfe_u32 v49, v56, 16, 1
	v_add3_u32 v49, v56, v49, s46
	s_waitcnt lgkmcnt(4)
	v_bfe_u32 v50, v58, 16, 1
	v_lshrrev_b32_e32 v49, 16, v49
	v_add3_u32 v50, v58, v50, s46
	v_and_or_b32 v49, v50, s47, v49
	s_waitcnt lgkmcnt(3)
	v_bfe_u32 v50, v60, 16, 1
	v_add3_u32 v50, v60, v50, s46
	s_waitcnt lgkmcnt(2)
	v_bfe_u32 v51, v62, 16, 1
	v_lshrrev_b32_e32 v50, 16, v50
	v_add3_u32 v51, v62, v51, s46
	v_and_or_b32 v50, v51, s47, v50
	s_waitcnt lgkmcnt(1)
	v_bfe_u32 v51, v64, 16, 1
	v_add_u32_e32 v68, s24, v38
	v_add3_u32 v51, v64, v51, s46
	s_waitcnt lgkmcnt(0)
	v_bfe_u32 v52, v66, 16, 1
	v_ashrrev_i32_e32 v69, 31, v68
	v_lshrrev_b32_e32 v51, 16, v51
	v_add3_u32 v52, v66, v52, s46
	v_lshlrev_b64 v[68:69], 11, v[68:69]
	v_and_or_b32 v51, v52, s47, v51
	v_lshl_add_u64 v[68:69], v[28:29], 0, v[68:69]
	global_store_dwordx4 v[68:69], v[48:51], off
	v_bfe_u32 v52, v67, 16, 1
	v_add3_u32 v52, v67, v52, s46
	v_bfe_u32 v48, v55, 16, 1
	v_add3_u32 v48, v55, v48, s46
	v_bfe_u32 v49, v53, 16, 1
	v_lshrrev_b32_e32 v48, 16, v48
	v_add3_u32 v49, v53, v49, s46
	v_and_or_b32 v48, v49, s47, v48
	v_bfe_u32 v49, v57, 16, 1
	v_add3_u32 v49, v57, v49, s46
	v_bfe_u32 v50, v59, 16, 1
	v_lshrrev_b32_e32 v49, 16, v49
	v_add3_u32 v50, v59, v50, s46
	v_and_or_b32 v49, v50, s47, v49
	v_bfe_u32 v50, v61, 16, 1
	v_add3_u32 v50, v61, v50, s46
	v_bfe_u32 v51, v63, 16, 1
	v_lshrrev_b32_e32 v50, 16, v50
	v_add3_u32 v51, v63, v51, s46
	v_and_or_b32 v50, v51, s47, v50
	v_bfe_u32 v51, v65, 16, 1
	v_add3_u32 v51, v65, v51, s46
	v_lshrrev_b32_e32 v51, 16, v51
	v_and_or_b32 v51, v52, s47, v51
	v_add_u32_e32 v52, s24, v39
	v_ashrrev_i32_e32 v53, 31, v52
	v_lshlrev_b64 v[52:53], 11, v[52:53]
	v_lshl_add_u64 v[28:29], v[28:29], 0, v[52:53]
	global_store_dwordx4 v[28:29], v[48:51], off
	s_waitcnt lgkmcnt(0)

; #define LDS_WAIT() asm volatile("s_waitcnt lgkmcnt(0)" ::: "memory")
; __device__ __forceinline__ void tr_item(const float* W, int ld, int K, int nblk, int item, bf16* WT, bool gu, LAS float* scr, int lane) {
;     const int kb = item / nblk, nb = item % nblk, k0 = 64 * kb, n0 = 32 * nb;
;     int drow0 = n0;
;     if (gu) { const int bj = n0 / FF, j = n0 - bj * FF; drow0 = 256 * (j / 128) + 128 * bj + (j % 128); }
;     { float t_[32];
; #pragma unroll
;       for (int i = 0; i < 32; ++i) t_[i] = W[(size_t)(k0 + 2 * i + (lane >> 5)) * ld + n0 + (lane & 31)];
; #pragma unroll
;       for (int i = 0; i < 32; ++i) scr[(2 * i + (lane >> 5)) * 33 + (lane & 31)] = t_[i]; }
;     LDS_WAIT(); asm volatile("" ::: "memory");
.LBB0_1148:
	s_andn2_b64 vcc, exec, s[24:25]
	s_cbranch_vccnz .LBB0_1150
	s_add_i32 s16, s37, 0xf800
	s_and_b32 s24, s16, 0xffff
	s_mul_i32 s24, s24, 0xaaab
	s_lshr_b32 s25, s24, 21
	s_mul_i32 s24, s25, 48
	s_sub_i32 s16, s16, s24
	s_lshl_b32 s16, s16, 5
	s_and_b32 s24, s16, 0xffe0
	v_lshl_add_u32 v64, s25, 6, v30
	s_lshl_b32 s16, s24, 2
	v_lshl_add_u64 v[28:29], v[10:11], 0, s[16:17]
	v_add_u32_e32 v50, 2, v64
	v_add_u32_e32 v52, 4, v64
	v_add_u32_e32 v54, 6, v64
	v_add_u32_e32 v56, 8, v64
	v_add_u32_e32 v58, 10, v64
	v_add_u32_e32 v60, 12, v64
	v_add_u32_e32 v62, 14, v64
	v_mad_i64_i32 v[48:49], s[26:27], v64, s48, v[28:29]
	v_mad_i64_i32 v[50:51], s[26:27], v50, s48, v[28:29]
	v_mad_i64_i32 v[52:53], s[26:27], v52, s48, v[28:29]
	v_mad_i64_i32 v[54:55], s[26:27], v54, s48, v[28:29]
	v_mad_i64_i32 v[56:57], s[26:27], v56, s48, v[28:29]
	v_mad_i64_i32 v[58:59], s[26:27], v58, s48, v[28:29]
	v_mad_i64_i32 v[60:61], s[26:27], v60, s48, v[28:29]
	v_mad_i64_i32 v[62:63], s[26:27], v62, s48, v[28:29]
	global_load_dword v65, v[48:49], off nt
	global_load_dword v66, v[50:51], off nt
	global_load_dword v67, v[52:53], off nt
	global_load_dword v68, v[54:55], off nt
	global_load_dword v69, v[56:57], off nt
	global_load_dword v70, v[58:59], off nt
	global_load_dword v71, v[60:61], off nt
	global_load_dword v72, v[62:63], off nt
	v_add_u32_e32 v48, 16, v64
	v_add_u32_e32 v50, 18, v64
	v_add_u32_e32 v52, 20, v64
	v_add_u32_e32 v54, 22, v64
	v_add_u32_e32 v56, 24, v64
	v_add_u32_e32 v58, 26, v64
	v_add_u32_e32 v60, 28, v64
	v_add_u32_e32 v62, 30, v64
	v_mad_i64_i32 v[48:49], s[26:27], v48, s48, v[28:29]
	v_mad_i64_i32 v[50:51], s[26:27], v50, s48, v[28:29]
	v_mad_i64_i32 v[52:53], s[26:27], v52, s48, v[28:29]
	v_mad_i64_i32 v[54:55], s[26:27], v54, s48, v[28:29]
	v_mad_i64_i32 v[56:57], s[26:27], v56, s48, v[28:29]
	v_mad_i64_i32 v[58:59], s[26:27], v58, s48, v[28:29]
	v_mad_i64_i32 v[60:61], s[26:27], v60, s48, v[28:29]
	v_mad_i64_i32 v[62:63], s[26:27], v62, s48, v[28:29]
	global_load_dword v73, v[48:49], off nt
	global_load_dword v74, v[50:51], off nt
	global_load_dword v75, v[52:53], off nt
	global_load_dword v76, v[54:55], off nt
	global_load_dword v77, v[56:57], off nt
	global_load_dword v78, v[58:59], off nt
	global_load_dword v79, v[60:61], off nt
	global_load_dword v80, v[62:63], off nt
	v_add_u32_e32 v48, 32, v64
	v_add_u32_e32 v50, 34, v64
	v_add_u32_e32 v52, 36, v64
	v_add_u32_e32 v54, 38, v64
	v_add_u32_e32 v56, 40, v64
	v_add_u32_e32 v58, 42, v64
	v_add_u32_e32 v60, 44, v64
	v_add_u32_e32 v62, 46, v64
	v_mad_i64_i32 v[48:49], s[26:27], v48, s48, v[28:29]
	v_mad_i64_i32 v[50:51], s[26:27], v50, s48, v[28:29]
	v_mad_i64_i32 v[52:53], s[26:27], v52, s48, v[28:29]
	v_mad_i64_i32 v[54:55], s[26:27], v54, s48, v[28:29]
	v_mad_i64_i32 v[56:57], s[26:27], v56, s48, v[28:29]
	v_mad_i64_i32 v[58:59], s[26:27], v58, s48, v[28:29]
	v_mad_i64_i32 v[60:61], s[26:27], v60, s48, v[28:29]
	v_mad_i64_i32 v[62:63], s[26:27], v62, s48, v[28:29]
	global_load_dword v81, v[48:49], off nt
	global_load_dword v82, v[50:51], off nt
	global_load_dword v83, v[52:53], off nt
	global_load_dword v84, v[54:55], off nt
	global_load_dword v85, v[56:57], off nt
	global_load_dword v86, v[58:59], off nt
	global_load_dword v87, v[60:61], off nt
	s_nop 0
	global_load_dword v62, v[62:63], off nt
	v_add_u32_e32 v48, 48, v64
	v_add_u32_e32 v50, 50, v64
	v_add_u32_e32 v52, 52, v64
	v_add_u32_e32 v54, 54, v64
	v_add_u32_e32 v56, 56, v64
	v_add_u32_e32 v58, 58, v64
	v_add_u32_e32 v60, 60, v64
	v_add_u32_e32 v63, 62, v64
	v_mad_i64_i32 v[48:49], s[26:27], v48, s48, v[28:29]
	v_mad_i64_i32 v[50:51], s[26:27], v50, s48, v[28:29]
	v_mad_i64_i32 v[52:53], s[26:27], v52, s48, v[28:29]
	v_mad_i64_i32 v[54:55], s[26:27], v54, s48, v[28:29]
	v_mad_i64_i32 v[56:57], s[26:27], v56, s48, v[28:29]
	v_mad_i64_i32 v[58:59], s[26:27], v58, s48, v[28:29]
	v_mad_i64_i32 v[60:61], s[26:27], v60, s48, v[28:29]
	v_mad_i64_i32 v[28:29], s[26:27], v63, s48, v[28:29]
	global_load_dword v48, v[48:49], off nt
	s_nop 0
	global_load_dword v49, v[50:51], off nt
	s_nop 0
	global_load_dword v50, v[52:53], off nt
	global_load_dword v51, v[54:55], off nt
	s_nop 0
	global_load_dword v52, v[56:57], off nt
	global_load_dword v53, v[58:59], off nt
	global_load_dword v54, v[60:61], off nt
	s_nop 0
	global_load_dword v28, v[28:29], off nt
	s_waitcnt vmcnt(0)
	ds_write2_b32 v31, v65, v66 offset1:66
	ds_write2_b32 v31, v67, v68 offset0:132 offset1:198
	ds_write2_b32 v40, v69, v70 offset0:8 offset1:74
	ds_write2_b32 v40, v71, v72 offset0:140 offset1:206
	ds_write2_b32 v41, v73, v74 offset0:16 offset1:82
	ds_write2_b32 v41, v75, v76 offset0:148 offset1:214
	ds_write2_b32 v42, v77, v78 offset0:24 offset1:90
	ds_write2_b32 v42, v79, v80 offset0:156 offset1:222
	ds_write2_b32 v43, v81, v82 offset0:32 offset1:98
	ds_write2_b32 v43, v83, v84 offset0:164 offset1:230
	ds_write2_b32 v44, v85, v86 offset0:40 offset1:106
	ds_write2_b32 v44, v87, v62 offset0:172 offset1:238
	ds_write2_b32 v45, v48, v49 offset0:48 offset1:114
	ds_write2_b32 v45, v50, v51 offset0:180 offset1:246
	ds_write2_b32 v46, v52, v53 offset0:56 offset1:122
	ds_write2_b32 v46, v54, v28 offset0:188 offset1:254
	s_waitcnt lgkmcnt(0)
; #define GAS __attribute__((address_space(1)))
; #define LAS __attribute__((address_space(3)))
; #define LDS_WAIT() asm volatile("s_waitcnt lgkmcnt(0)" ::: "memory")
; __device__ __forceinline__ unsigned pk2(float lo, float hi) { return f2bf(lo) | (f2bf(hi) << 16); }
; __device__ __forceinline__ void tr_item(const float* W, int ld, int K, int nblk, int item, bf16* WT, bool gu, LAS float* scr, int lane) {
;     ...
;     const int c = lane & 7;
; #pragma unroll
;     for (int j = 0; j < 4; ++j) { const int n = (lane >> 3) + 8 * j; const LAS float* s = scr + (8 * c) * 33 + n;
;         v4u o; o.x = pk2(s[0 * 33], s[1 * 33]); o.y = pk2(s[2 * 33], s[3 * 33]); o.z = pk2(s[4 * 33], s[5 * 33]); o.w = pk2(s[6 * 33], s[7 * 33]);
;         *(GAS v4u*)(WT + (size_t)(drow0 + n) * K + k0 + 8 * c) = o; }
;     LDS_WAIT(); asm volatile("" ::: "memory");
	ds_read2_b32 v[28:29], v36 offset1:8
	ds_read2_b32 v[54:55], v36 offset0:33 offset1:41
	ds_read2_b32 v[56:57], v36 offset0:66 offset1:74
	ds_read2_b32 v[58:59], v36 offset0:99 offset1:107
	ds_read2_b32 v[60:61], v36 offset0:132 offset1:140
	s_waitcnt lgkmcnt(4)
	v_bfe_u32 v48, v28, 16, 1
	v_add3_u32 v28, v28, v48, s46
	s_waitcnt lgkmcnt(3)
	v_bfe_u32 v48, v54, 16, 1
	v_lshrrev_b32_e32 v28, 16, v28
	v_add3_u32 v48, v54, v48, s46
	ds_read2_b32 v[62:63], v36 offset0:165 offset1:173
	v_and_or_b32 v48, v48, s47, v28
	s_waitcnt lgkmcnt(3)
	v_bfe_u32 v28, v56, 16, 1
	v_add3_u32 v28, v56, v28, s46
	s_waitcnt lgkmcnt(2)
	v_bfe_u32 v49, v58, 16, 1
	ds_read2_b32 v[64:65], v36 offset0:198 offset1:206
	v_lshrrev_b32_e32 v28, 16, v28
	v_add3_u32 v49, v58, v49, s46
	ds_read2_b32 v[66:67], v36 offset0:231 offset1:239
	v_and_or_b32 v49, v49, s47, v28
	s_waitcnt lgkmcnt(3)
	v_bfe_u32 v28, v60, 16, 1
	v_add3_u32 v28, v60, v28, s46
	s_waitcnt lgkmcnt(2)
	v_bfe_u32 v50, v62, 16, 1
	v_lshrrev_b32_e32 v28, 16, v28
	v_add3_u32 v50, v62, v50, s46
	v_and_or_b32 v50, v50, s47, v28
	s_waitcnt lgkmcnt(1)
	v_bfe_u32 v28, v64, 16, 1
	v_add3_u32 v28, v64, v28, s46
	s_waitcnt lgkmcnt(0)
	v_bfe_u32 v51, v66, 16, 1
	v_lshrrev_b32_e32 v28, 16, v28
	v_add3_u32 v51, v66, v51, s46
	v_add_u32_e32 v68, s24, v35
	s_lshl_b32 s16, s25, 7
	v_and_or_b32 v51, v51, s47, v28
	v_ashrrev_i32_e32 v69, 31, v68
	v_bfe_u32 v28, v29, 16, 1
	v_lshl_add_u64 v[52:53], v[12:13], 0, s[16:17]
	v_lshlrev_b64 v[68:69], 11, v[68:69]
	v_add3_u32 v28, v29, v28, s46
	v_bfe_u32 v29, v55, 16, 1
	v_lshl_add_u64 v[68:69], v[52:53], 0, v[68:69]
	v_lshrrev_b32_e32 v28, 16, v28
	v_add3_u32 v29, v55, v29, s46
	global_store_dwordx4 v[68:69], v[48:51], off
	ds_read2_b32 v[54:55], v36 offset0:16 offset1:24
	v_add_u32_e32 v68, s24, v38
	v_and_or_b32 v48, v29, s47, v28
	v_bfe_u32 v28, v57, 16, 1
	v_add3_u32 v28, v57, v28, s46
	v_bfe_u32 v29, v59, 16, 1
	v_lshrrev_b32_e32 v28, 16, v28
	v_add3_u32 v29, v59, v29, s46
	v_and_or_b32 v49, v29, s47, v28
	v_bfe_u32 v28, v61, 16, 1
	v_add3_u32 v28, v61, v28, s46
	v_bfe_u32 v29, v63, 16, 1
	v_lshrrev_b32_e32 v28, 16, v28
	v_add3_u32 v29, v63, v29, s46
	v_and_or_b32 v50, v29, s47, v28
	v_bfe_u32 v28, v65, 16, 1
	v_add3_u32 v28, v65, v28, s46
	v_bfe_u32 v29, v67, 16, 1
	v_lshrrev_b32_e32 v28, 16, v28
	v_add3_u32 v29, v67, v29, s46
	v_and_or_b32 v51, v29, s47, v28
	v_add_u32_e32 v28, s24, v37
	v_ashrrev_i32_e32 v29, 31, v28
	v_lshlrev_b64 v[28:29], 11, v[28:29]
	v_lshl_add_u64 v[28:29], v[52:53], 0, v[28:29]
	global_store_dwordx4 v[28:29], v[48:51], off
	ds_read2_b32 v[28:29], v36 offset0:49 offset1:57
	ds_read2_b32 v[56:57], v36 offset0:82 offset1:90
	ds_read2_b32 v[58:59], v36 offset0:115 offset1:123
	s_waitcnt lgkmcnt(3)
	v_bfe_u32 v48, v54, 16, 1
	v_add3_u32 v48, v54, v48, s46
	s_waitcnt lgkmcnt(2)
	v_bfe_u32 v49, v28, 16, 1
	ds_read2_b32 v[60:61], v36 offset0:148 offset1:156
	v_lshrrev_b32_e32 v48, 16, v48
	v_add3_u32 v28, v28, v49, s46
	ds_read2_b32 v[62:63], v36 offset0:181 offset1:189
	v_and_or_b32 v48, v28, s47, v48
	s_waitcnt lgkmcnt(3)
	v_bfe_u32 v28, v56, 16, 1
	v_add3_u32 v28, v56, v28, s46
	s_waitcnt lgkmcnt(2)
	v_bfe_u32 v49, v58, 16, 1
	ds_read2_b32 v[64:65], v36 offset0:214 offset1:222
	v_lshrrev_b32_e32 v28, 16, v28
	v_add3_u32 v49, v58, v49, s46
	ds_read2_b32 v[66:67], v36 offset0:247 offset1:255
	v_and_or_b32 v49, v49, s47, v28
	s_waitcnt lgkmcnt(3)
	v_bfe_u32 v28, v60, 16, 1
	v_add3_u32 v28, v60, v28, s46
	s_waitcnt lgkmcnt(2)
	v_bfe_u32 v50, v62, 16, 1
	v_lshrrev_b32_e32 v28, 16, v28
	v_add3_u32 v50, v62, v50, s46
	v_and_or_b32 v50, v50, s47, v28
	s_waitcnt lgkmcnt(1)
	v_bfe_u32 v28, v64, 16, 1
	v_add3_u32 v28, v64, v28, s46
	s_waitcnt lgkmcnt(0)
	v_bfe_u32 v51, v66, 16, 1
	v_ashrrev_i32_e32 v69, 31, v68
	v_lshrrev_b32_e32 v28, 16, v28
	v_add3_u32 v51, v66, v51, s46
	v_lshlrev_b64 v[68:69], 11, v[68:69]
	v_and_or_b32 v51, v51, s47, v28
	v_lshl_add_u64 v[68:69], v[52:53], 0, v[68:69]
	v_bfe_u32 v28, v55, 16, 1
	global_store_dwordx4 v[68:69], v[48:51], off
	v_add3_u32 v28, v55, v28, s46
	v_lshrrev_b32_e32 v28, 16, v28
	v_bfe_u32 v48, v29, 16, 1
	v_add3_u32 v29, v29, v48, s46
	v_and_or_b32 v48, v29, s47, v28
	v_bfe_u32 v28, v57, 16, 1
	v_add3_u32 v28, v57, v28, s46
	v_bfe_u32 v29, v59, 16, 1
	v_lshrrev_b32_e32 v28, 16, v28
	v_add3_u32 v29, v59, v29, s46
	v_and_or_b32 v49, v29, s47, v28
	v_bfe_u32 v28, v61, 16, 1
	v_add3_u32 v28, v61, v28, s46
	v_bfe_u32 v29, v63, 16, 1
	v_lshrrev_b32_e32 v28, 16, v28
	v_add3_u32 v29, v63, v29, s46
	v_and_or_b32 v50, v29, s47, v28
	v_bfe_u32 v28, v65, 16, 1
	v_add3_u32 v28, v65, v28, s46
	v_bfe_u32 v29, v67, 16, 1
	v_lshrrev_b32_e32 v28, 16, v28
	v_add3_u32 v29, v67, v29, s46
	v_and_or_b32 v51, v29, s47, v28
	v_add_u32_e32 v28, s24, v39
	v_ashrrev_i32_e32 v29, 31, v28
	v_lshlrev_b64 v[28:29], 11, v[28:29]
	v_lshl_add_u64 v[28:29], v[52:53], 0, v[28:29]
	global_store_dwordx4 v[28:29], v[48:51], off
	s_waitcnt lgkmcnt(0)

; #define LDS_WAIT() asm volatile("s_waitcnt lgkmcnt(0)" ::: "memory")
; __device__ __forceinline__ void tr_item(const float* W, int ld, int K, int nblk, int item, bf16* WT, bool gu, LAS float* scr, int lane) {
;     const int kb = item / nblk, nb = item % nblk, k0 = 64 * kb, n0 = 32 * nb;
;     int drow0 = n0;
;     if (gu) { const int bj = n0 / FF, j = n0 - bj * FF; drow0 = 256 * (j / 128) + 128 * bj + (j % 128); }
;     { float t_[32];
; #pragma unroll
;       for (int i = 0; i < 32; ++i) t_[i] = W[(size_t)(k0 + 2 * i + (lane >> 5)) * ld + n0 + (lane & 31)];
; #pragma unroll
;       for (int i = 0; i < 32; ++i) scr[(2 * i + (lane >> 5)) * 33 + (lane & 31)] = t_[i]; }
;     LDS_WAIT(); asm volatile("" ::: "memory");
.LBB0_1151:
	s_andn2_b64 vcc, exec, s[24:25]
	s_cbranch_vccnz .LBB0_1153
	s_add_i32 s16, s42, 0x2a00
	s_and_b32 s25, s16, 0x1ffc0
	s_and_b32 s24, s40, 0x3e0
	v_add_u32_e32 v28, s25, v30
	s_lshl_b32 s16, s24, 2
	v_ashrrev_i32_e32 v29, 31, v28
	v_lshl_add_u64 v[48:49], v[14:15], 0, s[16:17]
	v_lshlrev_b64 v[28:29], 12, v[28:29]
	v_lshl_add_u64 v[28:29], v[48:49], 0, v[28:29]
	v_add_co_u32_e32 v48, vcc, 0x2000, v28
	global_load_dword v50, v[28:29], off nt
	s_nop 0
	v_addc_co_u32_e32 v49, vcc, 0, v29, vcc
	global_load_dword v51, v[48:49], off nt
	v_add_co_u32_e32 v48, vcc, 0x4000, v28
	s_lshl_b32 s16, s25, 1
	s_nop 0
	v_addc_co_u32_e32 v49, vcc, 0, v29, vcc
	global_load_dword v52, v[48:49], off nt
	v_add_co_u32_e32 v48, vcc, 0x6000, v28
	s_nop 1
	v_addc_co_u32_e32 v49, vcc, 0, v29, vcc
	global_load_dword v53, v[48:49], off nt
	v_add_co_u32_e32 v48, vcc, 0x8000, v28
	s_nop 1
	v_addc_co_u32_e32 v49, vcc, 0, v29, vcc
	global_load_dword v54, v[48:49], off nt
	v_add_co_u32_e32 v48, vcc, 0xa000, v28
	s_nop 1
	v_addc_co_u32_e32 v49, vcc, 0, v29, vcc
	global_load_dword v55, v[48:49], off nt
	v_add_co_u32_e32 v48, vcc, 0xc000, v28
	s_nop 1
	v_addc_co_u32_e32 v49, vcc, 0, v29, vcc
	global_load_dword v56, v[48:49], off nt
	v_add_co_u32_e32 v48, vcc, 0xe000, v28
	s_nop 1
	v_addc_co_u32_e32 v49, vcc, 0, v29, vcc
	global_load_dword v57, v[48:49], off nt
	v_add_co_u32_e32 v48, vcc, 0x10000, v28
	s_nop 1
	v_addc_co_u32_e32 v49, vcc, 0, v29, vcc
	global_load_dword v58, v[48:49], off nt
	v_add_co_u32_e32 v48, vcc, 0x12000, v28
	s_nop 1
	v_addc_co_u32_e32 v49, vcc, 0, v29, vcc
	global_load_dword v59, v[48:49], off nt
	v_add_co_u32_e32 v48, vcc, 0x14000, v28
	s_nop 1
	v_addc_co_u32_e32 v49, vcc, 0, v29, vcc
	global_load_dword v60, v[48:49], off nt
	v_add_co_u32_e32 v48, vcc, 0x16000, v28
	s_nop 1
	v_addc_co_u32_e32 v49, vcc, 0, v29, vcc
	global_load_dword v61, v[48:49], off nt
	v_add_co_u32_e32 v48, vcc, 0x18000, v28
	s_nop 1
	v_addc_co_u32_e32 v49, vcc, 0, v29, vcc
	global_load_dword v62, v[48:49], off nt
	v_add_co_u32_e32 v48, vcc, 0x1a000, v28
	s_nop 1
	v_addc_co_u32_e32 v49, vcc, 0, v29, vcc
	global_load_dword v63, v[48:49], off nt
	v_add_co_u32_e32 v48, vcc, 0x1c000, v28
	s_nop 1
	v_addc_co_u32_e32 v49, vcc, 0, v29, vcc
	global_load_dword v64, v[48:49], off nt
	v_add_co_u32_e32 v48, vcc, 0x1e000, v28
	s_nop 1
	v_addc_co_u32_e32 v49, vcc, 0, v29, vcc
	global_load_dword v65, v[48:49], off nt
	v_add_co_u32_e32 v48, vcc, 0x20000, v28
	s_nop 1
	v_addc_co_u32_e32 v49, vcc, 0, v29, vcc
	global_load_dword v66, v[48:49], off nt
	v_add_co_u32_e32 v48, vcc, 0x22000, v28
	s_nop 1
	v_addc_co_u32_e32 v49, vcc, 0, v29, vcc
	global_load_dword v67, v[48:49], off nt
	v_add_co_u32_e32 v48, vcc, 0x24000, v28
	s_nop 1
	v_addc_co_u32_e32 v49, vcc, 0, v29, vcc
	global_load_dword v68, v[48:49], off nt
	v_add_co_u32_e32 v48, vcc, 0x26000, v28
	s_nop 1
	v_addc_co_u32_e32 v49, vcc, 0, v29, vcc
	global_load_dword v69, v[48:49], off nt
	v_add_co_u32_e32 v48, vcc, 0x28000, v28
	s_nop 1
	v_addc_co_u32_e32 v49, vcc, 0, v29, vcc
	global_load_dword v70, v[48:49], off nt
	v_add_co_u32_e32 v48, vcc, 0x2a000, v28
	s_nop 1
	v_addc_co_u32_e32 v49, vcc, 0, v29, vcc
	global_load_dword v71, v[48:49], off nt
	v_add_co_u32_e32 v48, vcc, 0x2c000, v28
	s_nop 1
	v_addc_co_u32_e32 v49, vcc, 0, v29, vcc
	global_load_dword v72, v[48:49], off nt
	v_add_co_u32_e32 v48, vcc, 0x2e000, v28
	s_nop 1
	v_addc_co_u32_e32 v49, vcc, 0, v29, vcc
	global_load_dword v73, v[48:49], off nt
	v_add_co_u32_e32 v48, vcc, 0x30000, v28
	s_nop 1
	v_addc_co_u32_e32 v49, vcc, 0, v29, vcc
	global_load_dword v74, v[48:49], off nt
	v_add_co_u32_e32 v48, vcc, 0x32000, v28
	s_nop 1
	v_addc_co_u32_e32 v49, vcc, 0, v29, vcc
	global_load_dword v75, v[48:49], off nt
	v_add_co_u32_e32 v48, vcc, 0x34000, v28
	s_nop 1
	v_addc_co_u32_e32 v49, vcc, 0, v29, vcc
	global_load_dword v76, v[48:49], off nt
	v_add_co_u32_e32 v48, vcc, 0x36000, v28
	s_nop 1
	v_addc_co_u32_e32 v49, vcc, 0, v29, vcc
	global_load_dword v77, v[48:49], off nt
	v_add_co_u32_e32 v48, vcc, 0x38000, v28
	s_nop 1
	v_addc_co_u32_e32 v49, vcc, 0, v29, vcc
	global_load_dword v78, v[48:49], off nt
	v_add_co_u32_e32 v48, vcc, 0x3a000, v28
	s_nop 1
	v_addc_co_u32_e32 v49, vcc, 0, v29, vcc
	global_load_dword v79, v[48:49], off nt
	v_add_co_u32_e32 v48, vcc, 0x3c000, v28
	s_nop 1
	v_addc_co_u32_e32 v49, vcc, 0, v29, vcc
	v_add_co_u32_e32 v28, vcc, 0x3e000, v28
	global_load_dword v48, v[48:49], off nt
	s_nop 0
	v_addc_co_u32_e32 v29, vcc, 0, v29, vcc
	global_load_dword v28, v[28:29], off nt
	s_waitcnt vmcnt(0)
	ds_write2_b32 v31, v50, v51 offset1:66
	ds_write2_b32 v31, v52, v53 offset0:132 offset1:198
	ds_write2_b32 v40, v54, v55 offset0:8 offset1:74
	ds_write2_b32 v40, v56, v57 offset0:140 offset1:206
	ds_write2_b32 v41, v58, v59 offset0:16 offset1:82
	ds_write2_b32 v41, v60, v61 offset0:148 offset1:214
	ds_write2_b32 v42, v62, v63 offset0:24 offset1:90
	ds_write2_b32 v42, v64, v65 offset0:156 offset1:222
	ds_write2_b32 v43, v66, v67 offset0:32 offset1:98
	ds_write2_b32 v43, v68, v69 offset0:164 offset1:230
	ds_write2_b32 v44, v70, v71 offset0:40 offset1:106
	ds_write2_b32 v44, v72, v73 offset0:172 offset1:238
	ds_write2_b32 v45, v74, v75 offset0:48 offset1:114
	ds_write2_b32 v45, v76, v77 offset0:180 offset1:246
	ds_write2_b32 v46, v78, v79 offset0:56 offset1:122
	ds_write2_b32 v46, v48, v28 offset0:188 offset1:254
	s_waitcnt lgkmcnt(0)
; #define GAS __attribute__((address_space(1)))
; #define LAS __attribute__((address_space(3)))
; #define LDS_WAIT() asm volatile("s_waitcnt lgkmcnt(0)" ::: "memory")
; __device__ __forceinline__ unsigned pk2(float lo, float hi) { return f2bf(lo) | (f2bf(hi) << 16); }
; __device__ __forceinline__ void tr_item(const float* W, int ld, int K, int nblk, int item, bf16* WT, bool gu, LAS float* scr, int lane) {
;     ...
;     const int c = lane & 7;
; #pragma unroll
;     for (int j = 0; j < 4; ++j) { const int n = (lane >> 3) + 8 * j; const LAS float* s = scr + (8 * c) * 33 + n;
;         v4u o; o.x = pk2(s[0 * 33], s[1 * 33]); o.y = pk2(s[2 * 33], s[3 * 33]); o.z = pk2(s[4 * 33], s[5 * 33]); o.w = pk2(s[6 * 33], s[7 * 33]);
;         *(GAS v4u*)(WT + (size_t)(drow0 + n) * K + k0 + 8 * c) = o; }
;     LDS_WAIT(); asm volatile("" ::: "memory");
	ds_read2_b32 v[52:53], v36 offset0:33 offset1:41
	ds_read2_b32 v[54:55], v36 offset1:8
	ds_read2_b32 v[56:57], v36 offset0:66 offset1:74
	ds_read2_b32 v[58:59], v36 offset0:99 offset1:107
	ds_read2_b32 v[60:61], v36 offset0:132 offset1:140
	ds_read2_b32 v[62:63], v36 offset0:165 offset1:173
	ds_read2_b32 v[64:65], v36 offset0:198 offset1:206
	ds_read2_b32 v[66:67], v36 offset0:231 offset1:239
	s_waitcnt lgkmcnt(7)
	v_bfe_u32 v49, v52, 16, 1
	s_waitcnt lgkmcnt(6)
	v_bfe_u32 v48, v54, 16, 1
	v_add3_u32 v48, v54, v48, s46
	v_lshrrev_b32_e32 v48, 16, v48
	v_add3_u32 v49, v52, v49, s46
	v_and_or_b32 v48, v49, s47, v48
	s_waitcnt lgkmcnt(5)
	v_bfe_u32 v49, v56, 16, 1
	v_add3_u32 v49, v56, v49, s46
	s_waitcnt lgkmcnt(4)
	v_bfe_u32 v50, v58, 16, 1
	v_lshrrev_b32_e32 v49, 16, v49
	v_add3_u32 v50, v58, v50, s46
	v_and_or_b32 v49, v50, s47, v49
	s_waitcnt lgkmcnt(3)
	v_bfe_u32 v50, v60, 16, 1
	v_add3_u32 v50, v60, v50, s46
	s_waitcnt lgkmcnt(2)
	v_bfe_u32 v51, v62, 16, 1
	v_lshrrev_b32_e32 v50, 16, v50
	v_add3_u32 v51, v62, v51, s46
	v_and_or_b32 v50, v51, s47, v50
	s_waitcnt lgkmcnt(1)
	v_bfe_u32 v51, v64, 16, 1
	v_add_u32_e32 v68, s24, v35
	v_add3_u32 v51, v64, v51, s46
	s_waitcnt lgkmcnt(0)
	v_bfe_u32 v52, v66, 16, 1
	v_ashrrev_i32_e32 v69, 31, v68
	v_lshl_add_u64 v[28:29], v[24:25], 0, s[16:17]
	v_lshrrev_b32_e32 v51, 16, v51
	v_add3_u32 v52, v66, v52, s46
	v_lshlrev_b64 v[68:69], 11, v[68:69]
	v_and_or_b32 v51, v52, s47, v51
	v_lshl_add_u64 v[68:69], v[28:29], 0, v[68:69]
	global_store_dwordx4 v[68:69], v[48:51], off
	v_bfe_u32 v52, v67, 16, 1
	v_add3_u32 v52, v67, v52, s46
	v_bfe_u32 v48, v55, 16, 1
	v_add3_u32 v48, v55, v48, s46
	v_bfe_u32 v49, v53, 16, 1
	v_lshrrev_b32_e32 v48, 16, v48
	v_add3_u32 v49, v53, v49, s46
	v_and_or_b32 v48, v49, s47, v48
	v_bfe_u32 v49, v57, 16, 1
	v_add3_u32 v49, v57, v49, s46
	v_bfe_u32 v50, v59, 16, 1
	v_lshrrev_b32_e32 v49, 16, v49
	v_add3_u32 v50, v59, v50, s46
	v_and_or_b32 v49, v50, s47, v49
	v_bfe_u32 v50, v61, 16, 1
	v_add3_u32 v50, v61, v50, s46
	v_bfe_u32 v51, v63, 16, 1
	v_lshrrev_b32_e32 v50, 16, v50
	v_add3_u32 v51, v63, v51, s46
	v_and_or_b32 v50, v51, s47, v50
	v_bfe_u32 v51, v65, 16, 1
	v_add3_u32 v51, v65, v51, s46
	v_lshrrev_b32_e32 v51, 16, v51
	v_and_or_b32 v51, v52, s47, v51
	v_add_u32_e32 v52, s24, v37
	v_ashrrev_i32_e32 v53, 31, v52
	v_lshlrev_b64 v[52:53], 11, v[52:53]
	v_lshl_add_u64 v[52:53], v[28:29], 0, v[52:53]
	global_store_dwordx4 v[52:53], v[48:51], off
	ds_read2_b32 v[52:53], v36 offset0:49 offset1:57
	ds_read2_b32 v[54:55], v36 offset0:16 offset1:24
	ds_read2_b32 v[56:57], v36 offset0:82 offset1:90
	ds_read2_b32 v[58:59], v36 offset0:115 offset1:123
	ds_read2_b32 v[60:61], v36 offset0:148 offset1:156
	ds_read2_b32 v[62:63], v36 offset0:181 offset1:189
	ds_read2_b32 v[64:65], v36 offset0:214 offset1:222
	ds_read2_b32 v[66:67], v36 offset0:247 offset1:255
	s_waitcnt lgkmcnt(7)
	v_bfe_u32 v49, v52, 16, 1
	s_waitcnt lgkmcnt(6)
	v_bfe_u32 v48, v54, 16, 1
	v_add3_u32 v48, v54, v48, s46
	v_lshrrev_b32_e32 v48, 16, v48
	v_add3_u32 v49, v52, v49, s46
	v_and_or_b32 v48, v49, s47, v48
	s_waitcnt lgkmcnt(5)
	v_bfe_u32 v49, v56, 16, 1
	v_add3_u32 v49, v56, v49, s46
	s_waitcnt lgkmcnt(4)
	v_bfe_u32 v50, v58, 16, 1
	v_lshrrev_b32_e32 v49, 16, v49
	v_add3_u32 v50, v58, v50, s46
	v_and_or_b32 v49, v50, s47, v49
	s_waitcnt lgkmcnt(3)
	v_bfe_u32 v50, v60, 16, 1
	v_add3_u32 v50, v60, v50, s46
	s_waitcnt lgkmcnt(2)
	v_bfe_u32 v51, v62, 16, 1
	v_lshrrev_b32_e32 v50, 16, v50
	v_add3_u32 v51, v62, v51, s46
	v_and_or_b32 v50, v51, s47, v50
	s_waitcnt lgkmcnt(1)
	v_bfe_u32 v51, v64, 16, 1
	v_add_u32_e32 v68, s24, v38
	v_add3_u32 v51, v64, v51, s46
	s_waitcnt lgkmcnt(0)
	v_bfe_u32 v52, v66, 16, 1
	v_ashrrev_i32_e32 v69, 31, v68
	v_lshrrev_b32_e32 v51, 16, v51
	v_add3_u32 v52, v66, v52, s46
	v_lshlrev_b64 v[68:69], 11, v[68:69]
	v_and_or_b32 v51, v52, s47, v51
	v_lshl_add_u64 v[68:69], v[28:29], 0, v[68:69]
	global_store_dwordx4 v[68:69], v[48:51], off
	v_bfe_u32 v52, v67, 16, 1
	v_add3_u32 v52, v67, v52, s46
	v_bfe_u32 v48, v55, 16, 1
	v_add3_u32 v48, v55, v48, s46
	v_bfe_u32 v49, v53, 16, 1
	v_lshrrev_b32_e32 v48, 16, v48
	v_add3_u32 v49, v53, v49, s46
	v_and_or_b32 v48, v49, s47, v48
	v_bfe_u32 v49, v57, 16, 1
	v_add3_u32 v49, v57, v49, s46
	v_bfe_u32 v50, v59, 16, 1
	v_lshrrev_b32_e32 v49, 16, v49
	v_add3_u32 v50, v59, v50, s46
	v_and_or_b32 v49, v50, s47, v49
	v_bfe_u32 v50, v61, 16, 1
	v_add3_u32 v50, v61, v50, s46
	v_bfe_u32 v51, v63, 16, 1
	v_lshrrev_b32_e32 v50, 16, v50
	v_add3_u32 v51, v63, v51, s46
	v_and_or_b32 v50, v51, s47, v50
	v_bfe_u32 v51, v65, 16, 1
	v_add3_u32 v51, v65, v51, s46
	v_lshrrev_b32_e32 v51, 16, v51
	v_and_or_b32 v51, v52, s47, v51
	v_add_u32_e32 v52, s24, v39
	v_ashrrev_i32_e32 v53, 31, v52
	v_lshlrev_b64 v[52:53], 11, v[52:53]
	v_lshl_add_u64 v[28:29], v[28:29], 0, v[52:53]
	global_store_dwordx4 v[28:29], v[48:51], off
	s_waitcnt lgkmcnt(0)

; #define LDS_WAIT() asm volatile("s_waitcnt lgkmcnt(0)" ::: "memory")
; __device__ __forceinline__ void tr_item(const float* W, int ld, int K, int nblk, int item, bf16* WT, bool gu, LAS float* scr, int lane) {
;     const int kb = item / nblk, nb = item % nblk, k0 = 64 * kb, n0 = 32 * nb;
;     int drow0 = n0;
;     if (gu) { const int bj = n0 / FF, j = n0 - bj * FF; drow0 = 256 * (j / 128) + 128 * bj + (j % 128); }
;     { float t_[32];
; #pragma unroll
;       for (int i = 0; i < 32; ++i) t_[i] = W[(size_t)(k0 + 2 * i + (lane >> 5)) * ld + n0 + (lane & 31)];
; #pragma unroll
;       for (int i = 0; i < 32; ++i) scr[(2 * i + (lane >> 5)) * 33 + (lane & 31)] = t_[i]; }
;     LDS_WAIT(); asm volatile("" ::: "memory");
.LBB0_1154:
	s_andn2_b64 vcc, exec, s[24:25]
	s_cbranch_vccnz .LBB0_1131
	s_mul_hi_i32 s16, s37, 0x2aaaaaab
	s_lshr_b32 s24, s16, 31
	s_ashr_i32 s16, s16, 4
	s_add_i32 s16, s16, s24
	s_lshl_b32 s26, s16, 6
	s_mulk_i32 s16, 0xf400
	s_add_i32 s24, s40, s16
	v_add_u32_e32 v64, s26, v30
	s_ashr_i32 s25, s24, 31
	v_lshl_add_u64 v[28:29], s[24:25], 2, v[16:17]
	v_add_u32_e32 v50, 2, v64
	v_add_u32_e32 v52, 4, v64
	v_add_u32_e32 v54, 6, v64
	v_add_u32_e32 v56, 8, v64
	v_add_u32_e32 v58, 10, v64
	v_add_u32_e32 v60, 12, v64
	v_add_u32_e32 v62, 14, v64
	v_mad_i64_i32 v[48:49], s[50:51], v64, s49, v[28:29]
	v_mad_i64_i32 v[50:51], s[50:51], v50, s49, v[28:29]
	v_mad_i64_i32 v[52:53], s[50:51], v52, s49, v[28:29]
	v_mad_i64_i32 v[54:55], s[50:51], v54, s49, v[28:29]
	v_mad_i64_i32 v[56:57], s[50:51], v56, s49, v[28:29]
	v_mad_i64_i32 v[58:59], s[50:51], v58, s49, v[28:29]
	v_mad_i64_i32 v[60:61], s[50:51], v60, s49, v[28:29]
	v_mad_i64_i32 v[62:63], s[50:51], v62, s49, v[28:29]
	global_load_dword v65, v[48:49], off nt
	global_load_dword v66, v[50:51], off nt
	global_load_dword v67, v[52:53], off nt
	global_load_dword v68, v[54:55], off nt
	global_load_dword v69, v[56:57], off nt
	global_load_dword v70, v[58:59], off nt
	global_load_dword v71, v[60:61], off nt
	global_load_dword v72, v[62:63], off nt
	v_add_u32_e32 v48, 16, v64
	v_add_u32_e32 v50, 18, v64
	v_add_u32_e32 v52, 20, v64
	v_add_u32_e32 v54, 22, v64
	v_add_u32_e32 v56, 24, v64
	v_add_u32_e32 v58, 26, v64
	v_add_u32_e32 v60, 28, v64
	v_add_u32_e32 v62, 30, v64
	v_mad_i64_i32 v[48:49], s[50:51], v48, s49, v[28:29]
	v_mad_i64_i32 v[50:51], s[50:51], v50, s49, v[28:29]
	v_mad_i64_i32 v[52:53], s[50:51], v52, s49, v[28:29]
	v_mad_i64_i32 v[54:55], s[50:51], v54, s49, v[28:29]
	v_mad_i64_i32 v[56:57], s[50:51], v56, s49, v[28:29]
	v_mad_i64_i32 v[58:59], s[50:51], v58, s49, v[28:29]
	v_mad_i64_i32 v[60:61], s[50:51], v60, s49, v[28:29]
	v_mad_i64_i32 v[62:63], s[50:51], v62, s49, v[28:29]
	global_load_dword v73, v[48:49], off nt
	global_load_dword v74, v[50:51], off nt
	global_load_dword v75, v[52:53], off nt
	global_load_dword v76, v[54:55], off nt
	global_load_dword v77, v[56:57], off nt
	global_load_dword v78, v[58:59], off nt
	global_load_dword v79, v[60:61], off nt
	global_load_dword v80, v[62:63], off nt
	v_add_u32_e32 v48, 32, v64
	v_add_u32_e32 v50, 34, v64
	v_add_u32_e32 v52, 36, v64
	v_add_u32_e32 v54, 38, v64
	v_add_u32_e32 v56, 40, v64
	v_add_u32_e32 v58, 42, v64
	v_add_u32_e32 v60, 44, v64
	v_add_u32_e32 v62, 46, v64
	v_mad_i64_i32 v[48:49], s[50:51], v48, s49, v[28:29]
	v_mad_i64_i32 v[50:51], s[50:51], v50, s49, v[28:29]
	v_mad_i64_i32 v[52:53], s[50:51], v52, s49, v[28:29]
	v_mad_i64_i32 v[54:55], s[50:51], v54, s49, v[28:29]
	v_mad_i64_i32 v[56:57], s[50:51], v56, s49, v[28:29]
	v_mad_i64_i32 v[58:59], s[50:51], v58, s49, v[28:29]
	v_mad_i64_i32 v[60:61], s[50:51], v60, s49, v[28:29]
	v_mad_i64_i32 v[62:63], s[50:51], v62, s49, v[28:29]
	global_load_dword v81, v[48:49], off nt
	global_load_dword v82, v[50:51], off nt
	global_load_dword v83, v[52:53], off nt
	global_load_dword v84, v[54:55], off nt
	global_load_dword v85, v[56:57], off nt
	global_load_dword v86, v[58:59], off nt
	global_load_dword v87, v[60:61], off nt
	s_nop 0
	global_load_dword v62, v[62:63], off nt
	v_add_u32_e32 v48, 48, v64
	v_add_u32_e32 v50, 50, v64
	v_add_u32_e32 v52, 52, v64
	v_add_u32_e32 v54, 54, v64
	v_add_u32_e32 v56, 56, v64
	v_add_u32_e32 v58, 58, v64
	v_add_u32_e32 v60, 60, v64
	v_add_u32_e32 v63, 62, v64
	v_mad_i64_i32 v[48:49], s[50:51], v48, s49, v[28:29]
	v_mad_i64_i32 v[50:51], s[50:51], v50, s49, v[28:29]
	v_mad_i64_i32 v[52:53], s[50:51], v52, s49, v[28:29]
	v_mad_i64_i32 v[54:55], s[50:51], v54, s49, v[28:29]
	v_mad_i64_i32 v[56:57], s[50:51], v56, s49, v[28:29]
	v_mad_i64_i32 v[58:59], s[50:51], v58, s49, v[28:29]
	v_mad_i64_i32 v[60:61], s[50:51], v60, s49, v[28:29]
	v_mad_i64_i32 v[28:29], s[50:51], v63, s49, v[28:29]
	global_load_dword v48, v[48:49], off nt
	s_nop 0
	global_load_dword v49, v[50:51], off nt
	s_nop 0
	global_load_dword v50, v[52:53], off nt
	global_load_dword v51, v[54:55], off nt
	s_nop 0
	global_load_dword v52, v[56:57], off nt
	global_load_dword v53, v[58:59], off nt
	global_load_dword v54, v[60:61], off nt
	s_nop 0
	global_load_dword v28, v[28:29], off nt
	s_waitcnt vmcnt(0)
	ds_write2_b32 v31, v65, v66 offset1:66
	ds_write2_b32 v31, v67, v68 offset0:132 offset1:198
	ds_write2_b32 v40, v69, v70 offset0:8 offset1:74
	ds_write2_b32 v40, v71, v72 offset0:140 offset1:206
	ds_write2_b32 v41, v73, v74 offset0:16 offset1:82
	ds_write2_b32 v41, v75, v76 offset0:148 offset1:214
	ds_write2_b32 v42, v77, v78 offset0:24 offset1:90
	ds_write2_b32 v42, v79, v80 offset0:156 offset1:222
	ds_write2_b32 v43, v81, v82 offset0:32 offset1:98
	ds_write2_b32 v43, v83, v84 offset0:164 offset1:230
	ds_write2_b32 v44, v85, v86 offset0:40 offset1:106
	ds_write2_b32 v44, v87, v62 offset0:172 offset1:238
	ds_write2_b32 v45, v48, v49 offset0:48 offset1:114
	ds_write2_b32 v45, v50, v51 offset0:180 offset1:246
	ds_write2_b32 v46, v52, v53 offset0:56 offset1:122
	ds_write2_b32 v46, v54, v28 offset0:188 offset1:254
	s_waitcnt lgkmcnt(0)
; #define GAS __attribute__((address_space(1)))
; #define LAS __attribute__((address_space(3)))
; #define LDS_WAIT() asm volatile("s_waitcnt lgkmcnt(0)" ::: "memory")
; __device__ __forceinline__ unsigned pk2(float lo, float hi) { return f2bf(lo) | (f2bf(hi) << 16); }
; __device__ __forceinline__ void tr_item(const float* W, int ld, int K, int nblk, int item, bf16* WT, bool gu, LAS float* scr, int lane) {
;     ...
;     const int c = lane & 7;
; #pragma unroll
;     for (int j = 0; j < 4; ++j) { const int n = (lane >> 3) + 8 * j; const LAS float* s = scr + (8 * c) * 33 + n;
;         v4u o; o.x = pk2(s[0 * 33], s[1 * 33]); o.y = pk2(s[2 * 33], s[3 * 33]); o.z = pk2(s[4 * 33], s[5 * 33]); o.w = pk2(s[6 * 33], s[7 * 33]);
;         *(GAS v4u*)(WT + (size_t)(drow0 + n) * K + k0 + 8 * c) = o; }
;     LDS_WAIT(); asm volatile("" ::: "memory");
	ds_read2_b32 v[28:29], v36 offset1:8
	ds_read2_b32 v[54:55], v36 offset0:33 offset1:41
	ds_read2_b32 v[56:57], v36 offset0:66 offset1:74
	ds_read2_b32 v[58:59], v36 offset0:99 offset1:107
	ds_read2_b32 v[60:61], v36 offset0:132 offset1:140
	s_waitcnt lgkmcnt(4)
	v_bfe_u32 v48, v28, 16, 1
	v_add3_u32 v28, v28, v48, s46
	s_waitcnt lgkmcnt(3)
	v_bfe_u32 v48, v54, 16, 1
	v_lshrrev_b32_e32 v28, 16, v28
	v_add3_u32 v48, v54, v48, s46
	ds_read2_b32 v[62:63], v36 offset0:165 offset1:173
	v_and_or_b32 v48, v48, s47, v28
	s_waitcnt lgkmcnt(3)
	v_bfe_u32 v28, v56, 16, 1
	v_add3_u32 v28, v56, v28, s46
	s_waitcnt lgkmcnt(2)
	v_bfe_u32 v49, v58, 16, 1
	ds_read2_b32 v[64:65], v36 offset0:198 offset1:206
	v_lshrrev_b32_e32 v28, 16, v28
	v_add3_u32 v49, v58, v49, s46
	ds_read2_b32 v[66:67], v36 offset0:231 offset1:239
	v_and_or_b32 v49, v49, s47, v28
	s_waitcnt lgkmcnt(3)
	v_bfe_u32 v28, v60, 16, 1
	v_add3_u32 v28, v60, v28, s46
	s_waitcnt lgkmcnt(2)
	v_bfe_u32 v50, v62, 16, 1
	v_lshrrev_b32_e32 v28, 16, v28
	v_add3_u32 v50, v62, v50, s46
	v_and_or_b32 v50, v50, s47, v28
	s_waitcnt lgkmcnt(1)
	v_bfe_u32 v28, v64, 16, 1
	v_add3_u32 v28, v64, v28, s46
	s_waitcnt lgkmcnt(0)
	v_bfe_u32 v51, v66, 16, 1
	v_lshrrev_b32_e32 v28, 16, v28
	v_add3_u32 v51, v66, v51, s46
	v_add_u32_e32 v68, s24, v35
	s_ashr_i32 s27, s26, 31
	v_and_or_b32 v51, v51, s47, v28
	v_ashrrev_i32_e32 v69, 31, v68
	v_bfe_u32 v28, v29, 16, 1
	v_lshl_add_u64 v[52:53], s[26:27], 1, v[26:27]
	v_lshlrev_b64 v[70:71], 11, v[68:69]
	v_add3_u32 v28, v29, v28, s46
	v_bfe_u32 v29, v55, 16, 1
	v_lshl_add_u64 v[70:71], v[52:53], 0, v[70:71]
	v_lshrrev_b32_e32 v28, 16, v28
	v_add3_u32 v29, v55, v29, s46
	global_store_dwordx4 v[70:71], v[48:51], off
	ds_read2_b32 v[54:55], v36 offset0:16 offset1:24
	v_add_u32_e32 v70, 16, v68
	v_and_or_b32 v48, v29, s47, v28
	v_bfe_u32 v28, v57, 16, 1
	v_add3_u32 v28, v57, v28, s46
	v_bfe_u32 v29, v59, 16, 1
	v_lshrrev_b32_e32 v28, 16, v28
	v_add3_u32 v29, v59, v29, s46
	v_and_or_b32 v49, v29, s47, v28
	v_bfe_u32 v28, v61, 16, 1
	v_add3_u32 v28, v61, v28, s46
	v_bfe_u32 v29, v63, 16, 1
	v_lshrrev_b32_e32 v28, 16, v28
	v_add3_u32 v29, v63, v29, s46
	v_and_or_b32 v50, v29, s47, v28
	v_bfe_u32 v28, v65, 16, 1
	v_add3_u32 v28, v65, v28, s46
	v_bfe_u32 v29, v67, 16, 1
	v_lshrrev_b32_e32 v28, 16, v28
	v_add3_u32 v29, v67, v29, s46
	v_and_or_b32 v51, v29, s47, v28
	v_add_u32_e32 v28, 8, v68
	v_ashrrev_i32_e32 v29, 31, v28
	v_lshlrev_b64 v[28:29], 11, v[28:29]
	v_lshl_add_u64 v[28:29], v[52:53], 0, v[28:29]
	global_store_dwordx4 v[28:29], v[48:51], off
	ds_read2_b32 v[28:29], v36 offset0:49 offset1:57
	ds_read2_b32 v[56:57], v36 offset0:82 offset1:90
	ds_read2_b32 v[58:59], v36 offset0:115 offset1:123
	s_waitcnt lgkmcnt(3)
	v_bfe_u32 v48, v54, 16, 1
	v_add3_u32 v48, v54, v48, s46
	s_waitcnt lgkmcnt(2)
	v_bfe_u32 v49, v28, 16, 1
	ds_read2_b32 v[60:61], v36 offset0:148 offset1:156
	v_lshrrev_b32_e32 v48, 16, v48
	v_add3_u32 v28, v28, v49, s46
	ds_read2_b32 v[62:63], v36 offset0:181 offset1:189
	v_and_or_b32 v48, v28, s47, v48
	s_waitcnt lgkmcnt(3)
	v_bfe_u32 v28, v56, 16, 1
	v_add3_u32 v28, v56, v28, s46
	s_waitcnt lgkmcnt(2)
	v_bfe_u32 v49, v58, 16, 1
	ds_read2_b32 v[64:65], v36 offset0:214 offset1:222
	v_lshrrev_b32_e32 v28, 16, v28
	v_add3_u32 v49, v58, v49, s46
	ds_read2_b32 v[66:67], v36 offset0:247 offset1:255
	v_and_or_b32 v49, v49, s47, v28
	s_waitcnt lgkmcnt(3)
	v_bfe_u32 v28, v60, 16, 1
	v_add3_u32 v28, v60, v28, s46
	s_waitcnt lgkmcnt(2)
	v_bfe_u32 v50, v62, 16, 1
	v_lshrrev_b32_e32 v28, 16, v28
	v_add3_u32 v50, v62, v50, s46
	v_and_or_b32 v50, v50, s47, v28
	s_waitcnt lgkmcnt(1)
	v_bfe_u32 v28, v64, 16, 1
	v_add3_u32 v28, v64, v28, s46
	s_waitcnt lgkmcnt(0)
	v_bfe_u32 v51, v66, 16, 1
	v_ashrrev_i32_e32 v71, 31, v70
	v_lshrrev_b32_e32 v28, 16, v28
	v_add3_u32 v51, v66, v51, s46
	v_lshlrev_b64 v[70:71], 11, v[70:71]
	v_and_or_b32 v51, v51, s47, v28
	v_lshl_add_u64 v[70:71], v[52:53], 0, v[70:71]
	v_bfe_u32 v28, v55, 16, 1
	global_store_dwordx4 v[70:71], v[48:51], off
	v_add3_u32 v28, v55, v28, s46
	v_lshrrev_b32_e32 v28, 16, v28
	v_bfe_u32 v48, v29, 16, 1
	v_add3_u32 v29, v29, v48, s46
	v_and_or_b32 v48, v29, s47, v28
	v_bfe_u32 v28, v57, 16, 1
	v_add3_u32 v28, v57, v28, s46
	v_bfe_u32 v29, v59, 16, 1
	v_lshrrev_b32_e32 v28, 16, v28
	v_add3_u32 v29, v59, v29, s46
	v_and_or_b32 v49, v29, s47, v28
	v_bfe_u32 v28, v61, 16, 1
	v_add3_u32 v28, v61, v28, s46
	v_bfe_u32 v29, v63, 16, 1
	v_lshrrev_b32_e32 v28, 16, v28
	v_add3_u32 v29, v63, v29, s46
	v_and_or_b32 v50, v29, s47, v28
	v_bfe_u32 v28, v65, 16, 1
	v_add3_u32 v28, v65, v28, s46
	v_bfe_u32 v29, v67, 16, 1
	v_lshrrev_b32_e32 v28, 16, v28
	v_add3_u32 v29, v67, v29, s46
	v_and_or_b32 v51, v29, s47, v28
	v_add_u32_e32 v28, 24, v68
	v_ashrrev_i32_e32 v29, 31, v28
	v_lshlrev_b64 v[28:29], 11, v[28:29]
	v_lshl_add_u64 v[28:29], v[52:53], 0, v[28:29]
	global_store_dwordx4 v[28:29], v[48:51], off
	s_waitcnt lgkmcnt(0)
	s_branch .LBB0_1131

; __device__ __forceinline__ void tr_item8(const float* W, int ld, int K, int nblk, int item, unsigned char* WT, bool gu, float scale, LAS float* scr, int lane) {
;     const int kb = item / nblk, nb = item % nblk, k0 = 64 * kb, n0 = 32 * nb;
;     int drow0 = n0;
;     if (gu) { const int bj = n0 / FF, j = n0 - bj * FF; drow0 = 256 * (j / 128) + 128 * bj + (j % 128); }
;     { float t_[32];
; #pragma unroll
;       for (int i = 0; i < 32; ++i) t_[i] = W[(size_t)(k0 + 2 * i + (lane >> 5)) * ld + n0 + (lane & 31)];
; #pragma unroll
; __device__ __forceinline__ void convert_items(Frame& F, const Args& a, int lo, int hi, int w, int nw) {
;     ...
;         int r = it;
;         if (r < I_FI) { tr_item(a.in[7], 3 * D + 16, D, 96, r, (bf16*)(F.ws + WS_WFOXIN), false, scr, lane); continue; } r -= I_FI;
;         if (r < I_FO) { tr_item(a.in[9], D, D, 32, r, (bf16*)(F.ws + WS_WFOXOUT), false, scr, lane); continue; } r -= I_FO;
;         if (r < I_SI) { tr_item(a.in[10], D + 512, D, 48, r, (bf16*)(F.ws + WS_WSWAIN), false, scr, lane); continue; } r -= I_SI;
;         if (r < I_SO) { tr_item(a.in[12], D, D, 32, r, (bf16*)(F.ws + WS_WSWAOUT), false, scr, lane); continue; } r -= I_SO;
;         if (r < I_GU) { tr_item8(a.in[14], 2 * FF, D, 224, r, F.ws + WS_WGU, true, WSC_GU, scr, lane); continue; } r -= I_GU;
;         if (r < I_DN) { tr_item8(a.in[15], D, FF, 32, r, F.ws + WS_WDN, false, WSC_DN, scr, lane); continue; } r -= I_DN;
;         if (r < NE * I_GU) { const int e = r / I_GU, rr = r % I_GU; tr_item8(a.in[18] + (size_t)e * D * 2 * FF, 2 * FF, D, 224, rr, F.ws + WS_WMGU + (size_t)e * 2 * FF * D, true, WSC_GU, scr, lane); continue; } r -= NE * I_GU;
.LBB0_1161:
	s_cmpk_gt_i32 s16, 0x5ff
	s_mov_b64 s[6:7], -1
	s_cbranch_scc0 .LBB0_1183
	s_cmpk_gt_u32 s16, 0x7ff
	s_cbranch_scc0 .LBB0_1180
	s_cmpk_gt_u32 s16, 0xaff
	s_cbranch_scc0 .LBB0_1177
	s_cmpk_gt_u32 s16, 0xcff
	s_cbranch_scc0 .LBB0_1174
	s_cmpk_gt_u32 s16, 0x1aff
	s_cbranch_scc0 .LBB0_1171
	s_cmpk_gt_u32 s16, 0x21ff
	s_cbranch_scc0 .LBB0_1168
	s_add_i32 s4, s16, 0xde00
	s_bfe_u32 s6, s4, 0x70009
	s_mulk_i32 s6, 0x2493
	s_lshr_b32 s6, s6, 16
	s_mul_i32 s7, s6, 0xe00
	s_sub_i32 s4, s4, s7
	s_mul_i32 s7, s6, 0x1c00000
	s_add_u32 s8, s72, s7
	s_addc_u32 s9, s73, 0
	s_mul_i32 s6, s6, 0x700000
	s_add_u32 s6, s3, s6
	s_addc_u32 s7, s30, 0
	s_bfe_u32 s25, s4, 0xb0005
	s_mulk_i32 s25, 0x2493
	s_lshr_b32 s25, s25, 16
	s_mul_i32 s26, s25, 0xe0
	s_sub_i32 s26, s4, s26
	s_lshl_b32 s4, s26, 5
	s_and_b32 s27, s26, 0xffff
	s_cmpk_gt_u32 s27, 0x6f
	s_cselect_b32 s27, 0xfffff200, 0
	s_cselect_b32 s31, 0x80, 0
	s_add_i32 s4, s27, s4
	s_sext_i32_i16 s27, s4
	s_bfe_u32 s27, s27, 0x70018
	s_add_i32 s27, s4, s27
	s_sext_i32_i16 s36, s27
	s_and_b32 s27, s27, 0xff80
	s_sub_i32 s4, s4, s27
	s_lshl_b32 s36, s36, 1
	s_sext_i32_i16 s4, s4
	s_and_b32 s36, s36, 0xffffff00
	s_add_i32 s4, s31, s4
	s_lshl_b32 s26, s26, 7
	s_add_i32 s4, s4, s36
	s_lshl_b32 s25, s25, 6
	s_and_b32 s26, s26, 0x3ff80
	s_add_u32 s8, s8, s26
	s_addc_u32 s9, s9, 0
	v_add_u32_e32 v64, s25, v28
	v_lshl_add_u64 v[46:47], s[8:9], 0, v[0:1]
	v_mad_i64_i32 v[48:49], s[8:9], v64, s13, v[46:47]
	v_add_u32_e32 v50, 2, v64
	v_add_u32_e32 v52, 4, v64
	v_add_u32_e32 v54, 6, v64
	v_add_u32_e32 v56, 8, v64
	v_add_u32_e32 v58, 10, v64
	v_add_u32_e32 v60, 12, v64
	v_add_u32_e32 v62, 14, v64
	v_mad_i64_i32 v[50:51], s[8:9], v50, s13, v[46:47]
	v_mad_i64_i32 v[52:53], s[8:9], v52, s13, v[46:47]
	v_mad_i64_i32 v[54:55], s[8:9], v54, s13, v[46:47]
	v_mad_i64_i32 v[56:57], s[8:9], v56, s13, v[46:47]
	v_mad_i64_i32 v[58:59], s[8:9], v58, s13, v[46:47]
	v_mad_i64_i32 v[60:61], s[8:9], v60, s13, v[46:47]
	v_mad_i64_i32 v[62:63], s[8:9], v62, s13, v[46:47]
	global_load_dword v65, v[48:49], off nt
	global_load_dword v66, v[50:51], off nt
	global_load_dword v67, v[52:53], off nt
	global_load_dword v68, v[54:55], off nt
	global_load_dword v69, v[56:57], off nt
	global_load_dword v70, v[58:59], off nt
	global_load_dword v71, v[60:61], off nt
	global_load_dword v72, v[62:63], off nt
	v_add_u32_e32 v48, 16, v64
	v_mad_i64_i32 v[48:49], s[8:9], v48, s13, v[46:47]
	v_add_u32_e32 v50, 18, v64
	v_add_u32_e32 v52, 20, v64
	v_add_u32_e32 v54, 22, v64
	v_add_u32_e32 v56, 24, v64
	v_add_u32_e32 v58, 26, v64
	v_add_u32_e32 v60, 28, v64
	v_add_u32_e32 v62, 30, v64
	v_mad_i64_i32 v[50:51], s[8:9], v50, s13, v[46:47]
	v_mad_i64_i32 v[52:53], s[8:9], v52, s13, v[46:47]
	v_mad_i64_i32 v[54:55], s[8:9], v54, s13, v[46:47]
	v_mad_i64_i32 v[56:57], s[8:9], v56, s13, v[46:47]
	v_mad_i64_i32 v[58:59], s[8:9], v58, s13, v[46:47]
	v_mad_i64_i32 v[60:61], s[8:9], v60, s13, v[46:47]
	v_mad_i64_i32 v[62:63], s[8:9], v62, s13, v[46:47]
	global_load_dword v73, v[48:49], off nt
	global_load_dword v74, v[50:51], off nt
	global_load_dword v75, v[52:53], off nt
	global_load_dword v76, v[54:55], off nt
	global_load_dword v77, v[56:57], off nt
	global_load_dword v78, v[58:59], off nt
	global_load_dword v79, v[60:61], off nt
	global_load_dword v80, v[62:63], off nt
	v_add_u32_e32 v48, 32, v64
	v_add_u32_e32 v50, 34, v64
	v_add_u32_e32 v52, 36, v64
	v_add_u32_e32 v54, 38, v64
	v_add_u32_e32 v60, 44, v64
	v_mad_i64_i32 v[48:49], s[8:9], v48, s13, v[46:47]
	v_mad_i64_i32 v[50:51], s[8:9], v50, s13, v[46:47]
	v_mad_i64_i32 v[52:53], s[8:9], v52, s13, v[46:47]
	v_mad_i64_i32 v[54:55], s[8:9], v54, s13, v[46:47]
	v_add_u32_e32 v56, 40, v64
	v_add_u32_e32 v58, 42, v64
	v_mad_i64_i32 v[60:61], s[8:9], v60, s13, v[46:47]
	v_add_u32_e32 v62, 46, v64
	v_mad_i64_i32 v[56:57], s[8:9], v56, s13, v[46:47]
	v_mad_i64_i32 v[58:59], s[8:9], v58, s13, v[46:47]
	v_mad_i64_i32 v[62:63], s[8:9], v62, s13, v[46:47]
	global_load_dword v81, v[48:49], off nt
	global_load_dword v82, v[50:51], off nt
	global_load_dword v83, v[52:53], off nt
	global_load_dword v84, v[54:55], off nt
	global_load_dword v85, v[56:57], off nt
	global_load_dword v86, v[58:59], off nt
	s_nop 0
	global_load_dword v60, v[60:61], off nt
	s_nop 0
	global_load_dword v61, v[62:63], off nt
	v_add_u32_e32 v48, 48, v64
	v_add_u32_e32 v50, 50, v64
	v_add_u32_e32 v52, 52, v64
	v_add_u32_e32 v54, 54, v64
	v_mad_i64_i32 v[48:49], s[8:9], v48, s13, v[46:47]
	v_mad_i64_i32 v[50:51], s[8:9], v50, s13, v[46:47]
	v_mad_i64_i32 v[52:53], s[8:9], v52, s13, v[46:47]
	v_mad_i64_i32 v[54:55], s[8:9], v54, s13, v[46:47]
	v_add_u32_e32 v56, 56, v64
	v_add_u32_e32 v58, 58, v64
	v_mad_i64_i32 v[56:57], s[8:9], v56, s13, v[46:47]
	v_mad_i64_i32 v[58:59], s[8:9], v58, s13, v[46:47]
	global_load_dword v62, v[48:49], off nt
	s_nop 0
	global_load_dword v50, v[50:51], off nt
	s_nop 0
	global_load_dword v51, v[52:53], off nt
	s_nop 0
	global_load_dword v52, v[54:55], off nt
	global_load_dword v53, v[56:57], off nt
	s_nop 0
	global_load_dword v54, v[58:59], off nt
	v_add_u32_e32 v48, 60, v64
	v_add_u32_e32 v55, 62, v64
	v_mad_i64_i32 v[48:49], s[8:9], v48, s13, v[46:47]
	v_mad_i64_i32 v[46:47], s[8:9], v55, s13, v[46:47]
	global_load_dword v48, v[48:49], off nt
	s_nop 0
	global_load_dword v46, v[46:47], off nt
	s_waitcnt vmcnt(0)
; __device__ __forceinline__ unsigned cvt_pk4_fp8(float a, float b, float c, float d) { int w = 0; w = __builtin_amdgcn_cvt_pk_fp8_f32(a, b, w, false); w = __builtin_amdgcn_cvt_pk_fp8_f32(c, d, w, true); return (unsigned)w; }
; #define GAS __attribute__((address_space(1)))
; #define LAS __attribute__((address_space(3)))
; #define LDS_WAIT() asm volatile("s_waitcnt lgkmcnt(0)" ::: "memory")
; __device__ __forceinline__ void tr_item8(const float* W, int ld, int K, int nblk, int item, unsigned char* WT, bool gu, float scale, LAS float* scr, int lane) {
;     ...
;       for (int i = 0; i < 32; ++i) scr[(2 * i + (lane >> 5)) * 33 + (lane & 31)] = t_[i] * scale; }
;     LDS_WAIT(); asm volatile("" ::: "memory");
;     const int c = lane & 3;
; #pragma unroll
;     for (int j = 0; j < 2; ++j) { const int n = (lane >> 2) + 16 * j; const LAS float* sp = scr + (16 * c) * 33 + n;
;         v4u o; o.x = pg8::cvt_pk4_fp8(sp[0 * 33], sp[1 * 33], sp[2 * 33], sp[3 * 33]); o.y = pg8::cvt_pk4_fp8(sp[4 * 33], sp[5 * 33], sp[6 * 33], sp[7 * 33]);
;         o.z = pg8::cvt_pk4_fp8(sp[8 * 33], sp[9 * 33], sp[10 * 33], sp[11 * 33]); o.w = pg8::cvt_pk4_fp8(sp[12 * 33], sp[13 * 33], sp[14 * 33], sp[15 * 33]);
;         *(GAS v4u*)(WT + (size_t)(drow0 + n) * K + k0 + 16 * c) = o; }
;     LDS_WAIT(); asm volatile("" ::: "memory");
	v_mul_f32_e32 v47, 0x42800000, v65
	v_mul_f32_e32 v49, 0x42800000, v66
	ds_write2_b32 v29, v47, v49 offset1:66
	v_mul_f32_e32 v47, 0x42800000, v67
	v_mul_f32_e32 v49, 0x42800000, v68
	ds_write2_b32 v29, v47, v49 offset0:132 offset1:198
	v_mul_f32_e32 v47, 0x42800000, v69
	v_mul_f32_e32 v49, 0x42800000, v70
	ds_write2_b32 v38, v47, v49 offset0:8 offset1:74
	v_mul_f32_e32 v47, 0x42800000, v71
	v_mul_f32_e32 v49, 0x42800000, v72
	ds_write2_b32 v38, v47, v49 offset0:140 offset1:206
	s_add_u32 s6, s6, s25
	s_addc_u32 s7, s7, 0
	v_mul_f32_e32 v47, 0x42800000, v73
	v_mul_f32_e32 v49, 0x42800000, v74
	ds_write2_b32 v39, v47, v49 offset0:16 offset1:82
	v_mul_f32_e32 v47, 0x42800000, v75
	v_mul_f32_e32 v49, 0x42800000, v76
	ds_write2_b32 v39, v47, v49 offset0:148 offset1:214
	v_mul_f32_e32 v47, 0x42800000, v77
	v_mul_f32_e32 v49, 0x42800000, v78
	ds_write2_b32 v40, v47, v49 offset0:24 offset1:90
	v_mul_f32_e32 v47, 0x42800000, v79
	v_mul_f32_e32 v49, 0x42800000, v80
	ds_write2_b32 v40, v47, v49 offset0:156 offset1:222
	v_mul_f32_e32 v47, 0x42800000, v81
	v_mul_f32_e32 v49, 0x42800000, v82
	ds_write2_b32 v41, v47, v49 offset0:32 offset1:98
	v_mul_f32_e32 v47, 0x42800000, v83
	v_mul_f32_e32 v49, 0x42800000, v84
	ds_write2_b32 v41, v47, v49 offset0:164 offset1:230
	v_mul_f32_e32 v47, 0x42800000, v85
	v_mul_f32_e32 v49, 0x42800000, v86
	ds_write2_b32 v42, v47, v49 offset0:40 offset1:106
	v_mul_f32_e32 v47, 0x42800000, v60
	v_mul_f32_e32 v49, 0x42800000, v61
	ds_write2_b32 v42, v47, v49 offset0:172 offset1:238
	v_add_u32_e32 v84, s4, v30
	v_ashrrev_i32_e32 v85, 31, v84
	v_lshlrev_b64 v[84:85], 10, v[84:85]
	v_mul_f32_e32 v47, 0x42800000, v62
	v_mul_f32_e32 v49, 0x42800000, v50
	ds_write2_b32 v43, v47, v49 offset0:48 offset1:114
	v_mul_f32_e32 v47, 0x42800000, v51
	v_mul_f32_e32 v49, 0x42800000, v52
	ds_write2_b32 v43, v47, v49 offset0:180 offset1:246
	v_mul_f32_e32 v47, 0x42800000, v53
	v_mul_f32_e32 v49, 0x42800000, v54
	ds_write2_b32 v44, v47, v49 offset0:56 offset1:122
	v_mov_b32_e32 v49, v1
	v_lshl_add_u64 v[50:51], s[6:7], 0, v[2:3]
	v_mul_f32_e32 v47, 0x42800000, v48
	v_mul_f32_e32 v46, 0x42800000, v46
	ds_write2_b32 v44, v47, v46 offset0:188 offset1:254
	s_waitcnt lgkmcnt(0)
	ds_read2_b32 v[52:53], v31 offset1:16
	ds_read2_b32 v[54:55], v31 offset0:33 offset1:49
	ds_read2_b32 v[56:57], v31 offset0:66 offset1:82
	ds_read2_b32 v[58:59], v31 offset0:99 offset1:115
	ds_read2_b32 v[60:61], v31 offset0:132 offset1:148
	ds_read2_b32 v[62:63], v31 offset0:165 offset1:181
	ds_read2_b32 v[64:65], v31 offset0:198 offset1:214
	ds_read2_b32 v[66:67], v31 offset0:231 offset1:247
	ds_read2_b32 v[68:69], v45 offset0:8 offset1:24
	ds_read2_b32 v[70:71], v45 offset0:41 offset1:57
	ds_read2_b32 v[72:73], v45 offset0:74 offset1:90
	ds_read2_b32 v[74:75], v45 offset0:107 offset1:123
	ds_read2_b32 v[76:77], v45 offset0:140 offset1:156
	ds_read2_b32 v[78:79], v45 offset0:173 offset1:189
	v_mov_b32_e32 v46, v1
	v_mov_b32_e32 v47, v1
	v_mov_b32_e32 v48, v1
	ds_read2_b32 v[80:81], v45 offset0:206 offset1:222
	ds_read2_b32 v[82:83], v45 offset0:239 offset1:255
	s_waitcnt lgkmcnt(14)
	v_cvt_pk_fp8_f32 v46, v52, v54
	s_waitcnt lgkmcnt(10)
	v_cvt_pk_fp8_f32 v47, v60, v62
	s_waitcnt lgkmcnt(6)
	v_cvt_pk_fp8_f32 v48, v68, v70
	s_waitcnt lgkmcnt(2)
	v_cvt_pk_fp8_f32 v49, v76, v78
	v_cvt_pk_fp8_f32 v46, v56, v58 op_sel:[0,0,1]
	v_cvt_pk_fp8_f32 v47, v64, v66 op_sel:[0,0,1]
	v_cvt_pk_fp8_f32 v48, v72, v74 op_sel:[0,0,1]
	s_waitcnt lgkmcnt(0)
	v_cvt_pk_fp8_f32 v49, v80, v82 op_sel:[0,0,1]
	v_lshl_add_u64 v[84:85], v[50:51], 0, v[84:85]
	v_add_u32_e32 v52, s4, v32
	s_mov_b64 s[6:7], 0
	global_store_dwordx4 v[84:85], v[46:49], off
	s_nop 1
	v_mov_b32_e32 v46, v1
	v_mov_b32_e32 v47, v1
	v_mov_b32_e32 v48, v1
	v_mov_b32_e32 v49, v1
	v_cvt_pk_fp8_f32 v46, v53, v55
	v_cvt_pk_fp8_f32 v47, v61, v63
	v_cvt_pk_fp8_f32 v48, v69, v71
	v_cvt_pk_fp8_f32 v49, v77, v79
	v_cvt_pk_fp8_f32 v46, v57, v59 op_sel:[0,0,1]
	v_cvt_pk_fp8_f32 v47, v65, v67 op_sel:[0,0,1]
	v_cvt_pk_fp8_f32 v48, v73, v75 op_sel:[0,0,1]
	v_cvt_pk_fp8_f32 v49, v81, v83 op_sel:[0,0,1]
	v_ashrrev_i32_e32 v53, 31, v52
	v_lshlrev_b64 v[52:53], 10, v[52:53]
	v_lshl_add_u64 v[50:51], v[50:51], 0, v[52:53]
	global_store_dwordx4 v[50:51], v[46:49], off
	s_waitcnt lgkmcnt(0)
; __device__ __forceinline__ void tr_item8(const float* W, int ld, int K, int nblk, int item, unsigned char* WT, bool gu, float scale, LAS float* scr, int lane) {
;     const int kb = item / nblk, nb = item % nblk, k0 = 64 * kb, n0 = 32 * nb;
;     int drow0 = n0;
;     if (gu) { const int bj = n0 / FF, j = n0 - bj * FF; drow0 = 256 * (j / 128) + 128 * bj + (j % 128); }
;     { float t_[32];
; #pragma unroll
;       for (int i = 0; i < 32; ++i) t_[i] = W[(size_t)(k0 + 2 * i + (lane >> 5)) * ld + n0 + (lane & 31)];
; #pragma unroll
.LBB0_1168:
	s_andn2_b64 vcc, exec, s[6:7]
	s_cbranch_vccnz .LBB0_1170
	s_lshl_b32 s4, s16, 5
	s_and_b32 s6, s11, 0x1ffc0
	s_and_b32 s8, s4, 0x3e0
	v_add_u32_e32 v46, s6, v28
	s_lshl_b32 s4, s8, 2
	v_ashrrev_i32_e32 v47, 31, v46
	v_lshl_add_u64 v[48:49], v[4:5], 0, s[4:5]
	v_lshlrev_b64 v[46:47], 12, v[46:47]
	v_lshl_add_u64 v[46:47], v[48:49], 0, v[46:47]
	v_add_co_u32_e32 v48, vcc, 0x2000, v46
	s_mov_b32 s7, s5
	s_nop 0
	v_addc_co_u32_e32 v49, vcc, 0, v47, vcc
	v_add_co_u32_e32 v50, vcc, 0x4000, v46
	s_nop 1
	v_addc_co_u32_e32 v51, vcc, 0, v47, vcc
	v_add_co_u32_e32 v52, vcc, 0x6000, v46
	s_nop 1
	v_addc_co_u32_e32 v53, vcc, 0, v47, vcc
	v_add_co_u32_e32 v54, vcc, 0x8000, v46
	s_nop 1
	v_addc_co_u32_e32 v55, vcc, 0, v47, vcc
	v_add_co_u32_e32 v56, vcc, 0xa000, v46
	s_nop 1
	v_addc_co_u32_e32 v57, vcc, 0, v47, vcc
	v_add_co_u32_e32 v58, vcc, 0xc000, v46
	s_nop 1
	v_addc_co_u32_e32 v59, vcc, 0, v47, vcc
	v_add_co_u32_e32 v60, vcc, 0xe000, v46
	s_nop 1
	v_addc_co_u32_e32 v61, vcc, 0, v47, vcc
	global_load_dword v64, v[46:47], off nt
	global_load_dword v65, v[48:49], off nt
	global_load_dword v66, v[50:51], off nt
	global_load_dword v67, v[52:53], off nt
	global_load_dword v68, v[54:55], off nt
	global_load_dword v69, v[56:57], off nt
	global_load_dword v70, v[58:59], off nt
	global_load_dword v71, v[60:61], off nt
	v_add_co_u32_e32 v48, vcc, 0x10000, v46
	s_nop 1
	v_addc_co_u32_e32 v49, vcc, 0, v47, vcc
	v_add_co_u32_e32 v50, vcc, 0x12000, v46
	s_nop 1
	v_addc_co_u32_e32 v51, vcc, 0, v47, vcc
	v_add_co_u32_e32 v52, vcc, 0x14000, v46
	s_nop 1
	v_addc_co_u32_e32 v53, vcc, 0, v47, vcc
	v_add_co_u32_e32 v54, vcc, 0x16000, v46
	s_nop 1
	v_addc_co_u32_e32 v55, vcc, 0, v47, vcc
	v_add_co_u32_e32 v56, vcc, 0x18000, v46
	s_nop 1
	v_addc_co_u32_e32 v57, vcc, 0, v47, vcc
	v_add_co_u32_e32 v58, vcc, 0x1a000, v46
	s_nop 1
	v_addc_co_u32_e32 v59, vcc, 0, v47, vcc
	v_add_co_u32_e32 v60, vcc, 0x1c000, v46
	s_nop 1
	v_addc_co_u32_e32 v61, vcc, 0, v47, vcc
	v_add_co_u32_e32 v62, vcc, 0x1e000, v46
	s_nop 1
	v_addc_co_u32_e32 v63, vcc, 0, v47, vcc
	global_load_dword v72, v[48:49], off nt
	global_load_dword v73, v[50:51], off nt
	global_load_dword v74, v[52:53], off nt
	global_load_dword v75, v[54:55], off nt
	global_load_dword v76, v[56:57], off nt
	global_load_dword v77, v[58:59], off nt
	global_load_dword v78, v[60:61], off nt
	global_load_dword v79, v[62:63], off nt
	v_add_co_u32_e32 v48, vcc, 0x20000, v46
	s_nop 1
	v_addc_co_u32_e32 v49, vcc, 0, v47, vcc
	v_add_co_u32_e32 v50, vcc, 0x22000, v46
	s_nop 1
	v_addc_co_u32_e32 v51, vcc, 0, v47, vcc
	v_add_co_u32_e32 v52, vcc, 0x24000, v46
	s_nop 1
	v_addc_co_u32_e32 v53, vcc, 0, v47, vcc
	v_add_co_u32_e32 v54, vcc, 0x26000, v46
	s_nop 1
	v_addc_co_u32_e32 v55, vcc, 0, v47, vcc
	v_add_co_u32_e32 v56, vcc, 0x28000, v46
	s_nop 1
	v_addc_co_u32_e32 v57, vcc, 0, v47, vcc
	v_add_co_u32_e32 v58, vcc, 0x2a000, v46
	s_nop 1
	v_addc_co_u32_e32 v59, vcc, 0, v47, vcc
	v_add_co_u32_e32 v60, vcc, 0x2c000, v46
	s_nop 1
	v_addc_co_u32_e32 v61, vcc, 0, v47, vcc
	v_add_co_u32_e32 v62, vcc, 0x2e000, v46
	s_nop 1
	v_addc_co_u32_e32 v63, vcc, 0, v47, vcc
	global_load_dword v80, v[48:49], off nt
	global_load_dword v81, v[50:51], off nt
	global_load_dword v82, v[52:53], off nt
	global_load_dword v83, v[54:55], off nt
	global_load_dword v84, v[56:57], off nt
	global_load_dword v85, v[58:59], off nt
	s_nop 0
	global_load_dword v60, v[60:61], off nt
	s_nop 0
	global_load_dword v61, v[62:63], off nt
	v_add_co_u32_e32 v48, vcc, 0x30000, v46
	s_nop 1
	v_addc_co_u32_e32 v49, vcc, 0, v47, vcc
	v_add_co_u32_e32 v50, vcc, 0x32000, v46
	s_nop 1
	v_addc_co_u32_e32 v51, vcc, 0, v47, vcc
	v_add_co_u32_e32 v52, vcc, 0x34000, v46
	s_nop 1
	v_addc_co_u32_e32 v53, vcc, 0, v47, vcc
	v_add_co_u32_e32 v54, vcc, 0x36000, v46
	s_nop 1
	v_addc_co_u32_e32 v55, vcc, 0, v47, vcc
	v_add_co_u32_e32 v56, vcc, 0x38000, v46
	s_nop 1
	v_addc_co_u32_e32 v57, vcc, 0, v47, vcc
	v_add_co_u32_e32 v58, vcc, 0x3a000, v46
	s_nop 1
	v_addc_co_u32_e32 v59, vcc, 0, v47, vcc
	global_load_dword v62, v[48:49], off nt
	s_nop 0
	global_load_dword v50, v[50:51], off nt
	s_nop 0
	global_load_dword v51, v[52:53], off nt
	s_nop 0
	global_load_dword v52, v[54:55], off nt
	global_load_dword v53, v[56:57], off nt
	s_nop 0
	global_load_dword v54, v[58:59], off nt
	v_add_co_u32_e32 v48, vcc, 0x3c000, v46
	s_nop 1
	v_addc_co_u32_e32 v49, vcc, 0, v47, vcc
	v_add_co_u32_e32 v46, vcc, 0x3e000, v46
	s_nop 1
	v_addc_co_u32_e32 v47, vcc, 0, v47, vcc
	global_load_dword v48, v[48:49], off nt
	s_nop 0
	global_load_dword v46, v[46:47], off nt
	s_waitcnt vmcnt(0)
; __device__ __forceinline__ unsigned cvt_pk4_fp8(float a, float b, float c, float d) { int w = 0; w = __builtin_amdgcn_cvt_pk_fp8_f32(a, b, w, false); w = __builtin_amdgcn_cvt_pk_fp8_f32(c, d, w, true); return (unsigned)w; }
; #define GAS __attribute__((address_space(1)))
; #define LAS __attribute__((address_space(3)))
; #define LDS_WAIT() asm volatile("s_waitcnt lgkmcnt(0)" ::: "memory")
; __device__ __forceinline__ void tr_item8(const float* W, int ld, int K, int nblk, int item, unsigned char* WT, bool gu, float scale, LAS float* scr, int lane) {
;     ...
;       for (int i = 0; i < 32; ++i) scr[(2 * i + (lane >> 5)) * 33 + (lane & 31)] = t_[i] * scale; }
;     LDS_WAIT(); asm volatile("" ::: "memory");
;     const int c = lane & 3;
; #pragma unroll
;     for (int j = 0; j < 2; ++j) { const int n = (lane >> 2) + 16 * j; const LAS float* sp = scr + (16 * c) * 33 + n;
;         v4u o; o.x = pg8::cvt_pk4_fp8(sp[0 * 33], sp[1 * 33], sp[2 * 33], sp[3 * 33]); o.y = pg8::cvt_pk4_fp8(sp[4 * 33], sp[5 * 33], sp[6 * 33], sp[7 * 33]);
;         o.z = pg8::cvt_pk4_fp8(sp[8 * 33], sp[9 * 33], sp[10 * 33], sp[11 * 33]); o.w = pg8::cvt_pk4_fp8(sp[12 * 33], sp[13 * 33], sp[14 * 33], sp[15 * 33]);
;         *(GAS v4u*)(WT + (size_t)(drow0 + n) * K + k0 + 16 * c) = o; }
;     LDS_WAIT(); asm volatile("" ::: "memory");
	v_mul_f32_e32 v47, 0x43000000, v64
	v_mul_f32_e32 v49, 0x43000000, v65
	ds_write2_b32 v29, v47, v49 offset1:66
	v_mul_f32_e32 v47, 0x43000000, v66
	v_mul_f32_e32 v49, 0x43000000, v67
	ds_write2_b32 v29, v47, v49 offset0:132 offset1:198
	v_mul_f32_e32 v47, 0x43000000, v68
	v_mul_f32_e32 v49, 0x43000000, v69
	ds_write2_b32 v38, v47, v49 offset0:8 offset1:74
	v_mul_f32_e32 v47, 0x43000000, v70
	v_mul_f32_e32 v49, 0x43000000, v71
	ds_write2_b32 v38, v47, v49 offset0:140 offset1:206
	v_mul_f32_e32 v47, 0x43000000, v72
	v_mul_f32_e32 v49, 0x43000000, v73
	ds_write2_b32 v39, v47, v49 offset0:16 offset1:82
	v_mul_f32_e32 v47, 0x43000000, v74
	v_mul_f32_e32 v49, 0x43000000, v75
	ds_write2_b32 v39, v47, v49 offset0:148 offset1:214
	v_mul_f32_e32 v47, 0x43000000, v76
	v_mul_f32_e32 v49, 0x43000000, v77
	ds_write2_b32 v40, v47, v49 offset0:24 offset1:90
	v_mul_f32_e32 v47, 0x43000000, v78
	v_mul_f32_e32 v49, 0x43000000, v79
	ds_write2_b32 v40, v47, v49 offset0:156 offset1:222
	v_mul_f32_e32 v47, 0x43000000, v80
	v_mul_f32_e32 v49, 0x43000000, v81
	ds_write2_b32 v41, v47, v49 offset0:32 offset1:98
	v_mul_f32_e32 v47, 0x43000000, v82
	v_mul_f32_e32 v49, 0x43000000, v83
	ds_write2_b32 v41, v47, v49 offset0:164 offset1:230
	v_mul_f32_e32 v47, 0x43000000, v84
	v_mul_f32_e32 v49, 0x43000000, v85
	ds_write2_b32 v42, v47, v49 offset0:40 offset1:106
	v_mul_f32_e32 v47, 0x43000000, v60
	v_mul_f32_e32 v49, 0x43000000, v61
	ds_write2_b32 v42, v47, v49 offset0:172 offset1:238
	v_mul_f32_e32 v47, 0x43000000, v62
	v_mul_f32_e32 v49, 0x43000000, v50
	ds_write2_b32 v43, v47, v49 offset0:48 offset1:114
	v_mul_f32_e32 v47, 0x43000000, v51
	v_mul_f32_e32 v49, 0x43000000, v52
	ds_write2_b32 v43, v47, v49 offset0:180 offset1:246
	v_mul_f32_e32 v47, 0x43000000, v53
	v_mul_f32_e32 v49, 0x43000000, v54
	ds_write2_b32 v44, v47, v49 offset0:56 offset1:122
	v_mov_b32_e32 v49, 0
	v_lshl_add_u64 v[50:51], v[18:19], 0, s[6:7]
	v_mul_f32_e32 v47, 0x43000000, v48
	v_mul_f32_e32 v46, 0x43000000, v46
	ds_write2_b32 v44, v47, v46 offset0:188 offset1:254
	s_waitcnt lgkmcnt(0)
	ds_read2_b32 v[52:53], v31 offset1:16
	ds_read2_b32 v[54:55], v31 offset0:33 offset1:49
	ds_read2_b32 v[56:57], v31 offset0:66 offset1:82
	ds_read2_b32 v[58:59], v31 offset0:99 offset1:115
	ds_read2_b32 v[60:61], v31 offset0:132 offset1:148
	ds_read2_b32 v[62:63], v31 offset0:165 offset1:181
	ds_read2_b32 v[64:65], v31 offset0:198 offset1:214
	ds_read2_b32 v[66:67], v31 offset0:231 offset1:247
	ds_read2_b32 v[68:69], v45 offset0:8 offset1:24
	ds_read2_b32 v[70:71], v45 offset0:41 offset1:57
	ds_read2_b32 v[72:73], v45 offset0:74 offset1:90
	ds_read2_b32 v[74:75], v45 offset0:107 offset1:123
	ds_read2_b32 v[76:77], v45 offset0:140 offset1:156
	ds_read2_b32 v[78:79], v45 offset0:173 offset1:189
	v_mov_b32_e32 v46, 0
	v_mov_b32_e32 v47, 0
	v_mov_b32_e32 v48, 0
	ds_read2_b32 v[80:81], v45 offset0:206 offset1:222
	ds_read2_b32 v[82:83], v45 offset0:239 offset1:255
	s_waitcnt lgkmcnt(14)
	v_cvt_pk_fp8_f32 v46, v52, v54
	s_waitcnt lgkmcnt(10)
	v_cvt_pk_fp8_f32 v47, v60, v62
	s_waitcnt lgkmcnt(6)
	v_cvt_pk_fp8_f32 v48, v68, v70
	s_waitcnt lgkmcnt(2)
	v_cvt_pk_fp8_f32 v49, v76, v78
	v_cvt_pk_fp8_f32 v46, v56, v58 op_sel:[0,0,1]
	v_cvt_pk_fp8_f32 v47, v64, v66 op_sel:[0,0,1]
	v_cvt_pk_fp8_f32 v48, v72, v74 op_sel:[0,0,1]
	s_waitcnt lgkmcnt(0)
	v_cvt_pk_fp8_f32 v49, v80, v82 op_sel:[0,0,1]
	v_add_u32_e32 v52, s8, v30
	v_mad_i64_i32 v[84:85], s[6:7], v52, s12, v[50:51]
	global_store_dwordx4 v[84:85], v[46:49], off
	v_add_u32_e32 v52, s8, v32
	v_mad_i64_i32 v[50:51], s[6:7], v52, s12, v[50:51]
	v_mov_b32_e32 v46, 0
	v_mov_b32_e32 v47, 0
	v_mov_b32_e32 v48, 0
	v_mov_b32_e32 v49, 0
	v_cvt_pk_fp8_f32 v46, v53, v55
	v_cvt_pk_fp8_f32 v47, v61, v63
	v_cvt_pk_fp8_f32 v48, v69, v71
	v_cvt_pk_fp8_f32 v49, v77, v79
	v_cvt_pk_fp8_f32 v46, v57, v59 op_sel:[0,0,1]
	v_cvt_pk_fp8_f32 v47, v65, v67 op_sel:[0,0,1]
	v_cvt_pk_fp8_f32 v48, v73, v75 op_sel:[0,0,1]
	v_cvt_pk_fp8_f32 v49, v81, v83 op_sel:[0,0,1]
	global_store_dwordx4 v[50:51], v[46:49], off
	s_waitcnt lgkmcnt(0)

; __device__ __forceinline__ void tr_item8(const float* W, int ld, int K, int nblk, int item, unsigned char* WT, bool gu, float scale, LAS float* scr, int lane) {
;     const int kb = item / nblk, nb = item % nblk, k0 = 64 * kb, n0 = 32 * nb;
;     int drow0 = n0;
;     if (gu) { const int bj = n0 / FF, j = n0 - bj * FF; drow0 = 256 * (j / 128) + 128 * bj + (j % 128); }
;     { float t_[32];
; #pragma unroll
;       for (int i = 0; i < 32; ++i) t_[i] = W[(size_t)(k0 + 2 * i + (lane >> 5)) * ld + n0 + (lane & 31)];
; #pragma unroll
;       for (int i = 0; i < 32; ++i) scr[(2 * i + (lane >> 5)) * 33 + (lane & 31)] = t_[i] * scale; }
; __device__ __forceinline__ void convert_items(Frame& F, const Args& a, int lo, int hi, int w, int nw) {
;     ...
;         if (r < I_GU) { tr_item8(a.in[14], 2 * FF, D, 224, r, F.ws + WS_WGU, true, WSC_GU, scr, lane); continue; } r -= I_GU;
.LBB0_1171:
	s_andn2_b64 vcc, exec, s[6:7]
	s_cbranch_vccnz .LBB0_1173
	s_add_i32 s4, s16, 0xf300
	s_bfe_u32 s6, s4, 0xb0005
	s_mulk_i32 s6, 0x2493
	s_lshr_b32 s6, s6, 16
	s_mul_i32 s7, s6, 0xe0
	s_sub_i32 s4, s4, s7
	s_lshl_b32 s7, s4, 5
	s_and_b32 s8, s4, 0xffff
	s_cmpk_gt_u32 s8, 0x6f
	s_cselect_b32 s25, 0xfffff200, 0
	s_cselect_b32 s26, 0x80, 0
	s_lshl_b32 s4, s4, 7
	s_lshl_b32 s6, s6, 6
	s_and_b32 s4, s4, 0x3ff80
	v_add_u32_e32 v64, s6, v28
	v_lshl_add_u64 v[46:47], v[6:7], 0, s[4:5]
	v_mad_i64_i32 v[48:49], s[8:9], v64, s13, v[46:47]
	v_add_u32_e32 v50, 2, v64
	v_add_u32_e32 v52, 4, v64
	v_add_u32_e32 v54, 6, v64
	v_add_u32_e32 v56, 8, v64
	v_add_u32_e32 v58, 10, v64
	v_add_u32_e32 v60, 12, v64
	v_add_u32_e32 v62, 14, v64
	v_mad_i64_i32 v[50:51], s[8:9], v50, s13, v[46:47]
	v_mad_i64_i32 v[52:53], s[8:9], v52, s13, v[46:47]
	v_mad_i64_i32 v[54:55], s[8:9], v54, s13, v[46:47]
	v_mad_i64_i32 v[56:57], s[8:9], v56, s13, v[46:47]
	v_mad_i64_i32 v[58:59], s[8:9], v58, s13, v[46:47]
	v_mad_i64_i32 v[60:61], s[8:9], v60, s13, v[46:47]
	v_mad_i64_i32 v[62:63], s[8:9], v62, s13, v[46:47]
	global_load_dword v65, v[48:49], off nt
	global_load_dword v66, v[50:51], off nt
	global_load_dword v67, v[52:53], off nt
	global_load_dword v68, v[54:55], off nt
	global_load_dword v69, v[56:57], off nt
	global_load_dword v70, v[58:59], off nt
	global_load_dword v71, v[60:61], off nt
	global_load_dword v72, v[62:63], off nt
	v_add_u32_e32 v48, 16, v64
	v_mad_i64_i32 v[48:49], s[8:9], v48, s13, v[46:47]
	v_add_u32_e32 v50, 18, v64
	v_add_u32_e32 v52, 20, v64
	v_add_u32_e32 v54, 22, v64
	v_add_u32_e32 v56, 24, v64
	v_add_u32_e32 v58, 26, v64
	v_add_u32_e32 v60, 28, v64
	v_add_u32_e32 v62, 30, v64
	v_mad_i64_i32 v[50:51], s[8:9], v50, s13, v[46:47]
	v_mad_i64_i32 v[52:53], s[8:9], v52, s13, v[46:47]
	v_mad_i64_i32 v[54:55], s[8:9], v54, s13, v[46:47]
	v_mad_i64_i32 v[56:57], s[8:9], v56, s13, v[46:47]
	v_mad_i64_i32 v[58:59], s[8:9], v58, s13, v[46:47]
	v_mad_i64_i32 v[60:61], s[8:9], v60, s13, v[46:47]
	v_mad_i64_i32 v[62:63], s[8:9], v62, s13, v[46:47]
	global_load_dword v73, v[48:49], off nt
	global_load_dword v74, v[50:51], off nt
	global_load_dword v75, v[52:53], off nt
	global_load_dword v76, v[54:55], off nt
	global_load_dword v77, v[56:57], off nt
	global_load_dword v78, v[58:59], off nt
	global_load_dword v79, v[60:61], off nt
	global_load_dword v80, v[62:63], off nt
	v_add_u32_e32 v48, 32, v64
	v_add_u32_e32 v50, 34, v64
	v_add_u32_e32 v52, 36, v64
	v_add_u32_e32 v54, 38, v64
	v_add_u32_e32 v60, 44, v64
	v_mad_i64_i32 v[48:49], s[8:9], v48, s13, v[46:47]
	v_mad_i64_i32 v[50:51], s[8:9], v50, s13, v[46:47]
	v_mad_i64_i32 v[52:53], s[8:9], v52, s13, v[46:47]
	v_mad_i64_i32 v[54:55], s[8:9], v54, s13, v[46:47]
	v_add_u32_e32 v56, 40, v64
	v_add_u32_e32 v58, 42, v64
	v_mad_i64_i32 v[60:61], s[8:9], v60, s13, v[46:47]
	v_add_u32_e32 v62, 46, v64
	v_mad_i64_i32 v[56:57], s[8:9], v56, s13, v[46:47]
	v_mad_i64_i32 v[58:59], s[8:9], v58, s13, v[46:47]
	v_mad_i64_i32 v[62:63], s[8:9], v62, s13, v[46:47]
	global_load_dword v81, v[48:49], off nt
	global_load_dword v82, v[50:51], off nt
	global_load_dword v83, v[52:53], off nt
	global_load_dword v84, v[54:55], off nt
	global_load_dword v85, v[56:57], off nt
	global_load_dword v86, v[58:59], off nt
	s_nop 0
	global_load_dword v60, v[60:61], off nt
	s_nop 0
	global_load_dword v61, v[62:63], off nt
	v_add_u32_e32 v48, 48, v64
	v_add_u32_e32 v50, 50, v64
	v_add_u32_e32 v52, 52, v64
	v_add_u32_e32 v54, 54, v64
	v_mad_i64_i32 v[48:49], s[8:9], v48, s13, v[46:47]
	v_mad_i64_i32 v[50:51], s[8:9], v50, s13, v[46:47]
	v_mad_i64_i32 v[52:53], s[8:9], v52, s13, v[46:47]
	v_mad_i64_i32 v[54:55], s[8:9], v54, s13, v[46:47]
	v_add_u32_e32 v56, 56, v64
	v_add_u32_e32 v58, 58, v64
	v_mad_i64_i32 v[56:57], s[8:9], v56, s13, v[46:47]
	v_mad_i64_i32 v[58:59], s[8:9], v58, s13, v[46:47]
	global_load_dword v62, v[48:49], off nt
	s_nop 0
	global_load_dword v50, v[50:51], off nt
	s_nop 0
	global_load_dword v51, v[52:53], off nt
	s_nop 0
	global_load_dword v52, v[54:55], off nt
	global_load_dword v53, v[56:57], off nt
	s_nop 0
	global_load_dword v54, v[58:59], off nt
	v_add_u32_e32 v48, 60, v64
	v_add_u32_e32 v55, 62, v64
	v_mad_i64_i32 v[48:49], s[8:9], v48, s13, v[46:47]
	v_mad_i64_i32 v[46:47], s[8:9], v55, s13, v[46:47]
	global_load_dword v48, v[48:49], off nt
	s_nop 0
	global_load_dword v46, v[46:47], off nt
	s_waitcnt vmcnt(0)
; __device__ __forceinline__ unsigned cvt_pk4_fp8(float a, float b, float c, float d) { int w = 0; w = __builtin_amdgcn_cvt_pk_fp8_f32(a, b, w, false); w = __builtin_amdgcn_cvt_pk_fp8_f32(c, d, w, true); return (unsigned)w; }
; #define GAS __attribute__((address_space(1)))
; #define LAS __attribute__((address_space(3)))
; #define LDS_WAIT() asm volatile("s_waitcnt lgkmcnt(0)" ::: "memory")
; __device__ __forceinline__ void tr_item8(const float* W, int ld, int K, int nblk, int item, unsigned char* WT, bool gu, float scale, LAS float* scr, int lane) {
;     ...
;     if (gu) { const int bj = n0 / FF, j = n0 - bj * FF; drow0 = 256 * (j / 128) + 128 * bj + (j % 128); }
;     ...
;       for (int i = 0; i < 32; ++i) scr[(2 * i + (lane >> 5)) * 33 + (lane & 31)] = t_[i] * scale; }
;     LDS_WAIT(); asm volatile("" ::: "memory");
;     const int c = lane & 3;
; #pragma unroll
;     for (int j = 0; j < 2; ++j) { const int n = (lane >> 2) + 16 * j; const LAS float* sp = scr + (16 * c) * 33 + n;
;         v4u o; o.x = pg8::cvt_pk4_fp8(sp[0 * 33], sp[1 * 33], sp[2 * 33], sp[3 * 33]); o.y = pg8::cvt_pk4_fp8(sp[4 * 33], sp[5 * 33], sp[6 * 33], sp[7 * 33]);
;         o.z = pg8::cvt_pk4_fp8(sp[8 * 33], sp[9 * 33], sp[10 * 33], sp[11 * 33]); o.w = pg8::cvt_pk4_fp8(sp[12 * 33], sp[13 * 33], sp[14 * 33], sp[15 * 33]);
;         *(GAS v4u*)(WT + (size_t)(drow0 + n) * K + k0 + 16 * c) = o; }
;     LDS_WAIT(); asm volatile("" ::: "memory");
	v_mul_f32_e32 v47, 0x42800000, v65
	v_mul_f32_e32 v49, 0x42800000, v66
	ds_write2_b32 v29, v47, v49 offset1:66
	v_mul_f32_e32 v47, 0x42800000, v67
	v_mul_f32_e32 v49, 0x42800000, v68
	ds_write2_b32 v29, v47, v49 offset0:132 offset1:198
	v_mul_f32_e32 v47, 0x42800000, v69
	v_mul_f32_e32 v49, 0x42800000, v70
	ds_write2_b32 v38, v47, v49 offset0:8 offset1:74
	v_mul_f32_e32 v47, 0x42800000, v71
	v_mul_f32_e32 v49, 0x42800000, v72
	ds_write2_b32 v38, v47, v49 offset0:140 offset1:206
	s_add_i32 s4, s25, s7
	s_sext_i32_i16 s7, s4
	s_bfe_u32 s7, s7, 0x70018
	s_add_i32 s7, s4, s7
	s_sext_i32_i16 s8, s7
	s_and_b32 s7, s7, 0xff80
	s_sub_i32 s4, s4, s7
	s_lshl_b32 s8, s8, 1
	s_sext_i32_i16 s4, s4
	v_mul_f32_e32 v47, 0x42800000, v73
	v_mul_f32_e32 v49, 0x42800000, v74
	ds_write2_b32 v39, v47, v49 offset0:16 offset1:82
	v_mul_f32_e32 v47, 0x42800000, v75
	v_mul_f32_e32 v49, 0x42800000, v76
	ds_write2_b32 v39, v47, v49 offset0:148 offset1:214
	v_mul_f32_e32 v47, 0x42800000, v77
	v_mul_f32_e32 v49, 0x42800000, v78
	ds_write2_b32 v40, v47, v49 offset0:24 offset1:90
	v_mul_f32_e32 v47, 0x42800000, v79
	v_mul_f32_e32 v49, 0x42800000, v80
	ds_write2_b32 v40, v47, v49 offset0:156 offset1:222
	s_and_b32 s8, s8, 0xffffff00
	s_add_i32 s4, s26, s4
	s_add_i32 s4, s4, s8
	s_mov_b32 s7, s5
	v_mul_f32_e32 v47, 0x42800000, v81
	v_mul_f32_e32 v49, 0x42800000, v82
	ds_write2_b32 v41, v47, v49 offset0:32 offset1:98
	v_mul_f32_e32 v47, 0x42800000, v83
	v_mul_f32_e32 v49, 0x42800000, v84
	ds_write2_b32 v41, v47, v49 offset0:164 offset1:230
	v_mul_f32_e32 v47, 0x42800000, v85
	v_mul_f32_e32 v49, 0x42800000, v86
	ds_write2_b32 v42, v47, v49 offset0:40 offset1:106
	v_mul_f32_e32 v47, 0x42800000, v60
	v_mul_f32_e32 v49, 0x42800000, v61
	ds_write2_b32 v42, v47, v49 offset0:172 offset1:238
	v_add_u32_e32 v84, s4, v30
	v_ashrrev_i32_e32 v85, 31, v84
	v_lshlrev_b64 v[84:85], 10, v[84:85]
	v_mul_f32_e32 v47, 0x42800000, v62
	v_mul_f32_e32 v49, 0x42800000, v50
	ds_write2_b32 v43, v47, v49 offset0:48 offset1:114
	v_mul_f32_e32 v47, 0x42800000, v51
	v_mul_f32_e32 v49, 0x42800000, v52
	ds_write2_b32 v43, v47, v49 offset0:180 offset1:246
	v_mul_f32_e32 v47, 0x42800000, v53
	v_mul_f32_e32 v49, 0x42800000, v54
	ds_write2_b32 v44, v47, v49 offset0:56 offset1:122
	v_mov_b32_e32 v49, 0
	v_lshl_add_u64 v[50:51], v[20:21], 0, s[6:7]
	v_mul_f32_e32 v47, 0x42800000, v48
	v_mul_f32_e32 v46, 0x42800000, v46
	ds_write2_b32 v44, v47, v46 offset0:188 offset1:254
	s_waitcnt lgkmcnt(0)
	ds_read2_b32 v[52:53], v31 offset1:16
	ds_read2_b32 v[54:55], v31 offset0:33 offset1:49
	ds_read2_b32 v[56:57], v31 offset0:66 offset1:82
	ds_read2_b32 v[58:59], v31 offset0:99 offset1:115
	ds_read2_b32 v[60:61], v31 offset0:132 offset1:148
	ds_read2_b32 v[62:63], v31 offset0:165 offset1:181
	ds_read2_b32 v[64:65], v31 offset0:198 offset1:214
	ds_read2_b32 v[66:67], v31 offset0:231 offset1:247
	ds_read2_b32 v[68:69], v45 offset0:8 offset1:24
	ds_read2_b32 v[70:71], v45 offset0:41 offset1:57
	ds_read2_b32 v[72:73], v45 offset0:74 offset1:90
	ds_read2_b32 v[74:75], v45 offset0:107 offset1:123
	ds_read2_b32 v[76:77], v45 offset0:140 offset1:156
	ds_read2_b32 v[78:79], v45 offset0:173 offset1:189
	v_mov_b32_e32 v46, 0
	v_mov_b32_e32 v47, 0
	v_mov_b32_e32 v48, 0
	ds_read2_b32 v[80:81], v45 offset0:206 offset1:222
	ds_read2_b32 v[82:83], v45 offset0:239 offset1:255
	s_waitcnt lgkmcnt(14)
	v_cvt_pk_fp8_f32 v46, v52, v54
	s_waitcnt lgkmcnt(10)
	v_cvt_pk_fp8_f32 v47, v60, v62
	s_waitcnt lgkmcnt(6)
	v_cvt_pk_fp8_f32 v48, v68, v70
	s_waitcnt lgkmcnt(2)
	v_cvt_pk_fp8_f32 v49, v76, v78
	v_cvt_pk_fp8_f32 v46, v56, v58 op_sel:[0,0,1]
	v_cvt_pk_fp8_f32 v47, v64, v66 op_sel:[0,0,1]
	v_cvt_pk_fp8_f32 v48, v72, v74 op_sel:[0,0,1]
	s_waitcnt lgkmcnt(0)
	v_cvt_pk_fp8_f32 v49, v80, v82 op_sel:[0,0,1]
	v_lshl_add_u64 v[84:85], v[50:51], 0, v[84:85]
	v_add_u32_e32 v52, s4, v32
	global_store_dwordx4 v[84:85], v[46:49], off
	s_nop 1
	v_mov_b32_e32 v46, 0
	v_mov_b32_e32 v47, 0
	v_mov_b32_e32 v48, 0
	v_mov_b32_e32 v49, 0
	v_cvt_pk_fp8_f32 v46, v53, v55
	v_cvt_pk_fp8_f32 v47, v61, v63
	v_cvt_pk_fp8_f32 v48, v69, v71
	v_cvt_pk_fp8_f32 v49, v77, v79
	v_cvt_pk_fp8_f32 v46, v57, v59 op_sel:[0,0,1]
	v_cvt_pk_fp8_f32 v47, v65, v67 op_sel:[0,0,1]
	v_cvt_pk_fp8_f32 v48, v73, v75 op_sel:[0,0,1]
	v_cvt_pk_fp8_f32 v49, v81, v83 op_sel:[0,0,1]
	v_ashrrev_i32_e32 v53, 31, v52
	v_lshlrev_b64 v[52:53], 10, v[52:53]
	v_lshl_add_u64 v[50:51], v[50:51], 0, v[52:53]
	global_store_dwordx4 v[50:51], v[46:49], off
	s_waitcnt lgkmcnt(0)

; __device__ __forceinline__ void tr_item(const float* W, int ld, int K, int nblk, int item, bf16* WT, bool gu, LAS float* scr, int lane) {
;     const int kb = item / nblk, nb = item % nblk, k0 = 64 * kb, n0 = 32 * nb;
;     int drow0 = n0;
;     if (gu) { const int bj = n0 / FF, j = n0 - bj * FF; drow0 = 256 * (j / 128) + 128 * bj + (j % 128); }
;     { float t_[32];
; #pragma unroll
;       for (int i = 0; i < 32; ++i) t_[i] = W[(size_t)(k0 + 2 * i + (lane >> 5)) * ld + n0 + (lane & 31)];
; #pragma unroll
;       for (int i = 0; i < 32; ++i) scr[(2 * i + (lane >> 5)) * 33 + (lane & 31)] = t_[i]; }
; __device__ __forceinline__ void convert_items(Frame& F, const Args& a, int lo, int hi, int w, int nw) {
;     ...
;         if (r < I_SO) { tr_item(a.in[12], D, D, 32, r, (bf16*)(F.ws + WS_WSWAOUT), false, scr, lane); continue; } r -= I_SO;
.LBB0_1174:
	s_andn2_b64 vcc, exec, s[6:7]
	s_cbranch_vccnz .LBB0_1176
	s_add_i32 s4, s11, 0x2000
	s_and_b32 s7, s4, 0x1ffc0
	s_and_b32 s6, s10, 0x3e0
	v_add_u32_e32 v46, s7, v28
	s_lshl_b32 s4, s6, 2
	v_ashrrev_i32_e32 v47, 31, v46
	v_lshl_add_u64 v[48:49], v[8:9], 0, s[4:5]
	v_lshlrev_b64 v[46:47], 12, v[46:47]
	v_lshl_add_u64 v[46:47], v[48:49], 0, v[46:47]
	v_add_co_u32_e32 v48, vcc, 0x2000, v46
	s_lshl_b32 s4, s7, 1
	s_nop 0
	v_addc_co_u32_e32 v49, vcc, 0, v47, vcc
	v_add_co_u32_e32 v50, vcc, 0x4000, v46
	s_nop 1
	v_addc_co_u32_e32 v51, vcc, 0, v47, vcc
	v_add_co_u32_e32 v52, vcc, 0x6000, v46
	s_nop 1
	v_addc_co_u32_e32 v53, vcc, 0, v47, vcc
	v_add_co_u32_e32 v54, vcc, 0x8000, v46
	s_nop 1
	v_addc_co_u32_e32 v55, vcc, 0, v47, vcc
	v_add_co_u32_e32 v56, vcc, 0xa000, v46
	s_nop 1
	v_addc_co_u32_e32 v57, vcc, 0, v47, vcc
	v_add_co_u32_e32 v58, vcc, 0xc000, v46
	s_nop 1
	v_addc_co_u32_e32 v59, vcc, 0, v47, vcc
	v_add_co_u32_e32 v60, vcc, 0xe000, v46
	s_nop 1
	v_addc_co_u32_e32 v61, vcc, 0, v47, vcc
	global_load_dword v64, v[46:47], off nt
	global_load_dword v65, v[48:49], off nt
	global_load_dword v66, v[50:51], off nt
	global_load_dword v67, v[52:53], off nt
	global_load_dword v68, v[54:55], off nt
	global_load_dword v69, v[56:57], off nt
	global_load_dword v70, v[58:59], off nt
	global_load_dword v71, v[60:61], off nt
	v_add_co_u32_e32 v48, vcc, 0x10000, v46
	s_nop 1
	v_addc_co_u32_e32 v49, vcc, 0, v47, vcc
	v_add_co_u32_e32 v50, vcc, 0x12000, v46
	s_nop 1
	v_addc_co_u32_e32 v51, vcc, 0, v47, vcc
	v_add_co_u32_e32 v52, vcc, 0x14000, v46
	s_nop 1
	v_addc_co_u32_e32 v53, vcc, 0, v47, vcc
	v_add_co_u32_e32 v54, vcc, 0x16000, v46
	s_nop 1
	v_addc_co_u32_e32 v55, vcc, 0, v47, vcc
	v_add_co_u32_e32 v56, vcc, 0x18000, v46
	s_nop 1
	v_addc_co_u32_e32 v57, vcc, 0, v47, vcc
	v_add_co_u32_e32 v58, vcc, 0x1a000, v46
	s_nop 1
	v_addc_co_u32_e32 v59, vcc, 0, v47, vcc
	v_add_co_u32_e32 v60, vcc, 0x1c000, v46
	s_nop 1
	v_addc_co_u32_e32 v61, vcc, 0, v47, vcc
	v_add_co_u32_e32 v62, vcc, 0x1e000, v46
	s_nop 1
	v_addc_co_u32_e32 v63, vcc, 0, v47, vcc
	global_load_dword v72, v[48:49], off nt
	global_load_dword v73, v[50:51], off nt
	global_load_dword v74, v[52:53], off nt
	global_load_dword v75, v[54:55], off nt
	global_load_dword v76, v[56:57], off nt
	global_load_dword v77, v[58:59], off nt
	global_load_dword v78, v[60:61], off nt
	global_load_dword v79, v[62:63], off nt
	v_add_co_u32_e32 v48, vcc, 0x20000, v46
	s_nop 1
	v_addc_co_u32_e32 v49, vcc, 0, v47, vcc
	v_add_co_u32_e32 v50, vcc, 0x22000, v46
	s_nop 1
	v_addc_co_u32_e32 v51, vcc, 0, v47, vcc
	v_add_co_u32_e32 v52, vcc, 0x24000, v46
	s_nop 1
	v_addc_co_u32_e32 v53, vcc, 0, v47, vcc
	v_add_co_u32_e32 v54, vcc, 0x26000, v46
	s_nop 1
	v_addc_co_u32_e32 v55, vcc, 0, v47, vcc
	v_add_co_u32_e32 v56, vcc, 0x28000, v46
	s_nop 1
	v_addc_co_u32_e32 v57, vcc, 0, v47, vcc
	v_add_co_u32_e32 v58, vcc, 0x2a000, v46
	s_nop 1
	v_addc_co_u32_e32 v59, vcc, 0, v47, vcc
	v_add_co_u32_e32 v60, vcc, 0x2c000, v46
	s_nop 1
	v_addc_co_u32_e32 v61, vcc, 0, v47, vcc
	v_add_co_u32_e32 v62, vcc, 0x2e000, v46
	s_nop 1
	v_addc_co_u32_e32 v63, vcc, 0, v47, vcc
	global_load_dword v80, v[48:49], off nt
	global_load_dword v81, v[50:51], off nt
	global_load_dword v82, v[52:53], off nt
	global_load_dword v83, v[54:55], off nt
	global_load_dword v84, v[56:57], off nt
	global_load_dword v85, v[58:59], off nt
	global_load_dword v86, v[60:61], off nt
	s_nop 0
	global_load_dword v62, v[62:63], off nt
	v_add_co_u32_e32 v48, vcc, 0x30000, v46
	s_nop 1
	v_addc_co_u32_e32 v49, vcc, 0, v47, vcc
	v_add_co_u32_e32 v50, vcc, 0x32000, v46
	s_nop 1
	v_addc_co_u32_e32 v51, vcc, 0, v47, vcc
	v_add_co_u32_e32 v52, vcc, 0x34000, v46
	s_nop 1
	v_addc_co_u32_e32 v53, vcc, 0, v47, vcc
	v_add_co_u32_e32 v54, vcc, 0x36000, v46
	s_nop 1
	v_addc_co_u32_e32 v55, vcc, 0, v47, vcc
	v_add_co_u32_e32 v56, vcc, 0x38000, v46
	s_nop 1
	v_addc_co_u32_e32 v57, vcc, 0, v47, vcc
	v_add_co_u32_e32 v58, vcc, 0x3a000, v46
	s_nop 1
	v_addc_co_u32_e32 v59, vcc, 0, v47, vcc
	v_add_co_u32_e32 v60, vcc, 0x3c000, v46
	s_nop 1
	v_addc_co_u32_e32 v61, vcc, 0, v47, vcc
	v_add_co_u32_e32 v46, vcc, 0x3e000, v46
	s_nop 1
	v_addc_co_u32_e32 v47, vcc, 0, v47, vcc
	global_load_dword v48, v[48:49], off nt
	s_nop 0
	global_load_dword v49, v[50:51], off nt
	s_nop 0
	global_load_dword v50, v[52:53], off nt
	global_load_dword v51, v[54:55], off nt
	s_nop 0
	global_load_dword v52, v[56:57], off nt
	global_load_dword v53, v[58:59], off nt
	global_load_dword v54, v[60:61], off nt
	s_nop 0
	global_load_dword v46, v[46:47], off nt
	s_waitcnt vmcnt(0)
	ds_write2_b32 v29, v64, v65 offset1:66
	ds_write2_b32 v29, v66, v67 offset0:132 offset1:198
	ds_write2_b32 v38, v68, v69 offset0:8 offset1:74
	ds_write2_b32 v38, v70, v71 offset0:140 offset1:206
	ds_write2_b32 v39, v72, v73 offset0:16 offset1:82
	ds_write2_b32 v39, v74, v75 offset0:148 offset1:214
	ds_write2_b32 v40, v76, v77 offset0:24 offset1:90
	ds_write2_b32 v40, v78, v79 offset0:156 offset1:222
	ds_write2_b32 v41, v80, v81 offset0:32 offset1:98
	ds_write2_b32 v41, v82, v83 offset0:164 offset1:230
	ds_write2_b32 v42, v84, v85 offset0:40 offset1:106
	ds_write2_b32 v42, v86, v62 offset0:172 offset1:238
	ds_write2_b32 v43, v48, v49 offset0:48 offset1:114
	ds_write2_b32 v43, v50, v51 offset0:180 offset1:246
	ds_write2_b32 v44, v52, v53 offset0:56 offset1:122
	ds_write2_b32 v44, v54, v46 offset0:188 offset1:254
	s_waitcnt lgkmcnt(0)
; #define GAS __attribute__((address_space(1)))
; #define LAS __attribute__((address_space(3)))
; #define LDS_WAIT() asm volatile("s_waitcnt lgkmcnt(0)" ::: "memory")
; __device__ __forceinline__ unsigned pk2(float lo, float hi) { return f2bf(lo) | (f2bf(hi) << 16); }
; __device__ __forceinline__ void tr_item(const float* W, int ld, int K, int nblk, int item, bf16* WT, bool gu, LAS float* scr, int lane) {
;     ...
;       for (int i = 0; i < 32; ++i) scr[(2 * i + (lane >> 5)) * 33 + (lane & 31)] = t_[i]; }
;     LDS_WAIT(); asm volatile("" ::: "memory");
;     const int c = lane & 7;
; #pragma unroll
;     for (int j = 0; j < 4; ++j) { const int n = (lane >> 3) + 8 * j; const LAS float* s = scr + (8 * c) * 33 + n;
;         v4u o; o.x = pk2(s[0 * 33], s[1 * 33]); o.y = pk2(s[2 * 33], s[3 * 33]); o.z = pk2(s[4 * 33], s[5 * 33]); o.w = pk2(s[6 * 33], s[7 * 33]);
;         *(GAS v4u*)(WT + (size_t)(drow0 + n) * K + k0 + 8 * c) = o; }
;     LDS_WAIT(); asm volatile("" ::: "memory");
	ds_read2_b32 v[50:51], v34 offset1:8
	ds_read2_b32 v[54:55], v34 offset0:33 offset1:41
	ds_read2_b32 v[56:57], v34 offset0:66 offset1:74
	ds_read2_b32 v[58:59], v34 offset0:99 offset1:107
	ds_read2_b32 v[60:61], v34 offset0:132 offset1:140
	s_waitcnt lgkmcnt(4)
	v_bfe_u32 v46, v50, 16, 1
	v_add3_u32 v46, v50, v46, s14
	s_waitcnt lgkmcnt(3)
	v_bfe_u32 v47, v54, 16, 1
	v_lshrrev_b32_e32 v46, 16, v46
	v_add3_u32 v47, v54, v47, s14
	ds_read2_b32 v[62:63], v34 offset0:165 offset1:173
	v_and_or_b32 v46, v47, s15, v46
	s_waitcnt lgkmcnt(3)
	v_bfe_u32 v47, v56, 16, 1
	v_add3_u32 v47, v56, v47, s14
	s_waitcnt lgkmcnt(2)
	v_bfe_u32 v48, v58, 16, 1
	ds_read2_b32 v[64:65], v34 offset0:198 offset1:206
	v_lshrrev_b32_e32 v47, 16, v47
	v_add3_u32 v48, v58, v48, s14
	ds_read2_b32 v[66:67], v34 offset0:231 offset1:239
	v_and_or_b32 v47, v48, s15, v47
	s_waitcnt lgkmcnt(3)
	v_bfe_u32 v48, v60, 16, 1
	v_add3_u32 v48, v60, v48, s14
	s_waitcnt lgkmcnt(2)
	v_bfe_u32 v49, v62, 16, 1
	v_lshrrev_b32_e32 v48, 16, v48
	v_add3_u32 v49, v62, v49, s14
	v_and_or_b32 v48, v49, s15, v48
	s_waitcnt lgkmcnt(1)
	v_bfe_u32 v49, v64, 16, 1
	v_add_u32_e32 v68, s6, v33
	v_add3_u32 v49, v64, v49, s14
	s_waitcnt lgkmcnt(0)
	v_bfe_u32 v50, v66, 16, 1
	v_ashrrev_i32_e32 v69, 31, v68
	v_lshl_add_u64 v[52:53], v[22:23], 0, s[4:5]
	v_lshrrev_b32_e32 v49, 16, v49
	v_add3_u32 v50, v66, v50, s14
	v_lshlrev_b64 v[68:69], 11, v[68:69]
	v_and_or_b32 v49, v50, s15, v49
	v_lshl_add_u64 v[68:69], v[52:53], 0, v[68:69]
	global_store_dwordx4 v[68:69], v[46:49], off
	v_bfe_u32 v50, v67, 16, 1
	v_add3_u32 v50, v67, v50, s14
	v_bfe_u32 v46, v51, 16, 1
	v_add3_u32 v46, v51, v46, s14
	v_bfe_u32 v47, v55, 16, 1
	v_lshrrev_b32_e32 v46, 16, v46
	v_add3_u32 v47, v55, v47, s14
	v_and_or_b32 v46, v47, s15, v46
	v_bfe_u32 v47, v57, 16, 1
	v_add3_u32 v47, v57, v47, s14
	v_bfe_u32 v48, v59, 16, 1
	v_lshrrev_b32_e32 v47, 16, v47
	v_add3_u32 v48, v59, v48, s14
	v_and_or_b32 v47, v48, s15, v47
	v_bfe_u32 v48, v61, 16, 1
	v_add3_u32 v48, v61, v48, s14
	v_bfe_u32 v49, v63, 16, 1
	v_lshrrev_b32_e32 v48, 16, v48
	v_add3_u32 v49, v63, v49, s14
	v_and_or_b32 v48, v49, s15, v48
	v_bfe_u32 v49, v65, 16, 1
	v_add3_u32 v49, v65, v49, s14
	v_lshrrev_b32_e32 v49, 16, v49
	v_and_or_b32 v49, v50, s15, v49
	v_add_u32_e32 v50, s6, v35
	v_ashrrev_i32_e32 v51, 31, v50
	v_lshlrev_b64 v[50:51], 11, v[50:51]
	ds_read2_b32 v[54:55], v34 offset0:16 offset1:24
	v_lshl_add_u64 v[50:51], v[52:53], 0, v[50:51]
	global_store_dwordx4 v[50:51], v[46:49], off
	ds_read2_b32 v[50:51], v34 offset0:49 offset1:57
	ds_read2_b32 v[56:57], v34 offset0:82 offset1:90
	ds_read2_b32 v[58:59], v34 offset0:115 offset1:123
	s_waitcnt lgkmcnt(3)
	v_bfe_u32 v46, v54, 16, 1
	v_add3_u32 v46, v54, v46, s14
	s_waitcnt lgkmcnt(2)
	v_bfe_u32 v47, v50, 16, 1
	ds_read2_b32 v[60:61], v34 offset0:148 offset1:156
	v_lshrrev_b32_e32 v46, 16, v46
	v_add3_u32 v47, v50, v47, s14
	ds_read2_b32 v[62:63], v34 offset0:181 offset1:189
	v_and_or_b32 v46, v47, s15, v46
	s_waitcnt lgkmcnt(3)
	v_bfe_u32 v47, v56, 16, 1
	v_add3_u32 v47, v56, v47, s14
	s_waitcnt lgkmcnt(2)
	v_bfe_u32 v48, v58, 16, 1
	ds_read2_b32 v[64:65], v34 offset0:214 offset1:222
	v_lshrrev_b32_e32 v47, 16, v47
	v_add3_u32 v48, v58, v48, s14
	ds_read2_b32 v[66:67], v34 offset0:247 offset1:255
	v_and_or_b32 v47, v48, s15, v47
	s_waitcnt lgkmcnt(3)
	v_bfe_u32 v48, v60, 16, 1
	v_add3_u32 v48, v60, v48, s14
	s_waitcnt lgkmcnt(2)
	v_bfe_u32 v49, v62, 16, 1
	v_lshrrev_b32_e32 v48, 16, v48
	v_add3_u32 v49, v62, v49, s14
	v_and_or_b32 v48, v49, s15, v48
	s_waitcnt lgkmcnt(1)
	v_bfe_u32 v49, v64, 16, 1
	v_add_u32_e32 v68, s6, v36
	v_add3_u32 v49, v64, v49, s14
	s_waitcnt lgkmcnt(0)
	v_bfe_u32 v50, v66, 16, 1
	v_ashrrev_i32_e32 v69, 31, v68
	v_lshrrev_b32_e32 v49, 16, v49
	v_add3_u32 v50, v66, v50, s14
	v_lshlrev_b64 v[68:69], 11, v[68:69]
	v_and_or_b32 v49, v50, s15, v49
	v_lshl_add_u64 v[68:69], v[52:53], 0, v[68:69]
	global_store_dwordx4 v[68:69], v[46:49], off
	v_bfe_u32 v50, v67, 16, 1
	v_add3_u32 v50, v67, v50, s14
	v_bfe_u32 v46, v55, 16, 1
	v_add3_u32 v46, v55, v46, s14
	v_bfe_u32 v47, v51, 16, 1
	v_lshrrev_b32_e32 v46, 16, v46
	v_add3_u32 v47, v51, v47, s14
	v_and_or_b32 v46, v47, s15, v46
	v_bfe_u32 v47, v57, 16, 1
	v_add3_u32 v47, v57, v47, s14
	v_bfe_u32 v48, v59, 16, 1
	v_lshrrev_b32_e32 v47, 16, v47
	v_add3_u32 v48, v59, v48, s14
	v_and_or_b32 v47, v48, s15, v47
	v_bfe_u32 v48, v61, 16, 1
	v_add3_u32 v48, v61, v48, s14
	v_bfe_u32 v49, v63, 16, 1
	v_lshrrev_b32_e32 v48, 16, v48
	v_add3_u32 v49, v63, v49, s14
	v_and_or_b32 v48, v49, s15, v48
	v_bfe_u32 v49, v65, 16, 1
	v_add3_u32 v49, v65, v49, s14
	v_lshrrev_b32_e32 v49, 16, v49
	v_and_or_b32 v49, v50, s15, v49
	v_add_u32_e32 v50, s6, v37
	v_ashrrev_i32_e32 v51, 31, v50
	v_lshlrev_b64 v[50:51], 11, v[50:51]
	v_lshl_add_u64 v[50:51], v[52:53], 0, v[50:51]
	global_store_dwordx4 v[50:51], v[46:49], off
	s_waitcnt lgkmcnt(0)

; __device__ __forceinline__ void tr_item(const float* W, int ld, int K, int nblk, int item, bf16* WT, bool gu, LAS float* scr, int lane) {
;     const int kb = item / nblk, nb = item % nblk, k0 = 64 * kb, n0 = 32 * nb;
;     int drow0 = n0;
;     if (gu) { const int bj = n0 / FF, j = n0 - bj * FF; drow0 = 256 * (j / 128) + 128 * bj + (j % 128); }
;     { float t_[32];
; #pragma unroll
;       for (int i = 0; i < 32; ++i) t_[i] = W[(size_t)(k0 + 2 * i + (lane >> 5)) * ld + n0 + (lane & 31)];
; #pragma unroll
;       for (int i = 0; i < 32; ++i) scr[(2 * i + (lane >> 5)) * 33 + (lane & 31)] = t_[i]; }
; __device__ __forceinline__ void convert_items(Frame& F, const Args& a, int lo, int hi, int w, int nw) {
;     ...
;         if (r < I_SI) { tr_item(a.in[10], D + 512, D, 48, r, (bf16*)(F.ws + WS_WSWAIN), false, scr, lane); continue; } r -= I_SI;
.LBB0_1177:
	s_andn2_b64 vcc, exec, s[6:7]
	s_cbranch_vccnz .LBB0_1179
	s_add_i32 s4, s16, 0xf800
	s_and_b32 s6, s4, 0xffff
	s_mul_i32 s6, s6, 0xaaab
	s_lshr_b32 s7, s6, 21
	s_mul_i32 s6, s7, 48
	s_sub_i32 s4, s4, s6
	s_lshl_b32 s4, s4, 5
	s_and_b32 s6, s4, 0xffe0
	v_lshl_add_u32 v64, s7, 6, v28
	s_lshl_b32 s4, s6, 2
	v_lshl_add_u64 v[46:47], v[10:11], 0, s[4:5]
	v_add_u32_e32 v50, 2, v64
	v_add_u32_e32 v52, 4, v64
	v_add_u32_e32 v54, 6, v64
	v_add_u32_e32 v56, 8, v64
	v_add_u32_e32 v58, 10, v64
	v_add_u32_e32 v60, 12, v64
	v_add_u32_e32 v62, 14, v64
	v_mad_i64_i32 v[48:49], s[8:9], v64, s17, v[46:47]
	v_mad_i64_i32 v[50:51], s[8:9], v50, s17, v[46:47]
	v_mad_i64_i32 v[52:53], s[8:9], v52, s17, v[46:47]
	v_mad_i64_i32 v[54:55], s[8:9], v54, s17, v[46:47]
	v_mad_i64_i32 v[56:57], s[8:9], v56, s17, v[46:47]
	v_mad_i64_i32 v[58:59], s[8:9], v58, s17, v[46:47]
	v_mad_i64_i32 v[60:61], s[8:9], v60, s17, v[46:47]
	v_mad_i64_i32 v[62:63], s[8:9], v62, s17, v[46:47]
	global_load_dword v65, v[48:49], off nt
	global_load_dword v66, v[50:51], off nt
	global_load_dword v67, v[52:53], off nt
	global_load_dword v68, v[54:55], off nt
	global_load_dword v69, v[56:57], off nt
	global_load_dword v70, v[58:59], off nt
	global_load_dword v71, v[60:61], off nt
	global_load_dword v72, v[62:63], off nt
	v_add_u32_e32 v48, 16, v64
	v_add_u32_e32 v50, 18, v64
	v_add_u32_e32 v52, 20, v64
	v_add_u32_e32 v54, 22, v64
	v_add_u32_e32 v56, 24, v64
	v_add_u32_e32 v58, 26, v64
	v_add_u32_e32 v60, 28, v64
	v_add_u32_e32 v62, 30, v64
	v_mad_i64_i32 v[48:49], s[8:9], v48, s17, v[46:47]
	v_mad_i64_i32 v[50:51], s[8:9], v50, s17, v[46:47]
	v_mad_i64_i32 v[52:53], s[8:9], v52, s17, v[46:47]
	v_mad_i64_i32 v[54:55], s[8:9], v54, s17, v[46:47]
	v_mad_i64_i32 v[56:57], s[8:9], v56, s17, v[46:47]
	v_mad_i64_i32 v[58:59], s[8:9], v58, s17, v[46:47]
	v_mad_i64_i32 v[60:61], s[8:9], v60, s17, v[46:47]
	v_mad_i64_i32 v[62:63], s[8:9], v62, s17, v[46:47]
	global_load_dword v73, v[48:49], off nt
	global_load_dword v74, v[50:51], off nt
	global_load_dword v75, v[52:53], off nt
	global_load_dword v76, v[54:55], off nt
	global_load_dword v77, v[56:57], off nt
	global_load_dword v78, v[58:59], off nt
	global_load_dword v79, v[60:61], off nt
	global_load_dword v80, v[62:63], off nt
	v_add_u32_e32 v48, 32, v64
	v_add_u32_e32 v50, 34, v64
	v_add_u32_e32 v52, 36, v64
	v_add_u32_e32 v54, 38, v64
	v_add_u32_e32 v56, 40, v64
	v_add_u32_e32 v58, 42, v64
	v_add_u32_e32 v60, 44, v64
	v_add_u32_e32 v62, 46, v64
	v_mad_i64_i32 v[48:49], s[8:9], v48, s17, v[46:47]
	v_mad_i64_i32 v[50:51], s[8:9], v50, s17, v[46:47]
	v_mad_i64_i32 v[52:53], s[8:9], v52, s17, v[46:47]
	v_mad_i64_i32 v[54:55], s[8:9], v54, s17, v[46:47]
	v_mad_i64_i32 v[56:57], s[8:9], v56, s17, v[46:47]
	v_mad_i64_i32 v[58:59], s[8:9], v58, s17, v[46:47]
	v_mad_i64_i32 v[60:61], s[8:9], v60, s17, v[46:47]
	v_mad_i64_i32 v[62:63], s[8:9], v62, s17, v[46:47]
	global_load_dword v81, v[48:49], off nt
	global_load_dword v82, v[50:51], off nt
	global_load_dword v83, v[52:53], off nt
	global_load_dword v84, v[54:55], off nt
	global_load_dword v85, v[56:57], off nt
	global_load_dword v86, v[58:59], off nt
	global_load_dword v87, v[60:61], off nt
	s_nop 0
	global_load_dword v62, v[62:63], off nt
	v_add_u32_e32 v48, 48, v64
	v_add_u32_e32 v50, 50, v64
	v_add_u32_e32 v52, 52, v64
	v_add_u32_e32 v54, 54, v64
	v_add_u32_e32 v56, 56, v64
	v_add_u32_e32 v58, 58, v64
	v_add_u32_e32 v60, 60, v64
	v_add_u32_e32 v63, 62, v64
	v_mad_i64_i32 v[48:49], s[8:9], v48, s17, v[46:47]
	v_mad_i64_i32 v[50:51], s[8:9], v50, s17, v[46:47]
	v_mad_i64_i32 v[52:53], s[8:9], v52, s17, v[46:47]
	v_mad_i64_i32 v[54:55], s[8:9], v54, s17, v[46:47]
	v_mad_i64_i32 v[56:57], s[8:9], v56, s17, v[46:47]
	v_mad_i64_i32 v[58:59], s[8:9], v58, s17, v[46:47]
	v_mad_i64_i32 v[60:61], s[8:9], v60, s17, v[46:47]
	v_mad_i64_i32 v[46:47], s[8:9], v63, s17, v[46:47]
	global_load_dword v48, v[48:49], off nt
	s_nop 0
	global_load_dword v49, v[50:51], off nt
	s_nop 0
	global_load_dword v50, v[52:53], off nt
	global_load_dword v51, v[54:55], off nt
	s_nop 0
	global_load_dword v52, v[56:57], off nt
	global_load_dword v53, v[58:59], off nt
	global_load_dword v54, v[60:61], off nt
	s_nop 0
	global_load_dword v46, v[46:47], off nt
	s_waitcnt vmcnt(0)
	ds_write2_b32 v29, v65, v66 offset1:66
	ds_write2_b32 v29, v67, v68 offset0:132 offset1:198
	ds_write2_b32 v38, v69, v70 offset0:8 offset1:74
	ds_write2_b32 v38, v71, v72 offset0:140 offset1:206
	ds_write2_b32 v39, v73, v74 offset0:16 offset1:82
	ds_write2_b32 v39, v75, v76 offset0:148 offset1:214
	ds_write2_b32 v40, v77, v78 offset0:24 offset1:90
	ds_write2_b32 v40, v79, v80 offset0:156 offset1:222
	ds_write2_b32 v41, v81, v82 offset0:32 offset1:98
	ds_write2_b32 v41, v83, v84 offset0:164 offset1:230
	ds_write2_b32 v42, v85, v86 offset0:40 offset1:106
	ds_write2_b32 v42, v87, v62 offset0:172 offset1:238
	ds_write2_b32 v43, v48, v49 offset0:48 offset1:114
	ds_write2_b32 v43, v50, v51 offset0:180 offset1:246
	ds_write2_b32 v44, v52, v53 offset0:56 offset1:122
	ds_write2_b32 v44, v54, v46 offset0:188 offset1:254
	s_waitcnt lgkmcnt(0)
; #define GAS __attribute__((address_space(1)))
; #define LAS __attribute__((address_space(3)))
; #define LDS_WAIT() asm volatile("s_waitcnt lgkmcnt(0)" ::: "memory")
; __device__ __forceinline__ unsigned pk2(float lo, float hi) { return f2bf(lo) | (f2bf(hi) << 16); }
; __device__ __forceinline__ void tr_item(const float* W, int ld, int K, int nblk, int item, bf16* WT, bool gu, LAS float* scr, int lane) {
;     ...
;       for (int i = 0; i < 32; ++i) scr[(2 * i + (lane >> 5)) * 33 + (lane & 31)] = t_[i]; }
;     LDS_WAIT(); asm volatile("" ::: "memory");
;     const int c = lane & 7;
; #pragma unroll
;     for (int j = 0; j < 4; ++j) { const int n = (lane >> 3) + 8 * j; const LAS float* s = scr + (8 * c) * 33 + n;
;         v4u o; o.x = pk2(s[0 * 33], s[1 * 33]); o.y = pk2(s[2 * 33], s[3 * 33]); o.z = pk2(s[4 * 33], s[5 * 33]); o.w = pk2(s[6 * 33], s[7 * 33]);
;         *(GAS v4u*)(WT + (size_t)(drow0 + n) * K + k0 + 8 * c) = o; }
;     LDS_WAIT(); asm volatile("" ::: "memory");
	ds_read2_b32 v[50:51], v34 offset1:8
	ds_read2_b32 v[54:55], v34 offset0:33 offset1:41
	ds_read2_b32 v[56:57], v34 offset0:66 offset1:74
	ds_read2_b32 v[58:59], v34 offset0:99 offset1:107
	ds_read2_b32 v[60:61], v34 offset0:132 offset1:140
	s_waitcnt lgkmcnt(4)
	v_bfe_u32 v46, v50, 16, 1
	v_add3_u32 v46, v50, v46, s14
	s_waitcnt lgkmcnt(3)
	v_bfe_u32 v47, v54, 16, 1
	v_lshrrev_b32_e32 v46, 16, v46
	v_add3_u32 v47, v54, v47, s14
	ds_read2_b32 v[62:63], v34 offset0:165 offset1:173
	v_and_or_b32 v46, v47, s15, v46
	s_waitcnt lgkmcnt(3)
	v_bfe_u32 v47, v56, 16, 1
	v_add3_u32 v47, v56, v47, s14
	s_waitcnt lgkmcnt(2)
	v_bfe_u32 v48, v58, 16, 1
	ds_read2_b32 v[64:65], v34 offset0:198 offset1:206
	v_lshrrev_b32_e32 v47, 16, v47
	v_add3_u32 v48, v58, v48, s14
	ds_read2_b32 v[66:67], v34 offset0:231 offset1:239
	v_and_or_b32 v47, v48, s15, v47
	s_waitcnt lgkmcnt(3)
	v_bfe_u32 v48, v60, 16, 1
	v_add3_u32 v48, v60, v48, s14
	s_waitcnt lgkmcnt(2)
	v_bfe_u32 v49, v62, 16, 1
	v_lshrrev_b32_e32 v48, 16, v48
	v_add3_u32 v49, v62, v49, s14
	v_and_or_b32 v48, v49, s15, v48
	s_waitcnt lgkmcnt(1)
	v_bfe_u32 v49, v64, 16, 1
	v_add_u32_e32 v68, s6, v33
	s_lshl_b32 s4, s7, 7
	v_add3_u32 v49, v64, v49, s14
	s_waitcnt lgkmcnt(0)
	v_bfe_u32 v50, v66, 16, 1
	v_ashrrev_i32_e32 v69, 31, v68
	v_lshl_add_u64 v[52:53], v[12:13], 0, s[4:5]
	v_lshrrev_b32_e32 v49, 16, v49
	v_add3_u32 v50, v66, v50, s14
	v_lshlrev_b64 v[68:69], 11, v[68:69]
	v_and_or_b32 v49, v50, s15, v49
	v_lshl_add_u64 v[68:69], v[52:53], 0, v[68:69]
	global_store_dwordx4 v[68:69], v[46:49], off
	v_bfe_u32 v50, v67, 16, 1
	v_add3_u32 v50, v67, v50, s14
	v_bfe_u32 v46, v51, 16, 1
	v_add3_u32 v46, v51, v46, s14
	v_bfe_u32 v47, v55, 16, 1
	v_lshrrev_b32_e32 v46, 16, v46
	v_add3_u32 v47, v55, v47, s14
	v_and_or_b32 v46, v47, s15, v46
	v_bfe_u32 v47, v57, 16, 1
	v_add3_u32 v47, v57, v47, s14
	v_bfe_u32 v48, v59, 16, 1
	v_lshrrev_b32_e32 v47, 16, v47
	v_add3_u32 v48, v59, v48, s14
	v_and_or_b32 v47, v48, s15, v47
	v_bfe_u32 v48, v61, 16, 1
	v_add3_u32 v48, v61, v48, s14
	v_bfe_u32 v49, v63, 16, 1
	v_lshrrev_b32_e32 v48, 16, v48
	v_add3_u32 v49, v63, v49, s14
	v_and_or_b32 v48, v49, s15, v48
	v_bfe_u32 v49, v65, 16, 1
	v_add3_u32 v49, v65, v49, s14
	v_lshrrev_b32_e32 v49, 16, v49
	v_and_or_b32 v49, v50, s15, v49
	v_add_u32_e32 v50, s6, v35
	v_ashrrev_i32_e32 v51, 31, v50
	v_lshlrev_b64 v[50:51], 11, v[50:51]
	ds_read2_b32 v[54:55], v34 offset0:16 offset1:24
	v_lshl_add_u64 v[50:51], v[52:53], 0, v[50:51]
	global_store_dwordx4 v[50:51], v[46:49], off
	ds_read2_b32 v[50:51], v34 offset0:49 offset1:57
	ds_read2_b32 v[56:57], v34 offset0:82 offset1:90
	ds_read2_b32 v[58:59], v34 offset0:115 offset1:123
	s_waitcnt lgkmcnt(3)
	v_bfe_u32 v46, v54, 16, 1
	v_add3_u32 v46, v54, v46, s14
	s_waitcnt lgkmcnt(2)
	v_bfe_u32 v47, v50, 16, 1
	ds_read2_b32 v[60:61], v34 offset0:148 offset1:156
	v_lshrrev_b32_e32 v46, 16, v46
	v_add3_u32 v47, v50, v47, s14
	ds_read2_b32 v[62:63], v34 offset0:181 offset1:189
	v_and_or_b32 v46, v47, s15, v46
	s_waitcnt lgkmcnt(3)
	v_bfe_u32 v47, v56, 16, 1
	v_add3_u32 v47, v56, v47, s14
	s_waitcnt lgkmcnt(2)
	v_bfe_u32 v48, v58, 16, 1
	ds_read2_b32 v[64:65], v34 offset0:214 offset1:222
	v_lshrrev_b32_e32 v47, 16, v47
	v_add3_u32 v48, v58, v48, s14
	ds_read2_b32 v[66:67], v34 offset0:247 offset1:255
	v_and_or_b32 v47, v48, s15, v47
	s_waitcnt lgkmcnt(3)
	v_bfe_u32 v48, v60, 16, 1
	v_add3_u32 v48, v60, v48, s14
	s_waitcnt lgkmcnt(2)
	v_bfe_u32 v49, v62, 16, 1
	v_lshrrev_b32_e32 v48, 16, v48
	v_add3_u32 v49, v62, v49, s14
	v_and_or_b32 v48, v49, s15, v48
	s_waitcnt lgkmcnt(1)
	v_bfe_u32 v49, v64, 16, 1
	v_add_u32_e32 v68, s6, v36
	v_add3_u32 v49, v64, v49, s14
	s_waitcnt lgkmcnt(0)
	v_bfe_u32 v50, v66, 16, 1
	v_ashrrev_i32_e32 v69, 31, v68
	v_lshrrev_b32_e32 v49, 16, v49
	v_add3_u32 v50, v66, v50, s14
	v_lshlrev_b64 v[68:69], 11, v[68:69]
	v_and_or_b32 v49, v50, s15, v49
	v_lshl_add_u64 v[68:69], v[52:53], 0, v[68:69]
	global_store_dwordx4 v[68:69], v[46:49], off
	v_bfe_u32 v50, v67, 16, 1
	v_add3_u32 v50, v67, v50, s14
	v_bfe_u32 v46, v55, 16, 1
	v_add3_u32 v46, v55, v46, s14
	v_bfe_u32 v47, v51, 16, 1
	v_lshrrev_b32_e32 v46, 16, v46
	v_add3_u32 v47, v51, v47, s14
	v_and_or_b32 v46, v47, s15, v46
	v_bfe_u32 v47, v57, 16, 1
	v_add3_u32 v47, v57, v47, s14
	v_bfe_u32 v48, v59, 16, 1
	v_lshrrev_b32_e32 v47, 16, v47
	v_add3_u32 v48, v59, v48, s14
	v_and_or_b32 v47, v48, s15, v47
	v_bfe_u32 v48, v61, 16, 1
	v_add3_u32 v48, v61, v48, s14
	v_bfe_u32 v49, v63, 16, 1
	v_lshrrev_b32_e32 v48, 16, v48
	v_add3_u32 v49, v63, v49, s14
	v_and_or_b32 v48, v49, s15, v48
	v_bfe_u32 v49, v65, 16, 1
	v_add3_u32 v49, v65, v49, s14
	v_lshrrev_b32_e32 v49, 16, v49
	v_and_or_b32 v49, v50, s15, v49
	v_add_u32_e32 v50, s6, v37
	v_ashrrev_i32_e32 v51, 31, v50
	v_lshlrev_b64 v[50:51], 11, v[50:51]
	v_lshl_add_u64 v[50:51], v[52:53], 0, v[50:51]
	global_store_dwordx4 v[50:51], v[46:49], off
	s_waitcnt lgkmcnt(0)

; __device__ __forceinline__ void tr_item(const float* W, int ld, int K, int nblk, int item, bf16* WT, bool gu, LAS float* scr, int lane) {
;     const int kb = item / nblk, nb = item % nblk, k0 = 64 * kb, n0 = 32 * nb;
;     int drow0 = n0;
;     if (gu) { const int bj = n0 / FF, j = n0 - bj * FF; drow0 = 256 * (j / 128) + 128 * bj + (j % 128); }
;     { float t_[32];
; #pragma unroll
;       for (int i = 0; i < 32; ++i) t_[i] = W[(size_t)(k0 + 2 * i + (lane >> 5)) * ld + n0 + (lane & 31)];
; #pragma unroll
;       for (int i = 0; i < 32; ++i) scr[(2 * i + (lane >> 5)) * 33 + (lane & 31)] = t_[i]; }
; __device__ __forceinline__ void convert_items(Frame& F, const Args& a, int lo, int hi, int w, int nw) {
;     ...
;         if (r < I_FO) { tr_item(a.in[9], D, D, 32, r, (bf16*)(F.ws + WS_WFOXOUT), false, scr, lane); continue; } r -= I_FO;
.LBB0_1180:
	s_andn2_b64 vcc, exec, s[6:7]
	s_cbranch_vccnz .LBB0_1182
	s_add_i32 s4, s11, 0x2a00
	s_and_b32 s7, s4, 0x1ffc0
	s_and_b32 s6, s10, 0x3e0
	v_add_u32_e32 v46, s7, v28
	s_lshl_b32 s4, s6, 2
	v_ashrrev_i32_e32 v47, 31, v46
	v_lshl_add_u64 v[48:49], v[14:15], 0, s[4:5]
	v_lshlrev_b64 v[46:47], 12, v[46:47]
	v_lshl_add_u64 v[46:47], v[48:49], 0, v[46:47]
	v_add_co_u32_e32 v48, vcc, 0x2000, v46
	s_lshl_b32 s4, s7, 1
	s_nop 0
	v_addc_co_u32_e32 v49, vcc, 0, v47, vcc
	v_add_co_u32_e32 v50, vcc, 0x4000, v46
	s_nop 1
	v_addc_co_u32_e32 v51, vcc, 0, v47, vcc
	v_add_co_u32_e32 v52, vcc, 0x6000, v46
	s_nop 1
	v_addc_co_u32_e32 v53, vcc, 0, v47, vcc
	v_add_co_u32_e32 v54, vcc, 0x8000, v46
	s_nop 1
	v_addc_co_u32_e32 v55, vcc, 0, v47, vcc
	v_add_co_u32_e32 v56, vcc, 0xa000, v46
	s_nop 1
	v_addc_co_u32_e32 v57, vcc, 0, v47, vcc
	v_add_co_u32_e32 v58, vcc, 0xc000, v46
	s_nop 1
	v_addc_co_u32_e32 v59, vcc, 0, v47, vcc
	v_add_co_u32_e32 v60, vcc, 0xe000, v46
	s_nop 1
	v_addc_co_u32_e32 v61, vcc, 0, v47, vcc
	global_load_dword v64, v[46:47], off nt
	global_load_dword v65, v[48:49], off nt
	global_load_dword v66, v[50:51], off nt
	global_load_dword v67, v[52:53], off nt
	global_load_dword v68, v[54:55], off nt
	global_load_dword v69, v[56:57], off nt
	global_load_dword v70, v[58:59], off nt
	global_load_dword v71, v[60:61], off nt
	v_add_co_u32_e32 v48, vcc, 0x10000, v46
	s_nop 1
	v_addc_co_u32_e32 v49, vcc, 0, v47, vcc
	v_add_co_u32_e32 v50, vcc, 0x12000, v46
	s_nop 1
	v_addc_co_u32_e32 v51, vcc, 0, v47, vcc
	v_add_co_u32_e32 v52, vcc, 0x14000, v46
	s_nop 1
	v_addc_co_u32_e32 v53, vcc, 0, v47, vcc
	v_add_co_u32_e32 v54, vcc, 0x16000, v46
	s_nop 1
	v_addc_co_u32_e32 v55, vcc, 0, v47, vcc
	v_add_co_u32_e32 v56, vcc, 0x18000, v46
	s_nop 1
	v_addc_co_u32_e32 v57, vcc, 0, v47, vcc
	v_add_co_u32_e32 v58, vcc, 0x1a000, v46
	s_nop 1
	v_addc_co_u32_e32 v59, vcc, 0, v47, vcc
	v_add_co_u32_e32 v60, vcc, 0x1c000, v46
	s_nop 1
	v_addc_co_u32_e32 v61, vcc, 0, v47, vcc
	v_add_co_u32_e32 v62, vcc, 0x1e000, v46
	s_nop 1
	v_addc_co_u32_e32 v63, vcc, 0, v47, vcc
	global_load_dword v72, v[48:49], off nt
	global_load_dword v73, v[50:51], off nt
	global_load_dword v74, v[52:53], off nt
	global_load_dword v75, v[54:55], off nt
	global_load_dword v76, v[56:57], off nt
	global_load_dword v77, v[58:59], off nt
	global_load_dword v78, v[60:61], off nt
	global_load_dword v79, v[62:63], off nt
	v_add_co_u32_e32 v48, vcc, 0x20000, v46
	s_nop 1
	v_addc_co_u32_e32 v49, vcc, 0, v47, vcc
	v_add_co_u32_e32 v50, vcc, 0x22000, v46
	s_nop 1
	v_addc_co_u32_e32 v51, vcc, 0, v47, vcc
	v_add_co_u32_e32 v52, vcc, 0x24000, v46
	s_nop 1
	v_addc_co_u32_e32 v53, vcc, 0, v47, vcc
	v_add_co_u32_e32 v54, vcc, 0x26000, v46
	s_nop 1
	v_addc_co_u32_e32 v55, vcc, 0, v47, vcc
	v_add_co_u32_e32 v56, vcc, 0x28000, v46
	s_nop 1
	v_addc_co_u32_e32 v57, vcc, 0, v47, vcc
	v_add_co_u32_e32 v58, vcc, 0x2a000, v46
	s_nop 1
	v_addc_co_u32_e32 v59, vcc, 0, v47, vcc
	v_add_co_u32_e32 v60, vcc, 0x2c000, v46
	s_nop 1
	v_addc_co_u32_e32 v61, vcc, 0, v47, vcc
	v_add_co_u32_e32 v62, vcc, 0x2e000, v46
	s_nop 1
	v_addc_co_u32_e32 v63, vcc, 0, v47, vcc
	global_load_dword v80, v[48:49], off nt
	global_load_dword v81, v[50:51], off nt
	global_load_dword v82, v[52:53], off nt
	global_load_dword v83, v[54:55], off nt
	global_load_dword v84, v[56:57], off nt
	global_load_dword v85, v[58:59], off nt
	global_load_dword v86, v[60:61], off nt
	s_nop 0
	global_load_dword v62, v[62:63], off nt
	v_add_co_u32_e32 v48, vcc, 0x30000, v46
	s_nop 1
	v_addc_co_u32_e32 v49, vcc, 0, v47, vcc
	v_add_co_u32_e32 v50, vcc, 0x32000, v46
	s_nop 1
	v_addc_co_u32_e32 v51, vcc, 0, v47, vcc
	v_add_co_u32_e32 v52, vcc, 0x34000, v46
	s_nop 1
	v_addc_co_u32_e32 v53, vcc, 0, v47, vcc
	v_add_co_u32_e32 v54, vcc, 0x36000, v46
	s_nop 1
	v_addc_co_u32_e32 v55, vcc, 0, v47, vcc
	v_add_co_u32_e32 v56, vcc, 0x38000, v46
	s_nop 1
	v_addc_co_u32_e32 v57, vcc, 0, v47, vcc
	v_add_co_u32_e32 v58, vcc, 0x3a000, v46
	s_nop 1
	v_addc_co_u32_e32 v59, vcc, 0, v47, vcc
	v_add_co_u32_e32 v60, vcc, 0x3c000, v46
	s_nop 1
	v_addc_co_u32_e32 v61, vcc, 0, v47, vcc
	v_add_co_u32_e32 v46, vcc, 0x3e000, v46
	s_nop 1
	v_addc_co_u32_e32 v47, vcc, 0, v47, vcc
	global_load_dword v48, v[48:49], off nt
	s_nop 0
	global_load_dword v49, v[50:51], off nt
	s_nop 0
	global_load_dword v50, v[52:53], off nt
	global_load_dword v51, v[54:55], off nt
	s_nop 0
	global_load_dword v52, v[56:57], off nt
	global_load_dword v53, v[58:59], off nt
	global_load_dword v54, v[60:61], off nt
	s_nop 0
	global_load_dword v46, v[46:47], off nt
	s_waitcnt vmcnt(0)
	ds_write2_b32 v29, v64, v65 offset1:66
	ds_write2_b32 v29, v66, v67 offset0:132 offset1:198
	ds_write2_b32 v38, v68, v69 offset0:8 offset1:74
	ds_write2_b32 v38, v70, v71 offset0:140 offset1:206
	ds_write2_b32 v39, v72, v73 offset0:16 offset1:82
	ds_write2_b32 v39, v74, v75 offset0:148 offset1:214
	ds_write2_b32 v40, v76, v77 offset0:24 offset1:90
	ds_write2_b32 v40, v78, v79 offset0:156 offset1:222
	ds_write2_b32 v41, v80, v81 offset0:32 offset1:98
	ds_write2_b32 v41, v82, v83 offset0:164 offset1:230
	ds_write2_b32 v42, v84, v85 offset0:40 offset1:106
	ds_write2_b32 v42, v86, v62 offset0:172 offset1:238
	ds_write2_b32 v43, v48, v49 offset0:48 offset1:114
	ds_write2_b32 v43, v50, v51 offset0:180 offset1:246
	ds_write2_b32 v44, v52, v53 offset0:56 offset1:122
	ds_write2_b32 v44, v54, v46 offset0:188 offset1:254
	s_waitcnt lgkmcnt(0)
; #define GAS __attribute__((address_space(1)))
; #define LAS __attribute__((address_space(3)))
; #define LDS_WAIT() asm volatile("s_waitcnt lgkmcnt(0)" ::: "memory")
; __device__ __forceinline__ unsigned pk2(float lo, float hi) { return f2bf(lo) | (f2bf(hi) << 16); }
; __device__ __forceinline__ void tr_item(const float* W, int ld, int K, int nblk, int item, bf16* WT, bool gu, LAS float* scr, int lane) {
;     ...
;       for (int i = 0; i < 32; ++i) scr[(2 * i + (lane >> 5)) * 33 + (lane & 31)] = t_[i]; }
;     LDS_WAIT(); asm volatile("" ::: "memory");
;     const int c = lane & 7;
; #pragma unroll
;     for (int j = 0; j < 4; ++j) { const int n = (lane >> 3) + 8 * j; const LAS float* s = scr + (8 * c) * 33 + n;
;         v4u o; o.x = pk2(s[0 * 33], s[1 * 33]); o.y = pk2(s[2 * 33], s[3 * 33]); o.z = pk2(s[4 * 33], s[5 * 33]); o.w = pk2(s[6 * 33], s[7 * 33]);
;         *(GAS v4u*)(WT + (size_t)(drow0 + n) * K + k0 + 8 * c) = o; }
;     LDS_WAIT(); asm volatile("" ::: "memory");
	ds_read2_b32 v[50:51], v34 offset1:8
	ds_read2_b32 v[54:55], v34 offset0:33 offset1:41
	ds_read2_b32 v[56:57], v34 offset0:66 offset1:74
	ds_read2_b32 v[58:59], v34 offset0:99 offset1:107
	ds_read2_b32 v[60:61], v34 offset0:132 offset1:140
	s_waitcnt lgkmcnt(4)
	v_bfe_u32 v46, v50, 16, 1
	v_add3_u32 v46, v50, v46, s14
	s_waitcnt lgkmcnt(3)
	v_bfe_u32 v47, v54, 16, 1
	v_lshrrev_b32_e32 v46, 16, v46
	v_add3_u32 v47, v54, v47, s14
	ds_read2_b32 v[62:63], v34 offset0:165 offset1:173
	v_and_or_b32 v46, v47, s15, v46
	s_waitcnt lgkmcnt(3)
	v_bfe_u32 v47, v56, 16, 1
	v_add3_u32 v47, v56, v47, s14
	s_waitcnt lgkmcnt(2)
	v_bfe_u32 v48, v58, 16, 1
	ds_read2_b32 v[64:65], v34 offset0:198 offset1:206
	v_lshrrev_b32_e32 v47, 16, v47
	v_add3_u32 v48, v58, v48, s14
	ds_read2_b32 v[66:67], v34 offset0:231 offset1:239
	v_and_or_b32 v47, v48, s15, v47
	s_waitcnt lgkmcnt(3)
	v_bfe_u32 v48, v60, 16, 1
	v_add3_u32 v48, v60, v48, s14
	s_waitcnt lgkmcnt(2)
	v_bfe_u32 v49, v62, 16, 1
	v_lshrrev_b32_e32 v48, 16, v48
	v_add3_u32 v49, v62, v49, s14
	v_and_or_b32 v48, v49, s15, v48
	s_waitcnt lgkmcnt(1)
	v_bfe_u32 v49, v64, 16, 1
	v_add_u32_e32 v68, s6, v33
	v_add3_u32 v49, v64, v49, s14
	s_waitcnt lgkmcnt(0)
	v_bfe_u32 v50, v66, 16, 1
	v_ashrrev_i32_e32 v69, 31, v68
	v_lshl_add_u64 v[52:53], v[24:25], 0, s[4:5]
	v_lshrrev_b32_e32 v49, 16, v49
	v_add3_u32 v50, v66, v50, s14
	v_lshlrev_b64 v[68:69], 11, v[68:69]
	v_and_or_b32 v49, v50, s15, v49
	v_lshl_add_u64 v[68:69], v[52:53], 0, v[68:69]
	global_store_dwordx4 v[68:69], v[46:49], off
	v_bfe_u32 v50, v67, 16, 1
	v_add3_u32 v50, v67, v50, s14
	v_bfe_u32 v46, v51, 16, 1
	v_add3_u32 v46, v51, v46, s14
	v_bfe_u32 v47, v55, 16, 1
	v_lshrrev_b32_e32 v46, 16, v46
	v_add3_u32 v47, v55, v47, s14
	v_and_or_b32 v46, v47, s15, v46
	v_bfe_u32 v47, v57, 16, 1
	v_add3_u32 v47, v57, v47, s14
	v_bfe_u32 v48, v59, 16, 1
	v_lshrrev_b32_e32 v47, 16, v47
	v_add3_u32 v48, v59, v48, s14
	v_and_or_b32 v47, v48, s15, v47
	v_bfe_u32 v48, v61, 16, 1
	v_add3_u32 v48, v61, v48, s14
	v_bfe_u32 v49, v63, 16, 1
	v_lshrrev_b32_e32 v48, 16, v48
	v_add3_u32 v49, v63, v49, s14
	v_and_or_b32 v48, v49, s15, v48
	v_bfe_u32 v49, v65, 16, 1
	v_add3_u32 v49, v65, v49, s14
	v_lshrrev_b32_e32 v49, 16, v49
	v_and_or_b32 v49, v50, s15, v49
	v_add_u32_e32 v50, s6, v35
	v_ashrrev_i32_e32 v51, 31, v50
	v_lshlrev_b64 v[50:51], 11, v[50:51]
	ds_read2_b32 v[54:55], v34 offset0:16 offset1:24
	v_lshl_add_u64 v[50:51], v[52:53], 0, v[50:51]
	global_store_dwordx4 v[50:51], v[46:49], off
	ds_read2_b32 v[50:51], v34 offset0:49 offset1:57
	ds_read2_b32 v[56:57], v34 offset0:82 offset1:90
	ds_read2_b32 v[58:59], v34 offset0:115 offset1:123
	s_waitcnt lgkmcnt(3)
	v_bfe_u32 v46, v54, 16, 1
	v_add3_u32 v46, v54, v46, s14
	s_waitcnt lgkmcnt(2)
	v_bfe_u32 v47, v50, 16, 1
	ds_read2_b32 v[60:61], v34 offset0:148 offset1:156
	v_lshrrev_b32_e32 v46, 16, v46
	v_add3_u32 v47, v50, v47, s14
	ds_read2_b32 v[62:63], v34 offset0:181 offset1:189
	v_and_or_b32 v46, v47, s15, v46
	s_waitcnt lgkmcnt(3)
	v_bfe_u32 v47, v56, 16, 1
	v_add3_u32 v47, v56, v47, s14
	s_waitcnt lgkmcnt(2)
	v_bfe_u32 v48, v58, 16, 1
	ds_read2_b32 v[64:65], v34 offset0:214 offset1:222
	v_lshrrev_b32_e32 v47, 16, v47
	v_add3_u32 v48, v58, v48, s14
	ds_read2_b32 v[66:67], v34 offset0:247 offset1:255
	v_and_or_b32 v47, v48, s15, v47
	s_waitcnt lgkmcnt(3)
	v_bfe_u32 v48, v60, 16, 1
	v_add3_u32 v48, v60, v48, s14
	s_waitcnt lgkmcnt(2)
	v_bfe_u32 v49, v62, 16, 1
	v_lshrrev_b32_e32 v48, 16, v48
	v_add3_u32 v49, v62, v49, s14
	v_and_or_b32 v48, v49, s15, v48
	s_waitcnt lgkmcnt(1)
	v_bfe_u32 v49, v64, 16, 1
	v_add_u32_e32 v68, s6, v36
	v_add3_u32 v49, v64, v49, s14
	s_waitcnt lgkmcnt(0)
	v_bfe_u32 v50, v66, 16, 1
	v_ashrrev_i32_e32 v69, 31, v68
	v_lshrrev_b32_e32 v49, 16, v49
	v_add3_u32 v50, v66, v50, s14
	v_lshlrev_b64 v[68:69], 11, v[68:69]
	v_and_or_b32 v49, v50, s15, v49
	v_lshl_add_u64 v[68:69], v[52:53], 0, v[68:69]
	global_store_dwordx4 v[68:69], v[46:49], off
	v_bfe_u32 v50, v67, 16, 1
	v_add3_u32 v50, v67, v50, s14
	v_bfe_u32 v46, v55, 16, 1
	v_add3_u32 v46, v55, v46, s14
	v_bfe_u32 v47, v51, 16, 1
	v_lshrrev_b32_e32 v46, 16, v46
	v_add3_u32 v47, v51, v47, s14
	v_and_or_b32 v46, v47, s15, v46
	v_bfe_u32 v47, v57, 16, 1
	v_add3_u32 v47, v57, v47, s14
	v_bfe_u32 v48, v59, 16, 1
	v_lshrrev_b32_e32 v47, 16, v47
	v_add3_u32 v48, v59, v48, s14
	v_and_or_b32 v47, v48, s15, v47
	v_bfe_u32 v48, v61, 16, 1
	v_add3_u32 v48, v61, v48, s14
	v_bfe_u32 v49, v63, 16, 1
	v_lshrrev_b32_e32 v48, 16, v48
	v_add3_u32 v49, v63, v49, s14
	v_and_or_b32 v48, v49, s15, v48
	v_bfe_u32 v49, v65, 16, 1
	v_add3_u32 v49, v65, v49, s14
	v_lshrrev_b32_e32 v49, 16, v49
	v_and_or_b32 v49, v50, s15, v49
	v_add_u32_e32 v50, s6, v37
	v_ashrrev_i32_e32 v51, 31, v50
	v_lshlrev_b64 v[50:51], 11, v[50:51]
	v_lshl_add_u64 v[50:51], v[52:53], 0, v[50:51]
	global_store_dwordx4 v[50:51], v[46:49], off
	s_waitcnt lgkmcnt(0)

; __device__ __forceinline__ void tr_item(const float* W, int ld, int K, int nblk, int item, bf16* WT, bool gu, LAS float* scr, int lane) {
;     const int kb = item / nblk, nb = item % nblk, k0 = 64 * kb, n0 = 32 * nb;
;     int drow0 = n0;
;     if (gu) { const int bj = n0 / FF, j = n0 - bj * FF; drow0 = 256 * (j / 128) + 128 * bj + (j % 128); }
;     { float t_[32];
; #pragma unroll
;       for (int i = 0; i < 32; ++i) t_[i] = W[(size_t)(k0 + 2 * i + (lane >> 5)) * ld + n0 + (lane & 31)];
; #pragma unroll
;       for (int i = 0; i < 32; ++i) scr[(2 * i + (lane >> 5)) * 33 + (lane & 31)] = t_[i]; }
; __device__ __forceinline__ void convert_items(Frame& F, const Args& a, int lo, int hi, int w, int nw) {
;     ...
;         if (r < I_FI) { tr_item(a.in[7], 3 * D + 16, D, 96, r, (bf16*)(F.ws + WS_WFOXIN), false, scr, lane); continue; } r -= I_FI;
.LBB0_1183:
	s_andn2_b64 vcc, exec, s[6:7]
	s_cbranch_vccnz .LBB0_1160
	s_mul_hi_i32 s4, s16, 0x2aaaaaab
	s_lshr_b32 s6, s4, 31
	s_ashr_i32 s4, s4, 4
	s_add_i32 s4, s4, s6
	s_lshl_b32 s8, s4, 6
	s_mulk_i32 s4, 0xf400
	s_add_i32 s6, s10, s4
	v_add_u32_e32 v64, s8, v28
	s_ashr_i32 s7, s6, 31
	v_lshl_add_u64 v[46:47], s[6:7], 2, v[16:17]
	v_add_u32_e32 v50, 2, v64
	v_add_u32_e32 v52, 4, v64
	v_add_u32_e32 v54, 6, v64
	v_add_u32_e32 v56, 8, v64
	v_add_u32_e32 v58, 10, v64
	v_add_u32_e32 v60, 12, v64
	v_add_u32_e32 v62, 14, v64
	v_mad_i64_i32 v[48:49], s[26:27], v64, s24, v[46:47]
	v_mad_i64_i32 v[50:51], s[26:27], v50, s24, v[46:47]
	v_mad_i64_i32 v[52:53], s[26:27], v52, s24, v[46:47]
	v_mad_i64_i32 v[54:55], s[26:27], v54, s24, v[46:47]
	v_mad_i64_i32 v[56:57], s[26:27], v56, s24, v[46:47]
	v_mad_i64_i32 v[58:59], s[26:27], v58, s24, v[46:47]
	v_mad_i64_i32 v[60:61], s[26:27], v60, s24, v[46:47]
	v_mad_i64_i32 v[62:63], s[26:27], v62, s24, v[46:47]
	global_load_dword v65, v[48:49], off nt
	global_load_dword v66, v[50:51], off nt
	global_load_dword v67, v[52:53], off nt
	global_load_dword v68, v[54:55], off nt
	global_load_dword v69, v[56:57], off nt
	global_load_dword v70, v[58:59], off nt
	global_load_dword v71, v[60:61], off nt
	global_load_dword v72, v[62:63], off nt
	v_add_u32_e32 v48, 16, v64
	v_add_u32_e32 v50, 18, v64
	v_add_u32_e32 v52, 20, v64
	v_add_u32_e32 v54, 22, v64
	v_add_u32_e32 v56, 24, v64
	v_add_u32_e32 v58, 26, v64
	v_add_u32_e32 v60, 28, v64
	v_add_u32_e32 v62, 30, v64
	v_mad_i64_i32 v[48:49], s[26:27], v48, s24, v[46:47]
	v_mad_i64_i32 v[50:51], s[26:27], v50, s24, v[46:47]
	v_mad_i64_i32 v[52:53], s[26:27], v52, s24, v[46:47]
	v_mad_i64_i32 v[54:55], s[26:27], v54, s24, v[46:47]
	v_mad_i64_i32 v[56:57], s[26:27], v56, s24, v[46:47]
	v_mad_i64_i32 v[58:59], s[26:27], v58, s24, v[46:47]
	v_mad_i64_i32 v[60:61], s[26:27], v60, s24, v[46:47]
	v_mad_i64_i32 v[62:63], s[26:27], v62, s24, v[46:47]
	global_load_dword v73, v[48:49], off nt
	global_load_dword v74, v[50:51], off nt
	global_load_dword v75, v[52:53], off nt
	global_load_dword v76, v[54:55], off nt
	global_load_dword v77, v[56:57], off nt
	global_load_dword v78, v[58:59], off nt
	global_load_dword v79, v[60:61], off nt
	global_load_dword v80, v[62:63], off nt
	v_add_u32_e32 v48, 32, v64
	v_add_u32_e32 v50, 34, v64
	v_add_u32_e32 v52, 36, v64
	v_add_u32_e32 v54, 38, v64
	v_add_u32_e32 v56, 40, v64
	v_add_u32_e32 v58, 42, v64
	v_add_u32_e32 v60, 44, v64
	v_add_u32_e32 v62, 46, v64
	v_mad_i64_i32 v[48:49], s[26:27], v48, s24, v[46:47]
	v_mad_i64_i32 v[50:51], s[26:27], v50, s24, v[46:47]
	v_mad_i64_i32 v[52:53], s[26:27], v52, s24, v[46:47]
	v_mad_i64_i32 v[54:55], s[26:27], v54, s24, v[46:47]
	v_mad_i64_i32 v[56:57], s[26:27], v56, s24, v[46:47]
	v_mad_i64_i32 v[58:59], s[26:27], v58, s24, v[46:47]
	v_mad_i64_i32 v[60:61], s[26:27], v60, s24, v[46:47]
	v_mad_i64_i32 v[62:63], s[26:27], v62, s24, v[46:47]
	global_load_dword v81, v[48:49], off nt
	global_load_dword v82, v[50:51], off nt
	global_load_dword v83, v[52:53], off nt
	global_load_dword v84, v[54:55], off nt
	global_load_dword v85, v[56:57], off nt
	global_load_dword v86, v[58:59], off nt
	global_load_dword v87, v[60:61], off nt
	s_nop 0
	global_load_dword v62, v[62:63], off nt
	v_add_u32_e32 v48, 48, v64
	v_add_u32_e32 v50, 50, v64
	v_add_u32_e32 v52, 52, v64
	v_add_u32_e32 v54, 54, v64
	v_add_u32_e32 v56, 56, v64
	v_add_u32_e32 v58, 58, v64
	v_add_u32_e32 v60, 60, v64
	v_add_u32_e32 v63, 62, v64
	v_mad_i64_i32 v[48:49], s[26:27], v48, s24, v[46:47]
	v_mad_i64_i32 v[50:51], s[26:27], v50, s24, v[46:47]
	v_mad_i64_i32 v[52:53], s[26:27], v52, s24, v[46:47]
	v_mad_i64_i32 v[54:55], s[26:27], v54, s24, v[46:47]
	v_mad_i64_i32 v[56:57], s[26:27], v56, s24, v[46:47]
	v_mad_i64_i32 v[58:59], s[26:27], v58, s24, v[46:47]
	v_mad_i64_i32 v[60:61], s[26:27], v60, s24, v[46:47]
	v_mad_i64_i32 v[46:47], s[26:27], v63, s24, v[46:47]
	global_load_dword v48, v[48:49], off nt
	s_nop 0
	global_load_dword v49, v[50:51], off nt
	s_nop 0
	global_load_dword v50, v[52:53], off nt
	global_load_dword v51, v[54:55], off nt
	s_nop 0
	global_load_dword v52, v[56:57], off nt
	global_load_dword v53, v[58:59], off nt
	global_load_dword v54, v[60:61], off nt
	s_nop 0
	global_load_dword v46, v[46:47], off nt
	s_waitcnt vmcnt(0)
	ds_write2_b32 v29, v65, v66 offset1:66
	ds_write2_b32 v29, v67, v68 offset0:132 offset1:198
	ds_write2_b32 v38, v69, v70 offset0:8 offset1:74
	ds_write2_b32 v38, v71, v72 offset0:140 offset1:206
	ds_write2_b32 v39, v73, v74 offset0:16 offset1:82
	ds_write2_b32 v39, v75, v76 offset0:148 offset1:214
	ds_write2_b32 v40, v77, v78 offset0:24 offset1:90
	ds_write2_b32 v40, v79, v80 offset0:156 offset1:222
	ds_write2_b32 v41, v81, v82 offset0:32 offset1:98
	ds_write2_b32 v41, v83, v84 offset0:164 offset1:230
	ds_write2_b32 v42, v85, v86 offset0:40 offset1:106
	ds_write2_b32 v42, v87, v62 offset0:172 offset1:238
	ds_write2_b32 v43, v48, v49 offset0:48 offset1:114
	ds_write2_b32 v43, v50, v51 offset0:180 offset1:246
	ds_write2_b32 v44, v52, v53 offset0:56 offset1:122
	ds_write2_b32 v44, v54, v46 offset0:188 offset1:254
	s_waitcnt lgkmcnt(0)
; #define GAS __attribute__((address_space(1)))
; #define LAS __attribute__((address_space(3)))
; #define LDS_WAIT() asm volatile("s_waitcnt lgkmcnt(0)" ::: "memory")
; __device__ __forceinline__ unsigned pk2(float lo, float hi) { return f2bf(lo) | (f2bf(hi) << 16); }
; __device__ __forceinline__ void tr_item(const float* W, int ld, int K, int nblk, int item, bf16* WT, bool gu, LAS float* scr, int lane) {
;     ...
;       for (int i = 0; i < 32; ++i) scr[(2 * i + (lane >> 5)) * 33 + (lane & 31)] = t_[i]; }
;     LDS_WAIT(); asm volatile("" ::: "memory");
;     const int c = lane & 7;
; #pragma unroll
;     for (int j = 0; j < 4; ++j) { const int n = (lane >> 3) + 8 * j; const LAS float* s = scr + (8 * c) * 33 + n;
;         v4u o; o.x = pk2(s[0 * 33], s[1 * 33]); o.y = pk2(s[2 * 33], s[3 * 33]); o.z = pk2(s[4 * 33], s[5 * 33]); o.w = pk2(s[6 * 33], s[7 * 33]);
;         *(GAS v4u*)(WT + (size_t)(drow0 + n) * K + k0 + 8 * c) = o; }
;     LDS_WAIT(); asm volatile("" ::: "memory");
	ds_read2_b32 v[50:51], v34 offset1:8
	ds_read2_b32 v[54:55], v34 offset0:33 offset1:41
	ds_read2_b32 v[56:57], v34 offset0:66 offset1:74
	ds_read2_b32 v[58:59], v34 offset0:99 offset1:107
	ds_read2_b32 v[60:61], v34 offset0:132 offset1:140
	s_waitcnt lgkmcnt(4)
	v_bfe_u32 v46, v50, 16, 1
	v_add3_u32 v46, v50, v46, s14
	s_waitcnt lgkmcnt(3)
	v_bfe_u32 v47, v54, 16, 1
	v_lshrrev_b32_e32 v46, 16, v46
	v_add3_u32 v47, v54, v47, s14
	ds_read2_b32 v[62:63], v34 offset0:165 offset1:173
	v_and_or_b32 v46, v47, s15, v46
	s_waitcnt lgkmcnt(3)
	v_bfe_u32 v47, v56, 16, 1
	v_add3_u32 v47, v56, v47, s14
	s_waitcnt lgkmcnt(2)
	v_bfe_u32 v48, v58, 16, 1
	ds_read2_b32 v[64:65], v34 offset0:198 offset1:206
	v_lshrrev_b32_e32 v47, 16, v47
	v_add3_u32 v48, v58, v48, s14
	ds_read2_b32 v[66:67], v34 offset0:231 offset1:239
	v_and_or_b32 v47, v48, s15, v47
	s_waitcnt lgkmcnt(3)
	v_bfe_u32 v48, v60, 16, 1
	v_add3_u32 v48, v60, v48, s14
	s_waitcnt lgkmcnt(2)
	v_bfe_u32 v49, v62, 16, 1
	v_lshrrev_b32_e32 v48, 16, v48
	v_add3_u32 v49, v62, v49, s14
	v_and_or_b32 v48, v49, s15, v48
	s_waitcnt lgkmcnt(1)
	v_bfe_u32 v49, v64, 16, 1
	v_add_u32_e32 v68, s6, v33
	s_ashr_i32 s9, s8, 31
	v_add3_u32 v49, v64, v49, s14
	s_waitcnt lgkmcnt(0)
	v_bfe_u32 v50, v66, 16, 1
	v_ashrrev_i32_e32 v69, 31, v68
	v_lshl_add_u64 v[52:53], s[8:9], 1, v[26:27]
	v_lshrrev_b32_e32 v49, 16, v49
	v_add3_u32 v50, v66, v50, s14
	v_lshlrev_b64 v[70:71], 11, v[68:69]
	v_and_or_b32 v49, v50, s15, v49
	v_lshl_add_u64 v[70:71], v[52:53], 0, v[70:71]
	global_store_dwordx4 v[70:71], v[46:49], off
	v_bfe_u32 v50, v67, 16, 1
	v_add3_u32 v50, v67, v50, s14
	v_bfe_u32 v46, v51, 16, 1
	v_add3_u32 v46, v51, v46, s14
	v_bfe_u32 v47, v55, 16, 1
	v_lshrrev_b32_e32 v46, 16, v46
	v_add3_u32 v47, v55, v47, s14
	v_and_or_b32 v46, v47, s15, v46
	v_bfe_u32 v47, v57, 16, 1
	v_add3_u32 v47, v57, v47, s14
	v_bfe_u32 v48, v59, 16, 1
	v_lshrrev_b32_e32 v47, 16, v47
	v_add3_u32 v48, v59, v48, s14
	v_and_or_b32 v47, v48, s15, v47
	v_bfe_u32 v48, v61, 16, 1
	v_add3_u32 v48, v61, v48, s14
	v_bfe_u32 v49, v63, 16, 1
	v_lshrrev_b32_e32 v48, 16, v48
	v_add3_u32 v49, v63, v49, s14
	v_and_or_b32 v48, v49, s15, v48
	v_bfe_u32 v49, v65, 16, 1
	v_add3_u32 v49, v65, v49, s14
	v_lshrrev_b32_e32 v49, 16, v49
	v_and_or_b32 v49, v50, s15, v49
	v_add_u32_e32 v50, 8, v68
	v_ashrrev_i32_e32 v51, 31, v50
	v_lshlrev_b64 v[50:51], 11, v[50:51]
	ds_read2_b32 v[54:55], v34 offset0:16 offset1:24
	v_lshl_add_u64 v[50:51], v[52:53], 0, v[50:51]
	global_store_dwordx4 v[50:51], v[46:49], off
	ds_read2_b32 v[50:51], v34 offset0:49 offset1:57
	ds_read2_b32 v[56:57], v34 offset0:82 offset1:90
	ds_read2_b32 v[58:59], v34 offset0:115 offset1:123
	s_waitcnt lgkmcnt(3)
	v_bfe_u32 v46, v54, 16, 1
	v_add3_u32 v46, v54, v46, s14
	s_waitcnt lgkmcnt(2)
	v_bfe_u32 v47, v50, 16, 1
	ds_read2_b32 v[60:61], v34 offset0:148 offset1:156
	v_lshrrev_b32_e32 v46, 16, v46
	v_add3_u32 v47, v50, v47, s14
	ds_read2_b32 v[62:63], v34 offset0:181 offset1:189
	v_and_or_b32 v46, v47, s15, v46
	s_waitcnt lgkmcnt(3)
	v_bfe_u32 v47, v56, 16, 1
	v_add3_u32 v47, v56, v47, s14
	s_waitcnt lgkmcnt(2)
	v_bfe_u32 v48, v58, 16, 1
	ds_read2_b32 v[64:65], v34 offset0:214 offset1:222
	v_lshrrev_b32_e32 v47, 16, v47
	v_add3_u32 v48, v58, v48, s14
	ds_read2_b32 v[66:67], v34 offset0:247 offset1:255
	v_and_or_b32 v47, v48, s15, v47
	s_waitcnt lgkmcnt(3)
	v_bfe_u32 v48, v60, 16, 1
	v_add3_u32 v48, v60, v48, s14
	s_waitcnt lgkmcnt(2)
	v_bfe_u32 v49, v62, 16, 1
	v_lshrrev_b32_e32 v48, 16, v48
	v_add3_u32 v49, v62, v49, s14
	v_and_or_b32 v48, v49, s15, v48
	s_waitcnt lgkmcnt(1)
	v_bfe_u32 v49, v64, 16, 1
	v_add_u32_e32 v70, 16, v68
	v_add3_u32 v49, v64, v49, s14
	s_waitcnt lgkmcnt(0)
	v_bfe_u32 v50, v66, 16, 1
	v_ashrrev_i32_e32 v71, 31, v70
	v_lshrrev_b32_e32 v49, 16, v49
	v_add3_u32 v50, v66, v50, s14
	v_lshlrev_b64 v[70:71], 11, v[70:71]
	v_and_or_b32 v49, v50, s15, v49
	v_lshl_add_u64 v[70:71], v[52:53], 0, v[70:71]
	global_store_dwordx4 v[70:71], v[46:49], off
	v_bfe_u32 v50, v67, 16, 1
	v_add3_u32 v50, v67, v50, s14
	v_bfe_u32 v46, v55, 16, 1
	v_add3_u32 v46, v55, v46, s14
	v_bfe_u32 v47, v51, 16, 1
	v_lshrrev_b32_e32 v46, 16, v46
	v_add3_u32 v47, v51, v47, s14
	v_and_or_b32 v46, v47, s15, v46
	v_bfe_u32 v47, v57, 16, 1
	v_add3_u32 v47, v57, v47, s14
	v_bfe_u32 v48, v59, 16, 1
	v_lshrrev_b32_e32 v47, 16, v47
	v_add3_u32 v48, v59, v48, s14
	v_and_or_b32 v47, v48, s15, v47
	v_bfe_u32 v48, v61, 16, 1
	v_add3_u32 v48, v61, v48, s14
	v_bfe_u32 v49, v63, 16, 1
	v_lshrrev_b32_e32 v48, 16, v48
	v_add3_u32 v49, v63, v49, s14
	v_and_or_b32 v48, v49, s15, v48
	v_bfe_u32 v49, v65, 16, 1
	v_add3_u32 v49, v65, v49, s14
	v_lshrrev_b32_e32 v49, 16, v49
	v_and_or_b32 v49, v50, s15, v49
	v_add_u32_e32 v50, 24, v68
	v_ashrrev_i32_e32 v51, 31, v50
	v_lshlrev_b64 v[50:51], 11, v[50:51]
	v_lshl_add_u64 v[50:51], v[52:53], 0, v[50:51]
	global_store_dwordx4 v[50:51], v[46:49], off
	s_waitcnt lgkmcnt(0)
	s_branch .LBB0_1160

; __device__ __forceinline__ void tr_item8(const float* W, int ld, int K, int nblk, int item, unsigned char* WT, bool gu, float scale, LAS float* scr, int lane) {
;     const int kb = item / nblk, nb = item % nblk, k0 = 64 * kb, n0 = 32 * nb;
;     int drow0 = n0;
;     if (gu) { const int bj = n0 / FF, j = n0 - bj * FF; drow0 = 256 * (j / 128) + 128 * bj + (j % 128); }
;     { float t_[32];
; #pragma unroll
;       for (int i = 0; i < 32; ++i) t_[i] = W[(size_t)(k0 + 2 * i + (lane >> 5)) * ld + n0 + (lane & 31)];
; #pragma unroll
;       for (int i = 0; i < 32; ++i) scr[(2 * i + (lane >> 5)) * 33 + (lane & 31)] = t_[i] * scale; }
; __device__ __forceinline__ void convert_items(Frame& F, const Args& a, int lo, int hi, int w, int nw) {
;     ...
;         { const int e = r / I_DN, rr = r % I_DN; tr_item8(a.in[19] + (size_t)e * FF * D, D, FF, 32, rr, F.ws + WS_WMDN + (size_t)e * D * FF, false, WSC_DN, scr, lane); }
.LBB0_1296:
	s_cmpk_gt_i32 s8, 0x5ff
	s_mov_b64 s[4:5], -1
	s_cbranch_scc0 .LBB0_1322
	s_cmpk_gt_u32 s8, 0x7ff
	s_cbranch_scc0 .LBB0_1319
	s_cmpk_gt_u32 s8, 0xaff
	s_cbranch_scc0 .LBB0_1316
	s_cmpk_gt_u32 s8, 0xcff
	s_cbranch_scc0 .LBB0_1313
	s_cmpk_gt_u32 s8, 0x1aff
	s_cbranch_scc0 .LBB0_1310
	s_cmpk_gt_u32 s8, 0x21ff
	s_cbranch_scc0 .LBB0_1307
	s_cmpk_gt_u32 s8, 0x91ff
	s_cbranch_scc0 .LBB0_1304
	s_add_i32 s0, s8, 0x6e00
	s_bfe_u32 s4, s0, 0x80008
	s_mulk_i32 s4, 0x2493
	s_lshr_b32 s4, s4, 16
	s_mul_i32 s5, s4, 0x700
	v_readlane_b32 s40, v254, 28
	s_sub_i32 s6, s0, s5
	s_mul_i32 s0, s4, 0xe00000
	v_readlane_b32 s46, v254, 34
	v_readlane_b32 s47, v254, 35
	s_add_u32 s7, s46, s0
	s_addc_u32 s31, s47, 0
	s_mul_i32 s4, s4, 0x380000
	s_add_u32 s4, s66, s4
	s_addc_u32 s5, s58, 0
	s_lshl_b32 s0, s6, 5
	s_and_b32 s0, s0, 0x3e0
	s_lshl_b32 s6, s6, 1
	s_and_b32 s6, s6, 0xfc0
	s_lshl_b32 s40, s0, 2
	v_readlane_b32 s41, v254, 29
	v_add_u32_e32 v28, s6, v30
	s_add_u32 s40, s7, s40
	s_addc_u32 s41, s31, 0
	v_ashrrev_i32_e32 v29, 31, v28
	v_lshl_add_u64 v[48:49], s[40:41], 0, v[0:1]
	v_lshlrev_b64 v[28:29], 12, v[28:29]
	v_lshl_add_u64 v[28:29], v[48:49], 0, v[28:29]
	s_movk_i32 s7, 0x2000
	v_add_co_u32_e32 v48, vcc, s7, v28
	s_movk_i32 s7, 0x4000
	s_nop 0
	v_addc_co_u32_e32 v49, vcc, 0, v29, vcc
	global_load_dword v50, v[28:29], off nt
	global_load_dword v51, v[48:49], off nt
	v_add_co_u32_e32 v48, vcc, s7, v28
	s_movk_i32 s7, 0x6000
	s_nop 0
	v_addc_co_u32_e32 v49, vcc, 0, v29, vcc
	global_load_dword v52, v[48:49], off nt
	v_add_co_u32_e32 v48, vcc, s7, v28
	s_mov_b32 s7, 0x8000
	s_nop 0
	v_addc_co_u32_e32 v49, vcc, 0, v29, vcc
	global_load_dword v53, v[48:49], off nt
	v_add_co_u32_e32 v48, vcc, s7, v28
	s_mov_b32 s7, 0xa000
	s_nop 0
	v_addc_co_u32_e32 v49, vcc, 0, v29, vcc
	global_load_dword v54, v[48:49], off nt
	v_add_co_u32_e32 v48, vcc, s7, v28
	s_mov_b32 s7, 0xc000
	s_nop 0
	v_addc_co_u32_e32 v49, vcc, 0, v29, vcc
	global_load_dword v55, v[48:49], off nt
	v_add_co_u32_e32 v48, vcc, s7, v28
	s_mov_b32 s7, 0xe000
	s_nop 0
	v_addc_co_u32_e32 v49, vcc, 0, v29, vcc
	global_load_dword v56, v[48:49], off nt
	v_add_co_u32_e32 v48, vcc, s7, v28
	s_mov_b32 s7, 0x10000
	s_nop 0
	v_addc_co_u32_e32 v49, vcc, 0, v29, vcc
	global_load_dword v57, v[48:49], off nt
	v_add_co_u32_e32 v48, vcc, s7, v28
	s_mov_b32 s7, 0x12000
	s_nop 0
	v_addc_co_u32_e32 v49, vcc, 0, v29, vcc
	global_load_dword v58, v[48:49], off nt
	v_add_co_u32_e32 v48, vcc, s7, v28
	s_mov_b32 s7, 0x14000
	s_nop 0
	v_addc_co_u32_e32 v49, vcc, 0, v29, vcc
	global_load_dword v59, v[48:49], off nt
	v_add_co_u32_e32 v48, vcc, s7, v28
	s_mov_b32 s7, 0x16000
	s_nop 0
	v_addc_co_u32_e32 v49, vcc, 0, v29, vcc
	global_load_dword v60, v[48:49], off nt
	v_add_co_u32_e32 v48, vcc, s7, v28
	s_mov_b32 s7, 0x18000
	s_nop 0
	v_addc_co_u32_e32 v49, vcc, 0, v29, vcc
	global_load_dword v61, v[48:49], off nt
	v_add_co_u32_e32 v48, vcc, s7, v28
	s_mov_b32 s7, 0x1a000
	s_nop 0
	v_addc_co_u32_e32 v49, vcc, 0, v29, vcc
	global_load_dword v62, v[48:49], off nt
	v_add_co_u32_e32 v48, vcc, s7, v28
	s_mov_b32 s7, 0x1c000
	s_nop 0
	v_addc_co_u32_e32 v49, vcc, 0, v29, vcc
	global_load_dword v63, v[48:49], off nt
	v_add_co_u32_e32 v48, vcc, s7, v28
	s_mov_b32 s7, 0x1e000
	s_nop 0
	v_addc_co_u32_e32 v49, vcc, 0, v29, vcc
	global_load_dword v64, v[48:49], off nt
	v_add_co_u32_e32 v48, vcc, s7, v28
	s_mov_b32 s7, 0x20000
	s_nop 0
	v_addc_co_u32_e32 v49, vcc, 0, v29, vcc
	global_load_dword v65, v[48:49], off nt
	v_add_co_u32_e32 v48, vcc, s7, v28
	s_mov_b32 s7, 0x22000
	s_nop 0
	v_addc_co_u32_e32 v49, vcc, 0, v29, vcc
	global_load_dword v66, v[48:49], off nt
	v_add_co_u32_e32 v48, vcc, s7, v28
	s_mov_b32 s7, 0x24000
	s_nop 0
	v_addc_co_u32_e32 v49, vcc, 0, v29, vcc
	global_load_dword v67, v[48:49], off nt
	v_add_co_u32_e32 v48, vcc, s7, v28
	s_mov_b32 s7, 0x26000
	s_nop 0
	v_addc_co_u32_e32 v49, vcc, 0, v29, vcc
	global_load_dword v68, v[48:49], off nt
	v_add_co_u32_e32 v48, vcc, s7, v28
	s_mov_b32 s7, 0x28000
	s_nop 0
	v_addc_co_u32_e32 v49, vcc, 0, v29, vcc
	global_load_dword v69, v[48:49], off nt
	v_add_co_u32_e32 v48, vcc, s7, v28
	s_mov_b32 s7, 0x2a000
	s_nop 0
	v_addc_co_u32_e32 v49, vcc, 0, v29, vcc
	global_load_dword v70, v[48:49], off nt
	v_add_co_u32_e32 v48, vcc, s7, v28
	s_mov_b32 s7, 0x2c000
	s_nop 0
	v_addc_co_u32_e32 v49, vcc, 0, v29, vcc
	global_load_dword v71, v[48:49], off nt
	v_add_co_u32_e32 v48, vcc, s7, v28
	s_mov_b32 s7, 0x2e000
	s_nop 0
	v_addc_co_u32_e32 v49, vcc, 0, v29, vcc
	global_load_dword v72, v[48:49], off nt
	v_add_co_u32_e32 v48, vcc, s7, v28
	s_mov_b32 s7, 0x30000
	s_nop 0
	v_addc_co_u32_e32 v49, vcc, 0, v29, vcc
	global_load_dword v73, v[48:49], off nt
	v_add_co_u32_e32 v48, vcc, s7, v28
	s_mov_b32 s7, 0x32000
	s_nop 0
	v_addc_co_u32_e32 v49, vcc, 0, v29, vcc
	global_load_dword v74, v[48:49], off nt
	v_add_co_u32_e32 v48, vcc, s7, v28
	s_mov_b32 s7, 0x34000
	s_nop 0
	v_addc_co_u32_e32 v49, vcc, 0, v29, vcc
	global_load_dword v75, v[48:49], off nt
	v_add_co_u32_e32 v48, vcc, s7, v28
	s_mov_b32 s7, 0x36000
	s_nop 0
	v_addc_co_u32_e32 v49, vcc, 0, v29, vcc
	global_load_dword v76, v[48:49], off nt
	v_add_co_u32_e32 v48, vcc, s7, v28
	s_mov_b32 s7, 0x38000
	s_nop 0
	v_addc_co_u32_e32 v49, vcc, 0, v29, vcc
	global_load_dword v77, v[48:49], off nt
	v_add_co_u32_e32 v48, vcc, s7, v28
	s_mov_b32 s7, 0x3a000
	s_nop 0
	v_addc_co_u32_e32 v49, vcc, 0, v29, vcc
	global_load_dword v78, v[48:49], off nt
	v_add_co_u32_e32 v48, vcc, s7, v28
	s_mov_b32 s7, 0x3c000
	s_nop 0
	v_addc_co_u32_e32 v49, vcc, 0, v29, vcc
	global_load_dword v79, v[48:49], off nt
	v_add_co_u32_e32 v48, vcc, s7, v28
	s_mov_b32 s7, 0x3e000
	s_nop 0
	v_addc_co_u32_e32 v49, vcc, 0, v29, vcc
	v_add_co_u32_e32 v28, vcc, s7, v28
	global_load_dword v48, v[48:49], off nt
	s_nop 0
	v_addc_co_u32_e32 v29, vcc, 0, v29, vcc
	global_load_dword v28, v[28:29], off nt
	s_waitcnt vmcnt(31)
; __device__ __forceinline__ unsigned cvt_pk4_fp8(float a, float b, float c, float d) { int w = 0; w = __builtin_amdgcn_cvt_pk_fp8_f32(a, b, w, false); w = __builtin_amdgcn_cvt_pk_fp8_f32(c, d, w, true); return (unsigned)w; }
; #define GAS __attribute__((address_space(1)))
; #define LAS __attribute__((address_space(3)))
; #define LDS_WAIT() asm volatile("s_waitcnt lgkmcnt(0)" ::: "memory")
; __device__ __forceinline__ void tr_item8(const float* W, int ld, int K, int nblk, int item, unsigned char* WT, bool gu, float scale, LAS float* scr, int lane) {
;     ...
;       for (int i = 0; i < 32; ++i) scr[(2 * i + (lane >> 5)) * 33 + (lane & 31)] = t_[i] * scale; }
;     LDS_WAIT(); asm volatile("" ::: "memory");
;     const int c = lane & 3;
; #pragma unroll
;     for (int j = 0; j < 2; ++j) { const int n = (lane >> 2) + 16 * j; const LAS float* sp = scr + (16 * c) * 33 + n;
;         v4u o; o.x = pg8::cvt_pk4_fp8(sp[0 * 33], sp[1 * 33], sp[2 * 33], sp[3 * 33]); o.y = pg8::cvt_pk4_fp8(sp[4 * 33], sp[5 * 33], sp[6 * 33], sp[7 * 33]);
;         o.z = pg8::cvt_pk4_fp8(sp[8 * 33], sp[9 * 33], sp[10 * 33], sp[11 * 33]); o.w = pg8::cvt_pk4_fp8(sp[12 * 33], sp[13 * 33], sp[14 * 33], sp[15 * 33]);
;         *(GAS v4u*)(WT + (size_t)(drow0 + n) * K + k0 + 16 * c) = o; }
;     LDS_WAIT(); asm volatile("" ::: "memory");
	v_mul_f32_e32 v29, 0x43000000, v50
	s_waitcnt vmcnt(30)
	v_mul_f32_e32 v49, 0x43000000, v51
	ds_write2_b32 v31, v29, v49 offset1:66
	s_waitcnt vmcnt(29)
	v_mul_f32_e32 v29, 0x43000000, v52
	s_waitcnt vmcnt(28)
	v_mul_f32_e32 v49, 0x43000000, v53
	ds_write2_b32 v31, v29, v49 offset0:132 offset1:198
	s_waitcnt vmcnt(27)
	v_mul_f32_e32 v29, 0x43000000, v54
	s_waitcnt vmcnt(26)
	v_mul_f32_e32 v49, 0x43000000, v55
	ds_write2_b32 v40, v29, v49 offset0:8 offset1:74
	s_waitcnt vmcnt(25)
	v_mul_f32_e32 v29, 0x43000000, v56
	s_waitcnt vmcnt(24)
	v_mul_f32_e32 v49, 0x43000000, v57
	ds_write2_b32 v40, v29, v49 offset0:140 offset1:206
	s_waitcnt vmcnt(23)
	v_mul_f32_e32 v29, 0x43000000, v58
	s_waitcnt vmcnt(22)
	v_mul_f32_e32 v49, 0x43000000, v59
	ds_write2_b32 v41, v29, v49 offset0:16 offset1:82
	s_waitcnt vmcnt(21)
	v_mul_f32_e32 v29, 0x43000000, v60
	s_waitcnt vmcnt(20)
	v_mul_f32_e32 v49, 0x43000000, v61
	ds_write2_b32 v41, v29, v49 offset0:148 offset1:214
	s_waitcnt vmcnt(19)
	v_mul_f32_e32 v29, 0x43000000, v62
	s_waitcnt vmcnt(18)
	v_mul_f32_e32 v49, 0x43000000, v63
	ds_write2_b32 v42, v29, v49 offset0:24 offset1:90
	s_waitcnt vmcnt(17)
	v_mul_f32_e32 v29, 0x43000000, v64
	s_waitcnt vmcnt(16)
	v_mul_f32_e32 v49, 0x43000000, v65
	ds_write2_b32 v42, v29, v49 offset0:156 offset1:222
	s_waitcnt vmcnt(15)
	v_mul_f32_e32 v29, 0x43000000, v66
	s_waitcnt vmcnt(14)
	v_mul_f32_e32 v49, 0x43000000, v67
	ds_write2_b32 v43, v29, v49 offset0:32 offset1:98
	s_waitcnt vmcnt(13)
	v_mul_f32_e32 v29, 0x43000000, v68
	s_waitcnt vmcnt(12)
	v_mul_f32_e32 v49, 0x43000000, v69
	ds_write2_b32 v43, v29, v49 offset0:164 offset1:230
	s_waitcnt vmcnt(11)
	v_mul_f32_e32 v29, 0x43000000, v70
	s_waitcnt vmcnt(10)
	v_mul_f32_e32 v49, 0x43000000, v71
	ds_write2_b32 v44, v29, v49 offset0:40 offset1:106
	s_waitcnt vmcnt(9)
	v_mul_f32_e32 v29, 0x43000000, v72
	s_waitcnt vmcnt(8)
	v_mul_f32_e32 v49, 0x43000000, v73
	ds_write2_b32 v44, v29, v49 offset0:172 offset1:238
	v_mov_b32_e32 v50, v1
	v_mov_b32_e32 v51, v1
	s_waitcnt vmcnt(7)
	v_mul_f32_e32 v29, 0x43000000, v74
	s_add_u32 s4, s4, s6
	s_addc_u32 s5, s5, 0
	v_readlane_b32 s42, v254, 30
	v_readlane_b32 s43, v254, 31
	v_readlane_b32 s44, v254, 32
	s_waitcnt vmcnt(6)
	v_mul_f32_e32 v49, 0x43000000, v75
	ds_write2_b32 v45, v29, v49 offset0:48 offset1:114
	v_readlane_b32 s45, v254, 33
	s_waitcnt vmcnt(5)
	v_mul_f32_e32 v29, 0x43000000, v76
	s_waitcnt vmcnt(4)
	v_mul_f32_e32 v49, 0x43000000, v77
	ds_write2_b32 v45, v29, v49 offset0:180 offset1:246
	s_waitcnt vmcnt(3)
	v_mul_f32_e32 v29, 0x43000000, v78
	s_waitcnt vmcnt(2)
	v_mul_f32_e32 v49, 0x43000000, v79
	ds_write2_b32 v46, v29, v49 offset0:56 offset1:122
	v_mov_b32_e32 v49, v1
	s_waitcnt vmcnt(1)
	v_mul_f32_e32 v29, 0x43000000, v48
	v_mov_b32_e32 v48, v1
	s_waitcnt vmcnt(0)
	v_mul_f32_e32 v28, 0x43000000, v28
	ds_write2_b32 v46, v29, v28 offset0:188 offset1:254
	s_waitcnt lgkmcnt(0)
	ds_read2_b32 v[52:53], v33 offset1:16
	ds_read2_b32 v[54:55], v33 offset0:33 offset1:49
	ds_read2_b32 v[56:57], v33 offset0:66 offset1:82
	ds_read2_b32 v[58:59], v33 offset0:99 offset1:115
	ds_read2_b32 v[60:61], v33 offset0:132 offset1:148
	ds_read2_b32 v[62:63], v33 offset0:165 offset1:181
	ds_read2_b32 v[64:65], v33 offset0:198 offset1:214
	ds_read2_b32 v[66:67], v33 offset0:231 offset1:247
	ds_read2_b32 v[68:69], v47 offset0:8 offset1:24
	ds_read2_b32 v[70:71], v47 offset0:41 offset1:57
	ds_read2_b32 v[72:73], v47 offset0:74 offset1:90
	ds_read2_b32 v[74:75], v47 offset0:107 offset1:123
	ds_read2_b32 v[76:77], v47 offset0:140 offset1:156
	ds_read2_b32 v[78:79], v47 offset0:173 offset1:189
	ds_read2_b32 v[80:81], v47 offset0:206 offset1:222
	ds_read2_b32 v[82:83], v47 offset0:239 offset1:255
	s_waitcnt lgkmcnt(14)
	v_cvt_pk_fp8_f32 v48, v52, v54
	s_waitcnt lgkmcnt(10)
	v_cvt_pk_fp8_f32 v49, v60, v62
	s_waitcnt lgkmcnt(6)
	v_cvt_pk_fp8_f32 v50, v68, v70
	s_waitcnt lgkmcnt(2)
	v_cvt_pk_fp8_f32 v51, v76, v78
	v_cvt_pk_fp8_f32 v48, v56, v58 op_sel:[0,0,1]
	v_cvt_pk_fp8_f32 v49, v64, v66 op_sel:[0,0,1]
	v_cvt_pk_fp8_f32 v50, v72, v74 op_sel:[0,0,1]
	s_waitcnt lgkmcnt(0)
	v_cvt_pk_fp8_f32 v51, v80, v82 op_sel:[0,0,1]
	v_lshl_add_u64 v[28:29], s[4:5], 0, v[2:3]
	v_add_u32_e32 v52, s0, v32
	v_mad_i64_i32 v[84:85], s[4:5], v52, s13, v[28:29]
	global_store_dwordx4 v[84:85], v[48:51], off
	v_add_u32_e32 v52, s0, v34
	v_mad_i64_i32 v[28:29], s[4:5], v52, s13, v[28:29]
	v_mov_b32_e32 v48, v1
	v_mov_b32_e32 v49, v1
	v_mov_b32_e32 v50, v1
	v_mov_b32_e32 v51, v1
	v_cvt_pk_fp8_f32 v48, v53, v55
	v_cvt_pk_fp8_f32 v49, v61, v63
	v_cvt_pk_fp8_f32 v50, v69, v71
	v_cvt_pk_fp8_f32 v51, v77, v79
	v_cvt_pk_fp8_f32 v48, v57, v59 op_sel:[0,0,1]
	v_cvt_pk_fp8_f32 v49, v65, v67 op_sel:[0,0,1]
	v_cvt_pk_fp8_f32 v50, v73, v75 op_sel:[0,0,1]
	v_cvt_pk_fp8_f32 v51, v81, v83 op_sel:[0,0,1]
	s_mov_b64 s[4:5], 0
	global_store_dwordx4 v[28:29], v[48:51], off
	s_waitcnt lgkmcnt(0)
; __device__ __forceinline__ void tr_item8(const float* W, int ld, int K, int nblk, int item, unsigned char* WT, bool gu, float scale, LAS float* scr, int lane) {
;     const int kb = item / nblk, nb = item % nblk, k0 = 64 * kb, n0 = 32 * nb;
;     int drow0 = n0;
;     if (gu) { const int bj = n0 / FF, j = n0 - bj * FF; drow0 = 256 * (j / 128) + 128 * bj + (j % 128); }
;     { float t_[32];
; #pragma unroll
;       for (int i = 0; i < 32; ++i) t_[i] = W[(size_t)(k0 + 2 * i + (lane >> 5)) * ld + n0 + (lane & 31)];
; #pragma unroll
;       for (int i = 0; i < 32; ++i) scr[(2 * i + (lane >> 5)) * 33 + (lane & 31)] = t_[i] * scale; }
; __device__ __forceinline__ void convert_items(Frame& F, const Args& a, int lo, int hi, int w, int nw) {
;     ...
;         if (r < NE * I_GU) { const int e = r / I_GU, rr = r % I_GU; tr_item8(a.in[18] + (size_t)e * D * 2 * FF, 2 * FF, D, 224, rr, F.ws + WS_WMGU + (size_t)e * 2 * FF * D, true, WSC_GU, scr, lane); continue; } r -= NE * I_GU;
.LBB0_1304:
	s_andn2_b64 vcc, exec, s[4:5]
	s_cbranch_vccnz .LBB0_1306
	s_add_i32 s0, s8, 0xde00
	s_bfe_u32 s4, s0, 0x70009
	s_mulk_i32 s4, 0x2493
	s_lshr_b32 s4, s4, 16
	s_mul_i32 s5, s4, 0xe00
	v_readlane_b32 s40, v254, 28
	s_sub_i32 s0, s0, s5
	s_mul_i32 s5, s4, 0x1c00000
	v_readlane_b32 s44, v254, 32
	v_readlane_b32 s45, v254, 33
	s_add_u32 s7, s44, s5
	s_addc_u32 s31, s45, 0
	s_mul_i32 s4, s4, 0x700000
	s_add_u32 s4, s36, s4
	s_addc_u32 s5, s37, 0
	s_bfe_u32 s6, s0, 0xb0005
	s_mulk_i32 s6, 0x2493
	s_lshr_b32 s6, s6, 16
	s_mul_i32 s40, s6, 0xe0
	v_readlane_b32 s41, v254, 29
	s_sub_i32 s40, s0, s40
	s_lshl_b32 s0, s40, 5
	s_and_b32 s41, s40, 0xffff
	s_cmpk_gt_u32 s41, 0x6f
	v_readlane_b32 s42, v254, 30
	s_cselect_b32 s41, 0xfffff200, 0
	s_cselect_b32 s42, 0x80, 0
	s_add_i32 s0, s41, s0
	s_sext_i32_i16 s41, s0
	s_bfe_u32 s41, s41, 0x70018
	v_readlane_b32 s43, v254, 31
	s_add_i32 s41, s0, s41
	s_sext_i32_i16 s43, s41
	s_and_b32 s41, s41, 0xff80
	s_sub_i32 s0, s0, s41
	s_lshl_b32 s43, s43, 1
	s_sext_i32_i16 s0, s0
	s_and_b32 s43, s43, 0xffffff00
	s_add_i32 s0, s42, s0
	s_lshl_b32 s40, s40, 7
	s_add_i32 s0, s0, s43
	s_lshl_b32 s6, s6, 6
	s_and_b32 s40, s40, 0x3ff80
	s_add_u32 s40, s7, s40
	s_addc_u32 s41, s31, 0
	v_add_u32_e32 v50, s6, v30
	v_lshl_add_u64 v[28:29], s[40:41], 0, v[0:1]
	v_mad_i64_i32 v[48:49], s[40:41], v50, s14, v[28:29]
	global_load_dword v51, v[48:49], off nt
	v_add_u32_e32 v48, 2, v50
	v_mad_i64_i32 v[48:49], s[40:41], v48, s14, v[28:29]
	global_load_dword v52, v[48:49], off nt
	v_add_u32_e32 v48, 4, v50
	v_mad_i64_i32 v[48:49], s[40:41], v48, s14, v[28:29]
	global_load_dword v53, v[48:49], off nt
	v_add_u32_e32 v48, 6, v50
	v_mad_i64_i32 v[48:49], s[40:41], v48, s14, v[28:29]
	global_load_dword v54, v[48:49], off nt
	v_add_u32_e32 v48, 8, v50
	v_mad_i64_i32 v[48:49], s[40:41], v48, s14, v[28:29]
	global_load_dword v55, v[48:49], off nt
	v_add_u32_e32 v48, 10, v50
	v_mad_i64_i32 v[48:49], s[40:41], v48, s14, v[28:29]
	global_load_dword v56, v[48:49], off nt
	v_add_u32_e32 v48, 12, v50
	v_mad_i64_i32 v[48:49], s[40:41], v48, s14, v[28:29]
	global_load_dword v57, v[48:49], off nt
	v_add_u32_e32 v48, 14, v50
	v_mad_i64_i32 v[48:49], s[40:41], v48, s14, v[28:29]
	global_load_dword v58, v[48:49], off nt
	v_add_u32_e32 v48, 16, v50
	v_mad_i64_i32 v[48:49], s[40:41], v48, s14, v[28:29]
	global_load_dword v59, v[48:49], off nt
	v_add_u32_e32 v48, 18, v50
	v_mad_i64_i32 v[48:49], s[40:41], v48, s14, v[28:29]
	global_load_dword v60, v[48:49], off nt
	v_add_u32_e32 v48, 20, v50
	v_mad_i64_i32 v[48:49], s[40:41], v48, s14, v[28:29]
	global_load_dword v61, v[48:49], off nt
	v_add_u32_e32 v48, 22, v50
	v_mad_i64_i32 v[48:49], s[40:41], v48, s14, v[28:29]
	global_load_dword v62, v[48:49], off nt
	v_add_u32_e32 v48, 24, v50
	v_mad_i64_i32 v[48:49], s[40:41], v48, s14, v[28:29]
	global_load_dword v63, v[48:49], off nt
	v_add_u32_e32 v48, 26, v50
	v_mad_i64_i32 v[48:49], s[40:41], v48, s14, v[28:29]
	global_load_dword v64, v[48:49], off nt
	v_add_u32_e32 v48, 28, v50
	v_mad_i64_i32 v[48:49], s[40:41], v48, s14, v[28:29]
	global_load_dword v65, v[48:49], off nt
	v_add_u32_e32 v48, 30, v50
	v_mad_i64_i32 v[48:49], s[40:41], v48, s14, v[28:29]
	global_load_dword v66, v[48:49], off nt
	v_add_u32_e32 v48, 32, v50
	v_mad_i64_i32 v[48:49], s[40:41], v48, s14, v[28:29]
	global_load_dword v67, v[48:49], off nt
	v_add_u32_e32 v48, 34, v50
	v_mad_i64_i32 v[48:49], s[40:41], v48, s14, v[28:29]
	global_load_dword v68, v[48:49], off nt
	v_add_u32_e32 v48, 36, v50
	v_mad_i64_i32 v[48:49], s[40:41], v48, s14, v[28:29]
	global_load_dword v69, v[48:49], off nt
	v_add_u32_e32 v48, 38, v50
	v_mad_i64_i32 v[48:49], s[40:41], v48, s14, v[28:29]
	global_load_dword v70, v[48:49], off nt
	v_add_u32_e32 v48, 40, v50
	v_mad_i64_i32 v[48:49], s[40:41], v48, s14, v[28:29]
	global_load_dword v71, v[48:49], off nt
	v_add_u32_e32 v48, 42, v50
	v_mad_i64_i32 v[48:49], s[40:41], v48, s14, v[28:29]
	global_load_dword v72, v[48:49], off nt
	v_add_u32_e32 v48, 44, v50
	v_mad_i64_i32 v[48:49], s[40:41], v48, s14, v[28:29]
	global_load_dword v73, v[48:49], off nt
	v_add_u32_e32 v48, 46, v50
	v_mad_i64_i32 v[48:49], s[40:41], v48, s14, v[28:29]
	global_load_dword v74, v[48:49], off nt
	v_add_u32_e32 v48, 48, v50
	v_mad_i64_i32 v[48:49], s[40:41], v48, s14, v[28:29]
	global_load_dword v75, v[48:49], off nt
	v_add_u32_e32 v48, 50, v50
	v_mad_i64_i32 v[48:49], s[40:41], v48, s14, v[28:29]
	global_load_dword v76, v[48:49], off nt
	v_add_u32_e32 v48, 52, v50
	v_mad_i64_i32 v[48:49], s[40:41], v48, s14, v[28:29]
	global_load_dword v77, v[48:49], off nt
	v_add_u32_e32 v48, 54, v50
	v_mad_i64_i32 v[48:49], s[40:41], v48, s14, v[28:29]
	global_load_dword v78, v[48:49], off nt
	v_add_u32_e32 v48, 56, v50
	v_mad_i64_i32 v[48:49], s[40:41], v48, s14, v[28:29]
	global_load_dword v79, v[48:49], off nt
	v_add_u32_e32 v48, 58, v50
	v_mad_i64_i32 v[48:49], s[40:41], v48, s14, v[28:29]
	global_load_dword v80, v[48:49], off nt
	v_add_u32_e32 v48, 60, v50
	v_mad_i64_i32 v[48:49], s[40:41], v48, s14, v[28:29]
	global_load_dword v48, v[48:49], off nt
	v_add_u32_e32 v49, 62, v50
	v_mad_i64_i32 v[28:29], s[40:41], v49, s14, v[28:29]
	global_load_dword v28, v[28:29], off nt
	s_waitcnt vmcnt(31)
; __device__ __forceinline__ unsigned cvt_pk4_fp8(float a, float b, float c, float d) { int w = 0; w = __builtin_amdgcn_cvt_pk_fp8_f32(a, b, w, false); w = __builtin_amdgcn_cvt_pk_fp8_f32(c, d, w, true); return (unsigned)w; }
; #define GAS __attribute__((address_space(1)))
; #define LAS __attribute__((address_space(3)))
; #define LDS_WAIT() asm volatile("s_waitcnt lgkmcnt(0)" ::: "memory")
; __device__ __forceinline__ void tr_item8(const float* W, int ld, int K, int nblk, int item, unsigned char* WT, bool gu, float scale, LAS float* scr, int lane) {
;     ...
;     if (gu) { const int bj = n0 / FF, j = n0 - bj * FF; drow0 = 256 * (j / 128) + 128 * bj + (j % 128); }
;     ...
;       for (int i = 0; i < 32; ++i) scr[(2 * i + (lane >> 5)) * 33 + (lane & 31)] = t_[i] * scale; }
;     LDS_WAIT(); asm volatile("" ::: "memory");
;     const int c = lane & 3;
; #pragma unroll
;     for (int j = 0; j < 2; ++j) { const int n = (lane >> 2) + 16 * j; const LAS float* sp = scr + (16 * c) * 33 + n;
;         v4u o; o.x = pg8::cvt_pk4_fp8(sp[0 * 33], sp[1 * 33], sp[2 * 33], sp[3 * 33]); o.y = pg8::cvt_pk4_fp8(sp[4 * 33], sp[5 * 33], sp[6 * 33], sp[7 * 33]);
;         o.z = pg8::cvt_pk4_fp8(sp[8 * 33], sp[9 * 33], sp[10 * 33], sp[11 * 33]); o.w = pg8::cvt_pk4_fp8(sp[12 * 33], sp[13 * 33], sp[14 * 33], sp[15 * 33]);
;         *(GAS v4u*)(WT + (size_t)(drow0 + n) * K + k0 + 16 * c) = o; }
;     LDS_WAIT(); asm volatile("" ::: "memory");
	v_mul_f32_e32 v29, 0x42800000, v51
	s_waitcnt vmcnt(30)
	v_mul_f32_e32 v49, 0x42800000, v52
	ds_write2_b32 v31, v29, v49 offset1:66
	s_waitcnt vmcnt(29)
	v_mul_f32_e32 v29, 0x42800000, v53
	s_waitcnt vmcnt(28)
	v_mul_f32_e32 v49, 0x42800000, v54
	ds_write2_b32 v31, v29, v49 offset0:132 offset1:198
	s_waitcnt vmcnt(27)
	v_mul_f32_e32 v29, 0x42800000, v55
	s_waitcnt vmcnt(26)
	v_mul_f32_e32 v49, 0x42800000, v56
	ds_write2_b32 v40, v29, v49 offset0:8 offset1:74
	s_waitcnt vmcnt(25)
	v_mul_f32_e32 v29, 0x42800000, v57
	s_waitcnt vmcnt(24)
	v_mul_f32_e32 v49, 0x42800000, v58
	ds_write2_b32 v40, v29, v49 offset0:140 offset1:206
	s_waitcnt vmcnt(23)
	v_mul_f32_e32 v29, 0x42800000, v59
	s_waitcnt vmcnt(22)
	v_mul_f32_e32 v49, 0x42800000, v60
	ds_write2_b32 v41, v29, v49 offset0:16 offset1:82
	s_waitcnt vmcnt(21)
	v_mul_f32_e32 v29, 0x42800000, v61
	s_waitcnt vmcnt(20)
	v_mul_f32_e32 v49, 0x42800000, v62
	ds_write2_b32 v41, v29, v49 offset0:148 offset1:214
	s_waitcnt vmcnt(19)
	v_mul_f32_e32 v29, 0x42800000, v63
	s_waitcnt vmcnt(18)
	v_mul_f32_e32 v49, 0x42800000, v64
	ds_write2_b32 v42, v29, v49 offset0:24 offset1:90
	s_waitcnt vmcnt(17)
	v_mul_f32_e32 v29, 0x42800000, v65
	s_waitcnt vmcnt(16)
	v_mul_f32_e32 v49, 0x42800000, v66
	ds_write2_b32 v42, v29, v49 offset0:156 offset1:222
	s_waitcnt vmcnt(15)
	v_mul_f32_e32 v29, 0x42800000, v67
	s_waitcnt vmcnt(14)
	v_mul_f32_e32 v49, 0x42800000, v68
	ds_write2_b32 v43, v29, v49 offset0:32 offset1:98
	s_waitcnt vmcnt(13)
	v_mul_f32_e32 v29, 0x42800000, v69
	v_mov_b32_e32 v50, v1
	v_mov_b32_e32 v51, v1
	s_add_u32 s4, s4, s6
	s_waitcnt vmcnt(12)
	v_mul_f32_e32 v49, 0x42800000, v70
	ds_write2_b32 v43, v29, v49 offset0:164 offset1:230
	v_add_u32_e32 v84, s0, v32
	s_addc_u32 s5, s5, 0
	s_waitcnt vmcnt(11)
	v_mul_f32_e32 v29, 0x42800000, v71
	v_ashrrev_i32_e32 v85, 31, v84
	v_lshlrev_b64 v[84:85], 10, v[84:85]
	v_readlane_b32 s46, v254, 34
	s_waitcnt vmcnt(10)
	v_mul_f32_e32 v49, 0x42800000, v72
	ds_write2_b32 v44, v29, v49 offset0:40 offset1:106
	v_readlane_b32 s47, v254, 35
	s_waitcnt vmcnt(9)
	v_mul_f32_e32 v29, 0x42800000, v73
	s_waitcnt vmcnt(8)
	v_mul_f32_e32 v49, 0x42800000, v74
	ds_write2_b32 v44, v29, v49 offset0:172 offset1:238
	s_waitcnt vmcnt(7)
	v_mul_f32_e32 v29, 0x42800000, v75
	s_waitcnt vmcnt(6)
	v_mul_f32_e32 v49, 0x42800000, v76
	ds_write2_b32 v45, v29, v49 offset0:48 offset1:114
	s_waitcnt vmcnt(5)
	v_mul_f32_e32 v29, 0x42800000, v77
	s_waitcnt vmcnt(4)
	v_mul_f32_e32 v49, 0x42800000, v78
	ds_write2_b32 v45, v29, v49 offset0:180 offset1:246
	s_waitcnt vmcnt(3)
	v_mul_f32_e32 v29, 0x42800000, v79
	s_waitcnt vmcnt(2)
	v_mul_f32_e32 v49, 0x42800000, v80
	ds_write2_b32 v46, v29, v49 offset0:56 offset1:122
	v_mov_b32_e32 v49, v1
	s_waitcnt vmcnt(1)
	v_mul_f32_e32 v29, 0x42800000, v48
	v_mov_b32_e32 v48, v1
	s_waitcnt vmcnt(0)
	v_mul_f32_e32 v28, 0x42800000, v28
	ds_write2_b32 v46, v29, v28 offset0:188 offset1:254
	s_waitcnt lgkmcnt(0)
	ds_read2_b32 v[52:53], v33 offset1:16
	ds_read2_b32 v[54:55], v33 offset0:33 offset1:49
	ds_read2_b32 v[56:57], v33 offset0:66 offset1:82
	ds_read2_b32 v[58:59], v33 offset0:99 offset1:115
	ds_read2_b32 v[60:61], v33 offset0:132 offset1:148
	ds_read2_b32 v[62:63], v33 offset0:165 offset1:181
	ds_read2_b32 v[64:65], v33 offset0:198 offset1:214
	ds_read2_b32 v[66:67], v33 offset0:231 offset1:247
	ds_read2_b32 v[68:69], v47 offset0:8 offset1:24
	ds_read2_b32 v[70:71], v47 offset0:41 offset1:57
	ds_read2_b32 v[72:73], v47 offset0:74 offset1:90
	ds_read2_b32 v[74:75], v47 offset0:107 offset1:123
	ds_read2_b32 v[76:77], v47 offset0:140 offset1:156
	ds_read2_b32 v[78:79], v47 offset0:173 offset1:189
	ds_read2_b32 v[80:81], v47 offset0:206 offset1:222
	ds_read2_b32 v[82:83], v47 offset0:239 offset1:255
	s_waitcnt lgkmcnt(14)
	v_cvt_pk_fp8_f32 v48, v52, v54
	s_waitcnt lgkmcnt(10)
	v_cvt_pk_fp8_f32 v49, v60, v62
	s_waitcnt lgkmcnt(6)
	v_cvt_pk_fp8_f32 v50, v68, v70
	s_waitcnt lgkmcnt(2)
	v_cvt_pk_fp8_f32 v51, v76, v78
	v_cvt_pk_fp8_f32 v48, v56, v58 op_sel:[0,0,1]
	v_cvt_pk_fp8_f32 v49, v64, v66 op_sel:[0,0,1]
	v_cvt_pk_fp8_f32 v50, v72, v74 op_sel:[0,0,1]
	s_waitcnt lgkmcnt(0)
	v_cvt_pk_fp8_f32 v51, v80, v82 op_sel:[0,0,1]
	v_lshl_add_u64 v[28:29], s[4:5], 0, v[2:3]
	v_lshl_add_u64 v[84:85], v[28:29], 0, v[84:85]
	v_add_u32_e32 v52, s0, v34
	global_store_dwordx4 v[84:85], v[48:51], off
	s_nop 1
	v_mov_b32_e32 v48, v1
	v_mov_b32_e32 v49, v1
	v_mov_b32_e32 v50, v1
	v_mov_b32_e32 v51, v1
	v_cvt_pk_fp8_f32 v48, v53, v55
	v_cvt_pk_fp8_f32 v49, v61, v63
	v_cvt_pk_fp8_f32 v50, v69, v71
	v_cvt_pk_fp8_f32 v51, v77, v79
	v_cvt_pk_fp8_f32 v48, v57, v59 op_sel:[0,0,1]
	v_cvt_pk_fp8_f32 v49, v65, v67 op_sel:[0,0,1]
	v_cvt_pk_fp8_f32 v50, v73, v75 op_sel:[0,0,1]
	v_cvt_pk_fp8_f32 v51, v81, v83 op_sel:[0,0,1]
	v_ashrrev_i32_e32 v53, 31, v52
	v_lshlrev_b64 v[52:53], 10, v[52:53]
	v_lshl_add_u64 v[28:29], v[28:29], 0, v[52:53]
	global_store_dwordx4 v[28:29], v[48:51], off
	s_waitcnt lgkmcnt(0)

; __device__ __forceinline__ void tr_item8(const float* W, int ld, int K, int nblk, int item, unsigned char* WT, bool gu, float scale, LAS float* scr, int lane) {
;     const int kb = item / nblk, nb = item % nblk, k0 = 64 * kb, n0 = 32 * nb;
;     int drow0 = n0;
;     if (gu) { const int bj = n0 / FF, j = n0 - bj * FF; drow0 = 256 * (j / 128) + 128 * bj + (j % 128); }
;     { float t_[32];
; #pragma unroll
;       for (int i = 0; i < 32; ++i) t_[i] = W[(size_t)(k0 + 2 * i + (lane >> 5)) * ld + n0 + (lane & 31)];
; #pragma unroll
;       for (int i = 0; i < 32; ++i) scr[(2 * i + (lane >> 5)) * 33 + (lane & 31)] = t_[i] * scale; }
; __device__ __forceinline__ void convert_items(Frame& F, const Args& a, int lo, int hi, int w, int nw) {
;     ...
;         if (r < I_DN) { tr_item8(a.in[15], D, FF, 32, r, F.ws + WS_WDN, false, WSC_DN, scr, lane); continue; } r -= I_DN;
.LBB0_1307:
	s_andn2_b64 vcc, exec, s[4:5]
	s_cbranch_vccnz .LBB0_1309
	s_lshl_b32 s0, s8, 5
	s_and_b32 s4, s11, 0x1ffc0
	s_and_b32 s6, s0, 0x3e0
	v_add_u32_e32 v28, s4, v30
	s_lshl_b32 s0, s6, 2
	v_ashrrev_i32_e32 v29, 31, v28
	v_lshl_add_u64 v[48:49], v[4:5], 0, s[0:1]
	v_lshlrev_b64 v[28:29], 12, v[28:29]
	v_lshl_add_u64 v[28:29], v[48:49], 0, v[28:29]
	v_add_co_u32_e32 v48, vcc, 0x2000, v28
	global_load_dword v50, v[28:29], off nt
	s_nop 0
	v_addc_co_u32_e32 v49, vcc, 0, v29, vcc
	global_load_dword v51, v[48:49], off nt
	v_add_co_u32_e32 v48, vcc, 0x4000, v28
	s_mov_b32 s5, s1
	s_nop 0
	v_addc_co_u32_e32 v49, vcc, 0, v29, vcc
	global_load_dword v52, v[48:49], off nt
	v_add_co_u32_e32 v48, vcc, 0x6000, v28
	s_nop 1
	v_addc_co_u32_e32 v49, vcc, 0, v29, vcc
	global_load_dword v53, v[48:49], off nt
	v_add_co_u32_e32 v48, vcc, 0x8000, v28
	s_nop 1
	v_addc_co_u32_e32 v49, vcc, 0, v29, vcc
	global_load_dword v54, v[48:49], off nt
	v_add_co_u32_e32 v48, vcc, 0xa000, v28
	s_nop 1
	v_addc_co_u32_e32 v49, vcc, 0, v29, vcc
	global_load_dword v55, v[48:49], off nt
	v_add_co_u32_e32 v48, vcc, 0xc000, v28
	s_nop 1
	v_addc_co_u32_e32 v49, vcc, 0, v29, vcc
	global_load_dword v56, v[48:49], off nt
	v_add_co_u32_e32 v48, vcc, 0xe000, v28
	s_nop 1
	v_addc_co_u32_e32 v49, vcc, 0, v29, vcc
	global_load_dword v57, v[48:49], off nt
	v_add_co_u32_e32 v48, vcc, 0x10000, v28
	s_nop 1
	v_addc_co_u32_e32 v49, vcc, 0, v29, vcc
	global_load_dword v58, v[48:49], off nt
	v_add_co_u32_e32 v48, vcc, 0x12000, v28
	s_nop 1
	v_addc_co_u32_e32 v49, vcc, 0, v29, vcc
	global_load_dword v59, v[48:49], off nt
	v_add_co_u32_e32 v48, vcc, 0x14000, v28
	s_nop 1
	v_addc_co_u32_e32 v49, vcc, 0, v29, vcc
	global_load_dword v60, v[48:49], off nt
	v_add_co_u32_e32 v48, vcc, 0x16000, v28
	s_nop 1
	v_addc_co_u32_e32 v49, vcc, 0, v29, vcc
	global_load_dword v61, v[48:49], off nt
	v_add_co_u32_e32 v48, vcc, 0x18000, v28
	s_nop 1
	v_addc_co_u32_e32 v49, vcc, 0, v29, vcc
	global_load_dword v62, v[48:49], off nt
	v_add_co_u32_e32 v48, vcc, 0x1a000, v28
	s_nop 1
	v_addc_co_u32_e32 v49, vcc, 0, v29, vcc
	global_load_dword v63, v[48:49], off nt
	v_add_co_u32_e32 v48, vcc, 0x1c000, v28
	s_nop 1
	v_addc_co_u32_e32 v49, vcc, 0, v29, vcc
	global_load_dword v64, v[48:49], off nt
	v_add_co_u32_e32 v48, vcc, 0x1e000, v28
	s_nop 1
	v_addc_co_u32_e32 v49, vcc, 0, v29, vcc
	global_load_dword v65, v[48:49], off nt
	v_add_co_u32_e32 v48, vcc, 0x20000, v28
	s_nop 1
	v_addc_co_u32_e32 v49, vcc, 0, v29, vcc
	global_load_dword v66, v[48:49], off nt
	v_add_co_u32_e32 v48, vcc, 0x22000, v28
	s_nop 1
	v_addc_co_u32_e32 v49, vcc, 0, v29, vcc
	global_load_dword v67, v[48:49], off nt
	v_add_co_u32_e32 v48, vcc, 0x24000, v28
	s_nop 1
	v_addc_co_u32_e32 v49, vcc, 0, v29, vcc
	global_load_dword v68, v[48:49], off nt
	v_add_co_u32_e32 v48, vcc, 0x26000, v28
	s_nop 1
	v_addc_co_u32_e32 v49, vcc, 0, v29, vcc
	global_load_dword v69, v[48:49], off nt
	v_add_co_u32_e32 v48, vcc, 0x28000, v28
	s_nop 1
	v_addc_co_u32_e32 v49, vcc, 0, v29, vcc
	global_load_dword v70, v[48:49], off nt
	v_add_co_u32_e32 v48, vcc, 0x2a000, v28
	s_nop 1
	v_addc_co_u32_e32 v49, vcc, 0, v29, vcc
	global_load_dword v71, v[48:49], off nt
	v_add_co_u32_e32 v48, vcc, 0x2c000, v28
	s_nop 1
	v_addc_co_u32_e32 v49, vcc, 0, v29, vcc
	global_load_dword v72, v[48:49], off nt
	v_add_co_u32_e32 v48, vcc, 0x2e000, v28
	s_nop 1
	v_addc_co_u32_e32 v49, vcc, 0, v29, vcc
	global_load_dword v73, v[48:49], off nt
	v_add_co_u32_e32 v48, vcc, 0x30000, v28
	s_nop 1
	v_addc_co_u32_e32 v49, vcc, 0, v29, vcc
	global_load_dword v74, v[48:49], off nt
	v_add_co_u32_e32 v48, vcc, 0x32000, v28
	s_nop 1
	v_addc_co_u32_e32 v49, vcc, 0, v29, vcc
	global_load_dword v75, v[48:49], off nt
	v_add_co_u32_e32 v48, vcc, 0x34000, v28
	s_nop 1
	v_addc_co_u32_e32 v49, vcc, 0, v29, vcc
	global_load_dword v76, v[48:49], off nt
	v_add_co_u32_e32 v48, vcc, 0x36000, v28
	s_nop 1
	v_addc_co_u32_e32 v49, vcc, 0, v29, vcc
	global_load_dword v77, v[48:49], off nt
	v_add_co_u32_e32 v48, vcc, 0x38000, v28
	s_nop 1
	v_addc_co_u32_e32 v49, vcc, 0, v29, vcc
	global_load_dword v78, v[48:49], off nt
	v_add_co_u32_e32 v48, vcc, 0x3a000, v28
	s_nop 1
	v_addc_co_u32_e32 v49, vcc, 0, v29, vcc
	global_load_dword v79, v[48:49], off nt
	v_add_co_u32_e32 v48, vcc, 0x3c000, v28
	s_nop 1
	v_addc_co_u32_e32 v49, vcc, 0, v29, vcc
	v_add_co_u32_e32 v28, vcc, 0x3e000, v28
	global_load_dword v48, v[48:49], off nt
	s_nop 0
	v_addc_co_u32_e32 v29, vcc, 0, v29, vcc
	global_load_dword v28, v[28:29], off nt
	s_waitcnt vmcnt(31)
	v_mul_f32_e32 v29, 0x43000000, v50
	s_waitcnt vmcnt(30)
; __device__ __forceinline__ unsigned cvt_pk4_fp8(float a, float b, float c, float d) { int w = 0; w = __builtin_amdgcn_cvt_pk_fp8_f32(a, b, w, false); w = __builtin_amdgcn_cvt_pk_fp8_f32(c, d, w, true); return (unsigned)w; }
; #define GAS __attribute__((address_space(1)))
; #define LAS __attribute__((address_space(3)))
; #define LDS_WAIT() asm volatile("s_waitcnt lgkmcnt(0)" ::: "memory")
; __device__ __forceinline__ void tr_item8(const float* W, int ld, int K, int nblk, int item, unsigned char* WT, bool gu, float scale, LAS float* scr, int lane) {
;     ...
;       for (int i = 0; i < 32; ++i) scr[(2 * i + (lane >> 5)) * 33 + (lane & 31)] = t_[i] * scale; }
;     LDS_WAIT(); asm volatile("" ::: "memory");
;     const int c = lane & 3;
; #pragma unroll
;     for (int j = 0; j < 2; ++j) { const int n = (lane >> 2) + 16 * j; const LAS float* sp = scr + (16 * c) * 33 + n;
;         v4u o; o.x = pg8::cvt_pk4_fp8(sp[0 * 33], sp[1 * 33], sp[2 * 33], sp[3 * 33]); o.y = pg8::cvt_pk4_fp8(sp[4 * 33], sp[5 * 33], sp[6 * 33], sp[7 * 33]);
;         o.z = pg8::cvt_pk4_fp8(sp[8 * 33], sp[9 * 33], sp[10 * 33], sp[11 * 33]); o.w = pg8::cvt_pk4_fp8(sp[12 * 33], sp[13 * 33], sp[14 * 33], sp[15 * 33]);
;         *(GAS v4u*)(WT + (size_t)(drow0 + n) * K + k0 + 16 * c) = o; }
;     LDS_WAIT(); asm volatile("" ::: "memory");
	v_mul_f32_e32 v49, 0x43000000, v51
	ds_write2_b32 v31, v29, v49 offset1:66
	s_waitcnt vmcnt(29)
	v_mul_f32_e32 v29, 0x43000000, v52
	s_waitcnt vmcnt(28)
	v_mul_f32_e32 v49, 0x43000000, v53
	ds_write2_b32 v31, v29, v49 offset0:132 offset1:198
	s_waitcnt vmcnt(27)
	v_mul_f32_e32 v29, 0x43000000, v54
	s_waitcnt vmcnt(26)
	v_mul_f32_e32 v49, 0x43000000, v55
	ds_write2_b32 v40, v29, v49 offset0:8 offset1:74
	s_waitcnt vmcnt(25)
	v_mul_f32_e32 v29, 0x43000000, v56
	s_waitcnt vmcnt(24)
	v_mul_f32_e32 v49, 0x43000000, v57
	ds_write2_b32 v40, v29, v49 offset0:140 offset1:206
	s_waitcnt vmcnt(23)
	v_mul_f32_e32 v29, 0x43000000, v58
	s_waitcnt vmcnt(22)
	v_mul_f32_e32 v49, 0x43000000, v59
	ds_write2_b32 v41, v29, v49 offset0:16 offset1:82
	s_waitcnt vmcnt(21)
	v_mul_f32_e32 v29, 0x43000000, v60
	s_waitcnt vmcnt(20)
	v_mul_f32_e32 v49, 0x43000000, v61
	ds_write2_b32 v41, v29, v49 offset0:148 offset1:214
	s_waitcnt vmcnt(19)
	v_mul_f32_e32 v29, 0x43000000, v62
	s_waitcnt vmcnt(18)
	v_mul_f32_e32 v49, 0x43000000, v63
	ds_write2_b32 v42, v29, v49 offset0:24 offset1:90
	s_waitcnt vmcnt(17)
	v_mul_f32_e32 v29, 0x43000000, v64
	s_waitcnt vmcnt(16)
	v_mul_f32_e32 v49, 0x43000000, v65
	ds_write2_b32 v42, v29, v49 offset0:156 offset1:222
	s_waitcnt vmcnt(15)
	v_mul_f32_e32 v29, 0x43000000, v66
	s_waitcnt vmcnt(14)
	v_mul_f32_e32 v49, 0x43000000, v67
	ds_write2_b32 v43, v29, v49 offset0:32 offset1:98
	s_waitcnt vmcnt(13)
	v_mul_f32_e32 v29, 0x43000000, v68
	s_waitcnt vmcnt(12)
	v_mul_f32_e32 v49, 0x43000000, v69
	ds_write2_b32 v43, v29, v49 offset0:164 offset1:230
	s_waitcnt vmcnt(11)
	v_mul_f32_e32 v29, 0x43000000, v70
	s_waitcnt vmcnt(10)
	v_mul_f32_e32 v49, 0x43000000, v71
	ds_write2_b32 v44, v29, v49 offset0:40 offset1:106
	s_waitcnt vmcnt(9)
	v_mul_f32_e32 v29, 0x43000000, v72
	s_waitcnt vmcnt(8)
	v_mul_f32_e32 v49, 0x43000000, v73
	ds_write2_b32 v44, v29, v49 offset0:172 offset1:238
	v_mov_b32_e32 v50, 0
	v_mov_b32_e32 v51, 0
	s_waitcnt vmcnt(7)
	v_mul_f32_e32 v29, 0x43000000, v74
	s_waitcnt vmcnt(6)
	v_mul_f32_e32 v49, 0x43000000, v75
	ds_write2_b32 v45, v29, v49 offset0:48 offset1:114
	s_waitcnt vmcnt(5)
	v_mul_f32_e32 v29, 0x43000000, v76
	s_waitcnt vmcnt(4)
	v_mul_f32_e32 v49, 0x43000000, v77
	ds_write2_b32 v45, v29, v49 offset0:180 offset1:246
	s_waitcnt vmcnt(3)
	v_mul_f32_e32 v29, 0x43000000, v78
	s_waitcnt vmcnt(2)
	v_mul_f32_e32 v49, 0x43000000, v79
	ds_write2_b32 v46, v29, v49 offset0:56 offset1:122
	v_mov_b32_e32 v49, 0
	s_waitcnt vmcnt(1)
	v_mul_f32_e32 v29, 0x43000000, v48
	v_mov_b32_e32 v48, 0
	s_waitcnt vmcnt(0)
	v_mul_f32_e32 v28, 0x43000000, v28
	ds_write2_b32 v46, v29, v28 offset0:188 offset1:254
	s_waitcnt lgkmcnt(0)
	ds_read2_b32 v[52:53], v33 offset1:16
	ds_read2_b32 v[54:55], v33 offset0:33 offset1:49
	ds_read2_b32 v[56:57], v33 offset0:66 offset1:82
	ds_read2_b32 v[58:59], v33 offset0:99 offset1:115
	ds_read2_b32 v[60:61], v33 offset0:132 offset1:148
	ds_read2_b32 v[62:63], v33 offset0:165 offset1:181
	ds_read2_b32 v[64:65], v33 offset0:198 offset1:214
	ds_read2_b32 v[66:67], v33 offset0:231 offset1:247
	ds_read2_b32 v[68:69], v47 offset0:8 offset1:24
	ds_read2_b32 v[70:71], v47 offset0:41 offset1:57
	ds_read2_b32 v[72:73], v47 offset0:74 offset1:90
	ds_read2_b32 v[74:75], v47 offset0:107 offset1:123
	ds_read2_b32 v[76:77], v47 offset0:140 offset1:156
	ds_read2_b32 v[78:79], v47 offset0:173 offset1:189
	ds_read2_b32 v[80:81], v47 offset0:206 offset1:222
	ds_read2_b32 v[82:83], v47 offset0:239 offset1:255
	s_waitcnt lgkmcnt(14)
	v_cvt_pk_fp8_f32 v48, v52, v54
	s_waitcnt lgkmcnt(10)
	v_cvt_pk_fp8_f32 v49, v60, v62
	s_waitcnt lgkmcnt(6)
	v_cvt_pk_fp8_f32 v50, v68, v70
	s_waitcnt lgkmcnt(2)
	v_cvt_pk_fp8_f32 v51, v76, v78
	v_cvt_pk_fp8_f32 v48, v56, v58 op_sel:[0,0,1]
	v_cvt_pk_fp8_f32 v49, v64, v66 op_sel:[0,0,1]
	v_cvt_pk_fp8_f32 v50, v72, v74 op_sel:[0,0,1]
	s_waitcnt lgkmcnt(0)
	v_cvt_pk_fp8_f32 v51, v80, v82 op_sel:[0,0,1]
	v_lshl_add_u64 v[28:29], v[16:17], 0, s[4:5]
	v_add_u32_e32 v52, s6, v32
	v_mad_i64_i32 v[84:85], s[4:5], v52, s13, v[28:29]
	global_store_dwordx4 v[84:85], v[48:51], off
	v_add_u32_e32 v52, s6, v34
	v_mad_i64_i32 v[28:29], s[4:5], v52, s13, v[28:29]
	v_mov_b32_e32 v48, 0
	v_mov_b32_e32 v49, 0
	v_mov_b32_e32 v50, 0
	v_mov_b32_e32 v51, 0
	v_cvt_pk_fp8_f32 v48, v53, v55
	v_cvt_pk_fp8_f32 v49, v61, v63
	v_cvt_pk_fp8_f32 v50, v69, v71
	v_cvt_pk_fp8_f32 v51, v77, v79
	v_cvt_pk_fp8_f32 v48, v57, v59 op_sel:[0,0,1]
	v_cvt_pk_fp8_f32 v49, v65, v67 op_sel:[0,0,1]
	v_cvt_pk_fp8_f32 v50, v73, v75 op_sel:[0,0,1]
	v_cvt_pk_fp8_f32 v51, v81, v83 op_sel:[0,0,1]
	global_store_dwordx4 v[28:29], v[48:51], off
	s_waitcnt lgkmcnt(0)

; __device__ __forceinline__ void tr_item8(const float* W, int ld, int K, int nblk, int item, unsigned char* WT, bool gu, float scale, LAS float* scr, int lane) {
;     const int kb = item / nblk, nb = item % nblk, k0 = 64 * kb, n0 = 32 * nb;
;     int drow0 = n0;
;     if (gu) { const int bj = n0 / FF, j = n0 - bj * FF; drow0 = 256 * (j / 128) + 128 * bj + (j % 128); }
;     { float t_[32];
; #pragma unroll
;       for (int i = 0; i < 32; ++i) t_[i] = W[(size_t)(k0 + 2 * i + (lane >> 5)) * ld + n0 + (lane & 31)];
; #pragma unroll
;       for (int i = 0; i < 32; ++i) scr[(2 * i + (lane >> 5)) * 33 + (lane & 31)] = t_[i] * scale; }
; __device__ __forceinline__ void convert_items(Frame& F, const Args& a, int lo, int hi, int w, int nw) {
;     ...
;         if (r < I_GU) { tr_item8(a.in[14], 2 * FF, D, 224, r, F.ws + WS_WGU, true, WSC_GU, scr, lane); continue; } r -= I_GU;
.LBB0_1310:
	s_andn2_b64 vcc, exec, s[4:5]
	s_cbranch_vccnz .LBB0_1312
	s_add_i32 s0, s8, 0xf300
	s_bfe_u32 s4, s0, 0xb0005
	s_mulk_i32 s4, 0x2493
	s_lshr_b32 s4, s4, 16
	s_mul_i32 s5, s4, 0xe0
	s_sub_i32 s0, s0, s5
	s_lshl_b32 s5, s0, 5
	s_and_b32 s6, s0, 0xffff
	s_cmpk_gt_u32 s6, 0x6f
	s_cselect_b32 s31, 0xfffff200, 0
	s_cselect_b32 s40, 0x80, 0
	s_lshl_b32 s0, s0, 7
	s_lshl_b32 s4, s4, 6
	s_and_b32 s0, s0, 0x3ff80
	v_add_u32_e32 v64, s4, v30
	v_lshl_add_u64 v[28:29], v[6:7], 0, s[0:1]
	v_mad_i64_i32 v[48:49], s[6:7], v64, s14, v[28:29]
	v_add_u32_e32 v50, 2, v64
	v_add_u32_e32 v52, 4, v64
	v_add_u32_e32 v54, 6, v64
	v_add_u32_e32 v56, 8, v64
	v_add_u32_e32 v58, 10, v64
	v_add_u32_e32 v60, 12, v64
	v_add_u32_e32 v62, 14, v64
	v_mad_i64_i32 v[50:51], s[6:7], v50, s14, v[28:29]
	v_mad_i64_i32 v[52:53], s[6:7], v52, s14, v[28:29]
	v_mad_i64_i32 v[54:55], s[6:7], v54, s14, v[28:29]
	v_mad_i64_i32 v[56:57], s[6:7], v56, s14, v[28:29]
	v_mad_i64_i32 v[58:59], s[6:7], v58, s14, v[28:29]
	v_mad_i64_i32 v[60:61], s[6:7], v60, s14, v[28:29]
	v_mad_i64_i32 v[62:63], s[6:7], v62, s14, v[28:29]
	global_load_dword v65, v[48:49], off nt
	global_load_dword v66, v[50:51], off nt
	global_load_dword v67, v[52:53], off nt
	global_load_dword v68, v[54:55], off nt
	global_load_dword v69, v[56:57], off nt
	global_load_dword v70, v[58:59], off nt
	global_load_dword v71, v[60:61], off nt
	global_load_dword v72, v[62:63], off nt
	v_add_u32_e32 v48, 16, v64
	v_mad_i64_i32 v[48:49], s[6:7], v48, s14, v[28:29]
	v_add_u32_e32 v50, 18, v64
	v_add_u32_e32 v52, 20, v64
	v_add_u32_e32 v54, 22, v64
	v_add_u32_e32 v56, 24, v64
	v_add_u32_e32 v58, 26, v64
	v_add_u32_e32 v60, 28, v64
	v_add_u32_e32 v62, 30, v64
	v_mad_i64_i32 v[50:51], s[6:7], v50, s14, v[28:29]
	v_mad_i64_i32 v[52:53], s[6:7], v52, s14, v[28:29]
	v_mad_i64_i32 v[54:55], s[6:7], v54, s14, v[28:29]
	v_mad_i64_i32 v[56:57], s[6:7], v56, s14, v[28:29]
	v_mad_i64_i32 v[58:59], s[6:7], v58, s14, v[28:29]
	v_mad_i64_i32 v[60:61], s[6:7], v60, s14, v[28:29]
	v_mad_i64_i32 v[62:63], s[6:7], v62, s14, v[28:29]
	global_load_dword v73, v[48:49], off nt
	global_load_dword v74, v[50:51], off nt
	global_load_dword v75, v[52:53], off nt
	global_load_dword v76, v[54:55], off nt
	global_load_dword v77, v[56:57], off nt
	global_load_dword v78, v[58:59], off nt
	global_load_dword v79, v[60:61], off nt
	global_load_dword v80, v[62:63], off nt
	v_add_u32_e32 v48, 32, v64
	v_add_u32_e32 v50, 34, v64
	v_add_u32_e32 v52, 36, v64
	v_add_u32_e32 v54, 38, v64
	v_add_u32_e32 v60, 44, v64
	v_mad_i64_i32 v[48:49], s[6:7], v48, s14, v[28:29]
	v_mad_i64_i32 v[50:51], s[6:7], v50, s14, v[28:29]
	v_mad_i64_i32 v[52:53], s[6:7], v52, s14, v[28:29]
	v_mad_i64_i32 v[54:55], s[6:7], v54, s14, v[28:29]
	v_add_u32_e32 v56, 40, v64
	v_add_u32_e32 v58, 42, v64
	v_mad_i64_i32 v[60:61], s[6:7], v60, s14, v[28:29]
	v_add_u32_e32 v62, 46, v64
	v_mad_i64_i32 v[56:57], s[6:7], v56, s14, v[28:29]
	v_mad_i64_i32 v[58:59], s[6:7], v58, s14, v[28:29]
	v_mad_i64_i32 v[62:63], s[6:7], v62, s14, v[28:29]
	global_load_dword v81, v[48:49], off nt
	global_load_dword v82, v[50:51], off nt
	global_load_dword v83, v[52:53], off nt
	global_load_dword v84, v[54:55], off nt
	global_load_dword v85, v[56:57], off nt
	global_load_dword v86, v[58:59], off nt
	s_nop 0
	global_load_dword v60, v[60:61], off nt
	s_nop 0
	global_load_dword v61, v[62:63], off nt
	v_add_u32_e32 v48, 48, v64
	v_add_u32_e32 v50, 50, v64
	v_add_u32_e32 v52, 52, v64
	v_add_u32_e32 v54, 54, v64
	v_mad_i64_i32 v[48:49], s[6:7], v48, s14, v[28:29]
	v_mad_i64_i32 v[50:51], s[6:7], v50, s14, v[28:29]
	v_mad_i64_i32 v[52:53], s[6:7], v52, s14, v[28:29]
	v_mad_i64_i32 v[54:55], s[6:7], v54, s14, v[28:29]
	v_add_u32_e32 v56, 56, v64
	v_add_u32_e32 v58, 58, v64
	v_mad_i64_i32 v[56:57], s[6:7], v56, s14, v[28:29]
	v_mad_i64_i32 v[58:59], s[6:7], v58, s14, v[28:29]
	global_load_dword v62, v[48:49], off nt
	s_nop 0
	global_load_dword v50, v[50:51], off nt
	s_nop 0
	global_load_dword v51, v[52:53], off nt
	s_nop 0
	global_load_dword v52, v[54:55], off nt
	global_load_dword v53, v[56:57], off nt
	s_nop 0
	global_load_dword v54, v[58:59], off nt
	v_add_u32_e32 v48, 60, v64
	v_add_u32_e32 v55, 62, v64
	v_mad_i64_i32 v[48:49], s[6:7], v48, s14, v[28:29]
	v_mad_i64_i32 v[28:29], s[6:7], v55, s14, v[28:29]
	global_load_dword v48, v[48:49], off nt
	s_nop 0
	global_load_dword v28, v[28:29], off nt
	s_waitcnt vmcnt(31)
	v_mul_f32_e32 v29, 0x42800000, v65
	s_waitcnt vmcnt(30)
	v_mul_f32_e32 v49, 0x42800000, v66
	ds_write2_b32 v31, v29, v49 offset1:66
	s_waitcnt vmcnt(29)
	v_mul_f32_e32 v29, 0x42800000, v67
	s_waitcnt vmcnt(28)
	v_mul_f32_e32 v49, 0x42800000, v68
	ds_write2_b32 v31, v29, v49 offset0:132 offset1:198
	s_waitcnt vmcnt(27)
	v_mul_f32_e32 v29, 0x42800000, v69
	s_waitcnt vmcnt(26)
; __device__ __forceinline__ unsigned cvt_pk4_fp8(float a, float b, float c, float d) { int w = 0; w = __builtin_amdgcn_cvt_pk_fp8_f32(a, b, w, false); w = __builtin_amdgcn_cvt_pk_fp8_f32(c, d, w, true); return (unsigned)w; }
; #define GAS __attribute__((address_space(1)))
; #define LAS __attribute__((address_space(3)))
; #define LDS_WAIT() asm volatile("s_waitcnt lgkmcnt(0)" ::: "memory")
; __device__ __forceinline__ void tr_item8(const float* W, int ld, int K, int nblk, int item, unsigned char* WT, bool gu, float scale, LAS float* scr, int lane) {
;     ...
;     if (gu) { const int bj = n0 / FF, j = n0 - bj * FF; drow0 = 256 * (j / 128) + 128 * bj + (j % 128); }
;     ...
;       for (int i = 0; i < 32; ++i) scr[(2 * i + (lane >> 5)) * 33 + (lane & 31)] = t_[i] * scale; }
;     LDS_WAIT(); asm volatile("" ::: "memory");
;     const int c = lane & 3;
; #pragma unroll
;     for (int j = 0; j < 2; ++j) { const int n = (lane >> 2) + 16 * j; const LAS float* sp = scr + (16 * c) * 33 + n;
;         v4u o; o.x = pg8::cvt_pk4_fp8(sp[0 * 33], sp[1 * 33], sp[2 * 33], sp[3 * 33]); o.y = pg8::cvt_pk4_fp8(sp[4 * 33], sp[5 * 33], sp[6 * 33], sp[7 * 33]);
;         o.z = pg8::cvt_pk4_fp8(sp[8 * 33], sp[9 * 33], sp[10 * 33], sp[11 * 33]); o.w = pg8::cvt_pk4_fp8(sp[12 * 33], sp[13 * 33], sp[14 * 33], sp[15 * 33]);
;         *(GAS v4u*)(WT + (size_t)(drow0 + n) * K + k0 + 16 * c) = o; }
;     LDS_WAIT(); asm volatile("" ::: "memory");
	v_mul_f32_e32 v49, 0x42800000, v70
	ds_write2_b32 v40, v29, v49 offset0:8 offset1:74
	s_waitcnt vmcnt(25)
	v_mul_f32_e32 v29, 0x42800000, v71
	s_waitcnt vmcnt(24)
	v_mul_f32_e32 v49, 0x42800000, v72
	ds_write2_b32 v40, v29, v49 offset0:140 offset1:206
	s_add_i32 s0, s31, s5
	s_sext_i32_i16 s5, s0
	s_bfe_u32 s5, s5, 0x70018
	s_add_i32 s5, s0, s5
	s_sext_i32_i16 s6, s5
	s_and_b32 s5, s5, 0xff80
	s_sub_i32 s0, s0, s5
	s_lshl_b32 s6, s6, 1
	s_sext_i32_i16 s0, s0
	s_waitcnt vmcnt(23)
	v_mul_f32_e32 v29, 0x42800000, v73
	s_waitcnt vmcnt(22)
	v_mul_f32_e32 v49, 0x42800000, v74
	ds_write2_b32 v41, v29, v49 offset0:16 offset1:82
	s_waitcnt vmcnt(21)
	v_mul_f32_e32 v29, 0x42800000, v75
	s_waitcnt vmcnt(20)
	v_mul_f32_e32 v49, 0x42800000, v76
	ds_write2_b32 v41, v29, v49 offset0:148 offset1:214
	s_waitcnt vmcnt(19)
	v_mul_f32_e32 v29, 0x42800000, v77
	s_waitcnt vmcnt(18)
	v_mul_f32_e32 v49, 0x42800000, v78
	ds_write2_b32 v42, v29, v49 offset0:24 offset1:90
	s_waitcnt vmcnt(17)
	v_mul_f32_e32 v29, 0x42800000, v79
	s_waitcnt vmcnt(16)
	v_mul_f32_e32 v49, 0x42800000, v80
	ds_write2_b32 v42, v29, v49 offset0:156 offset1:222
	s_and_b32 s6, s6, 0xffffff00
	s_add_i32 s0, s40, s0
	s_add_i32 s0, s0, s6
	s_mov_b32 s5, s1
	s_waitcnt vmcnt(15)
	v_mul_f32_e32 v29, 0x42800000, v81
	s_waitcnt vmcnt(14)
	v_mul_f32_e32 v49, 0x42800000, v82
	ds_write2_b32 v43, v29, v49 offset0:32 offset1:98
	s_waitcnt vmcnt(13)
	v_mul_f32_e32 v29, 0x42800000, v83
	s_waitcnt vmcnt(12)
	v_mul_f32_e32 v49, 0x42800000, v84
	ds_write2_b32 v43, v29, v49 offset0:164 offset1:230
	s_waitcnt vmcnt(11)
	v_mul_f32_e32 v29, 0x42800000, v85
	s_waitcnt vmcnt(10)
	v_mul_f32_e32 v49, 0x42800000, v86
	ds_write2_b32 v44, v29, v49 offset0:40 offset1:106
	s_waitcnt vmcnt(9)
	v_mul_f32_e32 v29, 0x42800000, v60
	s_waitcnt vmcnt(8)
	v_mul_f32_e32 v49, 0x42800000, v61
	ds_write2_b32 v44, v29, v49 offset0:172 offset1:238
	v_add_u32_e32 v84, s0, v32
	v_ashrrev_i32_e32 v85, 31, v84
	v_lshlrev_b64 v[84:85], 10, v[84:85]
	s_waitcnt vmcnt(7)
	v_mul_f32_e32 v29, 0x42800000, v62
	s_waitcnt vmcnt(6)
	v_mul_f32_e32 v49, 0x42800000, v50
	ds_write2_b32 v45, v29, v49 offset0:48 offset1:114
	s_waitcnt vmcnt(5)
	v_mul_f32_e32 v29, 0x42800000, v51
	s_waitcnt vmcnt(4)
	v_mul_f32_e32 v49, 0x42800000, v52
	ds_write2_b32 v45, v29, v49 offset0:180 offset1:246
	s_waitcnt vmcnt(3)
	v_mul_f32_e32 v29, 0x42800000, v53
	s_waitcnt vmcnt(2)
	v_mul_f32_e32 v49, 0x42800000, v54
	ds_write2_b32 v46, v29, v49 offset0:56 offset1:122
	v_mov_b32_e32 v49, 0
	v_mov_b32_e32 v50, 0
	s_waitcnt vmcnt(1)
	v_mul_f32_e32 v29, 0x42800000, v48
	s_waitcnt vmcnt(0)
	v_mul_f32_e32 v28, 0x42800000, v28
	ds_write2_b32 v46, v29, v28 offset0:188 offset1:254
	s_waitcnt lgkmcnt(0)
	ds_read2_b32 v[52:53], v33 offset1:16
	ds_read2_b32 v[54:55], v33 offset0:33 offset1:49
	ds_read2_b32 v[56:57], v33 offset0:66 offset1:82
	ds_read2_b32 v[58:59], v33 offset0:99 offset1:115
	ds_read2_b32 v[60:61], v33 offset0:132 offset1:148
	ds_read2_b32 v[62:63], v33 offset0:165 offset1:181
	ds_read2_b32 v[64:65], v33 offset0:198 offset1:214
	ds_read2_b32 v[66:67], v33 offset0:231 offset1:247
	ds_read2_b32 v[68:69], v47 offset0:8 offset1:24
	ds_read2_b32 v[70:71], v47 offset0:41 offset1:57
	ds_read2_b32 v[72:73], v47 offset0:74 offset1:90
	ds_read2_b32 v[74:75], v47 offset0:107 offset1:123
	ds_read2_b32 v[76:77], v47 offset0:140 offset1:156
	ds_read2_b32 v[78:79], v47 offset0:173 offset1:189
	v_mov_b32_e32 v48, 0
	ds_read2_b32 v[80:81], v47 offset0:206 offset1:222
	ds_read2_b32 v[82:83], v47 offset0:239 offset1:255
	v_mov_b32_e32 v51, 0
	s_waitcnt lgkmcnt(14)
	v_cvt_pk_fp8_f32 v48, v52, v54
	s_waitcnt lgkmcnt(10)
	v_cvt_pk_fp8_f32 v49, v60, v62
	s_waitcnt lgkmcnt(6)
	v_cvt_pk_fp8_f32 v50, v68, v70
	s_waitcnt lgkmcnt(2)
	v_cvt_pk_fp8_f32 v51, v76, v78
	v_cvt_pk_fp8_f32 v48, v56, v58 op_sel:[0,0,1]
	v_cvt_pk_fp8_f32 v49, v64, v66 op_sel:[0,0,1]
	v_cvt_pk_fp8_f32 v50, v72, v74 op_sel:[0,0,1]
	s_waitcnt lgkmcnt(0)
	v_cvt_pk_fp8_f32 v51, v80, v82 op_sel:[0,0,1]
	v_lshl_add_u64 v[28:29], v[18:19], 0, s[4:5]
	v_lshl_add_u64 v[84:85], v[28:29], 0, v[84:85]
	v_add_u32_e32 v52, s0, v34
	global_store_dwordx4 v[84:85], v[48:51], off
	s_nop 1
	v_mov_b32_e32 v48, 0
	v_mov_b32_e32 v49, 0
	v_mov_b32_e32 v50, 0
	v_mov_b32_e32 v51, 0
	v_cvt_pk_fp8_f32 v48, v53, v55
	v_cvt_pk_fp8_f32 v49, v61, v63
	v_cvt_pk_fp8_f32 v50, v69, v71
	v_cvt_pk_fp8_f32 v51, v77, v79
	v_cvt_pk_fp8_f32 v48, v57, v59 op_sel:[0,0,1]
	v_cvt_pk_fp8_f32 v49, v65, v67 op_sel:[0,0,1]
	v_cvt_pk_fp8_f32 v50, v73, v75 op_sel:[0,0,1]
	v_cvt_pk_fp8_f32 v51, v81, v83 op_sel:[0,0,1]
	v_ashrrev_i32_e32 v53, 31, v52
	v_lshlrev_b64 v[52:53], 10, v[52:53]
	v_lshl_add_u64 v[28:29], v[28:29], 0, v[52:53]
	global_store_dwordx4 v[28:29], v[48:51], off
	s_waitcnt lgkmcnt(0)

; __device__ __forceinline__ void tr_item(const float* W, int ld, int K, int nblk, int item, bf16* WT, bool gu, LAS float* scr, int lane) {
;     const int kb = item / nblk, nb = item % nblk, k0 = 64 * kb, n0 = 32 * nb;
;     int drow0 = n0;
;     if (gu) { const int bj = n0 / FF, j = n0 - bj * FF; drow0 = 256 * (j / 128) + 128 * bj + (j % 128); }
;     { float t_[32];
; #pragma unroll
;       for (int i = 0; i < 32; ++i) t_[i] = W[(size_t)(k0 + 2 * i + (lane >> 5)) * ld + n0 + (lane & 31)];
; #pragma unroll
;       for (int i = 0; i < 32; ++i) scr[(2 * i + (lane >> 5)) * 33 + (lane & 31)] = t_[i]; }
; __device__ __forceinline__ void convert_items(Frame& F, const Args& a, int lo, int hi, int w, int nw) {
;     ...
;         if (r < I_SO) { tr_item(a.in[12], D, D, 32, r, (bf16*)(F.ws + WS_WSWAOUT), false, scr, lane); continue; } r -= I_SO;
.LBB0_1313:
	s_andn2_b64 vcc, exec, s[4:5]
	s_cbranch_vccnz .LBB0_1315
	s_add_i32 s0, s11, 0x2000
	s_and_b32 s5, s0, 0x1ffc0
	s_and_b32 s4, s9, 0x3e0
	v_add_u32_e32 v28, s5, v30
	s_lshl_b32 s0, s4, 2
	v_ashrrev_i32_e32 v29, 31, v28
	v_lshl_add_u64 v[48:49], v[8:9], 0, s[0:1]
	v_lshlrev_b64 v[28:29], 12, v[28:29]
	v_lshl_add_u64 v[28:29], v[48:49], 0, v[28:29]
	v_add_co_u32_e32 v48, vcc, 0x2000, v28
	global_load_dword v50, v[28:29], off nt
	s_nop 0
	v_addc_co_u32_e32 v49, vcc, 0, v29, vcc
	global_load_dword v51, v[48:49], off nt
	v_add_co_u32_e32 v48, vcc, 0x4000, v28
	s_lshl_b32 s0, s5, 1
	s_nop 0
	v_addc_co_u32_e32 v49, vcc, 0, v29, vcc
	global_load_dword v52, v[48:49], off nt
	v_add_co_u32_e32 v48, vcc, 0x6000, v28
	s_nop 1
	v_addc_co_u32_e32 v49, vcc, 0, v29, vcc
	global_load_dword v53, v[48:49], off nt
	v_add_co_u32_e32 v48, vcc, 0x8000, v28
	s_nop 1
	v_addc_co_u32_e32 v49, vcc, 0, v29, vcc
	global_load_dword v54, v[48:49], off nt
	v_add_co_u32_e32 v48, vcc, 0xa000, v28
	s_nop 1
	v_addc_co_u32_e32 v49, vcc, 0, v29, vcc
	global_load_dword v55, v[48:49], off nt
	v_add_co_u32_e32 v48, vcc, 0xc000, v28
	s_nop 1
	v_addc_co_u32_e32 v49, vcc, 0, v29, vcc
	global_load_dword v56, v[48:49], off nt
	v_add_co_u32_e32 v48, vcc, 0xe000, v28
	s_nop 1
	v_addc_co_u32_e32 v49, vcc, 0, v29, vcc
	global_load_dword v57, v[48:49], off nt
	v_add_co_u32_e32 v48, vcc, 0x10000, v28
	s_nop 1
	v_addc_co_u32_e32 v49, vcc, 0, v29, vcc
	global_load_dword v58, v[48:49], off nt
	v_add_co_u32_e32 v48, vcc, 0x12000, v28
	s_nop 1
	v_addc_co_u32_e32 v49, vcc, 0, v29, vcc
	global_load_dword v59, v[48:49], off nt
	v_add_co_u32_e32 v48, vcc, 0x14000, v28
	s_nop 1
	v_addc_co_u32_e32 v49, vcc, 0, v29, vcc
	global_load_dword v60, v[48:49], off nt
	v_add_co_u32_e32 v48, vcc, 0x16000, v28
	s_nop 1
	v_addc_co_u32_e32 v49, vcc, 0, v29, vcc
	global_load_dword v61, v[48:49], off nt
	v_add_co_u32_e32 v48, vcc, 0x18000, v28
	s_nop 1
	v_addc_co_u32_e32 v49, vcc, 0, v29, vcc
	global_load_dword v62, v[48:49], off nt
	v_add_co_u32_e32 v48, vcc, 0x1a000, v28
	s_nop 1
	v_addc_co_u32_e32 v49, vcc, 0, v29, vcc
	global_load_dword v63, v[48:49], off nt
	v_add_co_u32_e32 v48, vcc, 0x1c000, v28
	s_nop 1
	v_addc_co_u32_e32 v49, vcc, 0, v29, vcc
	global_load_dword v64, v[48:49], off nt
	v_add_co_u32_e32 v48, vcc, 0x1e000, v28
	s_nop 1
	v_addc_co_u32_e32 v49, vcc, 0, v29, vcc
	global_load_dword v65, v[48:49], off nt
	v_add_co_u32_e32 v48, vcc, 0x20000, v28
	s_nop 1
	v_addc_co_u32_e32 v49, vcc, 0, v29, vcc
	global_load_dword v66, v[48:49], off nt
	v_add_co_u32_e32 v48, vcc, 0x22000, v28
	s_nop 1
	v_addc_co_u32_e32 v49, vcc, 0, v29, vcc
	global_load_dword v67, v[48:49], off nt
	v_add_co_u32_e32 v48, vcc, 0x24000, v28
	s_nop 1
	v_addc_co_u32_e32 v49, vcc, 0, v29, vcc
	global_load_dword v68, v[48:49], off nt
	v_add_co_u32_e32 v48, vcc, 0x26000, v28
	s_nop 1
	v_addc_co_u32_e32 v49, vcc, 0, v29, vcc
	global_load_dword v69, v[48:49], off nt
	v_add_co_u32_e32 v48, vcc, 0x28000, v28
	s_nop 1
	v_addc_co_u32_e32 v49, vcc, 0, v29, vcc
	global_load_dword v70, v[48:49], off nt
	v_add_co_u32_e32 v48, vcc, 0x2a000, v28
	s_nop 1
	v_addc_co_u32_e32 v49, vcc, 0, v29, vcc
	global_load_dword v71, v[48:49], off nt
	v_add_co_u32_e32 v48, vcc, 0x2c000, v28
	s_nop 1
	v_addc_co_u32_e32 v49, vcc, 0, v29, vcc
	global_load_dword v72, v[48:49], off nt
	v_add_co_u32_e32 v48, vcc, 0x2e000, v28
	s_nop 1
	v_addc_co_u32_e32 v49, vcc, 0, v29, vcc
	global_load_dword v73, v[48:49], off nt
	v_add_co_u32_e32 v48, vcc, 0x30000, v28
	s_nop 1
	v_addc_co_u32_e32 v49, vcc, 0, v29, vcc
	global_load_dword v74, v[48:49], off nt
	v_add_co_u32_e32 v48, vcc, 0x32000, v28
	s_nop 1
	v_addc_co_u32_e32 v49, vcc, 0, v29, vcc
	global_load_dword v75, v[48:49], off nt
	v_add_co_u32_e32 v48, vcc, 0x34000, v28
	s_nop 1
	v_addc_co_u32_e32 v49, vcc, 0, v29, vcc
	global_load_dword v76, v[48:49], off nt
	v_add_co_u32_e32 v48, vcc, 0x36000, v28
	s_nop 1
	v_addc_co_u32_e32 v49, vcc, 0, v29, vcc
	global_load_dword v77, v[48:49], off nt
	v_add_co_u32_e32 v48, vcc, 0x38000, v28
	s_nop 1
	v_addc_co_u32_e32 v49, vcc, 0, v29, vcc
	global_load_dword v78, v[48:49], off nt
	v_add_co_u32_e32 v48, vcc, 0x3a000, v28
	s_nop 1
	v_addc_co_u32_e32 v49, vcc, 0, v29, vcc
	global_load_dword v79, v[48:49], off nt
	v_add_co_u32_e32 v48, vcc, 0x3c000, v28
	s_nop 1
	v_addc_co_u32_e32 v49, vcc, 0, v29, vcc
	v_add_co_u32_e32 v28, vcc, 0x3e000, v28
	global_load_dword v48, v[48:49], off nt
	s_nop 0
	v_addc_co_u32_e32 v29, vcc, 0, v29, vcc
	global_load_dword v28, v[28:29], off nt
	s_waitcnt vmcnt(30)
	ds_write2_b32 v31, v50, v51 offset1:66
	s_waitcnt vmcnt(28)
	ds_write2_b32 v31, v52, v53 offset0:132 offset1:198
	s_waitcnt vmcnt(26)
	ds_write2_b32 v40, v54, v55 offset0:8 offset1:74
	s_waitcnt vmcnt(24)
	ds_write2_b32 v40, v56, v57 offset0:140 offset1:206
	s_waitcnt vmcnt(22)
	ds_write2_b32 v41, v58, v59 offset0:16 offset1:82
	s_waitcnt vmcnt(20)
	ds_write2_b32 v41, v60, v61 offset0:148 offset1:214
	s_waitcnt vmcnt(18)
	ds_write2_b32 v42, v62, v63 offset0:24 offset1:90
	s_waitcnt vmcnt(16)
	ds_write2_b32 v42, v64, v65 offset0:156 offset1:222
	s_waitcnt vmcnt(14)
	ds_write2_b32 v43, v66, v67 offset0:32 offset1:98
	s_waitcnt vmcnt(12)
	ds_write2_b32 v43, v68, v69 offset0:164 offset1:230
	s_waitcnt vmcnt(10)
	ds_write2_b32 v44, v70, v71 offset0:40 offset1:106
	s_waitcnt vmcnt(8)
; #define GAS __attribute__((address_space(1)))
; #define LAS __attribute__((address_space(3)))
; #define LDS_WAIT() asm volatile("s_waitcnt lgkmcnt(0)" ::: "memory")
; __device__ __forceinline__ unsigned pk2(float lo, float hi) { return f2bf(lo) | (f2bf(hi) << 16); }
; __device__ __forceinline__ void tr_item(const float* W, int ld, int K, int nblk, int item, bf16* WT, bool gu, LAS float* scr, int lane) {
;     ...
;       for (int i = 0; i < 32; ++i) scr[(2 * i + (lane >> 5)) * 33 + (lane & 31)] = t_[i]; }
;     LDS_WAIT(); asm volatile("" ::: "memory");
;     const int c = lane & 7;
; #pragma unroll
;     for (int j = 0; j < 4; ++j) { const int n = (lane >> 3) + 8 * j; const LAS float* s = scr + (8 * c) * 33 + n;
;         v4u o; o.x = pk2(s[0 * 33], s[1 * 33]); o.y = pk2(s[2 * 33], s[3 * 33]); o.z = pk2(s[4 * 33], s[5 * 33]); o.w = pk2(s[6 * 33], s[7 * 33]);
;         *(GAS v4u*)(WT + (size_t)(drow0 + n) * K + k0 + 8 * c) = o; }
;     LDS_WAIT(); asm volatile("" ::: "memory");
	ds_write2_b32 v44, v72, v73 offset0:172 offset1:238
	s_waitcnt vmcnt(6)
	ds_write2_b32 v45, v74, v75 offset0:48 offset1:114
	s_waitcnt vmcnt(4)
	ds_write2_b32 v45, v76, v77 offset0:180 offset1:246
	s_waitcnt vmcnt(2)
	ds_write2_b32 v46, v78, v79 offset0:56 offset1:122
	s_waitcnt vmcnt(0)
	ds_write2_b32 v46, v48, v28 offset0:188 offset1:254
	s_waitcnt lgkmcnt(0)
	ds_read2_b32 v[52:53], v36 offset0:33 offset1:41
	ds_read2_b32 v[54:55], v36 offset1:8
	ds_read2_b32 v[56:57], v36 offset0:66 offset1:74
	ds_read2_b32 v[58:59], v36 offset0:99 offset1:107
	ds_read2_b32 v[60:61], v36 offset0:132 offset1:140
	ds_read2_b32 v[62:63], v36 offset0:165 offset1:173
	ds_read2_b32 v[64:65], v36 offset0:198 offset1:206
	ds_read2_b32 v[66:67], v36 offset0:231 offset1:239
	s_waitcnt lgkmcnt(7)
	v_bfe_u32 v49, v52, 16, 1
	s_waitcnt lgkmcnt(6)
	v_bfe_u32 v48, v54, 16, 1
	v_add3_u32 v48, v54, v48, s15
	v_lshrrev_b32_e32 v48, 16, v48
	v_add3_u32 v49, v52, v49, s15
	v_and_or_b32 v48, v49, s16, v48
	s_waitcnt lgkmcnt(5)
	v_bfe_u32 v49, v56, 16, 1
	v_add3_u32 v49, v56, v49, s15
	s_waitcnt lgkmcnt(4)
	v_bfe_u32 v50, v58, 16, 1
	v_lshrrev_b32_e32 v49, 16, v49
	v_add3_u32 v50, v58, v50, s15
	v_and_or_b32 v49, v50, s16, v49
	s_waitcnt lgkmcnt(3)
	v_bfe_u32 v50, v60, 16, 1
	v_add3_u32 v50, v60, v50, s15
	s_waitcnt lgkmcnt(2)
	v_bfe_u32 v51, v62, 16, 1
	v_lshrrev_b32_e32 v50, 16, v50
	v_add3_u32 v51, v62, v51, s15
	v_and_or_b32 v50, v51, s16, v50
	s_waitcnt lgkmcnt(1)
	v_bfe_u32 v51, v64, 16, 1
	v_add_u32_e32 v68, s4, v35
	v_add3_u32 v51, v64, v51, s15
	s_waitcnt lgkmcnt(0)
	v_bfe_u32 v52, v66, 16, 1
	v_ashrrev_i32_e32 v69, 31, v68
	v_lshl_add_u64 v[28:29], v[20:21], 0, s[0:1]
	v_lshrrev_b32_e32 v51, 16, v51
	v_add3_u32 v52, v66, v52, s15
	v_lshlrev_b64 v[68:69], 11, v[68:69]
	v_and_or_b32 v51, v52, s16, v51
	v_lshl_add_u64 v[68:69], v[28:29], 0, v[68:69]
	global_store_dwordx4 v[68:69], v[48:51], off
	v_bfe_u32 v52, v67, 16, 1
	v_add3_u32 v52, v67, v52, s15
	v_bfe_u32 v48, v55, 16, 1
	v_add3_u32 v48, v55, v48, s15
	v_bfe_u32 v49, v53, 16, 1
	v_lshrrev_b32_e32 v48, 16, v48
	v_add3_u32 v49, v53, v49, s15
	v_and_or_b32 v48, v49, s16, v48
	v_bfe_u32 v49, v57, 16, 1
	v_add3_u32 v49, v57, v49, s15
	v_bfe_u32 v50, v59, 16, 1
	v_lshrrev_b32_e32 v49, 16, v49
	v_add3_u32 v50, v59, v50, s15
	v_and_or_b32 v49, v50, s16, v49
	v_bfe_u32 v50, v61, 16, 1
	v_add3_u32 v50, v61, v50, s15
	v_bfe_u32 v51, v63, 16, 1
	v_lshrrev_b32_e32 v50, 16, v50
	v_add3_u32 v51, v63, v51, s15
	v_and_or_b32 v50, v51, s16, v50
	v_bfe_u32 v51, v65, 16, 1
	v_add3_u32 v51, v65, v51, s15
	v_lshrrev_b32_e32 v51, 16, v51
	v_and_or_b32 v51, v52, s16, v51
	v_add_u32_e32 v52, s4, v37
	v_ashrrev_i32_e32 v53, 31, v52
	v_lshlrev_b64 v[52:53], 11, v[52:53]
	v_lshl_add_u64 v[52:53], v[28:29], 0, v[52:53]
	global_store_dwordx4 v[52:53], v[48:51], off
	ds_read2_b32 v[52:53], v36 offset0:49 offset1:57
	ds_read2_b32 v[54:55], v36 offset0:16 offset1:24
	ds_read2_b32 v[56:57], v36 offset0:82 offset1:90
	ds_read2_b32 v[58:59], v36 offset0:115 offset1:123
	ds_read2_b32 v[60:61], v36 offset0:148 offset1:156
	ds_read2_b32 v[62:63], v36 offset0:181 offset1:189
	ds_read2_b32 v[64:65], v36 offset0:214 offset1:222
	ds_read2_b32 v[66:67], v36 offset0:247 offset1:255
	s_waitcnt lgkmcnt(7)
	v_bfe_u32 v49, v52, 16, 1
	s_waitcnt lgkmcnt(6)
	v_bfe_u32 v48, v54, 16, 1
	v_add3_u32 v48, v54, v48, s15
	v_lshrrev_b32_e32 v48, 16, v48
	v_add3_u32 v49, v52, v49, s15
	v_and_or_b32 v48, v49, s16, v48
	s_waitcnt lgkmcnt(5)
	v_bfe_u32 v49, v56, 16, 1
	v_add3_u32 v49, v56, v49, s15
	s_waitcnt lgkmcnt(4)
	v_bfe_u32 v50, v58, 16, 1
	v_lshrrev_b32_e32 v49, 16, v49
	v_add3_u32 v50, v58, v50, s15
	v_and_or_b32 v49, v50, s16, v49
	s_waitcnt lgkmcnt(3)
	v_bfe_u32 v50, v60, 16, 1
	v_add3_u32 v50, v60, v50, s15
	s_waitcnt lgkmcnt(2)
	v_bfe_u32 v51, v62, 16, 1
	v_lshrrev_b32_e32 v50, 16, v50
	v_add3_u32 v51, v62, v51, s15
	v_and_or_b32 v50, v51, s16, v50
	s_waitcnt lgkmcnt(1)
	v_bfe_u32 v51, v64, 16, 1
	v_add_u32_e32 v68, s4, v38
	v_add3_u32 v51, v64, v51, s15
	s_waitcnt lgkmcnt(0)
	v_bfe_u32 v52, v66, 16, 1
	v_ashrrev_i32_e32 v69, 31, v68
	v_lshrrev_b32_e32 v51, 16, v51
	v_add3_u32 v52, v66, v52, s15
	v_lshlrev_b64 v[68:69], 11, v[68:69]
	v_and_or_b32 v51, v52, s16, v51
	v_lshl_add_u64 v[68:69], v[28:29], 0, v[68:69]
	global_store_dwordx4 v[68:69], v[48:51], off
	v_bfe_u32 v52, v67, 16, 1
	v_add3_u32 v52, v67, v52, s15
	v_bfe_u32 v48, v55, 16, 1
	v_add3_u32 v48, v55, v48, s15
	v_bfe_u32 v49, v53, 16, 1
	v_lshrrev_b32_e32 v48, 16, v48
	v_add3_u32 v49, v53, v49, s15
	v_and_or_b32 v48, v49, s16, v48
	v_bfe_u32 v49, v57, 16, 1
	v_add3_u32 v49, v57, v49, s15
	v_bfe_u32 v50, v59, 16, 1
	v_lshrrev_b32_e32 v49, 16, v49
	v_add3_u32 v50, v59, v50, s15
	v_and_or_b32 v49, v50, s16, v49
	v_bfe_u32 v50, v61, 16, 1
	v_add3_u32 v50, v61, v50, s15
	v_bfe_u32 v51, v63, 16, 1
	v_lshrrev_b32_e32 v50, 16, v50
	v_add3_u32 v51, v63, v51, s15
	v_and_or_b32 v50, v51, s16, v50
	v_bfe_u32 v51, v65, 16, 1
	v_add3_u32 v51, v65, v51, s15
	v_lshrrev_b32_e32 v51, 16, v51
	v_and_or_b32 v51, v52, s16, v51
	v_add_u32_e32 v52, s4, v39
	v_ashrrev_i32_e32 v53, 31, v52
	v_lshlrev_b64 v[52:53], 11, v[52:53]
	v_lshl_add_u64 v[28:29], v[28:29], 0, v[52:53]
	global_store_dwordx4 v[28:29], v[48:51], off
	s_waitcnt lgkmcnt(0)

; __device__ __forceinline__ void tr_item(const float* W, int ld, int K, int nblk, int item, bf16* WT, bool gu, LAS float* scr, int lane) {
;     const int kb = item / nblk, nb = item % nblk, k0 = 64 * kb, n0 = 32 * nb;
;     int drow0 = n0;
;     if (gu) { const int bj = n0 / FF, j = n0 - bj * FF; drow0 = 256 * (j / 128) + 128 * bj + (j % 128); }
;     { float t_[32];
; #pragma unroll
;       for (int i = 0; i < 32; ++i) t_[i] = W[(size_t)(k0 + 2 * i + (lane >> 5)) * ld + n0 + (lane & 31)];
; #pragma unroll
;       for (int i = 0; i < 32; ++i) scr[(2 * i + (lane >> 5)) * 33 + (lane & 31)] = t_[i]; }
; __device__ __forceinline__ void convert_items(Frame& F, const Args& a, int lo, int hi, int w, int nw) {
;     ...
;         if (r < I_SI) { tr_item(a.in[10], D + 512, D, 48, r, (bf16*)(F.ws + WS_WSWAIN), false, scr, lane); continue; } r -= I_SI;
.LBB0_1316:
	s_andn2_b64 vcc, exec, s[4:5]
	s_cbranch_vccnz .LBB0_1318
	s_add_i32 s0, s8, 0xf800
	s_and_b32 s4, s0, 0xffff
	s_mul_i32 s4, s4, 0xaaab
	s_lshr_b32 s5, s4, 21
	s_mul_i32 s4, s5, 48
	s_sub_i32 s0, s0, s4
	s_lshl_b32 s0, s0, 5
	s_and_b32 s4, s0, 0xffe0
	s_lshl_b32 s0, s4, 2
	v_lshl_add_u32 v50, s5, 6, v30
	v_lshl_add_u64 v[28:29], v[10:11], 0, s[0:1]
	v_mad_i64_i32 v[48:49], s[6:7], v50, s17, v[28:29]
	global_load_dword v51, v[48:49], off nt
	v_add_u32_e32 v48, 2, v50
	v_mad_i64_i32 v[48:49], s[6:7], v48, s17, v[28:29]
	global_load_dword v52, v[48:49], off nt
	v_add_u32_e32 v48, 4, v50
	v_mad_i64_i32 v[48:49], s[6:7], v48, s17, v[28:29]
	global_load_dword v53, v[48:49], off nt
	v_add_u32_e32 v48, 6, v50
	v_mad_i64_i32 v[48:49], s[6:7], v48, s17, v[28:29]
	global_load_dword v54, v[48:49], off nt
	v_add_u32_e32 v48, 8, v50
	v_mad_i64_i32 v[48:49], s[6:7], v48, s17, v[28:29]
	global_load_dword v55, v[48:49], off nt
	v_add_u32_e32 v48, 10, v50
	v_mad_i64_i32 v[48:49], s[6:7], v48, s17, v[28:29]
	global_load_dword v56, v[48:49], off nt
	v_add_u32_e32 v48, 12, v50
	v_mad_i64_i32 v[48:49], s[6:7], v48, s17, v[28:29]
	global_load_dword v57, v[48:49], off nt
	v_add_u32_e32 v48, 14, v50
	v_mad_i64_i32 v[48:49], s[6:7], v48, s17, v[28:29]
	global_load_dword v58, v[48:49], off nt
	v_add_u32_e32 v48, 16, v50
	v_mad_i64_i32 v[48:49], s[6:7], v48, s17, v[28:29]
	global_load_dword v59, v[48:49], off nt
	v_add_u32_e32 v48, 18, v50
	v_mad_i64_i32 v[48:49], s[6:7], v48, s17, v[28:29]
	global_load_dword v60, v[48:49], off nt
	v_add_u32_e32 v48, 20, v50
	v_mad_i64_i32 v[48:49], s[6:7], v48, s17, v[28:29]
	global_load_dword v61, v[48:49], off nt
	v_add_u32_e32 v48, 22, v50
	v_mad_i64_i32 v[48:49], s[6:7], v48, s17, v[28:29]
	global_load_dword v62, v[48:49], off nt
	v_add_u32_e32 v48, 24, v50
	v_mad_i64_i32 v[48:49], s[6:7], v48, s17, v[28:29]
	global_load_dword v63, v[48:49], off nt
	v_add_u32_e32 v48, 26, v50
	v_mad_i64_i32 v[48:49], s[6:7], v48, s17, v[28:29]
	global_load_dword v64, v[48:49], off nt
	v_add_u32_e32 v48, 28, v50
	v_mad_i64_i32 v[48:49], s[6:7], v48, s17, v[28:29]
	global_load_dword v65, v[48:49], off nt
	v_add_u32_e32 v48, 30, v50
	v_mad_i64_i32 v[48:49], s[6:7], v48, s17, v[28:29]
	global_load_dword v66, v[48:49], off nt
	v_add_u32_e32 v48, 32, v50
	v_mad_i64_i32 v[48:49], s[6:7], v48, s17, v[28:29]
	global_load_dword v67, v[48:49], off nt
	v_add_u32_e32 v48, 34, v50
	v_mad_i64_i32 v[48:49], s[6:7], v48, s17, v[28:29]
	global_load_dword v68, v[48:49], off nt
	v_add_u32_e32 v48, 36, v50
	v_mad_i64_i32 v[48:49], s[6:7], v48, s17, v[28:29]
	global_load_dword v69, v[48:49], off nt
	v_add_u32_e32 v48, 38, v50
	v_mad_i64_i32 v[48:49], s[6:7], v48, s17, v[28:29]
	global_load_dword v70, v[48:49], off nt
	v_add_u32_e32 v48, 40, v50
	v_mad_i64_i32 v[48:49], s[6:7], v48, s17, v[28:29]
	global_load_dword v71, v[48:49], off nt
	v_add_u32_e32 v48, 42, v50
	v_mad_i64_i32 v[48:49], s[6:7], v48, s17, v[28:29]
	global_load_dword v72, v[48:49], off nt
	v_add_u32_e32 v48, 44, v50
	v_mad_i64_i32 v[48:49], s[6:7], v48, s17, v[28:29]
	global_load_dword v73, v[48:49], off nt
	v_add_u32_e32 v48, 46, v50
	v_mad_i64_i32 v[48:49], s[6:7], v48, s17, v[28:29]
	global_load_dword v74, v[48:49], off nt
	v_add_u32_e32 v48, 48, v50
	v_mad_i64_i32 v[48:49], s[6:7], v48, s17, v[28:29]
	global_load_dword v75, v[48:49], off nt
	v_add_u32_e32 v48, 50, v50
	v_mad_i64_i32 v[48:49], s[6:7], v48, s17, v[28:29]
	global_load_dword v76, v[48:49], off nt
	v_add_u32_e32 v48, 52, v50
	v_mad_i64_i32 v[48:49], s[6:7], v48, s17, v[28:29]
	global_load_dword v77, v[48:49], off nt
	v_add_u32_e32 v48, 54, v50
	v_mad_i64_i32 v[48:49], s[6:7], v48, s17, v[28:29]
	global_load_dword v78, v[48:49], off nt
	v_add_u32_e32 v48, 56, v50
	v_mad_i64_i32 v[48:49], s[6:7], v48, s17, v[28:29]
	global_load_dword v79, v[48:49], off nt
	v_add_u32_e32 v48, 58, v50
	v_mad_i64_i32 v[48:49], s[6:7], v48, s17, v[28:29]
	global_load_dword v80, v[48:49], off nt
	v_add_u32_e32 v48, 60, v50
	v_mad_i64_i32 v[48:49], s[6:7], v48, s17, v[28:29]
	global_load_dword v48, v[48:49], off nt
	v_add_u32_e32 v49, 62, v50
	v_mad_i64_i32 v[28:29], s[6:7], v49, s17, v[28:29]
	global_load_dword v28, v[28:29], off nt
	s_waitcnt vmcnt(30)
	ds_write2_b32 v31, v51, v52 offset1:66
	s_waitcnt vmcnt(28)
	ds_write2_b32 v31, v53, v54 offset0:132 offset1:198
	s_waitcnt vmcnt(26)
	ds_write2_b32 v40, v55, v56 offset0:8 offset1:74
	s_waitcnt vmcnt(24)
	ds_write2_b32 v40, v57, v58 offset0:140 offset1:206
	s_waitcnt vmcnt(22)
	ds_write2_b32 v41, v59, v60 offset0:16 offset1:82
	s_waitcnt vmcnt(20)
	ds_write2_b32 v41, v61, v62 offset0:148 offset1:214
	s_waitcnt vmcnt(18)
	ds_write2_b32 v42, v63, v64 offset0:24 offset1:90
	s_waitcnt vmcnt(16)
	ds_write2_b32 v42, v65, v66 offset0:156 offset1:222
	s_waitcnt vmcnt(14)
	ds_write2_b32 v43, v67, v68 offset0:32 offset1:98
	s_waitcnt vmcnt(12)
	ds_write2_b32 v43, v69, v70 offset0:164 offset1:230
	s_waitcnt vmcnt(10)
	ds_write2_b32 v44, v71, v72 offset0:40 offset1:106
	s_waitcnt vmcnt(8)
	ds_write2_b32 v44, v73, v74 offset0:172 offset1:238
	s_waitcnt vmcnt(6)
	ds_write2_b32 v45, v75, v76 offset0:48 offset1:114
	s_waitcnt vmcnt(4)
; #define GAS __attribute__((address_space(1)))
; #define LAS __attribute__((address_space(3)))
; #define LDS_WAIT() asm volatile("s_waitcnt lgkmcnt(0)" ::: "memory")
; __device__ __forceinline__ unsigned pk2(float lo, float hi) { return f2bf(lo) | (f2bf(hi) << 16); }
; __device__ __forceinline__ void tr_item(const float* W, int ld, int K, int nblk, int item, bf16* WT, bool gu, LAS float* scr, int lane) {
;     ...
;       for (int i = 0; i < 32; ++i) scr[(2 * i + (lane >> 5)) * 33 + (lane & 31)] = t_[i]; }
;     LDS_WAIT(); asm volatile("" ::: "memory");
;     const int c = lane & 7;
; #pragma unroll
;     for (int j = 0; j < 4; ++j) { const int n = (lane >> 3) + 8 * j; const LAS float* s = scr + (8 * c) * 33 + n;
;         v4u o; o.x = pk2(s[0 * 33], s[1 * 33]); o.y = pk2(s[2 * 33], s[3 * 33]); o.z = pk2(s[4 * 33], s[5 * 33]); o.w = pk2(s[6 * 33], s[7 * 33]);
;         *(GAS v4u*)(WT + (size_t)(drow0 + n) * K + k0 + 8 * c) = o; }
;     LDS_WAIT(); asm volatile("" ::: "memory");
	ds_write2_b32 v45, v77, v78 offset0:180 offset1:246
	s_waitcnt vmcnt(2)
	ds_write2_b32 v46, v79, v80 offset0:56 offset1:122
	s_waitcnt vmcnt(0)
	ds_write2_b32 v46, v48, v28 offset0:188 offset1:254
	s_waitcnt lgkmcnt(0)
	ds_read2_b32 v[52:53], v36 offset0:33 offset1:41
	ds_read2_b32 v[54:55], v36 offset1:8
	ds_read2_b32 v[56:57], v36 offset0:66 offset1:74
	ds_read2_b32 v[58:59], v36 offset0:99 offset1:107
	ds_read2_b32 v[60:61], v36 offset0:132 offset1:140
	ds_read2_b32 v[62:63], v36 offset0:165 offset1:173
	ds_read2_b32 v[64:65], v36 offset0:198 offset1:206
	ds_read2_b32 v[66:67], v36 offset0:231 offset1:239
	s_waitcnt lgkmcnt(7)
	v_bfe_u32 v49, v52, 16, 1
	s_waitcnt lgkmcnt(6)
	v_bfe_u32 v48, v54, 16, 1
	v_add3_u32 v48, v54, v48, s15
	v_lshrrev_b32_e32 v48, 16, v48
	v_add3_u32 v49, v52, v49, s15
	v_and_or_b32 v48, v49, s16, v48
	s_waitcnt lgkmcnt(5)
	v_bfe_u32 v49, v56, 16, 1
	v_add3_u32 v49, v56, v49, s15
	s_waitcnt lgkmcnt(4)
	v_bfe_u32 v50, v58, 16, 1
	v_lshrrev_b32_e32 v49, 16, v49
	v_add3_u32 v50, v58, v50, s15
	v_and_or_b32 v49, v50, s16, v49
	s_waitcnt lgkmcnt(3)
	v_bfe_u32 v50, v60, 16, 1
	v_add3_u32 v50, v60, v50, s15
	s_waitcnt lgkmcnt(2)
	v_bfe_u32 v51, v62, 16, 1
	v_lshrrev_b32_e32 v50, 16, v50
	v_add3_u32 v51, v62, v51, s15
	v_and_or_b32 v50, v51, s16, v50
	s_waitcnt lgkmcnt(1)
	v_bfe_u32 v51, v64, 16, 1
	v_add_u32_e32 v68, s4, v35
	s_lshl_b32 s0, s5, 7
	v_add3_u32 v51, v64, v51, s15
	s_waitcnt lgkmcnt(0)
	v_bfe_u32 v52, v66, 16, 1
	v_ashrrev_i32_e32 v69, 31, v68
	v_lshl_add_u64 v[28:29], v[22:23], 0, s[0:1]
	v_lshrrev_b32_e32 v51, 16, v51
	v_add3_u32 v52, v66, v52, s15
	v_lshlrev_b64 v[68:69], 11, v[68:69]
	v_and_or_b32 v51, v52, s16, v51
	v_lshl_add_u64 v[68:69], v[28:29], 0, v[68:69]
	global_store_dwordx4 v[68:69], v[48:51], off
	v_bfe_u32 v52, v67, 16, 1
	v_add3_u32 v52, v67, v52, s15
	v_bfe_u32 v48, v55, 16, 1
	v_add3_u32 v48, v55, v48, s15
	v_bfe_u32 v49, v53, 16, 1
	v_lshrrev_b32_e32 v48, 16, v48
	v_add3_u32 v49, v53, v49, s15
	v_and_or_b32 v48, v49, s16, v48
	v_bfe_u32 v49, v57, 16, 1
	v_add3_u32 v49, v57, v49, s15
	v_bfe_u32 v50, v59, 16, 1
	v_lshrrev_b32_e32 v49, 16, v49
	v_add3_u32 v50, v59, v50, s15
	v_and_or_b32 v49, v50, s16, v49
	v_bfe_u32 v50, v61, 16, 1
	v_add3_u32 v50, v61, v50, s15
	v_bfe_u32 v51, v63, 16, 1
	v_lshrrev_b32_e32 v50, 16, v50
	v_add3_u32 v51, v63, v51, s15
	v_and_or_b32 v50, v51, s16, v50
	v_bfe_u32 v51, v65, 16, 1
	v_add3_u32 v51, v65, v51, s15
	v_lshrrev_b32_e32 v51, 16, v51
	v_and_or_b32 v51, v52, s16, v51
	v_add_u32_e32 v52, s4, v37
	v_ashrrev_i32_e32 v53, 31, v52
	v_lshlrev_b64 v[52:53], 11, v[52:53]
	v_lshl_add_u64 v[52:53], v[28:29], 0, v[52:53]
	global_store_dwordx4 v[52:53], v[48:51], off
	ds_read2_b32 v[52:53], v36 offset0:49 offset1:57
	ds_read2_b32 v[54:55], v36 offset0:16 offset1:24
	ds_read2_b32 v[56:57], v36 offset0:82 offset1:90
	ds_read2_b32 v[58:59], v36 offset0:115 offset1:123
	ds_read2_b32 v[60:61], v36 offset0:148 offset1:156
	ds_read2_b32 v[62:63], v36 offset0:181 offset1:189
	ds_read2_b32 v[64:65], v36 offset0:214 offset1:222
	ds_read2_b32 v[66:67], v36 offset0:247 offset1:255
	s_waitcnt lgkmcnt(7)
	v_bfe_u32 v49, v52, 16, 1
	s_waitcnt lgkmcnt(6)
	v_bfe_u32 v48, v54, 16, 1
	v_add3_u32 v48, v54, v48, s15
	v_lshrrev_b32_e32 v48, 16, v48
	v_add3_u32 v49, v52, v49, s15
	v_and_or_b32 v48, v49, s16, v48
	s_waitcnt lgkmcnt(5)
	v_bfe_u32 v49, v56, 16, 1
	v_add3_u32 v49, v56, v49, s15
	s_waitcnt lgkmcnt(4)
	v_bfe_u32 v50, v58, 16, 1
	v_lshrrev_b32_e32 v49, 16, v49
	v_add3_u32 v50, v58, v50, s15
	v_and_or_b32 v49, v50, s16, v49
	s_waitcnt lgkmcnt(3)
	v_bfe_u32 v50, v60, 16, 1
	v_add3_u32 v50, v60, v50, s15
	s_waitcnt lgkmcnt(2)
	v_bfe_u32 v51, v62, 16, 1
	v_lshrrev_b32_e32 v50, 16, v50
	v_add3_u32 v51, v62, v51, s15
	v_and_or_b32 v50, v51, s16, v50
	s_waitcnt lgkmcnt(1)
	v_bfe_u32 v51, v64, 16, 1
	v_add_u32_e32 v68, s4, v38
	v_add3_u32 v51, v64, v51, s15
	s_waitcnt lgkmcnt(0)
	v_bfe_u32 v52, v66, 16, 1
	v_ashrrev_i32_e32 v69, 31, v68
	v_lshrrev_b32_e32 v51, 16, v51
	v_add3_u32 v52, v66, v52, s15
	v_lshlrev_b64 v[68:69], 11, v[68:69]
	v_and_or_b32 v51, v52, s16, v51
	v_lshl_add_u64 v[68:69], v[28:29], 0, v[68:69]
	global_store_dwordx4 v[68:69], v[48:51], off
	v_bfe_u32 v52, v67, 16, 1
	v_add3_u32 v52, v67, v52, s15
	v_bfe_u32 v48, v55, 16, 1
	v_add3_u32 v48, v55, v48, s15
	v_bfe_u32 v49, v53, 16, 1
	v_lshrrev_b32_e32 v48, 16, v48
	v_add3_u32 v49, v53, v49, s15
	v_and_or_b32 v48, v49, s16, v48
	v_bfe_u32 v49, v57, 16, 1
	v_add3_u32 v49, v57, v49, s15
	v_bfe_u32 v50, v59, 16, 1
	v_lshrrev_b32_e32 v49, 16, v49
	v_add3_u32 v50, v59, v50, s15
	v_and_or_b32 v49, v50, s16, v49
	v_bfe_u32 v50, v61, 16, 1
	v_add3_u32 v50, v61, v50, s15
	v_bfe_u32 v51, v63, 16, 1
	v_lshrrev_b32_e32 v50, 16, v50
	v_add3_u32 v51, v63, v51, s15
	v_and_or_b32 v50, v51, s16, v50
	v_bfe_u32 v51, v65, 16, 1
	v_add3_u32 v51, v65, v51, s15
	v_lshrrev_b32_e32 v51, 16, v51
	v_and_or_b32 v51, v52, s16, v51
	v_add_u32_e32 v52, s4, v39
	v_ashrrev_i32_e32 v53, 31, v52
	v_lshlrev_b64 v[52:53], 11, v[52:53]
	v_lshl_add_u64 v[28:29], v[28:29], 0, v[52:53]
	global_store_dwordx4 v[28:29], v[48:51], off
	s_waitcnt lgkmcnt(0)

; #define LAS __attribute__((address_space(3)))
; __device__ __forceinline__ void tr_item(const float* W, int ld, int K, int nblk, int item, bf16* WT, bool gu, LAS float* scr, int lane) {
;     const int kb = item / nblk, nb = item % nblk, k0 = 64 * kb, n0 = 32 * nb;
;     int drow0 = n0;
;     if (gu) { const int bj = n0 / FF, j = n0 - bj * FF; drow0 = 256 * (j / 128) + 128 * bj + (j % 128); }
;     { float t_[32];
; #pragma unroll
;       for (int i = 0; i < 32; ++i) t_[i] = W[(size_t)(k0 + 2 * i + (lane >> 5)) * ld + n0 + (lane & 31)];
; #pragma unroll
;       for (int i = 0; i < 32; ++i) scr[(2 * i + (lane >> 5)) * 33 + (lane & 31)] = t_[i]; }
; __device__ __forceinline__ void convert_items(Frame& F, const Args& a, int lo, int hi, int w, int nw) {
;     ...
;         if (r < I_FO) { tr_item(a.in[9], D, D, 32, r, (bf16*)(F.ws + WS_WFOXOUT), false, scr, lane); continue; } r -= I_FO;
.LBB0_1319:
	s_andn2_b64 vcc, exec, s[4:5]
	s_cbranch_vccnz .LBB0_1321
	s_add_i32 s0, s11, 0x2a00
	s_and_b32 s5, s0, 0x1ffc0
	s_and_b32 s4, s9, 0x3e0
	v_add_u32_e32 v28, s5, v30
	s_lshl_b32 s0, s4, 2
	v_ashrrev_i32_e32 v29, 31, v28
	v_lshl_add_u64 v[48:49], v[12:13], 0, s[0:1]
	v_lshlrev_b64 v[28:29], 12, v[28:29]
	v_lshl_add_u64 v[28:29], v[48:49], 0, v[28:29]
	v_add_co_u32_e32 v48, vcc, 0x2000, v28
	global_load_dword v50, v[28:29], off nt
	s_nop 0
	v_addc_co_u32_e32 v49, vcc, 0, v29, vcc
	global_load_dword v51, v[48:49], off nt
	v_add_co_u32_e32 v48, vcc, 0x4000, v28
	s_lshl_b32 s0, s5, 1
	s_nop 0
	v_addc_co_u32_e32 v49, vcc, 0, v29, vcc
	global_load_dword v52, v[48:49], off nt
	v_add_co_u32_e32 v48, vcc, 0x6000, v28
	s_nop 1
	v_addc_co_u32_e32 v49, vcc, 0, v29, vcc
	global_load_dword v53, v[48:49], off nt
	v_add_co_u32_e32 v48, vcc, 0x8000, v28
	s_nop 1
	v_addc_co_u32_e32 v49, vcc, 0, v29, vcc
	global_load_dword v54, v[48:49], off nt
	v_add_co_u32_e32 v48, vcc, 0xa000, v28
	s_nop 1
	v_addc_co_u32_e32 v49, vcc, 0, v29, vcc
	global_load_dword v55, v[48:49], off nt
	v_add_co_u32_e32 v48, vcc, 0xc000, v28
	s_nop 1
	v_addc_co_u32_e32 v49, vcc, 0, v29, vcc
	global_load_dword v56, v[48:49], off nt
	v_add_co_u32_e32 v48, vcc, 0xe000, v28
	s_nop 1
	v_addc_co_u32_e32 v49, vcc, 0, v29, vcc
	global_load_dword v57, v[48:49], off nt
	v_add_co_u32_e32 v48, vcc, 0x10000, v28
	s_nop 1
	v_addc_co_u32_e32 v49, vcc, 0, v29, vcc
	global_load_dword v58, v[48:49], off nt
	v_add_co_u32_e32 v48, vcc, 0x12000, v28
	s_nop 1
	v_addc_co_u32_e32 v49, vcc, 0, v29, vcc
	global_load_dword v59, v[48:49], off nt
	v_add_co_u32_e32 v48, vcc, 0x14000, v28
	s_nop 1
	v_addc_co_u32_e32 v49, vcc, 0, v29, vcc
	global_load_dword v60, v[48:49], off nt
	v_add_co_u32_e32 v48, vcc, 0x16000, v28
	s_nop 1
	v_addc_co_u32_e32 v49, vcc, 0, v29, vcc
	global_load_dword v61, v[48:49], off nt
	v_add_co_u32_e32 v48, vcc, 0x18000, v28
	s_nop 1
	v_addc_co_u32_e32 v49, vcc, 0, v29, vcc
	global_load_dword v62, v[48:49], off nt
	v_add_co_u32_e32 v48, vcc, 0x1a000, v28
	s_nop 1
	v_addc_co_u32_e32 v49, vcc, 0, v29, vcc
	global_load_dword v63, v[48:49], off nt
	v_add_co_u32_e32 v48, vcc, 0x1c000, v28
	s_nop 1
	v_addc_co_u32_e32 v49, vcc, 0, v29, vcc
	global_load_dword v64, v[48:49], off nt
	v_add_co_u32_e32 v48, vcc, 0x1e000, v28
	s_nop 1
	v_addc_co_u32_e32 v49, vcc, 0, v29, vcc
	global_load_dword v65, v[48:49], off nt
	v_add_co_u32_e32 v48, vcc, 0x20000, v28
	s_nop 1
	v_addc_co_u32_e32 v49, vcc, 0, v29, vcc
	global_load_dword v66, v[48:49], off nt
	v_add_co_u32_e32 v48, vcc, 0x22000, v28
	s_nop 1
	v_addc_co_u32_e32 v49, vcc, 0, v29, vcc
	global_load_dword v67, v[48:49], off nt
	v_add_co_u32_e32 v48, vcc, 0x24000, v28
	s_nop 1
	v_addc_co_u32_e32 v49, vcc, 0, v29, vcc
	global_load_dword v68, v[48:49], off nt
	v_add_co_u32_e32 v48, vcc, 0x26000, v28
	s_nop 1
	v_addc_co_u32_e32 v49, vcc, 0, v29, vcc
	global_load_dword v69, v[48:49], off nt
	v_add_co_u32_e32 v48, vcc, 0x28000, v28
	s_nop 1
	v_addc_co_u32_e32 v49, vcc, 0, v29, vcc
	global_load_dword v70, v[48:49], off nt
	v_add_co_u32_e32 v48, vcc, 0x2a000, v28
	s_nop 1
	v_addc_co_u32_e32 v49, vcc, 0, v29, vcc
	global_load_dword v71, v[48:49], off nt
	v_add_co_u32_e32 v48, vcc, 0x2c000, v28
	s_nop 1
	v_addc_co_u32_e32 v49, vcc, 0, v29, vcc
	global_load_dword v72, v[48:49], off nt
	v_add_co_u32_e32 v48, vcc, 0x2e000, v28
	s_nop 1
	v_addc_co_u32_e32 v49, vcc, 0, v29, vcc
	global_load_dword v73, v[48:49], off nt
	v_add_co_u32_e32 v48, vcc, 0x30000, v28
	s_nop 1
	v_addc_co_u32_e32 v49, vcc, 0, v29, vcc
	global_load_dword v74, v[48:49], off nt
	v_add_co_u32_e32 v48, vcc, 0x32000, v28
	s_nop 1
	v_addc_co_u32_e32 v49, vcc, 0, v29, vcc
	global_load_dword v75, v[48:49], off nt
	v_add_co_u32_e32 v48, vcc, 0x34000, v28
	s_nop 1
	v_addc_co_u32_e32 v49, vcc, 0, v29, vcc
	global_load_dword v76, v[48:49], off nt
	v_add_co_u32_e32 v48, vcc, 0x36000, v28
	s_nop 1
	v_addc_co_u32_e32 v49, vcc, 0, v29, vcc
	global_load_dword v77, v[48:49], off nt
	v_add_co_u32_e32 v48, vcc, 0x38000, v28
	s_nop 1
	v_addc_co_u32_e32 v49, vcc, 0, v29, vcc
	global_load_dword v78, v[48:49], off nt
	v_add_co_u32_e32 v48, vcc, 0x3a000, v28
	s_nop 1
	v_addc_co_u32_e32 v49, vcc, 0, v29, vcc
	global_load_dword v79, v[48:49], off nt
	v_add_co_u32_e32 v48, vcc, 0x3c000, v28
	s_nop 1
	v_addc_co_u32_e32 v49, vcc, 0, v29, vcc
	v_add_co_u32_e32 v28, vcc, 0x3e000, v28
	global_load_dword v48, v[48:49], off nt
	s_nop 0
	v_addc_co_u32_e32 v29, vcc, 0, v29, vcc
	global_load_dword v28, v[28:29], off nt
	s_waitcnt vmcnt(30)
	ds_write2_b32 v31, v50, v51 offset1:66
	s_waitcnt vmcnt(28)
	ds_write2_b32 v31, v52, v53 offset0:132 offset1:198
	s_waitcnt vmcnt(26)
	ds_write2_b32 v40, v54, v55 offset0:8 offset1:74
	s_waitcnt vmcnt(24)
	ds_write2_b32 v40, v56, v57 offset0:140 offset1:206
	s_waitcnt vmcnt(22)
	ds_write2_b32 v41, v58, v59 offset0:16 offset1:82
	s_waitcnt vmcnt(20)
	ds_write2_b32 v41, v60, v61 offset0:148 offset1:214
	s_waitcnt vmcnt(18)
	ds_write2_b32 v42, v62, v63 offset0:24 offset1:90
	s_waitcnt vmcnt(16)
	ds_write2_b32 v42, v64, v65 offset0:156 offset1:222
	s_waitcnt vmcnt(14)
	ds_write2_b32 v43, v66, v67 offset0:32 offset1:98
	s_waitcnt vmcnt(12)
	ds_write2_b32 v43, v68, v69 offset0:164 offset1:230
	s_waitcnt vmcnt(10)
	ds_write2_b32 v44, v70, v71 offset0:40 offset1:106
	s_waitcnt vmcnt(8)
; #define GAS __attribute__((address_space(1)))
; #define LAS __attribute__((address_space(3)))
; #define LDS_WAIT() asm volatile("s_waitcnt lgkmcnt(0)" ::: "memory")
; __device__ __forceinline__ unsigned pk2(float lo, float hi) { return f2bf(lo) | (f2bf(hi) << 16); }
; __device__ __forceinline__ void tr_item(const float* W, int ld, int K, int nblk, int item, bf16* WT, bool gu, LAS float* scr, int lane) {
;     ...
;       for (int i = 0; i < 32; ++i) scr[(2 * i + (lane >> 5)) * 33 + (lane & 31)] = t_[i]; }
;     LDS_WAIT(); asm volatile("" ::: "memory");
;     const int c = lane & 7;
; #pragma unroll
;     for (int j = 0; j < 4; ++j) { const int n = (lane >> 3) + 8 * j; const LAS float* s = scr + (8 * c) * 33 + n;
;         v4u o; o.x = pk2(s[0 * 33], s[1 * 33]); o.y = pk2(s[2 * 33], s[3 * 33]); o.z = pk2(s[4 * 33], s[5 * 33]); o.w = pk2(s[6 * 33], s[7 * 33]);
;         *(GAS v4u*)(WT + (size_t)(drow0 + n) * K + k0 + 8 * c) = o; }
;     LDS_WAIT(); asm volatile("" ::: "memory");
	ds_write2_b32 v44, v72, v73 offset0:172 offset1:238
	s_waitcnt vmcnt(6)
	ds_write2_b32 v45, v74, v75 offset0:48 offset1:114
	s_waitcnt vmcnt(4)
	ds_write2_b32 v45, v76, v77 offset0:180 offset1:246
	s_waitcnt vmcnt(2)
	ds_write2_b32 v46, v78, v79 offset0:56 offset1:122
	s_waitcnt vmcnt(0)
	ds_write2_b32 v46, v48, v28 offset0:188 offset1:254
	s_waitcnt lgkmcnt(0)
	ds_read2_b32 v[52:53], v36 offset0:33 offset1:41
	ds_read2_b32 v[54:55], v36 offset1:8
	ds_read2_b32 v[56:57], v36 offset0:66 offset1:74
	ds_read2_b32 v[58:59], v36 offset0:99 offset1:107
	ds_read2_b32 v[60:61], v36 offset0:132 offset1:140
	ds_read2_b32 v[62:63], v36 offset0:165 offset1:173
	ds_read2_b32 v[64:65], v36 offset0:198 offset1:206
	ds_read2_b32 v[66:67], v36 offset0:231 offset1:239
	s_waitcnt lgkmcnt(7)
	v_bfe_u32 v49, v52, 16, 1
	s_waitcnt lgkmcnt(6)
	v_bfe_u32 v48, v54, 16, 1
	v_add3_u32 v48, v54, v48, s15
	v_lshrrev_b32_e32 v48, 16, v48
	v_add3_u32 v49, v52, v49, s15
	v_and_or_b32 v48, v49, s16, v48
	s_waitcnt lgkmcnt(5)
	v_bfe_u32 v49, v56, 16, 1
	v_add3_u32 v49, v56, v49, s15
	s_waitcnt lgkmcnt(4)
	v_bfe_u32 v50, v58, 16, 1
	v_lshrrev_b32_e32 v49, 16, v49
	v_add3_u32 v50, v58, v50, s15
	v_and_or_b32 v49, v50, s16, v49
	s_waitcnt lgkmcnt(3)
	v_bfe_u32 v50, v60, 16, 1
	v_add3_u32 v50, v60, v50, s15
	s_waitcnt lgkmcnt(2)
	v_bfe_u32 v51, v62, 16, 1
	v_lshrrev_b32_e32 v50, 16, v50
	v_add3_u32 v51, v62, v51, s15
	v_and_or_b32 v50, v51, s16, v50
	s_waitcnt lgkmcnt(1)
	v_bfe_u32 v51, v64, 16, 1
	v_add_u32_e32 v68, s4, v35
	v_add3_u32 v51, v64, v51, s15
	s_waitcnt lgkmcnt(0)
	v_bfe_u32 v52, v66, 16, 1
	v_ashrrev_i32_e32 v69, 31, v68
	v_lshl_add_u64 v[28:29], v[24:25], 0, s[0:1]
	v_lshrrev_b32_e32 v51, 16, v51
	v_add3_u32 v52, v66, v52, s15
	v_lshlrev_b64 v[68:69], 11, v[68:69]
	v_and_or_b32 v51, v52, s16, v51
	v_lshl_add_u64 v[68:69], v[28:29], 0, v[68:69]
	global_store_dwordx4 v[68:69], v[48:51], off
	v_bfe_u32 v52, v67, 16, 1
	v_add3_u32 v52, v67, v52, s15
	v_bfe_u32 v48, v55, 16, 1
	v_add3_u32 v48, v55, v48, s15
	v_bfe_u32 v49, v53, 16, 1
	v_lshrrev_b32_e32 v48, 16, v48
	v_add3_u32 v49, v53, v49, s15
	v_and_or_b32 v48, v49, s16, v48
	v_bfe_u32 v49, v57, 16, 1
	v_add3_u32 v49, v57, v49, s15
	v_bfe_u32 v50, v59, 16, 1
	v_lshrrev_b32_e32 v49, 16, v49
	v_add3_u32 v50, v59, v50, s15
	v_and_or_b32 v49, v50, s16, v49
	v_bfe_u32 v50, v61, 16, 1
	v_add3_u32 v50, v61, v50, s15
	v_bfe_u32 v51, v63, 16, 1
	v_lshrrev_b32_e32 v50, 16, v50
	v_add3_u32 v51, v63, v51, s15
	v_and_or_b32 v50, v51, s16, v50
	v_bfe_u32 v51, v65, 16, 1
	v_add3_u32 v51, v65, v51, s15
	v_lshrrev_b32_e32 v51, 16, v51
	v_and_or_b32 v51, v52, s16, v51
	v_add_u32_e32 v52, s4, v37
	v_ashrrev_i32_e32 v53, 31, v52
	v_lshlrev_b64 v[52:53], 11, v[52:53]
	v_lshl_add_u64 v[52:53], v[28:29], 0, v[52:53]
	global_store_dwordx4 v[52:53], v[48:51], off
	ds_read2_b32 v[52:53], v36 offset0:49 offset1:57
	ds_read2_b32 v[54:55], v36 offset0:16 offset1:24
	ds_read2_b32 v[56:57], v36 offset0:82 offset1:90
	ds_read2_b32 v[58:59], v36 offset0:115 offset1:123
	ds_read2_b32 v[60:61], v36 offset0:148 offset1:156
	ds_read2_b32 v[62:63], v36 offset0:181 offset1:189
	ds_read2_b32 v[64:65], v36 offset0:214 offset1:222
	ds_read2_b32 v[66:67], v36 offset0:247 offset1:255
	s_waitcnt lgkmcnt(7)
	v_bfe_u32 v49, v52, 16, 1
	s_waitcnt lgkmcnt(6)
	v_bfe_u32 v48, v54, 16, 1
	v_add3_u32 v48, v54, v48, s15
	v_lshrrev_b32_e32 v48, 16, v48
	v_add3_u32 v49, v52, v49, s15
	v_and_or_b32 v48, v49, s16, v48
	s_waitcnt lgkmcnt(5)
	v_bfe_u32 v49, v56, 16, 1
	v_add3_u32 v49, v56, v49, s15
	s_waitcnt lgkmcnt(4)
	v_bfe_u32 v50, v58, 16, 1
	v_lshrrev_b32_e32 v49, 16, v49
	v_add3_u32 v50, v58, v50, s15
	v_and_or_b32 v49, v50, s16, v49
	s_waitcnt lgkmcnt(3)
	v_bfe_u32 v50, v60, 16, 1
	v_add3_u32 v50, v60, v50, s15
	s_waitcnt lgkmcnt(2)
	v_bfe_u32 v51, v62, 16, 1
	v_lshrrev_b32_e32 v50, 16, v50
	v_add3_u32 v51, v62, v51, s15
	v_and_or_b32 v50, v51, s16, v50
	s_waitcnt lgkmcnt(1)
	v_bfe_u32 v51, v64, 16, 1
	v_add_u32_e32 v68, s4, v38
	v_add3_u32 v51, v64, v51, s15
	s_waitcnt lgkmcnt(0)
	v_bfe_u32 v52, v66, 16, 1
	v_ashrrev_i32_e32 v69, 31, v68
	v_lshrrev_b32_e32 v51, 16, v51
	v_add3_u32 v52, v66, v52, s15
	v_lshlrev_b64 v[68:69], 11, v[68:69]
	v_and_or_b32 v51, v52, s16, v51
	v_lshl_add_u64 v[68:69], v[28:29], 0, v[68:69]
	global_store_dwordx4 v[68:69], v[48:51], off
	v_bfe_u32 v52, v67, 16, 1
	v_add3_u32 v52, v67, v52, s15
	v_bfe_u32 v48, v55, 16, 1
	v_add3_u32 v48, v55, v48, s15
	v_bfe_u32 v49, v53, 16, 1
	v_lshrrev_b32_e32 v48, 16, v48
	v_add3_u32 v49, v53, v49, s15
	v_and_or_b32 v48, v49, s16, v48
	v_bfe_u32 v49, v57, 16, 1
	v_add3_u32 v49, v57, v49, s15
	v_bfe_u32 v50, v59, 16, 1
	v_lshrrev_b32_e32 v49, 16, v49
	v_add3_u32 v50, v59, v50, s15
	v_and_or_b32 v49, v50, s16, v49
	v_bfe_u32 v50, v61, 16, 1
	v_add3_u32 v50, v61, v50, s15
	v_bfe_u32 v51, v63, 16, 1
	v_lshrrev_b32_e32 v50, 16, v50
	v_add3_u32 v51, v63, v51, s15
	v_and_or_b32 v50, v51, s16, v50
	v_bfe_u32 v51, v65, 16, 1
	v_add3_u32 v51, v65, v51, s15
	v_lshrrev_b32_e32 v51, 16, v51
	v_and_or_b32 v51, v52, s16, v51
	v_add_u32_e32 v52, s4, v39
	v_ashrrev_i32_e32 v53, 31, v52
	v_lshlrev_b64 v[52:53], 11, v[52:53]
	v_lshl_add_u64 v[28:29], v[28:29], 0, v[52:53]
	global_store_dwordx4 v[28:29], v[48:51], off
	s_waitcnt lgkmcnt(0)

; #define LAS __attribute__((address_space(3)))
; __device__ __forceinline__ void tr_item(const float* W, int ld, int K, int nblk, int item, bf16* WT, bool gu, LAS float* scr, int lane) {
;     const int kb = item / nblk, nb = item % nblk, k0 = 64 * kb, n0 = 32 * nb;
;     int drow0 = n0;
;     if (gu) { const int bj = n0 / FF, j = n0 - bj * FF; drow0 = 256 * (j / 128) + 128 * bj + (j % 128); }
;     { float t_[32];
; #pragma unroll
;       for (int i = 0; i < 32; ++i) t_[i] = W[(size_t)(k0 + 2 * i + (lane >> 5)) * ld + n0 + (lane & 31)];
; #pragma unroll
;       for (int i = 0; i < 32; ++i) scr[(2 * i + (lane >> 5)) * 33 + (lane & 31)] = t_[i]; }
; __device__ __forceinline__ void convert_items(Frame& F, const Args& a, int lo, int hi, int w, int nw) {
;     ...
;         if (r < I_FI) { tr_item(a.in[7], 3 * D + 16, D, 96, r, (bf16*)(F.ws + WS_WFOXIN), false, scr, lane); continue; } r -= I_FI;
.LBB0_1322:
	s_andn2_b64 vcc, exec, s[4:5]
	s_cbranch_vccnz .LBB0_1295
	s_mul_hi_i32 s0, s8, 0x2aaaaaab
	s_lshr_b32 s4, s0, 31
	s_ashr_i32 s0, s0, 4
	s_add_i32 s0, s0, s4
	s_lshl_b32 s6, s0, 6
	s_mulk_i32 s0, 0xf400
	s_add_i32 s4, s9, s0
	s_ashr_i32 s5, s4, 31
	v_add_u32_e32 v50, s6, v30
	v_lshl_add_u64 v[28:29], s[4:5], 2, v[14:15]
	v_mad_i64_i32 v[48:49], s[40:41], v50, s30, v[28:29]
	global_load_dword v51, v[48:49], off nt
	v_add_u32_e32 v48, 2, v50
	v_mad_i64_i32 v[48:49], s[40:41], v48, s30, v[28:29]
	global_load_dword v52, v[48:49], off nt
	v_add_u32_e32 v48, 4, v50
	v_mad_i64_i32 v[48:49], s[40:41], v48, s30, v[28:29]
	global_load_dword v53, v[48:49], off nt
	v_add_u32_e32 v48, 6, v50
	v_mad_i64_i32 v[48:49], s[40:41], v48, s30, v[28:29]
	global_load_dword v54, v[48:49], off nt
	v_add_u32_e32 v48, 8, v50
	v_mad_i64_i32 v[48:49], s[40:41], v48, s30, v[28:29]
	global_load_dword v55, v[48:49], off nt
	v_add_u32_e32 v48, 10, v50
	v_mad_i64_i32 v[48:49], s[40:41], v48, s30, v[28:29]
	global_load_dword v56, v[48:49], off nt
	v_add_u32_e32 v48, 12, v50
	v_mad_i64_i32 v[48:49], s[40:41], v48, s30, v[28:29]
	global_load_dword v57, v[48:49], off nt
	v_add_u32_e32 v48, 14, v50
	v_mad_i64_i32 v[48:49], s[40:41], v48, s30, v[28:29]
	global_load_dword v58, v[48:49], off nt
	v_add_u32_e32 v48, 16, v50
	v_mad_i64_i32 v[48:49], s[40:41], v48, s30, v[28:29]
	global_load_dword v59, v[48:49], off nt
	v_add_u32_e32 v48, 18, v50
	v_mad_i64_i32 v[48:49], s[40:41], v48, s30, v[28:29]
	global_load_dword v60, v[48:49], off nt
	v_add_u32_e32 v48, 20, v50
	v_mad_i64_i32 v[48:49], s[40:41], v48, s30, v[28:29]
	global_load_dword v61, v[48:49], off nt
	v_add_u32_e32 v48, 22, v50
	v_mad_i64_i32 v[48:49], s[40:41], v48, s30, v[28:29]
	global_load_dword v62, v[48:49], off nt
	v_add_u32_e32 v48, 24, v50
	v_mad_i64_i32 v[48:49], s[40:41], v48, s30, v[28:29]
	global_load_dword v63, v[48:49], off nt
	v_add_u32_e32 v48, 26, v50
	v_mad_i64_i32 v[48:49], s[40:41], v48, s30, v[28:29]
	global_load_dword v64, v[48:49], off nt
	v_add_u32_e32 v48, 28, v50
	v_mad_i64_i32 v[48:49], s[40:41], v48, s30, v[28:29]
	global_load_dword v65, v[48:49], off nt
	v_add_u32_e32 v48, 30, v50
	v_mad_i64_i32 v[48:49], s[40:41], v48, s30, v[28:29]
	global_load_dword v66, v[48:49], off nt
	v_add_u32_e32 v48, 32, v50
	v_mad_i64_i32 v[48:49], s[40:41], v48, s30, v[28:29]
	global_load_dword v67, v[48:49], off nt
	v_add_u32_e32 v48, 34, v50
	v_mad_i64_i32 v[48:49], s[40:41], v48, s30, v[28:29]
	global_load_dword v68, v[48:49], off nt
	v_add_u32_e32 v48, 36, v50
	v_mad_i64_i32 v[48:49], s[40:41], v48, s30, v[28:29]
	global_load_dword v69, v[48:49], off nt
	v_add_u32_e32 v48, 38, v50
	v_mad_i64_i32 v[48:49], s[40:41], v48, s30, v[28:29]
	global_load_dword v70, v[48:49], off nt
	v_add_u32_e32 v48, 40, v50
	v_mad_i64_i32 v[48:49], s[40:41], v48, s30, v[28:29]
	global_load_dword v71, v[48:49], off nt
	v_add_u32_e32 v48, 42, v50
	v_mad_i64_i32 v[48:49], s[40:41], v48, s30, v[28:29]
	global_load_dword v72, v[48:49], off nt
	v_add_u32_e32 v48, 44, v50
	v_mad_i64_i32 v[48:49], s[40:41], v48, s30, v[28:29]
	global_load_dword v73, v[48:49], off nt
	v_add_u32_e32 v48, 46, v50
	v_mad_i64_i32 v[48:49], s[40:41], v48, s30, v[28:29]
	global_load_dword v74, v[48:49], off nt
	v_add_u32_e32 v48, 48, v50
	v_mad_i64_i32 v[48:49], s[40:41], v48, s30, v[28:29]
	global_load_dword v75, v[48:49], off nt
	v_add_u32_e32 v48, 50, v50
	v_mad_i64_i32 v[48:49], s[40:41], v48, s30, v[28:29]
	global_load_dword v76, v[48:49], off nt
	v_add_u32_e32 v48, 52, v50
	v_mad_i64_i32 v[48:49], s[40:41], v48, s30, v[28:29]
	global_load_dword v77, v[48:49], off nt
	v_add_u32_e32 v48, 54, v50
	v_mad_i64_i32 v[48:49], s[40:41], v48, s30, v[28:29]
	global_load_dword v78, v[48:49], off nt
	v_add_u32_e32 v48, 56, v50
	v_mad_i64_i32 v[48:49], s[40:41], v48, s30, v[28:29]
	global_load_dword v79, v[48:49], off nt
	v_add_u32_e32 v48, 58, v50
	v_mad_i64_i32 v[48:49], s[40:41], v48, s30, v[28:29]
	global_load_dword v80, v[48:49], off nt
	v_add_u32_e32 v48, 60, v50
	v_mad_i64_i32 v[48:49], s[40:41], v48, s30, v[28:29]
	global_load_dword v48, v[48:49], off nt
	v_add_u32_e32 v49, 62, v50
	v_mad_i64_i32 v[28:29], s[40:41], v49, s30, v[28:29]
	global_load_dword v28, v[28:29], off nt
	s_waitcnt vmcnt(30)
	ds_write2_b32 v31, v51, v52 offset1:66
	s_waitcnt vmcnt(28)
	ds_write2_b32 v31, v53, v54 offset0:132 offset1:198
	s_waitcnt vmcnt(26)
	ds_write2_b32 v40, v55, v56 offset0:8 offset1:74
	s_waitcnt vmcnt(24)
	ds_write2_b32 v40, v57, v58 offset0:140 offset1:206
	s_waitcnt vmcnt(22)
	ds_write2_b32 v41, v59, v60 offset0:16 offset1:82
	s_waitcnt vmcnt(20)
	ds_write2_b32 v41, v61, v62 offset0:148 offset1:214
	s_waitcnt vmcnt(18)
	ds_write2_b32 v42, v63, v64 offset0:24 offset1:90
	s_waitcnt vmcnt(16)
	ds_write2_b32 v42, v65, v66 offset0:156 offset1:222
	s_waitcnt vmcnt(14)
	ds_write2_b32 v43, v67, v68 offset0:32 offset1:98
	s_waitcnt vmcnt(12)
	ds_write2_b32 v43, v69, v70 offset0:164 offset1:230
	s_waitcnt vmcnt(10)
	ds_write2_b32 v44, v71, v72 offset0:40 offset1:106
	s_waitcnt vmcnt(8)
	ds_write2_b32 v44, v73, v74 offset0:172 offset1:238
	s_waitcnt vmcnt(6)
	ds_write2_b32 v45, v75, v76 offset0:48 offset1:114
	s_waitcnt vmcnt(4)
; #define GAS __attribute__((address_space(1)))
; #define LAS __attribute__((address_space(3)))
; #define LDS_WAIT() asm volatile("s_waitcnt lgkmcnt(0)" ::: "memory")
; __device__ __forceinline__ unsigned pk2(float lo, float hi) { return f2bf(lo) | (f2bf(hi) << 16); }
; __device__ __forceinline__ void tr_item(const float* W, int ld, int K, int nblk, int item, bf16* WT, bool gu, LAS float* scr, int lane) {
;     ...
;       for (int i = 0; i < 32; ++i) scr[(2 * i + (lane >> 5)) * 33 + (lane & 31)] = t_[i]; }
;     LDS_WAIT(); asm volatile("" ::: "memory");
;     const int c = lane & 7;
; #pragma unroll
;     for (int j = 0; j < 4; ++j) { const int n = (lane >> 3) + 8 * j; const LAS float* s = scr + (8 * c) * 33 + n;
;         v4u o; o.x = pk2(s[0 * 33], s[1 * 33]); o.y = pk2(s[2 * 33], s[3 * 33]); o.z = pk2(s[4 * 33], s[5 * 33]); o.w = pk2(s[6 * 33], s[7 * 33]);
;         *(GAS v4u*)(WT + (size_t)(drow0 + n) * K + k0 + 8 * c) = o; }
;     LDS_WAIT(); asm volatile("" ::: "memory");
	ds_write2_b32 v45, v77, v78 offset0:180 offset1:246
	s_waitcnt vmcnt(2)
	ds_write2_b32 v46, v79, v80 offset0:56 offset1:122
	s_waitcnt vmcnt(0)
	ds_write2_b32 v46, v48, v28 offset0:188 offset1:254
	s_waitcnt lgkmcnt(0)
	ds_read2_b32 v[52:53], v36 offset0:33 offset1:41
	ds_read2_b32 v[54:55], v36 offset1:8
	ds_read2_b32 v[56:57], v36 offset0:66 offset1:74
	ds_read2_b32 v[58:59], v36 offset0:99 offset1:107
	ds_read2_b32 v[60:61], v36 offset0:132 offset1:140
	ds_read2_b32 v[62:63], v36 offset0:165 offset1:173
	ds_read2_b32 v[64:65], v36 offset0:198 offset1:206
	ds_read2_b32 v[66:67], v36 offset0:231 offset1:239
	s_waitcnt lgkmcnt(7)
	v_bfe_u32 v49, v52, 16, 1
	s_waitcnt lgkmcnt(6)
	v_bfe_u32 v48, v54, 16, 1
	v_add3_u32 v48, v54, v48, s15
	v_lshrrev_b32_e32 v48, 16, v48
	v_add3_u32 v49, v52, v49, s15
	v_and_or_b32 v48, v49, s16, v48
	s_waitcnt lgkmcnt(5)
	v_bfe_u32 v49, v56, 16, 1
	v_add3_u32 v49, v56, v49, s15
	s_waitcnt lgkmcnt(4)
	v_bfe_u32 v50, v58, 16, 1
	v_lshrrev_b32_e32 v49, 16, v49
	v_add3_u32 v50, v58, v50, s15
	v_and_or_b32 v49, v50, s16, v49
	s_waitcnt lgkmcnt(3)
	v_bfe_u32 v50, v60, 16, 1
	v_add3_u32 v50, v60, v50, s15
	s_waitcnt lgkmcnt(2)
	v_bfe_u32 v51, v62, 16, 1
	v_lshrrev_b32_e32 v50, 16, v50
	v_add3_u32 v51, v62, v51, s15
	v_and_or_b32 v50, v51, s16, v50
	s_waitcnt lgkmcnt(1)
	v_bfe_u32 v51, v64, 16, 1
	v_add_u32_e32 v68, s4, v35
	s_ashr_i32 s7, s6, 31
	v_add3_u32 v51, v64, v51, s15
	s_waitcnt lgkmcnt(0)
	v_bfe_u32 v52, v66, 16, 1
	v_ashrrev_i32_e32 v69, 31, v68
	v_lshl_add_u64 v[28:29], s[6:7], 1, v[26:27]
	v_lshrrev_b32_e32 v51, 16, v51
	v_add3_u32 v52, v66, v52, s15
	v_lshlrev_b64 v[70:71], 11, v[68:69]
	v_and_or_b32 v51, v52, s16, v51
	v_lshl_add_u64 v[70:71], v[28:29], 0, v[70:71]
	global_store_dwordx4 v[70:71], v[48:51], off
	v_bfe_u32 v52, v67, 16, 1
	v_add3_u32 v52, v67, v52, s15
	v_bfe_u32 v48, v55, 16, 1
	v_add3_u32 v48, v55, v48, s15
	v_bfe_u32 v49, v53, 16, 1
	v_lshrrev_b32_e32 v48, 16, v48
	v_add3_u32 v49, v53, v49, s15
	v_and_or_b32 v48, v49, s16, v48
	v_bfe_u32 v49, v57, 16, 1
	v_add3_u32 v49, v57, v49, s15
	v_bfe_u32 v50, v59, 16, 1
	v_lshrrev_b32_e32 v49, 16, v49
	v_add3_u32 v50, v59, v50, s15
	v_and_or_b32 v49, v50, s16, v49
	v_bfe_u32 v50, v61, 16, 1
	v_add3_u32 v50, v61, v50, s15
	v_bfe_u32 v51, v63, 16, 1
	v_lshrrev_b32_e32 v50, 16, v50
	v_add3_u32 v51, v63, v51, s15
	v_and_or_b32 v50, v51, s16, v50
	v_bfe_u32 v51, v65, 16, 1
	v_add3_u32 v51, v65, v51, s15
	v_lshrrev_b32_e32 v51, 16, v51
	v_and_or_b32 v51, v52, s16, v51
	v_add_u32_e32 v52, 8, v68
	v_ashrrev_i32_e32 v53, 31, v52
	v_lshlrev_b64 v[52:53], 11, v[52:53]
	v_lshl_add_u64 v[52:53], v[28:29], 0, v[52:53]
	global_store_dwordx4 v[52:53], v[48:51], off
	ds_read2_b32 v[52:53], v36 offset0:49 offset1:57
	ds_read2_b32 v[54:55], v36 offset0:16 offset1:24
	ds_read2_b32 v[56:57], v36 offset0:82 offset1:90
	ds_read2_b32 v[58:59], v36 offset0:115 offset1:123
	ds_read2_b32 v[60:61], v36 offset0:148 offset1:156
	ds_read2_b32 v[62:63], v36 offset0:181 offset1:189
	ds_read2_b32 v[64:65], v36 offset0:214 offset1:222
	ds_read2_b32 v[66:67], v36 offset0:247 offset1:255
	s_waitcnt lgkmcnt(7)
	v_bfe_u32 v49, v52, 16, 1
	s_waitcnt lgkmcnt(6)
	v_bfe_u32 v48, v54, 16, 1
	v_add3_u32 v48, v54, v48, s15
	v_lshrrev_b32_e32 v48, 16, v48
	v_add3_u32 v49, v52, v49, s15
	v_and_or_b32 v48, v49, s16, v48
	s_waitcnt lgkmcnt(5)
	v_bfe_u32 v49, v56, 16, 1
	v_add3_u32 v49, v56, v49, s15
	s_waitcnt lgkmcnt(4)
	v_bfe_u32 v50, v58, 16, 1
	v_lshrrev_b32_e32 v49, 16, v49
	v_add3_u32 v50, v58, v50, s15
	v_and_or_b32 v49, v50, s16, v49
	s_waitcnt lgkmcnt(3)
	v_bfe_u32 v50, v60, 16, 1
	v_add3_u32 v50, v60, v50, s15
	s_waitcnt lgkmcnt(2)
	v_bfe_u32 v51, v62, 16, 1
	v_lshrrev_b32_e32 v50, 16, v50
	v_add3_u32 v51, v62, v51, s15
	v_and_or_b32 v50, v51, s16, v50
	s_waitcnt lgkmcnt(1)
	v_bfe_u32 v51, v64, 16, 1
	v_add_u32_e32 v70, 16, v68
	v_add3_u32 v51, v64, v51, s15
	s_waitcnt lgkmcnt(0)
	v_bfe_u32 v52, v66, 16, 1
	v_ashrrev_i32_e32 v71, 31, v70
	v_lshrrev_b32_e32 v51, 16, v51
	v_add3_u32 v52, v66, v52, s15
	v_lshlrev_b64 v[70:71], 11, v[70:71]
	v_and_or_b32 v51, v52, s16, v51
	v_lshl_add_u64 v[70:71], v[28:29], 0, v[70:71]
	global_store_dwordx4 v[70:71], v[48:51], off
	v_bfe_u32 v52, v67, 16, 1
	v_add3_u32 v52, v67, v52, s15
	v_bfe_u32 v48, v55, 16, 1
	v_add3_u32 v48, v55, v48, s15
	v_bfe_u32 v49, v53, 16, 1
	v_lshrrev_b32_e32 v48, 16, v48
	v_add3_u32 v49, v53, v49, s15
	v_and_or_b32 v48, v49, s16, v48
	v_bfe_u32 v49, v57, 16, 1
	v_add3_u32 v49, v57, v49, s15
	v_bfe_u32 v50, v59, 16, 1
	v_lshrrev_b32_e32 v49, 16, v49
	v_add3_u32 v50, v59, v50, s15
	v_and_or_b32 v49, v50, s16, v49
	v_bfe_u32 v50, v61, 16, 1
	v_add3_u32 v50, v61, v50, s15
	v_bfe_u32 v51, v63, 16, 1
	v_lshrrev_b32_e32 v50, 16, v50
	v_add3_u32 v51, v63, v51, s15
	v_and_or_b32 v50, v51, s16, v50
	v_bfe_u32 v51, v65, 16, 1
	v_add3_u32 v51, v65, v51, s15
	v_lshrrev_b32_e32 v51, 16, v51
	v_and_or_b32 v51, v52, s16, v51
	v_add_u32_e32 v52, 24, v68
	v_ashrrev_i32_e32 v53, 31, v52
	v_lshlrev_b64 v[52:53], 11, v[52:53]
	v_lshl_add_u64 v[28:29], v[28:29], 0, v[52:53]
	global_store_dwordx4 v[28:29], v[48:51], off
	s_waitcnt lgkmcnt(0)
	s_branch .LBB0_1295

; #define LAS __attribute__((address_space(3)))
; __device__ __forceinline__ void tr_item8(const float* W, int ld, int K, int nblk, int item, unsigned char* WT, bool gu, float scale, LAS float* scr, int lane) {
;     const int kb = item / nblk, nb = item % nblk, k0 = 64 * kb, n0 = 32 * nb;
;     int drow0 = n0;
;     if (gu) { const int bj = n0 / FF, j = n0 - bj * FF; drow0 = 256 * (j / 128) + 128 * bj + (j % 128); }
;     { float t_[32];
; #pragma unroll
;       for (int i = 0; i < 32; ++i) t_[i] = W[(size_t)(k0 + 2 * i + (lane >> 5)) * ld + n0 + (lane & 31)];
; __device__ __forceinline__ void convert_items(Frame& F, const Args& a, int lo, int hi, int w, int nw) {
;     ...
;     for (int it = lo + w; it < hi; it += nw) {
;         int r = it;
;         if (r < I_FI) { tr_item(a.in[7], 3 * D + 16, D, 96, r, (bf16*)(F.ws + WS_WFOXIN), false, scr, lane); continue; } r -= I_FI;
;         if (r < I_FO) { tr_item(a.in[9], D, D, 32, r, (bf16*)(F.ws + WS_WFOXOUT), false, scr, lane); continue; } r -= I_FO;
;         if (r < I_SI) { tr_item(a.in[10], D + 512, D, 48, r, (bf16*)(F.ws + WS_WSWAIN), false, scr, lane); continue; } r -= I_SI;
;         if (r < I_SO) { tr_item(a.in[12], D, D, 32, r, (bf16*)(F.ws + WS_WSWAOUT), false, scr, lane); continue; } r -= I_SO;
;         if (r < I_GU) { tr_item8(a.in[14], 2 * FF, D, 224, r, F.ws + WS_WGU, true, WSC_GU, scr, lane); continue; } r -= I_GU;
;         if (r < I_DN) { tr_item8(a.in[15], D, FF, 32, r, F.ws + WS_WDN, false, WSC_DN, scr, lane); continue; } r -= I_DN;
;         if (r < NE * I_GU) { const int e = r / I_GU, rr = r % I_GU; tr_item8(a.in[18] + (size_t)e * D * 2 * FF, 2 * FF, D, 224, rr, F.ws + WS_WMGU + (size_t)e * 2 * FF * D, true, WSC_GU, scr, lane); continue; } r -= NE * I_GU;
;         { const int e = r / I_DN, rr = r % I_DN; tr_item8(a.in[19] + (size_t)e * FF * D, D, FF, 32, rr, F.ws + WS_WMDN + (size_t)e * D * FF, false, WSC_DN, scr, lane); }
.LBB0_1330:
	s_cmpk_gt_i32 s8, 0x5ff
	s_mov_b64 s[4:5], -1
	s_cbranch_scc0 .LBB0_1356
	s_cmpk_gt_u32 s8, 0x7ff
	s_cbranch_scc0 .LBB0_1353
	s_cmpk_gt_u32 s8, 0xaff
	s_cbranch_scc0 .LBB0_1350
	s_cmpk_gt_u32 s8, 0xcff
	s_cbranch_scc0 .LBB0_1347
	s_cmpk_gt_u32 s8, 0x1aff
	s_cbranch_scc0 .LBB0_1344
	s_cmpk_gt_u32 s8, 0x21ff
	s_cbranch_scc0 .LBB0_1341
	s_cmpk_gt_u32 s8, 0x91ff
	s_cbranch_scc0 .LBB0_1338
	s_add_i32 s0, s8, 0x6e00
	s_bfe_u32 s4, s0, 0x80008
	s_mulk_i32 s4, 0x2493
	s_lshr_b32 s4, s4, 16
	s_mul_i32 s5, s4, 0x700
	v_readlane_b32 s40, v254, 28
	s_sub_i32 s6, s0, s5
	s_mul_i32 s0, s4, 0xe00000
	v_readlane_b32 s46, v254, 34
	v_readlane_b32 s47, v254, 35
	s_add_u32 s7, s46, s0
	s_addc_u32 s31, s47, 0
	s_mul_i32 s4, s4, 0x380000
	s_add_u32 s4, s66, s4
	s_addc_u32 s5, s58, 0
	s_lshl_b32 s0, s6, 5
	s_and_b32 s0, s0, 0x3e0
	s_lshl_b32 s6, s6, 1
	s_and_b32 s6, s6, 0xfc0
	s_lshl_b32 s40, s0, 2
	v_readlane_b32 s41, v254, 29
	v_add_u32_e32 v28, s6, v30
	s_add_u32 s40, s7, s40
	s_addc_u32 s41, s31, 0
	v_ashrrev_i32_e32 v29, 31, v28
	v_lshl_add_u64 v[48:49], s[40:41], 0, v[0:1]
	v_lshlrev_b64 v[28:29], 12, v[28:29]
	v_lshl_add_u64 v[28:29], v[48:49], 0, v[28:29]
	s_movk_i32 s7, 0x2000
	v_add_co_u32_e32 v48, vcc, s7, v28
	s_movk_i32 s7, 0x4000
	s_nop 0
	v_addc_co_u32_e32 v49, vcc, 0, v29, vcc
	global_load_dword v50, v[28:29], off nt
	global_load_dword v51, v[48:49], off nt
	v_add_co_u32_e32 v48, vcc, s7, v28
	s_movk_i32 s7, 0x6000
	s_nop 0
	v_addc_co_u32_e32 v49, vcc, 0, v29, vcc
	global_load_dword v52, v[48:49], off nt
	v_add_co_u32_e32 v48, vcc, s7, v28
	s_mov_b32 s7, 0x8000
	s_nop 0
	v_addc_co_u32_e32 v49, vcc, 0, v29, vcc
	global_load_dword v53, v[48:49], off nt
	v_add_co_u32_e32 v48, vcc, s7, v28
	s_mov_b32 s7, 0xa000
	s_nop 0
	v_addc_co_u32_e32 v49, vcc, 0, v29, vcc
	global_load_dword v54, v[48:49], off nt
	v_add_co_u32_e32 v48, vcc, s7, v28
	s_mov_b32 s7, 0xc000
	s_nop 0
	v_addc_co_u32_e32 v49, vcc, 0, v29, vcc
	global_load_dword v55, v[48:49], off nt
	v_add_co_u32_e32 v48, vcc, s7, v28
	s_mov_b32 s7, 0xe000
	s_nop 0
	v_addc_co_u32_e32 v49, vcc, 0, v29, vcc
	global_load_dword v56, v[48:49], off nt
	v_add_co_u32_e32 v48, vcc, s7, v28
	s_mov_b32 s7, 0x10000
	s_nop 0
	v_addc_co_u32_e32 v49, vcc, 0, v29, vcc
	global_load_dword v57, v[48:49], off nt
	v_add_co_u32_e32 v48, vcc, s7, v28
	s_mov_b32 s7, 0x12000
	s_nop 0
	v_addc_co_u32_e32 v49, vcc, 0, v29, vcc
	global_load_dword v58, v[48:49], off nt
	v_add_co_u32_e32 v48, vcc, s7, v28
	s_mov_b32 s7, 0x14000
	s_nop 0
	v_addc_co_u32_e32 v49, vcc, 0, v29, vcc
	global_load_dword v59, v[48:49], off nt
	v_add_co_u32_e32 v48, vcc, s7, v28
	s_mov_b32 s7, 0x16000
	s_nop 0
	v_addc_co_u32_e32 v49, vcc, 0, v29, vcc
	global_load_dword v60, v[48:49], off nt
	v_add_co_u32_e32 v48, vcc, s7, v28
	s_mov_b32 s7, 0x18000
	s_nop 0
	v_addc_co_u32_e32 v49, vcc, 0, v29, vcc
	global_load_dword v61, v[48:49], off nt
	v_add_co_u32_e32 v48, vcc, s7, v28
	s_mov_b32 s7, 0x1a000
	s_nop 0
	v_addc_co_u32_e32 v49, vcc, 0, v29, vcc
	global_load_dword v62, v[48:49], off nt
	v_add_co_u32_e32 v48, vcc, s7, v28
	s_mov_b32 s7, 0x1c000
	s_nop 0
	v_addc_co_u32_e32 v49, vcc, 0, v29, vcc
	global_load_dword v63, v[48:49], off nt
	v_add_co_u32_e32 v48, vcc, s7, v28
	s_mov_b32 s7, 0x1e000
	s_nop 0
	v_addc_co_u32_e32 v49, vcc, 0, v29, vcc
	global_load_dword v64, v[48:49], off nt
	v_add_co_u32_e32 v48, vcc, s7, v28
	s_mov_b32 s7, 0x20000
	s_nop 0
	v_addc_co_u32_e32 v49, vcc, 0, v29, vcc
	global_load_dword v65, v[48:49], off nt
	v_add_co_u32_e32 v48, vcc, s7, v28
	s_mov_b32 s7, 0x22000
	s_nop 0
	v_addc_co_u32_e32 v49, vcc, 0, v29, vcc
	global_load_dword v66, v[48:49], off nt
	v_add_co_u32_e32 v48, vcc, s7, v28
	s_mov_b32 s7, 0x24000
	s_nop 0
	v_addc_co_u32_e32 v49, vcc, 0, v29, vcc
	global_load_dword v67, v[48:49], off nt
	v_add_co_u32_e32 v48, vcc, s7, v28
	s_mov_b32 s7, 0x26000
	s_nop 0
	v_addc_co_u32_e32 v49, vcc, 0, v29, vcc
	global_load_dword v68, v[48:49], off nt
	v_add_co_u32_e32 v48, vcc, s7, v28
	s_mov_b32 s7, 0x28000
	s_nop 0
	v_addc_co_u32_e32 v49, vcc, 0, v29, vcc
	global_load_dword v69, v[48:49], off nt
	v_add_co_u32_e32 v48, vcc, s7, v28
	s_mov_b32 s7, 0x2a000
	s_nop 0
	v_addc_co_u32_e32 v49, vcc, 0, v29, vcc
	global_load_dword v70, v[48:49], off nt
	v_add_co_u32_e32 v48, vcc, s7, v28
	s_mov_b32 s7, 0x2c000
	s_nop 0
	v_addc_co_u32_e32 v49, vcc, 0, v29, vcc
	global_load_dword v71, v[48:49], off nt
	v_add_co_u32_e32 v48, vcc, s7, v28
	s_mov_b32 s7, 0x2e000
	s_nop 0
	v_addc_co_u32_e32 v49, vcc, 0, v29, vcc
	global_load_dword v72, v[48:49], off nt
	v_add_co_u32_e32 v48, vcc, s7, v28
	s_mov_b32 s7, 0x30000
	s_nop 0
	v_addc_co_u32_e32 v49, vcc, 0, v29, vcc
	global_load_dword v73, v[48:49], off nt
	v_add_co_u32_e32 v48, vcc, s7, v28
	s_mov_b32 s7, 0x32000
	s_nop 0
	v_addc_co_u32_e32 v49, vcc, 0, v29, vcc
	global_load_dword v74, v[48:49], off nt
	v_add_co_u32_e32 v48, vcc, s7, v28
	s_mov_b32 s7, 0x34000
	s_nop 0
	v_addc_co_u32_e32 v49, vcc, 0, v29, vcc
	global_load_dword v75, v[48:49], off nt
	v_add_co_u32_e32 v48, vcc, s7, v28
	s_mov_b32 s7, 0x36000
	s_nop 0
	v_addc_co_u32_e32 v49, vcc, 0, v29, vcc
	global_load_dword v76, v[48:49], off nt
	v_add_co_u32_e32 v48, vcc, s7, v28
	s_mov_b32 s7, 0x38000
	s_nop 0
	v_addc_co_u32_e32 v49, vcc, 0, v29, vcc
	global_load_dword v77, v[48:49], off nt
	v_add_co_u32_e32 v48, vcc, s7, v28
	s_mov_b32 s7, 0x3a000
	s_nop 0
	v_addc_co_u32_e32 v49, vcc, 0, v29, vcc
	global_load_dword v78, v[48:49], off nt
	v_add_co_u32_e32 v48, vcc, s7, v28
	s_mov_b32 s7, 0x3c000
	s_nop 0
	v_addc_co_u32_e32 v49, vcc, 0, v29, vcc
	global_load_dword v79, v[48:49], off nt
	v_add_co_u32_e32 v48, vcc, s7, v28
	s_mov_b32 s7, 0x3e000
	s_nop 0
	v_addc_co_u32_e32 v49, vcc, 0, v29, vcc
	v_add_co_u32_e32 v28, vcc, s7, v28
	global_load_dword v48, v[48:49], off nt
	s_nop 0
	v_addc_co_u32_e32 v29, vcc, 0, v29, vcc
	global_load_dword v28, v[28:29], off nt
	s_waitcnt vmcnt(0)
; __device__ __forceinline__ unsigned cvt_pk4_fp8(float a, float b, float c, float d) { int w = 0; w = __builtin_amdgcn_cvt_pk_fp8_f32(a, b, w, false); w = __builtin_amdgcn_cvt_pk_fp8_f32(c, d, w, true); return (unsigned)w; }
; #define GAS __attribute__((address_space(1)))
; #define LAS __attribute__((address_space(3)))
; #define LDS_WAIT() asm volatile("s_waitcnt lgkmcnt(0)" ::: "memory")
; __device__ __forceinline__ void tr_item8(const float* W, int ld, int K, int nblk, int item, unsigned char* WT, bool gu, float scale, LAS float* scr, int lane) {
;     ...
; #pragma unroll
;       for (int i = 0; i < 32; ++i) scr[(2 * i + (lane >> 5)) * 33 + (lane & 31)] = t_[i] * scale; }
;     LDS_WAIT(); asm volatile("" ::: "memory");
;     const int c = lane & 3;
; #pragma unroll
;     for (int j = 0; j < 2; ++j) { const int n = (lane >> 2) + 16 * j; const LAS float* sp = scr + (16 * c) * 33 + n;
;         v4u o; o.x = pg8::cvt_pk4_fp8(sp[0 * 33], sp[1 * 33], sp[2 * 33], sp[3 * 33]); o.y = pg8::cvt_pk4_fp8(sp[4 * 33], sp[5 * 33], sp[6 * 33], sp[7 * 33]);
;         o.z = pg8::cvt_pk4_fp8(sp[8 * 33], sp[9 * 33], sp[10 * 33], sp[11 * 33]); o.w = pg8::cvt_pk4_fp8(sp[12 * 33], sp[13 * 33], sp[14 * 33], sp[15 * 33]);
;         *(GAS v4u*)(WT + (size_t)(drow0 + n) * K + k0 + 16 * c) = o; }
;     LDS_WAIT(); asm volatile("" ::: "memory");
	v_mul_f32_e32 v29, 0x43000000, v50
	v_mul_f32_e32 v49, 0x43000000, v51
	ds_write2_b32 v31, v29, v49 offset1:66
	v_mul_f32_e32 v29, 0x43000000, v52
	v_mul_f32_e32 v49, 0x43000000, v53
	ds_write2_b32 v31, v29, v49 offset0:132 offset1:198
	v_mul_f32_e32 v29, 0x43000000, v54
	v_mul_f32_e32 v49, 0x43000000, v55
	ds_write2_b32 v40, v29, v49 offset0:8 offset1:74
	v_mul_f32_e32 v29, 0x43000000, v56
	v_mul_f32_e32 v49, 0x43000000, v57
	ds_write2_b32 v40, v29, v49 offset0:140 offset1:206
	v_mul_f32_e32 v29, 0x43000000, v58
	v_mul_f32_e32 v49, 0x43000000, v59
	ds_write2_b32 v41, v29, v49 offset0:16 offset1:82
	v_mul_f32_e32 v29, 0x43000000, v60
	v_mul_f32_e32 v49, 0x43000000, v61
	ds_write2_b32 v41, v29, v49 offset0:148 offset1:214
	v_mul_f32_e32 v29, 0x43000000, v62
	v_mul_f32_e32 v49, 0x43000000, v63
	ds_write2_b32 v42, v29, v49 offset0:24 offset1:90
	v_mul_f32_e32 v29, 0x43000000, v64
	v_mul_f32_e32 v49, 0x43000000, v65
	ds_write2_b32 v42, v29, v49 offset0:156 offset1:222
	v_mul_f32_e32 v29, 0x43000000, v66
	v_mul_f32_e32 v49, 0x43000000, v67
	ds_write2_b32 v43, v29, v49 offset0:32 offset1:98
	v_mul_f32_e32 v29, 0x43000000, v68
	v_mul_f32_e32 v49, 0x43000000, v69
	ds_write2_b32 v43, v29, v49 offset0:164 offset1:230
	v_mul_f32_e32 v29, 0x43000000, v70
	v_mul_f32_e32 v49, 0x43000000, v71
	ds_write2_b32 v44, v29, v49 offset0:40 offset1:106
	v_mul_f32_e32 v29, 0x43000000, v72
	v_mul_f32_e32 v49, 0x43000000, v73
	ds_write2_b32 v44, v29, v49 offset0:172 offset1:238
	v_mov_b32_e32 v50, v1
	v_mov_b32_e32 v51, v1
	v_mul_f32_e32 v29, 0x43000000, v74
	s_add_u32 s4, s4, s6
	s_addc_u32 s5, s5, 0
	v_readlane_b32 s42, v254, 30
	v_readlane_b32 s43, v254, 31
	v_readlane_b32 s44, v254, 32
	v_mul_f32_e32 v49, 0x43000000, v75
	ds_write2_b32 v45, v29, v49 offset0:48 offset1:114
	v_readlane_b32 s45, v254, 33
	v_mul_f32_e32 v29, 0x43000000, v76
	v_mul_f32_e32 v49, 0x43000000, v77
	ds_write2_b32 v45, v29, v49 offset0:180 offset1:246
	v_mul_f32_e32 v29, 0x43000000, v78
	v_mul_f32_e32 v49, 0x43000000, v79
	ds_write2_b32 v46, v29, v49 offset0:56 offset1:122
	v_mov_b32_e32 v49, v1
	v_mul_f32_e32 v29, 0x43000000, v48
	v_mov_b32_e32 v48, v1
	v_mul_f32_e32 v28, 0x43000000, v28
	ds_write2_b32 v46, v29, v28 offset0:188 offset1:254
	s_waitcnt lgkmcnt(0)
	ds_read2_b32 v[52:53], v33 offset1:16
	ds_read2_b32 v[54:55], v33 offset0:33 offset1:49
	ds_read2_b32 v[56:57], v33 offset0:66 offset1:82
	ds_read2_b32 v[58:59], v33 offset0:99 offset1:115
	ds_read2_b32 v[60:61], v33 offset0:132 offset1:148
	ds_read2_b32 v[62:63], v33 offset0:165 offset1:181
	ds_read2_b32 v[64:65], v33 offset0:198 offset1:214
	ds_read2_b32 v[66:67], v33 offset0:231 offset1:247
	ds_read2_b32 v[68:69], v47 offset0:8 offset1:24
	ds_read2_b32 v[70:71], v47 offset0:41 offset1:57
	ds_read2_b32 v[72:73], v47 offset0:74 offset1:90
	ds_read2_b32 v[74:75], v47 offset0:107 offset1:123
	ds_read2_b32 v[76:77], v47 offset0:140 offset1:156
	ds_read2_b32 v[78:79], v47 offset0:173 offset1:189
	ds_read2_b32 v[80:81], v47 offset0:206 offset1:222
	ds_read2_b32 v[82:83], v47 offset0:239 offset1:255
	s_waitcnt lgkmcnt(14)
	v_cvt_pk_fp8_f32 v48, v52, v54
	s_waitcnt lgkmcnt(10)
	v_cvt_pk_fp8_f32 v49, v60, v62
	s_waitcnt lgkmcnt(6)
	v_cvt_pk_fp8_f32 v50, v68, v70
	s_waitcnt lgkmcnt(2)
	v_cvt_pk_fp8_f32 v51, v76, v78
	v_cvt_pk_fp8_f32 v48, v56, v58 op_sel:[0,0,1]
	v_cvt_pk_fp8_f32 v49, v64, v66 op_sel:[0,0,1]
	v_cvt_pk_fp8_f32 v50, v72, v74 op_sel:[0,0,1]
	s_waitcnt lgkmcnt(0)
	v_cvt_pk_fp8_f32 v51, v80, v82 op_sel:[0,0,1]
	v_lshl_add_u64 v[28:29], s[4:5], 0, v[2:3]
	v_add_u32_e32 v52, s0, v32
	v_mad_i64_i32 v[84:85], s[4:5], v52, s13, v[28:29]
	global_store_dwordx4 v[84:85], v[48:51], off
	v_add_u32_e32 v52, s0, v34
	v_mad_i64_i32 v[28:29], s[4:5], v52, s13, v[28:29]
	v_mov_b32_e32 v48, v1
	v_mov_b32_e32 v49, v1
	v_mov_b32_e32 v50, v1
	v_mov_b32_e32 v51, v1
	v_cvt_pk_fp8_f32 v48, v53, v55
	v_cvt_pk_fp8_f32 v49, v61, v63
	v_cvt_pk_fp8_f32 v50, v69, v71
	v_cvt_pk_fp8_f32 v51, v77, v79
	v_cvt_pk_fp8_f32 v48, v57, v59 op_sel:[0,0,1]
	v_cvt_pk_fp8_f32 v49, v65, v67 op_sel:[0,0,1]
	v_cvt_pk_fp8_f32 v50, v73, v75 op_sel:[0,0,1]
	v_cvt_pk_fp8_f32 v51, v81, v83 op_sel:[0,0,1]
	s_mov_b64 s[4:5], 0
	global_store_dwordx4 v[28:29], v[48:51], off
	s_waitcnt lgkmcnt(0)
; #define LAS __attribute__((address_space(3)))
; __device__ __forceinline__ void tr_item8(const float* W, int ld, int K, int nblk, int item, unsigned char* WT, bool gu, float scale, LAS float* scr, int lane) {
;     const int kb = item / nblk, nb = item % nblk, k0 = 64 * kb, n0 = 32 * nb;
;     int drow0 = n0;
;     if (gu) { const int bj = n0 / FF, j = n0 - bj * FF; drow0 = 256 * (j / 128) + 128 * bj + (j % 128); }
;     { float t_[32];
; #pragma unroll
;       for (int i = 0; i < 32; ++i) t_[i] = W[(size_t)(k0 + 2 * i + (lane >> 5)) * ld + n0 + (lane & 31)];
; __device__ __forceinline__ void convert_items(Frame& F, const Args& a, int lo, int hi, int w, int nw) {
;     ...
;         if (r < NE * I_GU) { const int e = r / I_GU, rr = r % I_GU; tr_item8(a.in[18] + (size_t)e * D * 2 * FF, 2 * FF, D, 224, rr, F.ws + WS_WMGU + (size_t)e * 2 * FF * D, true, WSC_GU, scr, lane); continue; } r -= NE * I_GU;
.LBB0_1338:
	s_andn2_b64 vcc, exec, s[4:5]
	s_cbranch_vccnz .LBB0_1340
	s_add_i32 s0, s8, 0xde00
	s_bfe_u32 s4, s0, 0x70009
	s_mulk_i32 s4, 0x2493
	s_lshr_b32 s4, s4, 16
	s_mul_i32 s5, s4, 0xe00
	v_readlane_b32 s40, v254, 28
	s_sub_i32 s0, s0, s5
	s_mul_i32 s5, s4, 0x1c00000
	v_readlane_b32 s44, v254, 32
	v_readlane_b32 s45, v254, 33
	s_add_u32 s7, s44, s5
	s_addc_u32 s31, s45, 0
	s_mul_i32 s4, s4, 0x700000
	s_add_u32 s4, s36, s4
	s_addc_u32 s5, s37, 0
	s_bfe_u32 s6, s0, 0xb0005
	s_mulk_i32 s6, 0x2493
	s_lshr_b32 s6, s6, 16
	s_mul_i32 s40, s6, 0xe0
	v_readlane_b32 s41, v254, 29
	s_sub_i32 s40, s0, s40
	s_lshl_b32 s0, s40, 5
	s_and_b32 s41, s40, 0xffff
	s_cmpk_gt_u32 s41, 0x6f
	v_readlane_b32 s42, v254, 30
	s_cselect_b32 s41, 0xfffff200, 0
	s_cselect_b32 s42, 0x80, 0
	s_add_i32 s0, s41, s0
	s_sext_i32_i16 s41, s0
	s_bfe_u32 s41, s41, 0x70018
	v_readlane_b32 s43, v254, 31
	s_add_i32 s41, s0, s41
	s_sext_i32_i16 s43, s41
	s_and_b32 s41, s41, 0xff80
	s_sub_i32 s0, s0, s41
	s_lshl_b32 s43, s43, 1
	s_sext_i32_i16 s0, s0
	s_and_b32 s43, s43, 0xffffff00
	s_add_i32 s0, s42, s0
	s_lshl_b32 s40, s40, 7
	s_add_i32 s0, s0, s43
	s_lshl_b32 s6, s6, 6
	s_and_b32 s40, s40, 0x3ff80
	s_add_u32 s40, s7, s40
	s_addc_u32 s41, s31, 0
	v_add_u32_e32 v50, s6, v30
	v_lshl_add_u64 v[28:29], s[40:41], 0, v[0:1]
	v_mad_i64_i32 v[48:49], s[40:41], v50, s14, v[28:29]
	global_load_dword v51, v[48:49], off nt
	v_add_u32_e32 v48, 2, v50
	v_mad_i64_i32 v[48:49], s[40:41], v48, s14, v[28:29]
	global_load_dword v52, v[48:49], off nt
	v_add_u32_e32 v48, 4, v50
	v_mad_i64_i32 v[48:49], s[40:41], v48, s14, v[28:29]
	global_load_dword v53, v[48:49], off nt
	v_add_u32_e32 v48, 6, v50
	v_mad_i64_i32 v[48:49], s[40:41], v48, s14, v[28:29]
	global_load_dword v54, v[48:49], off nt
	v_add_u32_e32 v48, 8, v50
	v_mad_i64_i32 v[48:49], s[40:41], v48, s14, v[28:29]
	global_load_dword v55, v[48:49], off nt
	v_add_u32_e32 v48, 10, v50
	v_mad_i64_i32 v[48:49], s[40:41], v48, s14, v[28:29]
	global_load_dword v56, v[48:49], off nt
	v_add_u32_e32 v48, 12, v50
	v_mad_i64_i32 v[48:49], s[40:41], v48, s14, v[28:29]
	global_load_dword v57, v[48:49], off nt
	v_add_u32_e32 v48, 14, v50
	v_mad_i64_i32 v[48:49], s[40:41], v48, s14, v[28:29]
	global_load_dword v58, v[48:49], off nt
	v_add_u32_e32 v48, 16, v50
	v_mad_i64_i32 v[48:49], s[40:41], v48, s14, v[28:29]
	global_load_dword v59, v[48:49], off nt
	v_add_u32_e32 v48, 18, v50
	v_mad_i64_i32 v[48:49], s[40:41], v48, s14, v[28:29]
	global_load_dword v60, v[48:49], off nt
	v_add_u32_e32 v48, 20, v50
	v_mad_i64_i32 v[48:49], s[40:41], v48, s14, v[28:29]
	global_load_dword v61, v[48:49], off nt
	v_add_u32_e32 v48, 22, v50
	v_mad_i64_i32 v[48:49], s[40:41], v48, s14, v[28:29]
	global_load_dword v62, v[48:49], off nt
	v_add_u32_e32 v48, 24, v50
	v_mad_i64_i32 v[48:49], s[40:41], v48, s14, v[28:29]
	global_load_dword v63, v[48:49], off nt
	v_add_u32_e32 v48, 26, v50
	v_mad_i64_i32 v[48:49], s[40:41], v48, s14, v[28:29]
	global_load_dword v64, v[48:49], off nt
	v_add_u32_e32 v48, 28, v50
	v_mad_i64_i32 v[48:49], s[40:41], v48, s14, v[28:29]
	global_load_dword v65, v[48:49], off nt
	v_add_u32_e32 v48, 30, v50
	v_mad_i64_i32 v[48:49], s[40:41], v48, s14, v[28:29]
	global_load_dword v66, v[48:49], off nt
	v_add_u32_e32 v48, 32, v50
	v_mad_i64_i32 v[48:49], s[40:41], v48, s14, v[28:29]
	global_load_dword v67, v[48:49], off nt
	v_add_u32_e32 v48, 34, v50
	v_mad_i64_i32 v[48:49], s[40:41], v48, s14, v[28:29]
	global_load_dword v68, v[48:49], off nt
	v_add_u32_e32 v48, 36, v50
	v_mad_i64_i32 v[48:49], s[40:41], v48, s14, v[28:29]
	global_load_dword v69, v[48:49], off nt
	v_add_u32_e32 v48, 38, v50
	v_mad_i64_i32 v[48:49], s[40:41], v48, s14, v[28:29]
	global_load_dword v70, v[48:49], off nt
	v_add_u32_e32 v48, 40, v50
	v_mad_i64_i32 v[48:49], s[40:41], v48, s14, v[28:29]
	global_load_dword v71, v[48:49], off nt
	v_add_u32_e32 v48, 42, v50
	v_mad_i64_i32 v[48:49], s[40:41], v48, s14, v[28:29]
	global_load_dword v72, v[48:49], off nt
	v_add_u32_e32 v48, 44, v50
	v_mad_i64_i32 v[48:49], s[40:41], v48, s14, v[28:29]
	global_load_dword v73, v[48:49], off nt
	v_add_u32_e32 v48, 46, v50
	v_mad_i64_i32 v[48:49], s[40:41], v48, s14, v[28:29]
	global_load_dword v74, v[48:49], off nt
	v_add_u32_e32 v48, 48, v50
	v_mad_i64_i32 v[48:49], s[40:41], v48, s14, v[28:29]
	global_load_dword v75, v[48:49], off nt
	v_add_u32_e32 v48, 50, v50
	v_mad_i64_i32 v[48:49], s[40:41], v48, s14, v[28:29]
	global_load_dword v76, v[48:49], off nt
	v_add_u32_e32 v48, 52, v50
	v_mad_i64_i32 v[48:49], s[40:41], v48, s14, v[28:29]
	global_load_dword v77, v[48:49], off nt
	v_add_u32_e32 v48, 54, v50
	v_mad_i64_i32 v[48:49], s[40:41], v48, s14, v[28:29]
	global_load_dword v78, v[48:49], off nt
	v_add_u32_e32 v48, 56, v50
	v_mad_i64_i32 v[48:49], s[40:41], v48, s14, v[28:29]
	global_load_dword v79, v[48:49], off nt
	v_add_u32_e32 v48, 58, v50
	v_mad_i64_i32 v[48:49], s[40:41], v48, s14, v[28:29]
	global_load_dword v80, v[48:49], off nt
	v_add_u32_e32 v48, 60, v50
	v_mad_i64_i32 v[48:49], s[40:41], v48, s14, v[28:29]
	global_load_dword v48, v[48:49], off nt
	v_add_u32_e32 v49, 62, v50
	v_mad_i64_i32 v[28:29], s[40:41], v49, s14, v[28:29]
	global_load_dword v28, v[28:29], off nt
	s_waitcnt vmcnt(0)
; __device__ __forceinline__ unsigned cvt_pk4_fp8(float a, float b, float c, float d) { int w = 0; w = __builtin_amdgcn_cvt_pk_fp8_f32(a, b, w, false); w = __builtin_amdgcn_cvt_pk_fp8_f32(c, d, w, true); return (unsigned)w; }
; #define GAS __attribute__((address_space(1)))
; #define LAS __attribute__((address_space(3)))
; #define LDS_WAIT() asm volatile("s_waitcnt lgkmcnt(0)" ::: "memory")
; __device__ __forceinline__ void tr_item8(const float* W, int ld, int K, int nblk, int item, unsigned char* WT, bool gu, float scale, LAS float* scr, int lane) {
;     ...
; #pragma unroll
;       for (int i = 0; i < 32; ++i) scr[(2 * i + (lane >> 5)) * 33 + (lane & 31)] = t_[i] * scale; }
;     LDS_WAIT(); asm volatile("" ::: "memory");
;     const int c = lane & 3;
; #pragma unroll
;     for (int j = 0; j < 2; ++j) { const int n = (lane >> 2) + 16 * j; const LAS float* sp = scr + (16 * c) * 33 + n;
;         v4u o; o.x = pg8::cvt_pk4_fp8(sp[0 * 33], sp[1 * 33], sp[2 * 33], sp[3 * 33]); o.y = pg8::cvt_pk4_fp8(sp[4 * 33], sp[5 * 33], sp[6 * 33], sp[7 * 33]);
;         o.z = pg8::cvt_pk4_fp8(sp[8 * 33], sp[9 * 33], sp[10 * 33], sp[11 * 33]); o.w = pg8::cvt_pk4_fp8(sp[12 * 33], sp[13 * 33], sp[14 * 33], sp[15 * 33]);
;         *(GAS v4u*)(WT + (size_t)(drow0 + n) * K + k0 + 16 * c) = o; }
;     LDS_WAIT(); asm volatile("" ::: "memory");
	v_mul_f32_e32 v29, 0x42800000, v51
	v_mul_f32_e32 v49, 0x42800000, v52
	ds_write2_b32 v31, v29, v49 offset1:66
	v_mul_f32_e32 v29, 0x42800000, v53
	v_mul_f32_e32 v49, 0x42800000, v54
	ds_write2_b32 v31, v29, v49 offset0:132 offset1:198
	v_mul_f32_e32 v29, 0x42800000, v55
	v_mul_f32_e32 v49, 0x42800000, v56
	ds_write2_b32 v40, v29, v49 offset0:8 offset1:74
	v_mul_f32_e32 v29, 0x42800000, v57
	v_mul_f32_e32 v49, 0x42800000, v58
	ds_write2_b32 v40, v29, v49 offset0:140 offset1:206
	v_mul_f32_e32 v29, 0x42800000, v59
	v_mul_f32_e32 v49, 0x42800000, v60
	ds_write2_b32 v41, v29, v49 offset0:16 offset1:82
	v_mul_f32_e32 v29, 0x42800000, v61
	v_mul_f32_e32 v49, 0x42800000, v62
	ds_write2_b32 v41, v29, v49 offset0:148 offset1:214
	v_mul_f32_e32 v29, 0x42800000, v63
	v_mul_f32_e32 v49, 0x42800000, v64
	ds_write2_b32 v42, v29, v49 offset0:24 offset1:90
	v_mul_f32_e32 v29, 0x42800000, v65
	v_mul_f32_e32 v49, 0x42800000, v66
	ds_write2_b32 v42, v29, v49 offset0:156 offset1:222
	v_mul_f32_e32 v29, 0x42800000, v67
	v_mul_f32_e32 v49, 0x42800000, v68
	ds_write2_b32 v43, v29, v49 offset0:32 offset1:98
	v_mul_f32_e32 v29, 0x42800000, v69
	v_mov_b32_e32 v50, v1
	v_mov_b32_e32 v51, v1
	s_add_u32 s4, s4, s6
	v_mul_f32_e32 v49, 0x42800000, v70
	ds_write2_b32 v43, v29, v49 offset0:164 offset1:230
	v_add_u32_e32 v84, s0, v32
	s_addc_u32 s5, s5, 0
	v_mul_f32_e32 v29, 0x42800000, v71
	v_ashrrev_i32_e32 v85, 31, v84
	v_lshlrev_b64 v[84:85], 10, v[84:85]
	v_readlane_b32 s46, v254, 34
	v_mul_f32_e32 v49, 0x42800000, v72
	ds_write2_b32 v44, v29, v49 offset0:40 offset1:106
	v_readlane_b32 s47, v254, 35
	v_mul_f32_e32 v29, 0x42800000, v73
	v_mul_f32_e32 v49, 0x42800000, v74
	ds_write2_b32 v44, v29, v49 offset0:172 offset1:238
	v_mul_f32_e32 v29, 0x42800000, v75
	v_mul_f32_e32 v49, 0x42800000, v76
	ds_write2_b32 v45, v29, v49 offset0:48 offset1:114
	v_mul_f32_e32 v29, 0x42800000, v77
	v_mul_f32_e32 v49, 0x42800000, v78
	ds_write2_b32 v45, v29, v49 offset0:180 offset1:246
	v_mul_f32_e32 v29, 0x42800000, v79
	v_mul_f32_e32 v49, 0x42800000, v80
	ds_write2_b32 v46, v29, v49 offset0:56 offset1:122
	v_mov_b32_e32 v49, v1
	v_mul_f32_e32 v29, 0x42800000, v48
	v_mov_b32_e32 v48, v1
	v_mul_f32_e32 v28, 0x42800000, v28
	ds_write2_b32 v46, v29, v28 offset0:188 offset1:254
	s_waitcnt lgkmcnt(0)
	ds_read2_b32 v[52:53], v33 offset1:16
	ds_read2_b32 v[54:55], v33 offset0:33 offset1:49
	ds_read2_b32 v[56:57], v33 offset0:66 offset1:82
	ds_read2_b32 v[58:59], v33 offset0:99 offset1:115
	ds_read2_b32 v[60:61], v33 offset0:132 offset1:148
	ds_read2_b32 v[62:63], v33 offset0:165 offset1:181
	ds_read2_b32 v[64:65], v33 offset0:198 offset1:214
	ds_read2_b32 v[66:67], v33 offset0:231 offset1:247
	ds_read2_b32 v[68:69], v47 offset0:8 offset1:24
	ds_read2_b32 v[70:71], v47 offset0:41 offset1:57
	ds_read2_b32 v[72:73], v47 offset0:74 offset1:90
	ds_read2_b32 v[74:75], v47 offset0:107 offset1:123
	ds_read2_b32 v[76:77], v47 offset0:140 offset1:156
	ds_read2_b32 v[78:79], v47 offset0:173 offset1:189
	ds_read2_b32 v[80:81], v47 offset0:206 offset1:222
	ds_read2_b32 v[82:83], v47 offset0:239 offset1:255
	s_waitcnt lgkmcnt(14)
	v_cvt_pk_fp8_f32 v48, v52, v54
	s_waitcnt lgkmcnt(10)
	v_cvt_pk_fp8_f32 v49, v60, v62
	s_waitcnt lgkmcnt(6)
	v_cvt_pk_fp8_f32 v50, v68, v70
	s_waitcnt lgkmcnt(2)
	v_cvt_pk_fp8_f32 v51, v76, v78
	v_cvt_pk_fp8_f32 v48, v56, v58 op_sel:[0,0,1]
	v_cvt_pk_fp8_f32 v49, v64, v66 op_sel:[0,0,1]
	v_cvt_pk_fp8_f32 v50, v72, v74 op_sel:[0,0,1]
	s_waitcnt lgkmcnt(0)
	v_cvt_pk_fp8_f32 v51, v80, v82 op_sel:[0,0,1]
	v_lshl_add_u64 v[28:29], s[4:5], 0, v[2:3]
	v_lshl_add_u64 v[84:85], v[28:29], 0, v[84:85]
	v_add_u32_e32 v52, s0, v34
	global_store_dwordx4 v[84:85], v[48:51], off
	s_nop 1
	v_mov_b32_e32 v48, v1
	v_mov_b32_e32 v49, v1
	v_mov_b32_e32 v50, v1
	v_mov_b32_e32 v51, v1
	v_cvt_pk_fp8_f32 v48, v53, v55
	v_cvt_pk_fp8_f32 v49, v61, v63
	v_cvt_pk_fp8_f32 v50, v69, v71
	v_cvt_pk_fp8_f32 v51, v77, v79
	v_cvt_pk_fp8_f32 v48, v57, v59 op_sel:[0,0,1]
	v_cvt_pk_fp8_f32 v49, v65, v67 op_sel:[0,0,1]
	v_cvt_pk_fp8_f32 v50, v73, v75 op_sel:[0,0,1]
	v_cvt_pk_fp8_f32 v51, v81, v83 op_sel:[0,0,1]
	v_ashrrev_i32_e32 v53, 31, v52
	v_lshlrev_b64 v[52:53], 10, v[52:53]
	v_lshl_add_u64 v[28:29], v[28:29], 0, v[52:53]
	global_store_dwordx4 v[28:29], v[48:51], off
	s_waitcnt lgkmcnt(0)

; #define LAS __attribute__((address_space(3)))
; __device__ __forceinline__ void tr_item8(const float* W, int ld, int K, int nblk, int item, unsigned char* WT, bool gu, float scale, LAS float* scr, int lane) {
;     const int kb = item / nblk, nb = item % nblk, k0 = 64 * kb, n0 = 32 * nb;
;     int drow0 = n0;
;     if (gu) { const int bj = n0 / FF, j = n0 - bj * FF; drow0 = 256 * (j / 128) + 128 * bj + (j % 128); }
;     { float t_[32];
; #pragma unroll
;       for (int i = 0; i < 32; ++i) t_[i] = W[(size_t)(k0 + 2 * i + (lane >> 5)) * ld + n0 + (lane & 31)];
; __device__ __forceinline__ void convert_items(Frame& F, const Args& a, int lo, int hi, int w, int nw) {
;     ...
;         if (r < I_DN) { tr_item8(a.in[15], D, FF, 32, r, F.ws + WS_WDN, false, WSC_DN, scr, lane); continue; } r -= I_DN;
.LBB0_1341:
	s_andn2_b64 vcc, exec, s[4:5]
	s_cbranch_vccnz .LBB0_1343
	s_lshl_b32 s0, s8, 5
	s_and_b32 s4, s12, 0x1ffc0
	s_and_b32 s6, s0, 0x3e0
	v_add_u32_e32 v28, s4, v30
	s_lshl_b32 s0, s6, 2
	v_ashrrev_i32_e32 v29, 31, v28
	v_lshl_add_u64 v[48:49], v[4:5], 0, s[0:1]
	v_lshlrev_b64 v[28:29], 12, v[28:29]
	v_lshl_add_u64 v[28:29], v[48:49], 0, v[28:29]
	v_add_co_u32_e32 v48, vcc, 0x2000, v28
	global_load_dword v50, v[28:29], off nt
	s_nop 0
	v_addc_co_u32_e32 v49, vcc, 0, v29, vcc
	global_load_dword v51, v[48:49], off nt
	v_add_co_u32_e32 v48, vcc, 0x4000, v28
	s_mov_b32 s5, s1
	s_nop 0
	v_addc_co_u32_e32 v49, vcc, 0, v29, vcc
	global_load_dword v52, v[48:49], off nt
	v_add_co_u32_e32 v48, vcc, 0x6000, v28
	s_nop 1
	v_addc_co_u32_e32 v49, vcc, 0, v29, vcc
	global_load_dword v53, v[48:49], off nt
	v_add_co_u32_e32 v48, vcc, 0x8000, v28
	s_nop 1
	v_addc_co_u32_e32 v49, vcc, 0, v29, vcc
	global_load_dword v54, v[48:49], off nt
	v_add_co_u32_e32 v48, vcc, 0xa000, v28
	s_nop 1
	v_addc_co_u32_e32 v49, vcc, 0, v29, vcc
	global_load_dword v55, v[48:49], off nt
	v_add_co_u32_e32 v48, vcc, 0xc000, v28
	s_nop 1
	v_addc_co_u32_e32 v49, vcc, 0, v29, vcc
	global_load_dword v56, v[48:49], off nt
	v_add_co_u32_e32 v48, vcc, 0xe000, v28
	s_nop 1
	v_addc_co_u32_e32 v49, vcc, 0, v29, vcc
	global_load_dword v57, v[48:49], off nt
	v_add_co_u32_e32 v48, vcc, 0x10000, v28
	s_nop 1
	v_addc_co_u32_e32 v49, vcc, 0, v29, vcc
	global_load_dword v58, v[48:49], off nt
	v_add_co_u32_e32 v48, vcc, 0x12000, v28
	s_nop 1
	v_addc_co_u32_e32 v49, vcc, 0, v29, vcc
	global_load_dword v59, v[48:49], off nt
	v_add_co_u32_e32 v48, vcc, 0x14000, v28
	s_nop 1
	v_addc_co_u32_e32 v49, vcc, 0, v29, vcc
	global_load_dword v60, v[48:49], off nt
	v_add_co_u32_e32 v48, vcc, 0x16000, v28
	s_nop 1
	v_addc_co_u32_e32 v49, vcc, 0, v29, vcc
	global_load_dword v61, v[48:49], off nt
	v_add_co_u32_e32 v48, vcc, 0x18000, v28
	s_nop 1
	v_addc_co_u32_e32 v49, vcc, 0, v29, vcc
	global_load_dword v62, v[48:49], off nt
	v_add_co_u32_e32 v48, vcc, 0x1a000, v28
	s_nop 1
	v_addc_co_u32_e32 v49, vcc, 0, v29, vcc
	global_load_dword v63, v[48:49], off nt
	v_add_co_u32_e32 v48, vcc, 0x1c000, v28
	s_nop 1
	v_addc_co_u32_e32 v49, vcc, 0, v29, vcc
	global_load_dword v64, v[48:49], off nt
	v_add_co_u32_e32 v48, vcc, 0x1e000, v28
	s_nop 1
	v_addc_co_u32_e32 v49, vcc, 0, v29, vcc
	global_load_dword v65, v[48:49], off nt
	v_add_co_u32_e32 v48, vcc, 0x20000, v28
	s_nop 1
	v_addc_co_u32_e32 v49, vcc, 0, v29, vcc
	global_load_dword v66, v[48:49], off nt
	v_add_co_u32_e32 v48, vcc, 0x22000, v28
	s_nop 1
	v_addc_co_u32_e32 v49, vcc, 0, v29, vcc
	global_load_dword v67, v[48:49], off nt
	v_add_co_u32_e32 v48, vcc, 0x24000, v28
	s_nop 1
	v_addc_co_u32_e32 v49, vcc, 0, v29, vcc
	global_load_dword v68, v[48:49], off nt
	v_add_co_u32_e32 v48, vcc, 0x26000, v28
	s_nop 1
	v_addc_co_u32_e32 v49, vcc, 0, v29, vcc
	global_load_dword v69, v[48:49], off nt
	v_add_co_u32_e32 v48, vcc, 0x28000, v28
	s_nop 1
	v_addc_co_u32_e32 v49, vcc, 0, v29, vcc
	global_load_dword v70, v[48:49], off nt
	v_add_co_u32_e32 v48, vcc, 0x2a000, v28
	s_nop 1
	v_addc_co_u32_e32 v49, vcc, 0, v29, vcc
	global_load_dword v71, v[48:49], off nt
	v_add_co_u32_e32 v48, vcc, 0x2c000, v28
	s_nop 1
	v_addc_co_u32_e32 v49, vcc, 0, v29, vcc
	global_load_dword v72, v[48:49], off nt
	v_add_co_u32_e32 v48, vcc, 0x2e000, v28
	s_nop 1
	v_addc_co_u32_e32 v49, vcc, 0, v29, vcc
	global_load_dword v73, v[48:49], off nt
	v_add_co_u32_e32 v48, vcc, 0x30000, v28
	s_nop 1
	v_addc_co_u32_e32 v49, vcc, 0, v29, vcc
	global_load_dword v74, v[48:49], off nt
	v_add_co_u32_e32 v48, vcc, 0x32000, v28
	s_nop 1
	v_addc_co_u32_e32 v49, vcc, 0, v29, vcc
	global_load_dword v75, v[48:49], off nt
	v_add_co_u32_e32 v48, vcc, 0x34000, v28
	s_nop 1
	v_addc_co_u32_e32 v49, vcc, 0, v29, vcc
	global_load_dword v76, v[48:49], off nt
	v_add_co_u32_e32 v48, vcc, 0x36000, v28
	s_nop 1
	v_addc_co_u32_e32 v49, vcc, 0, v29, vcc
	global_load_dword v77, v[48:49], off nt
	v_add_co_u32_e32 v48, vcc, 0x38000, v28
	s_nop 1
	v_addc_co_u32_e32 v49, vcc, 0, v29, vcc
	global_load_dword v78, v[48:49], off nt
	v_add_co_u32_e32 v48, vcc, 0x3a000, v28
	s_nop 1
	v_addc_co_u32_e32 v49, vcc, 0, v29, vcc
	global_load_dword v79, v[48:49], off nt
	v_add_co_u32_e32 v48, vcc, 0x3c000, v28
	s_nop 1
	v_addc_co_u32_e32 v49, vcc, 0, v29, vcc
	v_add_co_u32_e32 v28, vcc, 0x3e000, v28
	global_load_dword v48, v[48:49], off nt
	s_nop 0
	v_addc_co_u32_e32 v29, vcc, 0, v29, vcc
	global_load_dword v28, v[28:29], off nt
	s_waitcnt vmcnt(0)
; __device__ __forceinline__ unsigned cvt_pk4_fp8(float a, float b, float c, float d) { int w = 0; w = __builtin_amdgcn_cvt_pk_fp8_f32(a, b, w, false); w = __builtin_amdgcn_cvt_pk_fp8_f32(c, d, w, true); return (unsigned)w; }
; #define GAS __attribute__((address_space(1)))
; #define LAS __attribute__((address_space(3)))
; #define LDS_WAIT() asm volatile("s_waitcnt lgkmcnt(0)" ::: "memory")
; __device__ __forceinline__ void tr_item8(const float* W, int ld, int K, int nblk, int item, unsigned char* WT, bool gu, float scale, LAS float* scr, int lane) {
;     ...
; #pragma unroll
;       for (int i = 0; i < 32; ++i) scr[(2 * i + (lane >> 5)) * 33 + (lane & 31)] = t_[i] * scale; }
;     LDS_WAIT(); asm volatile("" ::: "memory");
;     const int c = lane & 3;
; #pragma unroll
;     for (int j = 0; j < 2; ++j) { const int n = (lane >> 2) + 16 * j; const LAS float* sp = scr + (16 * c) * 33 + n;
;         v4u o; o.x = pg8::cvt_pk4_fp8(sp[0 * 33], sp[1 * 33], sp[2 * 33], sp[3 * 33]); o.y = pg8::cvt_pk4_fp8(sp[4 * 33], sp[5 * 33], sp[6 * 33], sp[7 * 33]);
;         o.z = pg8::cvt_pk4_fp8(sp[8 * 33], sp[9 * 33], sp[10 * 33], sp[11 * 33]); o.w = pg8::cvt_pk4_fp8(sp[12 * 33], sp[13 * 33], sp[14 * 33], sp[15 * 33]);
;         *(GAS v4u*)(WT + (size_t)(drow0 + n) * K + k0 + 16 * c) = o; }
;     LDS_WAIT(); asm volatile("" ::: "memory");
	v_mul_f32_e32 v29, 0x43000000, v50
	v_mul_f32_e32 v49, 0x43000000, v51
	ds_write2_b32 v31, v29, v49 offset1:66
	v_mul_f32_e32 v29, 0x43000000, v52
	v_mul_f32_e32 v49, 0x43000000, v53
	ds_write2_b32 v31, v29, v49 offset0:132 offset1:198
	v_mul_f32_e32 v29, 0x43000000, v54
	v_mul_f32_e32 v49, 0x43000000, v55
	ds_write2_b32 v40, v29, v49 offset0:8 offset1:74
	v_mul_f32_e32 v29, 0x43000000, v56
	v_mul_f32_e32 v49, 0x43000000, v57
	ds_write2_b32 v40, v29, v49 offset0:140 offset1:206
	v_mul_f32_e32 v29, 0x43000000, v58
	v_mul_f32_e32 v49, 0x43000000, v59
	ds_write2_b32 v41, v29, v49 offset0:16 offset1:82
	v_mul_f32_e32 v29, 0x43000000, v60
	v_mul_f32_e32 v49, 0x43000000, v61
	ds_write2_b32 v41, v29, v49 offset0:148 offset1:214
	v_mul_f32_e32 v29, 0x43000000, v62
	v_mul_f32_e32 v49, 0x43000000, v63
	ds_write2_b32 v42, v29, v49 offset0:24 offset1:90
	v_mul_f32_e32 v29, 0x43000000, v64
	v_mul_f32_e32 v49, 0x43000000, v65
	ds_write2_b32 v42, v29, v49 offset0:156 offset1:222
	v_mul_f32_e32 v29, 0x43000000, v66
	v_mul_f32_e32 v49, 0x43000000, v67
	ds_write2_b32 v43, v29, v49 offset0:32 offset1:98
	v_mul_f32_e32 v29, 0x43000000, v68
	v_mul_f32_e32 v49, 0x43000000, v69
	ds_write2_b32 v43, v29, v49 offset0:164 offset1:230
	v_mul_f32_e32 v29, 0x43000000, v70
	v_mul_f32_e32 v49, 0x43000000, v71
	ds_write2_b32 v44, v29, v49 offset0:40 offset1:106
	v_mul_f32_e32 v29, 0x43000000, v72
	v_mul_f32_e32 v49, 0x43000000, v73
	ds_write2_b32 v44, v29, v49 offset0:172 offset1:238
	v_mov_b32_e32 v50, 0
	v_mov_b32_e32 v51, 0
	v_mul_f32_e32 v29, 0x43000000, v74
	v_mul_f32_e32 v49, 0x43000000, v75
	ds_write2_b32 v45, v29, v49 offset0:48 offset1:114
	v_mul_f32_e32 v29, 0x43000000, v76
	v_mul_f32_e32 v49, 0x43000000, v77
	ds_write2_b32 v45, v29, v49 offset0:180 offset1:246
	v_mul_f32_e32 v29, 0x43000000, v78
	v_mul_f32_e32 v49, 0x43000000, v79
	ds_write2_b32 v46, v29, v49 offset0:56 offset1:122
	v_mov_b32_e32 v49, 0
	v_mul_f32_e32 v29, 0x43000000, v48
	v_mov_b32_e32 v48, 0
	v_mul_f32_e32 v28, 0x43000000, v28
	ds_write2_b32 v46, v29, v28 offset0:188 offset1:254
	s_waitcnt lgkmcnt(0)
	ds_read2_b32 v[52:53], v33 offset1:16
	ds_read2_b32 v[54:55], v33 offset0:33 offset1:49
	ds_read2_b32 v[56:57], v33 offset0:66 offset1:82
	ds_read2_b32 v[58:59], v33 offset0:99 offset1:115
	ds_read2_b32 v[60:61], v33 offset0:132 offset1:148
	ds_read2_b32 v[62:63], v33 offset0:165 offset1:181
	ds_read2_b32 v[64:65], v33 offset0:198 offset1:214
	ds_read2_b32 v[66:67], v33 offset0:231 offset1:247
	ds_read2_b32 v[68:69], v47 offset0:8 offset1:24
	ds_read2_b32 v[70:71], v47 offset0:41 offset1:57
	ds_read2_b32 v[72:73], v47 offset0:74 offset1:90
	ds_read2_b32 v[74:75], v47 offset0:107 offset1:123
	ds_read2_b32 v[76:77], v47 offset0:140 offset1:156
	ds_read2_b32 v[78:79], v47 offset0:173 offset1:189
	ds_read2_b32 v[80:81], v47 offset0:206 offset1:222
	ds_read2_b32 v[82:83], v47 offset0:239 offset1:255
	s_waitcnt lgkmcnt(14)
	v_cvt_pk_fp8_f32 v48, v52, v54
	s_waitcnt lgkmcnt(10)
	v_cvt_pk_fp8_f32 v49, v60, v62
	s_waitcnt lgkmcnt(6)
	v_cvt_pk_fp8_f32 v50, v68, v70
	s_waitcnt lgkmcnt(2)
	v_cvt_pk_fp8_f32 v51, v76, v78
	v_cvt_pk_fp8_f32 v48, v56, v58 op_sel:[0,0,1]
	v_cvt_pk_fp8_f32 v49, v64, v66 op_sel:[0,0,1]
	v_cvt_pk_fp8_f32 v50, v72, v74 op_sel:[0,0,1]
	s_waitcnt lgkmcnt(0)
	v_cvt_pk_fp8_f32 v51, v80, v82 op_sel:[0,0,1]
	v_lshl_add_u64 v[28:29], v[16:17], 0, s[4:5]
	v_add_u32_e32 v52, s6, v32
	v_mad_i64_i32 v[84:85], s[4:5], v52, s13, v[28:29]
	global_store_dwordx4 v[84:85], v[48:51], off
	v_add_u32_e32 v52, s6, v34
	v_mad_i64_i32 v[28:29], s[4:5], v52, s13, v[28:29]
	v_mov_b32_e32 v48, 0
	v_mov_b32_e32 v49, 0
	v_mov_b32_e32 v50, 0
	v_mov_b32_e32 v51, 0
	v_cvt_pk_fp8_f32 v48, v53, v55
	v_cvt_pk_fp8_f32 v49, v61, v63
	v_cvt_pk_fp8_f32 v50, v69, v71
	v_cvt_pk_fp8_f32 v51, v77, v79
	v_cvt_pk_fp8_f32 v48, v57, v59 op_sel:[0,0,1]
	v_cvt_pk_fp8_f32 v49, v65, v67 op_sel:[0,0,1]
	v_cvt_pk_fp8_f32 v50, v73, v75 op_sel:[0,0,1]
	v_cvt_pk_fp8_f32 v51, v81, v83 op_sel:[0,0,1]
	global_store_dwordx4 v[28:29], v[48:51], off
	s_waitcnt lgkmcnt(0)

; #define LAS __attribute__((address_space(3)))
; __device__ __forceinline__ void tr_item8(const float* W, int ld, int K, int nblk, int item, unsigned char* WT, bool gu, float scale, LAS float* scr, int lane) {
;     const int kb = item / nblk, nb = item % nblk, k0 = 64 * kb, n0 = 32 * nb;
;     int drow0 = n0;
;     if (gu) { const int bj = n0 / FF, j = n0 - bj * FF; drow0 = 256 * (j / 128) + 128 * bj + (j % 128); }
;     { float t_[32];
; #pragma unroll
;       for (int i = 0; i < 32; ++i) t_[i] = W[(size_t)(k0 + 2 * i + (lane >> 5)) * ld + n0 + (lane & 31)];
; __device__ __forceinline__ void convert_items(Frame& F, const Args& a, int lo, int hi, int w, int nw) {
;     ...
;         if (r < I_GU) { tr_item8(a.in[14], 2 * FF, D, 224, r, F.ws + WS_WGU, true, WSC_GU, scr, lane); continue; } r -= I_GU;
.LBB0_1344:
	s_andn2_b64 vcc, exec, s[4:5]
	s_cbranch_vccnz .LBB0_1346
	s_add_i32 s0, s8, 0xf300
	s_bfe_u32 s4, s0, 0xb0005
	s_mulk_i32 s4, 0x2493
	s_lshr_b32 s4, s4, 16
	s_mul_i32 s5, s4, 0xe0
	s_sub_i32 s0, s0, s5
	s_lshl_b32 s5, s0, 5
	s_and_b32 s6, s0, 0xffff
	s_cmpk_gt_u32 s6, 0x6f
	s_cselect_b32 s31, 0xfffff200, 0
	s_cselect_b32 s40, 0x80, 0
	s_lshl_b32 s0, s0, 7
	s_lshl_b32 s4, s4, 6
	s_and_b32 s0, s0, 0x3ff80
	v_add_u32_e32 v64, s4, v30
	v_lshl_add_u64 v[28:29], v[6:7], 0, s[0:1]
	v_mad_i64_i32 v[48:49], s[6:7], v64, s14, v[28:29]
	v_add_u32_e32 v50, 2, v64
	v_add_u32_e32 v52, 4, v64
	v_add_u32_e32 v54, 6, v64
	v_add_u32_e32 v56, 8, v64
	v_add_u32_e32 v58, 10, v64
	v_add_u32_e32 v60, 12, v64
	v_add_u32_e32 v62, 14, v64
	v_mad_i64_i32 v[50:51], s[6:7], v50, s14, v[28:29]
	v_mad_i64_i32 v[52:53], s[6:7], v52, s14, v[28:29]
	v_mad_i64_i32 v[54:55], s[6:7], v54, s14, v[28:29]
	v_mad_i64_i32 v[56:57], s[6:7], v56, s14, v[28:29]
	v_mad_i64_i32 v[58:59], s[6:7], v58, s14, v[28:29]
	v_mad_i64_i32 v[60:61], s[6:7], v60, s14, v[28:29]
	v_mad_i64_i32 v[62:63], s[6:7], v62, s14, v[28:29]
	global_load_dword v65, v[48:49], off nt
	global_load_dword v66, v[50:51], off nt
	global_load_dword v67, v[52:53], off nt
	global_load_dword v68, v[54:55], off nt
	global_load_dword v69, v[56:57], off nt
	global_load_dword v70, v[58:59], off nt
	global_load_dword v71, v[60:61], off nt
	global_load_dword v72, v[62:63], off nt
	v_add_u32_e32 v48, 16, v64
	v_mad_i64_i32 v[48:49], s[6:7], v48, s14, v[28:29]
	v_add_u32_e32 v50, 18, v64
	v_add_u32_e32 v52, 20, v64
	v_add_u32_e32 v54, 22, v64
	v_add_u32_e32 v56, 24, v64
	v_add_u32_e32 v58, 26, v64
	v_add_u32_e32 v60, 28, v64
	v_add_u32_e32 v62, 30, v64
	v_mad_i64_i32 v[50:51], s[6:7], v50, s14, v[28:29]
	v_mad_i64_i32 v[52:53], s[6:7], v52, s14, v[28:29]
	v_mad_i64_i32 v[54:55], s[6:7], v54, s14, v[28:29]
	v_mad_i64_i32 v[56:57], s[6:7], v56, s14, v[28:29]
	v_mad_i64_i32 v[58:59], s[6:7], v58, s14, v[28:29]
	v_mad_i64_i32 v[60:61], s[6:7], v60, s14, v[28:29]
	v_mad_i64_i32 v[62:63], s[6:7], v62, s14, v[28:29]
	global_load_dword v73, v[48:49], off nt
	global_load_dword v74, v[50:51], off nt
	global_load_dword v75, v[52:53], off nt
	global_load_dword v76, v[54:55], off nt
	global_load_dword v77, v[56:57], off nt
	global_load_dword v78, v[58:59], off nt
	global_load_dword v79, v[60:61], off nt
	global_load_dword v80, v[62:63], off nt
	v_add_u32_e32 v48, 32, v64
	v_add_u32_e32 v50, 34, v64
	v_add_u32_e32 v52, 36, v64
	v_add_u32_e32 v54, 38, v64
	v_add_u32_e32 v60, 44, v64
	v_mad_i64_i32 v[48:49], s[6:7], v48, s14, v[28:29]
	v_mad_i64_i32 v[50:51], s[6:7], v50, s14, v[28:29]
	v_mad_i64_i32 v[52:53], s[6:7], v52, s14, v[28:29]
	v_mad_i64_i32 v[54:55], s[6:7], v54, s14, v[28:29]
	v_add_u32_e32 v56, 40, v64
	v_add_u32_e32 v58, 42, v64
	v_mad_i64_i32 v[60:61], s[6:7], v60, s14, v[28:29]
	v_add_u32_e32 v62, 46, v64
	v_mad_i64_i32 v[56:57], s[6:7], v56, s14, v[28:29]
	v_mad_i64_i32 v[58:59], s[6:7], v58, s14, v[28:29]
	v_mad_i64_i32 v[62:63], s[6:7], v62, s14, v[28:29]
	global_load_dword v81, v[48:49], off nt
	global_load_dword v82, v[50:51], off nt
	global_load_dword v83, v[52:53], off nt
	global_load_dword v84, v[54:55], off nt
	global_load_dword v85, v[56:57], off nt
	global_load_dword v86, v[58:59], off nt
	s_nop 0
	global_load_dword v60, v[60:61], off nt
	s_nop 0
	global_load_dword v61, v[62:63], off nt
	v_add_u32_e32 v48, 48, v64
	v_add_u32_e32 v50, 50, v64
	v_add_u32_e32 v52, 52, v64
	v_add_u32_e32 v54, 54, v64
	v_mad_i64_i32 v[48:49], s[6:7], v48, s14, v[28:29]
	v_mad_i64_i32 v[50:51], s[6:7], v50, s14, v[28:29]
	v_mad_i64_i32 v[52:53], s[6:7], v52, s14, v[28:29]
	v_mad_i64_i32 v[54:55], s[6:7], v54, s14, v[28:29]
	v_add_u32_e32 v56, 56, v64
	v_add_u32_e32 v58, 58, v64
	v_mad_i64_i32 v[56:57], s[6:7], v56, s14, v[28:29]
	v_mad_i64_i32 v[58:59], s[6:7], v58, s14, v[28:29]
	global_load_dword v62, v[48:49], off nt
	s_nop 0
	global_load_dword v50, v[50:51], off nt
	s_nop 0
	global_load_dword v51, v[52:53], off nt
	s_nop 0
	global_load_dword v52, v[54:55], off nt
	global_load_dword v53, v[56:57], off nt
	s_nop 0
	global_load_dword v54, v[58:59], off nt
	v_add_u32_e32 v48, 60, v64
	v_add_u32_e32 v55, 62, v64
	v_mad_i64_i32 v[48:49], s[6:7], v48, s14, v[28:29]
	v_mad_i64_i32 v[28:29], s[6:7], v55, s14, v[28:29]
	global_load_dword v48, v[48:49], off nt
	s_nop 0
	global_load_dword v28, v[28:29], off nt
	s_waitcnt vmcnt(0)
; __device__ __forceinline__ unsigned cvt_pk4_fp8(float a, float b, float c, float d) { int w = 0; w = __builtin_amdgcn_cvt_pk_fp8_f32(a, b, w, false); w = __builtin_amdgcn_cvt_pk_fp8_f32(c, d, w, true); return (unsigned)w; }
; #define GAS __attribute__((address_space(1)))
; #define LAS __attribute__((address_space(3)))
; #define LDS_WAIT() asm volatile("s_waitcnt lgkmcnt(0)" ::: "memory")
; __device__ __forceinline__ void tr_item8(const float* W, int ld, int K, int nblk, int item, unsigned char* WT, bool gu, float scale, LAS float* scr, int lane) {
;     ...
; #pragma unroll
;       for (int i = 0; i < 32; ++i) scr[(2 * i + (lane >> 5)) * 33 + (lane & 31)] = t_[i] * scale; }
;     LDS_WAIT(); asm volatile("" ::: "memory");
;     const int c = lane & 3;
; #pragma unroll
;     for (int j = 0; j < 2; ++j) { const int n = (lane >> 2) + 16 * j; const LAS float* sp = scr + (16 * c) * 33 + n;
;         v4u o; o.x = pg8::cvt_pk4_fp8(sp[0 * 33], sp[1 * 33], sp[2 * 33], sp[3 * 33]); o.y = pg8::cvt_pk4_fp8(sp[4 * 33], sp[5 * 33], sp[6 * 33], sp[7 * 33]);
;         o.z = pg8::cvt_pk4_fp8(sp[8 * 33], sp[9 * 33], sp[10 * 33], sp[11 * 33]); o.w = pg8::cvt_pk4_fp8(sp[12 * 33], sp[13 * 33], sp[14 * 33], sp[15 * 33]);
;         *(GAS v4u*)(WT + (size_t)(drow0 + n) * K + k0 + 16 * c) = o; }
;     LDS_WAIT(); asm volatile("" ::: "memory");
	v_mul_f32_e32 v29, 0x42800000, v65
	v_mul_f32_e32 v49, 0x42800000, v66
	ds_write2_b32 v31, v29, v49 offset1:66
	v_mul_f32_e32 v29, 0x42800000, v67
	v_mul_f32_e32 v49, 0x42800000, v68
	ds_write2_b32 v31, v29, v49 offset0:132 offset1:198
	v_mul_f32_e32 v29, 0x42800000, v69
	v_mul_f32_e32 v49, 0x42800000, v70
	ds_write2_b32 v40, v29, v49 offset0:8 offset1:74
	v_mul_f32_e32 v29, 0x42800000, v71
	v_mul_f32_e32 v49, 0x42800000, v72
	ds_write2_b32 v40, v29, v49 offset0:140 offset1:206
	s_add_i32 s0, s31, s5
	s_sext_i32_i16 s5, s0
	s_bfe_u32 s5, s5, 0x70018
	s_add_i32 s5, s0, s5
	s_sext_i32_i16 s6, s5
	s_and_b32 s5, s5, 0xff80
	s_sub_i32 s0, s0, s5
	s_lshl_b32 s6, s6, 1
	s_sext_i32_i16 s0, s0
	v_mul_f32_e32 v29, 0x42800000, v73
	v_mul_f32_e32 v49, 0x42800000, v74
	ds_write2_b32 v41, v29, v49 offset0:16 offset1:82
	v_mul_f32_e32 v29, 0x42800000, v75
	v_mul_f32_e32 v49, 0x42800000, v76
	ds_write2_b32 v41, v29, v49 offset0:148 offset1:214
	v_mul_f32_e32 v29, 0x42800000, v77
	v_mul_f32_e32 v49, 0x42800000, v78
	ds_write2_b32 v42, v29, v49 offset0:24 offset1:90
	v_mul_f32_e32 v29, 0x42800000, v79
	v_mul_f32_e32 v49, 0x42800000, v80
	ds_write2_b32 v42, v29, v49 offset0:156 offset1:222
	s_and_b32 s6, s6, 0xffffff00
	s_add_i32 s0, s40, s0
	s_add_i32 s0, s0, s6
	s_mov_b32 s5, s1
	v_mul_f32_e32 v29, 0x42800000, v81
	v_mul_f32_e32 v49, 0x42800000, v82
	ds_write2_b32 v43, v29, v49 offset0:32 offset1:98
	v_mul_f32_e32 v29, 0x42800000, v83
	v_mul_f32_e32 v49, 0x42800000, v84
	ds_write2_b32 v43, v29, v49 offset0:164 offset1:230
	v_mul_f32_e32 v29, 0x42800000, v85
	v_mul_f32_e32 v49, 0x42800000, v86
	ds_write2_b32 v44, v29, v49 offset0:40 offset1:106
	v_mul_f32_e32 v29, 0x42800000, v60
	v_mul_f32_e32 v49, 0x42800000, v61
	ds_write2_b32 v44, v29, v49 offset0:172 offset1:238
	v_add_u32_e32 v84, s0, v32
	v_ashrrev_i32_e32 v85, 31, v84
	v_lshlrev_b64 v[84:85], 10, v[84:85]
	v_mul_f32_e32 v29, 0x42800000, v62
	v_mul_f32_e32 v49, 0x42800000, v50
	ds_write2_b32 v45, v29, v49 offset0:48 offset1:114
	v_mul_f32_e32 v29, 0x42800000, v51
	v_mul_f32_e32 v49, 0x42800000, v52
	ds_write2_b32 v45, v29, v49 offset0:180 offset1:246
	v_mul_f32_e32 v29, 0x42800000, v53
	v_mul_f32_e32 v49, 0x42800000, v54
	ds_write2_b32 v46, v29, v49 offset0:56 offset1:122
	v_mov_b32_e32 v49, 0
	v_mov_b32_e32 v50, 0
	v_mul_f32_e32 v29, 0x42800000, v48
	v_mul_f32_e32 v28, 0x42800000, v28
	ds_write2_b32 v46, v29, v28 offset0:188 offset1:254
	s_waitcnt lgkmcnt(0)
	ds_read2_b32 v[52:53], v33 offset1:16
	ds_read2_b32 v[54:55], v33 offset0:33 offset1:49
	ds_read2_b32 v[56:57], v33 offset0:66 offset1:82
	ds_read2_b32 v[58:59], v33 offset0:99 offset1:115
	ds_read2_b32 v[60:61], v33 offset0:132 offset1:148
	ds_read2_b32 v[62:63], v33 offset0:165 offset1:181
	ds_read2_b32 v[64:65], v33 offset0:198 offset1:214
	ds_read2_b32 v[66:67], v33 offset0:231 offset1:247
	ds_read2_b32 v[68:69], v47 offset0:8 offset1:24
	ds_read2_b32 v[70:71], v47 offset0:41 offset1:57
	ds_read2_b32 v[72:73], v47 offset0:74 offset1:90
	ds_read2_b32 v[74:75], v47 offset0:107 offset1:123
	ds_read2_b32 v[76:77], v47 offset0:140 offset1:156
	ds_read2_b32 v[78:79], v47 offset0:173 offset1:189
	v_mov_b32_e32 v48, 0
	ds_read2_b32 v[80:81], v47 offset0:206 offset1:222
	ds_read2_b32 v[82:83], v47 offset0:239 offset1:255
	v_mov_b32_e32 v51, 0
	s_waitcnt lgkmcnt(14)
	v_cvt_pk_fp8_f32 v48, v52, v54
	s_waitcnt lgkmcnt(10)
	v_cvt_pk_fp8_f32 v49, v60, v62
	s_waitcnt lgkmcnt(6)
	v_cvt_pk_fp8_f32 v50, v68, v70
	s_waitcnt lgkmcnt(2)
	v_cvt_pk_fp8_f32 v51, v76, v78
	v_cvt_pk_fp8_f32 v48, v56, v58 op_sel:[0,0,1]
	v_cvt_pk_fp8_f32 v49, v64, v66 op_sel:[0,0,1]
	v_cvt_pk_fp8_f32 v50, v72, v74 op_sel:[0,0,1]
	s_waitcnt lgkmcnt(0)
	v_cvt_pk_fp8_f32 v51, v80, v82 op_sel:[0,0,1]
	v_lshl_add_u64 v[28:29], v[18:19], 0, s[4:5]
	v_lshl_add_u64 v[84:85], v[28:29], 0, v[84:85]
	v_add_u32_e32 v52, s0, v34
	global_store_dwordx4 v[84:85], v[48:51], off
	s_nop 1
	v_mov_b32_e32 v48, 0
	v_mov_b32_e32 v49, 0
	v_mov_b32_e32 v50, 0
	v_mov_b32_e32 v51, 0
	v_cvt_pk_fp8_f32 v48, v53, v55
	v_cvt_pk_fp8_f32 v49, v61, v63
	v_cvt_pk_fp8_f32 v50, v69, v71
	v_cvt_pk_fp8_f32 v51, v77, v79
	v_cvt_pk_fp8_f32 v48, v57, v59 op_sel:[0,0,1]
	v_cvt_pk_fp8_f32 v49, v65, v67 op_sel:[0,0,1]
	v_cvt_pk_fp8_f32 v50, v73, v75 op_sel:[0,0,1]
	v_cvt_pk_fp8_f32 v51, v81, v83 op_sel:[0,0,1]
	v_ashrrev_i32_e32 v53, 31, v52
	v_lshlrev_b64 v[52:53], 10, v[52:53]
	v_lshl_add_u64 v[28:29], v[28:29], 0, v[52:53]
	global_store_dwordx4 v[28:29], v[48:51], off
	s_waitcnt lgkmcnt(0)

; #define LAS __attribute__((address_space(3)))
; __device__ __forceinline__ void tr_item(const float* W, int ld, int K, int nblk, int item, bf16* WT, bool gu, LAS float* scr, int lane) {
;     const int kb = item / nblk, nb = item % nblk, k0 = 64 * kb, n0 = 32 * nb;
;     int drow0 = n0;
;     if (gu) { const int bj = n0 / FF, j = n0 - bj * FF; drow0 = 256 * (j / 128) + 128 * bj + (j % 128); }
;     { float t_[32];
; #pragma unroll
;       for (int i = 0; i < 32; ++i) t_[i] = W[(size_t)(k0 + 2 * i + (lane >> 5)) * ld + n0 + (lane & 31)];
; #pragma unroll
;       for (int i = 0; i < 32; ++i) scr[(2 * i + (lane >> 5)) * 33 + (lane & 31)] = t_[i]; }
; __device__ __forceinline__ void convert_items(Frame& F, const Args& a, int lo, int hi, int w, int nw) {
;     ...
;         if (r < I_SO) { tr_item(a.in[12], D, D, 32, r, (bf16*)(F.ws + WS_WSWAOUT), false, scr, lane); continue; } r -= I_SO;
.LBB0_1347:
	s_andn2_b64 vcc, exec, s[4:5]
	s_cbranch_vccnz .LBB0_1349
	s_add_i32 s0, s12, 0x2000
	s_and_b32 s5, s0, 0x1ffc0
	s_and_b32 s4, s9, 0x3e0
	v_add_u32_e32 v28, s5, v30
	s_lshl_b32 s0, s4, 2
	v_ashrrev_i32_e32 v29, 31, v28
	v_lshl_add_u64 v[48:49], v[8:9], 0, s[0:1]
	v_lshlrev_b64 v[28:29], 12, v[28:29]
	v_lshl_add_u64 v[28:29], v[48:49], 0, v[28:29]
	v_add_co_u32_e32 v48, vcc, 0x2000, v28
	global_load_dword v50, v[28:29], off nt
	s_nop 0
	v_addc_co_u32_e32 v49, vcc, 0, v29, vcc
	global_load_dword v51, v[48:49], off nt
	v_add_co_u32_e32 v48, vcc, 0x4000, v28
	s_lshl_b32 s0, s5, 1
	s_nop 0
	v_addc_co_u32_e32 v49, vcc, 0, v29, vcc
	global_load_dword v52, v[48:49], off nt
	v_add_co_u32_e32 v48, vcc, 0x6000, v28
	s_nop 1
	v_addc_co_u32_e32 v49, vcc, 0, v29, vcc
	global_load_dword v53, v[48:49], off nt
	v_add_co_u32_e32 v48, vcc, 0x8000, v28
	s_nop 1
	v_addc_co_u32_e32 v49, vcc, 0, v29, vcc
	global_load_dword v54, v[48:49], off nt
	v_add_co_u32_e32 v48, vcc, 0xa000, v28
	s_nop 1
	v_addc_co_u32_e32 v49, vcc, 0, v29, vcc
	global_load_dword v55, v[48:49], off nt
	v_add_co_u32_e32 v48, vcc, 0xc000, v28
	s_nop 1
	v_addc_co_u32_e32 v49, vcc, 0, v29, vcc
	global_load_dword v56, v[48:49], off nt
	v_add_co_u32_e32 v48, vcc, 0xe000, v28
	s_nop 1
	v_addc_co_u32_e32 v49, vcc, 0, v29, vcc
	global_load_dword v57, v[48:49], off nt
	v_add_co_u32_e32 v48, vcc, 0x10000, v28
	s_nop 1
	v_addc_co_u32_e32 v49, vcc, 0, v29, vcc
	global_load_dword v58, v[48:49], off nt
	v_add_co_u32_e32 v48, vcc, 0x12000, v28
	s_nop 1
	v_addc_co_u32_e32 v49, vcc, 0, v29, vcc
	global_load_dword v59, v[48:49], off nt
	v_add_co_u32_e32 v48, vcc, 0x14000, v28
	s_nop 1
	v_addc_co_u32_e32 v49, vcc, 0, v29, vcc
	global_load_dword v60, v[48:49], off nt
	v_add_co_u32_e32 v48, vcc, 0x16000, v28
	s_nop 1
	v_addc_co_u32_e32 v49, vcc, 0, v29, vcc
	global_load_dword v61, v[48:49], off nt
	v_add_co_u32_e32 v48, vcc, 0x18000, v28
	s_nop 1
	v_addc_co_u32_e32 v49, vcc, 0, v29, vcc
	global_load_dword v62, v[48:49], off nt
	v_add_co_u32_e32 v48, vcc, 0x1a000, v28
	s_nop 1
	v_addc_co_u32_e32 v49, vcc, 0, v29, vcc
	global_load_dword v63, v[48:49], off nt
	v_add_co_u32_e32 v48, vcc, 0x1c000, v28
	s_nop 1
	v_addc_co_u32_e32 v49, vcc, 0, v29, vcc
	global_load_dword v64, v[48:49], off nt
	v_add_co_u32_e32 v48, vcc, 0x1e000, v28
	s_nop 1
	v_addc_co_u32_e32 v49, vcc, 0, v29, vcc
	global_load_dword v65, v[48:49], off nt
	v_add_co_u32_e32 v48, vcc, 0x20000, v28
	s_nop 1
	v_addc_co_u32_e32 v49, vcc, 0, v29, vcc
	global_load_dword v66, v[48:49], off nt
	v_add_co_u32_e32 v48, vcc, 0x22000, v28
	s_nop 1
	v_addc_co_u32_e32 v49, vcc, 0, v29, vcc
	global_load_dword v67, v[48:49], off nt
	v_add_co_u32_e32 v48, vcc, 0x24000, v28
	s_nop 1
	v_addc_co_u32_e32 v49, vcc, 0, v29, vcc
	global_load_dword v68, v[48:49], off nt
	v_add_co_u32_e32 v48, vcc, 0x26000, v28
	s_nop 1
	v_addc_co_u32_e32 v49, vcc, 0, v29, vcc
	global_load_dword v69, v[48:49], off nt
	v_add_co_u32_e32 v48, vcc, 0x28000, v28
	s_nop 1
	v_addc_co_u32_e32 v49, vcc, 0, v29, vcc
	global_load_dword v70, v[48:49], off nt
	v_add_co_u32_e32 v48, vcc, 0x2a000, v28
	s_nop 1
	v_addc_co_u32_e32 v49, vcc, 0, v29, vcc
	global_load_dword v71, v[48:49], off nt
	v_add_co_u32_e32 v48, vcc, 0x2c000, v28
	s_nop 1
	v_addc_co_u32_e32 v49, vcc, 0, v29, vcc
	global_load_dword v72, v[48:49], off nt
	v_add_co_u32_e32 v48, vcc, 0x2e000, v28
	s_nop 1
	v_addc_co_u32_e32 v49, vcc, 0, v29, vcc
	global_load_dword v73, v[48:49], off nt
	v_add_co_u32_e32 v48, vcc, 0x30000, v28
	s_nop 1
	v_addc_co_u32_e32 v49, vcc, 0, v29, vcc
	global_load_dword v74, v[48:49], off nt
	v_add_co_u32_e32 v48, vcc, 0x32000, v28
	s_nop 1
	v_addc_co_u32_e32 v49, vcc, 0, v29, vcc
	global_load_dword v75, v[48:49], off nt
	v_add_co_u32_e32 v48, vcc, 0x34000, v28
	s_nop 1
	v_addc_co_u32_e32 v49, vcc, 0, v29, vcc
	global_load_dword v76, v[48:49], off nt
	v_add_co_u32_e32 v48, vcc, 0x36000, v28
	s_nop 1
	v_addc_co_u32_e32 v49, vcc, 0, v29, vcc
	global_load_dword v77, v[48:49], off nt
	v_add_co_u32_e32 v48, vcc, 0x38000, v28
	s_nop 1
	v_addc_co_u32_e32 v49, vcc, 0, v29, vcc
	global_load_dword v78, v[48:49], off nt
	v_add_co_u32_e32 v48, vcc, 0x3a000, v28
	s_nop 1
	v_addc_co_u32_e32 v49, vcc, 0, v29, vcc
	global_load_dword v79, v[48:49], off nt
	v_add_co_u32_e32 v48, vcc, 0x3c000, v28
	s_nop 1
	v_addc_co_u32_e32 v49, vcc, 0, v29, vcc
	v_add_co_u32_e32 v28, vcc, 0x3e000, v28
	global_load_dword v48, v[48:49], off nt
	s_nop 0
	v_addc_co_u32_e32 v29, vcc, 0, v29, vcc
	global_load_dword v28, v[28:29], off nt
	s_waitcnt vmcnt(0)
	ds_write2_b32 v31, v50, v51 offset1:66
	ds_write2_b32 v31, v52, v53 offset0:132 offset1:198
	ds_write2_b32 v40, v54, v55 offset0:8 offset1:74
	ds_write2_b32 v40, v56, v57 offset0:140 offset1:206
	ds_write2_b32 v41, v58, v59 offset0:16 offset1:82
	ds_write2_b32 v41, v60, v61 offset0:148 offset1:214
	ds_write2_b32 v42, v62, v63 offset0:24 offset1:90
	ds_write2_b32 v42, v64, v65 offset0:156 offset1:222
	ds_write2_b32 v43, v66, v67 offset0:32 offset1:98
	ds_write2_b32 v43, v68, v69 offset0:164 offset1:230
	ds_write2_b32 v44, v70, v71 offset0:40 offset1:106
	ds_write2_b32 v44, v72, v73 offset0:172 offset1:238
	ds_write2_b32 v45, v74, v75 offset0:48 offset1:114
	ds_write2_b32 v45, v76, v77 offset0:180 offset1:246
	ds_write2_b32 v46, v78, v79 offset0:56 offset1:122
	ds_write2_b32 v46, v48, v28 offset0:188 offset1:254
	s_waitcnt lgkmcnt(0)
; #define GAS __attribute__((address_space(1)))
; #define LAS __attribute__((address_space(3)))
; #define LDS_WAIT() asm volatile("s_waitcnt lgkmcnt(0)" ::: "memory")
; __device__ __forceinline__ unsigned pk2(float lo, float hi) { return f2bf(lo) | (f2bf(hi) << 16); }
; __device__ __forceinline__ void tr_item(const float* W, int ld, int K, int nblk, int item, bf16* WT, bool gu, LAS float* scr, int lane) {
;     ...
;     LDS_WAIT(); asm volatile("" ::: "memory");
;     const int c = lane & 7;
; #pragma unroll
;     for (int j = 0; j < 4; ++j) { const int n = (lane >> 3) + 8 * j; const LAS float* s = scr + (8 * c) * 33 + n;
;         v4u o; o.x = pk2(s[0 * 33], s[1 * 33]); o.y = pk2(s[2 * 33], s[3 * 33]); o.z = pk2(s[4 * 33], s[5 * 33]); o.w = pk2(s[6 * 33], s[7 * 33]);
;         *(GAS v4u*)(WT + (size_t)(drow0 + n) * K + k0 + 8 * c) = o; }
;     LDS_WAIT(); asm volatile("" ::: "memory");
	ds_read2_b32 v[52:53], v36 offset0:33 offset1:41
	ds_read2_b32 v[54:55], v36 offset1:8
	ds_read2_b32 v[56:57], v36 offset0:66 offset1:74
	ds_read2_b32 v[58:59], v36 offset0:99 offset1:107
	ds_read2_b32 v[60:61], v36 offset0:132 offset1:140
	ds_read2_b32 v[62:63], v36 offset0:165 offset1:173
	ds_read2_b32 v[64:65], v36 offset0:198 offset1:206
	ds_read2_b32 v[66:67], v36 offset0:231 offset1:239
	s_waitcnt lgkmcnt(7)
	v_bfe_u32 v49, v52, 16, 1
	s_waitcnt lgkmcnt(6)
	v_bfe_u32 v48, v54, 16, 1
	v_add3_u32 v48, v54, v48, s15
	v_lshrrev_b32_e32 v48, 16, v48
	v_add3_u32 v49, v52, v49, s15
	v_and_or_b32 v48, v49, s16, v48
	s_waitcnt lgkmcnt(5)
	v_bfe_u32 v49, v56, 16, 1
	v_add3_u32 v49, v56, v49, s15
	s_waitcnt lgkmcnt(4)
	v_bfe_u32 v50, v58, 16, 1
	v_lshrrev_b32_e32 v49, 16, v49
	v_add3_u32 v50, v58, v50, s15
	v_and_or_b32 v49, v50, s16, v49
	s_waitcnt lgkmcnt(3)
	v_bfe_u32 v50, v60, 16, 1
	v_add3_u32 v50, v60, v50, s15
	s_waitcnt lgkmcnt(2)
	v_bfe_u32 v51, v62, 16, 1
	v_lshrrev_b32_e32 v50, 16, v50
	v_add3_u32 v51, v62, v51, s15
	v_and_or_b32 v50, v51, s16, v50
	s_waitcnt lgkmcnt(1)
	v_bfe_u32 v51, v64, 16, 1
	v_add_u32_e32 v68, s4, v35
	v_add3_u32 v51, v64, v51, s15
	s_waitcnt lgkmcnt(0)
	v_bfe_u32 v52, v66, 16, 1
	v_ashrrev_i32_e32 v69, 31, v68
	v_lshl_add_u64 v[28:29], v[20:21], 0, s[0:1]
	v_lshrrev_b32_e32 v51, 16, v51
	v_add3_u32 v52, v66, v52, s15
	v_lshlrev_b64 v[68:69], 11, v[68:69]
	v_and_or_b32 v51, v52, s16, v51
	v_lshl_add_u64 v[68:69], v[28:29], 0, v[68:69]
	global_store_dwordx4 v[68:69], v[48:51], off
	v_bfe_u32 v52, v67, 16, 1
	v_add3_u32 v52, v67, v52, s15
	v_bfe_u32 v48, v55, 16, 1
	v_add3_u32 v48, v55, v48, s15
	v_bfe_u32 v49, v53, 16, 1
	v_lshrrev_b32_e32 v48, 16, v48
	v_add3_u32 v49, v53, v49, s15
	v_and_or_b32 v48, v49, s16, v48
	v_bfe_u32 v49, v57, 16, 1
	v_add3_u32 v49, v57, v49, s15
	v_bfe_u32 v50, v59, 16, 1
	v_lshrrev_b32_e32 v49, 16, v49
	v_add3_u32 v50, v59, v50, s15
	v_and_or_b32 v49, v50, s16, v49
	v_bfe_u32 v50, v61, 16, 1
	v_add3_u32 v50, v61, v50, s15
	v_bfe_u32 v51, v63, 16, 1
	v_lshrrev_b32_e32 v50, 16, v50
	v_add3_u32 v51, v63, v51, s15
	v_and_or_b32 v50, v51, s16, v50
	v_bfe_u32 v51, v65, 16, 1
	v_add3_u32 v51, v65, v51, s15
	v_lshrrev_b32_e32 v51, 16, v51
	v_and_or_b32 v51, v52, s16, v51
	v_add_u32_e32 v52, s4, v37
	v_ashrrev_i32_e32 v53, 31, v52
	v_lshlrev_b64 v[52:53], 11, v[52:53]
	v_lshl_add_u64 v[52:53], v[28:29], 0, v[52:53]
	global_store_dwordx4 v[52:53], v[48:51], off
	ds_read2_b32 v[52:53], v36 offset0:49 offset1:57
	ds_read2_b32 v[54:55], v36 offset0:16 offset1:24
	ds_read2_b32 v[56:57], v36 offset0:82 offset1:90
	ds_read2_b32 v[58:59], v36 offset0:115 offset1:123
	ds_read2_b32 v[60:61], v36 offset0:148 offset1:156
	ds_read2_b32 v[62:63], v36 offset0:181 offset1:189
	ds_read2_b32 v[64:65], v36 offset0:214 offset1:222
	ds_read2_b32 v[66:67], v36 offset0:247 offset1:255
	s_waitcnt lgkmcnt(7)
	v_bfe_u32 v49, v52, 16, 1
	s_waitcnt lgkmcnt(6)
	v_bfe_u32 v48, v54, 16, 1
	v_add3_u32 v48, v54, v48, s15
	v_lshrrev_b32_e32 v48, 16, v48
	v_add3_u32 v49, v52, v49, s15
	v_and_or_b32 v48, v49, s16, v48
	s_waitcnt lgkmcnt(5)
	v_bfe_u32 v49, v56, 16, 1
	v_add3_u32 v49, v56, v49, s15
	s_waitcnt lgkmcnt(4)
	v_bfe_u32 v50, v58, 16, 1
	v_lshrrev_b32_e32 v49, 16, v49
	v_add3_u32 v50, v58, v50, s15
	v_and_or_b32 v49, v50, s16, v49
	s_waitcnt lgkmcnt(3)
	v_bfe_u32 v50, v60, 16, 1
	v_add3_u32 v50, v60, v50, s15
	s_waitcnt lgkmcnt(2)
	v_bfe_u32 v51, v62, 16, 1
	v_lshrrev_b32_e32 v50, 16, v50
	v_add3_u32 v51, v62, v51, s15
	v_and_or_b32 v50, v51, s16, v50
	s_waitcnt lgkmcnt(1)
	v_bfe_u32 v51, v64, 16, 1
	v_add_u32_e32 v68, s4, v38
	v_add3_u32 v51, v64, v51, s15
	s_waitcnt lgkmcnt(0)
	v_bfe_u32 v52, v66, 16, 1
	v_ashrrev_i32_e32 v69, 31, v68
	v_lshrrev_b32_e32 v51, 16, v51
	v_add3_u32 v52, v66, v52, s15
	v_lshlrev_b64 v[68:69], 11, v[68:69]
	v_and_or_b32 v51, v52, s16, v51
	v_lshl_add_u64 v[68:69], v[28:29], 0, v[68:69]
	global_store_dwordx4 v[68:69], v[48:51], off
	v_bfe_u32 v52, v67, 16, 1
	v_add3_u32 v52, v67, v52, s15
	v_bfe_u32 v48, v55, 16, 1
	v_add3_u32 v48, v55, v48, s15
	v_bfe_u32 v49, v53, 16, 1
	v_lshrrev_b32_e32 v48, 16, v48
	v_add3_u32 v49, v53, v49, s15
	v_and_or_b32 v48, v49, s16, v48
	v_bfe_u32 v49, v57, 16, 1
	v_add3_u32 v49, v57, v49, s15
	v_bfe_u32 v50, v59, 16, 1
	v_lshrrev_b32_e32 v49, 16, v49
	v_add3_u32 v50, v59, v50, s15
	v_and_or_b32 v49, v50, s16, v49
	v_bfe_u32 v50, v61, 16, 1
	v_add3_u32 v50, v61, v50, s15
	v_bfe_u32 v51, v63, 16, 1
	v_lshrrev_b32_e32 v50, 16, v50
	v_add3_u32 v51, v63, v51, s15
	v_and_or_b32 v50, v51, s16, v50
	v_bfe_u32 v51, v65, 16, 1
	v_add3_u32 v51, v65, v51, s15
	v_lshrrev_b32_e32 v51, 16, v51
	v_and_or_b32 v51, v52, s16, v51
	v_add_u32_e32 v52, s4, v39
	v_ashrrev_i32_e32 v53, 31, v52
	v_lshlrev_b64 v[52:53], 11, v[52:53]
	v_lshl_add_u64 v[28:29], v[28:29], 0, v[52:53]
	global_store_dwordx4 v[28:29], v[48:51], off
	s_waitcnt lgkmcnt(0)

; #define LAS __attribute__((address_space(3)))
; __device__ __forceinline__ void tr_item(const float* W, int ld, int K, int nblk, int item, bf16* WT, bool gu, LAS float* scr, int lane) {
;     const int kb = item / nblk, nb = item % nblk, k0 = 64 * kb, n0 = 32 * nb;
;     int drow0 = n0;
;     if (gu) { const int bj = n0 / FF, j = n0 - bj * FF; drow0 = 256 * (j / 128) + 128 * bj + (j % 128); }
;     { float t_[32];
; #pragma unroll
;       for (int i = 0; i < 32; ++i) t_[i] = W[(size_t)(k0 + 2 * i + (lane >> 5)) * ld + n0 + (lane & 31)];
; #pragma unroll
;       for (int i = 0; i < 32; ++i) scr[(2 * i + (lane >> 5)) * 33 + (lane & 31)] = t_[i]; }
; __device__ __forceinline__ void convert_items(Frame& F, const Args& a, int lo, int hi, int w, int nw) {
;     ...
;         if (r < I_SI) { tr_item(a.in[10], D + 512, D, 48, r, (bf16*)(F.ws + WS_WSWAIN), false, scr, lane); continue; } r -= I_SI;
.LBB0_1350:
	s_andn2_b64 vcc, exec, s[4:5]
	s_cbranch_vccnz .LBB0_1352
	s_add_i32 s0, s8, 0xf800
	s_and_b32 s4, s0, 0xffff
	s_mul_i32 s4, s4, 0xaaab
	s_lshr_b32 s5, s4, 21
	s_mul_i32 s4, s5, 48
	s_sub_i32 s0, s0, s4
	s_lshl_b32 s0, s0, 5
	s_and_b32 s4, s0, 0xffe0
	s_lshl_b32 s0, s4, 2
	v_lshl_add_u32 v50, s5, 6, v30
	v_lshl_add_u64 v[28:29], v[10:11], 0, s[0:1]
	v_mad_i64_i32 v[48:49], s[6:7], v50, s17, v[28:29]
	global_load_dword v51, v[48:49], off nt
	v_add_u32_e32 v48, 2, v50
	v_mad_i64_i32 v[48:49], s[6:7], v48, s17, v[28:29]
	global_load_dword v52, v[48:49], off nt
	v_add_u32_e32 v48, 4, v50
	v_mad_i64_i32 v[48:49], s[6:7], v48, s17, v[28:29]
	global_load_dword v53, v[48:49], off nt
	v_add_u32_e32 v48, 6, v50
	v_mad_i64_i32 v[48:49], s[6:7], v48, s17, v[28:29]
	global_load_dword v54, v[48:49], off nt
	v_add_u32_e32 v48, 8, v50
	v_mad_i64_i32 v[48:49], s[6:7], v48, s17, v[28:29]
	global_load_dword v55, v[48:49], off nt
	v_add_u32_e32 v48, 10, v50
	v_mad_i64_i32 v[48:49], s[6:7], v48, s17, v[28:29]
	global_load_dword v56, v[48:49], off nt
	v_add_u32_e32 v48, 12, v50
	v_mad_i64_i32 v[48:49], s[6:7], v48, s17, v[28:29]
	global_load_dword v57, v[48:49], off nt
	v_add_u32_e32 v48, 14, v50
	v_mad_i64_i32 v[48:49], s[6:7], v48, s17, v[28:29]
	global_load_dword v58, v[48:49], off nt
	v_add_u32_e32 v48, 16, v50
	v_mad_i64_i32 v[48:49], s[6:7], v48, s17, v[28:29]
	global_load_dword v59, v[48:49], off nt
	v_add_u32_e32 v48, 18, v50
	v_mad_i64_i32 v[48:49], s[6:7], v48, s17, v[28:29]
	global_load_dword v60, v[48:49], off nt
	v_add_u32_e32 v48, 20, v50
	v_mad_i64_i32 v[48:49], s[6:7], v48, s17, v[28:29]
	global_load_dword v61, v[48:49], off nt
	v_add_u32_e32 v48, 22, v50
	v_mad_i64_i32 v[48:49], s[6:7], v48, s17, v[28:29]
	global_load_dword v62, v[48:49], off nt
	v_add_u32_e32 v48, 24, v50
	v_mad_i64_i32 v[48:49], s[6:7], v48, s17, v[28:29]
	global_load_dword v63, v[48:49], off nt
	v_add_u32_e32 v48, 26, v50
	v_mad_i64_i32 v[48:49], s[6:7], v48, s17, v[28:29]
	global_load_dword v64, v[48:49], off nt
	v_add_u32_e32 v48, 28, v50
	v_mad_i64_i32 v[48:49], s[6:7], v48, s17, v[28:29]
	global_load_dword v65, v[48:49], off nt
	v_add_u32_e32 v48, 30, v50
	v_mad_i64_i32 v[48:49], s[6:7], v48, s17, v[28:29]
	global_load_dword v66, v[48:49], off nt
	v_add_u32_e32 v48, 32, v50
	v_mad_i64_i32 v[48:49], s[6:7], v48, s17, v[28:29]
	global_load_dword v67, v[48:49], off nt
	v_add_u32_e32 v48, 34, v50
	v_mad_i64_i32 v[48:49], s[6:7], v48, s17, v[28:29]
	global_load_dword v68, v[48:49], off nt
	v_add_u32_e32 v48, 36, v50
	v_mad_i64_i32 v[48:49], s[6:7], v48, s17, v[28:29]
	global_load_dword v69, v[48:49], off nt
	v_add_u32_e32 v48, 38, v50
	v_mad_i64_i32 v[48:49], s[6:7], v48, s17, v[28:29]
	global_load_dword v70, v[48:49], off nt
	v_add_u32_e32 v48, 40, v50
	v_mad_i64_i32 v[48:49], s[6:7], v48, s17, v[28:29]
	global_load_dword v71, v[48:49], off nt
	v_add_u32_e32 v48, 42, v50
	v_mad_i64_i32 v[48:49], s[6:7], v48, s17, v[28:29]
	global_load_dword v72, v[48:49], off nt
	v_add_u32_e32 v48, 44, v50
	v_mad_i64_i32 v[48:49], s[6:7], v48, s17, v[28:29]
	global_load_dword v73, v[48:49], off nt
	v_add_u32_e32 v48, 46, v50
	v_mad_i64_i32 v[48:49], s[6:7], v48, s17, v[28:29]
	global_load_dword v74, v[48:49], off nt
	v_add_u32_e32 v48, 48, v50
	v_mad_i64_i32 v[48:49], s[6:7], v48, s17, v[28:29]
	global_load_dword v75, v[48:49], off nt
	v_add_u32_e32 v48, 50, v50
	v_mad_i64_i32 v[48:49], s[6:7], v48, s17, v[28:29]
	global_load_dword v76, v[48:49], off nt
	v_add_u32_e32 v48, 52, v50
	v_mad_i64_i32 v[48:49], s[6:7], v48, s17, v[28:29]
	global_load_dword v77, v[48:49], off nt
	v_add_u32_e32 v48, 54, v50
	v_mad_i64_i32 v[48:49], s[6:7], v48, s17, v[28:29]
	global_load_dword v78, v[48:49], off nt
	v_add_u32_e32 v48, 56, v50
	v_mad_i64_i32 v[48:49], s[6:7], v48, s17, v[28:29]
	global_load_dword v79, v[48:49], off nt
	v_add_u32_e32 v48, 58, v50
	v_mad_i64_i32 v[48:49], s[6:7], v48, s17, v[28:29]
	global_load_dword v80, v[48:49], off nt
	v_add_u32_e32 v48, 60, v50
	v_mad_i64_i32 v[48:49], s[6:7], v48, s17, v[28:29]
	global_load_dword v48, v[48:49], off nt
	v_add_u32_e32 v49, 62, v50
	v_mad_i64_i32 v[28:29], s[6:7], v49, s17, v[28:29]
	global_load_dword v28, v[28:29], off nt
	s_waitcnt vmcnt(0)
	ds_write2_b32 v31, v51, v52 offset1:66
	ds_write2_b32 v31, v53, v54 offset0:132 offset1:198
	ds_write2_b32 v40, v55, v56 offset0:8 offset1:74
	ds_write2_b32 v40, v57, v58 offset0:140 offset1:206
	ds_write2_b32 v41, v59, v60 offset0:16 offset1:82
	ds_write2_b32 v41, v61, v62 offset0:148 offset1:214
	ds_write2_b32 v42, v63, v64 offset0:24 offset1:90
	ds_write2_b32 v42, v65, v66 offset0:156 offset1:222
	ds_write2_b32 v43, v67, v68 offset0:32 offset1:98
	ds_write2_b32 v43, v69, v70 offset0:164 offset1:230
	ds_write2_b32 v44, v71, v72 offset0:40 offset1:106
	ds_write2_b32 v44, v73, v74 offset0:172 offset1:238
	ds_write2_b32 v45, v75, v76 offset0:48 offset1:114
	ds_write2_b32 v45, v77, v78 offset0:180 offset1:246
	ds_write2_b32 v46, v79, v80 offset0:56 offset1:122
	ds_write2_b32 v46, v48, v28 offset0:188 offset1:254
	s_waitcnt lgkmcnt(0)
; #define GAS __attribute__((address_space(1)))
; #define LAS __attribute__((address_space(3)))
; #define LDS_WAIT() asm volatile("s_waitcnt lgkmcnt(0)" ::: "memory")
; __device__ __forceinline__ unsigned pk2(float lo, float hi) { return f2bf(lo) | (f2bf(hi) << 16); }
; __device__ __forceinline__ void tr_item(const float* W, int ld, int K, int nblk, int item, bf16* WT, bool gu, LAS float* scr, int lane) {
;     ...
;       for (int i = 0; i < 32; ++i) scr[(2 * i + (lane >> 5)) * 33 + (lane & 31)] = t_[i]; }
;     LDS_WAIT(); asm volatile("" ::: "memory");
;     const int c = lane & 7;
; #pragma unroll
;     for (int j = 0; j < 4; ++j) { const int n = (lane >> 3) + 8 * j; const LAS float* s = scr + (8 * c) * 33 + n;
;         v4u o; o.x = pk2(s[0 * 33], s[1 * 33]); o.y = pk2(s[2 * 33], s[3 * 33]); o.z = pk2(s[4 * 33], s[5 * 33]); o.w = pk2(s[6 * 33], s[7 * 33]);
;         *(GAS v4u*)(WT + (size_t)(drow0 + n) * K + k0 + 8 * c) = o; }
;     LDS_WAIT(); asm volatile("" ::: "memory");
	ds_read2_b32 v[52:53], v36 offset0:33 offset1:41
	ds_read2_b32 v[54:55], v36 offset1:8
	ds_read2_b32 v[56:57], v36 offset0:66 offset1:74
	ds_read2_b32 v[58:59], v36 offset0:99 offset1:107
	ds_read2_b32 v[60:61], v36 offset0:132 offset1:140
	ds_read2_b32 v[62:63], v36 offset0:165 offset1:173
	ds_read2_b32 v[64:65], v36 offset0:198 offset1:206
	ds_read2_b32 v[66:67], v36 offset0:231 offset1:239
	s_waitcnt lgkmcnt(7)
	v_bfe_u32 v49, v52, 16, 1
	s_waitcnt lgkmcnt(6)
	v_bfe_u32 v48, v54, 16, 1
	v_add3_u32 v48, v54, v48, s15
	v_lshrrev_b32_e32 v48, 16, v48
	v_add3_u32 v49, v52, v49, s15
	v_and_or_b32 v48, v49, s16, v48
	s_waitcnt lgkmcnt(5)
	v_bfe_u32 v49, v56, 16, 1
	v_add3_u32 v49, v56, v49, s15
	s_waitcnt lgkmcnt(4)
	v_bfe_u32 v50, v58, 16, 1
	v_lshrrev_b32_e32 v49, 16, v49
	v_add3_u32 v50, v58, v50, s15
	v_and_or_b32 v49, v50, s16, v49
	s_waitcnt lgkmcnt(3)
	v_bfe_u32 v50, v60, 16, 1
	v_add3_u32 v50, v60, v50, s15
	s_waitcnt lgkmcnt(2)
	v_bfe_u32 v51, v62, 16, 1
	v_lshrrev_b32_e32 v50, 16, v50
	v_add3_u32 v51, v62, v51, s15
	v_and_or_b32 v50, v51, s16, v50
	s_waitcnt lgkmcnt(1)
	v_bfe_u32 v51, v64, 16, 1
	v_add_u32_e32 v68, s4, v35
	s_lshl_b32 s0, s5, 7
	v_add3_u32 v51, v64, v51, s15
	s_waitcnt lgkmcnt(0)
	v_bfe_u32 v52, v66, 16, 1
	v_ashrrev_i32_e32 v69, 31, v68
	v_lshl_add_u64 v[28:29], v[22:23], 0, s[0:1]
	v_lshrrev_b32_e32 v51, 16, v51
	v_add3_u32 v52, v66, v52, s15
	v_lshlrev_b64 v[68:69], 11, v[68:69]
	v_and_or_b32 v51, v52, s16, v51
	v_lshl_add_u64 v[68:69], v[28:29], 0, v[68:69]
	global_store_dwordx4 v[68:69], v[48:51], off
	v_bfe_u32 v52, v67, 16, 1
	v_add3_u32 v52, v67, v52, s15
	v_bfe_u32 v48, v55, 16, 1
	v_add3_u32 v48, v55, v48, s15
	v_bfe_u32 v49, v53, 16, 1
	v_lshrrev_b32_e32 v48, 16, v48
	v_add3_u32 v49, v53, v49, s15
	v_and_or_b32 v48, v49, s16, v48
	v_bfe_u32 v49, v57, 16, 1
	v_add3_u32 v49, v57, v49, s15
	v_bfe_u32 v50, v59, 16, 1
	v_lshrrev_b32_e32 v49, 16, v49
	v_add3_u32 v50, v59, v50, s15
	v_and_or_b32 v49, v50, s16, v49
	v_bfe_u32 v50, v61, 16, 1
	v_add3_u32 v50, v61, v50, s15
	v_bfe_u32 v51, v63, 16, 1
	v_lshrrev_b32_e32 v50, 16, v50
	v_add3_u32 v51, v63, v51, s15
	v_and_or_b32 v50, v51, s16, v50
	v_bfe_u32 v51, v65, 16, 1
	v_add3_u32 v51, v65, v51, s15
	v_lshrrev_b32_e32 v51, 16, v51
	v_and_or_b32 v51, v52, s16, v51
	v_add_u32_e32 v52, s4, v37
	v_ashrrev_i32_e32 v53, 31, v52
	v_lshlrev_b64 v[52:53], 11, v[52:53]
	v_lshl_add_u64 v[52:53], v[28:29], 0, v[52:53]
	global_store_dwordx4 v[52:53], v[48:51], off
	ds_read2_b32 v[52:53], v36 offset0:49 offset1:57
	ds_read2_b32 v[54:55], v36 offset0:16 offset1:24
	ds_read2_b32 v[56:57], v36 offset0:82 offset1:90
	ds_read2_b32 v[58:59], v36 offset0:115 offset1:123
	ds_read2_b32 v[60:61], v36 offset0:148 offset1:156
	ds_read2_b32 v[62:63], v36 offset0:181 offset1:189
	ds_read2_b32 v[64:65], v36 offset0:214 offset1:222
	ds_read2_b32 v[66:67], v36 offset0:247 offset1:255
	s_waitcnt lgkmcnt(7)
	v_bfe_u32 v49, v52, 16, 1
	s_waitcnt lgkmcnt(6)
	v_bfe_u32 v48, v54, 16, 1
	v_add3_u32 v48, v54, v48, s15
	v_lshrrev_b32_e32 v48, 16, v48
	v_add3_u32 v49, v52, v49, s15
	v_and_or_b32 v48, v49, s16, v48
	s_waitcnt lgkmcnt(5)
	v_bfe_u32 v49, v56, 16, 1
	v_add3_u32 v49, v56, v49, s15
	s_waitcnt lgkmcnt(4)
	v_bfe_u32 v50, v58, 16, 1
	v_lshrrev_b32_e32 v49, 16, v49
	v_add3_u32 v50, v58, v50, s15
	v_and_or_b32 v49, v50, s16, v49
	s_waitcnt lgkmcnt(3)
	v_bfe_u32 v50, v60, 16, 1
	v_add3_u32 v50, v60, v50, s15
	s_waitcnt lgkmcnt(2)
	v_bfe_u32 v51, v62, 16, 1
	v_lshrrev_b32_e32 v50, 16, v50
	v_add3_u32 v51, v62, v51, s15
	v_and_or_b32 v50, v51, s16, v50
	s_waitcnt lgkmcnt(1)
	v_bfe_u32 v51, v64, 16, 1
	v_add_u32_e32 v68, s4, v38
	v_add3_u32 v51, v64, v51, s15
	s_waitcnt lgkmcnt(0)
	v_bfe_u32 v52, v66, 16, 1
	v_ashrrev_i32_e32 v69, 31, v68
	v_lshrrev_b32_e32 v51, 16, v51
	v_add3_u32 v52, v66, v52, s15
	v_lshlrev_b64 v[68:69], 11, v[68:69]
	v_and_or_b32 v51, v52, s16, v51
	v_lshl_add_u64 v[68:69], v[28:29], 0, v[68:69]
	global_store_dwordx4 v[68:69], v[48:51], off
	v_bfe_u32 v52, v67, 16, 1
	v_add3_u32 v52, v67, v52, s15
	v_bfe_u32 v48, v55, 16, 1
	v_add3_u32 v48, v55, v48, s15
	v_bfe_u32 v49, v53, 16, 1
	v_lshrrev_b32_e32 v48, 16, v48
	v_add3_u32 v49, v53, v49, s15
	v_and_or_b32 v48, v49, s16, v48
	v_bfe_u32 v49, v57, 16, 1
	v_add3_u32 v49, v57, v49, s15
	v_bfe_u32 v50, v59, 16, 1
	v_lshrrev_b32_e32 v49, 16, v49
	v_add3_u32 v50, v59, v50, s15
	v_and_or_b32 v49, v50, s16, v49
	v_bfe_u32 v50, v61, 16, 1
	v_add3_u32 v50, v61, v50, s15
	v_bfe_u32 v51, v63, 16, 1
	v_lshrrev_b32_e32 v50, 16, v50
	v_add3_u32 v51, v63, v51, s15
	v_and_or_b32 v50, v51, s16, v50
	v_bfe_u32 v51, v65, 16, 1
	v_add3_u32 v51, v65, v51, s15
	v_lshrrev_b32_e32 v51, 16, v51
	v_and_or_b32 v51, v52, s16, v51
	v_add_u32_e32 v52, s4, v39
	v_ashrrev_i32_e32 v53, 31, v52
	v_lshlrev_b64 v[52:53], 11, v[52:53]
	v_lshl_add_u64 v[28:29], v[28:29], 0, v[52:53]
	global_store_dwordx4 v[28:29], v[48:51], off
	s_waitcnt lgkmcnt(0)

; #define LAS __attribute__((address_space(3)))
; __device__ __forceinline__ void tr_item(const float* W, int ld, int K, int nblk, int item, bf16* WT, bool gu, LAS float* scr, int lane) {
;     const int kb = item / nblk, nb = item % nblk, k0 = 64 * kb, n0 = 32 * nb;
;     int drow0 = n0;
;     if (gu) { const int bj = n0 / FF, j = n0 - bj * FF; drow0 = 256 * (j / 128) + 128 * bj + (j % 128); }
;     { float t_[32];
; #pragma unroll
;       for (int i = 0; i < 32; ++i) t_[i] = W[(size_t)(k0 + 2 * i + (lane >> 5)) * ld + n0 + (lane & 31)];
; #pragma unroll
;       for (int i = 0; i < 32; ++i) scr[(2 * i + (lane >> 5)) * 33 + (lane & 31)] = t_[i]; }
; __device__ __forceinline__ void convert_items(Frame& F, const Args& a, int lo, int hi, int w, int nw) {
;     ...
;         if (r < I_FO) { tr_item(a.in[9], D, D, 32, r, (bf16*)(F.ws + WS_WFOXOUT), false, scr, lane); continue; } r -= I_FO;
.LBB0_1353:
	s_andn2_b64 vcc, exec, s[4:5]
	s_cbranch_vccnz .LBB0_1355
	s_add_i32 s0, s12, 0x2a00
	s_and_b32 s5, s0, 0x1ffc0
	s_and_b32 s4, s9, 0x3e0
	v_add_u32_e32 v28, s5, v30
	s_lshl_b32 s0, s4, 2
	v_ashrrev_i32_e32 v29, 31, v28
	v_lshl_add_u64 v[48:49], v[12:13], 0, s[0:1]
	v_lshlrev_b64 v[28:29], 12, v[28:29]
	v_lshl_add_u64 v[28:29], v[48:49], 0, v[28:29]
	v_add_co_u32_e32 v48, vcc, 0x2000, v28
	global_load_dword v50, v[28:29], off nt
	s_nop 0
	v_addc_co_u32_e32 v49, vcc, 0, v29, vcc
	global_load_dword v51, v[48:49], off nt
	v_add_co_u32_e32 v48, vcc, 0x4000, v28
	s_lshl_b32 s0, s5, 1
	s_nop 0
	v_addc_co_u32_e32 v49, vcc, 0, v29, vcc
	global_load_dword v52, v[48:49], off nt
	v_add_co_u32_e32 v48, vcc, 0x6000, v28
	s_nop 1
	v_addc_co_u32_e32 v49, vcc, 0, v29, vcc
	global_load_dword v53, v[48:49], off nt
	v_add_co_u32_e32 v48, vcc, 0x8000, v28
	s_nop 1
	v_addc_co_u32_e32 v49, vcc, 0, v29, vcc
	global_load_dword v54, v[48:49], off nt
	v_add_co_u32_e32 v48, vcc, 0xa000, v28
	s_nop 1
	v_addc_co_u32_e32 v49, vcc, 0, v29, vcc
	global_load_dword v55, v[48:49], off nt
	v_add_co_u32_e32 v48, vcc, 0xc000, v28
	s_nop 1
	v_addc_co_u32_e32 v49, vcc, 0, v29, vcc
	global_load_dword v56, v[48:49], off nt
	v_add_co_u32_e32 v48, vcc, 0xe000, v28
	s_nop 1
	v_addc_co_u32_e32 v49, vcc, 0, v29, vcc
	global_load_dword v57, v[48:49], off nt
	v_add_co_u32_e32 v48, vcc, 0x10000, v28
	s_nop 1
	v_addc_co_u32_e32 v49, vcc, 0, v29, vcc
	global_load_dword v58, v[48:49], off nt
	v_add_co_u32_e32 v48, vcc, 0x12000, v28
	s_nop 1
	v_addc_co_u32_e32 v49, vcc, 0, v29, vcc
	global_load_dword v59, v[48:49], off nt
	v_add_co_u32_e32 v48, vcc, 0x14000, v28
	s_nop 1
	v_addc_co_u32_e32 v49, vcc, 0, v29, vcc
	global_load_dword v60, v[48:49], off nt
	v_add_co_u32_e32 v48, vcc, 0x16000, v28
	s_nop 1
	v_addc_co_u32_e32 v49, vcc, 0, v29, vcc
	global_load_dword v61, v[48:49], off nt
	v_add_co_u32_e32 v48, vcc, 0x18000, v28
	s_nop 1
	v_addc_co_u32_e32 v49, vcc, 0, v29, vcc
	global_load_dword v62, v[48:49], off nt
	v_add_co_u32_e32 v48, vcc, 0x1a000, v28
	s_nop 1
	v_addc_co_u32_e32 v49, vcc, 0, v29, vcc
	global_load_dword v63, v[48:49], off nt
	v_add_co_u32_e32 v48, vcc, 0x1c000, v28
	s_nop 1
	v_addc_co_u32_e32 v49, vcc, 0, v29, vcc
	global_load_dword v64, v[48:49], off nt
	v_add_co_u32_e32 v48, vcc, 0x1e000, v28
	s_nop 1
	v_addc_co_u32_e32 v49, vcc, 0, v29, vcc
	global_load_dword v65, v[48:49], off nt
	v_add_co_u32_e32 v48, vcc, 0x20000, v28
	s_nop 1
	v_addc_co_u32_e32 v49, vcc, 0, v29, vcc
	global_load_dword v66, v[48:49], off nt
	v_add_co_u32_e32 v48, vcc, 0x22000, v28
	s_nop 1
	v_addc_co_u32_e32 v49, vcc, 0, v29, vcc
	global_load_dword v67, v[48:49], off nt
	v_add_co_u32_e32 v48, vcc, 0x24000, v28
	s_nop 1
	v_addc_co_u32_e32 v49, vcc, 0, v29, vcc
	global_load_dword v68, v[48:49], off nt
	v_add_co_u32_e32 v48, vcc, 0x26000, v28
	s_nop 1
	v_addc_co_u32_e32 v49, vcc, 0, v29, vcc
	global_load_dword v69, v[48:49], off nt
	v_add_co_u32_e32 v48, vcc, 0x28000, v28
	s_nop 1
	v_addc_co_u32_e32 v49, vcc, 0, v29, vcc
	global_load_dword v70, v[48:49], off nt
	v_add_co_u32_e32 v48, vcc, 0x2a000, v28
	s_nop 1
	v_addc_co_u32_e32 v49, vcc, 0, v29, vcc
	global_load_dword v71, v[48:49], off nt
	v_add_co_u32_e32 v48, vcc, 0x2c000, v28
	s_nop 1
	v_addc_co_u32_e32 v49, vcc, 0, v29, vcc
	global_load_dword v72, v[48:49], off nt
	v_add_co_u32_e32 v48, vcc, 0x2e000, v28
	s_nop 1
	v_addc_co_u32_e32 v49, vcc, 0, v29, vcc
	global_load_dword v73, v[48:49], off nt
	v_add_co_u32_e32 v48, vcc, 0x30000, v28
	s_nop 1
	v_addc_co_u32_e32 v49, vcc, 0, v29, vcc
	global_load_dword v74, v[48:49], off nt
	v_add_co_u32_e32 v48, vcc, 0x32000, v28
	s_nop 1
	v_addc_co_u32_e32 v49, vcc, 0, v29, vcc
	global_load_dword v75, v[48:49], off nt
	v_add_co_u32_e32 v48, vcc, 0x34000, v28
	s_nop 1
	v_addc_co_u32_e32 v49, vcc, 0, v29, vcc
	global_load_dword v76, v[48:49], off nt
	v_add_co_u32_e32 v48, vcc, 0x36000, v28
	s_nop 1
	v_addc_co_u32_e32 v49, vcc, 0, v29, vcc
	global_load_dword v77, v[48:49], off nt
	v_add_co_u32_e32 v48, vcc, 0x38000, v28
	s_nop 1
	v_addc_co_u32_e32 v49, vcc, 0, v29, vcc
	global_load_dword v78, v[48:49], off nt
	v_add_co_u32_e32 v48, vcc, 0x3a000, v28
	s_nop 1
	v_addc_co_u32_e32 v49, vcc, 0, v29, vcc
	global_load_dword v79, v[48:49], off nt
	v_add_co_u32_e32 v48, vcc, 0x3c000, v28
	s_nop 1
	v_addc_co_u32_e32 v49, vcc, 0, v29, vcc
	v_add_co_u32_e32 v28, vcc, 0x3e000, v28
	global_load_dword v48, v[48:49], off nt
	s_nop 0
	v_addc_co_u32_e32 v29, vcc, 0, v29, vcc
	global_load_dword v28, v[28:29], off nt
	s_waitcnt vmcnt(0)
	ds_write2_b32 v31, v50, v51 offset1:66
	ds_write2_b32 v31, v52, v53 offset0:132 offset1:198
	ds_write2_b32 v40, v54, v55 offset0:8 offset1:74
	ds_write2_b32 v40, v56, v57 offset0:140 offset1:206
	ds_write2_b32 v41, v58, v59 offset0:16 offset1:82
	ds_write2_b32 v41, v60, v61 offset0:148 offset1:214
	ds_write2_b32 v42, v62, v63 offset0:24 offset1:90
	ds_write2_b32 v42, v64, v65 offset0:156 offset1:222
	ds_write2_b32 v43, v66, v67 offset0:32 offset1:98
	ds_write2_b32 v43, v68, v69 offset0:164 offset1:230
	ds_write2_b32 v44, v70, v71 offset0:40 offset1:106
	ds_write2_b32 v44, v72, v73 offset0:172 offset1:238
	ds_write2_b32 v45, v74, v75 offset0:48 offset1:114
	ds_write2_b32 v45, v76, v77 offset0:180 offset1:246
	ds_write2_b32 v46, v78, v79 offset0:56 offset1:122
	ds_write2_b32 v46, v48, v28 offset0:188 offset1:254
	s_waitcnt lgkmcnt(0)
; #define GAS __attribute__((address_space(1)))
; #define LAS __attribute__((address_space(3)))
; #define LDS_WAIT() asm volatile("s_waitcnt lgkmcnt(0)" ::: "memory")
; __device__ __forceinline__ unsigned pk2(float lo, float hi) { return f2bf(lo) | (f2bf(hi) << 16); }
; __device__ __forceinline__ void tr_item(const float* W, int ld, int K, int nblk, int item, bf16* WT, bool gu, LAS float* scr, int lane) {
;     ...
;     LDS_WAIT(); asm volatile("" ::: "memory");
;     const int c = lane & 7;
; #pragma unroll
;     for (int j = 0; j < 4; ++j) { const int n = (lane >> 3) + 8 * j; const LAS float* s = scr + (8 * c) * 33 + n;
;         v4u o; o.x = pk2(s[0 * 33], s[1 * 33]); o.y = pk2(s[2 * 33], s[3 * 33]); o.z = pk2(s[4 * 33], s[5 * 33]); o.w = pk2(s[6 * 33], s[7 * 33]);
;         *(GAS v4u*)(WT + (size_t)(drow0 + n) * K + k0 + 8 * c) = o; }
;     LDS_WAIT(); asm volatile("" ::: "memory");
	ds_read2_b32 v[52:53], v36 offset0:33 offset1:41
	ds_read2_b32 v[54:55], v36 offset1:8
	ds_read2_b32 v[56:57], v36 offset0:66 offset1:74
	ds_read2_b32 v[58:59], v36 offset0:99 offset1:107
	ds_read2_b32 v[60:61], v36 offset0:132 offset1:140
	ds_read2_b32 v[62:63], v36 offset0:165 offset1:173
	ds_read2_b32 v[64:65], v36 offset0:198 offset1:206
	ds_read2_b32 v[66:67], v36 offset0:231 offset1:239
	s_waitcnt lgkmcnt(7)
	v_bfe_u32 v49, v52, 16, 1
	s_waitcnt lgkmcnt(6)
	v_bfe_u32 v48, v54, 16, 1
	v_add3_u32 v48, v54, v48, s15
	v_lshrrev_b32_e32 v48, 16, v48
	v_add3_u32 v49, v52, v49, s15
	v_and_or_b32 v48, v49, s16, v48
	s_waitcnt lgkmcnt(5)
	v_bfe_u32 v49, v56, 16, 1
	v_add3_u32 v49, v56, v49, s15
	s_waitcnt lgkmcnt(4)
	v_bfe_u32 v50, v58, 16, 1
	v_lshrrev_b32_e32 v49, 16, v49
	v_add3_u32 v50, v58, v50, s15
	v_and_or_b32 v49, v50, s16, v49
	s_waitcnt lgkmcnt(3)
	v_bfe_u32 v50, v60, 16, 1
	v_add3_u32 v50, v60, v50, s15
	s_waitcnt lgkmcnt(2)
	v_bfe_u32 v51, v62, 16, 1
	v_lshrrev_b32_e32 v50, 16, v50
	v_add3_u32 v51, v62, v51, s15
	v_and_or_b32 v50, v51, s16, v50
	s_waitcnt lgkmcnt(1)
	v_bfe_u32 v51, v64, 16, 1
	v_add_u32_e32 v68, s4, v35
	v_add3_u32 v51, v64, v51, s15
	s_waitcnt lgkmcnt(0)
	v_bfe_u32 v52, v66, 16, 1
	v_ashrrev_i32_e32 v69, 31, v68
	v_lshl_add_u64 v[28:29], v[24:25], 0, s[0:1]
	v_lshrrev_b32_e32 v51, 16, v51
	v_add3_u32 v52, v66, v52, s15
	v_lshlrev_b64 v[68:69], 11, v[68:69]
	v_and_or_b32 v51, v52, s16, v51
	v_lshl_add_u64 v[68:69], v[28:29], 0, v[68:69]
	global_store_dwordx4 v[68:69], v[48:51], off
	v_bfe_u32 v52, v67, 16, 1
	v_add3_u32 v52, v67, v52, s15
	v_bfe_u32 v48, v55, 16, 1
	v_add3_u32 v48, v55, v48, s15
	v_bfe_u32 v49, v53, 16, 1
	v_lshrrev_b32_e32 v48, 16, v48
	v_add3_u32 v49, v53, v49, s15
	v_and_or_b32 v48, v49, s16, v48
	v_bfe_u32 v49, v57, 16, 1
	v_add3_u32 v49, v57, v49, s15
	v_bfe_u32 v50, v59, 16, 1
	v_lshrrev_b32_e32 v49, 16, v49
	v_add3_u32 v50, v59, v50, s15
	v_and_or_b32 v49, v50, s16, v49
	v_bfe_u32 v50, v61, 16, 1
	v_add3_u32 v50, v61, v50, s15
	v_bfe_u32 v51, v63, 16, 1
	v_lshrrev_b32_e32 v50, 16, v50
	v_add3_u32 v51, v63, v51, s15
	v_and_or_b32 v50, v51, s16, v50
	v_bfe_u32 v51, v65, 16, 1
	v_add3_u32 v51, v65, v51, s15
	v_lshrrev_b32_e32 v51, 16, v51
	v_and_or_b32 v51, v52, s16, v51
	v_add_u32_e32 v52, s4, v37
	v_ashrrev_i32_e32 v53, 31, v52
	v_lshlrev_b64 v[52:53], 11, v[52:53]
	v_lshl_add_u64 v[52:53], v[28:29], 0, v[52:53]
	global_store_dwordx4 v[52:53], v[48:51], off
	ds_read2_b32 v[52:53], v36 offset0:49 offset1:57
	ds_read2_b32 v[54:55], v36 offset0:16 offset1:24
	ds_read2_b32 v[56:57], v36 offset0:82 offset1:90
	ds_read2_b32 v[58:59], v36 offset0:115 offset1:123
	ds_read2_b32 v[60:61], v36 offset0:148 offset1:156
	ds_read2_b32 v[62:63], v36 offset0:181 offset1:189
	ds_read2_b32 v[64:65], v36 offset0:214 offset1:222
	ds_read2_b32 v[66:67], v36 offset0:247 offset1:255
	s_waitcnt lgkmcnt(7)
	v_bfe_u32 v49, v52, 16, 1
	s_waitcnt lgkmcnt(6)
	v_bfe_u32 v48, v54, 16, 1
	v_add3_u32 v48, v54, v48, s15
	v_lshrrev_b32_e32 v48, 16, v48
	v_add3_u32 v49, v52, v49, s15
	v_and_or_b32 v48, v49, s16, v48
	s_waitcnt lgkmcnt(5)
	v_bfe_u32 v49, v56, 16, 1
	v_add3_u32 v49, v56, v49, s15
	s_waitcnt lgkmcnt(4)
	v_bfe_u32 v50, v58, 16, 1
	v_lshrrev_b32_e32 v49, 16, v49
	v_add3_u32 v50, v58, v50, s15
	v_and_or_b32 v49, v50, s16, v49
	s_waitcnt lgkmcnt(3)
	v_bfe_u32 v50, v60, 16, 1
	v_add3_u32 v50, v60, v50, s15
	s_waitcnt lgkmcnt(2)
	v_bfe_u32 v51, v62, 16, 1
	v_lshrrev_b32_e32 v50, 16, v50
	v_add3_u32 v51, v62, v51, s15
	v_and_or_b32 v50, v51, s16, v50
	s_waitcnt lgkmcnt(1)
	v_bfe_u32 v51, v64, 16, 1
	v_add_u32_e32 v68, s4, v38
	v_add3_u32 v51, v64, v51, s15
	s_waitcnt lgkmcnt(0)
	v_bfe_u32 v52, v66, 16, 1
	v_ashrrev_i32_e32 v69, 31, v68
	v_lshrrev_b32_e32 v51, 16, v51
	v_add3_u32 v52, v66, v52, s15
	v_lshlrev_b64 v[68:69], 11, v[68:69]
	v_and_or_b32 v51, v52, s16, v51
	v_lshl_add_u64 v[68:69], v[28:29], 0, v[68:69]
	global_store_dwordx4 v[68:69], v[48:51], off
	v_bfe_u32 v52, v67, 16, 1
	v_add3_u32 v52, v67, v52, s15
	v_bfe_u32 v48, v55, 16, 1
	v_add3_u32 v48, v55, v48, s15
	v_bfe_u32 v49, v53, 16, 1
	v_lshrrev_b32_e32 v48, 16, v48
	v_add3_u32 v49, v53, v49, s15
	v_and_or_b32 v48, v49, s16, v48
	v_bfe_u32 v49, v57, 16, 1
	v_add3_u32 v49, v57, v49, s15
	v_bfe_u32 v50, v59, 16, 1
	v_lshrrev_b32_e32 v49, 16, v49
	v_add3_u32 v50, v59, v50, s15
	v_and_or_b32 v49, v50, s16, v49
	v_bfe_u32 v50, v61, 16, 1
	v_add3_u32 v50, v61, v50, s15
	v_bfe_u32 v51, v63, 16, 1
	v_lshrrev_b32_e32 v50, 16, v50
	v_add3_u32 v51, v63, v51, s15
	v_and_or_b32 v50, v51, s16, v50
	v_bfe_u32 v51, v65, 16, 1
	v_add3_u32 v51, v65, v51, s15
	v_lshrrev_b32_e32 v51, 16, v51
	v_and_or_b32 v51, v52, s16, v51
	v_add_u32_e32 v52, s4, v39
	v_ashrrev_i32_e32 v53, 31, v52
	v_lshlrev_b64 v[52:53], 11, v[52:53]
	v_lshl_add_u64 v[28:29], v[28:29], 0, v[52:53]
	global_store_dwordx4 v[28:29], v[48:51], off
	s_waitcnt lgkmcnt(0)

; #define LAS __attribute__((address_space(3)))
; __device__ __forceinline__ void tr_item(const float* W, int ld, int K, int nblk, int item, bf16* WT, bool gu, LAS float* scr, int lane) {
;     const int kb = item / nblk, nb = item % nblk, k0 = 64 * kb, n0 = 32 * nb;
;     int drow0 = n0;
;     if (gu) { const int bj = n0 / FF, j = n0 - bj * FF; drow0 = 256 * (j / 128) + 128 * bj + (j % 128); }
;     { float t_[32];
; #pragma unroll
;       for (int i = 0; i < 32; ++i) t_[i] = W[(size_t)(k0 + 2 * i + (lane >> 5)) * ld + n0 + (lane & 31)];
; #pragma unroll
;       for (int i = 0; i < 32; ++i) scr[(2 * i + (lane >> 5)) * 33 + (lane & 31)] = t_[i]; }
; __device__ __forceinline__ void convert_items(Frame& F, const Args& a, int lo, int hi, int w, int nw) {
;     ...
;         if (r < I_FI) { tr_item(a.in[7], 3 * D + 16, D, 96, r, (bf16*)(F.ws + WS_WFOXIN), false, scr, lane); continue; } r -= I_FI;
.LBB0_1356:
	s_andn2_b64 vcc, exec, s[4:5]
	s_cbranch_vccnz .LBB0_1329
	s_mul_hi_i32 s0, s8, 0x2aaaaaab
	s_lshr_b32 s4, s0, 31
	s_ashr_i32 s0, s0, 4
	s_add_i32 s0, s0, s4
	s_lshl_b32 s6, s0, 6
	s_mulk_i32 s0, 0xf400
	s_add_i32 s4, s9, s0
	s_ashr_i32 s5, s4, 31
	v_add_u32_e32 v50, s6, v30
	v_lshl_add_u64 v[28:29], s[4:5], 2, v[14:15]
	v_mad_i64_i32 v[48:49], s[40:41], v50, s30, v[28:29]
	global_load_dword v51, v[48:49], off nt
	v_add_u32_e32 v48, 2, v50
	v_mad_i64_i32 v[48:49], s[40:41], v48, s30, v[28:29]
	global_load_dword v52, v[48:49], off nt
	v_add_u32_e32 v48, 4, v50
	v_mad_i64_i32 v[48:49], s[40:41], v48, s30, v[28:29]
	global_load_dword v53, v[48:49], off nt
	v_add_u32_e32 v48, 6, v50
	v_mad_i64_i32 v[48:49], s[40:41], v48, s30, v[28:29]
	global_load_dword v54, v[48:49], off nt
	v_add_u32_e32 v48, 8, v50
	v_mad_i64_i32 v[48:49], s[40:41], v48, s30, v[28:29]
	global_load_dword v55, v[48:49], off nt
	v_add_u32_e32 v48, 10, v50
	v_mad_i64_i32 v[48:49], s[40:41], v48, s30, v[28:29]
	global_load_dword v56, v[48:49], off nt
	v_add_u32_e32 v48, 12, v50
	v_mad_i64_i32 v[48:49], s[40:41], v48, s30, v[28:29]
	global_load_dword v57, v[48:49], off nt
	v_add_u32_e32 v48, 14, v50
	v_mad_i64_i32 v[48:49], s[40:41], v48, s30, v[28:29]
	global_load_dword v58, v[48:49], off nt
	v_add_u32_e32 v48, 16, v50
	v_mad_i64_i32 v[48:49], s[40:41], v48, s30, v[28:29]
	global_load_dword v59, v[48:49], off nt
	v_add_u32_e32 v48, 18, v50
	v_mad_i64_i32 v[48:49], s[40:41], v48, s30, v[28:29]
	global_load_dword v60, v[48:49], off nt
	v_add_u32_e32 v48, 20, v50
	v_mad_i64_i32 v[48:49], s[40:41], v48, s30, v[28:29]
	global_load_dword v61, v[48:49], off nt
	v_add_u32_e32 v48, 22, v50
	v_mad_i64_i32 v[48:49], s[40:41], v48, s30, v[28:29]
	global_load_dword v62, v[48:49], off nt
	v_add_u32_e32 v48, 24, v50
	v_mad_i64_i32 v[48:49], s[40:41], v48, s30, v[28:29]
	global_load_dword v63, v[48:49], off nt
	v_add_u32_e32 v48, 26, v50
	v_mad_i64_i32 v[48:49], s[40:41], v48, s30, v[28:29]
	global_load_dword v64, v[48:49], off nt
	v_add_u32_e32 v48, 28, v50
	v_mad_i64_i32 v[48:49], s[40:41], v48, s30, v[28:29]
	global_load_dword v65, v[48:49], off nt
	v_add_u32_e32 v48, 30, v50
	v_mad_i64_i32 v[48:49], s[40:41], v48, s30, v[28:29]
	global_load_dword v66, v[48:49], off nt
	v_add_u32_e32 v48, 32, v50
	v_mad_i64_i32 v[48:49], s[40:41], v48, s30, v[28:29]
	global_load_dword v67, v[48:49], off nt
	v_add_u32_e32 v48, 34, v50
	v_mad_i64_i32 v[48:49], s[40:41], v48, s30, v[28:29]
	global_load_dword v68, v[48:49], off nt
	v_add_u32_e32 v48, 36, v50
	v_mad_i64_i32 v[48:49], s[40:41], v48, s30, v[28:29]
	global_load_dword v69, v[48:49], off nt
	v_add_u32_e32 v48, 38, v50
	v_mad_i64_i32 v[48:49], s[40:41], v48, s30, v[28:29]
	global_load_dword v70, v[48:49], off nt
	v_add_u32_e32 v48, 40, v50
	v_mad_i64_i32 v[48:49], s[40:41], v48, s30, v[28:29]
	global_load_dword v71, v[48:49], off nt
	v_add_u32_e32 v48, 42, v50
	v_mad_i64_i32 v[48:49], s[40:41], v48, s30, v[28:29]
	global_load_dword v72, v[48:49], off nt
	v_add_u32_e32 v48, 44, v50
	v_mad_i64_i32 v[48:49], s[40:41], v48, s30, v[28:29]
	global_load_dword v73, v[48:49], off nt
	v_add_u32_e32 v48, 46, v50
	v_mad_i64_i32 v[48:49], s[40:41], v48, s30, v[28:29]
	global_load_dword v74, v[48:49], off nt
	v_add_u32_e32 v48, 48, v50
	v_mad_i64_i32 v[48:49], s[40:41], v48, s30, v[28:29]
	global_load_dword v75, v[48:49], off nt
	v_add_u32_e32 v48, 50, v50
	v_mad_i64_i32 v[48:49], s[40:41], v48, s30, v[28:29]
	global_load_dword v76, v[48:49], off nt
	v_add_u32_e32 v48, 52, v50
	v_mad_i64_i32 v[48:49], s[40:41], v48, s30, v[28:29]
	global_load_dword v77, v[48:49], off nt
	v_add_u32_e32 v48, 54, v50
	v_mad_i64_i32 v[48:49], s[40:41], v48, s30, v[28:29]
	global_load_dword v78, v[48:49], off nt
	v_add_u32_e32 v48, 56, v50
	v_mad_i64_i32 v[48:49], s[40:41], v48, s30, v[28:29]
	global_load_dword v79, v[48:49], off nt
	v_add_u32_e32 v48, 58, v50
	v_mad_i64_i32 v[48:49], s[40:41], v48, s30, v[28:29]
	global_load_dword v80, v[48:49], off nt
	v_add_u32_e32 v48, 60, v50
	v_mad_i64_i32 v[48:49], s[40:41], v48, s30, v[28:29]
	global_load_dword v48, v[48:49], off nt
	v_add_u32_e32 v49, 62, v50
	v_mad_i64_i32 v[28:29], s[40:41], v49, s30, v[28:29]
	global_load_dword v28, v[28:29], off nt
	s_waitcnt vmcnt(0)
	ds_write2_b32 v31, v51, v52 offset1:66
	ds_write2_b32 v31, v53, v54 offset0:132 offset1:198
	ds_write2_b32 v40, v55, v56 offset0:8 offset1:74
	ds_write2_b32 v40, v57, v58 offset0:140 offset1:206
	ds_write2_b32 v41, v59, v60 offset0:16 offset1:82
	ds_write2_b32 v41, v61, v62 offset0:148 offset1:214
	ds_write2_b32 v42, v63, v64 offset0:24 offset1:90
	ds_write2_b32 v42, v65, v66 offset0:156 offset1:222
	ds_write2_b32 v43, v67, v68 offset0:32 offset1:98
	ds_write2_b32 v43, v69, v70 offset0:164 offset1:230
	ds_write2_b32 v44, v71, v72 offset0:40 offset1:106
	ds_write2_b32 v44, v73, v74 offset0:172 offset1:238
	ds_write2_b32 v45, v75, v76 offset0:48 offset1:114
	ds_write2_b32 v45, v77, v78 offset0:180 offset1:246
	ds_write2_b32 v46, v79, v80 offset0:56 offset1:122
	ds_write2_b32 v46, v48, v28 offset0:188 offset1:254
	s_waitcnt lgkmcnt(0)
; #define GAS __attribute__((address_space(1)))
; #define LAS __attribute__((address_space(3)))
; #define LDS_WAIT() asm volatile("s_waitcnt lgkmcnt(0)" ::: "memory")
; __device__ __forceinline__ unsigned pk2(float lo, float hi) { return f2bf(lo) | (f2bf(hi) << 16); }
; __device__ __forceinline__ void tr_item(const float* W, int ld, int K, int nblk, int item, bf16* WT, bool gu, LAS float* scr, int lane) {
;     ...
;     LDS_WAIT(); asm volatile("" ::: "memory");
;     const int c = lane & 7;
; #pragma unroll
;     for (int j = 0; j < 4; ++j) { const int n = (lane >> 3) + 8 * j; const LAS float* s = scr + (8 * c) * 33 + n;
;         v4u o; o.x = pk2(s[0 * 33], s[1 * 33]); o.y = pk2(s[2 * 33], s[3 * 33]); o.z = pk2(s[4 * 33], s[5 * 33]); o.w = pk2(s[6 * 33], s[7 * 33]);
;         *(GAS v4u*)(WT + (size_t)(drow0 + n) * K + k0 + 8 * c) = o; }
;     LDS_WAIT(); asm volatile("" ::: "memory");
	ds_read2_b32 v[52:53], v36 offset0:33 offset1:41
	ds_read2_b32 v[54:55], v36 offset1:8
	ds_read2_b32 v[56:57], v36 offset0:66 offset1:74
	ds_read2_b32 v[58:59], v36 offset0:99 offset1:107
	ds_read2_b32 v[60:61], v36 offset0:132 offset1:140
	ds_read2_b32 v[62:63], v36 offset0:165 offset1:173
	ds_read2_b32 v[64:65], v36 offset0:198 offset1:206
	ds_read2_b32 v[66:67], v36 offset0:231 offset1:239
	s_waitcnt lgkmcnt(7)
	v_bfe_u32 v49, v52, 16, 1
	s_waitcnt lgkmcnt(6)
	v_bfe_u32 v48, v54, 16, 1
	v_add3_u32 v48, v54, v48, s15
	v_lshrrev_b32_e32 v48, 16, v48
	v_add3_u32 v49, v52, v49, s15
	v_and_or_b32 v48, v49, s16, v48
	s_waitcnt lgkmcnt(5)
	v_bfe_u32 v49, v56, 16, 1
	v_add3_u32 v49, v56, v49, s15
	s_waitcnt lgkmcnt(4)
	v_bfe_u32 v50, v58, 16, 1
	v_lshrrev_b32_e32 v49, 16, v49
	v_add3_u32 v50, v58, v50, s15
	v_and_or_b32 v49, v50, s16, v49
	s_waitcnt lgkmcnt(3)
	v_bfe_u32 v50, v60, 16, 1
	v_add3_u32 v50, v60, v50, s15
	s_waitcnt lgkmcnt(2)
	v_bfe_u32 v51, v62, 16, 1
	v_lshrrev_b32_e32 v50, 16, v50
	v_add3_u32 v51, v62, v51, s15
	v_and_or_b32 v50, v51, s16, v50
	s_waitcnt lgkmcnt(1)
	v_bfe_u32 v51, v64, 16, 1
	v_add_u32_e32 v68, s4, v35
	s_ashr_i32 s7, s6, 31
	v_add3_u32 v51, v64, v51, s15
	s_waitcnt lgkmcnt(0)
	v_bfe_u32 v52, v66, 16, 1
	v_ashrrev_i32_e32 v69, 31, v68
	v_lshl_add_u64 v[28:29], s[6:7], 1, v[26:27]
	v_lshrrev_b32_e32 v51, 16, v51
	v_add3_u32 v52, v66, v52, s15
	v_lshlrev_b64 v[70:71], 11, v[68:69]
	v_and_or_b32 v51, v52, s16, v51
	v_lshl_add_u64 v[70:71], v[28:29], 0, v[70:71]
	global_store_dwordx4 v[70:71], v[48:51], off
	v_bfe_u32 v52, v67, 16, 1
	v_add3_u32 v52, v67, v52, s15
	v_bfe_u32 v48, v55, 16, 1
	v_add3_u32 v48, v55, v48, s15
	v_bfe_u32 v49, v53, 16, 1
	v_lshrrev_b32_e32 v48, 16, v48
	v_add3_u32 v49, v53, v49, s15
	v_and_or_b32 v48, v49, s16, v48
	v_bfe_u32 v49, v57, 16, 1
	v_add3_u32 v49, v57, v49, s15
	v_bfe_u32 v50, v59, 16, 1
	v_lshrrev_b32_e32 v49, 16, v49
	v_add3_u32 v50, v59, v50, s15
	v_and_or_b32 v49, v50, s16, v49
	v_bfe_u32 v50, v61, 16, 1
	v_add3_u32 v50, v61, v50, s15
	v_bfe_u32 v51, v63, 16, 1
	v_lshrrev_b32_e32 v50, 16, v50
	v_add3_u32 v51, v63, v51, s15
	v_and_or_b32 v50, v51, s16, v50
	v_bfe_u32 v51, v65, 16, 1
	v_add3_u32 v51, v65, v51, s15
	v_lshrrev_b32_e32 v51, 16, v51
	v_and_or_b32 v51, v52, s16, v51
	v_add_u32_e32 v52, 8, v68
	v_ashrrev_i32_e32 v53, 31, v52
	v_lshlrev_b64 v[52:53], 11, v[52:53]
	v_lshl_add_u64 v[52:53], v[28:29], 0, v[52:53]
	global_store_dwordx4 v[52:53], v[48:51], off
	ds_read2_b32 v[52:53], v36 offset0:49 offset1:57
	ds_read2_b32 v[54:55], v36 offset0:16 offset1:24
	ds_read2_b32 v[56:57], v36 offset0:82 offset1:90
	ds_read2_b32 v[58:59], v36 offset0:115 offset1:123
	ds_read2_b32 v[60:61], v36 offset0:148 offset1:156
	ds_read2_b32 v[62:63], v36 offset0:181 offset1:189
	ds_read2_b32 v[64:65], v36 offset0:214 offset1:222
	ds_read2_b32 v[66:67], v36 offset0:247 offset1:255
	s_waitcnt lgkmcnt(7)
	v_bfe_u32 v49, v52, 16, 1
	s_waitcnt lgkmcnt(6)
	v_bfe_u32 v48, v54, 16, 1
	v_add3_u32 v48, v54, v48, s15
	v_lshrrev_b32_e32 v48, 16, v48
	v_add3_u32 v49, v52, v49, s15
	v_and_or_b32 v48, v49, s16, v48
	s_waitcnt lgkmcnt(5)
	v_bfe_u32 v49, v56, 16, 1
	v_add3_u32 v49, v56, v49, s15
	s_waitcnt lgkmcnt(4)
	v_bfe_u32 v50, v58, 16, 1
	v_lshrrev_b32_e32 v49, 16, v49
	v_add3_u32 v50, v58, v50, s15
	v_and_or_b32 v49, v50, s16, v49
	s_waitcnt lgkmcnt(3)
	v_bfe_u32 v50, v60, 16, 1
	v_add3_u32 v50, v60, v50, s15
	s_waitcnt lgkmcnt(2)
	v_bfe_u32 v51, v62, 16, 1
	v_lshrrev_b32_e32 v50, 16, v50
	v_add3_u32 v51, v62, v51, s15
	v_and_or_b32 v50, v51, s16, v50
	s_waitcnt lgkmcnt(1)
	v_bfe_u32 v51, v64, 16, 1
	v_add_u32_e32 v70, 16, v68
	v_add3_u32 v51, v64, v51, s15
	s_waitcnt lgkmcnt(0)
	v_bfe_u32 v52, v66, 16, 1
	v_ashrrev_i32_e32 v71, 31, v70
	v_lshrrev_b32_e32 v51, 16, v51
	v_add3_u32 v52, v66, v52, s15
	v_lshlrev_b64 v[70:71], 11, v[70:71]
	v_and_or_b32 v51, v52, s16, v51
	v_lshl_add_u64 v[70:71], v[28:29], 0, v[70:71]
	global_store_dwordx4 v[70:71], v[48:51], off
	v_bfe_u32 v52, v67, 16, 1
	v_add3_u32 v52, v67, v52, s15
	v_bfe_u32 v48, v55, 16, 1
	v_add3_u32 v48, v55, v48, s15
	v_bfe_u32 v49, v53, 16, 1
	v_lshrrev_b32_e32 v48, 16, v48
	v_add3_u32 v49, v53, v49, s15
	v_and_or_b32 v48, v49, s16, v48
	v_bfe_u32 v49, v57, 16, 1
	v_add3_u32 v49, v57, v49, s15
	v_bfe_u32 v50, v59, 16, 1
	v_lshrrev_b32_e32 v49, 16, v49
	v_add3_u32 v50, v59, v50, s15
	v_and_or_b32 v49, v50, s16, v49
	v_bfe_u32 v50, v61, 16, 1
	v_add3_u32 v50, v61, v50, s15
	v_bfe_u32 v51, v63, 16, 1
	v_lshrrev_b32_e32 v50, 16, v50
	v_add3_u32 v51, v63, v51, s15
	v_and_or_b32 v50, v51, s16, v50
	v_bfe_u32 v51, v65, 16, 1
	v_add3_u32 v51, v65, v51, s15
	v_lshrrev_b32_e32 v51, 16, v51
	v_and_or_b32 v51, v52, s16, v51
	v_add_u32_e32 v52, 24, v68
	v_ashrrev_i32_e32 v53, 31, v52
	v_lshlrev_b64 v[52:53], 11, v[52:53]
	v_lshl_add_u64 v[28:29], v[28:29], 0, v[52:53]
	global_store_dwordx4 v[28:29], v[48:51], off
	s_waitcnt lgkmcnt(0)
	s_branch .LBB0_1329

; __device__ __forceinline__ int pg8_lane_id() { int l; asm volatile("v_mbcnt_lo_u32_b32 %0, -1, 0\n\tv_mbcnt_hi_u32_b32 %0, -1, %0" : "=v"(l)); return l; }
; __device__ __forceinline__ void swa_phase(char* lds, const bf16* Q, const bf16* K2, const bf16* V2, bf16* O, const float* sinks, const float* rel_bias, LAS float* tbl, int v, int G, const int wid) {
;     { const int lane = pg8::pg8_lane_id(), tid = wid * 64 + lane;
;       for (int i = tid; i < 16 * 256; i += NWAVES * 64) { const int hq = i >> 8, k = i & 255; tbl[i] = (k < 255) ? rel_bias[t5_bucket(k - 191) * NH + hq] * LOG2E : 0.f; } }
.LBB0_1362:
	s_or_b64 exec, exec, s[8:9]
	v_cmp_gt_u32_sdwa s[8:9], v0, s12 src0_sel:BYTE_0 src1_sel:DWORD
	v_ashrrev_i32_e32 v3, 8, v0
	v_readlane_b32 s40, v254, 5
	v_cndmask_b32_e64 v4, 0, 16, s[8:9]
	v_add_u32_e32 v2, v2, v4
	v_lshl_add_u32 v2, v2, 4, v3
	v_ashrrev_i32_e32 v3, 31, v2
	v_readlane_b32 s50, v254, 15
	v_readlane_b32 s51, v254, 16
	v_readlane_b32 s41, v254, 6
	v_readlane_b32 s42, v254, 7
	v_lshl_add_u64 v[2:3], v[2:3], 2, s[50:51]
	global_load_dword v2, v[2:3], off nt
	v_readlane_b32 s43, v254, 8
	v_readlane_b32 s44, v254, 9
	v_readlane_b32 s45, v254, 10
	v_readlane_b32 s46, v254, 11
	v_readlane_b32 s47, v254, 12
	v_readlane_b32 s48, v254, 13
	v_readlane_b32 s49, v254, 14
	v_readlane_b32 s52, v254, 17
	v_readlane_b32 s53, v254, 18
	v_readlane_b32 s54, v254, 19
	v_readlane_b32 s55, v254, 20
	s_waitcnt vmcnt(0)
	v_mul_f32_e32 v2, 0x3fb8aa3b, v2

; #define LAS __attribute__((address_space(3)))
; __device__ __forceinline__ void tr_item8(const float* W, int ld, int K, int nblk, int item, unsigned char* WT, bool gu, float scale, LAS float* scr, int lane) {
;     const int kb = item / nblk, nb = item % nblk, k0 = 64 * kb, n0 = 32 * nb;
;     int drow0 = n0;
;     if (gu) { const int bj = n0 / FF, j = n0 - bj * FF; drow0 = 256 * (j / 128) + 128 * bj + (j % 128); }
;     { float t_[32];
; #pragma unroll
;       for (int i = 0; i < 32; ++i) t_[i] = W[(size_t)(k0 + 2 * i + (lane >> 5)) * ld + n0 + (lane & 31)];
; #pragma unroll
;       for (int i = 0; i < 32; ++i) scr[(2 * i + (lane >> 5)) * 33 + (lane & 31)] = t_[i] * scale; }
; __device__ __forceinline__ void convert_items(Frame& F, const Args& a, int lo, int hi, int w, int nw) {
;     ...
;     for (int it = lo + w; it < hi; it += nw) {
;         int r = it;
;         if (r < I_FI) { tr_item(a.in[7], 3 * D + 16, D, 96, r, (bf16*)(F.ws + WS_WFOXIN), false, scr, lane); continue; } r -= I_FI;
;         if (r < I_FO) { tr_item(a.in[9], D, D, 32, r, (bf16*)(F.ws + WS_WFOXOUT), false, scr, lane); continue; } r -= I_FO;
;         if (r < I_SI) { tr_item(a.in[10], D + 512, D, 48, r, (bf16*)(F.ws + WS_WSWAIN), false, scr, lane); continue; } r -= I_SI;
;         if (r < I_SO) { tr_item(a.in[12], D, D, 32, r, (bf16*)(F.ws + WS_WSWAOUT), false, scr, lane); continue; } r -= I_SO;
;         if (r < I_GU) { tr_item8(a.in[14], 2 * FF, D, 224, r, F.ws + WS_WGU, true, WSC_GU, scr, lane); continue; } r -= I_GU;
;         if (r < I_DN) { tr_item8(a.in[15], D, FF, 32, r, F.ws + WS_WDN, false, WSC_DN, scr, lane); continue; } r -= I_DN;
;         if (r < NE * I_GU) { const int e = r / I_GU, rr = r % I_GU; tr_item8(a.in[18] + (size_t)e * D * 2 * FF, 2 * FF, D, 224, rr, F.ws + WS_WMGU + (size_t)e * 2 * FF * D, true, WSC_GU, scr, lane); continue; } r -= NE * I_GU;
;         { const int e = r / I_DN, rr = r % I_DN; tr_item8(a.in[19] + (size_t)e * FF * D, D, FF, 32, rr, F.ws + WS_WMDN + (size_t)e * D * FF, false, WSC_DN, scr, lane); }
.LBB0_1406:
	s_cmpk_gt_i32 s3, 0x5ff
	s_mov_b64 s[4:5], -1
	s_cbranch_scc0 .LBB0_1432
	s_cmpk_gt_u32 s3, 0x7ff
	s_cbranch_scc0 .LBB0_1429
	s_cmpk_gt_u32 s3, 0xaff
	s_cbranch_scc0 .LBB0_1426
	s_cmpk_gt_u32 s3, 0xcff
	s_cbranch_scc0 .LBB0_1423
	s_cmpk_gt_u32 s3, 0x1aff
	s_cbranch_scc0 .LBB0_1420
	s_cmpk_gt_u32 s3, 0x21ff
	s_cbranch_scc0 .LBB0_1417
	s_cmpk_gt_u32 s3, 0x91ff
	s_cbranch_scc0 .LBB0_1414
	s_add_i32 s0, s3, 0x6e00
	s_bfe_u32 s4, s0, 0x80008
	s_mulk_i32 s4, 0x2493
	s_lshr_b32 s4, s4, 16
	s_mul_i32 s5, s4, 0x700
	s_sub_i32 s6, s0, s5
	s_mul_i32 s0, s4, 0xe00000
	s_add_u32 s7, s74, s0
	s_addc_u32 s61, s75, 0
	s_mul_i32 s4, s4, 0x380000
	s_add_u32 s4, s66, s4
	s_addc_u32 s5, s88, 0
	s_lshl_b32 s0, s6, 5
	s_and_b32 s0, s0, 0x3e0
	s_lshl_b32 s6, s6, 1
	s_and_b32 s6, s6, 0xfc0
	s_lshl_b32 s62, s0, 2
	v_add_u32_e32 v46, s6, v28
	s_add_u32 s62, s7, s62
	s_addc_u32 s63, s61, 0
	v_ashrrev_i32_e32 v47, 31, v46
	v_lshl_add_u64 v[48:49], s[62:63], 0, v[0:1]
	v_lshlrev_b64 v[46:47], 12, v[46:47]
	v_lshl_add_u64 v[46:47], v[48:49], 0, v[46:47]
	v_add_co_u32_e32 v48, vcc, s10, v46
	s_add_u32 s4, s4, s6
	s_nop 0
	v_addc_co_u32_e32 v49, vcc, 0, v47, vcc
	v_add_co_u32_e32 v50, vcc, s11, v46
	s_addc_u32 s5, s5, 0
	s_nop 0
	v_addc_co_u32_e32 v51, vcc, 0, v47, vcc
	v_add_co_u32_e32 v52, vcc, s12, v46
	s_nop 1
	v_addc_co_u32_e32 v53, vcc, 0, v47, vcc
	v_add_co_u32_e32 v54, vcc, s13, v46
	s_nop 1
	v_addc_co_u32_e32 v55, vcc, 0, v47, vcc
	v_add_co_u32_e32 v56, vcc, s14, v46
	s_nop 1
	v_addc_co_u32_e32 v57, vcc, 0, v47, vcc
	v_add_co_u32_e32 v58, vcc, s15, v46
	s_nop 1
	v_addc_co_u32_e32 v59, vcc, 0, v47, vcc
	v_add_co_u32_e32 v60, vcc, s16, v46
	s_nop 1
	v_addc_co_u32_e32 v61, vcc, 0, v47, vcc
	global_load_dword v64, v[46:47], off nt
	global_load_dword v65, v[48:49], off nt
	global_load_dword v66, v[50:51], off nt
	global_load_dword v67, v[52:53], off nt
	global_load_dword v68, v[54:55], off nt
	global_load_dword v69, v[56:57], off nt
	global_load_dword v70, v[58:59], off nt
	global_load_dword v71, v[60:61], off nt
	v_add_co_u32_e32 v48, vcc, s17, v46
	s_nop 1
	v_addc_co_u32_e32 v49, vcc, 0, v47, vcc
	v_add_co_u32_e32 v50, vcc, s26, v46
	s_nop 1
	v_addc_co_u32_e32 v51, vcc, 0, v47, vcc
	v_add_co_u32_e32 v52, vcc, s27, v46
	s_nop 1
	v_addc_co_u32_e32 v53, vcc, 0, v47, vcc
	v_add_co_u32_e32 v54, vcc, s30, v46
	s_nop 1
	v_addc_co_u32_e32 v55, vcc, 0, v47, vcc
	v_add_co_u32_e32 v56, vcc, s31, v46
	s_nop 1
	v_addc_co_u32_e32 v57, vcc, 0, v47, vcc
	v_add_co_u32_e32 v58, vcc, s36, v46
	s_nop 1
	v_addc_co_u32_e32 v59, vcc, 0, v47, vcc
	v_add_co_u32_e32 v60, vcc, s37, v46
	s_nop 1
	v_addc_co_u32_e32 v61, vcc, 0, v47, vcc
	v_add_co_u32_e32 v62, vcc, s38, v46
	s_nop 1
	v_addc_co_u32_e32 v63, vcc, 0, v47, vcc
	global_load_dword v72, v[48:49], off nt
	global_load_dword v73, v[50:51], off nt
	global_load_dword v74, v[52:53], off nt
	global_load_dword v75, v[54:55], off nt
	global_load_dword v76, v[56:57], off nt
	global_load_dword v77, v[58:59], off nt
	global_load_dword v78, v[60:61], off nt
	global_load_dword v79, v[62:63], off nt
	v_add_co_u32_e32 v48, vcc, s39, v46
	s_nop 1
	v_addc_co_u32_e32 v49, vcc, 0, v47, vcc
	v_add_co_u32_e32 v50, vcc, s40, v46
	s_nop 1
	v_addc_co_u32_e32 v51, vcc, 0, v47, vcc
	v_add_co_u32_e32 v52, vcc, s41, v46
	s_nop 1
	v_addc_co_u32_e32 v53, vcc, 0, v47, vcc
	v_add_co_u32_e32 v54, vcc, s42, v46
	s_nop 1
	v_addc_co_u32_e32 v55, vcc, 0, v47, vcc
	v_add_co_u32_e32 v56, vcc, s43, v46
	s_nop 1
	v_addc_co_u32_e32 v57, vcc, 0, v47, vcc
	v_add_co_u32_e32 v58, vcc, s44, v46
	s_nop 1
	v_addc_co_u32_e32 v59, vcc, 0, v47, vcc
	v_add_co_u32_e32 v60, vcc, s45, v46
	s_nop 1
	v_addc_co_u32_e32 v61, vcc, 0, v47, vcc
	v_add_co_u32_e32 v62, vcc, s46, v46
	s_nop 1
	v_addc_co_u32_e32 v63, vcc, 0, v47, vcc
	global_load_dword v80, v[48:49], off nt
	global_load_dword v81, v[50:51], off nt
	global_load_dword v82, v[52:53], off nt
	global_load_dword v83, v[54:55], off nt
	global_load_dword v84, v[56:57], off nt
	global_load_dword v85, v[58:59], off nt
	s_nop 0
	global_load_dword v60, v[60:61], off nt
	s_nop 0
	global_load_dword v61, v[62:63], off nt
	v_add_co_u32_e32 v48, vcc, s47, v46
	s_nop 1
	v_addc_co_u32_e32 v49, vcc, 0, v47, vcc
	v_add_co_u32_e32 v50, vcc, s48, v46
	s_nop 1
	v_addc_co_u32_e32 v51, vcc, 0, v47, vcc
	v_add_co_u32_e32 v52, vcc, s49, v46
	s_nop 1
	v_addc_co_u32_e32 v53, vcc, 0, v47, vcc
	v_add_co_u32_e32 v54, vcc, s50, v46
	s_nop 1
	v_addc_co_u32_e32 v55, vcc, 0, v47, vcc
	v_add_co_u32_e32 v56, vcc, s51, v46
	s_nop 1
	v_addc_co_u32_e32 v57, vcc, 0, v47, vcc
	v_add_co_u32_e32 v58, vcc, s52, v46
	s_nop 1
	v_addc_co_u32_e32 v59, vcc, 0, v47, vcc
	global_load_dword v62, v[48:49], off nt
	s_nop 0
	global_load_dword v50, v[50:51], off nt
	s_nop 0
	global_load_dword v51, v[52:53], off nt
	s_nop 0
	global_load_dword v52, v[54:55], off nt
	global_load_dword v53, v[56:57], off nt
	s_nop 0
	global_load_dword v54, v[58:59], off nt
	v_add_co_u32_e32 v48, vcc, s53, v46
	s_nop 1
	v_addc_co_u32_e32 v49, vcc, 0, v47, vcc
	v_add_co_u32_e32 v46, vcc, s54, v46
	s_nop 1
	v_addc_co_u32_e32 v47, vcc, 0, v47, vcc
	global_load_dword v48, v[48:49], off nt
	s_nop 0
	global_load_dword v46, v[46:47], off nt
	s_waitcnt vmcnt(31)
	v_mul_f32_e32 v47, 0x43000000, v64
	s_waitcnt vmcnt(30)
	v_mul_f32_e32 v49, 0x43000000, v65
	ds_write2_b32 v29, v47, v49 offset1:66
	s_waitcnt vmcnt(29)
	v_mul_f32_e32 v47, 0x43000000, v66
	s_waitcnt vmcnt(28)
	v_mul_f32_e32 v49, 0x43000000, v67
	ds_write2_b32 v29, v47, v49 offset0:132 offset1:198
	s_waitcnt vmcnt(27)
	v_mul_f32_e32 v47, 0x43000000, v68
	s_waitcnt vmcnt(26)
	v_mul_f32_e32 v49, 0x43000000, v69
	ds_write2_b32 v38, v47, v49 offset0:8 offset1:74
	s_waitcnt vmcnt(25)
; __device__ __forceinline__ unsigned cvt_pk4_fp8(float a, float b, float c, float d) { int w = 0; w = __builtin_amdgcn_cvt_pk_fp8_f32(a, b, w, false); w = __builtin_amdgcn_cvt_pk_fp8_f32(c, d, w, true); return (unsigned)w; }
; #define GAS __attribute__((address_space(1)))
; #define LAS __attribute__((address_space(3)))
; #define LDS_WAIT() asm volatile("s_waitcnt lgkmcnt(0)" ::: "memory")
; __device__ __forceinline__ void tr_item8(const float* W, int ld, int K, int nblk, int item, unsigned char* WT, bool gu, float scale, LAS float* scr, int lane) {
;     ...
; #pragma unroll
;       for (int i = 0; i < 32; ++i) scr[(2 * i + (lane >> 5)) * 33 + (lane & 31)] = t_[i] * scale; }
;     LDS_WAIT(); asm volatile("" ::: "memory");
;     const int c = lane & 3;
; #pragma unroll
;     for (int j = 0; j < 2; ++j) { const int n = (lane >> 2) + 16 * j; const LAS float* sp = scr + (16 * c) * 33 + n;
;         v4u o; o.x = pg8::cvt_pk4_fp8(sp[0 * 33], sp[1 * 33], sp[2 * 33], sp[3 * 33]); o.y = pg8::cvt_pk4_fp8(sp[4 * 33], sp[5 * 33], sp[6 * 33], sp[7 * 33]);
;         o.z = pg8::cvt_pk4_fp8(sp[8 * 33], sp[9 * 33], sp[10 * 33], sp[11 * 33]); o.w = pg8::cvt_pk4_fp8(sp[12 * 33], sp[13 * 33], sp[14 * 33], sp[15 * 33]);
;         *(GAS v4u*)(WT + (size_t)(drow0 + n) * K + k0 + 16 * c) = o; }
;     LDS_WAIT(); asm volatile("" ::: "memory");
	v_mul_f32_e32 v47, 0x43000000, v70
	s_waitcnt vmcnt(24)
	v_mul_f32_e32 v49, 0x43000000, v71
	ds_write2_b32 v38, v47, v49 offset0:140 offset1:206
	s_waitcnt vmcnt(23)
	v_mul_f32_e32 v47, 0x43000000, v72
	s_waitcnt vmcnt(22)
	v_mul_f32_e32 v49, 0x43000000, v73
	ds_write2_b32 v39, v47, v49 offset0:16 offset1:82
	s_waitcnt vmcnt(21)
	v_mul_f32_e32 v47, 0x43000000, v74
	s_waitcnt vmcnt(20)
	v_mul_f32_e32 v49, 0x43000000, v75
	ds_write2_b32 v39, v47, v49 offset0:148 offset1:214
	s_waitcnt vmcnt(19)
	v_mul_f32_e32 v47, 0x43000000, v76
	s_waitcnt vmcnt(18)
	v_mul_f32_e32 v49, 0x43000000, v77
	ds_write2_b32 v40, v47, v49 offset0:24 offset1:90
	s_waitcnt vmcnt(17)
	v_mul_f32_e32 v47, 0x43000000, v78
	s_waitcnt vmcnt(16)
	v_mul_f32_e32 v49, 0x43000000, v79
	ds_write2_b32 v40, v47, v49 offset0:156 offset1:222
	s_waitcnt vmcnt(15)
	v_mul_f32_e32 v47, 0x43000000, v80
	s_waitcnt vmcnt(14)
	v_mul_f32_e32 v49, 0x43000000, v81
	ds_write2_b32 v41, v47, v49 offset0:32 offset1:98
	s_waitcnt vmcnt(13)
	v_mul_f32_e32 v47, 0x43000000, v82
	s_waitcnt vmcnt(12)
	v_mul_f32_e32 v49, 0x43000000, v83
	ds_write2_b32 v41, v47, v49 offset0:164 offset1:230
	s_waitcnt vmcnt(11)
	v_mul_f32_e32 v47, 0x43000000, v84
	s_waitcnt vmcnt(10)
	v_mul_f32_e32 v49, 0x43000000, v85
	ds_write2_b32 v42, v47, v49 offset0:40 offset1:106
	s_waitcnt vmcnt(9)
	v_mul_f32_e32 v47, 0x43000000, v60
	s_waitcnt vmcnt(8)
	v_mul_f32_e32 v49, 0x43000000, v61
	ds_write2_b32 v42, v47, v49 offset0:172 offset1:238
	s_waitcnt vmcnt(7)
	v_mul_f32_e32 v47, 0x43000000, v62
	s_waitcnt vmcnt(6)
	v_mul_f32_e32 v49, 0x43000000, v50
	ds_write2_b32 v43, v47, v49 offset0:48 offset1:114
	s_waitcnt vmcnt(5)
	v_mul_f32_e32 v47, 0x43000000, v51
	s_waitcnt vmcnt(4)
	v_mul_f32_e32 v49, 0x43000000, v52
	ds_write2_b32 v43, v47, v49 offset0:180 offset1:246
	s_waitcnt vmcnt(3)
	v_mul_f32_e32 v47, 0x43000000, v53
	s_waitcnt vmcnt(2)
	v_mul_f32_e32 v49, 0x43000000, v54
	ds_write2_b32 v44, v47, v49 offset0:56 offset1:122
	v_mov_b32_e32 v49, v1
	v_lshl_add_u64 v[50:51], s[4:5], 0, v[2:3]
	s_waitcnt vmcnt(1)
	v_mul_f32_e32 v47, 0x43000000, v48
	s_waitcnt vmcnt(0)
	v_mul_f32_e32 v46, 0x43000000, v46
	ds_write2_b32 v44, v47, v46 offset0:188 offset1:254
	s_waitcnt lgkmcnt(0)
	ds_read2_b32 v[52:53], v31 offset1:16
	ds_read2_b32 v[54:55], v31 offset0:33 offset1:49
	ds_read2_b32 v[56:57], v31 offset0:66 offset1:82
	ds_read2_b32 v[58:59], v31 offset0:99 offset1:115
	ds_read2_b32 v[60:61], v31 offset0:132 offset1:148
	ds_read2_b32 v[62:63], v31 offset0:165 offset1:181
	ds_read2_b32 v[64:65], v31 offset0:198 offset1:214
	ds_read2_b32 v[66:67], v31 offset0:231 offset1:247
	ds_read2_b32 v[68:69], v45 offset0:8 offset1:24
	ds_read2_b32 v[70:71], v45 offset0:41 offset1:57
	ds_read2_b32 v[72:73], v45 offset0:74 offset1:90
	ds_read2_b32 v[74:75], v45 offset0:107 offset1:123
	ds_read2_b32 v[76:77], v45 offset0:140 offset1:156
	ds_read2_b32 v[78:79], v45 offset0:173 offset1:189
	v_mov_b32_e32 v46, v1
	v_mov_b32_e32 v47, v1
	v_mov_b32_e32 v48, v1
	ds_read2_b32 v[80:81], v45 offset0:206 offset1:222
	ds_read2_b32 v[82:83], v45 offset0:239 offset1:255
	s_waitcnt lgkmcnt(14)
	v_cvt_pk_fp8_f32 v46, v52, v54
	s_waitcnt lgkmcnt(10)
	v_cvt_pk_fp8_f32 v47, v60, v62
	s_waitcnt lgkmcnt(6)
	v_cvt_pk_fp8_f32 v48, v68, v70
	s_waitcnt lgkmcnt(2)
	v_cvt_pk_fp8_f32 v49, v76, v78
	v_cvt_pk_fp8_f32 v46, v56, v58 op_sel:[0,0,1]
	v_cvt_pk_fp8_f32 v47, v64, v66 op_sel:[0,0,1]
	v_cvt_pk_fp8_f32 v48, v72, v74 op_sel:[0,0,1]
	s_waitcnt lgkmcnt(0)
	v_cvt_pk_fp8_f32 v49, v80, v82 op_sel:[0,0,1]
	v_add_u32_e32 v52, s0, v30
	v_mad_i64_i32 v[84:85], s[4:5], v52, s55, v[50:51]
	global_store_dwordx4 v[84:85], v[46:49], off
	v_add_u32_e32 v52, s0, v32
	v_mad_i64_i32 v[50:51], s[4:5], v52, s55, v[50:51]
	v_mov_b32_e32 v46, v1
	v_mov_b32_e32 v47, v1
	v_mov_b32_e32 v48, v1
	v_mov_b32_e32 v49, v1
	v_cvt_pk_fp8_f32 v46, v53, v55
	v_cvt_pk_fp8_f32 v47, v61, v63
	v_cvt_pk_fp8_f32 v48, v69, v71
	v_cvt_pk_fp8_f32 v49, v77, v79
	v_cvt_pk_fp8_f32 v46, v57, v59 op_sel:[0,0,1]
	v_cvt_pk_fp8_f32 v47, v65, v67 op_sel:[0,0,1]
	v_cvt_pk_fp8_f32 v48, v73, v75 op_sel:[0,0,1]
	v_cvt_pk_fp8_f32 v49, v81, v83 op_sel:[0,0,1]
	s_mov_b64 s[4:5], 0
	global_store_dwordx4 v[50:51], v[46:49], off
	s_waitcnt lgkmcnt(0)
.LBB0_1414:
	s_andn2_b64 vcc, exec, s[4:5]
	s_cbranch_vccnz .LBB0_1416
; #define LAS __attribute__((address_space(3)))
; __device__ __forceinline__ void tr_item8(const float* W, int ld, int K, int nblk, int item, unsigned char* WT, bool gu, float scale, LAS float* scr, int lane) {
;     const int kb = item / nblk, nb = item % nblk, k0 = 64 * kb, n0 = 32 * nb;
;     int drow0 = n0;
;     if (gu) { const int bj = n0 / FF, j = n0 - bj * FF; drow0 = 256 * (j / 128) + 128 * bj + (j % 128); }
;     { float t_[32];
; #pragma unroll
;       for (int i = 0; i < 32; ++i) t_[i] = W[(size_t)(k0 + 2 * i + (lane >> 5)) * ld + n0 + (lane & 31)];
; #pragma unroll
;       for (int i = 0; i < 32; ++i) scr[(2 * i + (lane >> 5)) * 33 + (lane & 31)] = t_[i] * scale; }
; __device__ __forceinline__ void convert_items(Frame& F, const Args& a, int lo, int hi, int w, int nw) {
;     ...
;     for (int it = lo + w; it < hi; it += nw) {
;         int r = it;
;         if (r < I_FI) { tr_item(a.in[7], 3 * D + 16, D, 96, r, (bf16*)(F.ws + WS_WFOXIN), false, scr, lane); continue; } r -= I_FI;
;         if (r < I_FO) { tr_item(a.in[9], D, D, 32, r, (bf16*)(F.ws + WS_WFOXOUT), false, scr, lane); continue; } r -= I_FO;
;         if (r < I_SI) { tr_item(a.in[10], D + 512, D, 48, r, (bf16*)(F.ws + WS_WSWAIN), false, scr, lane); continue; } r -= I_SI;
;         if (r < I_SO) { tr_item(a.in[12], D, D, 32, r, (bf16*)(F.ws + WS_WSWAOUT), false, scr, lane); continue; } r -= I_SO;
;         if (r < I_GU) { tr_item8(a.in[14], 2 * FF, D, 224, r, F.ws + WS_WGU, true, WSC_GU, scr, lane); continue; } r -= I_GU;
;         if (r < I_DN) { tr_item8(a.in[15], D, FF, 32, r, F.ws + WS_WDN, false, WSC_DN, scr, lane); continue; } r -= I_DN;
;         if (r < NE * I_GU) { const int e = r / I_GU, rr = r % I_GU; tr_item8(a.in[18] + (size_t)e * D * 2 * FF, 2 * FF, D, 224, rr, F.ws + WS_WMGU + (size_t)e * 2 * FF * D, true, WSC_GU, scr, lane); continue; } r -= NE * I_GU;
	s_add_i32 s0, s3, 0xde00
	s_bfe_u32 s4, s0, 0x70009
	s_mulk_i32 s4, 0x2493
	s_lshr_b32 s4, s4, 16
	s_mul_i32 s5, s4, 0xe00
	s_sub_i32 s0, s0, s5
	s_mul_i32 s5, s4, 0x1c00000
	s_add_u32 s6, s72, s5
	s_addc_u32 s7, s73, 0
	s_mul_i32 s4, s4, 0x700000
	s_add_u32 s4, s89, s4
	s_addc_u32 s5, s90, 0
	s_bfe_u32 s61, s0, 0xb0005
	s_mulk_i32 s61, 0x2493
	s_lshr_b32 s61, s61, 16
	s_mul_i32 s62, s61, 0xe0
	s_sub_i32 s62, s0, s62
	s_lshl_b32 s0, s62, 5
	s_and_b32 s63, s62, 0xffff
	s_cmpk_gt_u32 s63, 0x6f
	s_cselect_b32 s63, 0xfffff200, 0
	s_cselect_b32 s64, 0x80, 0
	s_add_i32 s0, s63, s0
	s_sext_i32_i16 s63, s0
	s_bfe_u32 s63, s63, 0x70018
	s_add_i32 s63, s0, s63
	s_sext_i32_i16 s65, s63
	s_and_b32 s63, s63, 0xff80
	s_sub_i32 s0, s0, s63
	s_lshl_b32 s65, s65, 1
	s_sext_i32_i16 s0, s0
	s_and_b32 s65, s65, 0xffffff00
	s_add_i32 s0, s64, s0
	s_lshl_b32 s62, s62, 7
	s_add_i32 s0, s0, s65
	s_lshl_b32 s61, s61, 6
	s_and_b32 s62, s62, 0x3ff80
	s_add_u32 s6, s6, s62
	s_addc_u32 s7, s7, 0
	v_add_u32_e32 v64, s61, v28
	v_lshl_add_u64 v[46:47], s[6:7], 0, v[0:1]
	v_mad_i64_i32 v[48:49], s[6:7], v64, s56, v[46:47]
	v_add_u32_e32 v50, 2, v64
	v_add_u32_e32 v52, 4, v64
	v_add_u32_e32 v54, 6, v64
	v_add_u32_e32 v56, 8, v64
	v_add_u32_e32 v58, 10, v64
	v_add_u32_e32 v60, 12, v64
	v_add_u32_e32 v62, 14, v64
	v_mad_i64_i32 v[50:51], s[6:7], v50, s56, v[46:47]
	v_mad_i64_i32 v[52:53], s[6:7], v52, s56, v[46:47]
	v_mad_i64_i32 v[54:55], s[6:7], v54, s56, v[46:47]
	v_mad_i64_i32 v[56:57], s[6:7], v56, s56, v[46:47]
	v_mad_i64_i32 v[58:59], s[6:7], v58, s56, v[46:47]
	v_mad_i64_i32 v[60:61], s[6:7], v60, s56, v[46:47]
	v_mad_i64_i32 v[62:63], s[6:7], v62, s56, v[46:47]
	global_load_dword v65, v[48:49], off nt
	global_load_dword v66, v[50:51], off nt
	global_load_dword v67, v[52:53], off nt
	global_load_dword v68, v[54:55], off nt
	global_load_dword v69, v[56:57], off nt
	global_load_dword v70, v[58:59], off nt
	global_load_dword v71, v[60:61], off nt
	global_load_dword v72, v[62:63], off nt
	v_add_u32_e32 v48, 16, v64
	v_mad_i64_i32 v[48:49], s[6:7], v48, s56, v[46:47]
	v_add_u32_e32 v50, 18, v64
	v_add_u32_e32 v52, 20, v64
	v_add_u32_e32 v54, 22, v64
	v_add_u32_e32 v56, 24, v64
	v_add_u32_e32 v58, 26, v64
	v_add_u32_e32 v60, 28, v64
	v_add_u32_e32 v62, 30, v64
	v_mad_i64_i32 v[50:51], s[6:7], v50, s56, v[46:47]
	v_mad_i64_i32 v[52:53], s[6:7], v52, s56, v[46:47]
	v_mad_i64_i32 v[54:55], s[6:7], v54, s56, v[46:47]
	v_mad_i64_i32 v[56:57], s[6:7], v56, s56, v[46:47]
	v_mad_i64_i32 v[58:59], s[6:7], v58, s56, v[46:47]
	v_mad_i64_i32 v[60:61], s[6:7], v60, s56, v[46:47]
	v_mad_i64_i32 v[62:63], s[6:7], v62, s56, v[46:47]
	global_load_dword v73, v[48:49], off nt
	global_load_dword v74, v[50:51], off nt
	global_load_dword v75, v[52:53], off nt
	global_load_dword v76, v[54:55], off nt
	global_load_dword v77, v[56:57], off nt
	global_load_dword v78, v[58:59], off nt
	global_load_dword v79, v[60:61], off nt
	global_load_dword v80, v[62:63], off nt
	v_add_u32_e32 v48, 32, v64
	v_add_u32_e32 v50, 34, v64
	v_add_u32_e32 v52, 36, v64
	v_add_u32_e32 v54, 38, v64
	v_add_u32_e32 v60, 44, v64
	v_mad_i64_i32 v[48:49], s[6:7], v48, s56, v[46:47]
	v_mad_i64_i32 v[50:51], s[6:7], v50, s56, v[46:47]
	v_mad_i64_i32 v[52:53], s[6:7], v52, s56, v[46:47]
	v_mad_i64_i32 v[54:55], s[6:7], v54, s56, v[46:47]
	v_add_u32_e32 v56, 40, v64
	v_add_u32_e32 v58, 42, v64
	v_mad_i64_i32 v[60:61], s[6:7], v60, s56, v[46:47]
	v_add_u32_e32 v62, 46, v64
	v_mad_i64_i32 v[56:57], s[6:7], v56, s56, v[46:47]
	v_mad_i64_i32 v[58:59], s[6:7], v58, s56, v[46:47]
	v_mad_i64_i32 v[62:63], s[6:7], v62, s56, v[46:47]
	global_load_dword v81, v[48:49], off nt
	global_load_dword v82, v[50:51], off nt
	global_load_dword v83, v[52:53], off nt
	global_load_dword v84, v[54:55], off nt
	global_load_dword v85, v[56:57], off nt
	global_load_dword v86, v[58:59], off nt
	s_nop 0
	global_load_dword v60, v[60:61], off nt
	s_nop 0
	global_load_dword v61, v[62:63], off nt
	v_add_u32_e32 v48, 48, v64
	v_add_u32_e32 v50, 50, v64
	v_add_u32_e32 v52, 52, v64
	v_add_u32_e32 v54, 54, v64
	v_mad_i64_i32 v[48:49], s[6:7], v48, s56, v[46:47]
	v_mad_i64_i32 v[50:51], s[6:7], v50, s56, v[46:47]
	v_mad_i64_i32 v[52:53], s[6:7], v52, s56, v[46:47]
	v_mad_i64_i32 v[54:55], s[6:7], v54, s56, v[46:47]
	v_add_u32_e32 v56, 56, v64
	v_add_u32_e32 v58, 58, v64
	v_mad_i64_i32 v[56:57], s[6:7], v56, s56, v[46:47]
	v_mad_i64_i32 v[58:59], s[6:7], v58, s56, v[46:47]
	global_load_dword v62, v[48:49], off nt
	s_nop 0
	global_load_dword v50, v[50:51], off nt
	s_nop 0
	global_load_dword v51, v[52:53], off nt
	s_nop 0
	global_load_dword v52, v[54:55], off nt
	global_load_dword v53, v[56:57], off nt
	s_nop 0
	global_load_dword v54, v[58:59], off nt
	v_add_u32_e32 v48, 60, v64
	v_add_u32_e32 v55, 62, v64
	v_mad_i64_i32 v[48:49], s[6:7], v48, s56, v[46:47]
	v_mad_i64_i32 v[46:47], s[6:7], v55, s56, v[46:47]
	global_load_dword v48, v[48:49], off nt
	s_nop 0
	global_load_dword v46, v[46:47], off nt
	s_waitcnt vmcnt(31)
; __device__ __forceinline__ unsigned cvt_pk4_fp8(float a, float b, float c, float d) { int w = 0; w = __builtin_amdgcn_cvt_pk_fp8_f32(a, b, w, false); w = __builtin_amdgcn_cvt_pk_fp8_f32(c, d, w, true); return (unsigned)w; }
; #define GAS __attribute__((address_space(1)))
; #define LAS __attribute__((address_space(3)))
; #define LDS_WAIT() asm volatile("s_waitcnt lgkmcnt(0)" ::: "memory")
; __device__ __forceinline__ void tr_item8(const float* W, int ld, int K, int nblk, int item, unsigned char* WT, bool gu, float scale, LAS float* scr, int lane) {
;     ...
; #pragma unroll
;       for (int i = 0; i < 32; ++i) scr[(2 * i + (lane >> 5)) * 33 + (lane & 31)] = t_[i] * scale; }
;     LDS_WAIT(); asm volatile("" ::: "memory");
;     const int c = lane & 3;
; #pragma unroll
;     for (int j = 0; j < 2; ++j) { const int n = (lane >> 2) + 16 * j; const LAS float* sp = scr + (16 * c) * 33 + n;
;         v4u o; o.x = pg8::cvt_pk4_fp8(sp[0 * 33], sp[1 * 33], sp[2 * 33], sp[3 * 33]); o.y = pg8::cvt_pk4_fp8(sp[4 * 33], sp[5 * 33], sp[6 * 33], sp[7 * 33]);
;         o.z = pg8::cvt_pk4_fp8(sp[8 * 33], sp[9 * 33], sp[10 * 33], sp[11 * 33]); o.w = pg8::cvt_pk4_fp8(sp[12 * 33], sp[13 * 33], sp[14 * 33], sp[15 * 33]);
;         *(GAS v4u*)(WT + (size_t)(drow0 + n) * K + k0 + 16 * c) = o; }
;     LDS_WAIT(); asm volatile("" ::: "memory");
	v_mul_f32_e32 v47, 0x42800000, v65
	s_waitcnt vmcnt(30)
	v_mul_f32_e32 v49, 0x42800000, v66
	ds_write2_b32 v29, v47, v49 offset1:66
	s_waitcnt vmcnt(29)
	v_mul_f32_e32 v47, 0x42800000, v67
	s_waitcnt vmcnt(28)
	v_mul_f32_e32 v49, 0x42800000, v68
	ds_write2_b32 v29, v47, v49 offset0:132 offset1:198
	s_waitcnt vmcnt(27)
	v_mul_f32_e32 v47, 0x42800000, v69
	s_waitcnt vmcnt(26)
	v_mul_f32_e32 v49, 0x42800000, v70
	ds_write2_b32 v38, v47, v49 offset0:8 offset1:74
	s_waitcnt vmcnt(25)
	v_mul_f32_e32 v47, 0x42800000, v71
	s_waitcnt vmcnt(24)
	v_mul_f32_e32 v49, 0x42800000, v72
	ds_write2_b32 v38, v47, v49 offset0:140 offset1:206
	s_add_u32 s4, s4, s61
	s_addc_u32 s5, s5, 0
	s_waitcnt vmcnt(23)
	v_mul_f32_e32 v47, 0x42800000, v73
	s_waitcnt vmcnt(22)
	v_mul_f32_e32 v49, 0x42800000, v74
	ds_write2_b32 v39, v47, v49 offset0:16 offset1:82
	s_waitcnt vmcnt(21)
	v_mul_f32_e32 v47, 0x42800000, v75
	s_waitcnt vmcnt(20)
	v_mul_f32_e32 v49, 0x42800000, v76
	ds_write2_b32 v39, v47, v49 offset0:148 offset1:214
	s_waitcnt vmcnt(19)
	v_mul_f32_e32 v47, 0x42800000, v77
	s_waitcnt vmcnt(18)
	v_mul_f32_e32 v49, 0x42800000, v78
	ds_write2_b32 v40, v47, v49 offset0:24 offset1:90
	s_waitcnt vmcnt(17)
	v_mul_f32_e32 v47, 0x42800000, v79
	s_waitcnt vmcnt(16)
	v_mul_f32_e32 v49, 0x42800000, v80
	ds_write2_b32 v40, v47, v49 offset0:156 offset1:222
	s_waitcnt vmcnt(15)
	v_mul_f32_e32 v47, 0x42800000, v81
	s_waitcnt vmcnt(14)
	v_mul_f32_e32 v49, 0x42800000, v82
	ds_write2_b32 v41, v47, v49 offset0:32 offset1:98
	s_waitcnt vmcnt(13)
	v_mul_f32_e32 v47, 0x42800000, v83
	s_waitcnt vmcnt(12)
	v_mul_f32_e32 v49, 0x42800000, v84
	ds_write2_b32 v41, v47, v49 offset0:164 offset1:230
	s_waitcnt vmcnt(11)
	v_mul_f32_e32 v47, 0x42800000, v85
	s_waitcnt vmcnt(10)
	v_mul_f32_e32 v49, 0x42800000, v86
	ds_write2_b32 v42, v47, v49 offset0:40 offset1:106
	s_waitcnt vmcnt(9)
	v_mul_f32_e32 v47, 0x42800000, v60
	s_waitcnt vmcnt(8)
	v_mul_f32_e32 v49, 0x42800000, v61
	ds_write2_b32 v42, v47, v49 offset0:172 offset1:238
	v_add_u32_e32 v84, s0, v30
	v_ashrrev_i32_e32 v85, 31, v84
	v_lshlrev_b64 v[84:85], 10, v[84:85]
	s_waitcnt vmcnt(7)
	v_mul_f32_e32 v47, 0x42800000, v62
	s_waitcnt vmcnt(6)
	v_mul_f32_e32 v49, 0x42800000, v50
	ds_write2_b32 v43, v47, v49 offset0:48 offset1:114
	s_waitcnt vmcnt(5)
	v_mul_f32_e32 v47, 0x42800000, v51
	s_waitcnt vmcnt(4)
	v_mul_f32_e32 v49, 0x42800000, v52
	ds_write2_b32 v43, v47, v49 offset0:180 offset1:246
	s_waitcnt vmcnt(3)
	v_mul_f32_e32 v47, 0x42800000, v53
	s_waitcnt vmcnt(2)
	v_mul_f32_e32 v49, 0x42800000, v54
	ds_write2_b32 v44, v47, v49 offset0:56 offset1:122
	v_mov_b32_e32 v49, v1
	v_lshl_add_u64 v[50:51], s[4:5], 0, v[2:3]
	s_waitcnt vmcnt(1)
	v_mul_f32_e32 v47, 0x42800000, v48
	s_waitcnt vmcnt(0)
	v_mul_f32_e32 v46, 0x42800000, v46
	ds_write2_b32 v44, v47, v46 offset0:188 offset1:254
	s_waitcnt lgkmcnt(0)
	ds_read2_b32 v[52:53], v31 offset1:16
	ds_read2_b32 v[54:55], v31 offset0:33 offset1:49
	ds_read2_b32 v[56:57], v31 offset0:66 offset1:82
	ds_read2_b32 v[58:59], v31 offset0:99 offset1:115
	ds_read2_b32 v[60:61], v31 offset0:132 offset1:148
	ds_read2_b32 v[62:63], v31 offset0:165 offset1:181
	ds_read2_b32 v[64:65], v31 offset0:198 offset1:214
	ds_read2_b32 v[66:67], v31 offset0:231 offset1:247
	ds_read2_b32 v[68:69], v45 offset0:8 offset1:24
	ds_read2_b32 v[70:71], v45 offset0:41 offset1:57
	ds_read2_b32 v[72:73], v45 offset0:74 offset1:90
	ds_read2_b32 v[74:75], v45 offset0:107 offset1:123
	ds_read2_b32 v[76:77], v45 offset0:140 offset1:156
	ds_read2_b32 v[78:79], v45 offset0:173 offset1:189
	v_mov_b32_e32 v46, v1
	v_mov_b32_e32 v47, v1
	v_mov_b32_e32 v48, v1
	ds_read2_b32 v[80:81], v45 offset0:206 offset1:222
	ds_read2_b32 v[82:83], v45 offset0:239 offset1:255
	s_waitcnt lgkmcnt(14)
	v_cvt_pk_fp8_f32 v46, v52, v54
	s_waitcnt lgkmcnt(10)
	v_cvt_pk_fp8_f32 v47, v60, v62
	s_waitcnt lgkmcnt(6)
	v_cvt_pk_fp8_f32 v48, v68, v70
	s_waitcnt lgkmcnt(2)
	v_cvt_pk_fp8_f32 v49, v76, v78
	v_cvt_pk_fp8_f32 v46, v56, v58 op_sel:[0,0,1]
	v_cvt_pk_fp8_f32 v47, v64, v66 op_sel:[0,0,1]
	v_cvt_pk_fp8_f32 v48, v72, v74 op_sel:[0,0,1]
	s_waitcnt lgkmcnt(0)
	v_cvt_pk_fp8_f32 v49, v80, v82 op_sel:[0,0,1]
	v_lshl_add_u64 v[84:85], v[50:51], 0, v[84:85]
	v_add_u32_e32 v52, s0, v32
	global_store_dwordx4 v[84:85], v[46:49], off
	s_nop 1
	v_mov_b32_e32 v46, v1
	v_mov_b32_e32 v47, v1
	v_mov_b32_e32 v48, v1
	v_mov_b32_e32 v49, v1
	v_cvt_pk_fp8_f32 v46, v53, v55
	v_cvt_pk_fp8_f32 v47, v61, v63
	v_cvt_pk_fp8_f32 v48, v69, v71
	v_cvt_pk_fp8_f32 v49, v77, v79
	v_cvt_pk_fp8_f32 v46, v57, v59 op_sel:[0,0,1]
	v_cvt_pk_fp8_f32 v47, v65, v67 op_sel:[0,0,1]
	v_cvt_pk_fp8_f32 v48, v73, v75 op_sel:[0,0,1]
	v_cvt_pk_fp8_f32 v49, v81, v83 op_sel:[0,0,1]
	v_ashrrev_i32_e32 v53, 31, v52
	v_lshlrev_b64 v[52:53], 10, v[52:53]
	v_lshl_add_u64 v[50:51], v[50:51], 0, v[52:53]
	global_store_dwordx4 v[50:51], v[46:49], off
	s_waitcnt lgkmcnt(0)

; #define LAS __attribute__((address_space(3)))
; __device__ __forceinline__ void tr_item8(const float* W, int ld, int K, int nblk, int item, unsigned char* WT, bool gu, float scale, LAS float* scr, int lane) {
;     const int kb = item / nblk, nb = item % nblk, k0 = 64 * kb, n0 = 32 * nb;
;     int drow0 = n0;
;     if (gu) { const int bj = n0 / FF, j = n0 - bj * FF; drow0 = 256 * (j / 128) + 128 * bj + (j % 128); }
;     { float t_[32];
; #pragma unroll
;       for (int i = 0; i < 32; ++i) t_[i] = W[(size_t)(k0 + 2 * i + (lane >> 5)) * ld + n0 + (lane & 31)];
; #pragma unroll
;       for (int i = 0; i < 32; ++i) scr[(2 * i + (lane >> 5)) * 33 + (lane & 31)] = t_[i] * scale; }
; __device__ __forceinline__ void convert_items(Frame& F, const Args& a, int lo, int hi, int w, int nw) {
;     ...
;         if (r < I_DN) { tr_item8(a.in[15], D, FF, 32, r, F.ws + WS_WDN, false, WSC_DN, scr, lane); continue; } r -= I_DN;
.LBB0_1417:
	s_andn2_b64 vcc, exec, s[4:5]
	s_cbranch_vccnz .LBB0_1419
	s_lshl_b32 s0, s3, 5
	s_and_b32 s4, s9, 0x1ffc0
	s_and_b32 s6, s0, 0x3e0
	v_add_u32_e32 v46, s4, v28
	s_lshl_b32 s0, s6, 2
	v_ashrrev_i32_e32 v47, 31, v46
	v_lshl_add_u64 v[48:49], v[4:5], 0, s[0:1]
	v_lshlrev_b64 v[46:47], 12, v[46:47]
	v_lshl_add_u64 v[46:47], v[48:49], 0, v[46:47]
	v_add_co_u32_e32 v48, vcc, 0x2000, v46
	s_mov_b32 s5, s1
	s_nop 0
	v_addc_co_u32_e32 v49, vcc, 0, v47, vcc
	v_add_co_u32_e32 v50, vcc, 0x4000, v46
	s_nop 1
	v_addc_co_u32_e32 v51, vcc, 0, v47, vcc
	v_add_co_u32_e32 v52, vcc, 0x6000, v46
	s_nop 1
	v_addc_co_u32_e32 v53, vcc, 0, v47, vcc
	v_add_co_u32_e32 v54, vcc, 0x8000, v46
	s_nop 1
	v_addc_co_u32_e32 v55, vcc, 0, v47, vcc
	v_add_co_u32_e32 v56, vcc, 0xa000, v46
	s_nop 1
	v_addc_co_u32_e32 v57, vcc, 0, v47, vcc
	v_add_co_u32_e32 v58, vcc, 0xc000, v46
	s_nop 1
	v_addc_co_u32_e32 v59, vcc, 0, v47, vcc
	v_add_co_u32_e32 v60, vcc, 0xe000, v46
	s_nop 1
	v_addc_co_u32_e32 v61, vcc, 0, v47, vcc
	global_load_dword v64, v[46:47], off nt
	global_load_dword v65, v[48:49], off nt
	global_load_dword v66, v[50:51], off nt
	global_load_dword v67, v[52:53], off nt
	global_load_dword v68, v[54:55], off nt
	global_load_dword v69, v[56:57], off nt
	global_load_dword v70, v[58:59], off nt
	global_load_dword v71, v[60:61], off nt
	v_add_co_u32_e32 v48, vcc, 0x10000, v46
	s_nop 1
	v_addc_co_u32_e32 v49, vcc, 0, v47, vcc
	v_add_co_u32_e32 v50, vcc, 0x12000, v46
	s_nop 1
	v_addc_co_u32_e32 v51, vcc, 0, v47, vcc
	v_add_co_u32_e32 v52, vcc, 0x14000, v46
	s_nop 1
	v_addc_co_u32_e32 v53, vcc, 0, v47, vcc
	v_add_co_u32_e32 v54, vcc, 0x16000, v46
	s_nop 1
	v_addc_co_u32_e32 v55, vcc, 0, v47, vcc
	v_add_co_u32_e32 v56, vcc, 0x18000, v46
	s_nop 1
	v_addc_co_u32_e32 v57, vcc, 0, v47, vcc
	v_add_co_u32_e32 v58, vcc, 0x1a000, v46
	s_nop 1
	v_addc_co_u32_e32 v59, vcc, 0, v47, vcc
	v_add_co_u32_e32 v60, vcc, 0x1c000, v46
	s_nop 1
	v_addc_co_u32_e32 v61, vcc, 0, v47, vcc
	v_add_co_u32_e32 v62, vcc, 0x1e000, v46
	s_nop 1
	v_addc_co_u32_e32 v63, vcc, 0, v47, vcc
	global_load_dword v72, v[48:49], off nt
	global_load_dword v73, v[50:51], off nt
	global_load_dword v74, v[52:53], off nt
	global_load_dword v75, v[54:55], off nt
	global_load_dword v76, v[56:57], off nt
	global_load_dword v77, v[58:59], off nt
	global_load_dword v78, v[60:61], off nt
	global_load_dword v79, v[62:63], off nt
	v_add_co_u32_e32 v48, vcc, 0x20000, v46
	s_nop 1
	v_addc_co_u32_e32 v49, vcc, 0, v47, vcc
	v_add_co_u32_e32 v50, vcc, 0x22000, v46
	s_nop 1
	v_addc_co_u32_e32 v51, vcc, 0, v47, vcc
	v_add_co_u32_e32 v52, vcc, 0x24000, v46
	s_nop 1
	v_addc_co_u32_e32 v53, vcc, 0, v47, vcc
	v_add_co_u32_e32 v54, vcc, 0x26000, v46
	s_nop 1
	v_addc_co_u32_e32 v55, vcc, 0, v47, vcc
	v_add_co_u32_e32 v56, vcc, 0x28000, v46
	s_nop 1
	v_addc_co_u32_e32 v57, vcc, 0, v47, vcc
	v_add_co_u32_e32 v58, vcc, 0x2a000, v46
	s_nop 1
	v_addc_co_u32_e32 v59, vcc, 0, v47, vcc
	v_add_co_u32_e32 v60, vcc, 0x2c000, v46
	s_nop 1
	v_addc_co_u32_e32 v61, vcc, 0, v47, vcc
	v_add_co_u32_e32 v62, vcc, 0x2e000, v46
	s_nop 1
	v_addc_co_u32_e32 v63, vcc, 0, v47, vcc
	global_load_dword v80, v[48:49], off nt
	global_load_dword v81, v[50:51], off nt
	global_load_dword v82, v[52:53], off nt
	global_load_dword v83, v[54:55], off nt
	global_load_dword v84, v[56:57], off nt
	global_load_dword v85, v[58:59], off nt
	s_nop 0
	global_load_dword v60, v[60:61], off nt
	s_nop 0
	global_load_dword v61, v[62:63], off nt
	v_add_co_u32_e32 v48, vcc, 0x30000, v46
	s_nop 1
	v_addc_co_u32_e32 v49, vcc, 0, v47, vcc
	v_add_co_u32_e32 v50, vcc, 0x32000, v46
	s_nop 1
	v_addc_co_u32_e32 v51, vcc, 0, v47, vcc
	v_add_co_u32_e32 v52, vcc, 0x34000, v46
	s_nop 1
	v_addc_co_u32_e32 v53, vcc, 0, v47, vcc
	v_add_co_u32_e32 v54, vcc, 0x36000, v46
	s_nop 1
	v_addc_co_u32_e32 v55, vcc, 0, v47, vcc
	v_add_co_u32_e32 v56, vcc, 0x38000, v46
	s_nop 1
	v_addc_co_u32_e32 v57, vcc, 0, v47, vcc
	v_add_co_u32_e32 v58, vcc, 0x3a000, v46
	s_nop 1
	v_addc_co_u32_e32 v59, vcc, 0, v47, vcc
	global_load_dword v62, v[48:49], off nt
	s_nop 0
	global_load_dword v50, v[50:51], off nt
	s_nop 0
	global_load_dword v51, v[52:53], off nt
	s_nop 0
	global_load_dword v52, v[54:55], off nt
	global_load_dword v53, v[56:57], off nt
	s_nop 0
	global_load_dword v54, v[58:59], off nt
	v_add_co_u32_e32 v48, vcc, 0x3c000, v46
	s_nop 1
	v_addc_co_u32_e32 v49, vcc, 0, v47, vcc
	v_add_co_u32_e32 v46, vcc, 0x3e000, v46
	s_nop 1
	v_addc_co_u32_e32 v47, vcc, 0, v47, vcc
	global_load_dword v48, v[48:49], off nt
	s_nop 0
	global_load_dword v46, v[46:47], off nt
	s_waitcnt vmcnt(31)
	v_mul_f32_e32 v47, 0x43000000, v64
	s_waitcnt vmcnt(30)
; __device__ __forceinline__ unsigned cvt_pk4_fp8(float a, float b, float c, float d) { int w = 0; w = __builtin_amdgcn_cvt_pk_fp8_f32(a, b, w, false); w = __builtin_amdgcn_cvt_pk_fp8_f32(c, d, w, true); return (unsigned)w; }
; #define GAS __attribute__((address_space(1)))
; #define LAS __attribute__((address_space(3)))
; #define LDS_WAIT() asm volatile("s_waitcnt lgkmcnt(0)" ::: "memory")
; __device__ __forceinline__ void tr_item8(const float* W, int ld, int K, int nblk, int item, unsigned char* WT, bool gu, float scale, LAS float* scr, int lane) {
;     ...
; #pragma unroll
;       for (int i = 0; i < 32; ++i) scr[(2 * i + (lane >> 5)) * 33 + (lane & 31)] = t_[i] * scale; }
;     LDS_WAIT(); asm volatile("" ::: "memory");
;     const int c = lane & 3;
; #pragma unroll
;     for (int j = 0; j < 2; ++j) { const int n = (lane >> 2) + 16 * j; const LAS float* sp = scr + (16 * c) * 33 + n;
;         v4u o; o.x = pg8::cvt_pk4_fp8(sp[0 * 33], sp[1 * 33], sp[2 * 33], sp[3 * 33]); o.y = pg8::cvt_pk4_fp8(sp[4 * 33], sp[5 * 33], sp[6 * 33], sp[7 * 33]);
;         o.z = pg8::cvt_pk4_fp8(sp[8 * 33], sp[9 * 33], sp[10 * 33], sp[11 * 33]); o.w = pg8::cvt_pk4_fp8(sp[12 * 33], sp[13 * 33], sp[14 * 33], sp[15 * 33]);
;         *(GAS v4u*)(WT + (size_t)(drow0 + n) * K + k0 + 16 * c) = o; }
;     LDS_WAIT(); asm volatile("" ::: "memory");
	v_mul_f32_e32 v49, 0x43000000, v65
	ds_write2_b32 v29, v47, v49 offset1:66
	s_waitcnt vmcnt(29)
	v_mul_f32_e32 v47, 0x43000000, v66
	s_waitcnt vmcnt(28)
	v_mul_f32_e32 v49, 0x43000000, v67
	ds_write2_b32 v29, v47, v49 offset0:132 offset1:198
	s_waitcnt vmcnt(27)
	v_mul_f32_e32 v47, 0x43000000, v68
	s_waitcnt vmcnt(26)
	v_mul_f32_e32 v49, 0x43000000, v69
	ds_write2_b32 v38, v47, v49 offset0:8 offset1:74
	s_waitcnt vmcnt(25)
	v_mul_f32_e32 v47, 0x43000000, v70
	s_waitcnt vmcnt(24)
	v_mul_f32_e32 v49, 0x43000000, v71
	ds_write2_b32 v38, v47, v49 offset0:140 offset1:206
	s_waitcnt vmcnt(23)
	v_mul_f32_e32 v47, 0x43000000, v72
	s_waitcnt vmcnt(22)
	v_mul_f32_e32 v49, 0x43000000, v73
	ds_write2_b32 v39, v47, v49 offset0:16 offset1:82
	s_waitcnt vmcnt(21)
	v_mul_f32_e32 v47, 0x43000000, v74
	s_waitcnt vmcnt(20)
	v_mul_f32_e32 v49, 0x43000000, v75
	ds_write2_b32 v39, v47, v49 offset0:148 offset1:214
	s_waitcnt vmcnt(19)
	v_mul_f32_e32 v47, 0x43000000, v76
	s_waitcnt vmcnt(18)
	v_mul_f32_e32 v49, 0x43000000, v77
	ds_write2_b32 v40, v47, v49 offset0:24 offset1:90
	s_waitcnt vmcnt(17)
	v_mul_f32_e32 v47, 0x43000000, v78
	s_waitcnt vmcnt(16)
	v_mul_f32_e32 v49, 0x43000000, v79
	ds_write2_b32 v40, v47, v49 offset0:156 offset1:222
	s_waitcnt vmcnt(15)
	v_mul_f32_e32 v47, 0x43000000, v80
	s_waitcnt vmcnt(14)
	v_mul_f32_e32 v49, 0x43000000, v81
	ds_write2_b32 v41, v47, v49 offset0:32 offset1:98
	s_waitcnt vmcnt(13)
	v_mul_f32_e32 v47, 0x43000000, v82
	s_waitcnt vmcnt(12)
	v_mul_f32_e32 v49, 0x43000000, v83
	ds_write2_b32 v41, v47, v49 offset0:164 offset1:230
	s_waitcnt vmcnt(11)
	v_mul_f32_e32 v47, 0x43000000, v84
	s_waitcnt vmcnt(10)
	v_mul_f32_e32 v49, 0x43000000, v85
	ds_write2_b32 v42, v47, v49 offset0:40 offset1:106
	s_waitcnt vmcnt(9)
	v_mul_f32_e32 v47, 0x43000000, v60
	s_waitcnt vmcnt(8)
	v_mul_f32_e32 v49, 0x43000000, v61
	ds_write2_b32 v42, v47, v49 offset0:172 offset1:238
	s_waitcnt vmcnt(7)
	v_mul_f32_e32 v47, 0x43000000, v62
	s_waitcnt vmcnt(6)
	v_mul_f32_e32 v49, 0x43000000, v50
	ds_write2_b32 v43, v47, v49 offset0:48 offset1:114
	s_waitcnt vmcnt(5)
	v_mul_f32_e32 v47, 0x43000000, v51
	s_waitcnt vmcnt(4)
	v_mul_f32_e32 v49, 0x43000000, v52
	ds_write2_b32 v43, v47, v49 offset0:180 offset1:246
	s_waitcnt vmcnt(3)
	v_mul_f32_e32 v47, 0x43000000, v53
	s_waitcnt vmcnt(2)
	v_mul_f32_e32 v49, 0x43000000, v54
	ds_write2_b32 v44, v47, v49 offset0:56 offset1:122
	v_mov_b32_e32 v49, 0
	v_lshl_add_u64 v[50:51], v[16:17], 0, s[4:5]
	s_waitcnt vmcnt(1)
	v_mul_f32_e32 v47, 0x43000000, v48
	s_waitcnt vmcnt(0)
	v_mul_f32_e32 v46, 0x43000000, v46
	ds_write2_b32 v44, v47, v46 offset0:188 offset1:254
	s_waitcnt lgkmcnt(0)
	ds_read2_b32 v[52:53], v31 offset1:16
	ds_read2_b32 v[54:55], v31 offset0:33 offset1:49
	ds_read2_b32 v[56:57], v31 offset0:66 offset1:82
	ds_read2_b32 v[58:59], v31 offset0:99 offset1:115
	ds_read2_b32 v[60:61], v31 offset0:132 offset1:148
	ds_read2_b32 v[62:63], v31 offset0:165 offset1:181
	ds_read2_b32 v[64:65], v31 offset0:198 offset1:214
	ds_read2_b32 v[66:67], v31 offset0:231 offset1:247
	ds_read2_b32 v[68:69], v45 offset0:8 offset1:24
	ds_read2_b32 v[70:71], v45 offset0:41 offset1:57
	ds_read2_b32 v[72:73], v45 offset0:74 offset1:90
	ds_read2_b32 v[74:75], v45 offset0:107 offset1:123
	ds_read2_b32 v[76:77], v45 offset0:140 offset1:156
	ds_read2_b32 v[78:79], v45 offset0:173 offset1:189
	v_mov_b32_e32 v46, 0
	v_mov_b32_e32 v47, 0
	v_mov_b32_e32 v48, 0
	ds_read2_b32 v[80:81], v45 offset0:206 offset1:222
	ds_read2_b32 v[82:83], v45 offset0:239 offset1:255
	s_waitcnt lgkmcnt(14)
	v_cvt_pk_fp8_f32 v46, v52, v54
	s_waitcnt lgkmcnt(10)
	v_cvt_pk_fp8_f32 v47, v60, v62
	s_waitcnt lgkmcnt(6)
	v_cvt_pk_fp8_f32 v48, v68, v70
	s_waitcnt lgkmcnt(2)
	v_cvt_pk_fp8_f32 v49, v76, v78
	v_cvt_pk_fp8_f32 v46, v56, v58 op_sel:[0,0,1]
	v_cvt_pk_fp8_f32 v47, v64, v66 op_sel:[0,0,1]
	v_cvt_pk_fp8_f32 v48, v72, v74 op_sel:[0,0,1]
	s_waitcnt lgkmcnt(0)
	v_cvt_pk_fp8_f32 v49, v80, v82 op_sel:[0,0,1]
	v_add_u32_e32 v52, s6, v30
	v_mad_i64_i32 v[84:85], s[4:5], v52, s55, v[50:51]
	global_store_dwordx4 v[84:85], v[46:49], off
	v_add_u32_e32 v52, s6, v32
	v_mad_i64_i32 v[50:51], s[4:5], v52, s55, v[50:51]
	v_mov_b32_e32 v46, 0
	v_mov_b32_e32 v47, 0
	v_mov_b32_e32 v48, 0
	v_mov_b32_e32 v49, 0
	v_cvt_pk_fp8_f32 v46, v53, v55
	v_cvt_pk_fp8_f32 v47, v61, v63
	v_cvt_pk_fp8_f32 v48, v69, v71
	v_cvt_pk_fp8_f32 v49, v77, v79
	v_cvt_pk_fp8_f32 v46, v57, v59 op_sel:[0,0,1]
	v_cvt_pk_fp8_f32 v47, v65, v67 op_sel:[0,0,1]
	v_cvt_pk_fp8_f32 v48, v73, v75 op_sel:[0,0,1]
	v_cvt_pk_fp8_f32 v49, v81, v83 op_sel:[0,0,1]
	global_store_dwordx4 v[50:51], v[46:49], off
	s_waitcnt lgkmcnt(0)

; #define LAS __attribute__((address_space(3)))
; __device__ __forceinline__ void tr_item8(const float* W, int ld, int K, int nblk, int item, unsigned char* WT, bool gu, float scale, LAS float* scr, int lane) {
;     const int kb = item / nblk, nb = item % nblk, k0 = 64 * kb, n0 = 32 * nb;
;     int drow0 = n0;
;     if (gu) { const int bj = n0 / FF, j = n0 - bj * FF; drow0 = 256 * (j / 128) + 128 * bj + (j % 128); }
;     { float t_[32];
; #pragma unroll
;       for (int i = 0; i < 32; ++i) t_[i] = W[(size_t)(k0 + 2 * i + (lane >> 5)) * ld + n0 + (lane & 31)];
; #pragma unroll
;       for (int i = 0; i < 32; ++i) scr[(2 * i + (lane >> 5)) * 33 + (lane & 31)] = t_[i] * scale; }
; __device__ __forceinline__ void convert_items(Frame& F, const Args& a, int lo, int hi, int w, int nw) {
;     ...
;         if (r < I_GU) { tr_item8(a.in[14], 2 * FF, D, 224, r, F.ws + WS_WGU, true, WSC_GU, scr, lane); continue; } r -= I_GU;
.LBB0_1420:
	s_andn2_b64 vcc, exec, s[4:5]
	s_cbranch_vccnz .LBB0_1422
	s_add_i32 s0, s3, 0xf300
	s_bfe_u32 s4, s0, 0xb0005
	s_mulk_i32 s4, 0x2493
	s_lshr_b32 s4, s4, 16
	s_mul_i32 s5, s4, 0xe0
	s_sub_i32 s0, s0, s5
	s_lshl_b32 s5, s0, 5
	s_and_b32 s6, s0, 0xffff
	s_cmpk_gt_u32 s6, 0x6f
	s_cselect_b32 s61, 0xfffff200, 0
	s_cselect_b32 s62, 0x80, 0
	s_lshl_b32 s0, s0, 7
	s_lshl_b32 s4, s4, 6
	s_and_b32 s0, s0, 0x3ff80
	v_add_u32_e32 v64, s4, v28
	v_lshl_add_u64 v[46:47], v[6:7], 0, s[0:1]
	v_mad_i64_i32 v[48:49], s[6:7], v64, s56, v[46:47]
	v_add_u32_e32 v50, 2, v64
	v_add_u32_e32 v52, 4, v64
	v_add_u32_e32 v54, 6, v64
	v_add_u32_e32 v56, 8, v64
	v_add_u32_e32 v58, 10, v64
	v_add_u32_e32 v60, 12, v64
	v_add_u32_e32 v62, 14, v64
	v_mad_i64_i32 v[50:51], s[6:7], v50, s56, v[46:47]
	v_mad_i64_i32 v[52:53], s[6:7], v52, s56, v[46:47]
	v_mad_i64_i32 v[54:55], s[6:7], v54, s56, v[46:47]
	v_mad_i64_i32 v[56:57], s[6:7], v56, s56, v[46:47]
	v_mad_i64_i32 v[58:59], s[6:7], v58, s56, v[46:47]
	v_mad_i64_i32 v[60:61], s[6:7], v60, s56, v[46:47]
	v_mad_i64_i32 v[62:63], s[6:7], v62, s56, v[46:47]
	global_load_dword v65, v[48:49], off nt
	global_load_dword v66, v[50:51], off nt
	global_load_dword v67, v[52:53], off nt
	global_load_dword v68, v[54:55], off nt
	global_load_dword v69, v[56:57], off nt
	global_load_dword v70, v[58:59], off nt
	global_load_dword v71, v[60:61], off nt
	global_load_dword v72, v[62:63], off nt
	v_add_u32_e32 v48, 16, v64
	v_mad_i64_i32 v[48:49], s[6:7], v48, s56, v[46:47]
	v_add_u32_e32 v50, 18, v64
	v_add_u32_e32 v52, 20, v64
	v_add_u32_e32 v54, 22, v64
	v_add_u32_e32 v56, 24, v64
	v_add_u32_e32 v58, 26, v64
	v_add_u32_e32 v60, 28, v64
	v_add_u32_e32 v62, 30, v64
	v_mad_i64_i32 v[50:51], s[6:7], v50, s56, v[46:47]
	v_mad_i64_i32 v[52:53], s[6:7], v52, s56, v[46:47]
	v_mad_i64_i32 v[54:55], s[6:7], v54, s56, v[46:47]
	v_mad_i64_i32 v[56:57], s[6:7], v56, s56, v[46:47]
	v_mad_i64_i32 v[58:59], s[6:7], v58, s56, v[46:47]
	v_mad_i64_i32 v[60:61], s[6:7], v60, s56, v[46:47]
	v_mad_i64_i32 v[62:63], s[6:7], v62, s56, v[46:47]
	global_load_dword v73, v[48:49], off nt
	global_load_dword v74, v[50:51], off nt
	global_load_dword v75, v[52:53], off nt
	global_load_dword v76, v[54:55], off nt
	global_load_dword v77, v[56:57], off nt
	global_load_dword v78, v[58:59], off nt
	global_load_dword v79, v[60:61], off nt
	global_load_dword v80, v[62:63], off nt
	v_add_u32_e32 v48, 32, v64
	v_add_u32_e32 v50, 34, v64
	v_add_u32_e32 v52, 36, v64
	v_add_u32_e32 v54, 38, v64
	v_add_u32_e32 v60, 44, v64
	v_mad_i64_i32 v[48:49], s[6:7], v48, s56, v[46:47]
	v_mad_i64_i32 v[50:51], s[6:7], v50, s56, v[46:47]
	v_mad_i64_i32 v[52:53], s[6:7], v52, s56, v[46:47]
	v_mad_i64_i32 v[54:55], s[6:7], v54, s56, v[46:47]
	v_add_u32_e32 v56, 40, v64
	v_add_u32_e32 v58, 42, v64
	v_mad_i64_i32 v[60:61], s[6:7], v60, s56, v[46:47]
	v_add_u32_e32 v62, 46, v64
	v_mad_i64_i32 v[56:57], s[6:7], v56, s56, v[46:47]
	v_mad_i64_i32 v[58:59], s[6:7], v58, s56, v[46:47]
	v_mad_i64_i32 v[62:63], s[6:7], v62, s56, v[46:47]
	global_load_dword v81, v[48:49], off nt
	global_load_dword v82, v[50:51], off nt
	global_load_dword v83, v[52:53], off nt
	global_load_dword v84, v[54:55], off nt
	global_load_dword v85, v[56:57], off nt
	global_load_dword v86, v[58:59], off nt
	s_nop 0
	global_load_dword v60, v[60:61], off nt
	s_nop 0
	global_load_dword v61, v[62:63], off nt
	v_add_u32_e32 v48, 48, v64
	v_add_u32_e32 v50, 50, v64
	v_add_u32_e32 v52, 52, v64
	v_add_u32_e32 v54, 54, v64
	v_mad_i64_i32 v[48:49], s[6:7], v48, s56, v[46:47]
	v_mad_i64_i32 v[50:51], s[6:7], v50, s56, v[46:47]
	v_mad_i64_i32 v[52:53], s[6:7], v52, s56, v[46:47]
	v_mad_i64_i32 v[54:55], s[6:7], v54, s56, v[46:47]
	v_add_u32_e32 v56, 56, v64
	v_add_u32_e32 v58, 58, v64
	v_mad_i64_i32 v[56:57], s[6:7], v56, s56, v[46:47]
	v_mad_i64_i32 v[58:59], s[6:7], v58, s56, v[46:47]
	global_load_dword v62, v[48:49], off nt
	s_nop 0
	global_load_dword v50, v[50:51], off nt
	s_nop 0
	global_load_dword v51, v[52:53], off nt
	s_nop 0
	global_load_dword v52, v[54:55], off nt
	global_load_dword v53, v[56:57], off nt
	s_nop 0
	global_load_dword v54, v[58:59], off nt
	v_add_u32_e32 v48, 60, v64
	v_add_u32_e32 v55, 62, v64
	v_mad_i64_i32 v[48:49], s[6:7], v48, s56, v[46:47]
	v_mad_i64_i32 v[46:47], s[6:7], v55, s56, v[46:47]
	global_load_dword v48, v[48:49], off nt
	s_nop 0
	global_load_dword v46, v[46:47], off nt
	s_waitcnt vmcnt(31)
	v_mul_f32_e32 v47, 0x42800000, v65
	s_waitcnt vmcnt(30)
	v_mul_f32_e32 v49, 0x42800000, v66
	ds_write2_b32 v29, v47, v49 offset1:66
	s_waitcnt vmcnt(29)
	v_mul_f32_e32 v47, 0x42800000, v67
	s_waitcnt vmcnt(28)
	v_mul_f32_e32 v49, 0x42800000, v68
	ds_write2_b32 v29, v47, v49 offset0:132 offset1:198
	s_waitcnt vmcnt(27)
	v_mul_f32_e32 v47, 0x42800000, v69
	s_waitcnt vmcnt(26)
; __device__ __forceinline__ unsigned cvt_pk4_fp8(float a, float b, float c, float d) { int w = 0; w = __builtin_amdgcn_cvt_pk_fp8_f32(a, b, w, false); w = __builtin_amdgcn_cvt_pk_fp8_f32(c, d, w, true); return (unsigned)w; }
; #define GAS __attribute__((address_space(1)))
; #define LAS __attribute__((address_space(3)))
; #define LDS_WAIT() asm volatile("s_waitcnt lgkmcnt(0)" ::: "memory")
; __device__ __forceinline__ void tr_item8(const float* W, int ld, int K, int nblk, int item, unsigned char* WT, bool gu, float scale, LAS float* scr, int lane) {
;     ...
; #pragma unroll
;       for (int i = 0; i < 32; ++i) scr[(2 * i + (lane >> 5)) * 33 + (lane & 31)] = t_[i] * scale; }
;     LDS_WAIT(); asm volatile("" ::: "memory");
;     const int c = lane & 3;
; #pragma unroll
;     for (int j = 0; j < 2; ++j) { const int n = (lane >> 2) + 16 * j; const LAS float* sp = scr + (16 * c) * 33 + n;
;         v4u o; o.x = pg8::cvt_pk4_fp8(sp[0 * 33], sp[1 * 33], sp[2 * 33], sp[3 * 33]); o.y = pg8::cvt_pk4_fp8(sp[4 * 33], sp[5 * 33], sp[6 * 33], sp[7 * 33]);
;         o.z = pg8::cvt_pk4_fp8(sp[8 * 33], sp[9 * 33], sp[10 * 33], sp[11 * 33]); o.w = pg8::cvt_pk4_fp8(sp[12 * 33], sp[13 * 33], sp[14 * 33], sp[15 * 33]);
;         *(GAS v4u*)(WT + (size_t)(drow0 + n) * K + k0 + 16 * c) = o; }
;     LDS_WAIT(); asm volatile("" ::: "memory");
	v_mul_f32_e32 v49, 0x42800000, v70
	ds_write2_b32 v38, v47, v49 offset0:8 offset1:74
	s_waitcnt vmcnt(25)
	v_mul_f32_e32 v47, 0x42800000, v71
	s_waitcnt vmcnt(24)
	v_mul_f32_e32 v49, 0x42800000, v72
	ds_write2_b32 v38, v47, v49 offset0:140 offset1:206
	s_add_i32 s0, s61, s5
	s_sext_i32_i16 s5, s0
	s_bfe_u32 s5, s5, 0x70018
	s_add_i32 s5, s0, s5
	s_sext_i32_i16 s6, s5
	s_and_b32 s5, s5, 0xff80
	s_sub_i32 s0, s0, s5
	s_lshl_b32 s6, s6, 1
	s_sext_i32_i16 s0, s0
	s_waitcnt vmcnt(23)
	v_mul_f32_e32 v47, 0x42800000, v73
	s_waitcnt vmcnt(22)
	v_mul_f32_e32 v49, 0x42800000, v74
	ds_write2_b32 v39, v47, v49 offset0:16 offset1:82
	s_waitcnt vmcnt(21)
	v_mul_f32_e32 v47, 0x42800000, v75
	s_waitcnt vmcnt(20)
	v_mul_f32_e32 v49, 0x42800000, v76
	ds_write2_b32 v39, v47, v49 offset0:148 offset1:214
	s_waitcnt vmcnt(19)
	v_mul_f32_e32 v47, 0x42800000, v77
	s_waitcnt vmcnt(18)
	v_mul_f32_e32 v49, 0x42800000, v78
	ds_write2_b32 v40, v47, v49 offset0:24 offset1:90
	s_waitcnt vmcnt(17)
	v_mul_f32_e32 v47, 0x42800000, v79
	s_waitcnt vmcnt(16)
	v_mul_f32_e32 v49, 0x42800000, v80
	ds_write2_b32 v40, v47, v49 offset0:156 offset1:222
	s_and_b32 s6, s6, 0xffffff00
	s_add_i32 s0, s62, s0
	s_add_i32 s0, s0, s6
	s_mov_b32 s5, s1
	s_waitcnt vmcnt(15)
	v_mul_f32_e32 v47, 0x42800000, v81
	s_waitcnt vmcnt(14)
	v_mul_f32_e32 v49, 0x42800000, v82
	ds_write2_b32 v41, v47, v49 offset0:32 offset1:98
	s_waitcnt vmcnt(13)
	v_mul_f32_e32 v47, 0x42800000, v83
	s_waitcnt vmcnt(12)
	v_mul_f32_e32 v49, 0x42800000, v84
	ds_write2_b32 v41, v47, v49 offset0:164 offset1:230
	s_waitcnt vmcnt(11)
	v_mul_f32_e32 v47, 0x42800000, v85
	s_waitcnt vmcnt(10)
	v_mul_f32_e32 v49, 0x42800000, v86
	ds_write2_b32 v42, v47, v49 offset0:40 offset1:106
	s_waitcnt vmcnt(9)
	v_mul_f32_e32 v47, 0x42800000, v60
	s_waitcnt vmcnt(8)
	v_mul_f32_e32 v49, 0x42800000, v61
	ds_write2_b32 v42, v47, v49 offset0:172 offset1:238
	v_add_u32_e32 v84, s0, v30
	v_ashrrev_i32_e32 v85, 31, v84
	v_lshlrev_b64 v[84:85], 10, v[84:85]
	s_waitcnt vmcnt(7)
	v_mul_f32_e32 v47, 0x42800000, v62
	s_waitcnt vmcnt(6)
	v_mul_f32_e32 v49, 0x42800000, v50
	ds_write2_b32 v43, v47, v49 offset0:48 offset1:114
	s_waitcnt vmcnt(5)
	v_mul_f32_e32 v47, 0x42800000, v51
	s_waitcnt vmcnt(4)
	v_mul_f32_e32 v49, 0x42800000, v52
	ds_write2_b32 v43, v47, v49 offset0:180 offset1:246
	s_waitcnt vmcnt(3)
	v_mul_f32_e32 v47, 0x42800000, v53
	s_waitcnt vmcnt(2)
	v_mul_f32_e32 v49, 0x42800000, v54
	ds_write2_b32 v44, v47, v49 offset0:56 offset1:122
	v_mov_b32_e32 v49, 0
	v_lshl_add_u64 v[50:51], v[18:19], 0, s[4:5]
	s_waitcnt vmcnt(1)
	v_mul_f32_e32 v47, 0x42800000, v48
	s_waitcnt vmcnt(0)
	v_mul_f32_e32 v46, 0x42800000, v46
	ds_write2_b32 v44, v47, v46 offset0:188 offset1:254
	s_waitcnt lgkmcnt(0)
	ds_read2_b32 v[52:53], v31 offset1:16
	ds_read2_b32 v[54:55], v31 offset0:33 offset1:49
	ds_read2_b32 v[56:57], v31 offset0:66 offset1:82
	ds_read2_b32 v[58:59], v31 offset0:99 offset1:115
	ds_read2_b32 v[60:61], v31 offset0:132 offset1:148
	ds_read2_b32 v[62:63], v31 offset0:165 offset1:181
	ds_read2_b32 v[64:65], v31 offset0:198 offset1:214
	ds_read2_b32 v[66:67], v31 offset0:231 offset1:247
	ds_read2_b32 v[68:69], v45 offset0:8 offset1:24
	ds_read2_b32 v[70:71], v45 offset0:41 offset1:57
	ds_read2_b32 v[72:73], v45 offset0:74 offset1:90
	ds_read2_b32 v[74:75], v45 offset0:107 offset1:123
	ds_read2_b32 v[76:77], v45 offset0:140 offset1:156
	ds_read2_b32 v[78:79], v45 offset0:173 offset1:189
	v_mov_b32_e32 v46, 0
	v_mov_b32_e32 v47, 0
	v_mov_b32_e32 v48, 0
	ds_read2_b32 v[80:81], v45 offset0:206 offset1:222
	ds_read2_b32 v[82:83], v45 offset0:239 offset1:255
	s_waitcnt lgkmcnt(14)
	v_cvt_pk_fp8_f32 v46, v52, v54
	s_waitcnt lgkmcnt(10)
	v_cvt_pk_fp8_f32 v47, v60, v62
	s_waitcnt lgkmcnt(6)
	v_cvt_pk_fp8_f32 v48, v68, v70
	s_waitcnt lgkmcnt(2)
	v_cvt_pk_fp8_f32 v49, v76, v78
	v_cvt_pk_fp8_f32 v46, v56, v58 op_sel:[0,0,1]
	v_cvt_pk_fp8_f32 v47, v64, v66 op_sel:[0,0,1]
	v_cvt_pk_fp8_f32 v48, v72, v74 op_sel:[0,0,1]
	s_waitcnt lgkmcnt(0)
	v_cvt_pk_fp8_f32 v49, v80, v82 op_sel:[0,0,1]
	v_lshl_add_u64 v[84:85], v[50:51], 0, v[84:85]
	v_add_u32_e32 v52, s0, v32
	global_store_dwordx4 v[84:85], v[46:49], off
	s_nop 1
	v_mov_b32_e32 v46, 0
	v_mov_b32_e32 v47, 0
	v_mov_b32_e32 v48, 0
	v_mov_b32_e32 v49, 0
	v_cvt_pk_fp8_f32 v46, v53, v55
	v_cvt_pk_fp8_f32 v47, v61, v63
	v_cvt_pk_fp8_f32 v48, v69, v71
	v_cvt_pk_fp8_f32 v49, v77, v79
	v_cvt_pk_fp8_f32 v46, v57, v59 op_sel:[0,0,1]
	v_cvt_pk_fp8_f32 v47, v65, v67 op_sel:[0,0,1]
	v_cvt_pk_fp8_f32 v48, v73, v75 op_sel:[0,0,1]
	v_cvt_pk_fp8_f32 v49, v81, v83 op_sel:[0,0,1]
	v_ashrrev_i32_e32 v53, 31, v52
	v_lshlrev_b64 v[52:53], 10, v[52:53]
	v_lshl_add_u64 v[50:51], v[50:51], 0, v[52:53]
	global_store_dwordx4 v[50:51], v[46:49], off
	s_waitcnt lgkmcnt(0)

; #define LAS __attribute__((address_space(3)))
; __device__ __forceinline__ void tr_item(const float* W, int ld, int K, int nblk, int item, bf16* WT, bool gu, LAS float* scr, int lane) {
;     const int kb = item / nblk, nb = item % nblk, k0 = 64 * kb, n0 = 32 * nb;
;     int drow0 = n0;
;     if (gu) { const int bj = n0 / FF, j = n0 - bj * FF; drow0 = 256 * (j / 128) + 128 * bj + (j % 128); }
;     { float t_[32];
; #pragma unroll
;       for (int i = 0; i < 32; ++i) t_[i] = W[(size_t)(k0 + 2 * i + (lane >> 5)) * ld + n0 + (lane & 31)];
; #pragma unroll
;       for (int i = 0; i < 32; ++i) scr[(2 * i + (lane >> 5)) * 33 + (lane & 31)] = t_[i]; }
; __device__ __forceinline__ void convert_items(Frame& F, const Args& a, int lo, int hi, int w, int nw) {
;     ...
;         if (r < I_SO) { tr_item(a.in[12], D, D, 32, r, (bf16*)(F.ws + WS_WSWAOUT), false, scr, lane); continue; } r -= I_SO;
.LBB0_1423:
	s_andn2_b64 vcc, exec, s[4:5]
	s_cbranch_vccnz .LBB0_1425
	s_add_i32 s0, s9, 0x2000
	s_and_b32 s5, s0, 0x1ffc0
	s_and_b32 s4, s8, 0x3e0
	v_add_u32_e32 v46, s5, v28
	s_lshl_b32 s0, s4, 2
	v_ashrrev_i32_e32 v47, 31, v46
	v_lshl_add_u64 v[48:49], v[8:9], 0, s[0:1]
	v_lshlrev_b64 v[46:47], 12, v[46:47]
	v_lshl_add_u64 v[46:47], v[48:49], 0, v[46:47]
	v_add_co_u32_e32 v48, vcc, 0x2000, v46
	s_lshl_b32 s0, s5, 1
	s_nop 0
	v_addc_co_u32_e32 v49, vcc, 0, v47, vcc
	v_add_co_u32_e32 v50, vcc, 0x4000, v46
	s_nop 1
	v_addc_co_u32_e32 v51, vcc, 0, v47, vcc
	v_add_co_u32_e32 v52, vcc, 0x6000, v46
	s_nop 1
	v_addc_co_u32_e32 v53, vcc, 0, v47, vcc
	v_add_co_u32_e32 v54, vcc, 0x8000, v46
	s_nop 1
	v_addc_co_u32_e32 v55, vcc, 0, v47, vcc
	v_add_co_u32_e32 v56, vcc, 0xa000, v46
	s_nop 1
	v_addc_co_u32_e32 v57, vcc, 0, v47, vcc
	v_add_co_u32_e32 v58, vcc, 0xc000, v46
	s_nop 1
	v_addc_co_u32_e32 v59, vcc, 0, v47, vcc
	v_add_co_u32_e32 v60, vcc, 0xe000, v46
	s_nop 1
	v_addc_co_u32_e32 v61, vcc, 0, v47, vcc
	global_load_dword v64, v[46:47], off nt
	global_load_dword v65, v[48:49], off nt
	global_load_dword v66, v[50:51], off nt
	global_load_dword v67, v[52:53], off nt
	global_load_dword v68, v[54:55], off nt
	global_load_dword v69, v[56:57], off nt
	global_load_dword v70, v[58:59], off nt
	global_load_dword v71, v[60:61], off nt
	v_add_co_u32_e32 v48, vcc, 0x10000, v46
	s_nop 1
	v_addc_co_u32_e32 v49, vcc, 0, v47, vcc
	v_add_co_u32_e32 v50, vcc, 0x12000, v46
	s_nop 1
	v_addc_co_u32_e32 v51, vcc, 0, v47, vcc
	v_add_co_u32_e32 v52, vcc, 0x14000, v46
	s_nop 1
	v_addc_co_u32_e32 v53, vcc, 0, v47, vcc
	v_add_co_u32_e32 v54, vcc, 0x16000, v46
	s_nop 1
	v_addc_co_u32_e32 v55, vcc, 0, v47, vcc
	v_add_co_u32_e32 v56, vcc, 0x18000, v46
	s_nop 1
	v_addc_co_u32_e32 v57, vcc, 0, v47, vcc
	v_add_co_u32_e32 v58, vcc, 0x1a000, v46
	s_nop 1
	v_addc_co_u32_e32 v59, vcc, 0, v47, vcc
	v_add_co_u32_e32 v60, vcc, 0x1c000, v46
	s_nop 1
	v_addc_co_u32_e32 v61, vcc, 0, v47, vcc
	v_add_co_u32_e32 v62, vcc, 0x1e000, v46
	s_nop 1
	v_addc_co_u32_e32 v63, vcc, 0, v47, vcc
	global_load_dword v72, v[48:49], off nt
	global_load_dword v73, v[50:51], off nt
	global_load_dword v74, v[52:53], off nt
	global_load_dword v75, v[54:55], off nt
	global_load_dword v76, v[56:57], off nt
	global_load_dword v77, v[58:59], off nt
	global_load_dword v78, v[60:61], off nt
	global_load_dword v79, v[62:63], off nt
	v_add_co_u32_e32 v48, vcc, 0x20000, v46
	s_nop 1
	v_addc_co_u32_e32 v49, vcc, 0, v47, vcc
	v_add_co_u32_e32 v50, vcc, 0x22000, v46
	s_nop 1
	v_addc_co_u32_e32 v51, vcc, 0, v47, vcc
	v_add_co_u32_e32 v52, vcc, 0x24000, v46
	s_nop 1
	v_addc_co_u32_e32 v53, vcc, 0, v47, vcc
	v_add_co_u32_e32 v54, vcc, 0x26000, v46
	s_nop 1
	v_addc_co_u32_e32 v55, vcc, 0, v47, vcc
	v_add_co_u32_e32 v56, vcc, 0x28000, v46
	s_nop 1
	v_addc_co_u32_e32 v57, vcc, 0, v47, vcc
	v_add_co_u32_e32 v58, vcc, 0x2a000, v46
	s_nop 1
	v_addc_co_u32_e32 v59, vcc, 0, v47, vcc
	v_add_co_u32_e32 v60, vcc, 0x2c000, v46
	s_nop 1
	v_addc_co_u32_e32 v61, vcc, 0, v47, vcc
	v_add_co_u32_e32 v62, vcc, 0x2e000, v46
	s_nop 1
	v_addc_co_u32_e32 v63, vcc, 0, v47, vcc
	global_load_dword v80, v[48:49], off nt
	global_load_dword v81, v[50:51], off nt
	global_load_dword v82, v[52:53], off nt
	global_load_dword v83, v[54:55], off nt
	global_load_dword v84, v[56:57], off nt
	global_load_dword v85, v[58:59], off nt
	global_load_dword v86, v[60:61], off nt
	s_nop 0
	global_load_dword v62, v[62:63], off nt
	v_add_co_u32_e32 v48, vcc, 0x30000, v46
	s_nop 1
	v_addc_co_u32_e32 v49, vcc, 0, v47, vcc
	v_add_co_u32_e32 v50, vcc, 0x32000, v46
	s_nop 1
	v_addc_co_u32_e32 v51, vcc, 0, v47, vcc
	v_add_co_u32_e32 v52, vcc, 0x34000, v46
	s_nop 1
	v_addc_co_u32_e32 v53, vcc, 0, v47, vcc
	v_add_co_u32_e32 v54, vcc, 0x36000, v46
	s_nop 1
	v_addc_co_u32_e32 v55, vcc, 0, v47, vcc
	v_add_co_u32_e32 v56, vcc, 0x38000, v46
	s_nop 1
	v_addc_co_u32_e32 v57, vcc, 0, v47, vcc
	v_add_co_u32_e32 v58, vcc, 0x3a000, v46
	s_nop 1
	v_addc_co_u32_e32 v59, vcc, 0, v47, vcc
	v_add_co_u32_e32 v60, vcc, 0x3c000, v46
	s_nop 1
	v_addc_co_u32_e32 v61, vcc, 0, v47, vcc
	v_add_co_u32_e32 v46, vcc, 0x3e000, v46
	s_nop 1
	v_addc_co_u32_e32 v47, vcc, 0, v47, vcc
	global_load_dword v48, v[48:49], off nt
	s_nop 0
	global_load_dword v49, v[50:51], off nt
	s_nop 0
	global_load_dword v50, v[52:53], off nt
	global_load_dword v51, v[54:55], off nt
	s_nop 0
	global_load_dword v52, v[56:57], off nt
	global_load_dword v53, v[58:59], off nt
	global_load_dword v54, v[60:61], off nt
	s_nop 0
	global_load_dword v46, v[46:47], off nt
	s_waitcnt vmcnt(30)
	ds_write2_b32 v29, v64, v65 offset1:66
	s_waitcnt vmcnt(28)
	ds_write2_b32 v29, v66, v67 offset0:132 offset1:198
	s_waitcnt vmcnt(26)
	ds_write2_b32 v38, v68, v69 offset0:8 offset1:74
	s_waitcnt vmcnt(24)
	ds_write2_b32 v38, v70, v71 offset0:140 offset1:206
	s_waitcnt vmcnt(22)
	ds_write2_b32 v39, v72, v73 offset0:16 offset1:82
	s_waitcnt vmcnt(20)
	ds_write2_b32 v39, v74, v75 offset0:148 offset1:214
	s_waitcnt vmcnt(18)
	ds_write2_b32 v40, v76, v77 offset0:24 offset1:90
	s_waitcnt vmcnt(16)
	ds_write2_b32 v40, v78, v79 offset0:156 offset1:222
	s_waitcnt vmcnt(14)
	ds_write2_b32 v41, v80, v81 offset0:32 offset1:98
	s_waitcnt vmcnt(12)
	ds_write2_b32 v41, v82, v83 offset0:164 offset1:230
	s_waitcnt vmcnt(10)
; #define GAS __attribute__((address_space(1)))
; #define LAS __attribute__((address_space(3)))
; #define LDS_WAIT() asm volatile("s_waitcnt lgkmcnt(0)" ::: "memory")
; __device__ __forceinline__ unsigned pk2(float lo, float hi) { return f2bf(lo) | (f2bf(hi) << 16); }
; __device__ __forceinline__ void tr_item(const float* W, int ld, int K, int nblk, int item, bf16* WT, bool gu, LAS float* scr, int lane) {
;     ...
;       for (int i = 0; i < 32; ++i) scr[(2 * i + (lane >> 5)) * 33 + (lane & 31)] = t_[i]; }
;     LDS_WAIT(); asm volatile("" ::: "memory");
;     const int c = lane & 7;
; #pragma unroll
;     for (int j = 0; j < 4; ++j) { const int n = (lane >> 3) + 8 * j; const LAS float* s = scr + (8 * c) * 33 + n;
;         v4u o; o.x = pk2(s[0 * 33], s[1 * 33]); o.y = pk2(s[2 * 33], s[3 * 33]); o.z = pk2(s[4 * 33], s[5 * 33]); o.w = pk2(s[6 * 33], s[7 * 33]);
;         *(GAS v4u*)(WT + (size_t)(drow0 + n) * K + k0 + 8 * c) = o; }
;     LDS_WAIT(); asm volatile("" ::: "memory");
	ds_write2_b32 v42, v84, v85 offset0:40 offset1:106
	s_waitcnt vmcnt(8)
	ds_write2_b32 v42, v86, v62 offset0:172 offset1:238
	s_waitcnt vmcnt(6)
	ds_write2_b32 v43, v48, v49 offset0:48 offset1:114
	s_waitcnt vmcnt(4)
	ds_write2_b32 v43, v50, v51 offset0:180 offset1:246
	s_waitcnt vmcnt(2)
	ds_write2_b32 v44, v52, v53 offset0:56 offset1:122
	s_waitcnt vmcnt(0)
	ds_write2_b32 v44, v54, v46 offset0:188 offset1:254
	s_waitcnt lgkmcnt(0)
	ds_read2_b32 v[50:51], v34 offset1:8
	ds_read2_b32 v[54:55], v34 offset0:33 offset1:41
	ds_read2_b32 v[56:57], v34 offset0:66 offset1:74
	ds_read2_b32 v[58:59], v34 offset0:99 offset1:107
	ds_read2_b32 v[60:61], v34 offset0:132 offset1:140
	s_waitcnt lgkmcnt(4)
	v_bfe_u32 v46, v50, 16, 1
	v_add3_u32 v46, v50, v46, s57
	s_waitcnt lgkmcnt(3)
	v_bfe_u32 v47, v54, 16, 1
	v_lshrrev_b32_e32 v46, 16, v46
	v_add3_u32 v47, v54, v47, s57
	ds_read2_b32 v[62:63], v34 offset0:165 offset1:173
	v_and_or_b32 v46, v47, s58, v46
	s_waitcnt lgkmcnt(3)
	v_bfe_u32 v47, v56, 16, 1
	v_add3_u32 v47, v56, v47, s57
	s_waitcnt lgkmcnt(2)
	v_bfe_u32 v48, v58, 16, 1
	ds_read2_b32 v[64:65], v34 offset0:198 offset1:206
	v_lshrrev_b32_e32 v47, 16, v47
	v_add3_u32 v48, v58, v48, s57
	ds_read2_b32 v[66:67], v34 offset0:231 offset1:239
	v_and_or_b32 v47, v48, s58, v47
	s_waitcnt lgkmcnt(3)
	v_bfe_u32 v48, v60, 16, 1
	v_add3_u32 v48, v60, v48, s57
	s_waitcnt lgkmcnt(2)
	v_bfe_u32 v49, v62, 16, 1
	v_lshrrev_b32_e32 v48, 16, v48
	v_add3_u32 v49, v62, v49, s57
	v_and_or_b32 v48, v49, s58, v48
	s_waitcnt lgkmcnt(1)
	v_bfe_u32 v49, v64, 16, 1
	v_add_u32_e32 v68, s4, v33
	v_add3_u32 v49, v64, v49, s57
	s_waitcnt lgkmcnt(0)
	v_bfe_u32 v50, v66, 16, 1
	v_ashrrev_i32_e32 v69, 31, v68
	v_lshl_add_u64 v[52:53], v[20:21], 0, s[0:1]
	v_lshrrev_b32_e32 v49, 16, v49
	v_add3_u32 v50, v66, v50, s57
	v_lshlrev_b64 v[68:69], 11, v[68:69]
	v_and_or_b32 v49, v50, s58, v49
	v_lshl_add_u64 v[68:69], v[52:53], 0, v[68:69]
	global_store_dwordx4 v[68:69], v[46:49], off
	v_bfe_u32 v50, v67, 16, 1
	v_add3_u32 v50, v67, v50, s57
	v_bfe_u32 v46, v51, 16, 1
	v_add3_u32 v46, v51, v46, s57
	v_bfe_u32 v47, v55, 16, 1
	v_lshrrev_b32_e32 v46, 16, v46
	v_add3_u32 v47, v55, v47, s57
	v_and_or_b32 v46, v47, s58, v46
	v_bfe_u32 v47, v57, 16, 1
	v_add3_u32 v47, v57, v47, s57
	v_bfe_u32 v48, v59, 16, 1
	v_lshrrev_b32_e32 v47, 16, v47
	v_add3_u32 v48, v59, v48, s57
	v_and_or_b32 v47, v48, s58, v47
	v_bfe_u32 v48, v61, 16, 1
	v_add3_u32 v48, v61, v48, s57
	v_bfe_u32 v49, v63, 16, 1
	v_lshrrev_b32_e32 v48, 16, v48
	v_add3_u32 v49, v63, v49, s57
	v_and_or_b32 v48, v49, s58, v48
	v_bfe_u32 v49, v65, 16, 1
	v_add3_u32 v49, v65, v49, s57
	v_lshrrev_b32_e32 v49, 16, v49
	v_and_or_b32 v49, v50, s58, v49
	v_add_u32_e32 v50, s4, v35
	v_ashrrev_i32_e32 v51, 31, v50
	v_lshlrev_b64 v[50:51], 11, v[50:51]
	ds_read2_b32 v[54:55], v34 offset0:16 offset1:24
	v_lshl_add_u64 v[50:51], v[52:53], 0, v[50:51]
	global_store_dwordx4 v[50:51], v[46:49], off
	ds_read2_b32 v[50:51], v34 offset0:49 offset1:57
	ds_read2_b32 v[56:57], v34 offset0:82 offset1:90
	ds_read2_b32 v[58:59], v34 offset0:115 offset1:123
	s_waitcnt lgkmcnt(3)
	v_bfe_u32 v46, v54, 16, 1
	v_add3_u32 v46, v54, v46, s57
	s_waitcnt lgkmcnt(2)
	v_bfe_u32 v47, v50, 16, 1
	ds_read2_b32 v[60:61], v34 offset0:148 offset1:156
	v_lshrrev_b32_e32 v46, 16, v46
	v_add3_u32 v47, v50, v47, s57
	ds_read2_b32 v[62:63], v34 offset0:181 offset1:189
	v_and_or_b32 v46, v47, s58, v46
	s_waitcnt lgkmcnt(3)
	v_bfe_u32 v47, v56, 16, 1
	v_add3_u32 v47, v56, v47, s57
	s_waitcnt lgkmcnt(2)
	v_bfe_u32 v48, v58, 16, 1
	ds_read2_b32 v[64:65], v34 offset0:214 offset1:222
	v_lshrrev_b32_e32 v47, 16, v47
	v_add3_u32 v48, v58, v48, s57
	ds_read2_b32 v[66:67], v34 offset0:247 offset1:255
	v_and_or_b32 v47, v48, s58, v47
	s_waitcnt lgkmcnt(3)
	v_bfe_u32 v48, v60, 16, 1
	v_add3_u32 v48, v60, v48, s57
	s_waitcnt lgkmcnt(2)
	v_bfe_u32 v49, v62, 16, 1
	v_lshrrev_b32_e32 v48, 16, v48
	v_add3_u32 v49, v62, v49, s57
	v_and_or_b32 v48, v49, s58, v48
	s_waitcnt lgkmcnt(1)
	v_bfe_u32 v49, v64, 16, 1
	v_add_u32_e32 v68, s4, v36
	v_add3_u32 v49, v64, v49, s57
	s_waitcnt lgkmcnt(0)
	v_bfe_u32 v50, v66, 16, 1
	v_ashrrev_i32_e32 v69, 31, v68
	v_lshrrev_b32_e32 v49, 16, v49
	v_add3_u32 v50, v66, v50, s57
	v_lshlrev_b64 v[68:69], 11, v[68:69]
	v_and_or_b32 v49, v50, s58, v49
	v_lshl_add_u64 v[68:69], v[52:53], 0, v[68:69]
	global_store_dwordx4 v[68:69], v[46:49], off
	v_bfe_u32 v50, v67, 16, 1
	v_add3_u32 v50, v67, v50, s57
	v_bfe_u32 v46, v55, 16, 1
	v_add3_u32 v46, v55, v46, s57
	v_bfe_u32 v47, v51, 16, 1
	v_lshrrev_b32_e32 v46, 16, v46
	v_add3_u32 v47, v51, v47, s57
	v_and_or_b32 v46, v47, s58, v46
	v_bfe_u32 v47, v57, 16, 1
	v_add3_u32 v47, v57, v47, s57
	v_bfe_u32 v48, v59, 16, 1
	v_lshrrev_b32_e32 v47, 16, v47
	v_add3_u32 v48, v59, v48, s57
	v_and_or_b32 v47, v48, s58, v47
	v_bfe_u32 v48, v61, 16, 1
	v_add3_u32 v48, v61, v48, s57
	v_bfe_u32 v49, v63, 16, 1
	v_lshrrev_b32_e32 v48, 16, v48
	v_add3_u32 v49, v63, v49, s57
	v_and_or_b32 v48, v49, s58, v48
	v_bfe_u32 v49, v65, 16, 1
	v_add3_u32 v49, v65, v49, s57
	v_lshrrev_b32_e32 v49, 16, v49
	v_and_or_b32 v49, v50, s58, v49
	v_add_u32_e32 v50, s4, v37
	v_ashrrev_i32_e32 v51, 31, v50
	v_lshlrev_b64 v[50:51], 11, v[50:51]
	v_lshl_add_u64 v[50:51], v[52:53], 0, v[50:51]
	global_store_dwordx4 v[50:51], v[46:49], off
	s_waitcnt lgkmcnt(0)

; #define LAS __attribute__((address_space(3)))
; __device__ __forceinline__ void tr_item(const float* W, int ld, int K, int nblk, int item, bf16* WT, bool gu, LAS float* scr, int lane) {
;     const int kb = item / nblk, nb = item % nblk, k0 = 64 * kb, n0 = 32 * nb;
;     int drow0 = n0;
;     if (gu) { const int bj = n0 / FF, j = n0 - bj * FF; drow0 = 256 * (j / 128) + 128 * bj + (j % 128); }
;     { float t_[32];
; #pragma unroll
;       for (int i = 0; i < 32; ++i) t_[i] = W[(size_t)(k0 + 2 * i + (lane >> 5)) * ld + n0 + (lane & 31)];
; #pragma unroll
;       for (int i = 0; i < 32; ++i) scr[(2 * i + (lane >> 5)) * 33 + (lane & 31)] = t_[i]; }
; __device__ __forceinline__ void convert_items(Frame& F, const Args& a, int lo, int hi, int w, int nw) {
;     ...
;         if (r < I_SI) { tr_item(a.in[10], D + 512, D, 48, r, (bf16*)(F.ws + WS_WSWAIN), false, scr, lane); continue; } r -= I_SI;
.LBB0_1426:
	s_andn2_b64 vcc, exec, s[4:5]
	s_cbranch_vccnz .LBB0_1428
	s_add_i32 s0, s3, 0xf800
	s_and_b32 s4, s0, 0xffff
	s_mul_i32 s4, s4, 0xaaab
	s_lshr_b32 s5, s4, 21
	s_mul_i32 s4, s5, 48
	s_sub_i32 s0, s0, s4
	s_lshl_b32 s0, s0, 5
	s_and_b32 s4, s0, 0xffe0
	v_lshl_add_u32 v64, s5, 6, v28
	s_lshl_b32 s0, s4, 2
	v_lshl_add_u64 v[46:47], v[10:11], 0, s[0:1]
	v_add_u32_e32 v50, 2, v64
	v_add_u32_e32 v52, 4, v64
	v_add_u32_e32 v54, 6, v64
	v_add_u32_e32 v56, 8, v64
	v_add_u32_e32 v58, 10, v64
	v_add_u32_e32 v60, 12, v64
	v_add_u32_e32 v62, 14, v64
	v_mad_i64_i32 v[48:49], s[6:7], v64, s59, v[46:47]
	v_mad_i64_i32 v[50:51], s[6:7], v50, s59, v[46:47]
	v_mad_i64_i32 v[52:53], s[6:7], v52, s59, v[46:47]
	v_mad_i64_i32 v[54:55], s[6:7], v54, s59, v[46:47]
	v_mad_i64_i32 v[56:57], s[6:7], v56, s59, v[46:47]
	v_mad_i64_i32 v[58:59], s[6:7], v58, s59, v[46:47]
	v_mad_i64_i32 v[60:61], s[6:7], v60, s59, v[46:47]
	v_mad_i64_i32 v[62:63], s[6:7], v62, s59, v[46:47]
	global_load_dword v65, v[48:49], off nt
	global_load_dword v66, v[50:51], off nt
	global_load_dword v67, v[52:53], off nt
	global_load_dword v68, v[54:55], off nt
	global_load_dword v69, v[56:57], off nt
	global_load_dword v70, v[58:59], off nt
	global_load_dword v71, v[60:61], off nt
	global_load_dword v72, v[62:63], off nt
	v_add_u32_e32 v48, 16, v64
	v_add_u32_e32 v50, 18, v64
	v_add_u32_e32 v52, 20, v64
	v_add_u32_e32 v54, 22, v64
	v_add_u32_e32 v56, 24, v64
	v_add_u32_e32 v58, 26, v64
	v_add_u32_e32 v60, 28, v64
	v_add_u32_e32 v62, 30, v64
	v_mad_i64_i32 v[48:49], s[6:7], v48, s59, v[46:47]
	v_mad_i64_i32 v[50:51], s[6:7], v50, s59, v[46:47]
	v_mad_i64_i32 v[52:53], s[6:7], v52, s59, v[46:47]
	v_mad_i64_i32 v[54:55], s[6:7], v54, s59, v[46:47]
	v_mad_i64_i32 v[56:57], s[6:7], v56, s59, v[46:47]
	v_mad_i64_i32 v[58:59], s[6:7], v58, s59, v[46:47]
	v_mad_i64_i32 v[60:61], s[6:7], v60, s59, v[46:47]
	v_mad_i64_i32 v[62:63], s[6:7], v62, s59, v[46:47]
	global_load_dword v73, v[48:49], off nt
	global_load_dword v74, v[50:51], off nt
	global_load_dword v75, v[52:53], off nt
	global_load_dword v76, v[54:55], off nt
	global_load_dword v77, v[56:57], off nt
	global_load_dword v78, v[58:59], off nt
	global_load_dword v79, v[60:61], off nt
	global_load_dword v80, v[62:63], off nt
	v_add_u32_e32 v48, 32, v64
	v_add_u32_e32 v50, 34, v64
	v_add_u32_e32 v52, 36, v64
	v_add_u32_e32 v54, 38, v64
	v_add_u32_e32 v56, 40, v64
	v_add_u32_e32 v58, 42, v64
	v_add_u32_e32 v60, 44, v64
	v_add_u32_e32 v62, 46, v64
	v_mad_i64_i32 v[48:49], s[6:7], v48, s59, v[46:47]
	v_mad_i64_i32 v[50:51], s[6:7], v50, s59, v[46:47]
	v_mad_i64_i32 v[52:53], s[6:7], v52, s59, v[46:47]
	v_mad_i64_i32 v[54:55], s[6:7], v54, s59, v[46:47]
	v_mad_i64_i32 v[56:57], s[6:7], v56, s59, v[46:47]
	v_mad_i64_i32 v[58:59], s[6:7], v58, s59, v[46:47]
	v_mad_i64_i32 v[60:61], s[6:7], v60, s59, v[46:47]
	v_mad_i64_i32 v[62:63], s[6:7], v62, s59, v[46:47]
	global_load_dword v81, v[48:49], off nt
	global_load_dword v82, v[50:51], off nt
	global_load_dword v83, v[52:53], off nt
	global_load_dword v84, v[54:55], off nt
	global_load_dword v85, v[56:57], off nt
	global_load_dword v86, v[58:59], off nt
	global_load_dword v87, v[60:61], off nt
	s_nop 0
	global_load_dword v62, v[62:63], off nt
	v_add_u32_e32 v48, 48, v64
	v_add_u32_e32 v50, 50, v64
	v_add_u32_e32 v52, 52, v64
	v_add_u32_e32 v54, 54, v64
	v_add_u32_e32 v56, 56, v64
	v_add_u32_e32 v58, 58, v64
	v_add_u32_e32 v60, 60, v64
	v_add_u32_e32 v63, 62, v64
	v_mad_i64_i32 v[48:49], s[6:7], v48, s59, v[46:47]
	v_mad_i64_i32 v[50:51], s[6:7], v50, s59, v[46:47]
	v_mad_i64_i32 v[52:53], s[6:7], v52, s59, v[46:47]
	v_mad_i64_i32 v[54:55], s[6:7], v54, s59, v[46:47]
	v_mad_i64_i32 v[56:57], s[6:7], v56, s59, v[46:47]
	v_mad_i64_i32 v[58:59], s[6:7], v58, s59, v[46:47]
	v_mad_i64_i32 v[60:61], s[6:7], v60, s59, v[46:47]
	v_mad_i64_i32 v[46:47], s[6:7], v63, s59, v[46:47]
	global_load_dword v48, v[48:49], off nt
	s_nop 0
	global_load_dword v49, v[50:51], off nt
	s_nop 0
	global_load_dword v50, v[52:53], off nt
	global_load_dword v51, v[54:55], off nt
	s_nop 0
	global_load_dword v52, v[56:57], off nt
	global_load_dword v53, v[58:59], off nt
	global_load_dword v54, v[60:61], off nt
	s_nop 0
	global_load_dword v46, v[46:47], off nt
	s_waitcnt vmcnt(30)
	ds_write2_b32 v29, v65, v66 offset1:66
	s_waitcnt vmcnt(28)
	ds_write2_b32 v29, v67, v68 offset0:132 offset1:198
	s_waitcnt vmcnt(26)
	ds_write2_b32 v38, v69, v70 offset0:8 offset1:74
	s_waitcnt vmcnt(24)
	ds_write2_b32 v38, v71, v72 offset0:140 offset1:206
	s_waitcnt vmcnt(22)
	ds_write2_b32 v39, v73, v74 offset0:16 offset1:82
	s_waitcnt vmcnt(20)
	ds_write2_b32 v39, v75, v76 offset0:148 offset1:214
	s_waitcnt vmcnt(18)
	ds_write2_b32 v40, v77, v78 offset0:24 offset1:90
	s_waitcnt vmcnt(16)
	ds_write2_b32 v40, v79, v80 offset0:156 offset1:222
	s_waitcnt vmcnt(14)
	ds_write2_b32 v41, v81, v82 offset0:32 offset1:98
	s_waitcnt vmcnt(12)
	ds_write2_b32 v41, v83, v84 offset0:164 offset1:230
	s_waitcnt vmcnt(10)
	ds_write2_b32 v42, v85, v86 offset0:40 offset1:106
	s_waitcnt vmcnt(8)
	ds_write2_b32 v42, v87, v62 offset0:172 offset1:238
	s_waitcnt vmcnt(6)
; #define GAS __attribute__((address_space(1)))
; #define LAS __attribute__((address_space(3)))
; #define LDS_WAIT() asm volatile("s_waitcnt lgkmcnt(0)" ::: "memory")
; __device__ __forceinline__ unsigned pk2(float lo, float hi) { return f2bf(lo) | (f2bf(hi) << 16); }
; __device__ __forceinline__ void tr_item(const float* W, int ld, int K, int nblk, int item, bf16* WT, bool gu, LAS float* scr, int lane) {
;     ...
;       for (int i = 0; i < 32; ++i) scr[(2 * i + (lane >> 5)) * 33 + (lane & 31)] = t_[i]; }
;     LDS_WAIT(); asm volatile("" ::: "memory");
;     const int c = lane & 7;
; #pragma unroll
;     for (int j = 0; j < 4; ++j) { const int n = (lane >> 3) + 8 * j; const LAS float* s = scr + (8 * c) * 33 + n;
;         v4u o; o.x = pk2(s[0 * 33], s[1 * 33]); o.y = pk2(s[2 * 33], s[3 * 33]); o.z = pk2(s[4 * 33], s[5 * 33]); o.w = pk2(s[6 * 33], s[7 * 33]);
;         *(GAS v4u*)(WT + (size_t)(drow0 + n) * K + k0 + 8 * c) = o; }
;     LDS_WAIT(); asm volatile("" ::: "memory");
	ds_write2_b32 v43, v48, v49 offset0:48 offset1:114
	s_waitcnt vmcnt(4)
	ds_write2_b32 v43, v50, v51 offset0:180 offset1:246
	s_waitcnt vmcnt(2)
	ds_write2_b32 v44, v52, v53 offset0:56 offset1:122
	s_waitcnt vmcnt(0)
	ds_write2_b32 v44, v54, v46 offset0:188 offset1:254
	s_waitcnt lgkmcnt(0)
	ds_read2_b32 v[50:51], v34 offset1:8
	ds_read2_b32 v[54:55], v34 offset0:33 offset1:41
	ds_read2_b32 v[56:57], v34 offset0:66 offset1:74
	ds_read2_b32 v[58:59], v34 offset0:99 offset1:107
	ds_read2_b32 v[60:61], v34 offset0:132 offset1:140
	s_waitcnt lgkmcnt(4)
	v_bfe_u32 v46, v50, 16, 1
	v_add3_u32 v46, v50, v46, s57
	s_waitcnt lgkmcnt(3)
	v_bfe_u32 v47, v54, 16, 1
	v_lshrrev_b32_e32 v46, 16, v46
	v_add3_u32 v47, v54, v47, s57
	ds_read2_b32 v[62:63], v34 offset0:165 offset1:173
	v_and_or_b32 v46, v47, s58, v46
	s_waitcnt lgkmcnt(3)
	v_bfe_u32 v47, v56, 16, 1
	v_add3_u32 v47, v56, v47, s57
	s_waitcnt lgkmcnt(2)
	v_bfe_u32 v48, v58, 16, 1
	ds_read2_b32 v[64:65], v34 offset0:198 offset1:206
	v_lshrrev_b32_e32 v47, 16, v47
	v_add3_u32 v48, v58, v48, s57
	ds_read2_b32 v[66:67], v34 offset0:231 offset1:239
	v_and_or_b32 v47, v48, s58, v47
	s_waitcnt lgkmcnt(3)
	v_bfe_u32 v48, v60, 16, 1
	v_add3_u32 v48, v60, v48, s57
	s_waitcnt lgkmcnt(2)
	v_bfe_u32 v49, v62, 16, 1
	v_lshrrev_b32_e32 v48, 16, v48
	v_add3_u32 v49, v62, v49, s57
	v_and_or_b32 v48, v49, s58, v48
	s_waitcnt lgkmcnt(1)
	v_bfe_u32 v49, v64, 16, 1
	v_add_u32_e32 v68, s4, v33
	s_lshl_b32 s0, s5, 7
	v_add3_u32 v49, v64, v49, s57
	s_waitcnt lgkmcnt(0)
	v_bfe_u32 v50, v66, 16, 1
	v_ashrrev_i32_e32 v69, 31, v68
	v_lshl_add_u64 v[52:53], v[22:23], 0, s[0:1]
	v_lshrrev_b32_e32 v49, 16, v49
	v_add3_u32 v50, v66, v50, s57
	v_lshlrev_b64 v[68:69], 11, v[68:69]
	v_and_or_b32 v49, v50, s58, v49
	v_lshl_add_u64 v[68:69], v[52:53], 0, v[68:69]
	global_store_dwordx4 v[68:69], v[46:49], off
	v_bfe_u32 v50, v67, 16, 1
	v_add3_u32 v50, v67, v50, s57
	v_bfe_u32 v46, v51, 16, 1
	v_add3_u32 v46, v51, v46, s57
	v_bfe_u32 v47, v55, 16, 1
	v_lshrrev_b32_e32 v46, 16, v46
	v_add3_u32 v47, v55, v47, s57
	v_and_or_b32 v46, v47, s58, v46
	v_bfe_u32 v47, v57, 16, 1
	v_add3_u32 v47, v57, v47, s57
	v_bfe_u32 v48, v59, 16, 1
	v_lshrrev_b32_e32 v47, 16, v47
	v_add3_u32 v48, v59, v48, s57
	v_and_or_b32 v47, v48, s58, v47
	v_bfe_u32 v48, v61, 16, 1
	v_add3_u32 v48, v61, v48, s57
	v_bfe_u32 v49, v63, 16, 1
	v_lshrrev_b32_e32 v48, 16, v48
	v_add3_u32 v49, v63, v49, s57
	v_and_or_b32 v48, v49, s58, v48
	v_bfe_u32 v49, v65, 16, 1
	v_add3_u32 v49, v65, v49, s57
	v_lshrrev_b32_e32 v49, 16, v49
	v_and_or_b32 v49, v50, s58, v49
	v_add_u32_e32 v50, s4, v35
	v_ashrrev_i32_e32 v51, 31, v50
	v_lshlrev_b64 v[50:51], 11, v[50:51]
	ds_read2_b32 v[54:55], v34 offset0:16 offset1:24
	v_lshl_add_u64 v[50:51], v[52:53], 0, v[50:51]
	global_store_dwordx4 v[50:51], v[46:49], off
	ds_read2_b32 v[50:51], v34 offset0:49 offset1:57
	ds_read2_b32 v[56:57], v34 offset0:82 offset1:90
	ds_read2_b32 v[58:59], v34 offset0:115 offset1:123
	s_waitcnt lgkmcnt(3)
	v_bfe_u32 v46, v54, 16, 1
	v_add3_u32 v46, v54, v46, s57
	s_waitcnt lgkmcnt(2)
	v_bfe_u32 v47, v50, 16, 1
	ds_read2_b32 v[60:61], v34 offset0:148 offset1:156
	v_lshrrev_b32_e32 v46, 16, v46
	v_add3_u32 v47, v50, v47, s57
	ds_read2_b32 v[62:63], v34 offset0:181 offset1:189
	v_and_or_b32 v46, v47, s58, v46
	s_waitcnt lgkmcnt(3)
	v_bfe_u32 v47, v56, 16, 1
	v_add3_u32 v47, v56, v47, s57
	s_waitcnt lgkmcnt(2)
	v_bfe_u32 v48, v58, 16, 1
	ds_read2_b32 v[64:65], v34 offset0:214 offset1:222
	v_lshrrev_b32_e32 v47, 16, v47
	v_add3_u32 v48, v58, v48, s57
	ds_read2_b32 v[66:67], v34 offset0:247 offset1:255
	v_and_or_b32 v47, v48, s58, v47
	s_waitcnt lgkmcnt(3)
	v_bfe_u32 v48, v60, 16, 1
	v_add3_u32 v48, v60, v48, s57
	s_waitcnt lgkmcnt(2)
	v_bfe_u32 v49, v62, 16, 1
	v_lshrrev_b32_e32 v48, 16, v48
	v_add3_u32 v49, v62, v49, s57
	v_and_or_b32 v48, v49, s58, v48
	s_waitcnt lgkmcnt(1)
	v_bfe_u32 v49, v64, 16, 1
	v_add_u32_e32 v68, s4, v36
	v_add3_u32 v49, v64, v49, s57
	s_waitcnt lgkmcnt(0)
	v_bfe_u32 v50, v66, 16, 1
	v_ashrrev_i32_e32 v69, 31, v68
	v_lshrrev_b32_e32 v49, 16, v49
	v_add3_u32 v50, v66, v50, s57
	v_lshlrev_b64 v[68:69], 11, v[68:69]
	v_and_or_b32 v49, v50, s58, v49
	v_lshl_add_u64 v[68:69], v[52:53], 0, v[68:69]
	global_store_dwordx4 v[68:69], v[46:49], off
	v_bfe_u32 v50, v67, 16, 1
	v_add3_u32 v50, v67, v50, s57
	v_bfe_u32 v46, v55, 16, 1
	v_add3_u32 v46, v55, v46, s57
	v_bfe_u32 v47, v51, 16, 1
	v_lshrrev_b32_e32 v46, 16, v46
	v_add3_u32 v47, v51, v47, s57
	v_and_or_b32 v46, v47, s58, v46
	v_bfe_u32 v47, v57, 16, 1
	v_add3_u32 v47, v57, v47, s57
	v_bfe_u32 v48, v59, 16, 1
	v_lshrrev_b32_e32 v47, 16, v47
	v_add3_u32 v48, v59, v48, s57
	v_and_or_b32 v47, v48, s58, v47
	v_bfe_u32 v48, v61, 16, 1
	v_add3_u32 v48, v61, v48, s57
	v_bfe_u32 v49, v63, 16, 1
	v_lshrrev_b32_e32 v48, 16, v48
	v_add3_u32 v49, v63, v49, s57
	v_and_or_b32 v48, v49, s58, v48
	v_bfe_u32 v49, v65, 16, 1
	v_add3_u32 v49, v65, v49, s57
	v_lshrrev_b32_e32 v49, 16, v49
	v_and_or_b32 v49, v50, s58, v49
	v_add_u32_e32 v50, s4, v37
	v_ashrrev_i32_e32 v51, 31, v50
	v_lshlrev_b64 v[50:51], 11, v[50:51]
	v_lshl_add_u64 v[50:51], v[52:53], 0, v[50:51]
	global_store_dwordx4 v[50:51], v[46:49], off
	s_waitcnt lgkmcnt(0)

; #define LAS __attribute__((address_space(3)))
; __device__ __forceinline__ void tr_item(const float* W, int ld, int K, int nblk, int item, bf16* WT, bool gu, LAS float* scr, int lane) {
;     const int kb = item / nblk, nb = item % nblk, k0 = 64 * kb, n0 = 32 * nb;
;     int drow0 = n0;
;     if (gu) { const int bj = n0 / FF, j = n0 - bj * FF; drow0 = 256 * (j / 128) + 128 * bj + (j % 128); }
;     { float t_[32];
; #pragma unroll
;       for (int i = 0; i < 32; ++i) t_[i] = W[(size_t)(k0 + 2 * i + (lane >> 5)) * ld + n0 + (lane & 31)];
; #pragma unroll
;       for (int i = 0; i < 32; ++i) scr[(2 * i + (lane >> 5)) * 33 + (lane & 31)] = t_[i]; }
; __device__ __forceinline__ void convert_items(Frame& F, const Args& a, int lo, int hi, int w, int nw) {
;     ...
;         if (r < I_FO) { tr_item(a.in[9], D, D, 32, r, (bf16*)(F.ws + WS_WFOXOUT), false, scr, lane); continue; } r -= I_FO;
.LBB0_1429:
	s_andn2_b64 vcc, exec, s[4:5]
	s_cbranch_vccnz .LBB0_1431
	s_add_i32 s0, s9, 0x2a00
	s_and_b32 s5, s0, 0x1ffc0
	s_and_b32 s4, s8, 0x3e0
	v_add_u32_e32 v46, s5, v28
	s_lshl_b32 s0, s4, 2
	v_ashrrev_i32_e32 v47, 31, v46
	v_lshl_add_u64 v[48:49], v[12:13], 0, s[0:1]
	v_lshlrev_b64 v[46:47], 12, v[46:47]
	v_lshl_add_u64 v[46:47], v[48:49], 0, v[46:47]
	v_add_co_u32_e32 v48, vcc, 0x2000, v46
	s_lshl_b32 s0, s5, 1
	s_nop 0
	v_addc_co_u32_e32 v49, vcc, 0, v47, vcc
	v_add_co_u32_e32 v50, vcc, 0x4000, v46
	s_nop 1
	v_addc_co_u32_e32 v51, vcc, 0, v47, vcc
	v_add_co_u32_e32 v52, vcc, 0x6000, v46
	s_nop 1
	v_addc_co_u32_e32 v53, vcc, 0, v47, vcc
	v_add_co_u32_e32 v54, vcc, 0x8000, v46
	s_nop 1
	v_addc_co_u32_e32 v55, vcc, 0, v47, vcc
	v_add_co_u32_e32 v56, vcc, 0xa000, v46
	s_nop 1
	v_addc_co_u32_e32 v57, vcc, 0, v47, vcc
	v_add_co_u32_e32 v58, vcc, 0xc000, v46
	s_nop 1
	v_addc_co_u32_e32 v59, vcc, 0, v47, vcc
	v_add_co_u32_e32 v60, vcc, 0xe000, v46
	s_nop 1
	v_addc_co_u32_e32 v61, vcc, 0, v47, vcc
	global_load_dword v64, v[46:47], off nt
	global_load_dword v65, v[48:49], off nt
	global_load_dword v66, v[50:51], off nt
	global_load_dword v67, v[52:53], off nt
	global_load_dword v68, v[54:55], off nt
	global_load_dword v69, v[56:57], off nt
	global_load_dword v70, v[58:59], off nt
	global_load_dword v71, v[60:61], off nt
	v_add_co_u32_e32 v48, vcc, 0x10000, v46
	s_nop 1
	v_addc_co_u32_e32 v49, vcc, 0, v47, vcc
	v_add_co_u32_e32 v50, vcc, 0x12000, v46
	s_nop 1
	v_addc_co_u32_e32 v51, vcc, 0, v47, vcc
	v_add_co_u32_e32 v52, vcc, 0x14000, v46
	s_nop 1
	v_addc_co_u32_e32 v53, vcc, 0, v47, vcc
	v_add_co_u32_e32 v54, vcc, 0x16000, v46
	s_nop 1
	v_addc_co_u32_e32 v55, vcc, 0, v47, vcc
	v_add_co_u32_e32 v56, vcc, 0x18000, v46
	s_nop 1
	v_addc_co_u32_e32 v57, vcc, 0, v47, vcc
	v_add_co_u32_e32 v58, vcc, 0x1a000, v46
	s_nop 1
	v_addc_co_u32_e32 v59, vcc, 0, v47, vcc
	v_add_co_u32_e32 v60, vcc, 0x1c000, v46
	s_nop 1
	v_addc_co_u32_e32 v61, vcc, 0, v47, vcc
	v_add_co_u32_e32 v62, vcc, 0x1e000, v46
	s_nop 1
	v_addc_co_u32_e32 v63, vcc, 0, v47, vcc
	global_load_dword v72, v[48:49], off nt
	global_load_dword v73, v[50:51], off nt
	global_load_dword v74, v[52:53], off nt
	global_load_dword v75, v[54:55], off nt
	global_load_dword v76, v[56:57], off nt
	global_load_dword v77, v[58:59], off nt
	global_load_dword v78, v[60:61], off nt
	global_load_dword v79, v[62:63], off nt
	v_add_co_u32_e32 v48, vcc, 0x20000, v46
	s_nop 1
	v_addc_co_u32_e32 v49, vcc, 0, v47, vcc
	v_add_co_u32_e32 v50, vcc, 0x22000, v46
	s_nop 1
	v_addc_co_u32_e32 v51, vcc, 0, v47, vcc
	v_add_co_u32_e32 v52, vcc, 0x24000, v46
	s_nop 1
	v_addc_co_u32_e32 v53, vcc, 0, v47, vcc
	v_add_co_u32_e32 v54, vcc, 0x26000, v46
	s_nop 1
	v_addc_co_u32_e32 v55, vcc, 0, v47, vcc
	v_add_co_u32_e32 v56, vcc, 0x28000, v46
	s_nop 1
	v_addc_co_u32_e32 v57, vcc, 0, v47, vcc
	v_add_co_u32_e32 v58, vcc, 0x2a000, v46
	s_nop 1
	v_addc_co_u32_e32 v59, vcc, 0, v47, vcc
	v_add_co_u32_e32 v60, vcc, 0x2c000, v46
	s_nop 1
	v_addc_co_u32_e32 v61, vcc, 0, v47, vcc
	v_add_co_u32_e32 v62, vcc, 0x2e000, v46
	s_nop 1
	v_addc_co_u32_e32 v63, vcc, 0, v47, vcc
	global_load_dword v80, v[48:49], off nt
	global_load_dword v81, v[50:51], off nt
	global_load_dword v82, v[52:53], off nt
	global_load_dword v83, v[54:55], off nt
	global_load_dword v84, v[56:57], off nt
	global_load_dword v85, v[58:59], off nt
	global_load_dword v86, v[60:61], off nt
	s_nop 0
	global_load_dword v62, v[62:63], off nt
	v_add_co_u32_e32 v48, vcc, 0x30000, v46
	s_nop 1
	v_addc_co_u32_e32 v49, vcc, 0, v47, vcc
	v_add_co_u32_e32 v50, vcc, 0x32000, v46
	s_nop 1
	v_addc_co_u32_e32 v51, vcc, 0, v47, vcc
	v_add_co_u32_e32 v52, vcc, 0x34000, v46
	s_nop 1
	v_addc_co_u32_e32 v53, vcc, 0, v47, vcc
	v_add_co_u32_e32 v54, vcc, 0x36000, v46
	s_nop 1
	v_addc_co_u32_e32 v55, vcc, 0, v47, vcc
	v_add_co_u32_e32 v56, vcc, 0x38000, v46
	s_nop 1
	v_addc_co_u32_e32 v57, vcc, 0, v47, vcc
	v_add_co_u32_e32 v58, vcc, 0x3a000, v46
	s_nop 1
	v_addc_co_u32_e32 v59, vcc, 0, v47, vcc
	v_add_co_u32_e32 v60, vcc, 0x3c000, v46
	s_nop 1
	v_addc_co_u32_e32 v61, vcc, 0, v47, vcc
	v_add_co_u32_e32 v46, vcc, 0x3e000, v46
	s_nop 1
	v_addc_co_u32_e32 v47, vcc, 0, v47, vcc
	global_load_dword v48, v[48:49], off nt
	s_nop 0
	global_load_dword v49, v[50:51], off nt
	s_nop 0
	global_load_dword v50, v[52:53], off nt
	global_load_dword v51, v[54:55], off nt
	s_nop 0
	global_load_dword v52, v[56:57], off nt
	global_load_dword v53, v[58:59], off nt
	global_load_dword v54, v[60:61], off nt
	s_nop 0
	global_load_dword v46, v[46:47], off nt
	s_waitcnt vmcnt(30)
	ds_write2_b32 v29, v64, v65 offset1:66
	s_waitcnt vmcnt(28)
	ds_write2_b32 v29, v66, v67 offset0:132 offset1:198
	s_waitcnt vmcnt(26)
	ds_write2_b32 v38, v68, v69 offset0:8 offset1:74
	s_waitcnt vmcnt(24)
	ds_write2_b32 v38, v70, v71 offset0:140 offset1:206
	s_waitcnt vmcnt(22)
	ds_write2_b32 v39, v72, v73 offset0:16 offset1:82
	s_waitcnt vmcnt(20)
	ds_write2_b32 v39, v74, v75 offset0:148 offset1:214
	s_waitcnt vmcnt(18)
	ds_write2_b32 v40, v76, v77 offset0:24 offset1:90
	s_waitcnt vmcnt(16)
	ds_write2_b32 v40, v78, v79 offset0:156 offset1:222
	s_waitcnt vmcnt(14)
	ds_write2_b32 v41, v80, v81 offset0:32 offset1:98
	s_waitcnt vmcnt(12)
	ds_write2_b32 v41, v82, v83 offset0:164 offset1:230
	s_waitcnt vmcnt(10)
; #define GAS __attribute__((address_space(1)))
; #define LAS __attribute__((address_space(3)))
; #define LDS_WAIT() asm volatile("s_waitcnt lgkmcnt(0)" ::: "memory")
; __device__ __forceinline__ unsigned pk2(float lo, float hi) { return f2bf(lo) | (f2bf(hi) << 16); }
; __device__ __forceinline__ void tr_item(const float* W, int ld, int K, int nblk, int item, bf16* WT, bool gu, LAS float* scr, int lane) {
;     ...
;       for (int i = 0; i < 32; ++i) scr[(2 * i + (lane >> 5)) * 33 + (lane & 31)] = t_[i]; }
;     LDS_WAIT(); asm volatile("" ::: "memory");
;     const int c = lane & 7;
; #pragma unroll
;     for (int j = 0; j < 4; ++j) { const int n = (lane >> 3) + 8 * j; const LAS float* s = scr + (8 * c) * 33 + n;
;         v4u o; o.x = pk2(s[0 * 33], s[1 * 33]); o.y = pk2(s[2 * 33], s[3 * 33]); o.z = pk2(s[4 * 33], s[5 * 33]); o.w = pk2(s[6 * 33], s[7 * 33]);
;         *(GAS v4u*)(WT + (size_t)(drow0 + n) * K + k0 + 8 * c) = o; }
;     LDS_WAIT(); asm volatile("" ::: "memory");
	ds_write2_b32 v42, v84, v85 offset0:40 offset1:106
	s_waitcnt vmcnt(8)
	ds_write2_b32 v42, v86, v62 offset0:172 offset1:238
	s_waitcnt vmcnt(6)
	ds_write2_b32 v43, v48, v49 offset0:48 offset1:114
	s_waitcnt vmcnt(4)
	ds_write2_b32 v43, v50, v51 offset0:180 offset1:246
	s_waitcnt vmcnt(2)
	ds_write2_b32 v44, v52, v53 offset0:56 offset1:122
	s_waitcnt vmcnt(0)
	ds_write2_b32 v44, v54, v46 offset0:188 offset1:254
	s_waitcnt lgkmcnt(0)
	ds_read2_b32 v[50:51], v34 offset1:8
	ds_read2_b32 v[54:55], v34 offset0:33 offset1:41
	ds_read2_b32 v[56:57], v34 offset0:66 offset1:74
	ds_read2_b32 v[58:59], v34 offset0:99 offset1:107
	ds_read2_b32 v[60:61], v34 offset0:132 offset1:140
	s_waitcnt lgkmcnt(4)
	v_bfe_u32 v46, v50, 16, 1
	v_add3_u32 v46, v50, v46, s57
	s_waitcnt lgkmcnt(3)
	v_bfe_u32 v47, v54, 16, 1
	v_lshrrev_b32_e32 v46, 16, v46
	v_add3_u32 v47, v54, v47, s57
	ds_read2_b32 v[62:63], v34 offset0:165 offset1:173
	v_and_or_b32 v46, v47, s58, v46
	s_waitcnt lgkmcnt(3)
	v_bfe_u32 v47, v56, 16, 1
	v_add3_u32 v47, v56, v47, s57
	s_waitcnt lgkmcnt(2)
	v_bfe_u32 v48, v58, 16, 1
	ds_read2_b32 v[64:65], v34 offset0:198 offset1:206
	v_lshrrev_b32_e32 v47, 16, v47
	v_add3_u32 v48, v58, v48, s57
	ds_read2_b32 v[66:67], v34 offset0:231 offset1:239
	v_and_or_b32 v47, v48, s58, v47
	s_waitcnt lgkmcnt(3)
	v_bfe_u32 v48, v60, 16, 1
	v_add3_u32 v48, v60, v48, s57
	s_waitcnt lgkmcnt(2)
	v_bfe_u32 v49, v62, 16, 1
	v_lshrrev_b32_e32 v48, 16, v48
	v_add3_u32 v49, v62, v49, s57
	v_and_or_b32 v48, v49, s58, v48
	s_waitcnt lgkmcnt(1)
	v_bfe_u32 v49, v64, 16, 1
	v_add_u32_e32 v68, s4, v33
	v_add3_u32 v49, v64, v49, s57
	s_waitcnt lgkmcnt(0)
	v_bfe_u32 v50, v66, 16, 1
	v_ashrrev_i32_e32 v69, 31, v68
	v_lshl_add_u64 v[52:53], v[24:25], 0, s[0:1]
	v_lshrrev_b32_e32 v49, 16, v49
	v_add3_u32 v50, v66, v50, s57
	v_lshlrev_b64 v[68:69], 11, v[68:69]
	v_and_or_b32 v49, v50, s58, v49
	v_lshl_add_u64 v[68:69], v[52:53], 0, v[68:69]
	global_store_dwordx4 v[68:69], v[46:49], off
	v_bfe_u32 v50, v67, 16, 1
	v_add3_u32 v50, v67, v50, s57
	v_bfe_u32 v46, v51, 16, 1
	v_add3_u32 v46, v51, v46, s57
	v_bfe_u32 v47, v55, 16, 1
	v_lshrrev_b32_e32 v46, 16, v46
	v_add3_u32 v47, v55, v47, s57
	v_and_or_b32 v46, v47, s58, v46
	v_bfe_u32 v47, v57, 16, 1
	v_add3_u32 v47, v57, v47, s57
	v_bfe_u32 v48, v59, 16, 1
	v_lshrrev_b32_e32 v47, 16, v47
	v_add3_u32 v48, v59, v48, s57
	v_and_or_b32 v47, v48, s58, v47
	v_bfe_u32 v48, v61, 16, 1
	v_add3_u32 v48, v61, v48, s57
	v_bfe_u32 v49, v63, 16, 1
	v_lshrrev_b32_e32 v48, 16, v48
	v_add3_u32 v49, v63, v49, s57
	v_and_or_b32 v48, v49, s58, v48
	v_bfe_u32 v49, v65, 16, 1
	v_add3_u32 v49, v65, v49, s57
	v_lshrrev_b32_e32 v49, 16, v49
	v_and_or_b32 v49, v50, s58, v49
	v_add_u32_e32 v50, s4, v35
	v_ashrrev_i32_e32 v51, 31, v50
	v_lshlrev_b64 v[50:51], 11, v[50:51]
	ds_read2_b32 v[54:55], v34 offset0:16 offset1:24
	v_lshl_add_u64 v[50:51], v[52:53], 0, v[50:51]
	global_store_dwordx4 v[50:51], v[46:49], off
	ds_read2_b32 v[50:51], v34 offset0:49 offset1:57
	ds_read2_b32 v[56:57], v34 offset0:82 offset1:90
	ds_read2_b32 v[58:59], v34 offset0:115 offset1:123
	s_waitcnt lgkmcnt(3)
	v_bfe_u32 v46, v54, 16, 1
	v_add3_u32 v46, v54, v46, s57
	s_waitcnt lgkmcnt(2)
	v_bfe_u32 v47, v50, 16, 1
	ds_read2_b32 v[60:61], v34 offset0:148 offset1:156
	v_lshrrev_b32_e32 v46, 16, v46
	v_add3_u32 v47, v50, v47, s57
	ds_read2_b32 v[62:63], v34 offset0:181 offset1:189
	v_and_or_b32 v46, v47, s58, v46
	s_waitcnt lgkmcnt(3)
	v_bfe_u32 v47, v56, 16, 1
	v_add3_u32 v47, v56, v47, s57
	s_waitcnt lgkmcnt(2)
	v_bfe_u32 v48, v58, 16, 1
	ds_read2_b32 v[64:65], v34 offset0:214 offset1:222
	v_lshrrev_b32_e32 v47, 16, v47
	v_add3_u32 v48, v58, v48, s57
	ds_read2_b32 v[66:67], v34 offset0:247 offset1:255
	v_and_or_b32 v47, v48, s58, v47
	s_waitcnt lgkmcnt(3)
	v_bfe_u32 v48, v60, 16, 1
	v_add3_u32 v48, v60, v48, s57
	s_waitcnt lgkmcnt(2)
	v_bfe_u32 v49, v62, 16, 1
	v_lshrrev_b32_e32 v48, 16, v48
	v_add3_u32 v49, v62, v49, s57
	v_and_or_b32 v48, v49, s58, v48
	s_waitcnt lgkmcnt(1)
	v_bfe_u32 v49, v64, 16, 1
	v_add_u32_e32 v68, s4, v36
	v_add3_u32 v49, v64, v49, s57
	s_waitcnt lgkmcnt(0)
	v_bfe_u32 v50, v66, 16, 1
	v_ashrrev_i32_e32 v69, 31, v68
	v_lshrrev_b32_e32 v49, 16, v49
	v_add3_u32 v50, v66, v50, s57
	v_lshlrev_b64 v[68:69], 11, v[68:69]
	v_and_or_b32 v49, v50, s58, v49
	v_lshl_add_u64 v[68:69], v[52:53], 0, v[68:69]
	global_store_dwordx4 v[68:69], v[46:49], off
	v_bfe_u32 v50, v67, 16, 1
	v_add3_u32 v50, v67, v50, s57
	v_bfe_u32 v46, v55, 16, 1
	v_add3_u32 v46, v55, v46, s57
	v_bfe_u32 v47, v51, 16, 1
	v_lshrrev_b32_e32 v46, 16, v46
	v_add3_u32 v47, v51, v47, s57
	v_and_or_b32 v46, v47, s58, v46
	v_bfe_u32 v47, v57, 16, 1
	v_add3_u32 v47, v57, v47, s57
	v_bfe_u32 v48, v59, 16, 1
	v_lshrrev_b32_e32 v47, 16, v47
	v_add3_u32 v48, v59, v48, s57
	v_and_or_b32 v47, v48, s58, v47
	v_bfe_u32 v48, v61, 16, 1
	v_add3_u32 v48, v61, v48, s57
	v_bfe_u32 v49, v63, 16, 1
	v_lshrrev_b32_e32 v48, 16, v48
	v_add3_u32 v49, v63, v49, s57
	v_and_or_b32 v48, v49, s58, v48
	v_bfe_u32 v49, v65, 16, 1
	v_add3_u32 v49, v65, v49, s57
	v_lshrrev_b32_e32 v49, 16, v49
	v_and_or_b32 v49, v50, s58, v49
	v_add_u32_e32 v50, s4, v37
	v_ashrrev_i32_e32 v51, 31, v50
	v_lshlrev_b64 v[50:51], 11, v[50:51]
	v_lshl_add_u64 v[50:51], v[52:53], 0, v[50:51]
	global_store_dwordx4 v[50:51], v[46:49], off
	s_waitcnt lgkmcnt(0)

; #define LAS __attribute__((address_space(3)))
; __device__ __forceinline__ void tr_item(const float* W, int ld, int K, int nblk, int item, bf16* WT, bool gu, LAS float* scr, int lane) {
;     const int kb = item / nblk, nb = item % nblk, k0 = 64 * kb, n0 = 32 * nb;
;     int drow0 = n0;
;     if (gu) { const int bj = n0 / FF, j = n0 - bj * FF; drow0 = 256 * (j / 128) + 128 * bj + (j % 128); }
;     { float t_[32];
; #pragma unroll
;       for (int i = 0; i < 32; ++i) t_[i] = W[(size_t)(k0 + 2 * i + (lane >> 5)) * ld + n0 + (lane & 31)];
; #pragma unroll
;       for (int i = 0; i < 32; ++i) scr[(2 * i + (lane >> 5)) * 33 + (lane & 31)] = t_[i]; }
; __device__ __forceinline__ void convert_items(Frame& F, const Args& a, int lo, int hi, int w, int nw) {
;     ...
;         if (r < I_FI) { tr_item(a.in[7], 3 * D + 16, D, 96, r, (bf16*)(F.ws + WS_WFOXIN), false, scr, lane); continue; } r -= I_FI;
.LBB0_1432:
	s_andn2_b64 vcc, exec, s[4:5]
	s_cbranch_vccnz .LBB0_1405
	s_mul_hi_i32 s0, s3, 0x2aaaaaab
	s_lshr_b32 s4, s0, 31
	s_ashr_i32 s0, s0, 4
	s_add_i32 s0, s0, s4
	s_lshl_b32 s6, s0, 6
	s_mulk_i32 s0, 0xf400
	s_add_i32 s4, s8, s0
	v_add_u32_e32 v64, s6, v28
	s_ashr_i32 s5, s4, 31
	v_lshl_add_u64 v[46:47], s[4:5], 2, v[14:15]
	v_add_u32_e32 v50, 2, v64
	v_add_u32_e32 v52, 4, v64
	v_add_u32_e32 v54, 6, v64
	v_add_u32_e32 v56, 8, v64
	v_add_u32_e32 v58, 10, v64
	v_add_u32_e32 v60, 12, v64
	v_add_u32_e32 v62, 14, v64
	v_mad_i64_i32 v[48:49], s[62:63], v64, s60, v[46:47]
	v_mad_i64_i32 v[50:51], s[62:63], v50, s60, v[46:47]
	v_mad_i64_i32 v[52:53], s[62:63], v52, s60, v[46:47]
	v_mad_i64_i32 v[54:55], s[62:63], v54, s60, v[46:47]
	v_mad_i64_i32 v[56:57], s[62:63], v56, s60, v[46:47]
	v_mad_i64_i32 v[58:59], s[62:63], v58, s60, v[46:47]
	v_mad_i64_i32 v[60:61], s[62:63], v60, s60, v[46:47]
	v_mad_i64_i32 v[62:63], s[62:63], v62, s60, v[46:47]
	global_load_dword v65, v[48:49], off nt
	global_load_dword v66, v[50:51], off nt
	global_load_dword v67, v[52:53], off nt
	global_load_dword v68, v[54:55], off nt
	global_load_dword v69, v[56:57], off nt
	global_load_dword v70, v[58:59], off nt
	global_load_dword v71, v[60:61], off nt
	global_load_dword v72, v[62:63], off nt
	v_add_u32_e32 v48, 16, v64
	v_add_u32_e32 v50, 18, v64
	v_add_u32_e32 v52, 20, v64
	v_add_u32_e32 v54, 22, v64
	v_add_u32_e32 v56, 24, v64
	v_add_u32_e32 v58, 26, v64
	v_add_u32_e32 v60, 28, v64
	v_add_u32_e32 v62, 30, v64
	v_mad_i64_i32 v[48:49], s[62:63], v48, s60, v[46:47]
	v_mad_i64_i32 v[50:51], s[62:63], v50, s60, v[46:47]
	v_mad_i64_i32 v[52:53], s[62:63], v52, s60, v[46:47]
	v_mad_i64_i32 v[54:55], s[62:63], v54, s60, v[46:47]
	v_mad_i64_i32 v[56:57], s[62:63], v56, s60, v[46:47]
	v_mad_i64_i32 v[58:59], s[62:63], v58, s60, v[46:47]
	v_mad_i64_i32 v[60:61], s[62:63], v60, s60, v[46:47]
	v_mad_i64_i32 v[62:63], s[62:63], v62, s60, v[46:47]
	global_load_dword v73, v[48:49], off nt
	global_load_dword v74, v[50:51], off nt
	global_load_dword v75, v[52:53], off nt
	global_load_dword v76, v[54:55], off nt
	global_load_dword v77, v[56:57], off nt
	global_load_dword v78, v[58:59], off nt
	global_load_dword v79, v[60:61], off nt
	global_load_dword v80, v[62:63], off nt
	v_add_u32_e32 v48, 32, v64
	v_add_u32_e32 v50, 34, v64
	v_add_u32_e32 v52, 36, v64
	v_add_u32_e32 v54, 38, v64
	v_add_u32_e32 v56, 40, v64
	v_add_u32_e32 v58, 42, v64
	v_add_u32_e32 v60, 44, v64
	v_add_u32_e32 v62, 46, v64
	v_mad_i64_i32 v[48:49], s[62:63], v48, s60, v[46:47]
	v_mad_i64_i32 v[50:51], s[62:63], v50, s60, v[46:47]
	v_mad_i64_i32 v[52:53], s[62:63], v52, s60, v[46:47]
	v_mad_i64_i32 v[54:55], s[62:63], v54, s60, v[46:47]
	v_mad_i64_i32 v[56:57], s[62:63], v56, s60, v[46:47]
	v_mad_i64_i32 v[58:59], s[62:63], v58, s60, v[46:47]
	v_mad_i64_i32 v[60:61], s[62:63], v60, s60, v[46:47]
	v_mad_i64_i32 v[62:63], s[62:63], v62, s60, v[46:47]
	global_load_dword v81, v[48:49], off nt
	global_load_dword v82, v[50:51], off nt
	global_load_dword v83, v[52:53], off nt
	global_load_dword v84, v[54:55], off nt
	global_load_dword v85, v[56:57], off nt
	global_load_dword v86, v[58:59], off nt
	global_load_dword v87, v[60:61], off nt
	s_nop 0
	global_load_dword v62, v[62:63], off nt
	v_add_u32_e32 v48, 48, v64
	v_add_u32_e32 v50, 50, v64
	v_add_u32_e32 v52, 52, v64
	v_add_u32_e32 v54, 54, v64
	v_add_u32_e32 v56, 56, v64
	v_add_u32_e32 v58, 58, v64
	v_add_u32_e32 v60, 60, v64
	v_add_u32_e32 v63, 62, v64
	v_mad_i64_i32 v[48:49], s[62:63], v48, s60, v[46:47]
	v_mad_i64_i32 v[50:51], s[62:63], v50, s60, v[46:47]
	v_mad_i64_i32 v[52:53], s[62:63], v52, s60, v[46:47]
	v_mad_i64_i32 v[54:55], s[62:63], v54, s60, v[46:47]
	v_mad_i64_i32 v[56:57], s[62:63], v56, s60, v[46:47]
	v_mad_i64_i32 v[58:59], s[62:63], v58, s60, v[46:47]
	v_mad_i64_i32 v[60:61], s[62:63], v60, s60, v[46:47]
	v_mad_i64_i32 v[46:47], s[62:63], v63, s60, v[46:47]
	global_load_dword v48, v[48:49], off nt
	s_nop 0
	global_load_dword v49, v[50:51], off nt
	s_nop 0
	global_load_dword v50, v[52:53], off nt
	global_load_dword v51, v[54:55], off nt
	s_nop 0
	global_load_dword v52, v[56:57], off nt
	global_load_dword v53, v[58:59], off nt
	global_load_dword v54, v[60:61], off nt
	s_nop 0
	global_load_dword v46, v[46:47], off nt
	s_waitcnt vmcnt(30)
	ds_write2_b32 v29, v65, v66 offset1:66
	s_waitcnt vmcnt(28)
	ds_write2_b32 v29, v67, v68 offset0:132 offset1:198
	s_waitcnt vmcnt(26)
	ds_write2_b32 v38, v69, v70 offset0:8 offset1:74
	s_waitcnt vmcnt(24)
	ds_write2_b32 v38, v71, v72 offset0:140 offset1:206
	s_waitcnt vmcnt(22)
	ds_write2_b32 v39, v73, v74 offset0:16 offset1:82
	s_waitcnt vmcnt(20)
	ds_write2_b32 v39, v75, v76 offset0:148 offset1:214
	s_waitcnt vmcnt(18)
	ds_write2_b32 v40, v77, v78 offset0:24 offset1:90
	s_waitcnt vmcnt(16)
	ds_write2_b32 v40, v79, v80 offset0:156 offset1:222
	s_waitcnt vmcnt(14)
	ds_write2_b32 v41, v81, v82 offset0:32 offset1:98
	s_waitcnt vmcnt(12)
	ds_write2_b32 v41, v83, v84 offset0:164 offset1:230
	s_waitcnt vmcnt(10)
	ds_write2_b32 v42, v85, v86 offset0:40 offset1:106
	s_waitcnt vmcnt(8)
	ds_write2_b32 v42, v87, v62 offset0:172 offset1:238
	s_waitcnt vmcnt(6)
; #define GAS __attribute__((address_space(1)))
; #define LAS __attribute__((address_space(3)))
; #define LDS_WAIT() asm volatile("s_waitcnt lgkmcnt(0)" ::: "memory")
; __device__ __forceinline__ unsigned pk2(float lo, float hi) { return f2bf(lo) | (f2bf(hi) << 16); }
; __device__ __forceinline__ void tr_item(const float* W, int ld, int K, int nblk, int item, bf16* WT, bool gu, LAS float* scr, int lane) {
;     ...
;       for (int i = 0; i < 32; ++i) scr[(2 * i + (lane >> 5)) * 33 + (lane & 31)] = t_[i]; }
;     LDS_WAIT(); asm volatile("" ::: "memory");
;     const int c = lane & 7;
; #pragma unroll
;     for (int j = 0; j < 4; ++j) { const int n = (lane >> 3) + 8 * j; const LAS float* s = scr + (8 * c) * 33 + n;
;         v4u o; o.x = pk2(s[0 * 33], s[1 * 33]); o.y = pk2(s[2 * 33], s[3 * 33]); o.z = pk2(s[4 * 33], s[5 * 33]); o.w = pk2(s[6 * 33], s[7 * 33]);
;         *(GAS v4u*)(WT + (size_t)(drow0 + n) * K + k0 + 8 * c) = o; }
;     LDS_WAIT(); asm volatile("" ::: "memory");
	ds_write2_b32 v43, v48, v49 offset0:48 offset1:114
	s_waitcnt vmcnt(4)
	ds_write2_b32 v43, v50, v51 offset0:180 offset1:246
	s_waitcnt vmcnt(2)
	ds_write2_b32 v44, v52, v53 offset0:56 offset1:122
	s_waitcnt vmcnt(0)
	ds_write2_b32 v44, v54, v46 offset0:188 offset1:254
	s_waitcnt lgkmcnt(0)
	ds_read2_b32 v[50:51], v34 offset1:8
	ds_read2_b32 v[54:55], v34 offset0:33 offset1:41
	ds_read2_b32 v[56:57], v34 offset0:66 offset1:74
	ds_read2_b32 v[58:59], v34 offset0:99 offset1:107
	ds_read2_b32 v[60:61], v34 offset0:132 offset1:140
	s_waitcnt lgkmcnt(4)
	v_bfe_u32 v46, v50, 16, 1
	v_add3_u32 v46, v50, v46, s57
	s_waitcnt lgkmcnt(3)
	v_bfe_u32 v47, v54, 16, 1
	v_lshrrev_b32_e32 v46, 16, v46
	v_add3_u32 v47, v54, v47, s57
	ds_read2_b32 v[62:63], v34 offset0:165 offset1:173
	v_and_or_b32 v46, v47, s58, v46
	s_waitcnt lgkmcnt(3)
	v_bfe_u32 v47, v56, 16, 1
	v_add3_u32 v47, v56, v47, s57
	s_waitcnt lgkmcnt(2)
	v_bfe_u32 v48, v58, 16, 1
	ds_read2_b32 v[64:65], v34 offset0:198 offset1:206
	v_lshrrev_b32_e32 v47, 16, v47
	v_add3_u32 v48, v58, v48, s57
	ds_read2_b32 v[66:67], v34 offset0:231 offset1:239
	v_and_or_b32 v47, v48, s58, v47
	s_waitcnt lgkmcnt(3)
	v_bfe_u32 v48, v60, 16, 1
	v_add3_u32 v48, v60, v48, s57
	s_waitcnt lgkmcnt(2)
	v_bfe_u32 v49, v62, 16, 1
	v_lshrrev_b32_e32 v48, 16, v48
	v_add3_u32 v49, v62, v49, s57
	v_and_or_b32 v48, v49, s58, v48
	s_waitcnt lgkmcnt(1)
	v_bfe_u32 v49, v64, 16, 1
	v_add_u32_e32 v68, s4, v33
	s_ashr_i32 s7, s6, 31
	v_add3_u32 v49, v64, v49, s57
	s_waitcnt lgkmcnt(0)
	v_bfe_u32 v50, v66, 16, 1
	v_ashrrev_i32_e32 v69, 31, v68
	v_lshl_add_u64 v[52:53], s[6:7], 1, v[26:27]
	v_lshrrev_b32_e32 v49, 16, v49
	v_add3_u32 v50, v66, v50, s57
	v_lshlrev_b64 v[70:71], 11, v[68:69]
	v_and_or_b32 v49, v50, s58, v49
	v_lshl_add_u64 v[70:71], v[52:53], 0, v[70:71]
	global_store_dwordx4 v[70:71], v[46:49], off
	v_bfe_u32 v50, v67, 16, 1
	v_add3_u32 v50, v67, v50, s57
	v_bfe_u32 v46, v51, 16, 1
	v_add3_u32 v46, v51, v46, s57
	v_bfe_u32 v47, v55, 16, 1
	v_lshrrev_b32_e32 v46, 16, v46
	v_add3_u32 v47, v55, v47, s57
	v_and_or_b32 v46, v47, s58, v46
	v_bfe_u32 v47, v57, 16, 1
	v_add3_u32 v47, v57, v47, s57
	v_bfe_u32 v48, v59, 16, 1
	v_lshrrev_b32_e32 v47, 16, v47
	v_add3_u32 v48, v59, v48, s57
	v_and_or_b32 v47, v48, s58, v47
	v_bfe_u32 v48, v61, 16, 1
	v_add3_u32 v48, v61, v48, s57
	v_bfe_u32 v49, v63, 16, 1
	v_lshrrev_b32_e32 v48, 16, v48
	v_add3_u32 v49, v63, v49, s57
	v_and_or_b32 v48, v49, s58, v48
	v_bfe_u32 v49, v65, 16, 1
	v_add3_u32 v49, v65, v49, s57
	v_lshrrev_b32_e32 v49, 16, v49
	v_and_or_b32 v49, v50, s58, v49
	v_add_u32_e32 v50, 8, v68
	v_ashrrev_i32_e32 v51, 31, v50
	v_lshlrev_b64 v[50:51], 11, v[50:51]
	ds_read2_b32 v[54:55], v34 offset0:16 offset1:24
	v_lshl_add_u64 v[50:51], v[52:53], 0, v[50:51]
	global_store_dwordx4 v[50:51], v[46:49], off
	ds_read2_b32 v[50:51], v34 offset0:49 offset1:57
	ds_read2_b32 v[56:57], v34 offset0:82 offset1:90
	ds_read2_b32 v[58:59], v34 offset0:115 offset1:123
	s_waitcnt lgkmcnt(3)
	v_bfe_u32 v46, v54, 16, 1
	v_add3_u32 v46, v54, v46, s57
	s_waitcnt lgkmcnt(2)
	v_bfe_u32 v47, v50, 16, 1
	ds_read2_b32 v[60:61], v34 offset0:148 offset1:156
	v_lshrrev_b32_e32 v46, 16, v46
	v_add3_u32 v47, v50, v47, s57
	ds_read2_b32 v[62:63], v34 offset0:181 offset1:189
	v_and_or_b32 v46, v47, s58, v46
	s_waitcnt lgkmcnt(3)
	v_bfe_u32 v47, v56, 16, 1
	v_add3_u32 v47, v56, v47, s57
	s_waitcnt lgkmcnt(2)
	v_bfe_u32 v48, v58, 16, 1
	ds_read2_b32 v[64:65], v34 offset0:214 offset1:222
	v_lshrrev_b32_e32 v47, 16, v47
	v_add3_u32 v48, v58, v48, s57
	ds_read2_b32 v[66:67], v34 offset0:247 offset1:255
	v_and_or_b32 v47, v48, s58, v47
	s_waitcnt lgkmcnt(3)
	v_bfe_u32 v48, v60, 16, 1
	v_add3_u32 v48, v60, v48, s57
	s_waitcnt lgkmcnt(2)
	v_bfe_u32 v49, v62, 16, 1
	v_lshrrev_b32_e32 v48, 16, v48
	v_add3_u32 v49, v62, v49, s57
	v_and_or_b32 v48, v49, s58, v48
	s_waitcnt lgkmcnt(1)
	v_bfe_u32 v49, v64, 16, 1
	v_add_u32_e32 v70, 16, v68
	v_add3_u32 v49, v64, v49, s57
	s_waitcnt lgkmcnt(0)
	v_bfe_u32 v50, v66, 16, 1
	v_ashrrev_i32_e32 v71, 31, v70
	v_lshrrev_b32_e32 v49, 16, v49
	v_add3_u32 v50, v66, v50, s57
	v_lshlrev_b64 v[70:71], 11, v[70:71]
	v_and_or_b32 v49, v50, s58, v49
	v_lshl_add_u64 v[70:71], v[52:53], 0, v[70:71]
	global_store_dwordx4 v[70:71], v[46:49], off
	v_bfe_u32 v50, v67, 16, 1
	v_add3_u32 v50, v67, v50, s57
	v_bfe_u32 v46, v55, 16, 1
	v_add3_u32 v46, v55, v46, s57
	v_bfe_u32 v47, v51, 16, 1
	v_lshrrev_b32_e32 v46, 16, v46
	v_add3_u32 v47, v51, v47, s57
	v_and_or_b32 v46, v47, s58, v46
	v_bfe_u32 v47, v57, 16, 1
	v_add3_u32 v47, v57, v47, s57
	v_bfe_u32 v48, v59, 16, 1
	v_lshrrev_b32_e32 v47, 16, v47
	v_add3_u32 v48, v59, v48, s57
	v_and_or_b32 v47, v48, s58, v47
	v_bfe_u32 v48, v61, 16, 1
	v_add3_u32 v48, v61, v48, s57
	v_bfe_u32 v49, v63, 16, 1
	v_lshrrev_b32_e32 v48, 16, v48
	v_add3_u32 v49, v63, v49, s57
	v_and_or_b32 v48, v49, s58, v48
	v_bfe_u32 v49, v65, 16, 1
	v_add3_u32 v49, v65, v49, s57
	v_lshrrev_b32_e32 v49, 16, v49
	v_and_or_b32 v49, v50, s58, v49
	v_add_u32_e32 v50, 24, v68
	v_ashrrev_i32_e32 v51, 31, v50
	v_lshlrev_b64 v[50:51], 11, v[50:51]
	v_lshl_add_u64 v[50:51], v[52:53], 0, v[50:51]
	global_store_dwordx4 v[50:51], v[46:49], off
	s_waitcnt lgkmcnt(0)
	s_branch .LBB0_1405
